# three quarters of the layer-1 w_down transposition moved into the idle slot of the layer-1 in-projection (33 region steps per idle workgroup)
# baseline (speedup 1.0000x reference)
; #define LAS __attribute__((address_space(3)))
; #define PHASE_IDS() int tid_l_ = threadIdx.x; asm volatile("" : "+v"(tid_l_)); const int tid = tid_l_, lane = tid & 63, wave = __builtin_amdgcn_readfirstlane(tid >> 6); \
;     const int gw = F.vcu * NWAVES + wave, NGW = F.G * NWAVES, gt = F.vcu * (NWAVES * 64) + tid, NGT = F.G * NWAVES * 64; (void)gw; (void)NGW; (void)gt; (void)NGT; (void)lane
; __global__ void __launch_bounds__(NWAVES * 64, 2) hybrid_fwd(Args args) {
;     ...
;     {
;         PHASE_IDS();
;         LAS float* scr = (LAS float*)(F.lds + RING_OFF + wave * 16384);
;         constexpr int I_IN = (DM / 64) * (NPROJ / 32), I_O = (DM / 64) * (DM / 32), I_UP = (DM / 64) * (FF / 32), I_DN = (FF / 64) * (DM / 32);
;         constexpr int I_L = I_IN + I_O + I_UP + I_DN;
;         for (int rep = 0; rep < REP_PRO; ++rep)
;         for (int it = gw; it < DEPTH * I_L; it += NGW) {
;             const int l = it / I_L; int r = it % I_L;
;             if (r < I_IN) { if (l >= PROJ_F8_FROM) p0_transpose_item_f8<true, 1>(args.in[2] + (size_t)l * DM * NSRC, DM, NSRC, NPROJ / 32, (unsigned char*)(ws + WS_WIN + l * SZ_WIN), WUP8_SCALE, args.in[1] + l * DM, args.in[1] + l * DM, DM, scr, r, lane);
;                 else p0_transpose_item<1, true>(args.in[2] + (size_t)l * DM * NSRC, DM, NSRC, NPROJ / 32, (bf16*)(ws + WS_WIN + l * SZ_WIN), args.in[1] + l * DM, args.in[1] + l * DM, DM, scr, r, lane); continue; } r -= I_IN;
;             if (r < I_O) { if (l >= WO_F8_FROM) p0_transpose_item_f8<true>(args.in[13] + (size_t)l * DM * DM, DM, DM, DM / 32, (unsigned char*)(ws + WS_WO + l * SZ_WO), 64.f, args.in[6] + l * 2048, args.in[12] + l * 2048, 2048, scr, r, lane);
;                 else p0_transpose_item<0, true>(args.in[13] + (size_t)l * DM * DM, DM, DM, DM / 32, (bf16*)(ws + WS_WO + l * SZ_WO), args.in[6] + l * 2048, args.in[12] + l * 2048, 2048, scr, r, lane); continue; } r -= I_O;
;             if (r < I_UP) { p0_transpose_item_f8<true>(args.in[15] + (size_t)l * DM * FF, DM, FF, FF / 32, (unsigned char*)(ws + WS_WUP + l * SZ_WUP), WUP8_SCALE, args.in[14] + l * DM, args.in[14] + l * DM, DM, scr, r, lane); continue; } r -= I_UP;
;             p0_transpose_item_f8<false>(args.in[16] + (size_t)l * FF * DM, FF, DM, DM / 32, (unsigned char*)(ws + WS_WDN + l * SZ_WDN), 128.f, args.in[16], args.in[16], 0, scr, r, lane);
;         }
.LBB0_11:
	s_or_b64 exec, exec, s[0:1]
	v_mov_b32_e32 v1, v0
	v_readlane_b32 s1, v253, 2
	v_readfirstlane_b32 s0, v1
	s_ashr_i32 s0, s0, 6
	s_lshl_b32 s1, s1, 3
	s_add_i32 s80, s0, s1
	s_lshl_b32 s0, s0, 14
	v_lshlrev_b32_e32 v2, 3, v1
	v_writelane_b32 v253, s1, 46
	s_add_i32 s1, s0, 0
	v_and_b32_e32 v18, 31, v1
	v_bfe_u32 v20, v1, 3, 3
	v_and_b32_e32 v8, 56, v2
	s_lshl_b32 s96, s83, 3
	s_lshl_b32 s76, s83, 9
	v_bfe_u32 v6, v1, 5, 1
	v_lshl_add_u32 v25, v18, 2, s1
	s_movk_i32 s0, 0x84
	v_mul_u32_u24_e32 v2, 0x84, v8
	v_lshlrev_b32_e32 v3, 2, v20
	s_cmp_gt_i32 s80, 0x2f3ff
	v_mad_u32_u24 v19, v6, s0, v25
	v_mov_b32_e32 v11, 0
	v_add3_u32 v21, s1, v2, v3
	v_or_b32_e32 v22, 8, v20
	v_or_b32_e32 v23, 16, v20
	v_or_b32_e32 v24, 24, v20
	s_cbranch_scc1 .Lco3_hop_192
	v_and_b32_e32 v249, 63, v0
	v_lshrrev_b32_e32 v250, 6, v0
	v_readlane_b32 s15, v253, 2
	s_lshr_b32 s22, s15, 3
	s_and_b32 s23, s15, 7
	v_lshrrev_b32_e32 v246, 5, v249
	v_lshl_add_u32 v247, v250, 4, v246
	v_and_b32_e32 v248, 31, v249
	v_xor_b32_e32 v248, v248, v250
	v_lshlrev_b32_e32 v248, 4, v248
	v_lshl_add_u32 v209, v247, 9, v248
	v_add_u32_e32 v210, 0x10000, v209
	v_lshlrev_b32_e32 v96, 2, v247
	v_and_b32_e32 v248, 31, v249
	v_lshlrev_b32_e32 v248, 4, v248
	s_mov_b32 s20, 0x10000
	v_mad_u32_u24 v74, v247, s20, v248
	s_mov_b32 s20, 0x4000
	v_mad_u32_u24 v75, v247, s20, v248
	s_mov_b32 s20, 0xb140
	v_mad_u32_u24 v76, v247, s20, v248
	v_and_b32_e32 v246, 7, v249
	v_lshrrev_b32_e32 v247, 5, v249
	v_lshl_add_u32 v247, v250, 2, v247
	v_xor_b32_e32 v247, v247, v246
	v_lshlrev_b32_e32 v247, 4, v247
	v_lshl_add_u32 v247, v246, 13, v247
	v_bfe_u32 v248, v249, 3, 2
	v_lshl_add_u32 v211, v248, 2, v247
	v_add_u32_e32 v212, 0x10000, v211
	v_and_b32_e32 v246, 7, v249
	v_lshrrev_b32_e32 v247, 5, v249
	v_lshl_add_u32 v247, v250, 2, v247
	v_add_u32_e32 v247, 2, v247
	v_xor_b32_e32 v247, v247, v246
	v_lshlrev_b32_e32 v247, 4, v247
	v_lshl_add_u32 v247, v246, 13, v247
	v_bfe_u32 v248, v249, 3, 2
	v_lshl_add_u32 v213, v248, 2, v247
	v_add_u32_e32 v214, 0x10000, v213
	v_and_b32_e32 v246, 15, v249
	v_lshrrev_b32_e32 v247, 1, v246
	v_lshlrev_b32_e32 v248, 2, v250
	v_xor_b32_e32 v248, v248, v247
	v_lshlrev_b32_e32 v248, 4, v248
	v_lshl_add_u32 v248, v246, 12, v248
	v_lshrrev_b32_e32 v247, 4, v249
	v_lshl_add_u32 v112, v247, 2, v248
	v_add_u32_e32 v113, 0x10000, v112
	v_and_b32_e32 v246, 15, v249
	v_lshrrev_b32_e32 v247, 1, v246
	v_lshlrev_b32_e32 v248, 2, v250
	v_add_u32_e32 v248, 1, v248
	v_xor_b32_e32 v248, v248, v247
	v_lshlrev_b32_e32 v248, 4, v248
	v_lshl_add_u32 v248, v246, 12, v248
	v_lshrrev_b32_e32 v247, 4, v249
	v_lshl_add_u32 v114, v247, 2, v248
	v_add_u32_e32 v115, 0x10000, v114
	v_and_b32_e32 v246, 15, v249
	v_lshrrev_b32_e32 v247, 1, v246
	v_lshlrev_b32_e32 v248, 2, v250
	v_add_u32_e32 v248, 2, v248
	v_xor_b32_e32 v248, v248, v247
	v_lshlrev_b32_e32 v248, 4, v248
	v_lshl_add_u32 v248, v246, 12, v248
	v_lshrrev_b32_e32 v247, 4, v249
	v_lshl_add_u32 v116, v247, 2, v248
	v_add_u32_e32 v117, 0x10000, v116
	v_and_b32_e32 v246, 15, v249
	v_lshrrev_b32_e32 v247, 1, v246
	v_lshlrev_b32_e32 v248, 2, v250
	v_add_u32_e32 v248, 3, v248
	v_xor_b32_e32 v248, v248, v247
	v_lshlrev_b32_e32 v248, 4, v248
	v_lshl_add_u32 v248, v246, 12, v248
	v_lshrrev_b32_e32 v247, 4, v249
	v_lshl_add_u32 v118, v247, 2, v248
	v_add_u32_e32 v119, 0x10000, v118
	v_lshrrev_b32_e32 v246, 3, v249
	v_lshl_add_u32 v246, v250, 4, v246
	v_and_b32_e32 v247, 7, v249
	v_lshlrev_b32_e32 v247, 4, v247
	v_lshl_add_u32 v77, v246, 12, v247
	v_lshl_add_u32 v79, v246, 14, v247
	v_and_b32_e32 v248, 63, v246
	v_lshlrev_b32_e32 v248, 1, v248
	v_lshrrev_b32_e32 v246, 6, v246
	v_or_b32_e32 v248, v248, v246
	v_lshl_add_u32 v81, v248, 12, v247
	v_lshrrev_b32_e32 v246, 3, v249
	v_lshl_add_u32 v246, v250, 4, v246
	v_add_u32_e32 v246, 8, v246
	v_and_b32_e32 v247, 7, v249
	v_lshlrev_b32_e32 v247, 4, v247
	v_lshl_add_u32 v78, v246, 12, v247
	v_lshl_add_u32 v80, v246, 14, v247
	v_and_b32_e32 v248, 63, v246
	v_lshlrev_b32_e32 v248, 1, v248
	v_lshrrev_b32_e32 v246, 6, v246
	v_or_b32_e32 v248, v248, v246
	v_lshl_add_u32 v82, v248, 12, v247
	v_lshrrev_b32_e32 v246, 4, v249
	v_lshl_add_u32 v246, v250, 4, v246
	v_and_b32_e32 v247, 15, v249
	v_lshlrev_b32_e32 v247, 4, v247
	v_lshl_add_u32 v83, v246, 13, v247
	v_and_b32_e32 v248, 63, v246
	v_lshlrev_b32_e32 v248, 1, v248
	v_lshrrev_b32_e32 v246, 6, v246
	v_or_b32_e32 v248, v248, v246
	v_lshl_add_u32 v87, v248, 13, v247
	v_lshrrev_b32_e32 v246, 4, v249
	v_lshl_add_u32 v246, v250, 4, v246
	v_add_u32_e32 v246, 4, v246
	v_and_b32_e32 v247, 15, v249
	v_lshlrev_b32_e32 v247, 4, v247
	v_lshl_add_u32 v84, v246, 13, v247
	v_and_b32_e32 v248, 63, v246
	v_lshlrev_b32_e32 v248, 1, v248
	v_lshrrev_b32_e32 v246, 6, v246
	v_or_b32_e32 v248, v248, v246
	v_lshl_add_u32 v88, v248, 13, v247
	v_lshrrev_b32_e32 v246, 4, v249
	v_lshl_add_u32 v246, v250, 4, v246
	v_add_u32_e32 v246, 8, v246
	v_and_b32_e32 v247, 15, v249
	v_lshlrev_b32_e32 v247, 4, v247
	v_lshl_add_u32 v85, v246, 13, v247
	v_and_b32_e32 v248, 63, v246
	v_lshlrev_b32_e32 v248, 1, v248
	v_lshrrev_b32_e32 v246, 6, v246
	v_or_b32_e32 v248, v248, v246
	v_lshl_add_u32 v89, v248, 13, v247
	v_lshrrev_b32_e32 v246, 4, v249
	v_lshl_add_u32 v246, v250, 4, v246
	v_add_u32_e32 v246, 12, v246
	v_and_b32_e32 v247, 15, v249
	v_lshlrev_b32_e32 v247, 4, v247
	v_lshl_add_u32 v86, v246, 13, v247
	v_and_b32_e32 v248, 63, v246
	v_lshlrev_b32_e32 v248, 1, v248
	v_lshrrev_b32_e32 v246, 6, v246
	v_or_b32_e32 v248, v248, v246
	v_lshl_add_u32 v90, v248, 13, v247
	v_mov_b32_e32 v95, 0x43e00000
	s_mov_b32 s62, 0xc3e00000
	s_mov_b32 s63, 0x7fff
	s_mov_b32 s64, 0x07060302
	v_readlane_b32 s10, v253, 5
;     ...
;     for (int i = 0; i < 32; ++i) v[i] = sc >= 0 ? W[(size_t)(k0 + 2 * i + (lane >> 5)) * Nsrc + sc] : 0.f;
; #pragma unroll
;     for (int i = 0; i < 32; ++i) { const int k = k0 + 2 * i + (lane >> 5); float x = v[i] * wscale; if (KS) x *= (k < ksplit ? ksA[k] : ksB[k - ksplit]); scr[(2 * i + (lane >> 5)) * 33 + (lane & 31)] = x; }
; __global__ void __launch_bounds__(NWAVES * 64, 2) hybrid_fwd(Args args) {
;     ...
;         for (int it = gw; it < DEPTH * I_L; it += NGW) {
;             const int l = it / I_L; int r = it % I_L;
;             if (r < I_IN) { if (l >= PROJ_F8_FROM) p0_transpose_item_f8<true, 1>(args.in[2] + (size_t)l * DM * NSRC, DM, NSRC, NPROJ / 32, (unsigned char*)(ws + WS_WIN + l * SZ_WIN), WUP8_SCALE, args.in[1] + l * DM, args.in[1] + l * DM, DM, scr, r, lane);
;                 else p0_transpose_item<1, true>(args.in[2] + (size_t)l * DM * NSRC, DM, NSRC, NPROJ / 32, (bf16*)(ws + WS_WIN + l * SZ_WIN), args.in[1] + l * DM, args.in[1] + l * DM, DM, scr, r, lane); continue; } r -= I_IN;
;             if (r < I_O) { if (l >= WO_F8_FROM) p0_transpose_item_f8<true>(args.in[13] + (size_t)l * DM * DM, DM, DM, DM / 32, (unsigned char*)(ws + WS_WO + l * SZ_WO), 64.f, args.in[6] + l * 2048, args.in[12] + l * 2048, 2048, scr, r, lane);
;                 else p0_transpose_item<0, true>(args.in[13] + (size_t)l * DM * DM, DM, DM, DM / 32, (bf16*)(ws + WS_WO + l * SZ_WO), args.in[6] + l * 2048, args.in[12] + l * 2048, 2048, scr, r, lane); continue; } r -= I_O;
;             if (r < I_UP) { p0_transpose_item_f8<true>(args.in[15] + (size_t)l * DM * FF, DM, FF, FF / 32, (unsigned char*)(ws + WS_WUP + l * SZ_WUP), WUP8_SCALE, args.in[14] + l * DM, args.in[14] + l * DM, DM, scr, r, lane); continue; } r -= I_UP;
	v_readlane_b32 s11, v253, 6
	s_lshl_b32 s20, s22, 9
	s_add_u32 s10, s10, s20
	s_addc_u32 s11, s11, 0
	global_load_dword v42, v96, s[10:11] offset:0
	global_load_dword v43, v96, s[10:11] offset:8
	global_load_dword v44, v96, s[10:11] offset:16
	global_load_dword v45, v96, s[10:11] offset:24
	global_load_dword v46, v96, s[10:11] offset:32
	global_load_dword v47, v96, s[10:11] offset:40
	global_load_dword v48, v96, s[10:11] offset:48
	global_load_dword v49, v96, s[10:11] offset:56
	v_readlane_b32 s10, v253, 5
	v_readlane_b32 s11, v253, 6
	s_lshl_b32 s20, s22, 9
	s_add_i32 s20, s20, 0x4000
	s_add_u32 s10, s10, s20
	s_addc_u32 s11, s11, 0
	global_load_dword v50, v96, s[10:11] offset:0
	global_load_dword v51, v96, s[10:11] offset:8
	global_load_dword v52, v96, s[10:11] offset:16
	global_load_dword v53, v96, s[10:11] offset:24
	global_load_dword v54, v96, s[10:11] offset:32
	global_load_dword v55, v96, s[10:11] offset:40
	global_load_dword v56, v96, s[10:11] offset:48
	global_load_dword v57, v96, s[10:11] offset:56
	v_readlane_b32 s10, v253, 15
	v_readlane_b32 s11, v253, 16
	v_readlane_b32 s20, v253, 27
	v_readlane_b32 s21, v253, 28
	s_sub_i32 s26, s22, 16
	s_cmp_lt_u32 s22, 16
	s_cselect_b32 s10, s10, s20
	s_cselect_b32 s11, s11, s21
	s_cselect_b32 s26, s22, s26
	s_lshl_b32 s20, s26, 9
	s_add_u32 s10, s10, s20
	s_addc_u32 s11, s11, 0
	global_load_dword v58, v96, s[10:11] offset:0
	global_load_dword v59, v96, s[10:11] offset:8
	global_load_dword v60, v96, s[10:11] offset:16
	global_load_dword v61, v96, s[10:11] offset:24
	global_load_dword v62, v96, s[10:11] offset:32
	global_load_dword v63, v96, s[10:11] offset:40
	global_load_dword v64, v96, s[10:11] offset:48
	global_load_dword v65, v96, s[10:11] offset:56
	v_readlane_b32 s10, v253, 15
	v_readlane_b32 s11, v253, 16
	v_readlane_b32 s20, v253, 27
	v_readlane_b32 s21, v253, 28
	s_sub_i32 s26, s22, 16
	s_cmp_lt_u32 s22, 16
	s_cselect_b32 s10, s10, s20
	s_cselect_b32 s11, s11, s21
	s_cselect_b32 s26, s22, s26
	s_lshl_b32 s20, s26, 9
	s_add_i32 s20, s20, 0x2000
	s_add_u32 s10, s10, s20
	s_addc_u32 s11, s11, 0
	global_load_dword v66, v96, s[10:11] offset:0
	global_load_dword v67, v96, s[10:11] offset:8
	global_load_dword v68, v96, s[10:11] offset:16
	global_load_dword v69, v96, s[10:11] offset:24
	global_load_dword v70, v96, s[10:11] offset:32
	global_load_dword v71, v96, s[10:11] offset:40
	global_load_dword v72, v96, s[10:11] offset:48
	global_load_dword v73, v96, s[10:11] offset:56
	v_readlane_b32 s10, v253, 31
	v_readlane_b32 s11, v253, 32
	s_lshl_b32 s20, s22, 9
	s_add_u32 s10, s10, s20
	s_addc_u32 s11, s11, 0
	global_load_dword v26, v96, s[10:11] offset:0
	global_load_dword v27, v96, s[10:11] offset:8
	global_load_dword v28, v96, s[10:11] offset:16
	global_load_dword v29, v96, s[10:11] offset:24
	global_load_dword v30, v96, s[10:11] offset:32
	global_load_dword v31, v96, s[10:11] offset:40
	global_load_dword v32, v96, s[10:11] offset:48
	global_load_dword v33, v96, s[10:11] offset:56
	v_readlane_b32 s10, v253, 31
	v_readlane_b32 s11, v253, 32
	s_lshl_b32 s20, s22, 9
	s_add_i32 s20, s20, 0x4000
	s_add_u32 s10, s10, s20
	s_addc_u32 s11, s11, 0
	global_load_dword v34, v96, s[10:11] offset:0
	global_load_dword v35, v96, s[10:11] offset:8
	global_load_dword v36, v96, s[10:11] offset:16
	global_load_dword v37, v96, s[10:11] offset:24
	global_load_dword v38, v96, s[10:11] offset:32
	global_load_dword v39, v96, s[10:11] offset:40
	global_load_dword v40, v96, s[10:11] offset:48
	global_load_dword v41, v96, s[10:11] offset:56
	s_waitcnt vmcnt(0)
	v_mul_f32_e32 v50, 0x42800000, v50
	v_mul_f32_e32 v51, 0x42800000, v51
	v_mul_f32_e32 v52, 0x42800000, v52
	v_mul_f32_e32 v53, 0x42800000, v53
	v_mul_f32_e32 v54, 0x42800000, v54
	v_mul_f32_e32 v55, 0x42800000, v55
	v_mul_f32_e32 v56, 0x42800000, v56
	v_mul_f32_e32 v57, 0x42800000, v57
	v_mul_f32_e32 v66, 0x42800000, v66
	v_mul_f32_e32 v67, 0x42800000, v67
	v_mul_f32_e32 v68, 0x42800000, v68
	v_mul_f32_e32 v69, 0x42800000, v69
	v_mul_f32_e32 v70, 0x42800000, v70
	v_mul_f32_e32 v71, 0x42800000, v71
	v_mul_f32_e32 v72, 0x42800000, v72
	v_mul_f32_e32 v73, 0x42800000, v73
	v_mul_f32_e32 v26, 0x42800000, v26
	v_mul_f32_e32 v27, 0x42800000, v27
	v_mul_f32_e32 v28, 0x42800000, v28
	v_mul_f32_e32 v29, 0x42800000, v29
	v_mul_f32_e32 v30, 0x42800000, v30
	v_mul_f32_e32 v31, 0x42800000, v31
	v_mul_f32_e32 v32, 0x42800000, v32
	v_mul_f32_e32 v33, 0x42800000, v33
	v_mul_f32_e32 v34, 0x42800000, v34
	v_mul_f32_e32 v35, 0x42800000, v35
	v_mul_f32_e32 v36, 0x42800000, v36
	v_mul_f32_e32 v37, 0x42800000, v37
	v_mul_f32_e32 v38, 0x42800000, v38
	v_mul_f32_e32 v39, 0x42800000, v39
	v_mul_f32_e32 v40, 0x42800000, v40
	v_mul_f32_e32 v41, 0x42800000, v41
	v_readlane_b32 s30, v253, 33
	v_readlane_b32 s31, v253, 34
	v_readlane_b32 s32, v253, 41
	v_readlane_b32 s33, v253, 42
	s_mul_i32 s20, s22, 0x800000
	s_lshl_b32 s21, s23, 9
	s_add_u32 s20, s20, s21
	s_add_u32 s30, s30, s20
	s_addc_u32 s31, s31, 0
	s_add_u32 s32, s32, 0xf600000
	s_addc_u32 s33, s33, 0
	s_lshl_b32 s20, s22, 7
	s_mul_i32 s21, s23, 0x80000
	s_add_u32 s20, s20, s21
	s_add_u32 s32, s32, s20
	s_addc_u32 s33, s33, 0
	v_readlane_b32 s34, v253, 33
	v_readlane_b32 s35, v253, 34
	v_readlane_b32 s36, v253, 41
	v_readlane_b32 s37, v253, 42
	s_add_u32 s34, s34, 0x10000000
	s_addc_u32 s35, s35, 0
	s_mul_i32 s20, s22, 0x800000
	s_lshl_b32 s21, s23, 9
	s_add_u32 s20, s20, s21
	s_add_u32 s34, s34, s20
	s_addc_u32 s35, s35, 0
	s_add_u32 s36, s36, 0x17600000
	s_addc_u32 s37, s37, 0
	s_lshl_b32 s20, s22, 7
	s_mul_i32 s21, s23, 0x80000
	s_add_u32 s20, s20, s21
	s_add_u32 s36, s36, s20
	s_addc_u32 s37, s37, 0
	v_readlane_b32 s38, v253, 35
; #define LDS_WAIT() asm volatile("s_waitcnt lgkmcnt(0)" ::: "memory")
;     const int pr = item >> 1, kb = 2 * (pr / nblk) + (item & 1), nb = pr % nblk, k0 = 64 * kb, n0 = 32 * nb;
;     const int nr = n0 + (lane & 31); const int sc = MAP == 1 ? src_col_in(nr) : nr;
;     float v[32];
; #pragma unroll
;     for (int i = 0; i < 32; ++i) v[i] = sc >= 0 ? W[(size_t)(k0 + 2 * i + (lane >> 5)) * Nsrc + sc] : 0.f;
; #pragma unroll
;     for (int i = 0; i < 32; ++i) { const int k = k0 + 2 * i + (lane >> 5); float x = v[i] * wscale; if (KS) x *= (k < ksplit ? ksA[k] : ksB[k - ksplit]); scr[(2 * i + (lane >> 5)) * 33 + (lane & 31)] = x; }
;     LDS_WAIT(); asm volatile("" ::: "memory");
; __global__ void __launch_bounds__(NWAVES * 64, 2) hybrid_fwd(Args args) {
;     ...
;             const int l = it / I_L; int r = it % I_L;
;             if (r < I_IN) { if (l >= PROJ_F8_FROM) p0_transpose_item_f8<true, 1>(args.in[2] + (size_t)l * DM * NSRC, DM, NSRC, NPROJ / 32, (unsigned char*)(ws + WS_WIN + l * SZ_WIN), WUP8_SCALE, args.in[1] + l * DM, args.in[1] + l * DM, DM, scr, r, lane);
;                 else p0_transpose_item<1, true>(args.in[2] + (size_t)l * DM * NSRC, DM, NSRC, NPROJ / 32, (bf16*)(ws + WS_WIN + l * SZ_WIN), args.in[1] + l * DM, args.in[1] + l * DM, DM, scr, r, lane); continue; } r -= I_IN;
;             if (r < I_O) { if (l >= WO_F8_FROM) p0_transpose_item_f8<true>(args.in[13] + (size_t)l * DM * DM, DM, DM, DM / 32, (unsigned char*)(ws + WS_WO + l * SZ_WO), 64.f, args.in[6] + l * 2048, args.in[12] + l * 2048, 2048, scr, r, lane);
;                 else p0_transpose_item<0, true>(args.in[13] + (size_t)l * DM * DM, DM, DM, DM / 32, (bf16*)(ws + WS_WO + l * SZ_WO), args.in[6] + l * 2048, args.in[12] + l * 2048, 2048, scr, r, lane); continue; } r -= I_O;
;             if (r < I_UP) { p0_transpose_item_f8<true>(args.in[15] + (size_t)l * DM * FF, DM, FF, FF / 32, (unsigned char*)(ws + WS_WUP + l * SZ_WUP), WUP8_SCALE, args.in[14] + l * DM, args.in[14] + l * DM, DM, scr, r, lane); continue; } r -= I_UP;
;             p0_transpose_item_f8<false>(args.in[16] + (size_t)l * FF * DM, FF, DM, DM / 32, (unsigned char*)(ws + WS_WDN + l * SZ_WDN), 128.f, args.in[16], args.in[16], 0, scr, r, lane);
	v_readlane_b32 s39, v253, 36
	v_readlane_b32 s40, v253, 41
	v_readlane_b32 s41, v253, 42
	s_mul_i32 s20, s22, 0x200000
	s_lshl_b32 s21, s23, 9
	s_add_u32 s20, s20, s21
	s_add_u32 s38, s38, s20
	s_addc_u32 s39, s39, 0
	s_add_u32 s40, s40, 0x1f600000
	s_addc_u32 s41, s41, 0
	s_lshl_b32 s20, s22, 7
	s_mul_i32 s21, s23, 0x200000
	s_add_u32 s20, s20, s21
	s_add_u32 s40, s40, s20
	s_addc_u32 s41, s41, 0
	v_readlane_b32 s42, v253, 35
	v_readlane_b32 s43, v253, 36
	v_readlane_b32 s44, v253, 41
	v_readlane_b32 s45, v253, 42
	s_add_u32 s42, s42, 0x10000000
	s_addc_u32 s43, s43, 0
	s_mul_i32 s20, s22, 0x200000
	s_lshl_b32 s21, s23, 9
	s_add_u32 s20, s20, s21
	s_add_u32 s42, s42, s20
	s_addc_u32 s43, s43, 0
	s_add_u32 s44, s44, 0x27600000
	s_addc_u32 s45, s45, 0
	s_lshl_b32 s20, s22, 7
	s_mul_i32 s21, s23, 0x200000
	s_add_u32 s20, s20, s21
	s_add_u32 s44, s44, s20
	s_addc_u32 s45, s45, 0
	v_readlane_b32 s46, v253, 7
	v_readlane_b32 s47, v253, 8
	v_readlane_b32 s48, v253, 41
	v_readlane_b32 s49, v253, 42
	s_mul_i32 s20, s22, 0x58a000
	s_add_u32 s46, s46, s20
	s_addc_u32 s47, s47, 0
	s_add_u32 s48, s48, 0x200000
	s_addc_u32 s49, s49, 0
	s_lshl_b32 s20, s22, 8
	s_add_u32 s48, s48, s20
	s_addc_u32 s49, s49, 0
	v_readlane_b32 s50, v253, 7
	v_readlane_b32 s51, v253, 8
	v_readlane_b32 s52, v253, 41
	v_readlane_b32 s53, v253, 42
	s_add_u32 s50, s50, 0xb140000
	s_addc_u32 s51, s51, 0
	s_mul_i32 s20, s22, 0x58a000
	s_add_u32 s50, s50, s20
	s_addc_u32 s51, s51, 0
	s_add_u32 s52, s52, 0x5c00000
	s_addc_u32 s53, s53, 0
	s_lshl_b32 s20, s22, 7
	s_add_u32 s52, s52, s20
	s_addc_u32 s53, s53, 0
	v_readlane_b32 s54, v253, 29
	v_readlane_b32 s55, v253, 30
	v_readlane_b32 s56, v253, 41
	v_readlane_b32 s57, v253, 42
	s_mul_i32 s20, s22, 0x200000
	s_lshl_b32 s21, s23, 9
	s_add_u32 s20, s20, s21
	s_add_u32 s54, s54, s20
	s_addc_u32 s55, s55, 0
	s_add_u32 s56, s56, 0xb600000
	s_addc_u32 s57, s57, 0
	s_lshl_b32 s20, s22, 8
	s_mul_i32 s21, s23, 0x100000
	s_add_u32 s20, s20, s21
	s_add_u32 s56, s56, s20
	s_addc_u32 s57, s57, 0
	v_readlane_b32 s58, v253, 29
	v_readlane_b32 s59, v253, 30
	v_readlane_b32 s60, v253, 41
	v_readlane_b32 s61, v253, 42
	s_add_u32 s58, s58, 0x4000000
	s_addc_u32 s59, s59, 0
	s_mul_i32 s20, s22, 0x200000
	s_lshl_b32 s21, s23, 9
	s_add_u32 s20, s20, s21
	s_add_u32 s58, s58, s20
	s_addc_u32 s59, s59, 0
	s_add_u32 s60, s60, 0xd600000
	s_addc_u32 s61, s61, 0
	s_lshl_b32 s20, s22, 7
	s_mul_i32 s21, s23, 0x80000
	s_add_u32 s20, s20, s21
	s_add_u32 s60, s60, s20
	s_addc_u32 s61, s61, 0
	s_mov_b64 s[8:9], s[30:31]
	global_load_dwordx4 v[144:147], v74, s[8:9]
	s_add_u32 s8, s8, 0x20000
	s_addc_u32 s9, s9, 0
	global_load_dwordx4 v[148:151], v74, s[8:9]
	s_add_u32 s8, s8, 0x20000
	s_addc_u32 s9, s9, 0
	global_load_dwordx4 v[152:155], v74, s[8:9]
	s_add_u32 s8, s8, 0x20000
	s_addc_u32 s9, s9, 0
	global_load_dwordx4 v[156:159], v74, s[8:9]
	s_add_u32 s8, s8, 0x20000
	s_addc_u32 s9, s9, 0
	global_load_dwordx4 v[160:163], v74, s[8:9]
	s_add_u32 s8, s8, 0x20000
	s_addc_u32 s9, s9, 0
	global_load_dwordx4 v[164:167], v74, s[8:9]
	s_add_u32 s8, s8, 0x20000
	s_addc_u32 s9, s9, 0
	global_load_dwordx4 v[168:171], v74, s[8:9]
	s_add_u32 s8, s8, 0x20000
	s_addc_u32 s9, s9, 0
	global_load_dwordx4 v[172:175], v74, s[8:9]
	s_add_u32 s8, s30, 0x1000
	s_addc_u32 s9, s31, 0
	global_load_dwordx4 v[176:179], v74, s[8:9]
	s_add_u32 s8, s8, 0x20000
	s_addc_u32 s9, s9, 0
	global_load_dwordx4 v[180:183], v74, s[8:9]
	s_add_u32 s8, s8, 0x20000
	s_addc_u32 s9, s9, 0
	global_load_dwordx4 v[184:187], v74, s[8:9]
	s_add_u32 s8, s8, 0x20000
	s_addc_u32 s9, s9, 0
	global_load_dwordx4 v[188:191], v74, s[8:9]
	s_add_u32 s8, s8, 0x20000
	s_addc_u32 s9, s9, 0
	global_load_dwordx4 v[192:195], v74, s[8:9]
	s_add_u32 s8, s8, 0x20000
	s_addc_u32 s9, s9, 0
	global_load_dwordx4 v[196:199], v74, s[8:9]
	s_add_u32 s8, s8, 0x20000
	s_addc_u32 s9, s9, 0
	global_load_dwordx4 v[200:203], v74, s[8:9]
	s_add_u32 s8, s8, 0x20000
	s_addc_u32 s9, s9, 0
	global_load_dwordx4 v[204:207], v74, s[8:9]
	s_waitcnt vmcnt(8)
	v_mul_f32_e32 v144, v26, v144
	v_mul_f32_e32 v145, v26, v145
	v_mul_f32_e32 v146, v26, v146
	v_mul_f32_e32 v147, v26, v147
	ds_write_b128 v209, v[144:147]
	v_mul_f32_e32 v148, v27, v148
	v_mul_f32_e32 v149, v27, v149
	v_mul_f32_e32 v150, v27, v150
	v_mul_f32_e32 v151, v27, v151
	ds_write_b128 v209, v[148:151] offset:1024
	v_mul_f32_e32 v152, v28, v152
	v_mul_f32_e32 v153, v28, v153
	v_mul_f32_e32 v154, v28, v154
	v_mul_f32_e32 v155, v28, v155
	ds_write_b128 v209, v[152:155] offset:2048
	v_mul_f32_e32 v156, v29, v156
	v_mul_f32_e32 v157, v29, v157
	v_mul_f32_e32 v158, v29, v158
	v_mul_f32_e32 v159, v29, v159
	ds_write_b128 v209, v[156:159] offset:3072
	v_mul_f32_e32 v160, v30, v160
	v_mul_f32_e32 v161, v30, v161
	v_mul_f32_e32 v162, v30, v162
	v_mul_f32_e32 v163, v30, v163
	ds_write_b128 v209, v[160:163] offset:4096
	v_mul_f32_e32 v164, v31, v164
	v_mul_f32_e32 v165, v31, v165
	v_mul_f32_e32 v166, v31, v166
	v_mul_f32_e32 v167, v31, v167
	ds_write_b128 v209, v[164:167] offset:5120
	v_mul_f32_e32 v168, v32, v168
	v_mul_f32_e32 v169, v32, v169
	v_mul_f32_e32 v170, v32, v170
	v_mul_f32_e32 v171, v32, v171
	ds_write_b128 v209, v[168:171] offset:6144
	v_mul_f32_e32 v172, v33, v172
	v_mul_f32_e32 v173, v33, v173
	v_mul_f32_e32 v174, v33, v174
	v_mul_f32_e32 v175, v33, v175
	ds_write_b128 v209, v[172:175] offset:7168
	s_waitcnt lgkmcnt(0)
	s_barrier
; #define GAS __attribute__((address_space(1)))
; #define LAS __attribute__((address_space(3)))
; #define LDS_WAIT() asm volatile("s_waitcnt lgkmcnt(0)" ::: "memory")
; __device__ __forceinline__ unsigned pk4_fp8(float a, float b, float c, float d) {
;     a = fminf(fmaxf(a, -448.f), 448.f); b = fminf(fmaxf(b, -448.f), 448.f); c = fminf(fmaxf(c, -448.f), 448.f); d = fminf(fmaxf(d, -448.f), 448.f);
;     int w = __builtin_amdgcn_cvt_pk_fp8_f32(a, b, 0, false); w = __builtin_amdgcn_cvt_pk_fp8_f32(c, d, w, true); return (unsigned)w; }
;     ...
;     for (int i = 0; i < 32; ++i) v[i] = sc >= 0 ? W[(size_t)(k0 + 2 * i + (lane >> 5)) * Nsrc + sc] : 0.f;
; #pragma unroll
;     for (int i = 0; i < 32; ++i) { const int k = k0 + 2 * i + (lane >> 5); float x = v[i] * wscale; if (KS) x *= (k < ksplit ? ksA[k] : ksB[k - ksplit]); scr[(2 * i + (lane >> 5)) * 33 + (lane & 31)] = x; }
;     LDS_WAIT(); asm volatile("" ::: "memory");
;     const int c = lane & 7;
; #pragma unroll
;     for (int j = 0; j < 4; ++j) { const int n = (lane >> 3) + 8 * j; const LAS float* s = scr + (8 * c) * 33 + n;
;         const unsigned long long o = (unsigned long long)pg8::pk4_fp8(s[0 * 33], s[1 * 33], s[2 * 33], s[3 * 33]) | ((unsigned long long)pg8::pk4_fp8(s[4 * 33], s[5 * 33], s[6 * 33], s[7 * 33]) << 32);
;         *(GAS unsigned long long*)(WT + (size_t)(n0 + n) * K + k0 + 8 * c) = o; }
;     LDS_WAIT(); asm volatile("" ::: "memory");
	s_add_u32 s8, s30, 0x2000
	s_addc_u32 s9, s31, 0
	global_load_dwordx4 v[144:147], v74, s[8:9]
	s_add_u32 s8, s8, 0x20000
	s_addc_u32 s9, s9, 0
	global_load_dwordx4 v[148:151], v74, s[8:9]
	s_add_u32 s8, s8, 0x20000
	s_addc_u32 s9, s9, 0
	global_load_dwordx4 v[152:155], v74, s[8:9]
	s_add_u32 s8, s8, 0x20000
	s_addc_u32 s9, s9, 0
	global_load_dwordx4 v[156:159], v74, s[8:9]
	s_add_u32 s8, s8, 0x20000
	s_addc_u32 s9, s9, 0
	global_load_dwordx4 v[160:163], v74, s[8:9]
	s_add_u32 s8, s8, 0x20000
	s_addc_u32 s9, s9, 0
	global_load_dwordx4 v[164:167], v74, s[8:9]
	s_add_u32 s8, s8, 0x20000
	s_addc_u32 s9, s9, 0
	global_load_dwordx4 v[168:171], v74, s[8:9]
	s_add_u32 s8, s8, 0x20000
	s_addc_u32 s9, s9, 0
	global_load_dwordx4 v[172:175], v74, s[8:9]
	s_mov_b64 s[6:7], s[32:33]
	ds_read_b32 v226, v211
	ds_read_b32 v227, v211 offset:512
	ds_read_b32 v228, v211 offset:1024
	ds_read_b32 v229, v211 offset:1536
	ds_read_b32 v230, v211 offset:2048
	ds_read_b32 v231, v211 offset:2560
	ds_read_b32 v232, v211 offset:3072
	ds_read_b32 v233, v211 offset:3584
	ds_read_b32 v234, v211 offset:4096
	ds_read_b32 v235, v211 offset:4608
	ds_read_b32 v236, v211 offset:5120
	ds_read_b32 v237, v211 offset:5632
	ds_read_b32 v238, v211 offset:6144
	ds_read_b32 v239, v211 offset:6656
	ds_read_b32 v240, v211 offset:7168
	ds_read_b32 v241, v211 offset:7680
	s_waitcnt lgkmcnt(0)
	v_max_f32_e32 v226, v226, v226
	v_max_f32_e32 v227, v227, v227
	v_max_f32_e32 v228, v228, v228
	v_max_f32_e32 v229, v229, v229
	v_max_f32_e32 v230, v230, v230
	v_max_f32_e32 v231, v231, v231
	v_max_f32_e32 v232, v232, v232
	v_max_f32_e32 v233, v233, v233
	v_max_f32_e32 v234, v234, v234
	v_max_f32_e32 v235, v235, v235
	v_max_f32_e32 v236, v236, v236
	v_max_f32_e32 v237, v237, v237
	v_max_f32_e32 v238, v238, v238
	v_max_f32_e32 v239, v239, v239
	v_max_f32_e32 v240, v240, v240
	v_max_f32_e32 v241, v241, v241
	v_med3_f32 v226, v226, s62, v95
	v_med3_f32 v227, v227, s62, v95
	v_med3_f32 v228, v228, s62, v95
	v_med3_f32 v229, v229, s62, v95
	v_med3_f32 v230, v230, s62, v95
	v_med3_f32 v231, v231, s62, v95
	v_med3_f32 v232, v232, s62, v95
	v_med3_f32 v233, v233, s62, v95
	v_med3_f32 v234, v234, s62, v95
	v_med3_f32 v235, v235, s62, v95
	v_med3_f32 v236, v236, s62, v95
	v_med3_f32 v237, v237, s62, v95
	v_med3_f32 v238, v238, s62, v95
	v_med3_f32 v239, v239, s62, v95
	v_med3_f32 v240, v240, s62, v95
	v_med3_f32 v241, v241, s62, v95
	v_mov_b32_e32 v242, 0
	v_mov_b32_e32 v243, 0
	v_mov_b32_e32 v244, 0
	v_mov_b32_e32 v245, 0
	v_cvt_pk_fp8_f32 v242, v226, v227
	v_cvt_pk_fp8_f32 v243, v230, v231
	v_cvt_pk_fp8_f32 v244, v234, v235
	v_cvt_pk_fp8_f32 v245, v238, v239
	v_cvt_pk_fp8_f32 v242, v228, v229 op_sel:[0,0,1]
	v_cvt_pk_fp8_f32 v243, v232, v233 op_sel:[0,0,1]
	v_cvt_pk_fp8_f32 v244, v236, v237 op_sel:[0,0,1]
	v_cvt_pk_fp8_f32 v245, v240, v241 op_sel:[0,0,1]
	s_nop 0
	global_store_dwordx4 v77, v[242:245], s[6:7]
	ds_read_b32 v226, v213
	ds_read_b32 v227, v213 offset:512
	ds_read_b32 v228, v213 offset:1024
	ds_read_b32 v229, v213 offset:1536
	ds_read_b32 v230, v213 offset:2048
	ds_read_b32 v231, v213 offset:2560
	ds_read_b32 v232, v213 offset:3072
	ds_read_b32 v233, v213 offset:3584
	ds_read_b32 v234, v213 offset:4096
	ds_read_b32 v235, v213 offset:4608
	ds_read_b32 v236, v213 offset:5120
	ds_read_b32 v237, v213 offset:5632
	ds_read_b32 v238, v213 offset:6144
	ds_read_b32 v239, v213 offset:6656
	ds_read_b32 v240, v213 offset:7168
	ds_read_b32 v241, v213 offset:7680
	s_waitcnt lgkmcnt(0)
	v_max_f32_e32 v226, v226, v226
	v_max_f32_e32 v227, v227, v227
	v_max_f32_e32 v228, v228, v228
	v_max_f32_e32 v229, v229, v229
	v_max_f32_e32 v230, v230, v230
	v_max_f32_e32 v231, v231, v231
	v_max_f32_e32 v232, v232, v232
	v_max_f32_e32 v233, v233, v233
	v_max_f32_e32 v234, v234, v234
	v_max_f32_e32 v235, v235, v235
	v_max_f32_e32 v236, v236, v236
	v_max_f32_e32 v237, v237, v237
	v_max_f32_e32 v238, v238, v238
	v_max_f32_e32 v239, v239, v239
	v_max_f32_e32 v240, v240, v240
	v_max_f32_e32 v241, v241, v241
	v_med3_f32 v226, v226, s62, v95
	v_med3_f32 v227, v227, s62, v95
	v_med3_f32 v228, v228, s62, v95
	v_med3_f32 v229, v229, s62, v95
	v_med3_f32 v230, v230, s62, v95
	v_med3_f32 v231, v231, s62, v95
	v_med3_f32 v232, v232, s62, v95
	v_med3_f32 v233, v233, s62, v95
	v_med3_f32 v234, v234, s62, v95
	v_med3_f32 v235, v235, s62, v95
	v_med3_f32 v236, v236, s62, v95
	v_med3_f32 v237, v237, s62, v95
	v_med3_f32 v238, v238, s62, v95
	v_med3_f32 v239, v239, s62, v95
	v_med3_f32 v240, v240, s62, v95
	v_med3_f32 v241, v241, s62, v95
	v_mov_b32_e32 v242, 0
	v_mov_b32_e32 v243, 0
	v_mov_b32_e32 v244, 0
	v_mov_b32_e32 v245, 0
	v_cvt_pk_fp8_f32 v242, v226, v227
	v_cvt_pk_fp8_f32 v243, v230, v231
	v_cvt_pk_fp8_f32 v244, v234, v235
	v_cvt_pk_fp8_f32 v245, v238, v239
	v_cvt_pk_fp8_f32 v242, v228, v229 op_sel:[0,0,1]
	v_cvt_pk_fp8_f32 v243, v232, v233 op_sel:[0,0,1]
	v_cvt_pk_fp8_f32 v244, v236, v237 op_sel:[0,0,1]
	v_cvt_pk_fp8_f32 v245, v240, v241 op_sel:[0,0,1]
	s_nop 0
	global_store_dwordx4 v78, v[242:245], s[6:7]
	s_waitcnt vmcnt(10)
	v_mul_f32_e32 v176, v26, v176
	v_mul_f32_e32 v177, v26, v177
	v_mul_f32_e32 v178, v26, v178
	v_mul_f32_e32 v179, v26, v179
	ds_write_b128 v210, v[176:179]
	v_mul_f32_e32 v180, v27, v180
	v_mul_f32_e32 v181, v27, v181
	v_mul_f32_e32 v182, v27, v182
	v_mul_f32_e32 v183, v27, v183
	ds_write_b128 v210, v[180:183] offset:1024
	v_mul_f32_e32 v184, v28, v184
	v_mul_f32_e32 v185, v28, v185
	v_mul_f32_e32 v186, v28, v186
	v_mul_f32_e32 v187, v28, v187
	ds_write_b128 v210, v[184:187] offset:2048
	v_mul_f32_e32 v188, v29, v188
	v_mul_f32_e32 v189, v29, v189
	v_mul_f32_e32 v190, v29, v190
	v_mul_f32_e32 v191, v29, v191
	ds_write_b128 v210, v[188:191] offset:3072
	v_mul_f32_e32 v192, v30, v192
	v_mul_f32_e32 v193, v30, v193
	v_mul_f32_e32 v194, v30, v194
	v_mul_f32_e32 v195, v30, v195
	ds_write_b128 v210, v[192:195] offset:4096
	v_mul_f32_e32 v196, v31, v196
	v_mul_f32_e32 v197, v31, v197
	v_mul_f32_e32 v198, v31, v198
	v_mul_f32_e32 v199, v31, v199
	ds_write_b128 v210, v[196:199] offset:5120
	v_mul_f32_e32 v200, v32, v200
	v_mul_f32_e32 v201, v32, v201
	v_mul_f32_e32 v202, v32, v202
	v_mul_f32_e32 v203, v32, v203
	ds_write_b128 v210, v[200:203] offset:6144
	v_mul_f32_e32 v204, v33, v204
	v_mul_f32_e32 v205, v33, v205
	v_mul_f32_e32 v206, v33, v206
	v_mul_f32_e32 v207, v33, v207
	ds_write_b128 v210, v[204:207] offset:7168
	s_waitcnt lgkmcnt(0)
	s_barrier
; #define GAS __attribute__((address_space(1)))
; #define LAS __attribute__((address_space(3)))
; #define LDS_WAIT() asm volatile("s_waitcnt lgkmcnt(0)" ::: "memory")
; __device__ __forceinline__ unsigned pk4_fp8(float a, float b, float c, float d) {
;     a = fminf(fmaxf(a, -448.f), 448.f); b = fminf(fmaxf(b, -448.f), 448.f); c = fminf(fmaxf(c, -448.f), 448.f); d = fminf(fmaxf(d, -448.f), 448.f);
;     int w = __builtin_amdgcn_cvt_pk_fp8_f32(a, b, 0, false); w = __builtin_amdgcn_cvt_pk_fp8_f32(c, d, w, true); return (unsigned)w; }
;     ...
;     for (int i = 0; i < 32; ++i) v[i] = sc >= 0 ? W[(size_t)(k0 + 2 * i + (lane >> 5)) * Nsrc + sc] : 0.f;
; #pragma unroll
;     for (int i = 0; i < 32; ++i) { const int k = k0 + 2 * i + (lane >> 5); float x = v[i] * wscale; if (KS) x *= (k < ksplit ? ksA[k] : ksB[k - ksplit]); scr[(2 * i + (lane >> 5)) * 33 + (lane & 31)] = x; }
;     LDS_WAIT(); asm volatile("" ::: "memory");
;     const int c = lane & 7;
; #pragma unroll
;     for (int j = 0; j < 4; ++j) { const int n = (lane >> 3) + 8 * j; const LAS float* s = scr + (8 * c) * 33 + n;
;         const unsigned long long o = (unsigned long long)pg8::pk4_fp8(s[0 * 33], s[1 * 33], s[2 * 33], s[3 * 33]) | ((unsigned long long)pg8::pk4_fp8(s[4 * 33], s[5 * 33], s[6 * 33], s[7 * 33]) << 32);
;         *(GAS unsigned long long*)(WT + (size_t)(n0 + n) * K + k0 + 8 * c) = o; }
;     LDS_WAIT(); asm volatile("" ::: "memory");
	s_add_u32 s8, s30, 0x3000
	s_addc_u32 s9, s31, 0
	global_load_dwordx4 v[176:179], v74, s[8:9]
	s_add_u32 s8, s8, 0x20000
	s_addc_u32 s9, s9, 0
	global_load_dwordx4 v[180:183], v74, s[8:9]
	s_add_u32 s8, s8, 0x20000
	s_addc_u32 s9, s9, 0
	global_load_dwordx4 v[184:187], v74, s[8:9]
	s_add_u32 s8, s8, 0x20000
	s_addc_u32 s9, s9, 0
	global_load_dwordx4 v[188:191], v74, s[8:9]
	s_add_u32 s8, s8, 0x20000
	s_addc_u32 s9, s9, 0
	global_load_dwordx4 v[192:195], v74, s[8:9]
	s_add_u32 s8, s8, 0x20000
	s_addc_u32 s9, s9, 0
	global_load_dwordx4 v[196:199], v74, s[8:9]
	s_add_u32 s8, s8, 0x20000
	s_addc_u32 s9, s9, 0
	global_load_dwordx4 v[200:203], v74, s[8:9]
	s_add_u32 s8, s8, 0x20000
	s_addc_u32 s9, s9, 0
	global_load_dwordx4 v[204:207], v74, s[8:9]
	s_add_u32 s6, s32, 0x400000
	s_addc_u32 s7, s33, 0
	ds_read_b32 v226, v212
	ds_read_b32 v227, v212 offset:512
	ds_read_b32 v228, v212 offset:1024
	ds_read_b32 v229, v212 offset:1536
	ds_read_b32 v230, v212 offset:2048
	ds_read_b32 v231, v212 offset:2560
	ds_read_b32 v232, v212 offset:3072
	ds_read_b32 v233, v212 offset:3584
	ds_read_b32 v234, v212 offset:4096
	ds_read_b32 v235, v212 offset:4608
	ds_read_b32 v236, v212 offset:5120
	ds_read_b32 v237, v212 offset:5632
	ds_read_b32 v238, v212 offset:6144
	ds_read_b32 v239, v212 offset:6656
	ds_read_b32 v240, v212 offset:7168
	ds_read_b32 v241, v212 offset:7680
	s_waitcnt lgkmcnt(0)
	v_max_f32_e32 v226, v226, v226
	v_max_f32_e32 v227, v227, v227
	v_max_f32_e32 v228, v228, v228
	v_max_f32_e32 v229, v229, v229
	v_max_f32_e32 v230, v230, v230
	v_max_f32_e32 v231, v231, v231
	v_max_f32_e32 v232, v232, v232
	v_max_f32_e32 v233, v233, v233
	v_max_f32_e32 v234, v234, v234
	v_max_f32_e32 v235, v235, v235
	v_max_f32_e32 v236, v236, v236
	v_max_f32_e32 v237, v237, v237
	v_max_f32_e32 v238, v238, v238
	v_max_f32_e32 v239, v239, v239
	v_max_f32_e32 v240, v240, v240
	v_max_f32_e32 v241, v241, v241
	v_med3_f32 v226, v226, s62, v95
	v_med3_f32 v227, v227, s62, v95
	v_med3_f32 v228, v228, s62, v95
	v_med3_f32 v229, v229, s62, v95
	v_med3_f32 v230, v230, s62, v95
	v_med3_f32 v231, v231, s62, v95
	v_med3_f32 v232, v232, s62, v95
	v_med3_f32 v233, v233, s62, v95
	v_med3_f32 v234, v234, s62, v95
	v_med3_f32 v235, v235, s62, v95
	v_med3_f32 v236, v236, s62, v95
	v_med3_f32 v237, v237, s62, v95
	v_med3_f32 v238, v238, s62, v95
	v_med3_f32 v239, v239, s62, v95
	v_med3_f32 v240, v240, s62, v95
	v_med3_f32 v241, v241, s62, v95
	v_mov_b32_e32 v242, 0
	v_mov_b32_e32 v243, 0
	v_mov_b32_e32 v244, 0
	v_mov_b32_e32 v245, 0
	v_cvt_pk_fp8_f32 v242, v226, v227
	v_cvt_pk_fp8_f32 v243, v230, v231
	v_cvt_pk_fp8_f32 v244, v234, v235
	v_cvt_pk_fp8_f32 v245, v238, v239
	v_cvt_pk_fp8_f32 v242, v228, v229 op_sel:[0,0,1]
	v_cvt_pk_fp8_f32 v243, v232, v233 op_sel:[0,0,1]
	v_cvt_pk_fp8_f32 v244, v236, v237 op_sel:[0,0,1]
	v_cvt_pk_fp8_f32 v245, v240, v241 op_sel:[0,0,1]
	s_nop 0
	global_store_dwordx4 v77, v[242:245], s[6:7]
	ds_read_b32 v226, v214
	ds_read_b32 v227, v214 offset:512
	ds_read_b32 v228, v214 offset:1024
	ds_read_b32 v229, v214 offset:1536
	ds_read_b32 v230, v214 offset:2048
	ds_read_b32 v231, v214 offset:2560
	ds_read_b32 v232, v214 offset:3072
	ds_read_b32 v233, v214 offset:3584
	ds_read_b32 v234, v214 offset:4096
	ds_read_b32 v235, v214 offset:4608
	ds_read_b32 v236, v214 offset:5120
	ds_read_b32 v237, v214 offset:5632
	ds_read_b32 v238, v214 offset:6144
	ds_read_b32 v239, v214 offset:6656
	ds_read_b32 v240, v214 offset:7168
	ds_read_b32 v241, v214 offset:7680
	s_waitcnt lgkmcnt(0)
	v_max_f32_e32 v226, v226, v226
	v_max_f32_e32 v227, v227, v227
	v_max_f32_e32 v228, v228, v228
	v_max_f32_e32 v229, v229, v229
	v_max_f32_e32 v230, v230, v230
	v_max_f32_e32 v231, v231, v231
	v_max_f32_e32 v232, v232, v232
	v_max_f32_e32 v233, v233, v233
	v_max_f32_e32 v234, v234, v234
	v_max_f32_e32 v235, v235, v235
	v_max_f32_e32 v236, v236, v236
	v_max_f32_e32 v237, v237, v237
	v_max_f32_e32 v238, v238, v238
	v_max_f32_e32 v239, v239, v239
	v_max_f32_e32 v240, v240, v240
	v_max_f32_e32 v241, v241, v241
	v_med3_f32 v226, v226, s62, v95
	v_med3_f32 v227, v227, s62, v95
	v_med3_f32 v228, v228, s62, v95
	v_med3_f32 v229, v229, s62, v95
	v_med3_f32 v230, v230, s62, v95
	v_med3_f32 v231, v231, s62, v95
	v_med3_f32 v232, v232, s62, v95
	v_med3_f32 v233, v233, s62, v95
	v_med3_f32 v234, v234, s62, v95
	v_med3_f32 v235, v235, s62, v95
	v_med3_f32 v236, v236, s62, v95
	v_med3_f32 v237, v237, s62, v95
	v_med3_f32 v238, v238, s62, v95
	v_med3_f32 v239, v239, s62, v95
	v_med3_f32 v240, v240, s62, v95
	v_med3_f32 v241, v241, s62, v95
	v_mov_b32_e32 v242, 0
	v_mov_b32_e32 v243, 0
	v_mov_b32_e32 v244, 0
	v_mov_b32_e32 v245, 0
	v_cvt_pk_fp8_f32 v242, v226, v227
	v_cvt_pk_fp8_f32 v243, v230, v231
	v_cvt_pk_fp8_f32 v244, v234, v235
	v_cvt_pk_fp8_f32 v245, v238, v239
	v_cvt_pk_fp8_f32 v242, v228, v229 op_sel:[0,0,1]
	v_cvt_pk_fp8_f32 v243, v232, v233 op_sel:[0,0,1]
	v_cvt_pk_fp8_f32 v244, v236, v237 op_sel:[0,0,1]
	v_cvt_pk_fp8_f32 v245, v240, v241 op_sel:[0,0,1]
	s_nop 0
	global_store_dwordx4 v78, v[242:245], s[6:7]
	s_waitcnt vmcnt(12)
	v_mul_f32_e32 v144, v26, v144
	v_mul_f32_e32 v145, v26, v145
	v_mul_f32_e32 v146, v26, v146
	v_mul_f32_e32 v147, v26, v147
	ds_write_b128 v209, v[144:147]
	v_mul_f32_e32 v148, v27, v148
	v_mul_f32_e32 v149, v27, v149
	v_mul_f32_e32 v150, v27, v150
	v_mul_f32_e32 v151, v27, v151
	ds_write_b128 v209, v[148:151] offset:1024
	v_mul_f32_e32 v152, v28, v152
	v_mul_f32_e32 v153, v28, v153
	v_mul_f32_e32 v154, v28, v154
	v_mul_f32_e32 v155, v28, v155
	ds_write_b128 v209, v[152:155] offset:2048
	v_mul_f32_e32 v156, v29, v156
	v_mul_f32_e32 v157, v29, v157
	v_mul_f32_e32 v158, v29, v158
	v_mul_f32_e32 v159, v29, v159
	ds_write_b128 v209, v[156:159] offset:3072
	v_mul_f32_e32 v160, v30, v160
	v_mul_f32_e32 v161, v30, v161
	v_mul_f32_e32 v162, v30, v162
	v_mul_f32_e32 v163, v30, v163
	ds_write_b128 v209, v[160:163] offset:4096
	v_mul_f32_e32 v164, v31, v164
	v_mul_f32_e32 v165, v31, v165
	v_mul_f32_e32 v166, v31, v166
	v_mul_f32_e32 v167, v31, v167
	ds_write_b128 v209, v[164:167] offset:5120
	v_mul_f32_e32 v168, v32, v168
	v_mul_f32_e32 v169, v32, v169
	v_mul_f32_e32 v170, v32, v170
	v_mul_f32_e32 v171, v32, v171
	ds_write_b128 v209, v[168:171] offset:6144
	v_mul_f32_e32 v172, v33, v172
	v_mul_f32_e32 v173, v33, v173
	v_mul_f32_e32 v174, v33, v174
	v_mul_f32_e32 v175, v33, v175
	ds_write_b128 v209, v[172:175] offset:7168
	s_waitcnt lgkmcnt(0)
	s_barrier
; #define GAS __attribute__((address_space(1)))
; #define LAS __attribute__((address_space(3)))
; #define LDS_WAIT() asm volatile("s_waitcnt lgkmcnt(0)" ::: "memory")
; __device__ __forceinline__ unsigned pk4_fp8(float a, float b, float c, float d) {
;     a = fminf(fmaxf(a, -448.f), 448.f); b = fminf(fmaxf(b, -448.f), 448.f); c = fminf(fmaxf(c, -448.f), 448.f); d = fminf(fmaxf(d, -448.f), 448.f);
;     int w = __builtin_amdgcn_cvt_pk_fp8_f32(a, b, 0, false); w = __builtin_amdgcn_cvt_pk_fp8_f32(c, d, w, true); return (unsigned)w; }
;     ...
;     for (int i = 0; i < 32; ++i) v[i] = sc >= 0 ? W[(size_t)(k0 + 2 * i + (lane >> 5)) * Nsrc + sc] : 0.f;
; #pragma unroll
;     for (int i = 0; i < 32; ++i) { const int k = k0 + 2 * i + (lane >> 5); float x = v[i] * wscale; if (KS) x *= (k < ksplit ? ksA[k] : ksB[k - ksplit]); scr[(2 * i + (lane >> 5)) * 33 + (lane & 31)] = x; }
;     LDS_WAIT(); asm volatile("" ::: "memory");
;     const int c = lane & 7;
; #pragma unroll
;     for (int j = 0; j < 4; ++j) { const int n = (lane >> 3) + 8 * j; const LAS float* s = scr + (8 * c) * 33 + n;
;         const unsigned long long o = (unsigned long long)pg8::pk4_fp8(s[0 * 33], s[1 * 33], s[2 * 33], s[3 * 33]) | ((unsigned long long)pg8::pk4_fp8(s[4 * 33], s[5 * 33], s[6 * 33], s[7 * 33]) << 32);
;         *(GAS unsigned long long*)(WT + (size_t)(n0 + n) * K + k0 + 8 * c) = o; }
;     LDS_WAIT(); asm volatile("" ::: "memory");
	s_add_u32 s8, s30, 0x4000
	s_addc_u32 s9, s31, 0
	global_load_dwordx4 v[144:147], v74, s[8:9]
	s_add_u32 s8, s8, 0x20000
	s_addc_u32 s9, s9, 0
	global_load_dwordx4 v[148:151], v74, s[8:9]
	s_add_u32 s8, s8, 0x20000
	s_addc_u32 s9, s9, 0
	global_load_dwordx4 v[152:155], v74, s[8:9]
	s_add_u32 s8, s8, 0x20000
	s_addc_u32 s9, s9, 0
	global_load_dwordx4 v[156:159], v74, s[8:9]
	s_add_u32 s8, s8, 0x20000
	s_addc_u32 s9, s9, 0
	global_load_dwordx4 v[160:163], v74, s[8:9]
	s_add_u32 s8, s8, 0x20000
	s_addc_u32 s9, s9, 0
	global_load_dwordx4 v[164:167], v74, s[8:9]
	s_add_u32 s8, s8, 0x20000
	s_addc_u32 s9, s9, 0
	global_load_dwordx4 v[168:171], v74, s[8:9]
	s_add_u32 s8, s8, 0x20000
	s_addc_u32 s9, s9, 0
	global_load_dwordx4 v[172:175], v74, s[8:9]
	s_add_u32 s6, s32, 0x800000
	s_addc_u32 s7, s33, 0
	ds_read_b32 v226, v211
	ds_read_b32 v227, v211 offset:512
	ds_read_b32 v228, v211 offset:1024
	ds_read_b32 v229, v211 offset:1536
	ds_read_b32 v230, v211 offset:2048
	ds_read_b32 v231, v211 offset:2560
	ds_read_b32 v232, v211 offset:3072
	ds_read_b32 v233, v211 offset:3584
	ds_read_b32 v234, v211 offset:4096
	ds_read_b32 v235, v211 offset:4608
	ds_read_b32 v236, v211 offset:5120
	ds_read_b32 v237, v211 offset:5632
	ds_read_b32 v238, v211 offset:6144
	ds_read_b32 v239, v211 offset:6656
	ds_read_b32 v240, v211 offset:7168
	ds_read_b32 v241, v211 offset:7680
	s_waitcnt lgkmcnt(0)
	v_max_f32_e32 v226, v226, v226
	v_max_f32_e32 v227, v227, v227
	v_max_f32_e32 v228, v228, v228
	v_max_f32_e32 v229, v229, v229
	v_max_f32_e32 v230, v230, v230
	v_max_f32_e32 v231, v231, v231
	v_max_f32_e32 v232, v232, v232
	v_max_f32_e32 v233, v233, v233
	v_max_f32_e32 v234, v234, v234
	v_max_f32_e32 v235, v235, v235
	v_max_f32_e32 v236, v236, v236
	v_max_f32_e32 v237, v237, v237
	v_max_f32_e32 v238, v238, v238
	v_max_f32_e32 v239, v239, v239
	v_max_f32_e32 v240, v240, v240
	v_max_f32_e32 v241, v241, v241
	v_med3_f32 v226, v226, s62, v95
	v_med3_f32 v227, v227, s62, v95
	v_med3_f32 v228, v228, s62, v95
	v_med3_f32 v229, v229, s62, v95
	v_med3_f32 v230, v230, s62, v95
	v_med3_f32 v231, v231, s62, v95
	v_med3_f32 v232, v232, s62, v95
	v_med3_f32 v233, v233, s62, v95
	v_med3_f32 v234, v234, s62, v95
	v_med3_f32 v235, v235, s62, v95
	v_med3_f32 v236, v236, s62, v95
	v_med3_f32 v237, v237, s62, v95
	v_med3_f32 v238, v238, s62, v95
	v_med3_f32 v239, v239, s62, v95
	v_med3_f32 v240, v240, s62, v95
	v_med3_f32 v241, v241, s62, v95
	v_mov_b32_e32 v242, 0
	v_mov_b32_e32 v243, 0
	v_mov_b32_e32 v244, 0
	v_mov_b32_e32 v245, 0
	v_cvt_pk_fp8_f32 v242, v226, v227
	v_cvt_pk_fp8_f32 v243, v230, v231
	v_cvt_pk_fp8_f32 v244, v234, v235
	v_cvt_pk_fp8_f32 v245, v238, v239
	v_cvt_pk_fp8_f32 v242, v228, v229 op_sel:[0,0,1]
	v_cvt_pk_fp8_f32 v243, v232, v233 op_sel:[0,0,1]
	v_cvt_pk_fp8_f32 v244, v236, v237 op_sel:[0,0,1]
	v_cvt_pk_fp8_f32 v245, v240, v241 op_sel:[0,0,1]
	s_nop 0
	global_store_dwordx4 v77, v[242:245], s[6:7]
	ds_read_b32 v226, v213
	ds_read_b32 v227, v213 offset:512
	ds_read_b32 v228, v213 offset:1024
	ds_read_b32 v229, v213 offset:1536
	ds_read_b32 v230, v213 offset:2048
	ds_read_b32 v231, v213 offset:2560
	ds_read_b32 v232, v213 offset:3072
	ds_read_b32 v233, v213 offset:3584
	ds_read_b32 v234, v213 offset:4096
	ds_read_b32 v235, v213 offset:4608
	ds_read_b32 v236, v213 offset:5120
	ds_read_b32 v237, v213 offset:5632
	ds_read_b32 v238, v213 offset:6144
	ds_read_b32 v239, v213 offset:6656
	ds_read_b32 v240, v213 offset:7168
	ds_read_b32 v241, v213 offset:7680
	s_waitcnt lgkmcnt(0)
	v_max_f32_e32 v226, v226, v226
	v_max_f32_e32 v227, v227, v227
	v_max_f32_e32 v228, v228, v228
	v_max_f32_e32 v229, v229, v229
	v_max_f32_e32 v230, v230, v230
	v_max_f32_e32 v231, v231, v231
	v_max_f32_e32 v232, v232, v232
	v_max_f32_e32 v233, v233, v233
	v_max_f32_e32 v234, v234, v234
	v_max_f32_e32 v235, v235, v235
	v_max_f32_e32 v236, v236, v236
	v_max_f32_e32 v237, v237, v237
	v_max_f32_e32 v238, v238, v238
	v_max_f32_e32 v239, v239, v239
	v_max_f32_e32 v240, v240, v240
	v_max_f32_e32 v241, v241, v241
	v_med3_f32 v226, v226, s62, v95
	v_med3_f32 v227, v227, s62, v95
	v_med3_f32 v228, v228, s62, v95
	v_med3_f32 v229, v229, s62, v95
	v_med3_f32 v230, v230, s62, v95
	v_med3_f32 v231, v231, s62, v95
	v_med3_f32 v232, v232, s62, v95
	v_med3_f32 v233, v233, s62, v95
	v_med3_f32 v234, v234, s62, v95
	v_med3_f32 v235, v235, s62, v95
	v_med3_f32 v236, v236, s62, v95
	v_med3_f32 v237, v237, s62, v95
	v_med3_f32 v238, v238, s62, v95
	v_med3_f32 v239, v239, s62, v95
	v_med3_f32 v240, v240, s62, v95
	v_med3_f32 v241, v241, s62, v95
	v_mov_b32_e32 v242, 0
	v_mov_b32_e32 v243, 0
	v_mov_b32_e32 v244, 0
	v_mov_b32_e32 v245, 0
	v_cvt_pk_fp8_f32 v242, v226, v227
	v_cvt_pk_fp8_f32 v243, v230, v231
	v_cvt_pk_fp8_f32 v244, v234, v235
	v_cvt_pk_fp8_f32 v245, v238, v239
	v_cvt_pk_fp8_f32 v242, v228, v229 op_sel:[0,0,1]
	v_cvt_pk_fp8_f32 v243, v232, v233 op_sel:[0,0,1]
	v_cvt_pk_fp8_f32 v244, v236, v237 op_sel:[0,0,1]
	v_cvt_pk_fp8_f32 v245, v240, v241 op_sel:[0,0,1]
	s_nop 0
	global_store_dwordx4 v78, v[242:245], s[6:7]
	s_waitcnt vmcnt(12)
	v_mul_f32_e32 v176, v26, v176
	v_mul_f32_e32 v177, v26, v177
	v_mul_f32_e32 v178, v26, v178
	v_mul_f32_e32 v179, v26, v179
	ds_write_b128 v210, v[176:179]
	v_mul_f32_e32 v180, v27, v180
	v_mul_f32_e32 v181, v27, v181
	v_mul_f32_e32 v182, v27, v182
	v_mul_f32_e32 v183, v27, v183
	ds_write_b128 v210, v[180:183] offset:1024
	v_mul_f32_e32 v184, v28, v184
	v_mul_f32_e32 v185, v28, v185
	v_mul_f32_e32 v186, v28, v186
	v_mul_f32_e32 v187, v28, v187
	ds_write_b128 v210, v[184:187] offset:2048
	v_mul_f32_e32 v188, v29, v188
	v_mul_f32_e32 v189, v29, v189
	v_mul_f32_e32 v190, v29, v190
	v_mul_f32_e32 v191, v29, v191
	ds_write_b128 v210, v[188:191] offset:3072
	v_mul_f32_e32 v192, v30, v192
	v_mul_f32_e32 v193, v30, v193
	v_mul_f32_e32 v194, v30, v194
	v_mul_f32_e32 v195, v30, v195
	ds_write_b128 v210, v[192:195] offset:4096
	v_mul_f32_e32 v196, v31, v196
	v_mul_f32_e32 v197, v31, v197
	v_mul_f32_e32 v198, v31, v198
	v_mul_f32_e32 v199, v31, v199
	ds_write_b128 v210, v[196:199] offset:5120
	v_mul_f32_e32 v200, v32, v200
	v_mul_f32_e32 v201, v32, v201
	v_mul_f32_e32 v202, v32, v202
	v_mul_f32_e32 v203, v32, v203
	ds_write_b128 v210, v[200:203] offset:6144
	v_mul_f32_e32 v204, v33, v204
	v_mul_f32_e32 v205, v33, v205
	v_mul_f32_e32 v206, v33, v206
	v_mul_f32_e32 v207, v33, v207
	ds_write_b128 v210, v[204:207] offset:7168
	s_waitcnt lgkmcnt(0)
	s_barrier
; #define GAS __attribute__((address_space(1)))
; #define LAS __attribute__((address_space(3)))
; #define LDS_WAIT() asm volatile("s_waitcnt lgkmcnt(0)" ::: "memory")
; __device__ __forceinline__ unsigned pk4_fp8(float a, float b, float c, float d) {
;     a = fminf(fmaxf(a, -448.f), 448.f); b = fminf(fmaxf(b, -448.f), 448.f); c = fminf(fmaxf(c, -448.f), 448.f); d = fminf(fmaxf(d, -448.f), 448.f);
;     int w = __builtin_amdgcn_cvt_pk_fp8_f32(a, b, 0, false); w = __builtin_amdgcn_cvt_pk_fp8_f32(c, d, w, true); return (unsigned)w; }
;     ...
;     for (int i = 0; i < 32; ++i) v[i] = sc >= 0 ? W[(size_t)(k0 + 2 * i + (lane >> 5)) * Nsrc + sc] : 0.f;
; #pragma unroll
;     for (int i = 0; i < 32; ++i) { const int k = k0 + 2 * i + (lane >> 5); float x = v[i] * wscale; if (KS) x *= (k < ksplit ? ksA[k] : ksB[k - ksplit]); scr[(2 * i + (lane >> 5)) * 33 + (lane & 31)] = x; }
;     LDS_WAIT(); asm volatile("" ::: "memory");
;     const int c = lane & 7;
; #pragma unroll
;     for (int j = 0; j < 4; ++j) { const int n = (lane >> 3) + 8 * j; const LAS float* s = scr + (8 * c) * 33 + n;
;         const unsigned long long o = (unsigned long long)pg8::pk4_fp8(s[0 * 33], s[1 * 33], s[2 * 33], s[3 * 33]) | ((unsigned long long)pg8::pk4_fp8(s[4 * 33], s[5 * 33], s[6 * 33], s[7 * 33]) << 32);
;         *(GAS unsigned long long*)(WT + (size_t)(n0 + n) * K + k0 + 8 * c) = o; }
;     LDS_WAIT(); asm volatile("" ::: "memory");
	s_add_u32 s8, s30, 0x5000
	s_addc_u32 s9, s31, 0
	global_load_dwordx4 v[176:179], v74, s[8:9]
	s_add_u32 s8, s8, 0x20000
	s_addc_u32 s9, s9, 0
	global_load_dwordx4 v[180:183], v74, s[8:9]
	s_add_u32 s8, s8, 0x20000
	s_addc_u32 s9, s9, 0
	global_load_dwordx4 v[184:187], v74, s[8:9]
	s_add_u32 s8, s8, 0x20000
	s_addc_u32 s9, s9, 0
	global_load_dwordx4 v[188:191], v74, s[8:9]
	s_add_u32 s8, s8, 0x20000
	s_addc_u32 s9, s9, 0
	global_load_dwordx4 v[192:195], v74, s[8:9]
	s_add_u32 s8, s8, 0x20000
	s_addc_u32 s9, s9, 0
	global_load_dwordx4 v[196:199], v74, s[8:9]
	s_add_u32 s8, s8, 0x20000
	s_addc_u32 s9, s9, 0
	global_load_dwordx4 v[200:203], v74, s[8:9]
	s_add_u32 s8, s8, 0x20000
	s_addc_u32 s9, s9, 0
	global_load_dwordx4 v[204:207], v74, s[8:9]
	s_add_u32 s6, s32, 0xc00000
	s_addc_u32 s7, s33, 0
	ds_read_b32 v226, v212
	ds_read_b32 v227, v212 offset:512
	ds_read_b32 v228, v212 offset:1024
	ds_read_b32 v229, v212 offset:1536
	ds_read_b32 v230, v212 offset:2048
	ds_read_b32 v231, v212 offset:2560
	ds_read_b32 v232, v212 offset:3072
	ds_read_b32 v233, v212 offset:3584
	ds_read_b32 v234, v212 offset:4096
	ds_read_b32 v235, v212 offset:4608
	ds_read_b32 v236, v212 offset:5120
	ds_read_b32 v237, v212 offset:5632
	ds_read_b32 v238, v212 offset:6144
	ds_read_b32 v239, v212 offset:6656
	ds_read_b32 v240, v212 offset:7168
	ds_read_b32 v241, v212 offset:7680
	s_waitcnt lgkmcnt(0)
	v_max_f32_e32 v226, v226, v226
	v_max_f32_e32 v227, v227, v227
	v_max_f32_e32 v228, v228, v228
	v_max_f32_e32 v229, v229, v229
	v_max_f32_e32 v230, v230, v230
	v_max_f32_e32 v231, v231, v231
	v_max_f32_e32 v232, v232, v232
	v_max_f32_e32 v233, v233, v233
	v_max_f32_e32 v234, v234, v234
	v_max_f32_e32 v235, v235, v235
	v_max_f32_e32 v236, v236, v236
	v_max_f32_e32 v237, v237, v237
	v_max_f32_e32 v238, v238, v238
	v_max_f32_e32 v239, v239, v239
	v_max_f32_e32 v240, v240, v240
	v_max_f32_e32 v241, v241, v241
	v_med3_f32 v226, v226, s62, v95
	v_med3_f32 v227, v227, s62, v95
	v_med3_f32 v228, v228, s62, v95
	v_med3_f32 v229, v229, s62, v95
	v_med3_f32 v230, v230, s62, v95
	v_med3_f32 v231, v231, s62, v95
	v_med3_f32 v232, v232, s62, v95
	v_med3_f32 v233, v233, s62, v95
	v_med3_f32 v234, v234, s62, v95
	v_med3_f32 v235, v235, s62, v95
	v_med3_f32 v236, v236, s62, v95
	v_med3_f32 v237, v237, s62, v95
	v_med3_f32 v238, v238, s62, v95
	v_med3_f32 v239, v239, s62, v95
	v_med3_f32 v240, v240, s62, v95
	v_med3_f32 v241, v241, s62, v95
	v_mov_b32_e32 v242, 0
	v_mov_b32_e32 v243, 0
	v_mov_b32_e32 v244, 0
	v_mov_b32_e32 v245, 0
	v_cvt_pk_fp8_f32 v242, v226, v227
	v_cvt_pk_fp8_f32 v243, v230, v231
	v_cvt_pk_fp8_f32 v244, v234, v235
	v_cvt_pk_fp8_f32 v245, v238, v239
	v_cvt_pk_fp8_f32 v242, v228, v229 op_sel:[0,0,1]
	v_cvt_pk_fp8_f32 v243, v232, v233 op_sel:[0,0,1]
	v_cvt_pk_fp8_f32 v244, v236, v237 op_sel:[0,0,1]
	v_cvt_pk_fp8_f32 v245, v240, v241 op_sel:[0,0,1]
	s_nop 0
	global_store_dwordx4 v77, v[242:245], s[6:7]
	ds_read_b32 v226, v214
	ds_read_b32 v227, v214 offset:512
	ds_read_b32 v228, v214 offset:1024
	ds_read_b32 v229, v214 offset:1536
	ds_read_b32 v230, v214 offset:2048
	ds_read_b32 v231, v214 offset:2560
	ds_read_b32 v232, v214 offset:3072
	ds_read_b32 v233, v214 offset:3584
	ds_read_b32 v234, v214 offset:4096
	ds_read_b32 v235, v214 offset:4608
	ds_read_b32 v236, v214 offset:5120
	ds_read_b32 v237, v214 offset:5632
	ds_read_b32 v238, v214 offset:6144
	ds_read_b32 v239, v214 offset:6656
	ds_read_b32 v240, v214 offset:7168
	ds_read_b32 v241, v214 offset:7680
	s_waitcnt lgkmcnt(0)
	v_max_f32_e32 v226, v226, v226
	v_max_f32_e32 v227, v227, v227
	v_max_f32_e32 v228, v228, v228
	v_max_f32_e32 v229, v229, v229
	v_max_f32_e32 v230, v230, v230
	v_max_f32_e32 v231, v231, v231
	v_max_f32_e32 v232, v232, v232
	v_max_f32_e32 v233, v233, v233
	v_max_f32_e32 v234, v234, v234
	v_max_f32_e32 v235, v235, v235
	v_max_f32_e32 v236, v236, v236
	v_max_f32_e32 v237, v237, v237
	v_max_f32_e32 v238, v238, v238
	v_max_f32_e32 v239, v239, v239
	v_max_f32_e32 v240, v240, v240
	v_max_f32_e32 v241, v241, v241
	v_med3_f32 v226, v226, s62, v95
	v_med3_f32 v227, v227, s62, v95
	v_med3_f32 v228, v228, s62, v95
	v_med3_f32 v229, v229, s62, v95
	v_med3_f32 v230, v230, s62, v95
	v_med3_f32 v231, v231, s62, v95
	v_med3_f32 v232, v232, s62, v95
	v_med3_f32 v233, v233, s62, v95
	v_med3_f32 v234, v234, s62, v95
	v_med3_f32 v235, v235, s62, v95
	v_med3_f32 v236, v236, s62, v95
	v_med3_f32 v237, v237, s62, v95
	v_med3_f32 v238, v238, s62, v95
	v_med3_f32 v239, v239, s62, v95
	v_med3_f32 v240, v240, s62, v95
	v_med3_f32 v241, v241, s62, v95
	v_mov_b32_e32 v242, 0
	v_mov_b32_e32 v243, 0
	v_mov_b32_e32 v244, 0
	v_mov_b32_e32 v245, 0
	v_cvt_pk_fp8_f32 v242, v226, v227
	v_cvt_pk_fp8_f32 v243, v230, v231
	v_cvt_pk_fp8_f32 v244, v234, v235
	v_cvt_pk_fp8_f32 v245, v238, v239
	v_cvt_pk_fp8_f32 v242, v228, v229 op_sel:[0,0,1]
	v_cvt_pk_fp8_f32 v243, v232, v233 op_sel:[0,0,1]
	v_cvt_pk_fp8_f32 v244, v236, v237 op_sel:[0,0,1]
	v_cvt_pk_fp8_f32 v245, v240, v241 op_sel:[0,0,1]
	s_nop 0
	global_store_dwordx4 v78, v[242:245], s[6:7]
	s_waitcnt vmcnt(12)
	v_mul_f32_e32 v144, v26, v144
	v_mul_f32_e32 v145, v26, v145
	v_mul_f32_e32 v146, v26, v146
	v_mul_f32_e32 v147, v26, v147
	ds_write_b128 v209, v[144:147]
	v_mul_f32_e32 v148, v27, v148
	v_mul_f32_e32 v149, v27, v149
	v_mul_f32_e32 v150, v27, v150
	v_mul_f32_e32 v151, v27, v151
	ds_write_b128 v209, v[148:151] offset:1024
	v_mul_f32_e32 v152, v28, v152
	v_mul_f32_e32 v153, v28, v153
	v_mul_f32_e32 v154, v28, v154
	v_mul_f32_e32 v155, v28, v155
	ds_write_b128 v209, v[152:155] offset:2048
	v_mul_f32_e32 v156, v29, v156
	v_mul_f32_e32 v157, v29, v157
	v_mul_f32_e32 v158, v29, v158
	v_mul_f32_e32 v159, v29, v159
	ds_write_b128 v209, v[156:159] offset:3072
	v_mul_f32_e32 v160, v30, v160
	v_mul_f32_e32 v161, v30, v161
	v_mul_f32_e32 v162, v30, v162
	v_mul_f32_e32 v163, v30, v163
	ds_write_b128 v209, v[160:163] offset:4096
	v_mul_f32_e32 v164, v31, v164
	v_mul_f32_e32 v165, v31, v165
	v_mul_f32_e32 v166, v31, v166
	v_mul_f32_e32 v167, v31, v167
	ds_write_b128 v209, v[164:167] offset:5120
	v_mul_f32_e32 v168, v32, v168
	v_mul_f32_e32 v169, v32, v169
	v_mul_f32_e32 v170, v32, v170
	v_mul_f32_e32 v171, v32, v171
	ds_write_b128 v209, v[168:171] offset:6144
	v_mul_f32_e32 v172, v33, v172
	v_mul_f32_e32 v173, v33, v173
	v_mul_f32_e32 v174, v33, v174
	v_mul_f32_e32 v175, v33, v175
	ds_write_b128 v209, v[172:175] offset:7168
	s_waitcnt lgkmcnt(0)
	s_barrier
; #define GAS __attribute__((address_space(1)))
; #define LAS __attribute__((address_space(3)))
; #define LDS_WAIT() asm volatile("s_waitcnt lgkmcnt(0)" ::: "memory")
; __device__ __forceinline__ unsigned pk4_fp8(float a, float b, float c, float d) {
;     a = fminf(fmaxf(a, -448.f), 448.f); b = fminf(fmaxf(b, -448.f), 448.f); c = fminf(fmaxf(c, -448.f), 448.f); d = fminf(fmaxf(d, -448.f), 448.f);
;     int w = __builtin_amdgcn_cvt_pk_fp8_f32(a, b, 0, false); w = __builtin_amdgcn_cvt_pk_fp8_f32(c, d, w, true); return (unsigned)w; }
;     ...
;     for (int i = 0; i < 32; ++i) v[i] = sc >= 0 ? W[(size_t)(k0 + 2 * i + (lane >> 5)) * Nsrc + sc] : 0.f;
; #pragma unroll
;     for (int i = 0; i < 32; ++i) { const int k = k0 + 2 * i + (lane >> 5); float x = v[i] * wscale; if (KS) x *= (k < ksplit ? ksA[k] : ksB[k - ksplit]); scr[(2 * i + (lane >> 5)) * 33 + (lane & 31)] = x; }
;     LDS_WAIT(); asm volatile("" ::: "memory");
;     const int c = lane & 7;
; #pragma unroll
;     for (int j = 0; j < 4; ++j) { const int n = (lane >> 3) + 8 * j; const LAS float* s = scr + (8 * c) * 33 + n;
;         const unsigned long long o = (unsigned long long)pg8::pk4_fp8(s[0 * 33], s[1 * 33], s[2 * 33], s[3 * 33]) | ((unsigned long long)pg8::pk4_fp8(s[4 * 33], s[5 * 33], s[6 * 33], s[7 * 33]) << 32);
;         *(GAS unsigned long long*)(WT + (size_t)(n0 + n) * K + k0 + 8 * c) = o; }
;     LDS_WAIT(); asm volatile("" ::: "memory");
	s_add_u32 s8, s30, 0x6000
	s_addc_u32 s9, s31, 0
	global_load_dwordx4 v[144:147], v74, s[8:9]
	s_add_u32 s8, s8, 0x20000
	s_addc_u32 s9, s9, 0
	global_load_dwordx4 v[148:151], v74, s[8:9]
	s_add_u32 s8, s8, 0x20000
	s_addc_u32 s9, s9, 0
	global_load_dwordx4 v[152:155], v74, s[8:9]
	s_add_u32 s8, s8, 0x20000
	s_addc_u32 s9, s9, 0
	global_load_dwordx4 v[156:159], v74, s[8:9]
	s_add_u32 s8, s8, 0x20000
	s_addc_u32 s9, s9, 0
	global_load_dwordx4 v[160:163], v74, s[8:9]
	s_add_u32 s8, s8, 0x20000
	s_addc_u32 s9, s9, 0
	global_load_dwordx4 v[164:167], v74, s[8:9]
	s_add_u32 s8, s8, 0x20000
	s_addc_u32 s9, s9, 0
	global_load_dwordx4 v[168:171], v74, s[8:9]
	s_add_u32 s8, s8, 0x20000
	s_addc_u32 s9, s9, 0
	global_load_dwordx4 v[172:175], v74, s[8:9]
	s_add_u32 s6, s32, 0x1000000
	s_addc_u32 s7, s33, 0
	ds_read_b32 v226, v211
	ds_read_b32 v227, v211 offset:512
	ds_read_b32 v228, v211 offset:1024
	ds_read_b32 v229, v211 offset:1536
	ds_read_b32 v230, v211 offset:2048
	ds_read_b32 v231, v211 offset:2560
	ds_read_b32 v232, v211 offset:3072
	ds_read_b32 v233, v211 offset:3584
	ds_read_b32 v234, v211 offset:4096
	ds_read_b32 v235, v211 offset:4608
	ds_read_b32 v236, v211 offset:5120
	ds_read_b32 v237, v211 offset:5632
	ds_read_b32 v238, v211 offset:6144
	ds_read_b32 v239, v211 offset:6656
	ds_read_b32 v240, v211 offset:7168
	ds_read_b32 v241, v211 offset:7680
	s_waitcnt lgkmcnt(0)
	v_max_f32_e32 v226, v226, v226
	v_max_f32_e32 v227, v227, v227
	v_max_f32_e32 v228, v228, v228
	v_max_f32_e32 v229, v229, v229
	v_max_f32_e32 v230, v230, v230
	v_max_f32_e32 v231, v231, v231
	v_max_f32_e32 v232, v232, v232
	v_max_f32_e32 v233, v233, v233
	v_max_f32_e32 v234, v234, v234
	v_max_f32_e32 v235, v235, v235
	v_max_f32_e32 v236, v236, v236
	v_max_f32_e32 v237, v237, v237
	v_max_f32_e32 v238, v238, v238
	v_max_f32_e32 v239, v239, v239
	v_max_f32_e32 v240, v240, v240
	v_max_f32_e32 v241, v241, v241
	v_med3_f32 v226, v226, s62, v95
	v_med3_f32 v227, v227, s62, v95
	v_med3_f32 v228, v228, s62, v95
	v_med3_f32 v229, v229, s62, v95
	v_med3_f32 v230, v230, s62, v95
	v_med3_f32 v231, v231, s62, v95
	v_med3_f32 v232, v232, s62, v95
	v_med3_f32 v233, v233, s62, v95
	v_med3_f32 v234, v234, s62, v95
	v_med3_f32 v235, v235, s62, v95
	v_med3_f32 v236, v236, s62, v95
	v_med3_f32 v237, v237, s62, v95
	v_med3_f32 v238, v238, s62, v95
	v_med3_f32 v239, v239, s62, v95
	v_med3_f32 v240, v240, s62, v95
	v_med3_f32 v241, v241, s62, v95
	v_mov_b32_e32 v242, 0
	v_mov_b32_e32 v243, 0
	v_mov_b32_e32 v244, 0
	v_mov_b32_e32 v245, 0
	v_cvt_pk_fp8_f32 v242, v226, v227
	v_cvt_pk_fp8_f32 v243, v230, v231
	v_cvt_pk_fp8_f32 v244, v234, v235
	v_cvt_pk_fp8_f32 v245, v238, v239
	v_cvt_pk_fp8_f32 v242, v228, v229 op_sel:[0,0,1]
	v_cvt_pk_fp8_f32 v243, v232, v233 op_sel:[0,0,1]
	v_cvt_pk_fp8_f32 v244, v236, v237 op_sel:[0,0,1]
	v_cvt_pk_fp8_f32 v245, v240, v241 op_sel:[0,0,1]
	s_nop 0
	global_store_dwordx4 v77, v[242:245], s[6:7]
	ds_read_b32 v226, v213
	ds_read_b32 v227, v213 offset:512
	ds_read_b32 v228, v213 offset:1024
	ds_read_b32 v229, v213 offset:1536
	ds_read_b32 v230, v213 offset:2048
	ds_read_b32 v231, v213 offset:2560
	ds_read_b32 v232, v213 offset:3072
	ds_read_b32 v233, v213 offset:3584
	ds_read_b32 v234, v213 offset:4096
	ds_read_b32 v235, v213 offset:4608
	ds_read_b32 v236, v213 offset:5120
	ds_read_b32 v237, v213 offset:5632
	ds_read_b32 v238, v213 offset:6144
	ds_read_b32 v239, v213 offset:6656
	ds_read_b32 v240, v213 offset:7168
	ds_read_b32 v241, v213 offset:7680
	s_waitcnt lgkmcnt(0)
	v_max_f32_e32 v226, v226, v226
	v_max_f32_e32 v227, v227, v227
	v_max_f32_e32 v228, v228, v228
	v_max_f32_e32 v229, v229, v229
	v_max_f32_e32 v230, v230, v230
	v_max_f32_e32 v231, v231, v231
	v_max_f32_e32 v232, v232, v232
	v_max_f32_e32 v233, v233, v233
	v_max_f32_e32 v234, v234, v234
	v_max_f32_e32 v235, v235, v235
	v_max_f32_e32 v236, v236, v236
	v_max_f32_e32 v237, v237, v237
	v_max_f32_e32 v238, v238, v238
	v_max_f32_e32 v239, v239, v239
	v_max_f32_e32 v240, v240, v240
	v_max_f32_e32 v241, v241, v241
	v_med3_f32 v226, v226, s62, v95
	v_med3_f32 v227, v227, s62, v95
	v_med3_f32 v228, v228, s62, v95
	v_med3_f32 v229, v229, s62, v95
	v_med3_f32 v230, v230, s62, v95
	v_med3_f32 v231, v231, s62, v95
	v_med3_f32 v232, v232, s62, v95
	v_med3_f32 v233, v233, s62, v95
	v_med3_f32 v234, v234, s62, v95
	v_med3_f32 v235, v235, s62, v95
	v_med3_f32 v236, v236, s62, v95
	v_med3_f32 v237, v237, s62, v95
	v_med3_f32 v238, v238, s62, v95
	v_med3_f32 v239, v239, s62, v95
	v_med3_f32 v240, v240, s62, v95
	v_med3_f32 v241, v241, s62, v95
	v_mov_b32_e32 v242, 0
	v_mov_b32_e32 v243, 0
	v_mov_b32_e32 v244, 0
	v_mov_b32_e32 v245, 0
	v_cvt_pk_fp8_f32 v242, v226, v227
	v_cvt_pk_fp8_f32 v243, v230, v231
	v_cvt_pk_fp8_f32 v244, v234, v235
	v_cvt_pk_fp8_f32 v245, v238, v239
	v_cvt_pk_fp8_f32 v242, v228, v229 op_sel:[0,0,1]
	v_cvt_pk_fp8_f32 v243, v232, v233 op_sel:[0,0,1]
	v_cvt_pk_fp8_f32 v244, v236, v237 op_sel:[0,0,1]
	v_cvt_pk_fp8_f32 v245, v240, v241 op_sel:[0,0,1]
	s_nop 0
	global_store_dwordx4 v78, v[242:245], s[6:7]
	s_waitcnt vmcnt(12)
	v_mul_f32_e32 v176, v26, v176
	v_mul_f32_e32 v177, v26, v177
	v_mul_f32_e32 v178, v26, v178
	v_mul_f32_e32 v179, v26, v179
	ds_write_b128 v210, v[176:179]
	v_mul_f32_e32 v180, v27, v180
	v_mul_f32_e32 v181, v27, v181
	v_mul_f32_e32 v182, v27, v182
	v_mul_f32_e32 v183, v27, v183
	ds_write_b128 v210, v[180:183] offset:1024
	v_mul_f32_e32 v184, v28, v184
	v_mul_f32_e32 v185, v28, v185
	v_mul_f32_e32 v186, v28, v186
	v_mul_f32_e32 v187, v28, v187
	ds_write_b128 v210, v[184:187] offset:2048
	v_mul_f32_e32 v188, v29, v188
	v_mul_f32_e32 v189, v29, v189
	v_mul_f32_e32 v190, v29, v190
	v_mul_f32_e32 v191, v29, v191
	ds_write_b128 v210, v[188:191] offset:3072
	v_mul_f32_e32 v192, v30, v192
	v_mul_f32_e32 v193, v30, v193
	v_mul_f32_e32 v194, v30, v194
	v_mul_f32_e32 v195, v30, v195
	ds_write_b128 v210, v[192:195] offset:4096
	v_mul_f32_e32 v196, v31, v196
	v_mul_f32_e32 v197, v31, v197
	v_mul_f32_e32 v198, v31, v198
	v_mul_f32_e32 v199, v31, v199
	ds_write_b128 v210, v[196:199] offset:5120
	v_mul_f32_e32 v200, v32, v200
	v_mul_f32_e32 v201, v32, v201
	v_mul_f32_e32 v202, v32, v202
	v_mul_f32_e32 v203, v32, v203
	ds_write_b128 v210, v[200:203] offset:6144
	v_mul_f32_e32 v204, v33, v204
	v_mul_f32_e32 v205, v33, v205
	v_mul_f32_e32 v206, v33, v206
	v_mul_f32_e32 v207, v33, v207
	ds_write_b128 v210, v[204:207] offset:7168
	s_waitcnt lgkmcnt(0)
	s_barrier
; #define GAS __attribute__((address_space(1)))
; #define LAS __attribute__((address_space(3)))
; #define LDS_WAIT() asm volatile("s_waitcnt lgkmcnt(0)" ::: "memory")
;     ...
; #pragma unroll
;     for (int i = 0; i < 32; ++i) v[i] = sc >= 0 ? W[(size_t)(k0 + 2 * i + (lane >> 5)) * Nsrc + sc] : 0.f;
; #pragma unroll
;     for (int i = 0; i < 32; ++i) { const int k = k0 + 2 * i + (lane >> 5); float x = v[i] * wscale; if (KS) x *= (k < ksplit ? ksA[k] : ksB[k - ksplit]); scr[(2 * i + (lane >> 5)) * 33 + (lane & 31)] = x; }
;     LDS_WAIT(); asm volatile("" ::: "memory");
;     const int c = lane & 7;
; #pragma unroll
;     for (int j = 0; j < 4; ++j) { const int n = (lane >> 3) + 8 * j; const LAS float* s = scr + (8 * c) * 33 + n;
;         const unsigned long long o = (unsigned long long)pg8::pk4_fp8(s[0 * 33], s[1 * 33], s[2 * 33], s[3 * 33]) | ((unsigned long long)pg8::pk4_fp8(s[4 * 33], s[5 * 33], s[6 * 33], s[7 * 33]) << 32);
;         *(GAS unsigned long long*)(WT + (size_t)(n0 + n) * K + k0 + 8 * c) = o; }
	s_add_u32 s8, s30, 0x7000
	s_addc_u32 s9, s31, 0
	global_load_dwordx4 v[176:179], v74, s[8:9]
	s_add_u32 s8, s8, 0x20000
	s_addc_u32 s9, s9, 0
	global_load_dwordx4 v[180:183], v74, s[8:9]
	s_add_u32 s8, s8, 0x20000
	s_addc_u32 s9, s9, 0
	global_load_dwordx4 v[184:187], v74, s[8:9]
	s_add_u32 s8, s8, 0x20000
	s_addc_u32 s9, s9, 0
	global_load_dwordx4 v[188:191], v74, s[8:9]
	s_add_u32 s8, s8, 0x20000
	s_addc_u32 s9, s9, 0
	global_load_dwordx4 v[192:195], v74, s[8:9]
	s_add_u32 s8, s8, 0x20000
	s_addc_u32 s9, s9, 0
	global_load_dwordx4 v[196:199], v74, s[8:9]
	s_add_u32 s8, s8, 0x20000
	s_addc_u32 s9, s9, 0
	global_load_dwordx4 v[200:203], v74, s[8:9]
	s_add_u32 s8, s8, 0x20000
	s_addc_u32 s9, s9, 0
	global_load_dwordx4 v[204:207], v74, s[8:9]
	s_add_u32 s6, s32, 0x1400000
	s_addc_u32 s7, s33, 0
	ds_read_b32 v226, v212
	ds_read_b32 v227, v212 offset:512
	ds_read_b32 v228, v212 offset:1024
	ds_read_b32 v229, v212 offset:1536
	ds_read_b32 v230, v212 offset:2048
	ds_read_b32 v231, v212 offset:2560
	ds_read_b32 v232, v212 offset:3072
	ds_read_b32 v233, v212 offset:3584
	ds_read_b32 v234, v212 offset:4096
	ds_read_b32 v235, v212 offset:4608
	ds_read_b32 v236, v212 offset:5120
	ds_read_b32 v237, v212 offset:5632
	ds_read_b32 v238, v212 offset:6144
	ds_read_b32 v239, v212 offset:6656
	ds_read_b32 v240, v212 offset:7168
	ds_read_b32 v241, v212 offset:7680
	s_waitcnt lgkmcnt(0)
	v_max_f32_e32 v226, v226, v226
	v_max_f32_e32 v227, v227, v227
	v_max_f32_e32 v228, v228, v228
	v_max_f32_e32 v229, v229, v229
	v_max_f32_e32 v230, v230, v230
	v_max_f32_e32 v231, v231, v231
	v_max_f32_e32 v232, v232, v232
	v_max_f32_e32 v233, v233, v233
	v_max_f32_e32 v234, v234, v234
	v_max_f32_e32 v235, v235, v235
	v_max_f32_e32 v236, v236, v236
	v_max_f32_e32 v237, v237, v237
	v_max_f32_e32 v238, v238, v238
	v_max_f32_e32 v239, v239, v239
	v_max_f32_e32 v240, v240, v240
	v_max_f32_e32 v241, v241, v241
	v_med3_f32 v226, v226, s62, v95
	v_med3_f32 v227, v227, s62, v95
	v_med3_f32 v228, v228, s62, v95
	v_med3_f32 v229, v229, s62, v95
	v_med3_f32 v230, v230, s62, v95
	v_med3_f32 v231, v231, s62, v95
	v_med3_f32 v232, v232, s62, v95
	v_med3_f32 v233, v233, s62, v95
	v_med3_f32 v234, v234, s62, v95
	v_med3_f32 v235, v235, s62, v95
	v_med3_f32 v236, v236, s62, v95
	v_med3_f32 v237, v237, s62, v95
	v_med3_f32 v238, v238, s62, v95
	v_med3_f32 v239, v239, s62, v95
	v_med3_f32 v240, v240, s62, v95
	v_med3_f32 v241, v241, s62, v95
	v_mov_b32_e32 v242, 0
	v_mov_b32_e32 v243, 0
	v_mov_b32_e32 v244, 0
	v_mov_b32_e32 v245, 0
	v_cvt_pk_fp8_f32 v242, v226, v227
	v_cvt_pk_fp8_f32 v243, v230, v231
	v_cvt_pk_fp8_f32 v244, v234, v235
	v_cvt_pk_fp8_f32 v245, v238, v239
	v_cvt_pk_fp8_f32 v242, v228, v229 op_sel:[0,0,1]
	v_cvt_pk_fp8_f32 v243, v232, v233 op_sel:[0,0,1]
	v_cvt_pk_fp8_f32 v244, v236, v237 op_sel:[0,0,1]
	v_cvt_pk_fp8_f32 v245, v240, v241 op_sel:[0,0,1]
	s_nop 0
	global_store_dwordx4 v77, v[242:245], s[6:7]
	ds_read_b32 v226, v214
	ds_read_b32 v227, v214 offset:512
	ds_read_b32 v228, v214 offset:1024
	ds_read_b32 v229, v214 offset:1536
	ds_read_b32 v230, v214 offset:2048
	ds_read_b32 v231, v214 offset:2560
	ds_read_b32 v232, v214 offset:3072
	ds_read_b32 v233, v214 offset:3584
	ds_read_b32 v234, v214 offset:4096
	ds_read_b32 v235, v214 offset:4608
	ds_read_b32 v236, v214 offset:5120
	ds_read_b32 v237, v214 offset:5632
	ds_read_b32 v238, v214 offset:6144
	ds_read_b32 v239, v214 offset:6656
	ds_read_b32 v240, v214 offset:7168
	ds_read_b32 v241, v214 offset:7680
	s_waitcnt lgkmcnt(0)
	v_max_f32_e32 v226, v226, v226
	v_max_f32_e32 v227, v227, v227
	v_max_f32_e32 v228, v228, v228
	v_max_f32_e32 v229, v229, v229
	v_max_f32_e32 v230, v230, v230
	v_max_f32_e32 v231, v231, v231
	v_max_f32_e32 v232, v232, v232
	v_max_f32_e32 v233, v233, v233
	v_max_f32_e32 v234, v234, v234
	v_max_f32_e32 v235, v235, v235
	v_max_f32_e32 v236, v236, v236
	v_max_f32_e32 v237, v237, v237
	v_max_f32_e32 v238, v238, v238
	v_max_f32_e32 v239, v239, v239
	v_max_f32_e32 v240, v240, v240
	v_max_f32_e32 v241, v241, v241
	v_med3_f32 v226, v226, s62, v95
	v_med3_f32 v227, v227, s62, v95
	v_med3_f32 v228, v228, s62, v95
	v_med3_f32 v229, v229, s62, v95
	v_med3_f32 v230, v230, s62, v95
	v_med3_f32 v231, v231, s62, v95
	v_med3_f32 v232, v232, s62, v95
	v_med3_f32 v233, v233, s62, v95
	v_med3_f32 v234, v234, s62, v95
	v_med3_f32 v235, v235, s62, v95
	v_med3_f32 v236, v236, s62, v95
	v_med3_f32 v237, v237, s62, v95
	v_med3_f32 v238, v238, s62, v95
	v_med3_f32 v239, v239, s62, v95
	v_med3_f32 v240, v240, s62, v95
	v_med3_f32 v241, v241, s62, v95
	v_mov_b32_e32 v242, 0
	v_mov_b32_e32 v243, 0
	v_mov_b32_e32 v244, 0
	v_mov_b32_e32 v245, 0
	v_cvt_pk_fp8_f32 v242, v226, v227
	v_cvt_pk_fp8_f32 v243, v230, v231
	v_cvt_pk_fp8_f32 v244, v234, v235
	v_cvt_pk_fp8_f32 v245, v238, v239
	v_cvt_pk_fp8_f32 v242, v228, v229 op_sel:[0,0,1]
	v_cvt_pk_fp8_f32 v243, v232, v233 op_sel:[0,0,1]
	v_cvt_pk_fp8_f32 v244, v236, v237 op_sel:[0,0,1]
	v_cvt_pk_fp8_f32 v245, v240, v241 op_sel:[0,0,1]
	s_nop 0
	global_store_dwordx4 v78, v[242:245], s[6:7]
	s_waitcnt vmcnt(12)
	v_mul_f32_e32 v144, v26, v144
	v_mul_f32_e32 v145, v26, v145
	v_mul_f32_e32 v146, v26, v146
	v_mul_f32_e32 v147, v26, v147
	ds_write_b128 v209, v[144:147]
	v_mul_f32_e32 v148, v27, v148
	v_mul_f32_e32 v149, v27, v149
	v_mul_f32_e32 v150, v27, v150
	v_mul_f32_e32 v151, v27, v151
	ds_write_b128 v209, v[148:151] offset:1024
	v_mul_f32_e32 v152, v28, v152
	v_mul_f32_e32 v153, v28, v153
	v_mul_f32_e32 v154, v28, v154
	v_mul_f32_e32 v155, v28, v155
	ds_write_b128 v209, v[152:155] offset:2048
	v_mul_f32_e32 v156, v29, v156
	v_mul_f32_e32 v157, v29, v157
	v_mul_f32_e32 v158, v29, v158
	v_mul_f32_e32 v159, v29, v159
	ds_write_b128 v209, v[156:159] offset:3072
	v_mul_f32_e32 v160, v30, v160
	v_mul_f32_e32 v161, v30, v161
	v_mul_f32_e32 v162, v30, v162
	v_mul_f32_e32 v163, v30, v163
	ds_write_b128 v209, v[160:163] offset:4096
	v_mul_f32_e32 v164, v31, v164
	v_mul_f32_e32 v165, v31, v165
	v_mul_f32_e32 v166, v31, v166
	v_mul_f32_e32 v167, v31, v167
	ds_write_b128 v209, v[164:167] offset:5120
	v_mul_f32_e32 v168, v32, v168
	v_mul_f32_e32 v169, v32, v169
	v_mul_f32_e32 v170, v32, v170
	v_mul_f32_e32 v171, v32, v171
	ds_write_b128 v209, v[168:171] offset:6144
	v_mul_f32_e32 v172, v33, v172
	v_mul_f32_e32 v173, v33, v173
	v_mul_f32_e32 v174, v33, v174
	v_mul_f32_e32 v175, v33, v175
	ds_write_b128 v209, v[172:175] offset:7168
	s_waitcnt lgkmcnt(0)
	s_barrier
; #define GAS __attribute__((address_space(1)))
; #define LAS __attribute__((address_space(3)))
; #define LDS_WAIT() asm volatile("s_waitcnt lgkmcnt(0)" ::: "memory")
;     ...
; #pragma unroll
;     for (int i = 0; i < 32; ++i) v[i] = sc >= 0 ? W[(size_t)(k0 + 2 * i + (lane >> 5)) * Nsrc + sc] : 0.f;
; #pragma unroll
;     for (int i = 0; i < 32; ++i) { const int k = k0 + 2 * i + (lane >> 5); float x = v[i] * wscale; if (KS) x *= (k < ksplit ? ksA[k] : ksB[k - ksplit]); scr[(2 * i + (lane >> 5)) * 33 + (lane & 31)] = x; }
;     LDS_WAIT(); asm volatile("" ::: "memory");
;     const int c = lane & 7;
; #pragma unroll
;     for (int j = 0; j < 4; ++j) { const int n = (lane >> 3) + 8 * j; const LAS float* s = scr + (8 * c) * 33 + n;
;         const unsigned long long o = (unsigned long long)pg8::pk4_fp8(s[0 * 33], s[1 * 33], s[2 * 33], s[3 * 33]) | ((unsigned long long)pg8::pk4_fp8(s[4 * 33], s[5 * 33], s[6 * 33], s[7 * 33]) << 32);
;         *(GAS unsigned long long*)(WT + (size_t)(n0 + n) * K + k0 + 8 * c) = o; }
	s_add_u32 s8, s30, 0x8000
	s_addc_u32 s9, s31, 0
	global_load_dwordx4 v[144:147], v74, s[8:9]
	s_add_u32 s8, s8, 0x20000
	s_addc_u32 s9, s9, 0
	global_load_dwordx4 v[148:151], v74, s[8:9]
	s_add_u32 s8, s8, 0x20000
	s_addc_u32 s9, s9, 0
	global_load_dwordx4 v[152:155], v74, s[8:9]
	s_add_u32 s8, s8, 0x20000
	s_addc_u32 s9, s9, 0
	global_load_dwordx4 v[156:159], v74, s[8:9]
	s_add_u32 s8, s8, 0x20000
	s_addc_u32 s9, s9, 0
	global_load_dwordx4 v[160:163], v74, s[8:9]
	s_add_u32 s8, s8, 0x20000
	s_addc_u32 s9, s9, 0
	global_load_dwordx4 v[164:167], v74, s[8:9]
	s_add_u32 s8, s8, 0x20000
	s_addc_u32 s9, s9, 0
	global_load_dwordx4 v[168:171], v74, s[8:9]
	s_add_u32 s8, s8, 0x20000
	s_addc_u32 s9, s9, 0
	global_load_dwordx4 v[172:175], v74, s[8:9]
	s_add_u32 s6, s32, 0x1800000
	s_addc_u32 s7, s33, 0
	ds_read_b32 v226, v211
	ds_read_b32 v227, v211 offset:512
	ds_read_b32 v228, v211 offset:1024
	ds_read_b32 v229, v211 offset:1536
	ds_read_b32 v230, v211 offset:2048
	ds_read_b32 v231, v211 offset:2560
	ds_read_b32 v232, v211 offset:3072
	ds_read_b32 v233, v211 offset:3584
	ds_read_b32 v234, v211 offset:4096
	ds_read_b32 v235, v211 offset:4608
	ds_read_b32 v236, v211 offset:5120
	ds_read_b32 v237, v211 offset:5632
	ds_read_b32 v238, v211 offset:6144
	ds_read_b32 v239, v211 offset:6656
	ds_read_b32 v240, v211 offset:7168
	ds_read_b32 v241, v211 offset:7680
	s_waitcnt lgkmcnt(0)
	v_max_f32_e32 v226, v226, v226
	v_max_f32_e32 v227, v227, v227
	v_max_f32_e32 v228, v228, v228
	v_max_f32_e32 v229, v229, v229
	v_max_f32_e32 v230, v230, v230
	v_max_f32_e32 v231, v231, v231
	v_max_f32_e32 v232, v232, v232
	v_max_f32_e32 v233, v233, v233
	v_max_f32_e32 v234, v234, v234
	v_max_f32_e32 v235, v235, v235
	v_max_f32_e32 v236, v236, v236
	v_max_f32_e32 v237, v237, v237
	v_max_f32_e32 v238, v238, v238
	v_max_f32_e32 v239, v239, v239
	v_max_f32_e32 v240, v240, v240
	v_max_f32_e32 v241, v241, v241
	v_med3_f32 v226, v226, s62, v95
	v_med3_f32 v227, v227, s62, v95
	v_med3_f32 v228, v228, s62, v95
	v_med3_f32 v229, v229, s62, v95
	v_med3_f32 v230, v230, s62, v95
	v_med3_f32 v231, v231, s62, v95
	v_med3_f32 v232, v232, s62, v95
	v_med3_f32 v233, v233, s62, v95
	v_med3_f32 v234, v234, s62, v95
	v_med3_f32 v235, v235, s62, v95
	v_med3_f32 v236, v236, s62, v95
	v_med3_f32 v237, v237, s62, v95
	v_med3_f32 v238, v238, s62, v95
	v_med3_f32 v239, v239, s62, v95
	v_med3_f32 v240, v240, s62, v95
	v_med3_f32 v241, v241, s62, v95
	v_mov_b32_e32 v242, 0
	v_mov_b32_e32 v243, 0
	v_mov_b32_e32 v244, 0
	v_mov_b32_e32 v245, 0
	v_cvt_pk_fp8_f32 v242, v226, v227
	v_cvt_pk_fp8_f32 v243, v230, v231
	v_cvt_pk_fp8_f32 v244, v234, v235
	v_cvt_pk_fp8_f32 v245, v238, v239
	v_cvt_pk_fp8_f32 v242, v228, v229 op_sel:[0,0,1]
	v_cvt_pk_fp8_f32 v243, v232, v233 op_sel:[0,0,1]
	v_cvt_pk_fp8_f32 v244, v236, v237 op_sel:[0,0,1]
	v_cvt_pk_fp8_f32 v245, v240, v241 op_sel:[0,0,1]
	s_nop 0
	global_store_dwordx4 v77, v[242:245], s[6:7]
	ds_read_b32 v226, v213
	ds_read_b32 v227, v213 offset:512
	ds_read_b32 v228, v213 offset:1024
	ds_read_b32 v229, v213 offset:1536
	ds_read_b32 v230, v213 offset:2048
	ds_read_b32 v231, v213 offset:2560
	ds_read_b32 v232, v213 offset:3072
	ds_read_b32 v233, v213 offset:3584
	ds_read_b32 v234, v213 offset:4096
	ds_read_b32 v235, v213 offset:4608
	ds_read_b32 v236, v213 offset:5120
	ds_read_b32 v237, v213 offset:5632
	ds_read_b32 v238, v213 offset:6144
	ds_read_b32 v239, v213 offset:6656
	ds_read_b32 v240, v213 offset:7168
	ds_read_b32 v241, v213 offset:7680
	s_waitcnt lgkmcnt(0)
	v_max_f32_e32 v226, v226, v226
	v_max_f32_e32 v227, v227, v227
	v_max_f32_e32 v228, v228, v228
	v_max_f32_e32 v229, v229, v229
	v_max_f32_e32 v230, v230, v230
	v_max_f32_e32 v231, v231, v231
	v_max_f32_e32 v232, v232, v232
	v_max_f32_e32 v233, v233, v233
	v_max_f32_e32 v234, v234, v234
	v_max_f32_e32 v235, v235, v235
	v_max_f32_e32 v236, v236, v236
	v_max_f32_e32 v237, v237, v237
	v_max_f32_e32 v238, v238, v238
	v_max_f32_e32 v239, v239, v239
	v_max_f32_e32 v240, v240, v240
	v_max_f32_e32 v241, v241, v241
	v_med3_f32 v226, v226, s62, v95
	v_med3_f32 v227, v227, s62, v95
	v_med3_f32 v228, v228, s62, v95
	v_med3_f32 v229, v229, s62, v95
	v_med3_f32 v230, v230, s62, v95
	v_med3_f32 v231, v231, s62, v95
	v_med3_f32 v232, v232, s62, v95
	v_med3_f32 v233, v233, s62, v95
	v_med3_f32 v234, v234, s62, v95
	v_med3_f32 v235, v235, s62, v95
	v_med3_f32 v236, v236, s62, v95
	v_med3_f32 v237, v237, s62, v95
	v_med3_f32 v238, v238, s62, v95
	v_med3_f32 v239, v239, s62, v95
	v_med3_f32 v240, v240, s62, v95
	v_med3_f32 v241, v241, s62, v95
	v_mov_b32_e32 v242, 0
	v_mov_b32_e32 v243, 0
	v_mov_b32_e32 v244, 0
	v_mov_b32_e32 v245, 0
	v_cvt_pk_fp8_f32 v242, v226, v227
	v_cvt_pk_fp8_f32 v243, v230, v231
	v_cvt_pk_fp8_f32 v244, v234, v235
	v_cvt_pk_fp8_f32 v245, v238, v239
	v_cvt_pk_fp8_f32 v242, v228, v229 op_sel:[0,0,1]
	v_cvt_pk_fp8_f32 v243, v232, v233 op_sel:[0,0,1]
	v_cvt_pk_fp8_f32 v244, v236, v237 op_sel:[0,0,1]
	v_cvt_pk_fp8_f32 v245, v240, v241 op_sel:[0,0,1]
	s_nop 0
	global_store_dwordx4 v78, v[242:245], s[6:7]
	s_waitcnt vmcnt(12)
	v_mul_f32_e32 v176, v26, v176
	v_mul_f32_e32 v177, v26, v177
	v_mul_f32_e32 v178, v26, v178
	v_mul_f32_e32 v179, v26, v179
	ds_write_b128 v210, v[176:179]
	v_mul_f32_e32 v180, v27, v180
	v_mul_f32_e32 v181, v27, v181
	v_mul_f32_e32 v182, v27, v182
	v_mul_f32_e32 v183, v27, v183
	ds_write_b128 v210, v[180:183] offset:1024
	v_mul_f32_e32 v184, v28, v184
	v_mul_f32_e32 v185, v28, v185
	v_mul_f32_e32 v186, v28, v186
	v_mul_f32_e32 v187, v28, v187
	ds_write_b128 v210, v[184:187] offset:2048
	v_mul_f32_e32 v188, v29, v188
	v_mul_f32_e32 v189, v29, v189
	v_mul_f32_e32 v190, v29, v190
	v_mul_f32_e32 v191, v29, v191
	ds_write_b128 v210, v[188:191] offset:3072
	v_mul_f32_e32 v192, v30, v192
	v_mul_f32_e32 v193, v30, v193
	v_mul_f32_e32 v194, v30, v194
	v_mul_f32_e32 v195, v30, v195
	ds_write_b128 v210, v[192:195] offset:4096
	v_mul_f32_e32 v196, v31, v196
	v_mul_f32_e32 v197, v31, v197
	v_mul_f32_e32 v198, v31, v198
	v_mul_f32_e32 v199, v31, v199
	ds_write_b128 v210, v[196:199] offset:5120
	v_mul_f32_e32 v200, v32, v200
	v_mul_f32_e32 v201, v32, v201
	v_mul_f32_e32 v202, v32, v202
	v_mul_f32_e32 v203, v32, v203
	ds_write_b128 v210, v[200:203] offset:6144
	v_mul_f32_e32 v204, v33, v204
	v_mul_f32_e32 v205, v33, v205
	v_mul_f32_e32 v206, v33, v206
	v_mul_f32_e32 v207, v33, v207
	ds_write_b128 v210, v[204:207] offset:7168
	s_waitcnt lgkmcnt(0)
	s_barrier
; #define GAS __attribute__((address_space(1)))
; #define LAS __attribute__((address_space(3)))
; #define LDS_WAIT() asm volatile("s_waitcnt lgkmcnt(0)" ::: "memory")
;     ...
; #pragma unroll
;     for (int i = 0; i < 32; ++i) v[i] = sc >= 0 ? W[(size_t)(k0 + 2 * i + (lane >> 5)) * Nsrc + sc] : 0.f;
; #pragma unroll
;     for (int i = 0; i < 32; ++i) { const int k = k0 + 2 * i + (lane >> 5); float x = v[i] * wscale; if (KS) x *= (k < ksplit ? ksA[k] : ksB[k - ksplit]); scr[(2 * i + (lane >> 5)) * 33 + (lane & 31)] = x; }
;     LDS_WAIT(); asm volatile("" ::: "memory");
;     const int c = lane & 7;
; #pragma unroll
;     for (int j = 0; j < 4; ++j) { const int n = (lane >> 3) + 8 * j; const LAS float* s = scr + (8 * c) * 33 + n;
;         const unsigned long long o = (unsigned long long)pg8::pk4_fp8(s[0 * 33], s[1 * 33], s[2 * 33], s[3 * 33]) | ((unsigned long long)pg8::pk4_fp8(s[4 * 33], s[5 * 33], s[6 * 33], s[7 * 33]) << 32);
;         *(GAS unsigned long long*)(WT + (size_t)(n0 + n) * K + k0 + 8 * c) = o; }
	s_add_u32 s8, s30, 0x9000
	s_addc_u32 s9, s31, 0
	global_load_dwordx4 v[176:179], v74, s[8:9]
	s_add_u32 s8, s8, 0x20000
	s_addc_u32 s9, s9, 0
	global_load_dwordx4 v[180:183], v74, s[8:9]
	s_add_u32 s8, s8, 0x20000
	s_addc_u32 s9, s9, 0
	global_load_dwordx4 v[184:187], v74, s[8:9]
	s_add_u32 s8, s8, 0x20000
	s_addc_u32 s9, s9, 0
	global_load_dwordx4 v[188:191], v74, s[8:9]
	s_add_u32 s8, s8, 0x20000
	s_addc_u32 s9, s9, 0
	global_load_dwordx4 v[192:195], v74, s[8:9]
	s_add_u32 s8, s8, 0x20000
	s_addc_u32 s9, s9, 0
	global_load_dwordx4 v[196:199], v74, s[8:9]
	s_add_u32 s8, s8, 0x20000
	s_addc_u32 s9, s9, 0
	global_load_dwordx4 v[200:203], v74, s[8:9]
	s_add_u32 s8, s8, 0x20000
	s_addc_u32 s9, s9, 0
	global_load_dwordx4 v[204:207], v74, s[8:9]
	s_add_u32 s6, s32, 0x1c00000
	s_addc_u32 s7, s33, 0
	ds_read_b32 v226, v212
	ds_read_b32 v227, v212 offset:512
	ds_read_b32 v228, v212 offset:1024
	ds_read_b32 v229, v212 offset:1536
	ds_read_b32 v230, v212 offset:2048
	ds_read_b32 v231, v212 offset:2560
	ds_read_b32 v232, v212 offset:3072
	ds_read_b32 v233, v212 offset:3584
	ds_read_b32 v234, v212 offset:4096
	ds_read_b32 v235, v212 offset:4608
	ds_read_b32 v236, v212 offset:5120
	ds_read_b32 v237, v212 offset:5632
	ds_read_b32 v238, v212 offset:6144
	ds_read_b32 v239, v212 offset:6656
	ds_read_b32 v240, v212 offset:7168
	ds_read_b32 v241, v212 offset:7680
	s_waitcnt lgkmcnt(0)
	v_max_f32_e32 v226, v226, v226
	v_max_f32_e32 v227, v227, v227
	v_max_f32_e32 v228, v228, v228
	v_max_f32_e32 v229, v229, v229
	v_max_f32_e32 v230, v230, v230
	v_max_f32_e32 v231, v231, v231
	v_max_f32_e32 v232, v232, v232
	v_max_f32_e32 v233, v233, v233
	v_max_f32_e32 v234, v234, v234
	v_max_f32_e32 v235, v235, v235
	v_max_f32_e32 v236, v236, v236
	v_max_f32_e32 v237, v237, v237
	v_max_f32_e32 v238, v238, v238
	v_max_f32_e32 v239, v239, v239
	v_max_f32_e32 v240, v240, v240
	v_max_f32_e32 v241, v241, v241
	v_med3_f32 v226, v226, s62, v95
	v_med3_f32 v227, v227, s62, v95
	v_med3_f32 v228, v228, s62, v95
	v_med3_f32 v229, v229, s62, v95
	v_med3_f32 v230, v230, s62, v95
	v_med3_f32 v231, v231, s62, v95
	v_med3_f32 v232, v232, s62, v95
	v_med3_f32 v233, v233, s62, v95
	v_med3_f32 v234, v234, s62, v95
	v_med3_f32 v235, v235, s62, v95
	v_med3_f32 v236, v236, s62, v95
	v_med3_f32 v237, v237, s62, v95
	v_med3_f32 v238, v238, s62, v95
	v_med3_f32 v239, v239, s62, v95
	v_med3_f32 v240, v240, s62, v95
	v_med3_f32 v241, v241, s62, v95
	v_mov_b32_e32 v242, 0
	v_mov_b32_e32 v243, 0
	v_mov_b32_e32 v244, 0
	v_mov_b32_e32 v245, 0
	v_cvt_pk_fp8_f32 v242, v226, v227
	v_cvt_pk_fp8_f32 v243, v230, v231
	v_cvt_pk_fp8_f32 v244, v234, v235
	v_cvt_pk_fp8_f32 v245, v238, v239
	v_cvt_pk_fp8_f32 v242, v228, v229 op_sel:[0,0,1]
	v_cvt_pk_fp8_f32 v243, v232, v233 op_sel:[0,0,1]
	v_cvt_pk_fp8_f32 v244, v236, v237 op_sel:[0,0,1]
	v_cvt_pk_fp8_f32 v245, v240, v241 op_sel:[0,0,1]
	s_nop 0
	global_store_dwordx4 v77, v[242:245], s[6:7]
	ds_read_b32 v226, v214
	ds_read_b32 v227, v214 offset:512
	ds_read_b32 v228, v214 offset:1024
	ds_read_b32 v229, v214 offset:1536
	ds_read_b32 v230, v214 offset:2048
	ds_read_b32 v231, v214 offset:2560
	ds_read_b32 v232, v214 offset:3072
	ds_read_b32 v233, v214 offset:3584
	ds_read_b32 v234, v214 offset:4096
	ds_read_b32 v235, v214 offset:4608
	ds_read_b32 v236, v214 offset:5120
	ds_read_b32 v237, v214 offset:5632
	ds_read_b32 v238, v214 offset:6144
	ds_read_b32 v239, v214 offset:6656
	ds_read_b32 v240, v214 offset:7168
	ds_read_b32 v241, v214 offset:7680
	s_waitcnt lgkmcnt(0)
	v_max_f32_e32 v226, v226, v226
	v_max_f32_e32 v227, v227, v227
	v_max_f32_e32 v228, v228, v228
	v_max_f32_e32 v229, v229, v229
	v_max_f32_e32 v230, v230, v230
	v_max_f32_e32 v231, v231, v231
	v_max_f32_e32 v232, v232, v232
	v_max_f32_e32 v233, v233, v233
	v_max_f32_e32 v234, v234, v234
	v_max_f32_e32 v235, v235, v235
	v_max_f32_e32 v236, v236, v236
	v_max_f32_e32 v237, v237, v237
	v_max_f32_e32 v238, v238, v238
	v_max_f32_e32 v239, v239, v239
	v_max_f32_e32 v240, v240, v240
	v_max_f32_e32 v241, v241, v241
	v_med3_f32 v226, v226, s62, v95
	v_med3_f32 v227, v227, s62, v95
	v_med3_f32 v228, v228, s62, v95
	v_med3_f32 v229, v229, s62, v95
	v_med3_f32 v230, v230, s62, v95
	v_med3_f32 v231, v231, s62, v95
	v_med3_f32 v232, v232, s62, v95
	v_med3_f32 v233, v233, s62, v95
	v_med3_f32 v234, v234, s62, v95
	v_med3_f32 v235, v235, s62, v95
	v_med3_f32 v236, v236, s62, v95
	v_med3_f32 v237, v237, s62, v95
	v_med3_f32 v238, v238, s62, v95
	v_med3_f32 v239, v239, s62, v95
	v_med3_f32 v240, v240, s62, v95
	v_med3_f32 v241, v241, s62, v95
	v_mov_b32_e32 v242, 0
	v_mov_b32_e32 v243, 0
	v_mov_b32_e32 v244, 0
	v_mov_b32_e32 v245, 0
	v_cvt_pk_fp8_f32 v242, v226, v227
	v_cvt_pk_fp8_f32 v243, v230, v231
	v_cvt_pk_fp8_f32 v244, v234, v235
	v_cvt_pk_fp8_f32 v245, v238, v239
	v_cvt_pk_fp8_f32 v242, v228, v229 op_sel:[0,0,1]
	v_cvt_pk_fp8_f32 v243, v232, v233 op_sel:[0,0,1]
	v_cvt_pk_fp8_f32 v244, v236, v237 op_sel:[0,0,1]
	v_cvt_pk_fp8_f32 v245, v240, v241 op_sel:[0,0,1]
	s_nop 0
	global_store_dwordx4 v78, v[242:245], s[6:7]
	s_waitcnt vmcnt(12)
	v_mul_f32_e32 v144, v26, v144
	v_mul_f32_e32 v145, v26, v145
	v_mul_f32_e32 v146, v26, v146
	v_mul_f32_e32 v147, v26, v147
	ds_write_b128 v209, v[144:147]
	v_mul_f32_e32 v148, v27, v148
	v_mul_f32_e32 v149, v27, v149
	v_mul_f32_e32 v150, v27, v150
	v_mul_f32_e32 v151, v27, v151
	ds_write_b128 v209, v[148:151] offset:1024
	v_mul_f32_e32 v152, v28, v152
	v_mul_f32_e32 v153, v28, v153
	v_mul_f32_e32 v154, v28, v154
	v_mul_f32_e32 v155, v28, v155
	ds_write_b128 v209, v[152:155] offset:2048
	v_mul_f32_e32 v156, v29, v156
	v_mul_f32_e32 v157, v29, v157
	v_mul_f32_e32 v158, v29, v158
	v_mul_f32_e32 v159, v29, v159
	ds_write_b128 v209, v[156:159] offset:3072
	v_mul_f32_e32 v160, v30, v160
	v_mul_f32_e32 v161, v30, v161
	v_mul_f32_e32 v162, v30, v162
	v_mul_f32_e32 v163, v30, v163
	ds_write_b128 v209, v[160:163] offset:4096
	v_mul_f32_e32 v164, v31, v164
	v_mul_f32_e32 v165, v31, v165
	v_mul_f32_e32 v166, v31, v166
	v_mul_f32_e32 v167, v31, v167
	ds_write_b128 v209, v[164:167] offset:5120
	v_mul_f32_e32 v168, v32, v168
	v_mul_f32_e32 v169, v32, v169
	v_mul_f32_e32 v170, v32, v170
	v_mul_f32_e32 v171, v32, v171
	ds_write_b128 v209, v[168:171] offset:6144
	v_mul_f32_e32 v172, v33, v172
	v_mul_f32_e32 v173, v33, v173
	v_mul_f32_e32 v174, v33, v174
	v_mul_f32_e32 v175, v33, v175
	ds_write_b128 v209, v[172:175] offset:7168
	s_waitcnt lgkmcnt(0)
	s_barrier
; #define GAS __attribute__((address_space(1)))
; #define LAS __attribute__((address_space(3)))
; #define LDS_WAIT() asm volatile("s_waitcnt lgkmcnt(0)" ::: "memory")
;     ...
; #pragma unroll
;     for (int i = 0; i < 32; ++i) v[i] = sc >= 0 ? W[(size_t)(k0 + 2 * i + (lane >> 5)) * Nsrc + sc] : 0.f;
; #pragma unroll
;     for (int i = 0; i < 32; ++i) { const int k = k0 + 2 * i + (lane >> 5); float x = v[i] * wscale; if (KS) x *= (k < ksplit ? ksA[k] : ksB[k - ksplit]); scr[(2 * i + (lane >> 5)) * 33 + (lane & 31)] = x; }
;     LDS_WAIT(); asm volatile("" ::: "memory");
;     const int c = lane & 7;
; #pragma unroll
;     for (int j = 0; j < 4; ++j) { const int n = (lane >> 3) + 8 * j; const LAS float* s = scr + (8 * c) * 33 + n;
;         const unsigned long long o = (unsigned long long)pg8::pk4_fp8(s[0 * 33], s[1 * 33], s[2 * 33], s[3 * 33]) | ((unsigned long long)pg8::pk4_fp8(s[4 * 33], s[5 * 33], s[6 * 33], s[7 * 33]) << 32);
;         *(GAS unsigned long long*)(WT + (size_t)(n0 + n) * K + k0 + 8 * c) = o; }
	s_add_u32 s8, s30, 0xa000
	s_addc_u32 s9, s31, 0
	global_load_dwordx4 v[144:147], v74, s[8:9]
	s_add_u32 s8, s8, 0x20000
	s_addc_u32 s9, s9, 0
	global_load_dwordx4 v[148:151], v74, s[8:9]
	s_add_u32 s8, s8, 0x20000
	s_addc_u32 s9, s9, 0
	global_load_dwordx4 v[152:155], v74, s[8:9]
	s_add_u32 s8, s8, 0x20000
	s_addc_u32 s9, s9, 0
	global_load_dwordx4 v[156:159], v74, s[8:9]
	s_add_u32 s8, s8, 0x20000
	s_addc_u32 s9, s9, 0
	global_load_dwordx4 v[160:163], v74, s[8:9]
	s_add_u32 s8, s8, 0x20000
	s_addc_u32 s9, s9, 0
	global_load_dwordx4 v[164:167], v74, s[8:9]
	s_add_u32 s8, s8, 0x20000
	s_addc_u32 s9, s9, 0
	global_load_dwordx4 v[168:171], v74, s[8:9]
	s_add_u32 s8, s8, 0x20000
	s_addc_u32 s9, s9, 0
	global_load_dwordx4 v[172:175], v74, s[8:9]
	s_add_u32 s6, s32, 0x2000000
	s_addc_u32 s7, s33, 0
	ds_read_b32 v226, v211
	ds_read_b32 v227, v211 offset:512
	ds_read_b32 v228, v211 offset:1024
	ds_read_b32 v229, v211 offset:1536
	ds_read_b32 v230, v211 offset:2048
	ds_read_b32 v231, v211 offset:2560
	ds_read_b32 v232, v211 offset:3072
	ds_read_b32 v233, v211 offset:3584
	ds_read_b32 v234, v211 offset:4096
	ds_read_b32 v235, v211 offset:4608
	ds_read_b32 v236, v211 offset:5120
	ds_read_b32 v237, v211 offset:5632
	ds_read_b32 v238, v211 offset:6144
	ds_read_b32 v239, v211 offset:6656
	ds_read_b32 v240, v211 offset:7168
	ds_read_b32 v241, v211 offset:7680
	s_waitcnt lgkmcnt(0)
	v_max_f32_e32 v226, v226, v226
	v_max_f32_e32 v227, v227, v227
	v_max_f32_e32 v228, v228, v228
	v_max_f32_e32 v229, v229, v229
	v_max_f32_e32 v230, v230, v230
	v_max_f32_e32 v231, v231, v231
	v_max_f32_e32 v232, v232, v232
	v_max_f32_e32 v233, v233, v233
	v_max_f32_e32 v234, v234, v234
	v_max_f32_e32 v235, v235, v235
	v_max_f32_e32 v236, v236, v236
	v_max_f32_e32 v237, v237, v237
	v_max_f32_e32 v238, v238, v238
	v_max_f32_e32 v239, v239, v239
	v_max_f32_e32 v240, v240, v240
	v_max_f32_e32 v241, v241, v241
	v_med3_f32 v226, v226, s62, v95
	v_med3_f32 v227, v227, s62, v95
	v_med3_f32 v228, v228, s62, v95
	v_med3_f32 v229, v229, s62, v95
	v_med3_f32 v230, v230, s62, v95
	v_med3_f32 v231, v231, s62, v95
	v_med3_f32 v232, v232, s62, v95
	v_med3_f32 v233, v233, s62, v95
	v_med3_f32 v234, v234, s62, v95
	v_med3_f32 v235, v235, s62, v95
	v_med3_f32 v236, v236, s62, v95
	v_med3_f32 v237, v237, s62, v95
	v_med3_f32 v238, v238, s62, v95
	v_med3_f32 v239, v239, s62, v95
	v_med3_f32 v240, v240, s62, v95
	v_med3_f32 v241, v241, s62, v95
	v_mov_b32_e32 v242, 0
	v_mov_b32_e32 v243, 0
	v_mov_b32_e32 v244, 0
	v_mov_b32_e32 v245, 0
	v_cvt_pk_fp8_f32 v242, v226, v227
	v_cvt_pk_fp8_f32 v243, v230, v231
	v_cvt_pk_fp8_f32 v244, v234, v235
	v_cvt_pk_fp8_f32 v245, v238, v239
	v_cvt_pk_fp8_f32 v242, v228, v229 op_sel:[0,0,1]
	v_cvt_pk_fp8_f32 v243, v232, v233 op_sel:[0,0,1]
	v_cvt_pk_fp8_f32 v244, v236, v237 op_sel:[0,0,1]
	v_cvt_pk_fp8_f32 v245, v240, v241 op_sel:[0,0,1]
	s_nop 0
	global_store_dwordx4 v77, v[242:245], s[6:7]
	ds_read_b32 v226, v213
	ds_read_b32 v227, v213 offset:512
	ds_read_b32 v228, v213 offset:1024
	ds_read_b32 v229, v213 offset:1536
	ds_read_b32 v230, v213 offset:2048
	ds_read_b32 v231, v213 offset:2560
	ds_read_b32 v232, v213 offset:3072
	ds_read_b32 v233, v213 offset:3584
	ds_read_b32 v234, v213 offset:4096
	ds_read_b32 v235, v213 offset:4608
	ds_read_b32 v236, v213 offset:5120
	ds_read_b32 v237, v213 offset:5632
	ds_read_b32 v238, v213 offset:6144
	ds_read_b32 v239, v213 offset:6656
	ds_read_b32 v240, v213 offset:7168
	ds_read_b32 v241, v213 offset:7680
	s_waitcnt lgkmcnt(0)
	v_max_f32_e32 v226, v226, v226
	v_max_f32_e32 v227, v227, v227
	v_max_f32_e32 v228, v228, v228
	v_max_f32_e32 v229, v229, v229
	v_max_f32_e32 v230, v230, v230
	v_max_f32_e32 v231, v231, v231
	v_max_f32_e32 v232, v232, v232
	v_max_f32_e32 v233, v233, v233
	v_max_f32_e32 v234, v234, v234
	v_max_f32_e32 v235, v235, v235
	v_max_f32_e32 v236, v236, v236
	v_max_f32_e32 v237, v237, v237
	v_max_f32_e32 v238, v238, v238
	v_max_f32_e32 v239, v239, v239
	v_max_f32_e32 v240, v240, v240
	v_max_f32_e32 v241, v241, v241
	v_med3_f32 v226, v226, s62, v95
	v_med3_f32 v227, v227, s62, v95
	v_med3_f32 v228, v228, s62, v95
	v_med3_f32 v229, v229, s62, v95
	v_med3_f32 v230, v230, s62, v95
	v_med3_f32 v231, v231, s62, v95
	v_med3_f32 v232, v232, s62, v95
	v_med3_f32 v233, v233, s62, v95
	v_med3_f32 v234, v234, s62, v95
	v_med3_f32 v235, v235, s62, v95
	v_med3_f32 v236, v236, s62, v95
	v_med3_f32 v237, v237, s62, v95
	v_med3_f32 v238, v238, s62, v95
	v_med3_f32 v239, v239, s62, v95
	v_med3_f32 v240, v240, s62, v95
	v_med3_f32 v241, v241, s62, v95
	v_mov_b32_e32 v242, 0
	v_mov_b32_e32 v243, 0
	v_mov_b32_e32 v244, 0
	v_mov_b32_e32 v245, 0
	v_cvt_pk_fp8_f32 v242, v226, v227
	v_cvt_pk_fp8_f32 v243, v230, v231
	v_cvt_pk_fp8_f32 v244, v234, v235
	v_cvt_pk_fp8_f32 v245, v238, v239
	v_cvt_pk_fp8_f32 v242, v228, v229 op_sel:[0,0,1]
	v_cvt_pk_fp8_f32 v243, v232, v233 op_sel:[0,0,1]
	v_cvt_pk_fp8_f32 v244, v236, v237 op_sel:[0,0,1]
	v_cvt_pk_fp8_f32 v245, v240, v241 op_sel:[0,0,1]
	s_nop 0
	global_store_dwordx4 v78, v[242:245], s[6:7]
	s_waitcnt vmcnt(12)
	v_mul_f32_e32 v176, v26, v176
	v_mul_f32_e32 v177, v26, v177
	v_mul_f32_e32 v178, v26, v178
	v_mul_f32_e32 v179, v26, v179
	ds_write_b128 v210, v[176:179]
	v_mul_f32_e32 v180, v27, v180
	v_mul_f32_e32 v181, v27, v181
	v_mul_f32_e32 v182, v27, v182
	v_mul_f32_e32 v183, v27, v183
	ds_write_b128 v210, v[180:183] offset:1024
	v_mul_f32_e32 v184, v28, v184
	v_mul_f32_e32 v185, v28, v185
	v_mul_f32_e32 v186, v28, v186
	v_mul_f32_e32 v187, v28, v187
	ds_write_b128 v210, v[184:187] offset:2048
	v_mul_f32_e32 v188, v29, v188
	v_mul_f32_e32 v189, v29, v189
	v_mul_f32_e32 v190, v29, v190
	v_mul_f32_e32 v191, v29, v191
	ds_write_b128 v210, v[188:191] offset:3072
	v_mul_f32_e32 v192, v30, v192
	v_mul_f32_e32 v193, v30, v193
	v_mul_f32_e32 v194, v30, v194
	v_mul_f32_e32 v195, v30, v195
	ds_write_b128 v210, v[192:195] offset:4096
	v_mul_f32_e32 v196, v31, v196
	v_mul_f32_e32 v197, v31, v197
	v_mul_f32_e32 v198, v31, v198
	v_mul_f32_e32 v199, v31, v199
	ds_write_b128 v210, v[196:199] offset:5120
	v_mul_f32_e32 v200, v32, v200
	v_mul_f32_e32 v201, v32, v201
	v_mul_f32_e32 v202, v32, v202
	v_mul_f32_e32 v203, v32, v203
	ds_write_b128 v210, v[200:203] offset:6144
	v_mul_f32_e32 v204, v33, v204
	v_mul_f32_e32 v205, v33, v205
	v_mul_f32_e32 v206, v33, v206
	v_mul_f32_e32 v207, v33, v207
	ds_write_b128 v210, v[204:207] offset:7168
	s_waitcnt lgkmcnt(0)
	s_barrier
; #define GAS __attribute__((address_space(1)))
; #define LAS __attribute__((address_space(3)))
; #define LDS_WAIT() asm volatile("s_waitcnt lgkmcnt(0)" ::: "memory")
;     ...
; #pragma unroll
;     for (int i = 0; i < 32; ++i) v[i] = sc >= 0 ? W[(size_t)(k0 + 2 * i + (lane >> 5)) * Nsrc + sc] : 0.f;
; #pragma unroll
;     for (int i = 0; i < 32; ++i) { const int k = k0 + 2 * i + (lane >> 5); float x = v[i] * wscale; if (KS) x *= (k < ksplit ? ksA[k] : ksB[k - ksplit]); scr[(2 * i + (lane >> 5)) * 33 + (lane & 31)] = x; }
;     LDS_WAIT(); asm volatile("" ::: "memory");
;     const int c = lane & 7;
; #pragma unroll
;     for (int j = 0; j < 4; ++j) { const int n = (lane >> 3) + 8 * j; const LAS float* s = scr + (8 * c) * 33 + n;
;         const unsigned long long o = (unsigned long long)pg8::pk4_fp8(s[0 * 33], s[1 * 33], s[2 * 33], s[3 * 33]) | ((unsigned long long)pg8::pk4_fp8(s[4 * 33], s[5 * 33], s[6 * 33], s[7 * 33]) << 32);
;         *(GAS unsigned long long*)(WT + (size_t)(n0 + n) * K + k0 + 8 * c) = o; }
	s_add_u32 s8, s30, 0xb000
	s_addc_u32 s9, s31, 0
	global_load_dwordx4 v[176:179], v74, s[8:9]
	s_add_u32 s8, s8, 0x20000
	s_addc_u32 s9, s9, 0
	global_load_dwordx4 v[180:183], v74, s[8:9]
	s_add_u32 s8, s8, 0x20000
	s_addc_u32 s9, s9, 0
	global_load_dwordx4 v[184:187], v74, s[8:9]
	s_add_u32 s8, s8, 0x20000
	s_addc_u32 s9, s9, 0
	global_load_dwordx4 v[188:191], v74, s[8:9]
	s_add_u32 s8, s8, 0x20000
	s_addc_u32 s9, s9, 0
	global_load_dwordx4 v[192:195], v74, s[8:9]
	s_add_u32 s8, s8, 0x20000
	s_addc_u32 s9, s9, 0
	global_load_dwordx4 v[196:199], v74, s[8:9]
	s_add_u32 s8, s8, 0x20000
	s_addc_u32 s9, s9, 0
	global_load_dwordx4 v[200:203], v74, s[8:9]
	s_add_u32 s8, s8, 0x20000
	s_addc_u32 s9, s9, 0
	global_load_dwordx4 v[204:207], v74, s[8:9]
	s_add_u32 s6, s32, 0x2400000
	s_addc_u32 s7, s33, 0
	ds_read_b32 v226, v212
	ds_read_b32 v227, v212 offset:512
	ds_read_b32 v228, v212 offset:1024
	ds_read_b32 v229, v212 offset:1536
	ds_read_b32 v230, v212 offset:2048
	ds_read_b32 v231, v212 offset:2560
	ds_read_b32 v232, v212 offset:3072
	ds_read_b32 v233, v212 offset:3584
	ds_read_b32 v234, v212 offset:4096
	ds_read_b32 v235, v212 offset:4608
	ds_read_b32 v236, v212 offset:5120
	ds_read_b32 v237, v212 offset:5632
	ds_read_b32 v238, v212 offset:6144
	ds_read_b32 v239, v212 offset:6656
	ds_read_b32 v240, v212 offset:7168
	ds_read_b32 v241, v212 offset:7680
	s_waitcnt lgkmcnt(0)
	v_max_f32_e32 v226, v226, v226
	v_max_f32_e32 v227, v227, v227
	v_max_f32_e32 v228, v228, v228
	v_max_f32_e32 v229, v229, v229
	v_max_f32_e32 v230, v230, v230
	v_max_f32_e32 v231, v231, v231
	v_max_f32_e32 v232, v232, v232
	v_max_f32_e32 v233, v233, v233
	v_max_f32_e32 v234, v234, v234
	v_max_f32_e32 v235, v235, v235
	v_max_f32_e32 v236, v236, v236
	v_max_f32_e32 v237, v237, v237
	v_max_f32_e32 v238, v238, v238
	v_max_f32_e32 v239, v239, v239
	v_max_f32_e32 v240, v240, v240
	v_max_f32_e32 v241, v241, v241
	v_med3_f32 v226, v226, s62, v95
	v_med3_f32 v227, v227, s62, v95
	v_med3_f32 v228, v228, s62, v95
	v_med3_f32 v229, v229, s62, v95
	v_med3_f32 v230, v230, s62, v95
	v_med3_f32 v231, v231, s62, v95
	v_med3_f32 v232, v232, s62, v95
	v_med3_f32 v233, v233, s62, v95
	v_med3_f32 v234, v234, s62, v95
	v_med3_f32 v235, v235, s62, v95
	v_med3_f32 v236, v236, s62, v95
	v_med3_f32 v237, v237, s62, v95
	v_med3_f32 v238, v238, s62, v95
	v_med3_f32 v239, v239, s62, v95
	v_med3_f32 v240, v240, s62, v95
	v_med3_f32 v241, v241, s62, v95
	v_mov_b32_e32 v242, 0
	v_mov_b32_e32 v243, 0
	v_mov_b32_e32 v244, 0
	v_mov_b32_e32 v245, 0
	v_cvt_pk_fp8_f32 v242, v226, v227
	v_cvt_pk_fp8_f32 v243, v230, v231
	v_cvt_pk_fp8_f32 v244, v234, v235
	v_cvt_pk_fp8_f32 v245, v238, v239
	v_cvt_pk_fp8_f32 v242, v228, v229 op_sel:[0,0,1]
	v_cvt_pk_fp8_f32 v243, v232, v233 op_sel:[0,0,1]
	v_cvt_pk_fp8_f32 v244, v236, v237 op_sel:[0,0,1]
	v_cvt_pk_fp8_f32 v245, v240, v241 op_sel:[0,0,1]
	s_nop 0
	global_store_dwordx4 v77, v[242:245], s[6:7]
	ds_read_b32 v226, v214
	ds_read_b32 v227, v214 offset:512
	ds_read_b32 v228, v214 offset:1024
	ds_read_b32 v229, v214 offset:1536
	ds_read_b32 v230, v214 offset:2048
	ds_read_b32 v231, v214 offset:2560
	ds_read_b32 v232, v214 offset:3072
	ds_read_b32 v233, v214 offset:3584
	ds_read_b32 v234, v214 offset:4096
	ds_read_b32 v235, v214 offset:4608
	ds_read_b32 v236, v214 offset:5120
	ds_read_b32 v237, v214 offset:5632
	ds_read_b32 v238, v214 offset:6144
	ds_read_b32 v239, v214 offset:6656
	ds_read_b32 v240, v214 offset:7168
	ds_read_b32 v241, v214 offset:7680
	s_waitcnt lgkmcnt(0)
	v_max_f32_e32 v226, v226, v226
	v_max_f32_e32 v227, v227, v227
	v_max_f32_e32 v228, v228, v228
	v_max_f32_e32 v229, v229, v229
	v_max_f32_e32 v230, v230, v230
	v_max_f32_e32 v231, v231, v231
	v_max_f32_e32 v232, v232, v232
	v_max_f32_e32 v233, v233, v233
	v_max_f32_e32 v234, v234, v234
	v_max_f32_e32 v235, v235, v235
	v_max_f32_e32 v236, v236, v236
	v_max_f32_e32 v237, v237, v237
	v_max_f32_e32 v238, v238, v238
	v_max_f32_e32 v239, v239, v239
	v_max_f32_e32 v240, v240, v240
	v_max_f32_e32 v241, v241, v241
	v_med3_f32 v226, v226, s62, v95
	v_med3_f32 v227, v227, s62, v95
	v_med3_f32 v228, v228, s62, v95
	v_med3_f32 v229, v229, s62, v95
	v_med3_f32 v230, v230, s62, v95
	v_med3_f32 v231, v231, s62, v95
	v_med3_f32 v232, v232, s62, v95
	v_med3_f32 v233, v233, s62, v95
	v_med3_f32 v234, v234, s62, v95
	v_med3_f32 v235, v235, s62, v95
	v_med3_f32 v236, v236, s62, v95
	v_med3_f32 v237, v237, s62, v95
	v_med3_f32 v238, v238, s62, v95
	v_med3_f32 v239, v239, s62, v95
	v_med3_f32 v240, v240, s62, v95
	v_med3_f32 v241, v241, s62, v95
	v_mov_b32_e32 v242, 0
	v_mov_b32_e32 v243, 0
	v_mov_b32_e32 v244, 0
	v_mov_b32_e32 v245, 0
	v_cvt_pk_fp8_f32 v242, v226, v227
	v_cvt_pk_fp8_f32 v243, v230, v231
	v_cvt_pk_fp8_f32 v244, v234, v235
	v_cvt_pk_fp8_f32 v245, v238, v239
	v_cvt_pk_fp8_f32 v242, v228, v229 op_sel:[0,0,1]
	v_cvt_pk_fp8_f32 v243, v232, v233 op_sel:[0,0,1]
	v_cvt_pk_fp8_f32 v244, v236, v237 op_sel:[0,0,1]
	v_cvt_pk_fp8_f32 v245, v240, v241 op_sel:[0,0,1]
	s_nop 0
	global_store_dwordx4 v78, v[242:245], s[6:7]
	s_waitcnt vmcnt(12)
	v_mul_f32_e32 v144, v26, v144
	v_mul_f32_e32 v145, v26, v145
	v_mul_f32_e32 v146, v26, v146
	v_mul_f32_e32 v147, v26, v147
	ds_write_b128 v209, v[144:147]
	v_mul_f32_e32 v148, v27, v148
	v_mul_f32_e32 v149, v27, v149
	v_mul_f32_e32 v150, v27, v150
	v_mul_f32_e32 v151, v27, v151
	ds_write_b128 v209, v[148:151] offset:1024
	v_mul_f32_e32 v152, v28, v152
	v_mul_f32_e32 v153, v28, v153
	v_mul_f32_e32 v154, v28, v154
	v_mul_f32_e32 v155, v28, v155
	ds_write_b128 v209, v[152:155] offset:2048
	v_mul_f32_e32 v156, v29, v156
	v_mul_f32_e32 v157, v29, v157
	v_mul_f32_e32 v158, v29, v158
	v_mul_f32_e32 v159, v29, v159
	ds_write_b128 v209, v[156:159] offset:3072
	v_mul_f32_e32 v160, v30, v160
	v_mul_f32_e32 v161, v30, v161
	v_mul_f32_e32 v162, v30, v162
	v_mul_f32_e32 v163, v30, v163
	ds_write_b128 v209, v[160:163] offset:4096
	v_mul_f32_e32 v164, v31, v164
	v_mul_f32_e32 v165, v31, v165
	v_mul_f32_e32 v166, v31, v166
	v_mul_f32_e32 v167, v31, v167
	ds_write_b128 v209, v[164:167] offset:5120
	v_mul_f32_e32 v168, v32, v168
	v_mul_f32_e32 v169, v32, v169
	v_mul_f32_e32 v170, v32, v170
	v_mul_f32_e32 v171, v32, v171
	ds_write_b128 v209, v[168:171] offset:6144
	v_mul_f32_e32 v172, v33, v172
	v_mul_f32_e32 v173, v33, v173
	v_mul_f32_e32 v174, v33, v174
	v_mul_f32_e32 v175, v33, v175
	ds_write_b128 v209, v[172:175] offset:7168
	s_waitcnt lgkmcnt(0)
	s_barrier
; #define GAS __attribute__((address_space(1)))
; #define LAS __attribute__((address_space(3)))
; #define LDS_WAIT() asm volatile("s_waitcnt lgkmcnt(0)" ::: "memory")
;     ...
; #pragma unroll
;     for (int i = 0; i < 32; ++i) v[i] = sc >= 0 ? W[(size_t)(k0 + 2 * i + (lane >> 5)) * Nsrc + sc] : 0.f;
; #pragma unroll
;     for (int i = 0; i < 32; ++i) { const int k = k0 + 2 * i + (lane >> 5); float x = v[i] * wscale; if (KS) x *= (k < ksplit ? ksA[k] : ksB[k - ksplit]); scr[(2 * i + (lane >> 5)) * 33 + (lane & 31)] = x; }
;     LDS_WAIT(); asm volatile("" ::: "memory");
;     const int c = lane & 7;
; #pragma unroll
;     for (int j = 0; j < 4; ++j) { const int n = (lane >> 3) + 8 * j; const LAS float* s = scr + (8 * c) * 33 + n;
;         const unsigned long long o = (unsigned long long)pg8::pk4_fp8(s[0 * 33], s[1 * 33], s[2 * 33], s[3 * 33]) | ((unsigned long long)pg8::pk4_fp8(s[4 * 33], s[5 * 33], s[6 * 33], s[7 * 33]) << 32);
;         *(GAS unsigned long long*)(WT + (size_t)(n0 + n) * K + k0 + 8 * c) = o; }
	s_add_u32 s8, s30, 0xc000
	s_addc_u32 s9, s31, 0
	global_load_dwordx4 v[144:147], v74, s[8:9]
	s_add_u32 s8, s8, 0x20000
	s_addc_u32 s9, s9, 0
	global_load_dwordx4 v[148:151], v74, s[8:9]
	s_add_u32 s8, s8, 0x20000
	s_addc_u32 s9, s9, 0
	global_load_dwordx4 v[152:155], v74, s[8:9]
	s_add_u32 s8, s8, 0x20000
	s_addc_u32 s9, s9, 0
	global_load_dwordx4 v[156:159], v74, s[8:9]
	s_add_u32 s8, s8, 0x20000
	s_addc_u32 s9, s9, 0
	global_load_dwordx4 v[160:163], v74, s[8:9]
	s_add_u32 s8, s8, 0x20000
	s_addc_u32 s9, s9, 0
	global_load_dwordx4 v[164:167], v74, s[8:9]
	s_add_u32 s8, s8, 0x20000
	s_addc_u32 s9, s9, 0
	global_load_dwordx4 v[168:171], v74, s[8:9]
	s_add_u32 s8, s8, 0x20000
	s_addc_u32 s9, s9, 0
	global_load_dwordx4 v[172:175], v74, s[8:9]
	s_add_u32 s6, s32, 0x2800000
	s_addc_u32 s7, s33, 0
	ds_read_b32 v226, v211
	ds_read_b32 v227, v211 offset:512
	ds_read_b32 v228, v211 offset:1024
	ds_read_b32 v229, v211 offset:1536
	ds_read_b32 v230, v211 offset:2048
	ds_read_b32 v231, v211 offset:2560
	ds_read_b32 v232, v211 offset:3072
	ds_read_b32 v233, v211 offset:3584
	ds_read_b32 v234, v211 offset:4096
	ds_read_b32 v235, v211 offset:4608
	ds_read_b32 v236, v211 offset:5120
	ds_read_b32 v237, v211 offset:5632
	ds_read_b32 v238, v211 offset:6144
	ds_read_b32 v239, v211 offset:6656
	ds_read_b32 v240, v211 offset:7168
	ds_read_b32 v241, v211 offset:7680
	s_waitcnt lgkmcnt(0)
	v_max_f32_e32 v226, v226, v226
	v_max_f32_e32 v227, v227, v227
	v_max_f32_e32 v228, v228, v228
	v_max_f32_e32 v229, v229, v229
	v_max_f32_e32 v230, v230, v230
	v_max_f32_e32 v231, v231, v231
	v_max_f32_e32 v232, v232, v232
	v_max_f32_e32 v233, v233, v233
	v_max_f32_e32 v234, v234, v234
	v_max_f32_e32 v235, v235, v235
	v_max_f32_e32 v236, v236, v236
	v_max_f32_e32 v237, v237, v237
	v_max_f32_e32 v238, v238, v238
	v_max_f32_e32 v239, v239, v239
	v_max_f32_e32 v240, v240, v240
	v_max_f32_e32 v241, v241, v241
	v_med3_f32 v226, v226, s62, v95
	v_med3_f32 v227, v227, s62, v95
	v_med3_f32 v228, v228, s62, v95
	v_med3_f32 v229, v229, s62, v95
	v_med3_f32 v230, v230, s62, v95
	v_med3_f32 v231, v231, s62, v95
	v_med3_f32 v232, v232, s62, v95
	v_med3_f32 v233, v233, s62, v95
	v_med3_f32 v234, v234, s62, v95
	v_med3_f32 v235, v235, s62, v95
	v_med3_f32 v236, v236, s62, v95
	v_med3_f32 v237, v237, s62, v95
	v_med3_f32 v238, v238, s62, v95
	v_med3_f32 v239, v239, s62, v95
	v_med3_f32 v240, v240, s62, v95
	v_med3_f32 v241, v241, s62, v95
	v_mov_b32_e32 v242, 0
	v_mov_b32_e32 v243, 0
	v_mov_b32_e32 v244, 0
	v_mov_b32_e32 v245, 0
	v_cvt_pk_fp8_f32 v242, v226, v227
	v_cvt_pk_fp8_f32 v243, v230, v231
	v_cvt_pk_fp8_f32 v244, v234, v235
	v_cvt_pk_fp8_f32 v245, v238, v239
	v_cvt_pk_fp8_f32 v242, v228, v229 op_sel:[0,0,1]
	v_cvt_pk_fp8_f32 v243, v232, v233 op_sel:[0,0,1]
	v_cvt_pk_fp8_f32 v244, v236, v237 op_sel:[0,0,1]
	v_cvt_pk_fp8_f32 v245, v240, v241 op_sel:[0,0,1]
	s_nop 0
	global_store_dwordx4 v77, v[242:245], s[6:7]
	ds_read_b32 v226, v213
	ds_read_b32 v227, v213 offset:512
	ds_read_b32 v228, v213 offset:1024
	ds_read_b32 v229, v213 offset:1536
	ds_read_b32 v230, v213 offset:2048
	ds_read_b32 v231, v213 offset:2560
	ds_read_b32 v232, v213 offset:3072
	ds_read_b32 v233, v213 offset:3584
	ds_read_b32 v234, v213 offset:4096
	ds_read_b32 v235, v213 offset:4608
	ds_read_b32 v236, v213 offset:5120
	ds_read_b32 v237, v213 offset:5632
	ds_read_b32 v238, v213 offset:6144
	ds_read_b32 v239, v213 offset:6656
	ds_read_b32 v240, v213 offset:7168
	ds_read_b32 v241, v213 offset:7680
	s_waitcnt lgkmcnt(0)
	v_max_f32_e32 v226, v226, v226
	v_max_f32_e32 v227, v227, v227
	v_max_f32_e32 v228, v228, v228
	v_max_f32_e32 v229, v229, v229
	v_max_f32_e32 v230, v230, v230
	v_max_f32_e32 v231, v231, v231
	v_max_f32_e32 v232, v232, v232
	v_max_f32_e32 v233, v233, v233
	v_max_f32_e32 v234, v234, v234
	v_max_f32_e32 v235, v235, v235
	v_max_f32_e32 v236, v236, v236
	v_max_f32_e32 v237, v237, v237
	v_max_f32_e32 v238, v238, v238
	v_max_f32_e32 v239, v239, v239
	v_max_f32_e32 v240, v240, v240
	v_max_f32_e32 v241, v241, v241
	v_med3_f32 v226, v226, s62, v95
	v_med3_f32 v227, v227, s62, v95
	v_med3_f32 v228, v228, s62, v95
	v_med3_f32 v229, v229, s62, v95
	v_med3_f32 v230, v230, s62, v95
	v_med3_f32 v231, v231, s62, v95
	v_med3_f32 v232, v232, s62, v95
	v_med3_f32 v233, v233, s62, v95
	v_med3_f32 v234, v234, s62, v95
	v_med3_f32 v235, v235, s62, v95
	v_med3_f32 v236, v236, s62, v95
	v_med3_f32 v237, v237, s62, v95
	v_med3_f32 v238, v238, s62, v95
	v_med3_f32 v239, v239, s62, v95
	v_med3_f32 v240, v240, s62, v95
	v_med3_f32 v241, v241, s62, v95
	v_mov_b32_e32 v242, 0
	v_mov_b32_e32 v243, 0
	v_mov_b32_e32 v244, 0
	v_mov_b32_e32 v245, 0
	v_cvt_pk_fp8_f32 v242, v226, v227
	v_cvt_pk_fp8_f32 v243, v230, v231
	v_cvt_pk_fp8_f32 v244, v234, v235
	v_cvt_pk_fp8_f32 v245, v238, v239
	v_cvt_pk_fp8_f32 v242, v228, v229 op_sel:[0,0,1]
	v_cvt_pk_fp8_f32 v243, v232, v233 op_sel:[0,0,1]
	v_cvt_pk_fp8_f32 v244, v236, v237 op_sel:[0,0,1]
	v_cvt_pk_fp8_f32 v245, v240, v241 op_sel:[0,0,1]
	s_nop 0
	global_store_dwordx4 v78, v[242:245], s[6:7]
	s_waitcnt vmcnt(12)
	v_mul_f32_e32 v176, v26, v176
	v_mul_f32_e32 v177, v26, v177
	v_mul_f32_e32 v178, v26, v178
	v_mul_f32_e32 v179, v26, v179
	ds_write_b128 v210, v[176:179]
	v_mul_f32_e32 v180, v27, v180
	v_mul_f32_e32 v181, v27, v181
	v_mul_f32_e32 v182, v27, v182
	v_mul_f32_e32 v183, v27, v183
	ds_write_b128 v210, v[180:183] offset:1024
	v_mul_f32_e32 v184, v28, v184
	v_mul_f32_e32 v185, v28, v185
	v_mul_f32_e32 v186, v28, v186
	v_mul_f32_e32 v187, v28, v187
	ds_write_b128 v210, v[184:187] offset:2048
	v_mul_f32_e32 v188, v29, v188
	v_mul_f32_e32 v189, v29, v189
	v_mul_f32_e32 v190, v29, v190
	v_mul_f32_e32 v191, v29, v191
	ds_write_b128 v210, v[188:191] offset:3072
	v_mul_f32_e32 v192, v30, v192
	v_mul_f32_e32 v193, v30, v193
	v_mul_f32_e32 v194, v30, v194
	v_mul_f32_e32 v195, v30, v195
	ds_write_b128 v210, v[192:195] offset:4096
	v_mul_f32_e32 v196, v31, v196
	v_mul_f32_e32 v197, v31, v197
	v_mul_f32_e32 v198, v31, v198
	v_mul_f32_e32 v199, v31, v199
	ds_write_b128 v210, v[196:199] offset:5120
	v_mul_f32_e32 v200, v32, v200
	v_mul_f32_e32 v201, v32, v201
	v_mul_f32_e32 v202, v32, v202
	v_mul_f32_e32 v203, v32, v203
	ds_write_b128 v210, v[200:203] offset:6144
	v_mul_f32_e32 v204, v33, v204
	v_mul_f32_e32 v205, v33, v205
	v_mul_f32_e32 v206, v33, v206
	v_mul_f32_e32 v207, v33, v207
	ds_write_b128 v210, v[204:207] offset:7168
	s_waitcnt lgkmcnt(0)
	s_barrier
; #define GAS __attribute__((address_space(1)))
; #define LAS __attribute__((address_space(3)))
; #define LDS_WAIT() asm volatile("s_waitcnt lgkmcnt(0)" ::: "memory")
;     ...
; #pragma unroll
;     for (int i = 0; i < 32; ++i) v[i] = sc >= 0 ? W[(size_t)(k0 + 2 * i + (lane >> 5)) * Nsrc + sc] : 0.f;
; #pragma unroll
;     for (int i = 0; i < 32; ++i) { const int k = k0 + 2 * i + (lane >> 5); float x = v[i] * wscale; if (KS) x *= (k < ksplit ? ksA[k] : ksB[k - ksplit]); scr[(2 * i + (lane >> 5)) * 33 + (lane & 31)] = x; }
;     LDS_WAIT(); asm volatile("" ::: "memory");
;     const int c = lane & 7;
; #pragma unroll
;     for (int j = 0; j < 4; ++j) { const int n = (lane >> 3) + 8 * j; const LAS float* s = scr + (8 * c) * 33 + n;
;         const unsigned long long o = (unsigned long long)pg8::pk4_fp8(s[0 * 33], s[1 * 33], s[2 * 33], s[3 * 33]) | ((unsigned long long)pg8::pk4_fp8(s[4 * 33], s[5 * 33], s[6 * 33], s[7 * 33]) << 32);
;         *(GAS unsigned long long*)(WT + (size_t)(n0 + n) * K + k0 + 8 * c) = o; }
	s_add_u32 s8, s30, 0xd000
	s_addc_u32 s9, s31, 0
	global_load_dwordx4 v[176:179], v74, s[8:9]
	s_add_u32 s8, s8, 0x20000
	s_addc_u32 s9, s9, 0
	global_load_dwordx4 v[180:183], v74, s[8:9]
	s_add_u32 s8, s8, 0x20000
	s_addc_u32 s9, s9, 0
	global_load_dwordx4 v[184:187], v74, s[8:9]
	s_add_u32 s8, s8, 0x20000
	s_addc_u32 s9, s9, 0
	global_load_dwordx4 v[188:191], v74, s[8:9]
	s_add_u32 s8, s8, 0x20000
	s_addc_u32 s9, s9, 0
	global_load_dwordx4 v[192:195], v74, s[8:9]
	s_add_u32 s8, s8, 0x20000
	s_addc_u32 s9, s9, 0
	global_load_dwordx4 v[196:199], v74, s[8:9]
	s_add_u32 s8, s8, 0x20000
	s_addc_u32 s9, s9, 0
	global_load_dwordx4 v[200:203], v74, s[8:9]
	s_add_u32 s8, s8, 0x20000
	s_addc_u32 s9, s9, 0
	global_load_dwordx4 v[204:207], v74, s[8:9]
	s_add_u32 s6, s32, 0x2c00000
	s_addc_u32 s7, s33, 0
	ds_read_b32 v226, v212
	ds_read_b32 v227, v212 offset:512
	ds_read_b32 v228, v212 offset:1024
	ds_read_b32 v229, v212 offset:1536
	ds_read_b32 v230, v212 offset:2048
	ds_read_b32 v231, v212 offset:2560
	ds_read_b32 v232, v212 offset:3072
	ds_read_b32 v233, v212 offset:3584
	ds_read_b32 v234, v212 offset:4096
	ds_read_b32 v235, v212 offset:4608
	ds_read_b32 v236, v212 offset:5120
	ds_read_b32 v237, v212 offset:5632
	ds_read_b32 v238, v212 offset:6144
	ds_read_b32 v239, v212 offset:6656
	ds_read_b32 v240, v212 offset:7168
	ds_read_b32 v241, v212 offset:7680
	s_waitcnt lgkmcnt(0)
	v_max_f32_e32 v226, v226, v226
	v_max_f32_e32 v227, v227, v227
	v_max_f32_e32 v228, v228, v228
	v_max_f32_e32 v229, v229, v229
	v_max_f32_e32 v230, v230, v230
	v_max_f32_e32 v231, v231, v231
	v_max_f32_e32 v232, v232, v232
	v_max_f32_e32 v233, v233, v233
	v_max_f32_e32 v234, v234, v234
	v_max_f32_e32 v235, v235, v235
	v_max_f32_e32 v236, v236, v236
	v_max_f32_e32 v237, v237, v237
	v_max_f32_e32 v238, v238, v238
	v_max_f32_e32 v239, v239, v239
	v_max_f32_e32 v240, v240, v240
	v_max_f32_e32 v241, v241, v241
	v_med3_f32 v226, v226, s62, v95
	v_med3_f32 v227, v227, s62, v95
	v_med3_f32 v228, v228, s62, v95
	v_med3_f32 v229, v229, s62, v95
	v_med3_f32 v230, v230, s62, v95
	v_med3_f32 v231, v231, s62, v95
	v_med3_f32 v232, v232, s62, v95
	v_med3_f32 v233, v233, s62, v95
	v_med3_f32 v234, v234, s62, v95
	v_med3_f32 v235, v235, s62, v95
	v_med3_f32 v236, v236, s62, v95
	v_med3_f32 v237, v237, s62, v95
	v_med3_f32 v238, v238, s62, v95
	v_med3_f32 v239, v239, s62, v95
	v_med3_f32 v240, v240, s62, v95
	v_med3_f32 v241, v241, s62, v95
	v_mov_b32_e32 v242, 0
	v_mov_b32_e32 v243, 0
	v_mov_b32_e32 v244, 0
	v_mov_b32_e32 v245, 0
	v_cvt_pk_fp8_f32 v242, v226, v227
	v_cvt_pk_fp8_f32 v243, v230, v231
	v_cvt_pk_fp8_f32 v244, v234, v235
	v_cvt_pk_fp8_f32 v245, v238, v239
	v_cvt_pk_fp8_f32 v242, v228, v229 op_sel:[0,0,1]
	v_cvt_pk_fp8_f32 v243, v232, v233 op_sel:[0,0,1]
	v_cvt_pk_fp8_f32 v244, v236, v237 op_sel:[0,0,1]
	v_cvt_pk_fp8_f32 v245, v240, v241 op_sel:[0,0,1]
	s_nop 0
	global_store_dwordx4 v77, v[242:245], s[6:7]
	ds_read_b32 v226, v214
	ds_read_b32 v227, v214 offset:512
	ds_read_b32 v228, v214 offset:1024
	ds_read_b32 v229, v214 offset:1536
	ds_read_b32 v230, v214 offset:2048
	ds_read_b32 v231, v214 offset:2560
	ds_read_b32 v232, v214 offset:3072
	ds_read_b32 v233, v214 offset:3584
	ds_read_b32 v234, v214 offset:4096
	ds_read_b32 v235, v214 offset:4608
	ds_read_b32 v236, v214 offset:5120
	ds_read_b32 v237, v214 offset:5632
	ds_read_b32 v238, v214 offset:6144
	ds_read_b32 v239, v214 offset:6656
	ds_read_b32 v240, v214 offset:7168
	ds_read_b32 v241, v214 offset:7680
	s_waitcnt lgkmcnt(0)
	v_max_f32_e32 v226, v226, v226
	v_max_f32_e32 v227, v227, v227
	v_max_f32_e32 v228, v228, v228
	v_max_f32_e32 v229, v229, v229
	v_max_f32_e32 v230, v230, v230
	v_max_f32_e32 v231, v231, v231
	v_max_f32_e32 v232, v232, v232
	v_max_f32_e32 v233, v233, v233
	v_max_f32_e32 v234, v234, v234
	v_max_f32_e32 v235, v235, v235
	v_max_f32_e32 v236, v236, v236
	v_max_f32_e32 v237, v237, v237
	v_max_f32_e32 v238, v238, v238
	v_max_f32_e32 v239, v239, v239
	v_max_f32_e32 v240, v240, v240
	v_max_f32_e32 v241, v241, v241
	v_med3_f32 v226, v226, s62, v95
	v_med3_f32 v227, v227, s62, v95
	v_med3_f32 v228, v228, s62, v95
	v_med3_f32 v229, v229, s62, v95
	v_med3_f32 v230, v230, s62, v95
	v_med3_f32 v231, v231, s62, v95
	v_med3_f32 v232, v232, s62, v95
	v_med3_f32 v233, v233, s62, v95
	v_med3_f32 v234, v234, s62, v95
	v_med3_f32 v235, v235, s62, v95
	v_med3_f32 v236, v236, s62, v95
	v_med3_f32 v237, v237, s62, v95
	v_med3_f32 v238, v238, s62, v95
	v_med3_f32 v239, v239, s62, v95
	v_med3_f32 v240, v240, s62, v95
	v_med3_f32 v241, v241, s62, v95
	v_mov_b32_e32 v242, 0
	v_mov_b32_e32 v243, 0
	v_mov_b32_e32 v244, 0
	v_mov_b32_e32 v245, 0
	v_cvt_pk_fp8_f32 v242, v226, v227
	v_cvt_pk_fp8_f32 v243, v230, v231
	v_cvt_pk_fp8_f32 v244, v234, v235
	v_cvt_pk_fp8_f32 v245, v238, v239
	v_cvt_pk_fp8_f32 v242, v228, v229 op_sel:[0,0,1]
	v_cvt_pk_fp8_f32 v243, v232, v233 op_sel:[0,0,1]
	v_cvt_pk_fp8_f32 v244, v236, v237 op_sel:[0,0,1]
	v_cvt_pk_fp8_f32 v245, v240, v241 op_sel:[0,0,1]
	s_nop 0
	global_store_dwordx4 v78, v[242:245], s[6:7]
	s_waitcnt vmcnt(12)
	v_mul_f32_e32 v144, v26, v144
	v_mul_f32_e32 v145, v26, v145
	v_mul_f32_e32 v146, v26, v146
	v_mul_f32_e32 v147, v26, v147
	ds_write_b128 v209, v[144:147]
	v_mul_f32_e32 v148, v27, v148
	v_mul_f32_e32 v149, v27, v149
	v_mul_f32_e32 v150, v27, v150
	v_mul_f32_e32 v151, v27, v151
	ds_write_b128 v209, v[148:151] offset:1024
	v_mul_f32_e32 v152, v28, v152
	v_mul_f32_e32 v153, v28, v153
	v_mul_f32_e32 v154, v28, v154
	v_mul_f32_e32 v155, v28, v155
	ds_write_b128 v209, v[152:155] offset:2048
	v_mul_f32_e32 v156, v29, v156
	v_mul_f32_e32 v157, v29, v157
	v_mul_f32_e32 v158, v29, v158
	v_mul_f32_e32 v159, v29, v159
	ds_write_b128 v209, v[156:159] offset:3072
	v_mul_f32_e32 v160, v30, v160
	v_mul_f32_e32 v161, v30, v161
	v_mul_f32_e32 v162, v30, v162
	v_mul_f32_e32 v163, v30, v163
	ds_write_b128 v209, v[160:163] offset:4096
	v_mul_f32_e32 v164, v31, v164
	v_mul_f32_e32 v165, v31, v165
	v_mul_f32_e32 v166, v31, v166
	v_mul_f32_e32 v167, v31, v167
	ds_write_b128 v209, v[164:167] offset:5120
	v_mul_f32_e32 v168, v32, v168
	v_mul_f32_e32 v169, v32, v169
	v_mul_f32_e32 v170, v32, v170
	v_mul_f32_e32 v171, v32, v171
	ds_write_b128 v209, v[168:171] offset:6144
	v_mul_f32_e32 v172, v33, v172
	v_mul_f32_e32 v173, v33, v173
	v_mul_f32_e32 v174, v33, v174
	v_mul_f32_e32 v175, v33, v175
	ds_write_b128 v209, v[172:175] offset:7168
	s_waitcnt lgkmcnt(0)
	s_barrier
; #define GAS __attribute__((address_space(1)))
; #define LAS __attribute__((address_space(3)))
; #define LDS_WAIT() asm volatile("s_waitcnt lgkmcnt(0)" ::: "memory")
;     ...
; #pragma unroll
;     for (int i = 0; i < 32; ++i) v[i] = sc >= 0 ? W[(size_t)(k0 + 2 * i + (lane >> 5)) * Nsrc + sc] : 0.f;
; #pragma unroll
;     for (int i = 0; i < 32; ++i) { const int k = k0 + 2 * i + (lane >> 5); float x = v[i] * wscale; if (KS) x *= (k < ksplit ? ksA[k] : ksB[k - ksplit]); scr[(2 * i + (lane >> 5)) * 33 + (lane & 31)] = x; }
;     LDS_WAIT(); asm volatile("" ::: "memory");
;     const int c = lane & 7;
; #pragma unroll
;     for (int j = 0; j < 4; ++j) { const int n = (lane >> 3) + 8 * j; const LAS float* s = scr + (8 * c) * 33 + n;
;         const unsigned long long o = (unsigned long long)pg8::pk4_fp8(s[0 * 33], s[1 * 33], s[2 * 33], s[3 * 33]) | ((unsigned long long)pg8::pk4_fp8(s[4 * 33], s[5 * 33], s[6 * 33], s[7 * 33]) << 32);
;         *(GAS unsigned long long*)(WT + (size_t)(n0 + n) * K + k0 + 8 * c) = o; }
	s_add_u32 s8, s30, 0xe000
	s_addc_u32 s9, s31, 0
	global_load_dwordx4 v[144:147], v74, s[8:9]
	s_add_u32 s8, s8, 0x20000
	s_addc_u32 s9, s9, 0
	global_load_dwordx4 v[148:151], v74, s[8:9]
	s_add_u32 s8, s8, 0x20000
	s_addc_u32 s9, s9, 0
	global_load_dwordx4 v[152:155], v74, s[8:9]
	s_add_u32 s8, s8, 0x20000
	s_addc_u32 s9, s9, 0
	global_load_dwordx4 v[156:159], v74, s[8:9]
	s_add_u32 s8, s8, 0x20000
	s_addc_u32 s9, s9, 0
	global_load_dwordx4 v[160:163], v74, s[8:9]
	s_add_u32 s8, s8, 0x20000
	s_addc_u32 s9, s9, 0
	global_load_dwordx4 v[164:167], v74, s[8:9]
	s_add_u32 s8, s8, 0x20000
	s_addc_u32 s9, s9, 0
	global_load_dwordx4 v[168:171], v74, s[8:9]
	s_add_u32 s8, s8, 0x20000
	s_addc_u32 s9, s9, 0
	global_load_dwordx4 v[172:175], v74, s[8:9]
	s_add_u32 s6, s32, 0x3000000
	s_addc_u32 s7, s33, 0
	ds_read_b32 v226, v211
	ds_read_b32 v227, v211 offset:512
	ds_read_b32 v228, v211 offset:1024
	ds_read_b32 v229, v211 offset:1536
	ds_read_b32 v230, v211 offset:2048
	ds_read_b32 v231, v211 offset:2560
	ds_read_b32 v232, v211 offset:3072
	ds_read_b32 v233, v211 offset:3584
	ds_read_b32 v234, v211 offset:4096
	ds_read_b32 v235, v211 offset:4608
	ds_read_b32 v236, v211 offset:5120
	ds_read_b32 v237, v211 offset:5632
	ds_read_b32 v238, v211 offset:6144
	ds_read_b32 v239, v211 offset:6656
	ds_read_b32 v240, v211 offset:7168
	ds_read_b32 v241, v211 offset:7680
	s_waitcnt lgkmcnt(0)
	v_max_f32_e32 v226, v226, v226
	v_max_f32_e32 v227, v227, v227
	v_max_f32_e32 v228, v228, v228
	v_max_f32_e32 v229, v229, v229
	v_max_f32_e32 v230, v230, v230
	v_max_f32_e32 v231, v231, v231
	v_max_f32_e32 v232, v232, v232
	v_max_f32_e32 v233, v233, v233
	v_max_f32_e32 v234, v234, v234
	v_max_f32_e32 v235, v235, v235
	v_max_f32_e32 v236, v236, v236
	v_max_f32_e32 v237, v237, v237
	v_max_f32_e32 v238, v238, v238
	v_max_f32_e32 v239, v239, v239
	v_max_f32_e32 v240, v240, v240
	v_max_f32_e32 v241, v241, v241
	v_med3_f32 v226, v226, s62, v95
	v_med3_f32 v227, v227, s62, v95
	v_med3_f32 v228, v228, s62, v95
	v_med3_f32 v229, v229, s62, v95
	v_med3_f32 v230, v230, s62, v95
	v_med3_f32 v231, v231, s62, v95
	v_med3_f32 v232, v232, s62, v95
	v_med3_f32 v233, v233, s62, v95
	v_med3_f32 v234, v234, s62, v95
	v_med3_f32 v235, v235, s62, v95
	v_med3_f32 v236, v236, s62, v95
	v_med3_f32 v237, v237, s62, v95
	v_med3_f32 v238, v238, s62, v95
	v_med3_f32 v239, v239, s62, v95
	v_med3_f32 v240, v240, s62, v95
	v_med3_f32 v241, v241, s62, v95
	v_mov_b32_e32 v242, 0
	v_mov_b32_e32 v243, 0
	v_mov_b32_e32 v244, 0
	v_mov_b32_e32 v245, 0
	v_cvt_pk_fp8_f32 v242, v226, v227
	v_cvt_pk_fp8_f32 v243, v230, v231
	v_cvt_pk_fp8_f32 v244, v234, v235
	v_cvt_pk_fp8_f32 v245, v238, v239
	v_cvt_pk_fp8_f32 v242, v228, v229 op_sel:[0,0,1]
	v_cvt_pk_fp8_f32 v243, v232, v233 op_sel:[0,0,1]
	v_cvt_pk_fp8_f32 v244, v236, v237 op_sel:[0,0,1]
	v_cvt_pk_fp8_f32 v245, v240, v241 op_sel:[0,0,1]
	s_nop 0
	global_store_dwordx4 v77, v[242:245], s[6:7]
	ds_read_b32 v226, v213
	ds_read_b32 v227, v213 offset:512
	ds_read_b32 v228, v213 offset:1024
	ds_read_b32 v229, v213 offset:1536
	ds_read_b32 v230, v213 offset:2048
	ds_read_b32 v231, v213 offset:2560
	ds_read_b32 v232, v213 offset:3072
	ds_read_b32 v233, v213 offset:3584
	ds_read_b32 v234, v213 offset:4096
	ds_read_b32 v235, v213 offset:4608
	ds_read_b32 v236, v213 offset:5120
	ds_read_b32 v237, v213 offset:5632
	ds_read_b32 v238, v213 offset:6144
	ds_read_b32 v239, v213 offset:6656
	ds_read_b32 v240, v213 offset:7168
	ds_read_b32 v241, v213 offset:7680
	s_waitcnt lgkmcnt(0)
	v_max_f32_e32 v226, v226, v226
	v_max_f32_e32 v227, v227, v227
	v_max_f32_e32 v228, v228, v228
	v_max_f32_e32 v229, v229, v229
	v_max_f32_e32 v230, v230, v230
	v_max_f32_e32 v231, v231, v231
	v_max_f32_e32 v232, v232, v232
	v_max_f32_e32 v233, v233, v233
	v_max_f32_e32 v234, v234, v234
	v_max_f32_e32 v235, v235, v235
	v_max_f32_e32 v236, v236, v236
	v_max_f32_e32 v237, v237, v237
	v_max_f32_e32 v238, v238, v238
	v_max_f32_e32 v239, v239, v239
	v_max_f32_e32 v240, v240, v240
	v_max_f32_e32 v241, v241, v241
	v_med3_f32 v226, v226, s62, v95
	v_med3_f32 v227, v227, s62, v95
	v_med3_f32 v228, v228, s62, v95
	v_med3_f32 v229, v229, s62, v95
	v_med3_f32 v230, v230, s62, v95
	v_med3_f32 v231, v231, s62, v95
	v_med3_f32 v232, v232, s62, v95
	v_med3_f32 v233, v233, s62, v95
	v_med3_f32 v234, v234, s62, v95
	v_med3_f32 v235, v235, s62, v95
	v_med3_f32 v236, v236, s62, v95
	v_med3_f32 v237, v237, s62, v95
	v_med3_f32 v238, v238, s62, v95
	v_med3_f32 v239, v239, s62, v95
	v_med3_f32 v240, v240, s62, v95
	v_med3_f32 v241, v241, s62, v95
	v_mov_b32_e32 v242, 0
	v_mov_b32_e32 v243, 0
	v_mov_b32_e32 v244, 0
	v_mov_b32_e32 v245, 0
	v_cvt_pk_fp8_f32 v242, v226, v227
	v_cvt_pk_fp8_f32 v243, v230, v231
	v_cvt_pk_fp8_f32 v244, v234, v235
	v_cvt_pk_fp8_f32 v245, v238, v239
	v_cvt_pk_fp8_f32 v242, v228, v229 op_sel:[0,0,1]
	v_cvt_pk_fp8_f32 v243, v232, v233 op_sel:[0,0,1]
	v_cvt_pk_fp8_f32 v244, v236, v237 op_sel:[0,0,1]
	v_cvt_pk_fp8_f32 v245, v240, v241 op_sel:[0,0,1]
	s_nop 0
	global_store_dwordx4 v78, v[242:245], s[6:7]
	s_waitcnt vmcnt(12)
	v_mul_f32_e32 v176, v26, v176
	v_mul_f32_e32 v177, v26, v177
	v_mul_f32_e32 v178, v26, v178
	v_mul_f32_e32 v179, v26, v179
	ds_write_b128 v210, v[176:179]
	v_mul_f32_e32 v180, v27, v180
	v_mul_f32_e32 v181, v27, v181
	v_mul_f32_e32 v182, v27, v182
	v_mul_f32_e32 v183, v27, v183
	ds_write_b128 v210, v[180:183] offset:1024
	v_mul_f32_e32 v184, v28, v184
	v_mul_f32_e32 v185, v28, v185
	v_mul_f32_e32 v186, v28, v186
	v_mul_f32_e32 v187, v28, v187
	ds_write_b128 v210, v[184:187] offset:2048
	v_mul_f32_e32 v188, v29, v188
	v_mul_f32_e32 v189, v29, v189
	v_mul_f32_e32 v190, v29, v190
	v_mul_f32_e32 v191, v29, v191
	ds_write_b128 v210, v[188:191] offset:3072
	v_mul_f32_e32 v192, v30, v192
	v_mul_f32_e32 v193, v30, v193
	v_mul_f32_e32 v194, v30, v194
	v_mul_f32_e32 v195, v30, v195
	ds_write_b128 v210, v[192:195] offset:4096
	v_mul_f32_e32 v196, v31, v196
	v_mul_f32_e32 v197, v31, v197
	v_mul_f32_e32 v198, v31, v198
	v_mul_f32_e32 v199, v31, v199
	ds_write_b128 v210, v[196:199] offset:5120
	v_mul_f32_e32 v200, v32, v200
	v_mul_f32_e32 v201, v32, v201
	v_mul_f32_e32 v202, v32, v202
	v_mul_f32_e32 v203, v32, v203
	ds_write_b128 v210, v[200:203] offset:6144
	v_mul_f32_e32 v204, v33, v204
	v_mul_f32_e32 v205, v33, v205
	v_mul_f32_e32 v206, v33, v206
	v_mul_f32_e32 v207, v33, v207
	ds_write_b128 v210, v[204:207] offset:7168
	s_waitcnt lgkmcnt(0)
	s_barrier
; #define GAS __attribute__((address_space(1)))
; #define LAS __attribute__((address_space(3)))
; #define LDS_WAIT() asm volatile("s_waitcnt lgkmcnt(0)" ::: "memory")
;     ...
; #pragma unroll
;     for (int i = 0; i < 32; ++i) v[i] = sc >= 0 ? W[(size_t)(k0 + 2 * i + (lane >> 5)) * Nsrc + sc] : 0.f;
; #pragma unroll
;     for (int i = 0; i < 32; ++i) { const int k = k0 + 2 * i + (lane >> 5); float x = v[i] * wscale; if (KS) x *= (k < ksplit ? ksA[k] : ksB[k - ksplit]); scr[(2 * i + (lane >> 5)) * 33 + (lane & 31)] = x; }
;     LDS_WAIT(); asm volatile("" ::: "memory");
;     const int c = lane & 7;
; #pragma unroll
;     for (int j = 0; j < 4; ++j) { const int n = (lane >> 3) + 8 * j; const LAS float* s = scr + (8 * c) * 33 + n;
;         const unsigned long long o = (unsigned long long)pg8::pk4_fp8(s[0 * 33], s[1 * 33], s[2 * 33], s[3 * 33]) | ((unsigned long long)pg8::pk4_fp8(s[4 * 33], s[5 * 33], s[6 * 33], s[7 * 33]) << 32);
;         *(GAS unsigned long long*)(WT + (size_t)(n0 + n) * K + k0 + 8 * c) = o; }
	s_add_u32 s8, s30, 0xf000
	s_addc_u32 s9, s31, 0
	global_load_dwordx4 v[176:179], v74, s[8:9]
	s_add_u32 s8, s8, 0x20000
	s_addc_u32 s9, s9, 0
	global_load_dwordx4 v[180:183], v74, s[8:9]
	s_add_u32 s8, s8, 0x20000
	s_addc_u32 s9, s9, 0
	global_load_dwordx4 v[184:187], v74, s[8:9]
	s_add_u32 s8, s8, 0x20000
	s_addc_u32 s9, s9, 0
	global_load_dwordx4 v[188:191], v74, s[8:9]
	s_add_u32 s8, s8, 0x20000
	s_addc_u32 s9, s9, 0
	global_load_dwordx4 v[192:195], v74, s[8:9]
	s_add_u32 s8, s8, 0x20000
	s_addc_u32 s9, s9, 0
	global_load_dwordx4 v[196:199], v74, s[8:9]
	s_add_u32 s8, s8, 0x20000
	s_addc_u32 s9, s9, 0
	global_load_dwordx4 v[200:203], v74, s[8:9]
	s_add_u32 s8, s8, 0x20000
	s_addc_u32 s9, s9, 0
	global_load_dwordx4 v[204:207], v74, s[8:9]
	s_add_u32 s6, s32, 0x3400000
	s_addc_u32 s7, s33, 0
	ds_read_b32 v226, v212
	ds_read_b32 v227, v212 offset:512
	ds_read_b32 v228, v212 offset:1024
	ds_read_b32 v229, v212 offset:1536
	ds_read_b32 v230, v212 offset:2048
	ds_read_b32 v231, v212 offset:2560
	ds_read_b32 v232, v212 offset:3072
	ds_read_b32 v233, v212 offset:3584
	ds_read_b32 v234, v212 offset:4096
	ds_read_b32 v235, v212 offset:4608
	ds_read_b32 v236, v212 offset:5120
	ds_read_b32 v237, v212 offset:5632
	ds_read_b32 v238, v212 offset:6144
	ds_read_b32 v239, v212 offset:6656
	ds_read_b32 v240, v212 offset:7168
	ds_read_b32 v241, v212 offset:7680
	s_waitcnt lgkmcnt(0)
	v_max_f32_e32 v226, v226, v226
	v_max_f32_e32 v227, v227, v227
	v_max_f32_e32 v228, v228, v228
	v_max_f32_e32 v229, v229, v229
	v_max_f32_e32 v230, v230, v230
	v_max_f32_e32 v231, v231, v231
	v_max_f32_e32 v232, v232, v232
	v_max_f32_e32 v233, v233, v233
	v_max_f32_e32 v234, v234, v234
	v_max_f32_e32 v235, v235, v235
	v_max_f32_e32 v236, v236, v236
	v_max_f32_e32 v237, v237, v237
	v_max_f32_e32 v238, v238, v238
	v_max_f32_e32 v239, v239, v239
	v_max_f32_e32 v240, v240, v240
	v_max_f32_e32 v241, v241, v241
	v_med3_f32 v226, v226, s62, v95
	v_med3_f32 v227, v227, s62, v95
	v_med3_f32 v228, v228, s62, v95
	v_med3_f32 v229, v229, s62, v95
	v_med3_f32 v230, v230, s62, v95
	v_med3_f32 v231, v231, s62, v95
	v_med3_f32 v232, v232, s62, v95
	v_med3_f32 v233, v233, s62, v95
	v_med3_f32 v234, v234, s62, v95
	v_med3_f32 v235, v235, s62, v95
	v_med3_f32 v236, v236, s62, v95
	v_med3_f32 v237, v237, s62, v95
	v_med3_f32 v238, v238, s62, v95
	v_med3_f32 v239, v239, s62, v95
	v_med3_f32 v240, v240, s62, v95
	v_med3_f32 v241, v241, s62, v95
	v_mov_b32_e32 v242, 0
	v_mov_b32_e32 v243, 0
	v_mov_b32_e32 v244, 0
	v_mov_b32_e32 v245, 0
	v_cvt_pk_fp8_f32 v242, v226, v227
	v_cvt_pk_fp8_f32 v243, v230, v231
	v_cvt_pk_fp8_f32 v244, v234, v235
	v_cvt_pk_fp8_f32 v245, v238, v239
	v_cvt_pk_fp8_f32 v242, v228, v229 op_sel:[0,0,1]
	v_cvt_pk_fp8_f32 v243, v232, v233 op_sel:[0,0,1]
	v_cvt_pk_fp8_f32 v244, v236, v237 op_sel:[0,0,1]
	v_cvt_pk_fp8_f32 v245, v240, v241 op_sel:[0,0,1]
	s_nop 0
	global_store_dwordx4 v77, v[242:245], s[6:7]
	ds_read_b32 v226, v214
	ds_read_b32 v227, v214 offset:512
	ds_read_b32 v228, v214 offset:1024
	ds_read_b32 v229, v214 offset:1536
	ds_read_b32 v230, v214 offset:2048
	ds_read_b32 v231, v214 offset:2560
	ds_read_b32 v232, v214 offset:3072
	ds_read_b32 v233, v214 offset:3584
	ds_read_b32 v234, v214 offset:4096
	ds_read_b32 v235, v214 offset:4608
	ds_read_b32 v236, v214 offset:5120
	ds_read_b32 v237, v214 offset:5632
	ds_read_b32 v238, v214 offset:6144
	ds_read_b32 v239, v214 offset:6656
	ds_read_b32 v240, v214 offset:7168
	ds_read_b32 v241, v214 offset:7680
	s_waitcnt lgkmcnt(0)
	v_max_f32_e32 v226, v226, v226
	v_max_f32_e32 v227, v227, v227
	v_max_f32_e32 v228, v228, v228
	v_max_f32_e32 v229, v229, v229
	v_max_f32_e32 v230, v230, v230
	v_max_f32_e32 v231, v231, v231
	v_max_f32_e32 v232, v232, v232
	v_max_f32_e32 v233, v233, v233
	v_max_f32_e32 v234, v234, v234
	v_max_f32_e32 v235, v235, v235
	v_max_f32_e32 v236, v236, v236
	v_max_f32_e32 v237, v237, v237
	v_max_f32_e32 v238, v238, v238
	v_max_f32_e32 v239, v239, v239
	v_max_f32_e32 v240, v240, v240
	v_max_f32_e32 v241, v241, v241
	v_med3_f32 v226, v226, s62, v95
	v_med3_f32 v227, v227, s62, v95
	v_med3_f32 v228, v228, s62, v95
	v_med3_f32 v229, v229, s62, v95
	v_med3_f32 v230, v230, s62, v95
	v_med3_f32 v231, v231, s62, v95
	v_med3_f32 v232, v232, s62, v95
	v_med3_f32 v233, v233, s62, v95
	v_med3_f32 v234, v234, s62, v95
	v_med3_f32 v235, v235, s62, v95
	v_med3_f32 v236, v236, s62, v95
	v_med3_f32 v237, v237, s62, v95
	v_med3_f32 v238, v238, s62, v95
	v_med3_f32 v239, v239, s62, v95
	v_med3_f32 v240, v240, s62, v95
	v_med3_f32 v241, v241, s62, v95
	v_mov_b32_e32 v242, 0
	v_mov_b32_e32 v243, 0
	v_mov_b32_e32 v244, 0
	v_mov_b32_e32 v245, 0
	v_cvt_pk_fp8_f32 v242, v226, v227
	v_cvt_pk_fp8_f32 v243, v230, v231
	v_cvt_pk_fp8_f32 v244, v234, v235
	v_cvt_pk_fp8_f32 v245, v238, v239
	v_cvt_pk_fp8_f32 v242, v228, v229 op_sel:[0,0,1]
	v_cvt_pk_fp8_f32 v243, v232, v233 op_sel:[0,0,1]
	v_cvt_pk_fp8_f32 v244, v236, v237 op_sel:[0,0,1]
	v_cvt_pk_fp8_f32 v245, v240, v241 op_sel:[0,0,1]
	s_nop 0
	global_store_dwordx4 v78, v[242:245], s[6:7]
	s_waitcnt vmcnt(12)
	v_mul_f32_e32 v144, v26, v144
	v_mul_f32_e32 v145, v26, v145
	v_mul_f32_e32 v146, v26, v146
	v_mul_f32_e32 v147, v26, v147
	ds_write_b128 v209, v[144:147]
	v_mul_f32_e32 v148, v27, v148
	v_mul_f32_e32 v149, v27, v149
	v_mul_f32_e32 v150, v27, v150
	v_mul_f32_e32 v151, v27, v151
	ds_write_b128 v209, v[148:151] offset:1024
	v_mul_f32_e32 v152, v28, v152
	v_mul_f32_e32 v153, v28, v153
	v_mul_f32_e32 v154, v28, v154
	v_mul_f32_e32 v155, v28, v155
	ds_write_b128 v209, v[152:155] offset:2048
	v_mul_f32_e32 v156, v29, v156
	v_mul_f32_e32 v157, v29, v157
	v_mul_f32_e32 v158, v29, v158
	v_mul_f32_e32 v159, v29, v159
	ds_write_b128 v209, v[156:159] offset:3072
	v_mul_f32_e32 v160, v30, v160
	v_mul_f32_e32 v161, v30, v161
	v_mul_f32_e32 v162, v30, v162
	v_mul_f32_e32 v163, v30, v163
	ds_write_b128 v209, v[160:163] offset:4096
	v_mul_f32_e32 v164, v31, v164
	v_mul_f32_e32 v165, v31, v165
	v_mul_f32_e32 v166, v31, v166
	v_mul_f32_e32 v167, v31, v167
	ds_write_b128 v209, v[164:167] offset:5120
	v_mul_f32_e32 v168, v32, v168
	v_mul_f32_e32 v169, v32, v169
	v_mul_f32_e32 v170, v32, v170
	v_mul_f32_e32 v171, v32, v171
	ds_write_b128 v209, v[168:171] offset:6144
	v_mul_f32_e32 v172, v33, v172
	v_mul_f32_e32 v173, v33, v173
	v_mul_f32_e32 v174, v33, v174
	v_mul_f32_e32 v175, v33, v175
	ds_write_b128 v209, v[172:175] offset:7168
	s_waitcnt lgkmcnt(0)
	s_barrier
; #define GAS __attribute__((address_space(1)))
; #define LAS __attribute__((address_space(3)))
; #define LDS_WAIT() asm volatile("s_waitcnt lgkmcnt(0)" ::: "memory")
;     ...
; #pragma unroll
;     for (int i = 0; i < 32; ++i) v[i] = sc >= 0 ? W[(size_t)(k0 + 2 * i + (lane >> 5)) * Nsrc + sc] : 0.f;
; #pragma unroll
;     for (int i = 0; i < 32; ++i) { const int k = k0 + 2 * i + (lane >> 5); float x = v[i] * wscale; if (KS) x *= (k < ksplit ? ksA[k] : ksB[k - ksplit]); scr[(2 * i + (lane >> 5)) * 33 + (lane & 31)] = x; }
;     LDS_WAIT(); asm volatile("" ::: "memory");
;     const int c = lane & 7;
; #pragma unroll
;     for (int j = 0; j < 4; ++j) { const int n = (lane >> 3) + 8 * j; const LAS float* s = scr + (8 * c) * 33 + n;
;         const unsigned long long o = (unsigned long long)pg8::pk4_fp8(s[0 * 33], s[1 * 33], s[2 * 33], s[3 * 33]) | ((unsigned long long)pg8::pk4_fp8(s[4 * 33], s[5 * 33], s[6 * 33], s[7 * 33]) << 32);
;         *(GAS unsigned long long*)(WT + (size_t)(n0 + n) * K + k0 + 8 * c) = o; }
	s_mov_b64 s[8:9], s[34:35]
	global_load_dwordx4 v[144:147], v74, s[8:9]
	s_add_u32 s8, s8, 0x20000
	s_addc_u32 s9, s9, 0
	global_load_dwordx4 v[148:151], v74, s[8:9]
	s_add_u32 s8, s8, 0x20000
	s_addc_u32 s9, s9, 0
	global_load_dwordx4 v[152:155], v74, s[8:9]
	s_add_u32 s8, s8, 0x20000
	s_addc_u32 s9, s9, 0
	global_load_dwordx4 v[156:159], v74, s[8:9]
	s_add_u32 s8, s8, 0x20000
	s_addc_u32 s9, s9, 0
	global_load_dwordx4 v[160:163], v74, s[8:9]
	s_add_u32 s8, s8, 0x20000
	s_addc_u32 s9, s9, 0
	global_load_dwordx4 v[164:167], v74, s[8:9]
	s_add_u32 s8, s8, 0x20000
	s_addc_u32 s9, s9, 0
	global_load_dwordx4 v[168:171], v74, s[8:9]
	s_add_u32 s8, s8, 0x20000
	s_addc_u32 s9, s9, 0
	global_load_dwordx4 v[172:175], v74, s[8:9]
	s_add_u32 s6, s32, 0x3800000
	s_addc_u32 s7, s33, 0
	ds_read_b32 v226, v211
	ds_read_b32 v227, v211 offset:512
	ds_read_b32 v228, v211 offset:1024
	ds_read_b32 v229, v211 offset:1536
	ds_read_b32 v230, v211 offset:2048
	ds_read_b32 v231, v211 offset:2560
	ds_read_b32 v232, v211 offset:3072
	ds_read_b32 v233, v211 offset:3584
	ds_read_b32 v234, v211 offset:4096
	ds_read_b32 v235, v211 offset:4608
	ds_read_b32 v236, v211 offset:5120
	ds_read_b32 v237, v211 offset:5632
	ds_read_b32 v238, v211 offset:6144
	ds_read_b32 v239, v211 offset:6656
	ds_read_b32 v240, v211 offset:7168
	ds_read_b32 v241, v211 offset:7680
	s_waitcnt lgkmcnt(0)
	v_max_f32_e32 v226, v226, v226
	v_max_f32_e32 v227, v227, v227
	v_max_f32_e32 v228, v228, v228
	v_max_f32_e32 v229, v229, v229
	v_max_f32_e32 v230, v230, v230
	v_max_f32_e32 v231, v231, v231
	v_max_f32_e32 v232, v232, v232
	v_max_f32_e32 v233, v233, v233
	v_max_f32_e32 v234, v234, v234
	v_max_f32_e32 v235, v235, v235
	v_max_f32_e32 v236, v236, v236
	v_max_f32_e32 v237, v237, v237
	v_max_f32_e32 v238, v238, v238
	v_max_f32_e32 v239, v239, v239
	v_max_f32_e32 v240, v240, v240
	v_max_f32_e32 v241, v241, v241
	v_med3_f32 v226, v226, s62, v95
	v_med3_f32 v227, v227, s62, v95
	v_med3_f32 v228, v228, s62, v95
	v_med3_f32 v229, v229, s62, v95
	v_med3_f32 v230, v230, s62, v95
	v_med3_f32 v231, v231, s62, v95
	v_med3_f32 v232, v232, s62, v95
	v_med3_f32 v233, v233, s62, v95
	v_med3_f32 v234, v234, s62, v95
	v_med3_f32 v235, v235, s62, v95
	v_med3_f32 v236, v236, s62, v95
	v_med3_f32 v237, v237, s62, v95
	v_med3_f32 v238, v238, s62, v95
	v_med3_f32 v239, v239, s62, v95
	v_med3_f32 v240, v240, s62, v95
	v_med3_f32 v241, v241, s62, v95
	v_mov_b32_e32 v242, 0
	v_mov_b32_e32 v243, 0
	v_mov_b32_e32 v244, 0
	v_mov_b32_e32 v245, 0
	v_cvt_pk_fp8_f32 v242, v226, v227
	v_cvt_pk_fp8_f32 v243, v230, v231
	v_cvt_pk_fp8_f32 v244, v234, v235
	v_cvt_pk_fp8_f32 v245, v238, v239
	v_cvt_pk_fp8_f32 v242, v228, v229 op_sel:[0,0,1]
	v_cvt_pk_fp8_f32 v243, v232, v233 op_sel:[0,0,1]
	v_cvt_pk_fp8_f32 v244, v236, v237 op_sel:[0,0,1]
	v_cvt_pk_fp8_f32 v245, v240, v241 op_sel:[0,0,1]
	s_nop 0
	global_store_dwordx4 v77, v[242:245], s[6:7]
	ds_read_b32 v226, v213
	ds_read_b32 v227, v213 offset:512
	ds_read_b32 v228, v213 offset:1024
	ds_read_b32 v229, v213 offset:1536
	ds_read_b32 v230, v213 offset:2048
	ds_read_b32 v231, v213 offset:2560
	ds_read_b32 v232, v213 offset:3072
	ds_read_b32 v233, v213 offset:3584
	ds_read_b32 v234, v213 offset:4096
	ds_read_b32 v235, v213 offset:4608
	ds_read_b32 v236, v213 offset:5120
	ds_read_b32 v237, v213 offset:5632
	ds_read_b32 v238, v213 offset:6144
	ds_read_b32 v239, v213 offset:6656
	ds_read_b32 v240, v213 offset:7168
	ds_read_b32 v241, v213 offset:7680
	s_waitcnt lgkmcnt(0)
	v_max_f32_e32 v226, v226, v226
	v_max_f32_e32 v227, v227, v227
	v_max_f32_e32 v228, v228, v228
	v_max_f32_e32 v229, v229, v229
	v_max_f32_e32 v230, v230, v230
	v_max_f32_e32 v231, v231, v231
	v_max_f32_e32 v232, v232, v232
	v_max_f32_e32 v233, v233, v233
	v_max_f32_e32 v234, v234, v234
	v_max_f32_e32 v235, v235, v235
	v_max_f32_e32 v236, v236, v236
	v_max_f32_e32 v237, v237, v237
	v_max_f32_e32 v238, v238, v238
	v_max_f32_e32 v239, v239, v239
	v_max_f32_e32 v240, v240, v240
	v_max_f32_e32 v241, v241, v241
	v_med3_f32 v226, v226, s62, v95
	v_med3_f32 v227, v227, s62, v95
	v_med3_f32 v228, v228, s62, v95
	v_med3_f32 v229, v229, s62, v95
	v_med3_f32 v230, v230, s62, v95
	v_med3_f32 v231, v231, s62, v95
	v_med3_f32 v232, v232, s62, v95
	v_med3_f32 v233, v233, s62, v95
	v_med3_f32 v234, v234, s62, v95
	v_med3_f32 v235, v235, s62, v95
	v_med3_f32 v236, v236, s62, v95
	v_med3_f32 v237, v237, s62, v95
	v_med3_f32 v238, v238, s62, v95
	v_med3_f32 v239, v239, s62, v95
	v_med3_f32 v240, v240, s62, v95
	v_med3_f32 v241, v241, s62, v95
	v_mov_b32_e32 v242, 0
	v_mov_b32_e32 v243, 0
	v_mov_b32_e32 v244, 0
	v_mov_b32_e32 v245, 0
	v_cvt_pk_fp8_f32 v242, v226, v227
	v_cvt_pk_fp8_f32 v243, v230, v231
	v_cvt_pk_fp8_f32 v244, v234, v235
	v_cvt_pk_fp8_f32 v245, v238, v239
	v_cvt_pk_fp8_f32 v242, v228, v229 op_sel:[0,0,1]
	v_cvt_pk_fp8_f32 v243, v232, v233 op_sel:[0,0,1]
	v_cvt_pk_fp8_f32 v244, v236, v237 op_sel:[0,0,1]
	v_cvt_pk_fp8_f32 v245, v240, v241 op_sel:[0,0,1]
	s_nop 0
	global_store_dwordx4 v78, v[242:245], s[6:7]
	s_waitcnt vmcnt(12)
	v_mul_f32_e32 v176, v26, v176
	v_mul_f32_e32 v177, v26, v177
	v_mul_f32_e32 v178, v26, v178
	v_mul_f32_e32 v179, v26, v179
	ds_write_b128 v210, v[176:179]
	v_mul_f32_e32 v180, v27, v180
	v_mul_f32_e32 v181, v27, v181
	v_mul_f32_e32 v182, v27, v182
	v_mul_f32_e32 v183, v27, v183
	ds_write_b128 v210, v[180:183] offset:1024
	v_mul_f32_e32 v184, v28, v184
	v_mul_f32_e32 v185, v28, v185
	v_mul_f32_e32 v186, v28, v186
	v_mul_f32_e32 v187, v28, v187
	ds_write_b128 v210, v[184:187] offset:2048
	v_mul_f32_e32 v188, v29, v188
	v_mul_f32_e32 v189, v29, v189
	v_mul_f32_e32 v190, v29, v190
	v_mul_f32_e32 v191, v29, v191
	ds_write_b128 v210, v[188:191] offset:3072
	v_mul_f32_e32 v192, v30, v192
	v_mul_f32_e32 v193, v30, v193
	v_mul_f32_e32 v194, v30, v194
	v_mul_f32_e32 v195, v30, v195
	ds_write_b128 v210, v[192:195] offset:4096
	v_mul_f32_e32 v196, v31, v196
	v_mul_f32_e32 v197, v31, v197
	v_mul_f32_e32 v198, v31, v198
	v_mul_f32_e32 v199, v31, v199
	ds_write_b128 v210, v[196:199] offset:5120
	v_mul_f32_e32 v200, v32, v200
	v_mul_f32_e32 v201, v32, v201
	v_mul_f32_e32 v202, v32, v202
	v_mul_f32_e32 v203, v32, v203
	ds_write_b128 v210, v[200:203] offset:6144
	v_mul_f32_e32 v204, v33, v204
	v_mul_f32_e32 v205, v33, v205
	v_mul_f32_e32 v206, v33, v206
	v_mul_f32_e32 v207, v33, v207
	ds_write_b128 v210, v[204:207] offset:7168
	s_waitcnt lgkmcnt(0)
	s_barrier
; #define GAS __attribute__((address_space(1)))
; #define LAS __attribute__((address_space(3)))
; #define LDS_WAIT() asm volatile("s_waitcnt lgkmcnt(0)" ::: "memory")
;     ...
; #pragma unroll
;     for (int i = 0; i < 32; ++i) v[i] = sc >= 0 ? W[(size_t)(k0 + 2 * i + (lane >> 5)) * Nsrc + sc] : 0.f;
; #pragma unroll
;     for (int i = 0; i < 32; ++i) { const int k = k0 + 2 * i + (lane >> 5); float x = v[i] * wscale; if (KS) x *= (k < ksplit ? ksA[k] : ksB[k - ksplit]); scr[(2 * i + (lane >> 5)) * 33 + (lane & 31)] = x; }
;     LDS_WAIT(); asm volatile("" ::: "memory");
;     const int c = lane & 7;
; #pragma unroll
;     for (int j = 0; j < 4; ++j) { const int n = (lane >> 3) + 8 * j; const LAS float* s = scr + (8 * c) * 33 + n;
;         const unsigned long long o = (unsigned long long)pg8::pk4_fp8(s[0 * 33], s[1 * 33], s[2 * 33], s[3 * 33]) | ((unsigned long long)pg8::pk4_fp8(s[4 * 33], s[5 * 33], s[6 * 33], s[7 * 33]) << 32);
;         *(GAS unsigned long long*)(WT + (size_t)(n0 + n) * K + k0 + 8 * c) = o; }
	s_add_u32 s8, s34, 0x1000
	s_addc_u32 s9, s35, 0
	global_load_dwordx4 v[176:179], v74, s[8:9]
	s_add_u32 s8, s8, 0x20000
	s_addc_u32 s9, s9, 0
	global_load_dwordx4 v[180:183], v74, s[8:9]
	s_add_u32 s8, s8, 0x20000
	s_addc_u32 s9, s9, 0
	global_load_dwordx4 v[184:187], v74, s[8:9]
	s_add_u32 s8, s8, 0x20000
	s_addc_u32 s9, s9, 0
	global_load_dwordx4 v[188:191], v74, s[8:9]
	s_add_u32 s8, s8, 0x20000
	s_addc_u32 s9, s9, 0
	global_load_dwordx4 v[192:195], v74, s[8:9]
	s_add_u32 s8, s8, 0x20000
	s_addc_u32 s9, s9, 0
	global_load_dwordx4 v[196:199], v74, s[8:9]
	s_add_u32 s8, s8, 0x20000
	s_addc_u32 s9, s9, 0
	global_load_dwordx4 v[200:203], v74, s[8:9]
	s_add_u32 s8, s8, 0x20000
	s_addc_u32 s9, s9, 0
	global_load_dwordx4 v[204:207], v74, s[8:9]
	s_add_u32 s6, s32, 0x3c00000
	s_addc_u32 s7, s33, 0
	ds_read_b32 v226, v212
	ds_read_b32 v227, v212 offset:512
	ds_read_b32 v228, v212 offset:1024
	ds_read_b32 v229, v212 offset:1536
	ds_read_b32 v230, v212 offset:2048
	ds_read_b32 v231, v212 offset:2560
	ds_read_b32 v232, v212 offset:3072
	ds_read_b32 v233, v212 offset:3584
	ds_read_b32 v234, v212 offset:4096
	ds_read_b32 v235, v212 offset:4608
	ds_read_b32 v236, v212 offset:5120
	ds_read_b32 v237, v212 offset:5632
	ds_read_b32 v238, v212 offset:6144
	ds_read_b32 v239, v212 offset:6656
	ds_read_b32 v240, v212 offset:7168
	ds_read_b32 v241, v212 offset:7680
	s_waitcnt lgkmcnt(0)
	v_max_f32_e32 v226, v226, v226
	v_max_f32_e32 v227, v227, v227
	v_max_f32_e32 v228, v228, v228
	v_max_f32_e32 v229, v229, v229
	v_max_f32_e32 v230, v230, v230
	v_max_f32_e32 v231, v231, v231
	v_max_f32_e32 v232, v232, v232
	v_max_f32_e32 v233, v233, v233
	v_max_f32_e32 v234, v234, v234
	v_max_f32_e32 v235, v235, v235
	v_max_f32_e32 v236, v236, v236
	v_max_f32_e32 v237, v237, v237
	v_max_f32_e32 v238, v238, v238
	v_max_f32_e32 v239, v239, v239
	v_max_f32_e32 v240, v240, v240
	v_max_f32_e32 v241, v241, v241
	v_med3_f32 v226, v226, s62, v95
	v_med3_f32 v227, v227, s62, v95
	v_med3_f32 v228, v228, s62, v95
	v_med3_f32 v229, v229, s62, v95
	v_med3_f32 v230, v230, s62, v95
	v_med3_f32 v231, v231, s62, v95
	v_med3_f32 v232, v232, s62, v95
	v_med3_f32 v233, v233, s62, v95
	v_med3_f32 v234, v234, s62, v95
	v_med3_f32 v235, v235, s62, v95
	v_med3_f32 v236, v236, s62, v95
	v_med3_f32 v237, v237, s62, v95
	v_med3_f32 v238, v238, s62, v95
	v_med3_f32 v239, v239, s62, v95
	v_med3_f32 v240, v240, s62, v95
	v_med3_f32 v241, v241, s62, v95
	v_mov_b32_e32 v242, 0
	v_mov_b32_e32 v243, 0
	v_mov_b32_e32 v244, 0
	v_mov_b32_e32 v245, 0
	v_cvt_pk_fp8_f32 v242, v226, v227
	v_cvt_pk_fp8_f32 v243, v230, v231
	v_cvt_pk_fp8_f32 v244, v234, v235
	v_cvt_pk_fp8_f32 v245, v238, v239
	v_cvt_pk_fp8_f32 v242, v228, v229 op_sel:[0,0,1]
	v_cvt_pk_fp8_f32 v243, v232, v233 op_sel:[0,0,1]
	v_cvt_pk_fp8_f32 v244, v236, v237 op_sel:[0,0,1]
	v_cvt_pk_fp8_f32 v245, v240, v241 op_sel:[0,0,1]
	s_nop 0
	global_store_dwordx4 v77, v[242:245], s[6:7]
	ds_read_b32 v226, v214
	ds_read_b32 v227, v214 offset:512
	ds_read_b32 v228, v214 offset:1024
	ds_read_b32 v229, v214 offset:1536
	ds_read_b32 v230, v214 offset:2048
	ds_read_b32 v231, v214 offset:2560
	ds_read_b32 v232, v214 offset:3072
	ds_read_b32 v233, v214 offset:3584
	ds_read_b32 v234, v214 offset:4096
	ds_read_b32 v235, v214 offset:4608
	ds_read_b32 v236, v214 offset:5120
	ds_read_b32 v237, v214 offset:5632
	ds_read_b32 v238, v214 offset:6144
	ds_read_b32 v239, v214 offset:6656
	ds_read_b32 v240, v214 offset:7168
	ds_read_b32 v241, v214 offset:7680
	s_waitcnt lgkmcnt(0)
	v_max_f32_e32 v226, v226, v226
	v_max_f32_e32 v227, v227, v227
	v_max_f32_e32 v228, v228, v228
	v_max_f32_e32 v229, v229, v229
	v_max_f32_e32 v230, v230, v230
	v_max_f32_e32 v231, v231, v231
	v_max_f32_e32 v232, v232, v232
	v_max_f32_e32 v233, v233, v233
	v_max_f32_e32 v234, v234, v234
	v_max_f32_e32 v235, v235, v235
	v_max_f32_e32 v236, v236, v236
	v_max_f32_e32 v237, v237, v237
	v_max_f32_e32 v238, v238, v238
	v_max_f32_e32 v239, v239, v239
	v_max_f32_e32 v240, v240, v240
	v_max_f32_e32 v241, v241, v241
	v_med3_f32 v226, v226, s62, v95
	v_med3_f32 v227, v227, s62, v95
	v_med3_f32 v228, v228, s62, v95
	v_med3_f32 v229, v229, s62, v95
	v_med3_f32 v230, v230, s62, v95
	v_med3_f32 v231, v231, s62, v95
	v_med3_f32 v232, v232, s62, v95
	v_med3_f32 v233, v233, s62, v95
	v_med3_f32 v234, v234, s62, v95
	v_med3_f32 v235, v235, s62, v95
	v_med3_f32 v236, v236, s62, v95
	v_med3_f32 v237, v237, s62, v95
	v_med3_f32 v238, v238, s62, v95
	v_med3_f32 v239, v239, s62, v95
	v_med3_f32 v240, v240, s62, v95
	v_med3_f32 v241, v241, s62, v95
	v_mov_b32_e32 v242, 0
	v_mov_b32_e32 v243, 0
	v_mov_b32_e32 v244, 0
	v_mov_b32_e32 v245, 0
	v_cvt_pk_fp8_f32 v242, v226, v227
	v_cvt_pk_fp8_f32 v243, v230, v231
	v_cvt_pk_fp8_f32 v244, v234, v235
	v_cvt_pk_fp8_f32 v245, v238, v239
	v_cvt_pk_fp8_f32 v242, v228, v229 op_sel:[0,0,1]
	v_cvt_pk_fp8_f32 v243, v232, v233 op_sel:[0,0,1]
	v_cvt_pk_fp8_f32 v244, v236, v237 op_sel:[0,0,1]
	v_cvt_pk_fp8_f32 v245, v240, v241 op_sel:[0,0,1]
	s_nop 0
	global_store_dwordx4 v78, v[242:245], s[6:7]
	s_waitcnt vmcnt(12)
	v_mul_f32_e32 v144, v34, v144
	v_mul_f32_e32 v145, v34, v145
	v_mul_f32_e32 v146, v34, v146
	v_mul_f32_e32 v147, v34, v147
	ds_write_b128 v209, v[144:147]
	v_mul_f32_e32 v148, v35, v148
	v_mul_f32_e32 v149, v35, v149
	v_mul_f32_e32 v150, v35, v150
	v_mul_f32_e32 v151, v35, v151
	ds_write_b128 v209, v[148:151] offset:1024
	v_mul_f32_e32 v152, v36, v152
	v_mul_f32_e32 v153, v36, v153
	v_mul_f32_e32 v154, v36, v154
	v_mul_f32_e32 v155, v36, v155
	ds_write_b128 v209, v[152:155] offset:2048
	v_mul_f32_e32 v156, v37, v156
	v_mul_f32_e32 v157, v37, v157
	v_mul_f32_e32 v158, v37, v158
	v_mul_f32_e32 v159, v37, v159
	ds_write_b128 v209, v[156:159] offset:3072
	v_mul_f32_e32 v160, v38, v160
	v_mul_f32_e32 v161, v38, v161
	v_mul_f32_e32 v162, v38, v162
	v_mul_f32_e32 v163, v38, v163
	ds_write_b128 v209, v[160:163] offset:4096
	v_mul_f32_e32 v164, v39, v164
	v_mul_f32_e32 v165, v39, v165
	v_mul_f32_e32 v166, v39, v166
	v_mul_f32_e32 v167, v39, v167
	ds_write_b128 v209, v[164:167] offset:5120
	v_mul_f32_e32 v168, v40, v168
	v_mul_f32_e32 v169, v40, v169
	v_mul_f32_e32 v170, v40, v170
	v_mul_f32_e32 v171, v40, v171
	ds_write_b128 v209, v[168:171] offset:6144
	v_mul_f32_e32 v172, v41, v172
	v_mul_f32_e32 v173, v41, v173
	v_mul_f32_e32 v174, v41, v174
	v_mul_f32_e32 v175, v41, v175
	ds_write_b128 v209, v[172:175] offset:7168
	s_waitcnt lgkmcnt(0)
	s_barrier
; #define GAS __attribute__((address_space(1)))
; #define LAS __attribute__((address_space(3)))
; #define LDS_WAIT() asm volatile("s_waitcnt lgkmcnt(0)" ::: "memory")
;     ...
; #pragma unroll
;     for (int i = 0; i < 32; ++i) v[i] = sc >= 0 ? W[(size_t)(k0 + 2 * i + (lane >> 5)) * Nsrc + sc] : 0.f;
; #pragma unroll
;     for (int i = 0; i < 32; ++i) { const int k = k0 + 2 * i + (lane >> 5); float x = v[i] * wscale; if (KS) x *= (k < ksplit ? ksA[k] : ksB[k - ksplit]); scr[(2 * i + (lane >> 5)) * 33 + (lane & 31)] = x; }
;     LDS_WAIT(); asm volatile("" ::: "memory");
;     const int c = lane & 7;
; #pragma unroll
;     for (int j = 0; j < 4; ++j) { const int n = (lane >> 3) + 8 * j; const LAS float* s = scr + (8 * c) * 33 + n;
;         const unsigned long long o = (unsigned long long)pg8::pk4_fp8(s[0 * 33], s[1 * 33], s[2 * 33], s[3 * 33]) | ((unsigned long long)pg8::pk4_fp8(s[4 * 33], s[5 * 33], s[6 * 33], s[7 * 33]) << 32);
;         *(GAS unsigned long long*)(WT + (size_t)(n0 + n) * K + k0 + 8 * c) = o; }
	s_add_u32 s8, s34, 0x2000
	s_addc_u32 s9, s35, 0
	global_load_dwordx4 v[144:147], v74, s[8:9]
	s_add_u32 s8, s8, 0x20000
	s_addc_u32 s9, s9, 0
	global_load_dwordx4 v[148:151], v74, s[8:9]
	s_add_u32 s8, s8, 0x20000
	s_addc_u32 s9, s9, 0
	global_load_dwordx4 v[152:155], v74, s[8:9]
	s_add_u32 s8, s8, 0x20000
	s_addc_u32 s9, s9, 0
	global_load_dwordx4 v[156:159], v74, s[8:9]
	s_add_u32 s8, s8, 0x20000
	s_addc_u32 s9, s9, 0
	global_load_dwordx4 v[160:163], v74, s[8:9]
	s_add_u32 s8, s8, 0x20000
	s_addc_u32 s9, s9, 0
	global_load_dwordx4 v[164:167], v74, s[8:9]
	s_add_u32 s8, s8, 0x20000
	s_addc_u32 s9, s9, 0
	global_load_dwordx4 v[168:171], v74, s[8:9]
	s_add_u32 s8, s8, 0x20000
	s_addc_u32 s9, s9, 0
	global_load_dwordx4 v[172:175], v74, s[8:9]
	s_mov_b64 s[6:7], s[36:37]
	ds_read_b32 v226, v211
	ds_read_b32 v227, v211 offset:512
	ds_read_b32 v228, v211 offset:1024
	ds_read_b32 v229, v211 offset:1536
	ds_read_b32 v230, v211 offset:2048
	ds_read_b32 v231, v211 offset:2560
	ds_read_b32 v232, v211 offset:3072
	ds_read_b32 v233, v211 offset:3584
	ds_read_b32 v234, v211 offset:4096
	ds_read_b32 v235, v211 offset:4608
	ds_read_b32 v236, v211 offset:5120
	ds_read_b32 v237, v211 offset:5632
	ds_read_b32 v238, v211 offset:6144
	ds_read_b32 v239, v211 offset:6656
	ds_read_b32 v240, v211 offset:7168
	ds_read_b32 v241, v211 offset:7680
	s_waitcnt lgkmcnt(0)
	v_max_f32_e32 v226, v226, v226
	v_max_f32_e32 v227, v227, v227
	v_max_f32_e32 v228, v228, v228
	v_max_f32_e32 v229, v229, v229
	v_max_f32_e32 v230, v230, v230
	v_max_f32_e32 v231, v231, v231
	v_max_f32_e32 v232, v232, v232
	v_max_f32_e32 v233, v233, v233
	v_max_f32_e32 v234, v234, v234
	v_max_f32_e32 v235, v235, v235
	v_max_f32_e32 v236, v236, v236
	v_max_f32_e32 v237, v237, v237
	v_max_f32_e32 v238, v238, v238
	v_max_f32_e32 v239, v239, v239
	v_max_f32_e32 v240, v240, v240
	v_max_f32_e32 v241, v241, v241
	v_med3_f32 v226, v226, s62, v95
	v_med3_f32 v227, v227, s62, v95
	v_med3_f32 v228, v228, s62, v95
	v_med3_f32 v229, v229, s62, v95
	v_med3_f32 v230, v230, s62, v95
	v_med3_f32 v231, v231, s62, v95
	v_med3_f32 v232, v232, s62, v95
	v_med3_f32 v233, v233, s62, v95
	v_med3_f32 v234, v234, s62, v95
	v_med3_f32 v235, v235, s62, v95
	v_med3_f32 v236, v236, s62, v95
	v_med3_f32 v237, v237, s62, v95
	v_med3_f32 v238, v238, s62, v95
	v_med3_f32 v239, v239, s62, v95
	v_med3_f32 v240, v240, s62, v95
	v_med3_f32 v241, v241, s62, v95
	v_mov_b32_e32 v242, 0
	v_mov_b32_e32 v243, 0
	v_mov_b32_e32 v244, 0
	v_mov_b32_e32 v245, 0
	v_cvt_pk_fp8_f32 v242, v226, v227
	v_cvt_pk_fp8_f32 v243, v230, v231
	v_cvt_pk_fp8_f32 v244, v234, v235
	v_cvt_pk_fp8_f32 v245, v238, v239
	v_cvt_pk_fp8_f32 v242, v228, v229 op_sel:[0,0,1]
	v_cvt_pk_fp8_f32 v243, v232, v233 op_sel:[0,0,1]
	v_cvt_pk_fp8_f32 v244, v236, v237 op_sel:[0,0,1]
	v_cvt_pk_fp8_f32 v245, v240, v241 op_sel:[0,0,1]
	s_nop 0
	global_store_dwordx4 v77, v[242:245], s[6:7]
	ds_read_b32 v226, v213
	ds_read_b32 v227, v213 offset:512
	ds_read_b32 v228, v213 offset:1024
	ds_read_b32 v229, v213 offset:1536
	ds_read_b32 v230, v213 offset:2048
	ds_read_b32 v231, v213 offset:2560
	ds_read_b32 v232, v213 offset:3072
	ds_read_b32 v233, v213 offset:3584
	ds_read_b32 v234, v213 offset:4096
	ds_read_b32 v235, v213 offset:4608
	ds_read_b32 v236, v213 offset:5120
	ds_read_b32 v237, v213 offset:5632
	ds_read_b32 v238, v213 offset:6144
	ds_read_b32 v239, v213 offset:6656
	ds_read_b32 v240, v213 offset:7168
	ds_read_b32 v241, v213 offset:7680
	s_waitcnt lgkmcnt(0)
	v_max_f32_e32 v226, v226, v226
	v_max_f32_e32 v227, v227, v227
	v_max_f32_e32 v228, v228, v228
	v_max_f32_e32 v229, v229, v229
	v_max_f32_e32 v230, v230, v230
	v_max_f32_e32 v231, v231, v231
	v_max_f32_e32 v232, v232, v232
	v_max_f32_e32 v233, v233, v233
	v_max_f32_e32 v234, v234, v234
	v_max_f32_e32 v235, v235, v235
	v_max_f32_e32 v236, v236, v236
	v_max_f32_e32 v237, v237, v237
	v_max_f32_e32 v238, v238, v238
	v_max_f32_e32 v239, v239, v239
	v_max_f32_e32 v240, v240, v240
	v_max_f32_e32 v241, v241, v241
	v_med3_f32 v226, v226, s62, v95
	v_med3_f32 v227, v227, s62, v95
	v_med3_f32 v228, v228, s62, v95
	v_med3_f32 v229, v229, s62, v95
	v_med3_f32 v230, v230, s62, v95
	v_med3_f32 v231, v231, s62, v95
	v_med3_f32 v232, v232, s62, v95
	v_med3_f32 v233, v233, s62, v95
	v_med3_f32 v234, v234, s62, v95
	v_med3_f32 v235, v235, s62, v95
	v_med3_f32 v236, v236, s62, v95
	v_med3_f32 v237, v237, s62, v95
	v_med3_f32 v238, v238, s62, v95
	v_med3_f32 v239, v239, s62, v95
	v_med3_f32 v240, v240, s62, v95
	v_med3_f32 v241, v241, s62, v95
	v_mov_b32_e32 v242, 0
	v_mov_b32_e32 v243, 0
	v_mov_b32_e32 v244, 0
	v_mov_b32_e32 v245, 0
	v_cvt_pk_fp8_f32 v242, v226, v227
	v_cvt_pk_fp8_f32 v243, v230, v231
	v_cvt_pk_fp8_f32 v244, v234, v235
	v_cvt_pk_fp8_f32 v245, v238, v239
	v_cvt_pk_fp8_f32 v242, v228, v229 op_sel:[0,0,1]
	v_cvt_pk_fp8_f32 v243, v232, v233 op_sel:[0,0,1]
	v_cvt_pk_fp8_f32 v244, v236, v237 op_sel:[0,0,1]
	v_cvt_pk_fp8_f32 v245, v240, v241 op_sel:[0,0,1]
	s_nop 0
	global_store_dwordx4 v78, v[242:245], s[6:7]
	s_waitcnt vmcnt(12)
	v_mul_f32_e32 v176, v34, v176
	v_mul_f32_e32 v177, v34, v177
	v_mul_f32_e32 v178, v34, v178
	v_mul_f32_e32 v179, v34, v179
	ds_write_b128 v210, v[176:179]
	v_mul_f32_e32 v180, v35, v180
	v_mul_f32_e32 v181, v35, v181
	v_mul_f32_e32 v182, v35, v182
	v_mul_f32_e32 v183, v35, v183
	ds_write_b128 v210, v[180:183] offset:1024
	v_mul_f32_e32 v184, v36, v184
	v_mul_f32_e32 v185, v36, v185
	v_mul_f32_e32 v186, v36, v186
	v_mul_f32_e32 v187, v36, v187
	ds_write_b128 v210, v[184:187] offset:2048
	v_mul_f32_e32 v188, v37, v188
	v_mul_f32_e32 v189, v37, v189
	v_mul_f32_e32 v190, v37, v190
	v_mul_f32_e32 v191, v37, v191
	ds_write_b128 v210, v[188:191] offset:3072
	v_mul_f32_e32 v192, v38, v192
	v_mul_f32_e32 v193, v38, v193
	v_mul_f32_e32 v194, v38, v194
	v_mul_f32_e32 v195, v38, v195
	ds_write_b128 v210, v[192:195] offset:4096
	v_mul_f32_e32 v196, v39, v196
	v_mul_f32_e32 v197, v39, v197
	v_mul_f32_e32 v198, v39, v198
	v_mul_f32_e32 v199, v39, v199
	ds_write_b128 v210, v[196:199] offset:5120
	v_mul_f32_e32 v200, v40, v200
	v_mul_f32_e32 v201, v40, v201
	v_mul_f32_e32 v202, v40, v202
	v_mul_f32_e32 v203, v40, v203
	ds_write_b128 v210, v[200:203] offset:6144
	v_mul_f32_e32 v204, v41, v204
	v_mul_f32_e32 v205, v41, v205
	v_mul_f32_e32 v206, v41, v206
	v_mul_f32_e32 v207, v41, v207
	ds_write_b128 v210, v[204:207] offset:7168
	s_waitcnt lgkmcnt(0)
	s_barrier
; #define GAS __attribute__((address_space(1)))
; #define LAS __attribute__((address_space(3)))
; #define LDS_WAIT() asm volatile("s_waitcnt lgkmcnt(0)" ::: "memory")
;     ...
; #pragma unroll
;     for (int i = 0; i < 32; ++i) v[i] = sc >= 0 ? W[(size_t)(k0 + 2 * i + (lane >> 5)) * Nsrc + sc] : 0.f;
; #pragma unroll
;     for (int i = 0; i < 32; ++i) { const int k = k0 + 2 * i + (lane >> 5); float x = v[i] * wscale; if (KS) x *= (k < ksplit ? ksA[k] : ksB[k - ksplit]); scr[(2 * i + (lane >> 5)) * 33 + (lane & 31)] = x; }
;     LDS_WAIT(); asm volatile("" ::: "memory");
;     const int c = lane & 7;
; #pragma unroll
;     for (int j = 0; j < 4; ++j) { const int n = (lane >> 3) + 8 * j; const LAS float* s = scr + (8 * c) * 33 + n;
;         const unsigned long long o = (unsigned long long)pg8::pk4_fp8(s[0 * 33], s[1 * 33], s[2 * 33], s[3 * 33]) | ((unsigned long long)pg8::pk4_fp8(s[4 * 33], s[5 * 33], s[6 * 33], s[7 * 33]) << 32);
;         *(GAS unsigned long long*)(WT + (size_t)(n0 + n) * K + k0 + 8 * c) = o; }
	s_add_u32 s8, s34, 0x3000
	s_addc_u32 s9, s35, 0
	global_load_dwordx4 v[176:179], v74, s[8:9]
	s_add_u32 s8, s8, 0x20000
	s_addc_u32 s9, s9, 0
	global_load_dwordx4 v[180:183], v74, s[8:9]
	s_add_u32 s8, s8, 0x20000
	s_addc_u32 s9, s9, 0
	global_load_dwordx4 v[184:187], v74, s[8:9]
	s_add_u32 s8, s8, 0x20000
	s_addc_u32 s9, s9, 0
	global_load_dwordx4 v[188:191], v74, s[8:9]
	s_add_u32 s8, s8, 0x20000
	s_addc_u32 s9, s9, 0
	global_load_dwordx4 v[192:195], v74, s[8:9]
	s_add_u32 s8, s8, 0x20000
	s_addc_u32 s9, s9, 0
	global_load_dwordx4 v[196:199], v74, s[8:9]
	s_add_u32 s8, s8, 0x20000
	s_addc_u32 s9, s9, 0
	global_load_dwordx4 v[200:203], v74, s[8:9]
	s_add_u32 s8, s8, 0x20000
	s_addc_u32 s9, s9, 0
	global_load_dwordx4 v[204:207], v74, s[8:9]
	s_add_u32 s6, s36, 0x400000
	s_addc_u32 s7, s37, 0
	ds_read_b32 v226, v212
	ds_read_b32 v227, v212 offset:512
	ds_read_b32 v228, v212 offset:1024
	ds_read_b32 v229, v212 offset:1536
	ds_read_b32 v230, v212 offset:2048
	ds_read_b32 v231, v212 offset:2560
	ds_read_b32 v232, v212 offset:3072
	ds_read_b32 v233, v212 offset:3584
	ds_read_b32 v234, v212 offset:4096
	ds_read_b32 v235, v212 offset:4608
	ds_read_b32 v236, v212 offset:5120
	ds_read_b32 v237, v212 offset:5632
	ds_read_b32 v238, v212 offset:6144
	ds_read_b32 v239, v212 offset:6656
	ds_read_b32 v240, v212 offset:7168
	ds_read_b32 v241, v212 offset:7680
	s_waitcnt lgkmcnt(0)
	v_max_f32_e32 v226, v226, v226
	v_max_f32_e32 v227, v227, v227
	v_max_f32_e32 v228, v228, v228
	v_max_f32_e32 v229, v229, v229
	v_max_f32_e32 v230, v230, v230
	v_max_f32_e32 v231, v231, v231
	v_max_f32_e32 v232, v232, v232
	v_max_f32_e32 v233, v233, v233
	v_max_f32_e32 v234, v234, v234
	v_max_f32_e32 v235, v235, v235
	v_max_f32_e32 v236, v236, v236
	v_max_f32_e32 v237, v237, v237
	v_max_f32_e32 v238, v238, v238
	v_max_f32_e32 v239, v239, v239
	v_max_f32_e32 v240, v240, v240
	v_max_f32_e32 v241, v241, v241
	v_med3_f32 v226, v226, s62, v95
	v_med3_f32 v227, v227, s62, v95
	v_med3_f32 v228, v228, s62, v95
	v_med3_f32 v229, v229, s62, v95
	v_med3_f32 v230, v230, s62, v95
	v_med3_f32 v231, v231, s62, v95
	v_med3_f32 v232, v232, s62, v95
	v_med3_f32 v233, v233, s62, v95
	v_med3_f32 v234, v234, s62, v95
	v_med3_f32 v235, v235, s62, v95
	v_med3_f32 v236, v236, s62, v95
	v_med3_f32 v237, v237, s62, v95
	v_med3_f32 v238, v238, s62, v95
	v_med3_f32 v239, v239, s62, v95
	v_med3_f32 v240, v240, s62, v95
	v_med3_f32 v241, v241, s62, v95
	v_mov_b32_e32 v242, 0
	v_mov_b32_e32 v243, 0
	v_mov_b32_e32 v244, 0
	v_mov_b32_e32 v245, 0
	v_cvt_pk_fp8_f32 v242, v226, v227
	v_cvt_pk_fp8_f32 v243, v230, v231
	v_cvt_pk_fp8_f32 v244, v234, v235
	v_cvt_pk_fp8_f32 v245, v238, v239
	v_cvt_pk_fp8_f32 v242, v228, v229 op_sel:[0,0,1]
	v_cvt_pk_fp8_f32 v243, v232, v233 op_sel:[0,0,1]
	v_cvt_pk_fp8_f32 v244, v236, v237 op_sel:[0,0,1]
	v_cvt_pk_fp8_f32 v245, v240, v241 op_sel:[0,0,1]
	s_nop 0
	global_store_dwordx4 v77, v[242:245], s[6:7]
	ds_read_b32 v226, v214
	ds_read_b32 v227, v214 offset:512
	ds_read_b32 v228, v214 offset:1024
	ds_read_b32 v229, v214 offset:1536
	ds_read_b32 v230, v214 offset:2048
	ds_read_b32 v231, v214 offset:2560
	ds_read_b32 v232, v214 offset:3072
	ds_read_b32 v233, v214 offset:3584
	ds_read_b32 v234, v214 offset:4096
	ds_read_b32 v235, v214 offset:4608
	ds_read_b32 v236, v214 offset:5120
	ds_read_b32 v237, v214 offset:5632
	ds_read_b32 v238, v214 offset:6144
	ds_read_b32 v239, v214 offset:6656
	ds_read_b32 v240, v214 offset:7168
	ds_read_b32 v241, v214 offset:7680
	s_waitcnt lgkmcnt(0)
	v_max_f32_e32 v226, v226, v226
	v_max_f32_e32 v227, v227, v227
	v_max_f32_e32 v228, v228, v228
	v_max_f32_e32 v229, v229, v229
	v_max_f32_e32 v230, v230, v230
	v_max_f32_e32 v231, v231, v231
	v_max_f32_e32 v232, v232, v232
	v_max_f32_e32 v233, v233, v233
	v_max_f32_e32 v234, v234, v234
	v_max_f32_e32 v235, v235, v235
	v_max_f32_e32 v236, v236, v236
	v_max_f32_e32 v237, v237, v237
	v_max_f32_e32 v238, v238, v238
	v_max_f32_e32 v239, v239, v239
	v_max_f32_e32 v240, v240, v240
	v_max_f32_e32 v241, v241, v241
	v_med3_f32 v226, v226, s62, v95
	v_med3_f32 v227, v227, s62, v95
	v_med3_f32 v228, v228, s62, v95
	v_med3_f32 v229, v229, s62, v95
	v_med3_f32 v230, v230, s62, v95
	v_med3_f32 v231, v231, s62, v95
	v_med3_f32 v232, v232, s62, v95
	v_med3_f32 v233, v233, s62, v95
	v_med3_f32 v234, v234, s62, v95
	v_med3_f32 v235, v235, s62, v95
	v_med3_f32 v236, v236, s62, v95
	v_med3_f32 v237, v237, s62, v95
	v_med3_f32 v238, v238, s62, v95
	v_med3_f32 v239, v239, s62, v95
	v_med3_f32 v240, v240, s62, v95
	v_med3_f32 v241, v241, s62, v95
	v_mov_b32_e32 v242, 0
	v_mov_b32_e32 v243, 0
	v_mov_b32_e32 v244, 0
	v_mov_b32_e32 v245, 0
	v_cvt_pk_fp8_f32 v242, v226, v227
	v_cvt_pk_fp8_f32 v243, v230, v231
	v_cvt_pk_fp8_f32 v244, v234, v235
	v_cvt_pk_fp8_f32 v245, v238, v239
	v_cvt_pk_fp8_f32 v242, v228, v229 op_sel:[0,0,1]
	v_cvt_pk_fp8_f32 v243, v232, v233 op_sel:[0,0,1]
	v_cvt_pk_fp8_f32 v244, v236, v237 op_sel:[0,0,1]
	v_cvt_pk_fp8_f32 v245, v240, v241 op_sel:[0,0,1]
	s_nop 0
	global_store_dwordx4 v78, v[242:245], s[6:7]
	s_waitcnt vmcnt(12)
	v_mul_f32_e32 v144, v34, v144
	v_mul_f32_e32 v145, v34, v145
	v_mul_f32_e32 v146, v34, v146
	v_mul_f32_e32 v147, v34, v147
	ds_write_b128 v209, v[144:147]
	v_mul_f32_e32 v148, v35, v148
	v_mul_f32_e32 v149, v35, v149
	v_mul_f32_e32 v150, v35, v150
	v_mul_f32_e32 v151, v35, v151
	ds_write_b128 v209, v[148:151] offset:1024
	v_mul_f32_e32 v152, v36, v152
	v_mul_f32_e32 v153, v36, v153
	v_mul_f32_e32 v154, v36, v154
	v_mul_f32_e32 v155, v36, v155
	ds_write_b128 v209, v[152:155] offset:2048
	v_mul_f32_e32 v156, v37, v156
	v_mul_f32_e32 v157, v37, v157
	v_mul_f32_e32 v158, v37, v158
	v_mul_f32_e32 v159, v37, v159
	ds_write_b128 v209, v[156:159] offset:3072
	v_mul_f32_e32 v160, v38, v160
	v_mul_f32_e32 v161, v38, v161
	v_mul_f32_e32 v162, v38, v162
	v_mul_f32_e32 v163, v38, v163
	ds_write_b128 v209, v[160:163] offset:4096
	v_mul_f32_e32 v164, v39, v164
	v_mul_f32_e32 v165, v39, v165
	v_mul_f32_e32 v166, v39, v166
	v_mul_f32_e32 v167, v39, v167
	ds_write_b128 v209, v[164:167] offset:5120
	v_mul_f32_e32 v168, v40, v168
	v_mul_f32_e32 v169, v40, v169
	v_mul_f32_e32 v170, v40, v170
	v_mul_f32_e32 v171, v40, v171
	ds_write_b128 v209, v[168:171] offset:6144
	v_mul_f32_e32 v172, v41, v172
	v_mul_f32_e32 v173, v41, v173
	v_mul_f32_e32 v174, v41, v174
	v_mul_f32_e32 v175, v41, v175
	ds_write_b128 v209, v[172:175] offset:7168
	s_waitcnt lgkmcnt(0)
	s_barrier
; #define GAS __attribute__((address_space(1)))
; #define LAS __attribute__((address_space(3)))
; #define LDS_WAIT() asm volatile("s_waitcnt lgkmcnt(0)" ::: "memory")
;     ...
; #pragma unroll
;     for (int i = 0; i < 32; ++i) v[i] = sc >= 0 ? W[(size_t)(k0 + 2 * i + (lane >> 5)) * Nsrc + sc] : 0.f;
; #pragma unroll
;     for (int i = 0; i < 32; ++i) { const int k = k0 + 2 * i + (lane >> 5); float x = v[i] * wscale; if (KS) x *= (k < ksplit ? ksA[k] : ksB[k - ksplit]); scr[(2 * i + (lane >> 5)) * 33 + (lane & 31)] = x; }
;     LDS_WAIT(); asm volatile("" ::: "memory");
;     const int c = lane & 7;
; #pragma unroll
;     for (int j = 0; j < 4; ++j) { const int n = (lane >> 3) + 8 * j; const LAS float* s = scr + (8 * c) * 33 + n;
;         const unsigned long long o = (unsigned long long)pg8::pk4_fp8(s[0 * 33], s[1 * 33], s[2 * 33], s[3 * 33]) | ((unsigned long long)pg8::pk4_fp8(s[4 * 33], s[5 * 33], s[6 * 33], s[7 * 33]) << 32);
;         *(GAS unsigned long long*)(WT + (size_t)(n0 + n) * K + k0 + 8 * c) = o; }
	s_add_u32 s8, s34, 0x4000
	s_addc_u32 s9, s35, 0
	global_load_dwordx4 v[144:147], v74, s[8:9]
	s_add_u32 s8, s8, 0x20000
	s_addc_u32 s9, s9, 0
	global_load_dwordx4 v[148:151], v74, s[8:9]
	s_add_u32 s8, s8, 0x20000
	s_addc_u32 s9, s9, 0
	global_load_dwordx4 v[152:155], v74, s[8:9]
	s_add_u32 s8, s8, 0x20000
	s_addc_u32 s9, s9, 0
	global_load_dwordx4 v[156:159], v74, s[8:9]
	s_add_u32 s8, s8, 0x20000
	s_addc_u32 s9, s9, 0
	global_load_dwordx4 v[160:163], v74, s[8:9]
	s_add_u32 s8, s8, 0x20000
	s_addc_u32 s9, s9, 0
	global_load_dwordx4 v[164:167], v74, s[8:9]
	s_add_u32 s8, s8, 0x20000
	s_addc_u32 s9, s9, 0
	global_load_dwordx4 v[168:171], v74, s[8:9]
	s_add_u32 s8, s8, 0x20000
	s_addc_u32 s9, s9, 0
	global_load_dwordx4 v[172:175], v74, s[8:9]
	s_add_u32 s6, s36, 0x800000
	s_addc_u32 s7, s37, 0
	ds_read_b32 v226, v211
	ds_read_b32 v227, v211 offset:512
	ds_read_b32 v228, v211 offset:1024
	ds_read_b32 v229, v211 offset:1536
	ds_read_b32 v230, v211 offset:2048
	ds_read_b32 v231, v211 offset:2560
	ds_read_b32 v232, v211 offset:3072
	ds_read_b32 v233, v211 offset:3584
	ds_read_b32 v234, v211 offset:4096
	ds_read_b32 v235, v211 offset:4608
	ds_read_b32 v236, v211 offset:5120
	ds_read_b32 v237, v211 offset:5632
	ds_read_b32 v238, v211 offset:6144
	ds_read_b32 v239, v211 offset:6656
	ds_read_b32 v240, v211 offset:7168
	ds_read_b32 v241, v211 offset:7680
	s_waitcnt lgkmcnt(0)
	v_max_f32_e32 v226, v226, v226
	v_max_f32_e32 v227, v227, v227
	v_max_f32_e32 v228, v228, v228
	v_max_f32_e32 v229, v229, v229
	v_max_f32_e32 v230, v230, v230
	v_max_f32_e32 v231, v231, v231
	v_max_f32_e32 v232, v232, v232
	v_max_f32_e32 v233, v233, v233
	v_max_f32_e32 v234, v234, v234
	v_max_f32_e32 v235, v235, v235
	v_max_f32_e32 v236, v236, v236
	v_max_f32_e32 v237, v237, v237
	v_max_f32_e32 v238, v238, v238
	v_max_f32_e32 v239, v239, v239
	v_max_f32_e32 v240, v240, v240
	v_max_f32_e32 v241, v241, v241
	v_med3_f32 v226, v226, s62, v95
	v_med3_f32 v227, v227, s62, v95
	v_med3_f32 v228, v228, s62, v95
	v_med3_f32 v229, v229, s62, v95
	v_med3_f32 v230, v230, s62, v95
	v_med3_f32 v231, v231, s62, v95
	v_med3_f32 v232, v232, s62, v95
	v_med3_f32 v233, v233, s62, v95
	v_med3_f32 v234, v234, s62, v95
	v_med3_f32 v235, v235, s62, v95
	v_med3_f32 v236, v236, s62, v95
	v_med3_f32 v237, v237, s62, v95
	v_med3_f32 v238, v238, s62, v95
	v_med3_f32 v239, v239, s62, v95
	v_med3_f32 v240, v240, s62, v95
	v_med3_f32 v241, v241, s62, v95
	v_mov_b32_e32 v242, 0
	v_mov_b32_e32 v243, 0
	v_mov_b32_e32 v244, 0
	v_mov_b32_e32 v245, 0
	v_cvt_pk_fp8_f32 v242, v226, v227
	v_cvt_pk_fp8_f32 v243, v230, v231
	v_cvt_pk_fp8_f32 v244, v234, v235
	v_cvt_pk_fp8_f32 v245, v238, v239
	v_cvt_pk_fp8_f32 v242, v228, v229 op_sel:[0,0,1]
	v_cvt_pk_fp8_f32 v243, v232, v233 op_sel:[0,0,1]
	v_cvt_pk_fp8_f32 v244, v236, v237 op_sel:[0,0,1]
	v_cvt_pk_fp8_f32 v245, v240, v241 op_sel:[0,0,1]
	s_nop 0
	global_store_dwordx4 v77, v[242:245], s[6:7]
	ds_read_b32 v226, v213
	ds_read_b32 v227, v213 offset:512
	ds_read_b32 v228, v213 offset:1024
	ds_read_b32 v229, v213 offset:1536
	ds_read_b32 v230, v213 offset:2048
	ds_read_b32 v231, v213 offset:2560
	ds_read_b32 v232, v213 offset:3072
	ds_read_b32 v233, v213 offset:3584
	ds_read_b32 v234, v213 offset:4096
	ds_read_b32 v235, v213 offset:4608
	ds_read_b32 v236, v213 offset:5120
	ds_read_b32 v237, v213 offset:5632
	ds_read_b32 v238, v213 offset:6144
	ds_read_b32 v239, v213 offset:6656
	ds_read_b32 v240, v213 offset:7168
	ds_read_b32 v241, v213 offset:7680
	s_waitcnt lgkmcnt(0)
	v_max_f32_e32 v226, v226, v226
	v_max_f32_e32 v227, v227, v227
	v_max_f32_e32 v228, v228, v228
	v_max_f32_e32 v229, v229, v229
	v_max_f32_e32 v230, v230, v230
	v_max_f32_e32 v231, v231, v231
	v_max_f32_e32 v232, v232, v232
	v_max_f32_e32 v233, v233, v233
	v_max_f32_e32 v234, v234, v234
	v_max_f32_e32 v235, v235, v235
	v_max_f32_e32 v236, v236, v236
	v_max_f32_e32 v237, v237, v237
	v_max_f32_e32 v238, v238, v238
	v_max_f32_e32 v239, v239, v239
	v_max_f32_e32 v240, v240, v240
	v_max_f32_e32 v241, v241, v241
	v_med3_f32 v226, v226, s62, v95
	v_med3_f32 v227, v227, s62, v95
	v_med3_f32 v228, v228, s62, v95
	v_med3_f32 v229, v229, s62, v95
	v_med3_f32 v230, v230, s62, v95
	v_med3_f32 v231, v231, s62, v95
	v_med3_f32 v232, v232, s62, v95
	v_med3_f32 v233, v233, s62, v95
	v_med3_f32 v234, v234, s62, v95
	v_med3_f32 v235, v235, s62, v95
	v_med3_f32 v236, v236, s62, v95
	v_med3_f32 v237, v237, s62, v95
	v_med3_f32 v238, v238, s62, v95
	v_med3_f32 v239, v239, s62, v95
	v_med3_f32 v240, v240, s62, v95
	v_med3_f32 v241, v241, s62, v95
	v_mov_b32_e32 v242, 0
	v_mov_b32_e32 v243, 0
	v_mov_b32_e32 v244, 0
	v_mov_b32_e32 v245, 0
	v_cvt_pk_fp8_f32 v242, v226, v227
	v_cvt_pk_fp8_f32 v243, v230, v231
	v_cvt_pk_fp8_f32 v244, v234, v235
	v_cvt_pk_fp8_f32 v245, v238, v239
	v_cvt_pk_fp8_f32 v242, v228, v229 op_sel:[0,0,1]
	v_cvt_pk_fp8_f32 v243, v232, v233 op_sel:[0,0,1]
	v_cvt_pk_fp8_f32 v244, v236, v237 op_sel:[0,0,1]
	v_cvt_pk_fp8_f32 v245, v240, v241 op_sel:[0,0,1]
	s_nop 0
	global_store_dwordx4 v78, v[242:245], s[6:7]
	s_waitcnt vmcnt(12)
	v_mul_f32_e32 v176, v34, v176
	v_mul_f32_e32 v177, v34, v177
	v_mul_f32_e32 v178, v34, v178
	v_mul_f32_e32 v179, v34, v179
	ds_write_b128 v210, v[176:179]
	v_mul_f32_e32 v180, v35, v180
	v_mul_f32_e32 v181, v35, v181
	v_mul_f32_e32 v182, v35, v182
	v_mul_f32_e32 v183, v35, v183
	ds_write_b128 v210, v[180:183] offset:1024
	v_mul_f32_e32 v184, v36, v184
	v_mul_f32_e32 v185, v36, v185
	v_mul_f32_e32 v186, v36, v186
	v_mul_f32_e32 v187, v36, v187
	ds_write_b128 v210, v[184:187] offset:2048
	v_mul_f32_e32 v188, v37, v188
	v_mul_f32_e32 v189, v37, v189
	v_mul_f32_e32 v190, v37, v190
	v_mul_f32_e32 v191, v37, v191
	ds_write_b128 v210, v[188:191] offset:3072
	v_mul_f32_e32 v192, v38, v192
	v_mul_f32_e32 v193, v38, v193
	v_mul_f32_e32 v194, v38, v194
	v_mul_f32_e32 v195, v38, v195
	ds_write_b128 v210, v[192:195] offset:4096
	v_mul_f32_e32 v196, v39, v196
	v_mul_f32_e32 v197, v39, v197
	v_mul_f32_e32 v198, v39, v198
	v_mul_f32_e32 v199, v39, v199
	ds_write_b128 v210, v[196:199] offset:5120
	v_mul_f32_e32 v200, v40, v200
	v_mul_f32_e32 v201, v40, v201
	v_mul_f32_e32 v202, v40, v202
	v_mul_f32_e32 v203, v40, v203
	ds_write_b128 v210, v[200:203] offset:6144
	v_mul_f32_e32 v204, v41, v204
	v_mul_f32_e32 v205, v41, v205
	v_mul_f32_e32 v206, v41, v206
	v_mul_f32_e32 v207, v41, v207
	ds_write_b128 v210, v[204:207] offset:7168
	s_waitcnt lgkmcnt(0)
	s_barrier
; #define GAS __attribute__((address_space(1)))
; #define LAS __attribute__((address_space(3)))
; #define LDS_WAIT() asm volatile("s_waitcnt lgkmcnt(0)" ::: "memory")
;     ...
; #pragma unroll
;     for (int i = 0; i < 32; ++i) v[i] = sc >= 0 ? W[(size_t)(k0 + 2 * i + (lane >> 5)) * Nsrc + sc] : 0.f;
; #pragma unroll
;     for (int i = 0; i < 32; ++i) { const int k = k0 + 2 * i + (lane >> 5); float x = v[i] * wscale; if (KS) x *= (k < ksplit ? ksA[k] : ksB[k - ksplit]); scr[(2 * i + (lane >> 5)) * 33 + (lane & 31)] = x; }
;     LDS_WAIT(); asm volatile("" ::: "memory");
;     const int c = lane & 7;
; #pragma unroll
;     for (int j = 0; j < 4; ++j) { const int n = (lane >> 3) + 8 * j; const LAS float* s = scr + (8 * c) * 33 + n;
;         const unsigned long long o = (unsigned long long)pg8::pk4_fp8(s[0 * 33], s[1 * 33], s[2 * 33], s[3 * 33]) | ((unsigned long long)pg8::pk4_fp8(s[4 * 33], s[5 * 33], s[6 * 33], s[7 * 33]) << 32);
;         *(GAS unsigned long long*)(WT + (size_t)(n0 + n) * K + k0 + 8 * c) = o; }
	s_add_u32 s8, s34, 0x5000
	s_addc_u32 s9, s35, 0
	global_load_dwordx4 v[176:179], v74, s[8:9]
	s_add_u32 s8, s8, 0x20000
	s_addc_u32 s9, s9, 0
	global_load_dwordx4 v[180:183], v74, s[8:9]
	s_add_u32 s8, s8, 0x20000
	s_addc_u32 s9, s9, 0
	global_load_dwordx4 v[184:187], v74, s[8:9]
	s_add_u32 s8, s8, 0x20000
	s_addc_u32 s9, s9, 0
	global_load_dwordx4 v[188:191], v74, s[8:9]
	s_add_u32 s8, s8, 0x20000
	s_addc_u32 s9, s9, 0
	global_load_dwordx4 v[192:195], v74, s[8:9]
	s_add_u32 s8, s8, 0x20000
	s_addc_u32 s9, s9, 0
	global_load_dwordx4 v[196:199], v74, s[8:9]
	s_add_u32 s8, s8, 0x20000
	s_addc_u32 s9, s9, 0
	global_load_dwordx4 v[200:203], v74, s[8:9]
	s_add_u32 s8, s8, 0x20000
	s_addc_u32 s9, s9, 0
	global_load_dwordx4 v[204:207], v74, s[8:9]
	s_add_u32 s6, s36, 0xc00000
	s_addc_u32 s7, s37, 0
	ds_read_b32 v226, v212
	ds_read_b32 v227, v212 offset:512
	ds_read_b32 v228, v212 offset:1024
	ds_read_b32 v229, v212 offset:1536
	ds_read_b32 v230, v212 offset:2048
	ds_read_b32 v231, v212 offset:2560
	ds_read_b32 v232, v212 offset:3072
	ds_read_b32 v233, v212 offset:3584
	ds_read_b32 v234, v212 offset:4096
	ds_read_b32 v235, v212 offset:4608
	ds_read_b32 v236, v212 offset:5120
	ds_read_b32 v237, v212 offset:5632
	ds_read_b32 v238, v212 offset:6144
	ds_read_b32 v239, v212 offset:6656
	ds_read_b32 v240, v212 offset:7168
	ds_read_b32 v241, v212 offset:7680
	s_waitcnt lgkmcnt(0)
	v_max_f32_e32 v226, v226, v226
	v_max_f32_e32 v227, v227, v227
	v_max_f32_e32 v228, v228, v228
	v_max_f32_e32 v229, v229, v229
	v_max_f32_e32 v230, v230, v230
	v_max_f32_e32 v231, v231, v231
	v_max_f32_e32 v232, v232, v232
	v_max_f32_e32 v233, v233, v233
	v_max_f32_e32 v234, v234, v234
	v_max_f32_e32 v235, v235, v235
	v_max_f32_e32 v236, v236, v236
	v_max_f32_e32 v237, v237, v237
	v_max_f32_e32 v238, v238, v238
	v_max_f32_e32 v239, v239, v239
	v_max_f32_e32 v240, v240, v240
	v_max_f32_e32 v241, v241, v241
	v_med3_f32 v226, v226, s62, v95
	v_med3_f32 v227, v227, s62, v95
	v_med3_f32 v228, v228, s62, v95
	v_med3_f32 v229, v229, s62, v95
	v_med3_f32 v230, v230, s62, v95
	v_med3_f32 v231, v231, s62, v95
	v_med3_f32 v232, v232, s62, v95
	v_med3_f32 v233, v233, s62, v95
	v_med3_f32 v234, v234, s62, v95
	v_med3_f32 v235, v235, s62, v95
	v_med3_f32 v236, v236, s62, v95
	v_med3_f32 v237, v237, s62, v95
	v_med3_f32 v238, v238, s62, v95
	v_med3_f32 v239, v239, s62, v95
	v_med3_f32 v240, v240, s62, v95
	v_med3_f32 v241, v241, s62, v95
	v_mov_b32_e32 v242, 0
	v_mov_b32_e32 v243, 0
	v_mov_b32_e32 v244, 0
	v_mov_b32_e32 v245, 0
	v_cvt_pk_fp8_f32 v242, v226, v227
	v_cvt_pk_fp8_f32 v243, v230, v231
	v_cvt_pk_fp8_f32 v244, v234, v235
	v_cvt_pk_fp8_f32 v245, v238, v239
	v_cvt_pk_fp8_f32 v242, v228, v229 op_sel:[0,0,1]
	v_cvt_pk_fp8_f32 v243, v232, v233 op_sel:[0,0,1]
	v_cvt_pk_fp8_f32 v244, v236, v237 op_sel:[0,0,1]
	v_cvt_pk_fp8_f32 v245, v240, v241 op_sel:[0,0,1]
	s_nop 0
	global_store_dwordx4 v77, v[242:245], s[6:7]
	ds_read_b32 v226, v214
	ds_read_b32 v227, v214 offset:512
	ds_read_b32 v228, v214 offset:1024
	ds_read_b32 v229, v214 offset:1536
	ds_read_b32 v230, v214 offset:2048
	ds_read_b32 v231, v214 offset:2560
	ds_read_b32 v232, v214 offset:3072
	ds_read_b32 v233, v214 offset:3584
	ds_read_b32 v234, v214 offset:4096
	ds_read_b32 v235, v214 offset:4608
	ds_read_b32 v236, v214 offset:5120
	ds_read_b32 v237, v214 offset:5632
	ds_read_b32 v238, v214 offset:6144
	ds_read_b32 v239, v214 offset:6656
	ds_read_b32 v240, v214 offset:7168
	ds_read_b32 v241, v214 offset:7680
	s_waitcnt lgkmcnt(0)
	v_max_f32_e32 v226, v226, v226
	v_max_f32_e32 v227, v227, v227
	v_max_f32_e32 v228, v228, v228
	v_max_f32_e32 v229, v229, v229
	v_max_f32_e32 v230, v230, v230
	v_max_f32_e32 v231, v231, v231
	v_max_f32_e32 v232, v232, v232
	v_max_f32_e32 v233, v233, v233
	v_max_f32_e32 v234, v234, v234
	v_max_f32_e32 v235, v235, v235
	v_max_f32_e32 v236, v236, v236
	v_max_f32_e32 v237, v237, v237
	v_max_f32_e32 v238, v238, v238
	v_max_f32_e32 v239, v239, v239
	v_max_f32_e32 v240, v240, v240
	v_max_f32_e32 v241, v241, v241
	v_med3_f32 v226, v226, s62, v95
	v_med3_f32 v227, v227, s62, v95
	v_med3_f32 v228, v228, s62, v95
	v_med3_f32 v229, v229, s62, v95
	v_med3_f32 v230, v230, s62, v95
	v_med3_f32 v231, v231, s62, v95
	v_med3_f32 v232, v232, s62, v95
	v_med3_f32 v233, v233, s62, v95
	v_med3_f32 v234, v234, s62, v95
	v_med3_f32 v235, v235, s62, v95
	v_med3_f32 v236, v236, s62, v95
	v_med3_f32 v237, v237, s62, v95
	v_med3_f32 v238, v238, s62, v95
	v_med3_f32 v239, v239, s62, v95
	v_med3_f32 v240, v240, s62, v95
	v_med3_f32 v241, v241, s62, v95
	v_mov_b32_e32 v242, 0
	v_mov_b32_e32 v243, 0
	v_mov_b32_e32 v244, 0
	v_mov_b32_e32 v245, 0
	v_cvt_pk_fp8_f32 v242, v226, v227
	v_cvt_pk_fp8_f32 v243, v230, v231
	v_cvt_pk_fp8_f32 v244, v234, v235
	v_cvt_pk_fp8_f32 v245, v238, v239
	v_cvt_pk_fp8_f32 v242, v228, v229 op_sel:[0,0,1]
	v_cvt_pk_fp8_f32 v243, v232, v233 op_sel:[0,0,1]
	v_cvt_pk_fp8_f32 v244, v236, v237 op_sel:[0,0,1]
	v_cvt_pk_fp8_f32 v245, v240, v241 op_sel:[0,0,1]
	s_nop 0
	global_store_dwordx4 v78, v[242:245], s[6:7]
	s_waitcnt vmcnt(12)
	v_mul_f32_e32 v144, v34, v144
	v_mul_f32_e32 v145, v34, v145
	v_mul_f32_e32 v146, v34, v146
	v_mul_f32_e32 v147, v34, v147
	ds_write_b128 v209, v[144:147]
	v_mul_f32_e32 v148, v35, v148
	v_mul_f32_e32 v149, v35, v149
	v_mul_f32_e32 v150, v35, v150
	v_mul_f32_e32 v151, v35, v151
	ds_write_b128 v209, v[148:151] offset:1024
	v_mul_f32_e32 v152, v36, v152
	v_mul_f32_e32 v153, v36, v153
	v_mul_f32_e32 v154, v36, v154
	v_mul_f32_e32 v155, v36, v155
	ds_write_b128 v209, v[152:155] offset:2048
	v_mul_f32_e32 v156, v37, v156
	v_mul_f32_e32 v157, v37, v157
	v_mul_f32_e32 v158, v37, v158
	v_mul_f32_e32 v159, v37, v159
	ds_write_b128 v209, v[156:159] offset:3072
	v_mul_f32_e32 v160, v38, v160
	v_mul_f32_e32 v161, v38, v161
	v_mul_f32_e32 v162, v38, v162
	v_mul_f32_e32 v163, v38, v163
	ds_write_b128 v209, v[160:163] offset:4096
	v_mul_f32_e32 v164, v39, v164
	v_mul_f32_e32 v165, v39, v165
	v_mul_f32_e32 v166, v39, v166
	v_mul_f32_e32 v167, v39, v167
	ds_write_b128 v209, v[164:167] offset:5120
	v_mul_f32_e32 v168, v40, v168
	v_mul_f32_e32 v169, v40, v169
	v_mul_f32_e32 v170, v40, v170
	v_mul_f32_e32 v171, v40, v171
	ds_write_b128 v209, v[168:171] offset:6144
	v_mul_f32_e32 v172, v41, v172
	v_mul_f32_e32 v173, v41, v173
	v_mul_f32_e32 v174, v41, v174
	v_mul_f32_e32 v175, v41, v175
	ds_write_b128 v209, v[172:175] offset:7168
	s_waitcnt lgkmcnt(0)
	s_barrier
; #define GAS __attribute__((address_space(1)))
; #define LAS __attribute__((address_space(3)))
; #define LDS_WAIT() asm volatile("s_waitcnt lgkmcnt(0)" ::: "memory")
;     ...
; #pragma unroll
;     for (int i = 0; i < 32; ++i) v[i] = sc >= 0 ? W[(size_t)(k0 + 2 * i + (lane >> 5)) * Nsrc + sc] : 0.f;
; #pragma unroll
;     for (int i = 0; i < 32; ++i) { const int k = k0 + 2 * i + (lane >> 5); float x = v[i] * wscale; if (KS) x *= (k < ksplit ? ksA[k] : ksB[k - ksplit]); scr[(2 * i + (lane >> 5)) * 33 + (lane & 31)] = x; }
;     LDS_WAIT(); asm volatile("" ::: "memory");
;     const int c = lane & 7;
; #pragma unroll
;     for (int j = 0; j < 4; ++j) { const int n = (lane >> 3) + 8 * j; const LAS float* s = scr + (8 * c) * 33 + n;
;         const unsigned long long o = (unsigned long long)pg8::pk4_fp8(s[0 * 33], s[1 * 33], s[2 * 33], s[3 * 33]) | ((unsigned long long)pg8::pk4_fp8(s[4 * 33], s[5 * 33], s[6 * 33], s[7 * 33]) << 32);
;         *(GAS unsigned long long*)(WT + (size_t)(n0 + n) * K + k0 + 8 * c) = o; }
	s_add_u32 s8, s34, 0x6000
	s_addc_u32 s9, s35, 0
	global_load_dwordx4 v[144:147], v74, s[8:9]
	s_add_u32 s8, s8, 0x20000
	s_addc_u32 s9, s9, 0
	global_load_dwordx4 v[148:151], v74, s[8:9]
	s_add_u32 s8, s8, 0x20000
	s_addc_u32 s9, s9, 0
	global_load_dwordx4 v[152:155], v74, s[8:9]
	s_add_u32 s8, s8, 0x20000
	s_addc_u32 s9, s9, 0
	global_load_dwordx4 v[156:159], v74, s[8:9]
	s_add_u32 s8, s8, 0x20000
	s_addc_u32 s9, s9, 0
	global_load_dwordx4 v[160:163], v74, s[8:9]
	s_add_u32 s8, s8, 0x20000
	s_addc_u32 s9, s9, 0
	global_load_dwordx4 v[164:167], v74, s[8:9]
	s_add_u32 s8, s8, 0x20000
	s_addc_u32 s9, s9, 0
	global_load_dwordx4 v[168:171], v74, s[8:9]
	s_add_u32 s8, s8, 0x20000
	s_addc_u32 s9, s9, 0
	global_load_dwordx4 v[172:175], v74, s[8:9]
	s_add_u32 s6, s36, 0x1000000
	s_addc_u32 s7, s37, 0
	ds_read_b32 v226, v211
	ds_read_b32 v227, v211 offset:512
	ds_read_b32 v228, v211 offset:1024
	ds_read_b32 v229, v211 offset:1536
	ds_read_b32 v230, v211 offset:2048
	ds_read_b32 v231, v211 offset:2560
	ds_read_b32 v232, v211 offset:3072
	ds_read_b32 v233, v211 offset:3584
	ds_read_b32 v234, v211 offset:4096
	ds_read_b32 v235, v211 offset:4608
	ds_read_b32 v236, v211 offset:5120
	ds_read_b32 v237, v211 offset:5632
	ds_read_b32 v238, v211 offset:6144
	ds_read_b32 v239, v211 offset:6656
	ds_read_b32 v240, v211 offset:7168
	ds_read_b32 v241, v211 offset:7680
	s_waitcnt lgkmcnt(0)
	v_max_f32_e32 v226, v226, v226
	v_max_f32_e32 v227, v227, v227
	v_max_f32_e32 v228, v228, v228
	v_max_f32_e32 v229, v229, v229
	v_max_f32_e32 v230, v230, v230
	v_max_f32_e32 v231, v231, v231
	v_max_f32_e32 v232, v232, v232
	v_max_f32_e32 v233, v233, v233
	v_max_f32_e32 v234, v234, v234
	v_max_f32_e32 v235, v235, v235
	v_max_f32_e32 v236, v236, v236
	v_max_f32_e32 v237, v237, v237
	v_max_f32_e32 v238, v238, v238
	v_max_f32_e32 v239, v239, v239
	v_max_f32_e32 v240, v240, v240
	v_max_f32_e32 v241, v241, v241
	v_med3_f32 v226, v226, s62, v95
	v_med3_f32 v227, v227, s62, v95
	v_med3_f32 v228, v228, s62, v95
	v_med3_f32 v229, v229, s62, v95
	v_med3_f32 v230, v230, s62, v95
	v_med3_f32 v231, v231, s62, v95
	v_med3_f32 v232, v232, s62, v95
	v_med3_f32 v233, v233, s62, v95
	v_med3_f32 v234, v234, s62, v95
	v_med3_f32 v235, v235, s62, v95
	v_med3_f32 v236, v236, s62, v95
	v_med3_f32 v237, v237, s62, v95
	v_med3_f32 v238, v238, s62, v95
	v_med3_f32 v239, v239, s62, v95
	v_med3_f32 v240, v240, s62, v95
	v_med3_f32 v241, v241, s62, v95
	v_mov_b32_e32 v242, 0
	v_mov_b32_e32 v243, 0
	v_mov_b32_e32 v244, 0
	v_mov_b32_e32 v245, 0
	v_cvt_pk_fp8_f32 v242, v226, v227
	v_cvt_pk_fp8_f32 v243, v230, v231
	v_cvt_pk_fp8_f32 v244, v234, v235
	v_cvt_pk_fp8_f32 v245, v238, v239
	v_cvt_pk_fp8_f32 v242, v228, v229 op_sel:[0,0,1]
	v_cvt_pk_fp8_f32 v243, v232, v233 op_sel:[0,0,1]
	v_cvt_pk_fp8_f32 v244, v236, v237 op_sel:[0,0,1]
	v_cvt_pk_fp8_f32 v245, v240, v241 op_sel:[0,0,1]
	s_nop 0
	global_store_dwordx4 v77, v[242:245], s[6:7]
	ds_read_b32 v226, v213
	ds_read_b32 v227, v213 offset:512
	ds_read_b32 v228, v213 offset:1024
	ds_read_b32 v229, v213 offset:1536
	ds_read_b32 v230, v213 offset:2048
	ds_read_b32 v231, v213 offset:2560
	ds_read_b32 v232, v213 offset:3072
	ds_read_b32 v233, v213 offset:3584
	ds_read_b32 v234, v213 offset:4096
	ds_read_b32 v235, v213 offset:4608
	ds_read_b32 v236, v213 offset:5120
	ds_read_b32 v237, v213 offset:5632
	ds_read_b32 v238, v213 offset:6144
	ds_read_b32 v239, v213 offset:6656
	ds_read_b32 v240, v213 offset:7168
	ds_read_b32 v241, v213 offset:7680
	s_waitcnt lgkmcnt(0)
	v_max_f32_e32 v226, v226, v226
	v_max_f32_e32 v227, v227, v227
	v_max_f32_e32 v228, v228, v228
	v_max_f32_e32 v229, v229, v229
	v_max_f32_e32 v230, v230, v230
	v_max_f32_e32 v231, v231, v231
	v_max_f32_e32 v232, v232, v232
	v_max_f32_e32 v233, v233, v233
	v_max_f32_e32 v234, v234, v234
	v_max_f32_e32 v235, v235, v235
	v_max_f32_e32 v236, v236, v236
	v_max_f32_e32 v237, v237, v237
	v_max_f32_e32 v238, v238, v238
	v_max_f32_e32 v239, v239, v239
	v_max_f32_e32 v240, v240, v240
	v_max_f32_e32 v241, v241, v241
	v_med3_f32 v226, v226, s62, v95
	v_med3_f32 v227, v227, s62, v95
	v_med3_f32 v228, v228, s62, v95
	v_med3_f32 v229, v229, s62, v95
	v_med3_f32 v230, v230, s62, v95
	v_med3_f32 v231, v231, s62, v95
	v_med3_f32 v232, v232, s62, v95
	v_med3_f32 v233, v233, s62, v95
	v_med3_f32 v234, v234, s62, v95
	v_med3_f32 v235, v235, s62, v95
	v_med3_f32 v236, v236, s62, v95
	v_med3_f32 v237, v237, s62, v95
	v_med3_f32 v238, v238, s62, v95
	v_med3_f32 v239, v239, s62, v95
	v_med3_f32 v240, v240, s62, v95
	v_med3_f32 v241, v241, s62, v95
	v_mov_b32_e32 v242, 0
	v_mov_b32_e32 v243, 0
	v_mov_b32_e32 v244, 0
	v_mov_b32_e32 v245, 0
	v_cvt_pk_fp8_f32 v242, v226, v227
	v_cvt_pk_fp8_f32 v243, v230, v231
	v_cvt_pk_fp8_f32 v244, v234, v235
	v_cvt_pk_fp8_f32 v245, v238, v239
	v_cvt_pk_fp8_f32 v242, v228, v229 op_sel:[0,0,1]
	v_cvt_pk_fp8_f32 v243, v232, v233 op_sel:[0,0,1]
	v_cvt_pk_fp8_f32 v244, v236, v237 op_sel:[0,0,1]
	v_cvt_pk_fp8_f32 v245, v240, v241 op_sel:[0,0,1]
	s_nop 0
	global_store_dwordx4 v78, v[242:245], s[6:7]
	s_waitcnt vmcnt(12)
	v_mul_f32_e32 v176, v34, v176
	v_mul_f32_e32 v177, v34, v177
	v_mul_f32_e32 v178, v34, v178
	v_mul_f32_e32 v179, v34, v179
	ds_write_b128 v210, v[176:179]
	v_mul_f32_e32 v180, v35, v180
	v_mul_f32_e32 v181, v35, v181
	v_mul_f32_e32 v182, v35, v182
	v_mul_f32_e32 v183, v35, v183
	ds_write_b128 v210, v[180:183] offset:1024
	v_mul_f32_e32 v184, v36, v184
	v_mul_f32_e32 v185, v36, v185
	v_mul_f32_e32 v186, v36, v186
	v_mul_f32_e32 v187, v36, v187
	ds_write_b128 v210, v[184:187] offset:2048
	v_mul_f32_e32 v188, v37, v188
	v_mul_f32_e32 v189, v37, v189
	v_mul_f32_e32 v190, v37, v190
	v_mul_f32_e32 v191, v37, v191
	ds_write_b128 v210, v[188:191] offset:3072
	v_mul_f32_e32 v192, v38, v192
	v_mul_f32_e32 v193, v38, v193
	v_mul_f32_e32 v194, v38, v194
	v_mul_f32_e32 v195, v38, v195
	ds_write_b128 v210, v[192:195] offset:4096
	v_mul_f32_e32 v196, v39, v196
	v_mul_f32_e32 v197, v39, v197
	v_mul_f32_e32 v198, v39, v198
	v_mul_f32_e32 v199, v39, v199
	ds_write_b128 v210, v[196:199] offset:5120
	v_mul_f32_e32 v200, v40, v200
	v_mul_f32_e32 v201, v40, v201
	v_mul_f32_e32 v202, v40, v202
	v_mul_f32_e32 v203, v40, v203
	ds_write_b128 v210, v[200:203] offset:6144
	v_mul_f32_e32 v204, v41, v204
	v_mul_f32_e32 v205, v41, v205
	v_mul_f32_e32 v206, v41, v206
	v_mul_f32_e32 v207, v41, v207
	ds_write_b128 v210, v[204:207] offset:7168
	s_waitcnt lgkmcnt(0)
	s_barrier
; #define GAS __attribute__((address_space(1)))
; #define LAS __attribute__((address_space(3)))
; #define LDS_WAIT() asm volatile("s_waitcnt lgkmcnt(0)" ::: "memory")
;     ...
; #pragma unroll
;     for (int i = 0; i < 32; ++i) v[i] = sc >= 0 ? W[(size_t)(k0 + 2 * i + (lane >> 5)) * Nsrc + sc] : 0.f;
; #pragma unroll
;     for (int i = 0; i < 32; ++i) { const int k = k0 + 2 * i + (lane >> 5); float x = v[i] * wscale; if (KS) x *= (k < ksplit ? ksA[k] : ksB[k - ksplit]); scr[(2 * i + (lane >> 5)) * 33 + (lane & 31)] = x; }
;     LDS_WAIT(); asm volatile("" ::: "memory");
;     const int c = lane & 7;
; #pragma unroll
;     for (int j = 0; j < 4; ++j) { const int n = (lane >> 3) + 8 * j; const LAS float* s = scr + (8 * c) * 33 + n;
;         const unsigned long long o = (unsigned long long)pg8::pk4_fp8(s[0 * 33], s[1 * 33], s[2 * 33], s[3 * 33]) | ((unsigned long long)pg8::pk4_fp8(s[4 * 33], s[5 * 33], s[6 * 33], s[7 * 33]) << 32);
;         *(GAS unsigned long long*)(WT + (size_t)(n0 + n) * K + k0 + 8 * c) = o; }
	s_add_u32 s8, s34, 0x7000
	s_addc_u32 s9, s35, 0
	global_load_dwordx4 v[176:179], v74, s[8:9]
	s_add_u32 s8, s8, 0x20000
	s_addc_u32 s9, s9, 0
	global_load_dwordx4 v[180:183], v74, s[8:9]
	s_add_u32 s8, s8, 0x20000
	s_addc_u32 s9, s9, 0
	global_load_dwordx4 v[184:187], v74, s[8:9]
	s_add_u32 s8, s8, 0x20000
	s_addc_u32 s9, s9, 0
	global_load_dwordx4 v[188:191], v74, s[8:9]
	s_add_u32 s8, s8, 0x20000
	s_addc_u32 s9, s9, 0
	global_load_dwordx4 v[192:195], v74, s[8:9]
	s_add_u32 s8, s8, 0x20000
	s_addc_u32 s9, s9, 0
	global_load_dwordx4 v[196:199], v74, s[8:9]
	s_add_u32 s8, s8, 0x20000
	s_addc_u32 s9, s9, 0
	global_load_dwordx4 v[200:203], v74, s[8:9]
	s_add_u32 s8, s8, 0x20000
	s_addc_u32 s9, s9, 0
	global_load_dwordx4 v[204:207], v74, s[8:9]
	s_add_u32 s6, s36, 0x1400000
	s_addc_u32 s7, s37, 0
	ds_read_b32 v226, v212
	ds_read_b32 v227, v212 offset:512
	ds_read_b32 v228, v212 offset:1024
	ds_read_b32 v229, v212 offset:1536
	ds_read_b32 v230, v212 offset:2048
	ds_read_b32 v231, v212 offset:2560
	ds_read_b32 v232, v212 offset:3072
	ds_read_b32 v233, v212 offset:3584
	ds_read_b32 v234, v212 offset:4096
	ds_read_b32 v235, v212 offset:4608
	ds_read_b32 v236, v212 offset:5120
	ds_read_b32 v237, v212 offset:5632
	ds_read_b32 v238, v212 offset:6144
	ds_read_b32 v239, v212 offset:6656
	ds_read_b32 v240, v212 offset:7168
	ds_read_b32 v241, v212 offset:7680
	s_waitcnt lgkmcnt(0)
	v_max_f32_e32 v226, v226, v226
	v_max_f32_e32 v227, v227, v227
	v_max_f32_e32 v228, v228, v228
	v_max_f32_e32 v229, v229, v229
	v_max_f32_e32 v230, v230, v230
	v_max_f32_e32 v231, v231, v231
	v_max_f32_e32 v232, v232, v232
	v_max_f32_e32 v233, v233, v233
	v_max_f32_e32 v234, v234, v234
	v_max_f32_e32 v235, v235, v235
	v_max_f32_e32 v236, v236, v236
	v_max_f32_e32 v237, v237, v237
	v_max_f32_e32 v238, v238, v238
	v_max_f32_e32 v239, v239, v239
	v_max_f32_e32 v240, v240, v240
	v_max_f32_e32 v241, v241, v241
	v_med3_f32 v226, v226, s62, v95
	v_med3_f32 v227, v227, s62, v95
	v_med3_f32 v228, v228, s62, v95
	v_med3_f32 v229, v229, s62, v95
	v_med3_f32 v230, v230, s62, v95
	v_med3_f32 v231, v231, s62, v95
	v_med3_f32 v232, v232, s62, v95
	v_med3_f32 v233, v233, s62, v95
	v_med3_f32 v234, v234, s62, v95
	v_med3_f32 v235, v235, s62, v95
	v_med3_f32 v236, v236, s62, v95
	v_med3_f32 v237, v237, s62, v95
	v_med3_f32 v238, v238, s62, v95
	v_med3_f32 v239, v239, s62, v95
	v_med3_f32 v240, v240, s62, v95
	v_med3_f32 v241, v241, s62, v95
	v_mov_b32_e32 v242, 0
	v_mov_b32_e32 v243, 0
	v_mov_b32_e32 v244, 0
	v_mov_b32_e32 v245, 0
	v_cvt_pk_fp8_f32 v242, v226, v227
	v_cvt_pk_fp8_f32 v243, v230, v231
	v_cvt_pk_fp8_f32 v244, v234, v235
	v_cvt_pk_fp8_f32 v245, v238, v239
	v_cvt_pk_fp8_f32 v242, v228, v229 op_sel:[0,0,1]
	v_cvt_pk_fp8_f32 v243, v232, v233 op_sel:[0,0,1]
	v_cvt_pk_fp8_f32 v244, v236, v237 op_sel:[0,0,1]
	v_cvt_pk_fp8_f32 v245, v240, v241 op_sel:[0,0,1]
	s_nop 0
	global_store_dwordx4 v77, v[242:245], s[6:7]
	ds_read_b32 v226, v214
	ds_read_b32 v227, v214 offset:512
	ds_read_b32 v228, v214 offset:1024
	ds_read_b32 v229, v214 offset:1536
	ds_read_b32 v230, v214 offset:2048
	ds_read_b32 v231, v214 offset:2560
	ds_read_b32 v232, v214 offset:3072
	ds_read_b32 v233, v214 offset:3584
	ds_read_b32 v234, v214 offset:4096
	ds_read_b32 v235, v214 offset:4608
	ds_read_b32 v236, v214 offset:5120
	ds_read_b32 v237, v214 offset:5632
	ds_read_b32 v238, v214 offset:6144
	ds_read_b32 v239, v214 offset:6656
	ds_read_b32 v240, v214 offset:7168
	ds_read_b32 v241, v214 offset:7680
	s_waitcnt lgkmcnt(0)
	v_max_f32_e32 v226, v226, v226
	v_max_f32_e32 v227, v227, v227
	v_max_f32_e32 v228, v228, v228
	v_max_f32_e32 v229, v229, v229
	v_max_f32_e32 v230, v230, v230
	v_max_f32_e32 v231, v231, v231
	v_max_f32_e32 v232, v232, v232
	v_max_f32_e32 v233, v233, v233
	v_max_f32_e32 v234, v234, v234
	v_max_f32_e32 v235, v235, v235
	v_max_f32_e32 v236, v236, v236
	v_max_f32_e32 v237, v237, v237
	v_max_f32_e32 v238, v238, v238
	v_max_f32_e32 v239, v239, v239
	v_max_f32_e32 v240, v240, v240
	v_max_f32_e32 v241, v241, v241
	v_med3_f32 v226, v226, s62, v95
	v_med3_f32 v227, v227, s62, v95
	v_med3_f32 v228, v228, s62, v95
	v_med3_f32 v229, v229, s62, v95
	v_med3_f32 v230, v230, s62, v95
	v_med3_f32 v231, v231, s62, v95
	v_med3_f32 v232, v232, s62, v95
	v_med3_f32 v233, v233, s62, v95
	v_med3_f32 v234, v234, s62, v95
	v_med3_f32 v235, v235, s62, v95
	v_med3_f32 v236, v236, s62, v95
	v_med3_f32 v237, v237, s62, v95
	v_med3_f32 v238, v238, s62, v95
	v_med3_f32 v239, v239, s62, v95
	v_med3_f32 v240, v240, s62, v95
	v_med3_f32 v241, v241, s62, v95
	v_mov_b32_e32 v242, 0
	v_mov_b32_e32 v243, 0
	v_mov_b32_e32 v244, 0
	v_mov_b32_e32 v245, 0
	v_cvt_pk_fp8_f32 v242, v226, v227
	v_cvt_pk_fp8_f32 v243, v230, v231
	v_cvt_pk_fp8_f32 v244, v234, v235
	v_cvt_pk_fp8_f32 v245, v238, v239
	v_cvt_pk_fp8_f32 v242, v228, v229 op_sel:[0,0,1]
	v_cvt_pk_fp8_f32 v243, v232, v233 op_sel:[0,0,1]
	v_cvt_pk_fp8_f32 v244, v236, v237 op_sel:[0,0,1]
	v_cvt_pk_fp8_f32 v245, v240, v241 op_sel:[0,0,1]
	s_nop 0
	global_store_dwordx4 v78, v[242:245], s[6:7]
	s_waitcnt vmcnt(12)
	v_mul_f32_e32 v144, v34, v144
	v_mul_f32_e32 v145, v34, v145
	v_mul_f32_e32 v146, v34, v146
	v_mul_f32_e32 v147, v34, v147
	ds_write_b128 v209, v[144:147]
	v_mul_f32_e32 v148, v35, v148
	v_mul_f32_e32 v149, v35, v149
	v_mul_f32_e32 v150, v35, v150
	v_mul_f32_e32 v151, v35, v151
	ds_write_b128 v209, v[148:151] offset:1024
	v_mul_f32_e32 v152, v36, v152
	v_mul_f32_e32 v153, v36, v153
	v_mul_f32_e32 v154, v36, v154
	v_mul_f32_e32 v155, v36, v155
	ds_write_b128 v209, v[152:155] offset:2048
	v_mul_f32_e32 v156, v37, v156
	v_mul_f32_e32 v157, v37, v157
	v_mul_f32_e32 v158, v37, v158
	v_mul_f32_e32 v159, v37, v159
	ds_write_b128 v209, v[156:159] offset:3072
	v_mul_f32_e32 v160, v38, v160
	v_mul_f32_e32 v161, v38, v161
	v_mul_f32_e32 v162, v38, v162
	v_mul_f32_e32 v163, v38, v163
	ds_write_b128 v209, v[160:163] offset:4096
	v_mul_f32_e32 v164, v39, v164
	v_mul_f32_e32 v165, v39, v165
	v_mul_f32_e32 v166, v39, v166
	v_mul_f32_e32 v167, v39, v167
	ds_write_b128 v209, v[164:167] offset:5120
	v_mul_f32_e32 v168, v40, v168
	v_mul_f32_e32 v169, v40, v169
	v_mul_f32_e32 v170, v40, v170
	v_mul_f32_e32 v171, v40, v171
	ds_write_b128 v209, v[168:171] offset:6144
	v_mul_f32_e32 v172, v41, v172
	v_mul_f32_e32 v173, v41, v173
	v_mul_f32_e32 v174, v41, v174
	v_mul_f32_e32 v175, v41, v175
	ds_write_b128 v209, v[172:175] offset:7168
	s_waitcnt lgkmcnt(0)
	s_barrier
; #define GAS __attribute__((address_space(1)))
; #define LAS __attribute__((address_space(3)))
; #define LDS_WAIT() asm volatile("s_waitcnt lgkmcnt(0)" ::: "memory")
;     ...
; #pragma unroll
;     for (int i = 0; i < 32; ++i) v[i] = sc >= 0 ? W[(size_t)(k0 + 2 * i + (lane >> 5)) * Nsrc + sc] : 0.f;
; #pragma unroll
;     for (int i = 0; i < 32; ++i) { const int k = k0 + 2 * i + (lane >> 5); float x = v[i] * wscale; if (KS) x *= (k < ksplit ? ksA[k] : ksB[k - ksplit]); scr[(2 * i + (lane >> 5)) * 33 + (lane & 31)] = x; }
;     LDS_WAIT(); asm volatile("" ::: "memory");
;     const int c = lane & 7;
; #pragma unroll
;     for (int j = 0; j < 4; ++j) { const int n = (lane >> 3) + 8 * j; const LAS float* s = scr + (8 * c) * 33 + n;
;         const unsigned long long o = (unsigned long long)pg8::pk4_fp8(s[0 * 33], s[1 * 33], s[2 * 33], s[3 * 33]) | ((unsigned long long)pg8::pk4_fp8(s[4 * 33], s[5 * 33], s[6 * 33], s[7 * 33]) << 32);
;         *(GAS unsigned long long*)(WT + (size_t)(n0 + n) * K + k0 + 8 * c) = o; }
	s_add_u32 s8, s34, 0x8000
	s_addc_u32 s9, s35, 0
	global_load_dwordx4 v[144:147], v74, s[8:9]
	s_add_u32 s8, s8, 0x20000
	s_addc_u32 s9, s9, 0
	global_load_dwordx4 v[148:151], v74, s[8:9]
	s_add_u32 s8, s8, 0x20000
	s_addc_u32 s9, s9, 0
	global_load_dwordx4 v[152:155], v74, s[8:9]
	s_add_u32 s8, s8, 0x20000
	s_addc_u32 s9, s9, 0
	global_load_dwordx4 v[156:159], v74, s[8:9]
	s_add_u32 s8, s8, 0x20000
	s_addc_u32 s9, s9, 0
	global_load_dwordx4 v[160:163], v74, s[8:9]
	s_add_u32 s8, s8, 0x20000
	s_addc_u32 s9, s9, 0
	global_load_dwordx4 v[164:167], v74, s[8:9]
	s_add_u32 s8, s8, 0x20000
	s_addc_u32 s9, s9, 0
	global_load_dwordx4 v[168:171], v74, s[8:9]
	s_add_u32 s8, s8, 0x20000
	s_addc_u32 s9, s9, 0
	global_load_dwordx4 v[172:175], v74, s[8:9]
	s_add_u32 s6, s36, 0x1800000
	s_addc_u32 s7, s37, 0
	ds_read_b32 v226, v211
	ds_read_b32 v227, v211 offset:512
	ds_read_b32 v228, v211 offset:1024
	ds_read_b32 v229, v211 offset:1536
	ds_read_b32 v230, v211 offset:2048
	ds_read_b32 v231, v211 offset:2560
	ds_read_b32 v232, v211 offset:3072
	ds_read_b32 v233, v211 offset:3584
	ds_read_b32 v234, v211 offset:4096
	ds_read_b32 v235, v211 offset:4608
	ds_read_b32 v236, v211 offset:5120
	ds_read_b32 v237, v211 offset:5632
	ds_read_b32 v238, v211 offset:6144
	ds_read_b32 v239, v211 offset:6656
	ds_read_b32 v240, v211 offset:7168
	ds_read_b32 v241, v211 offset:7680
	s_waitcnt lgkmcnt(0)
	v_max_f32_e32 v226, v226, v226
	v_max_f32_e32 v227, v227, v227
	v_max_f32_e32 v228, v228, v228
	v_max_f32_e32 v229, v229, v229
	v_max_f32_e32 v230, v230, v230
	v_max_f32_e32 v231, v231, v231
	v_max_f32_e32 v232, v232, v232
	v_max_f32_e32 v233, v233, v233
	v_max_f32_e32 v234, v234, v234
	v_max_f32_e32 v235, v235, v235
	v_max_f32_e32 v236, v236, v236
	v_max_f32_e32 v237, v237, v237
	v_max_f32_e32 v238, v238, v238
	v_max_f32_e32 v239, v239, v239
	v_max_f32_e32 v240, v240, v240
	v_max_f32_e32 v241, v241, v241
	v_med3_f32 v226, v226, s62, v95
	v_med3_f32 v227, v227, s62, v95
	v_med3_f32 v228, v228, s62, v95
	v_med3_f32 v229, v229, s62, v95
	v_med3_f32 v230, v230, s62, v95
	v_med3_f32 v231, v231, s62, v95
	v_med3_f32 v232, v232, s62, v95
	v_med3_f32 v233, v233, s62, v95
	v_med3_f32 v234, v234, s62, v95
	v_med3_f32 v235, v235, s62, v95
	v_med3_f32 v236, v236, s62, v95
	v_med3_f32 v237, v237, s62, v95
	v_med3_f32 v238, v238, s62, v95
	v_med3_f32 v239, v239, s62, v95
	v_med3_f32 v240, v240, s62, v95
	v_med3_f32 v241, v241, s62, v95
	v_mov_b32_e32 v242, 0
	v_mov_b32_e32 v243, 0
	v_mov_b32_e32 v244, 0
	v_mov_b32_e32 v245, 0
	v_cvt_pk_fp8_f32 v242, v226, v227
	v_cvt_pk_fp8_f32 v243, v230, v231
	v_cvt_pk_fp8_f32 v244, v234, v235
	v_cvt_pk_fp8_f32 v245, v238, v239
	v_cvt_pk_fp8_f32 v242, v228, v229 op_sel:[0,0,1]
	v_cvt_pk_fp8_f32 v243, v232, v233 op_sel:[0,0,1]
	v_cvt_pk_fp8_f32 v244, v236, v237 op_sel:[0,0,1]
	v_cvt_pk_fp8_f32 v245, v240, v241 op_sel:[0,0,1]
	s_nop 0
	global_store_dwordx4 v77, v[242:245], s[6:7]
	ds_read_b32 v226, v213
	ds_read_b32 v227, v213 offset:512
	ds_read_b32 v228, v213 offset:1024
	ds_read_b32 v229, v213 offset:1536
	ds_read_b32 v230, v213 offset:2048
	ds_read_b32 v231, v213 offset:2560
	ds_read_b32 v232, v213 offset:3072
	ds_read_b32 v233, v213 offset:3584
	ds_read_b32 v234, v213 offset:4096
	ds_read_b32 v235, v213 offset:4608
	ds_read_b32 v236, v213 offset:5120
	ds_read_b32 v237, v213 offset:5632
	ds_read_b32 v238, v213 offset:6144
	ds_read_b32 v239, v213 offset:6656
	ds_read_b32 v240, v213 offset:7168
	ds_read_b32 v241, v213 offset:7680
	s_waitcnt lgkmcnt(0)
	v_max_f32_e32 v226, v226, v226
	v_max_f32_e32 v227, v227, v227
	v_max_f32_e32 v228, v228, v228
	v_max_f32_e32 v229, v229, v229
	v_max_f32_e32 v230, v230, v230
	v_max_f32_e32 v231, v231, v231
	v_max_f32_e32 v232, v232, v232
	v_max_f32_e32 v233, v233, v233
	v_max_f32_e32 v234, v234, v234
	v_max_f32_e32 v235, v235, v235
	v_max_f32_e32 v236, v236, v236
	v_max_f32_e32 v237, v237, v237
	v_max_f32_e32 v238, v238, v238
	v_max_f32_e32 v239, v239, v239
	v_max_f32_e32 v240, v240, v240
	v_max_f32_e32 v241, v241, v241
	v_med3_f32 v226, v226, s62, v95
	v_med3_f32 v227, v227, s62, v95
	v_med3_f32 v228, v228, s62, v95
	v_med3_f32 v229, v229, s62, v95
	v_med3_f32 v230, v230, s62, v95
	v_med3_f32 v231, v231, s62, v95
	v_med3_f32 v232, v232, s62, v95
	v_med3_f32 v233, v233, s62, v95
	v_med3_f32 v234, v234, s62, v95
	v_med3_f32 v235, v235, s62, v95
	v_med3_f32 v236, v236, s62, v95
	v_med3_f32 v237, v237, s62, v95
	v_med3_f32 v238, v238, s62, v95
	v_med3_f32 v239, v239, s62, v95
	v_med3_f32 v240, v240, s62, v95
	v_med3_f32 v241, v241, s62, v95
	v_mov_b32_e32 v242, 0
	v_mov_b32_e32 v243, 0
	v_mov_b32_e32 v244, 0
	v_mov_b32_e32 v245, 0
	v_cvt_pk_fp8_f32 v242, v226, v227
	v_cvt_pk_fp8_f32 v243, v230, v231
	v_cvt_pk_fp8_f32 v244, v234, v235
	v_cvt_pk_fp8_f32 v245, v238, v239
	v_cvt_pk_fp8_f32 v242, v228, v229 op_sel:[0,0,1]
	v_cvt_pk_fp8_f32 v243, v232, v233 op_sel:[0,0,1]
	v_cvt_pk_fp8_f32 v244, v236, v237 op_sel:[0,0,1]
	v_cvt_pk_fp8_f32 v245, v240, v241 op_sel:[0,0,1]
	s_nop 0
	global_store_dwordx4 v78, v[242:245], s[6:7]
	s_waitcnt vmcnt(12)
	v_mul_f32_e32 v176, v34, v176
	v_mul_f32_e32 v177, v34, v177
	v_mul_f32_e32 v178, v34, v178
	v_mul_f32_e32 v179, v34, v179
	ds_write_b128 v210, v[176:179]
	v_mul_f32_e32 v180, v35, v180
	v_mul_f32_e32 v181, v35, v181
	v_mul_f32_e32 v182, v35, v182
	v_mul_f32_e32 v183, v35, v183
	ds_write_b128 v210, v[180:183] offset:1024
	v_mul_f32_e32 v184, v36, v184
	v_mul_f32_e32 v185, v36, v185
	v_mul_f32_e32 v186, v36, v186
	v_mul_f32_e32 v187, v36, v187
	ds_write_b128 v210, v[184:187] offset:2048
	v_mul_f32_e32 v188, v37, v188
	v_mul_f32_e32 v189, v37, v189
	v_mul_f32_e32 v190, v37, v190
	v_mul_f32_e32 v191, v37, v191
	ds_write_b128 v210, v[188:191] offset:3072
	v_mul_f32_e32 v192, v38, v192
	v_mul_f32_e32 v193, v38, v193
	v_mul_f32_e32 v194, v38, v194
	v_mul_f32_e32 v195, v38, v195
	ds_write_b128 v210, v[192:195] offset:4096
	v_mul_f32_e32 v196, v39, v196
	v_mul_f32_e32 v197, v39, v197
	v_mul_f32_e32 v198, v39, v198
	v_mul_f32_e32 v199, v39, v199
	ds_write_b128 v210, v[196:199] offset:5120
	v_mul_f32_e32 v200, v40, v200
	v_mul_f32_e32 v201, v40, v201
	v_mul_f32_e32 v202, v40, v202
	v_mul_f32_e32 v203, v40, v203
	ds_write_b128 v210, v[200:203] offset:6144
	v_mul_f32_e32 v204, v41, v204
	v_mul_f32_e32 v205, v41, v205
	v_mul_f32_e32 v206, v41, v206
	v_mul_f32_e32 v207, v41, v207
	ds_write_b128 v210, v[204:207] offset:7168
	s_waitcnt lgkmcnt(0)
	s_barrier
; #define GAS __attribute__((address_space(1)))
; #define LAS __attribute__((address_space(3)))
; #define LDS_WAIT() asm volatile("s_waitcnt lgkmcnt(0)" ::: "memory")
;     ...
; #pragma unroll
;     for (int i = 0; i < 32; ++i) v[i] = sc >= 0 ? W[(size_t)(k0 + 2 * i + (lane >> 5)) * Nsrc + sc] : 0.f;
; #pragma unroll
;     for (int i = 0; i < 32; ++i) { const int k = k0 + 2 * i + (lane >> 5); float x = v[i] * wscale; if (KS) x *= (k < ksplit ? ksA[k] : ksB[k - ksplit]); scr[(2 * i + (lane >> 5)) * 33 + (lane & 31)] = x; }
;     LDS_WAIT(); asm volatile("" ::: "memory");
;     const int c = lane & 7;
; #pragma unroll
;     for (int j = 0; j < 4; ++j) { const int n = (lane >> 3) + 8 * j; const LAS float* s = scr + (8 * c) * 33 + n;
;         const unsigned long long o = (unsigned long long)pg8::pk4_fp8(s[0 * 33], s[1 * 33], s[2 * 33], s[3 * 33]) | ((unsigned long long)pg8::pk4_fp8(s[4 * 33], s[5 * 33], s[6 * 33], s[7 * 33]) << 32);
;         *(GAS unsigned long long*)(WT + (size_t)(n0 + n) * K + k0 + 8 * c) = o; }
	s_add_u32 s8, s34, 0x9000
	s_addc_u32 s9, s35, 0
	global_load_dwordx4 v[176:179], v74, s[8:9]
	s_add_u32 s8, s8, 0x20000
	s_addc_u32 s9, s9, 0
	global_load_dwordx4 v[180:183], v74, s[8:9]
	s_add_u32 s8, s8, 0x20000
	s_addc_u32 s9, s9, 0
	global_load_dwordx4 v[184:187], v74, s[8:9]
	s_add_u32 s8, s8, 0x20000
	s_addc_u32 s9, s9, 0
	global_load_dwordx4 v[188:191], v74, s[8:9]
	s_add_u32 s8, s8, 0x20000
	s_addc_u32 s9, s9, 0
	global_load_dwordx4 v[192:195], v74, s[8:9]
	s_add_u32 s8, s8, 0x20000
	s_addc_u32 s9, s9, 0
	global_load_dwordx4 v[196:199], v74, s[8:9]
	s_add_u32 s8, s8, 0x20000
	s_addc_u32 s9, s9, 0
	global_load_dwordx4 v[200:203], v74, s[8:9]
	s_add_u32 s8, s8, 0x20000
	s_addc_u32 s9, s9, 0
	global_load_dwordx4 v[204:207], v74, s[8:9]
	s_add_u32 s6, s36, 0x1c00000
	s_addc_u32 s7, s37, 0
	ds_read_b32 v226, v212
	ds_read_b32 v227, v212 offset:512
	ds_read_b32 v228, v212 offset:1024
	ds_read_b32 v229, v212 offset:1536
	ds_read_b32 v230, v212 offset:2048
	ds_read_b32 v231, v212 offset:2560
	ds_read_b32 v232, v212 offset:3072
	ds_read_b32 v233, v212 offset:3584
	ds_read_b32 v234, v212 offset:4096
	ds_read_b32 v235, v212 offset:4608
	ds_read_b32 v236, v212 offset:5120
	ds_read_b32 v237, v212 offset:5632
	ds_read_b32 v238, v212 offset:6144
	ds_read_b32 v239, v212 offset:6656
	ds_read_b32 v240, v212 offset:7168
	ds_read_b32 v241, v212 offset:7680
	s_waitcnt lgkmcnt(0)
	v_max_f32_e32 v226, v226, v226
	v_max_f32_e32 v227, v227, v227
	v_max_f32_e32 v228, v228, v228
	v_max_f32_e32 v229, v229, v229
	v_max_f32_e32 v230, v230, v230
	v_max_f32_e32 v231, v231, v231
	v_max_f32_e32 v232, v232, v232
	v_max_f32_e32 v233, v233, v233
	v_max_f32_e32 v234, v234, v234
	v_max_f32_e32 v235, v235, v235
	v_max_f32_e32 v236, v236, v236
	v_max_f32_e32 v237, v237, v237
	v_max_f32_e32 v238, v238, v238
	v_max_f32_e32 v239, v239, v239
	v_max_f32_e32 v240, v240, v240
	v_max_f32_e32 v241, v241, v241
	v_med3_f32 v226, v226, s62, v95
	v_med3_f32 v227, v227, s62, v95
	v_med3_f32 v228, v228, s62, v95
	v_med3_f32 v229, v229, s62, v95
	v_med3_f32 v230, v230, s62, v95
	v_med3_f32 v231, v231, s62, v95
	v_med3_f32 v232, v232, s62, v95
	v_med3_f32 v233, v233, s62, v95
	v_med3_f32 v234, v234, s62, v95
	v_med3_f32 v235, v235, s62, v95
	v_med3_f32 v236, v236, s62, v95
	v_med3_f32 v237, v237, s62, v95
	v_med3_f32 v238, v238, s62, v95
	v_med3_f32 v239, v239, s62, v95
	v_med3_f32 v240, v240, s62, v95
	v_med3_f32 v241, v241, s62, v95
	v_mov_b32_e32 v242, 0
	v_mov_b32_e32 v243, 0
	v_mov_b32_e32 v244, 0
	v_mov_b32_e32 v245, 0
	v_cvt_pk_fp8_f32 v242, v226, v227
	v_cvt_pk_fp8_f32 v243, v230, v231
	v_cvt_pk_fp8_f32 v244, v234, v235
	v_cvt_pk_fp8_f32 v245, v238, v239
	v_cvt_pk_fp8_f32 v242, v228, v229 op_sel:[0,0,1]
	v_cvt_pk_fp8_f32 v243, v232, v233 op_sel:[0,0,1]
	v_cvt_pk_fp8_f32 v244, v236, v237 op_sel:[0,0,1]
	v_cvt_pk_fp8_f32 v245, v240, v241 op_sel:[0,0,1]
	s_nop 0
	global_store_dwordx4 v77, v[242:245], s[6:7]
	ds_read_b32 v226, v214
	ds_read_b32 v227, v214 offset:512
	ds_read_b32 v228, v214 offset:1024
	ds_read_b32 v229, v214 offset:1536
	ds_read_b32 v230, v214 offset:2048
	ds_read_b32 v231, v214 offset:2560
	ds_read_b32 v232, v214 offset:3072
	ds_read_b32 v233, v214 offset:3584
	ds_read_b32 v234, v214 offset:4096
	ds_read_b32 v235, v214 offset:4608
	ds_read_b32 v236, v214 offset:5120
	ds_read_b32 v237, v214 offset:5632
	ds_read_b32 v238, v214 offset:6144
	ds_read_b32 v239, v214 offset:6656
	ds_read_b32 v240, v214 offset:7168
	ds_read_b32 v241, v214 offset:7680
	s_waitcnt lgkmcnt(0)
	v_max_f32_e32 v226, v226, v226
	v_max_f32_e32 v227, v227, v227
	v_max_f32_e32 v228, v228, v228
	v_max_f32_e32 v229, v229, v229
	v_max_f32_e32 v230, v230, v230
	v_max_f32_e32 v231, v231, v231
	v_max_f32_e32 v232, v232, v232
	v_max_f32_e32 v233, v233, v233
	v_max_f32_e32 v234, v234, v234
	v_max_f32_e32 v235, v235, v235
	v_max_f32_e32 v236, v236, v236
	v_max_f32_e32 v237, v237, v237
	v_max_f32_e32 v238, v238, v238
	v_max_f32_e32 v239, v239, v239
	v_max_f32_e32 v240, v240, v240
	v_max_f32_e32 v241, v241, v241
	v_med3_f32 v226, v226, s62, v95
	v_med3_f32 v227, v227, s62, v95
	v_med3_f32 v228, v228, s62, v95
	v_med3_f32 v229, v229, s62, v95
	v_med3_f32 v230, v230, s62, v95
	v_med3_f32 v231, v231, s62, v95
	v_med3_f32 v232, v232, s62, v95
	v_med3_f32 v233, v233, s62, v95
	v_med3_f32 v234, v234, s62, v95
	v_med3_f32 v235, v235, s62, v95
	v_med3_f32 v236, v236, s62, v95
	v_med3_f32 v237, v237, s62, v95
	v_med3_f32 v238, v238, s62, v95
	v_med3_f32 v239, v239, s62, v95
	v_med3_f32 v240, v240, s62, v95
	v_med3_f32 v241, v241, s62, v95
	v_mov_b32_e32 v242, 0
	v_mov_b32_e32 v243, 0
	v_mov_b32_e32 v244, 0
	v_mov_b32_e32 v245, 0
	v_cvt_pk_fp8_f32 v242, v226, v227
	v_cvt_pk_fp8_f32 v243, v230, v231
	v_cvt_pk_fp8_f32 v244, v234, v235
	v_cvt_pk_fp8_f32 v245, v238, v239
	v_cvt_pk_fp8_f32 v242, v228, v229 op_sel:[0,0,1]
	v_cvt_pk_fp8_f32 v243, v232, v233 op_sel:[0,0,1]
	v_cvt_pk_fp8_f32 v244, v236, v237 op_sel:[0,0,1]
	v_cvt_pk_fp8_f32 v245, v240, v241 op_sel:[0,0,1]
	s_nop 0
	global_store_dwordx4 v78, v[242:245], s[6:7]
	s_waitcnt vmcnt(12)
	v_mul_f32_e32 v144, v34, v144
	v_mul_f32_e32 v145, v34, v145
	v_mul_f32_e32 v146, v34, v146
	v_mul_f32_e32 v147, v34, v147
	ds_write_b128 v209, v[144:147]
	v_mul_f32_e32 v148, v35, v148
	v_mul_f32_e32 v149, v35, v149
	v_mul_f32_e32 v150, v35, v150
	v_mul_f32_e32 v151, v35, v151
	ds_write_b128 v209, v[148:151] offset:1024
	v_mul_f32_e32 v152, v36, v152
	v_mul_f32_e32 v153, v36, v153
	v_mul_f32_e32 v154, v36, v154
	v_mul_f32_e32 v155, v36, v155
	ds_write_b128 v209, v[152:155] offset:2048
	v_mul_f32_e32 v156, v37, v156
	v_mul_f32_e32 v157, v37, v157
	v_mul_f32_e32 v158, v37, v158
	v_mul_f32_e32 v159, v37, v159
	ds_write_b128 v209, v[156:159] offset:3072
	v_mul_f32_e32 v160, v38, v160
	v_mul_f32_e32 v161, v38, v161
	v_mul_f32_e32 v162, v38, v162
	v_mul_f32_e32 v163, v38, v163
	ds_write_b128 v209, v[160:163] offset:4096
	v_mul_f32_e32 v164, v39, v164
	v_mul_f32_e32 v165, v39, v165
	v_mul_f32_e32 v166, v39, v166
	v_mul_f32_e32 v167, v39, v167
	ds_write_b128 v209, v[164:167] offset:5120
	v_mul_f32_e32 v168, v40, v168
	v_mul_f32_e32 v169, v40, v169
	v_mul_f32_e32 v170, v40, v170
	v_mul_f32_e32 v171, v40, v171
	ds_write_b128 v209, v[168:171] offset:6144
	v_mul_f32_e32 v172, v41, v172
	v_mul_f32_e32 v173, v41, v173
	v_mul_f32_e32 v174, v41, v174
	v_mul_f32_e32 v175, v41, v175
	ds_write_b128 v209, v[172:175] offset:7168
	s_waitcnt lgkmcnt(0)
	s_barrier
; #define GAS __attribute__((address_space(1)))
; #define LAS __attribute__((address_space(3)))
; #define LDS_WAIT() asm volatile("s_waitcnt lgkmcnt(0)" ::: "memory")
; __device__ __forceinline__ unsigned pk4_fp8(float a, float b, float c, float d) {
;     a = fminf(fmaxf(a, -448.f), 448.f); b = fminf(fmaxf(b, -448.f), 448.f); c = fminf(fmaxf(c, -448.f), 448.f); d = fminf(fmaxf(d, -448.f), 448.f);
;     int w = __builtin_amdgcn_cvt_pk_fp8_f32(a, b, 0, false); w = __builtin_amdgcn_cvt_pk_fp8_f32(c, d, w, true); return (unsigned)w; }
;     ...
;     for (int i = 0; i < 32; ++i) v[i] = sc >= 0 ? W[(size_t)(k0 + 2 * i + (lane >> 5)) * Nsrc + sc] : 0.f;
; #pragma unroll
;     for (int i = 0; i < 32; ++i) { const int k = k0 + 2 * i + (lane >> 5); float x = v[i] * wscale; if (KS) x *= (k < ksplit ? ksA[k] : ksB[k - ksplit]); scr[(2 * i + (lane >> 5)) * 33 + (lane & 31)] = x; }
;     LDS_WAIT(); asm volatile("" ::: "memory");
;     const int c = lane & 7;
; #pragma unroll
;     for (int j = 0; j < 4; ++j) { const int n = (lane >> 3) + 8 * j; const LAS float* s = scr + (8 * c) * 33 + n;
;         const unsigned long long o = (unsigned long long)pg8::pk4_fp8(s[0 * 33], s[1 * 33], s[2 * 33], s[3 * 33]) | ((unsigned long long)pg8::pk4_fp8(s[4 * 33], s[5 * 33], s[6 * 33], s[7 * 33]) << 32);
;         *(GAS unsigned long long*)(WT + (size_t)(n0 + n) * K + k0 + 8 * c) = o; }
	s_add_u32 s8, s34, 0xa000
	s_addc_u32 s9, s35, 0
	global_load_dwordx4 v[144:147], v74, s[8:9]
	s_add_u32 s8, s8, 0x20000
	s_addc_u32 s9, s9, 0
	global_load_dwordx4 v[148:151], v74, s[8:9]
	s_add_u32 s8, s8, 0x20000
	s_addc_u32 s9, s9, 0
	global_load_dwordx4 v[152:155], v74, s[8:9]
	s_add_u32 s8, s8, 0x20000
	s_addc_u32 s9, s9, 0
	global_load_dwordx4 v[156:159], v74, s[8:9]
	s_add_u32 s8, s8, 0x20000
	s_addc_u32 s9, s9, 0
	global_load_dwordx4 v[160:163], v74, s[8:9]
	s_add_u32 s8, s8, 0x20000
	s_addc_u32 s9, s9, 0
	global_load_dwordx4 v[164:167], v74, s[8:9]
	s_add_u32 s8, s8, 0x20000
	s_addc_u32 s9, s9, 0
	global_load_dwordx4 v[168:171], v74, s[8:9]
	s_add_u32 s8, s8, 0x20000
	s_addc_u32 s9, s9, 0
	global_load_dwordx4 v[172:175], v74, s[8:9]
	s_add_u32 s6, s36, 0x2000000
	s_addc_u32 s7, s37, 0
	ds_read_b32 v226, v211
	ds_read_b32 v227, v211 offset:512
	ds_read_b32 v228, v211 offset:1024
	ds_read_b32 v229, v211 offset:1536
	ds_read_b32 v230, v211 offset:2048
	ds_read_b32 v231, v211 offset:2560
	ds_read_b32 v232, v211 offset:3072
	ds_read_b32 v233, v211 offset:3584
	ds_read_b32 v234, v211 offset:4096
	ds_read_b32 v235, v211 offset:4608
	ds_read_b32 v236, v211 offset:5120
	ds_read_b32 v237, v211 offset:5632
	ds_read_b32 v238, v211 offset:6144
	ds_read_b32 v239, v211 offset:6656
	ds_read_b32 v240, v211 offset:7168
	ds_read_b32 v241, v211 offset:7680
	s_waitcnt lgkmcnt(0)
	v_max_f32_e32 v226, v226, v226
	v_max_f32_e32 v227, v227, v227
	v_max_f32_e32 v228, v228, v228
	v_max_f32_e32 v229, v229, v229
	v_max_f32_e32 v230, v230, v230
	v_max_f32_e32 v231, v231, v231
	v_max_f32_e32 v232, v232, v232
	v_max_f32_e32 v233, v233, v233
	v_max_f32_e32 v234, v234, v234
	v_max_f32_e32 v235, v235, v235
	v_max_f32_e32 v236, v236, v236
	v_max_f32_e32 v237, v237, v237
	v_max_f32_e32 v238, v238, v238
	v_max_f32_e32 v239, v239, v239
	v_max_f32_e32 v240, v240, v240
	v_max_f32_e32 v241, v241, v241
	v_med3_f32 v226, v226, s62, v95
	v_med3_f32 v227, v227, s62, v95
	v_med3_f32 v228, v228, s62, v95
	v_med3_f32 v229, v229, s62, v95
	v_med3_f32 v230, v230, s62, v95
	v_med3_f32 v231, v231, s62, v95
	v_med3_f32 v232, v232, s62, v95
	v_med3_f32 v233, v233, s62, v95
	v_med3_f32 v234, v234, s62, v95
	v_med3_f32 v235, v235, s62, v95
	v_med3_f32 v236, v236, s62, v95
	v_med3_f32 v237, v237, s62, v95
	v_med3_f32 v238, v238, s62, v95
	v_med3_f32 v239, v239, s62, v95
	v_med3_f32 v240, v240, s62, v95
	v_med3_f32 v241, v241, s62, v95
	v_mov_b32_e32 v242, 0
	v_mov_b32_e32 v243, 0
	v_mov_b32_e32 v244, 0
	v_mov_b32_e32 v245, 0
	v_cvt_pk_fp8_f32 v242, v226, v227
	v_cvt_pk_fp8_f32 v243, v230, v231
	v_cvt_pk_fp8_f32 v244, v234, v235
	v_cvt_pk_fp8_f32 v245, v238, v239
	v_cvt_pk_fp8_f32 v242, v228, v229 op_sel:[0,0,1]
	v_cvt_pk_fp8_f32 v243, v232, v233 op_sel:[0,0,1]
	v_cvt_pk_fp8_f32 v244, v236, v237 op_sel:[0,0,1]
	v_cvt_pk_fp8_f32 v245, v240, v241 op_sel:[0,0,1]
	s_nop 0
	global_store_dwordx4 v77, v[242:245], s[6:7]
	ds_read_b32 v226, v213
	ds_read_b32 v227, v213 offset:512
	ds_read_b32 v228, v213 offset:1024
	ds_read_b32 v229, v213 offset:1536
	ds_read_b32 v230, v213 offset:2048
	ds_read_b32 v231, v213 offset:2560
	ds_read_b32 v232, v213 offset:3072
	ds_read_b32 v233, v213 offset:3584
	ds_read_b32 v234, v213 offset:4096
	ds_read_b32 v235, v213 offset:4608
	ds_read_b32 v236, v213 offset:5120
	ds_read_b32 v237, v213 offset:5632
	ds_read_b32 v238, v213 offset:6144
	ds_read_b32 v239, v213 offset:6656
	ds_read_b32 v240, v213 offset:7168
	ds_read_b32 v241, v213 offset:7680
	s_waitcnt lgkmcnt(0)
	v_max_f32_e32 v226, v226, v226
	v_max_f32_e32 v227, v227, v227
	v_max_f32_e32 v228, v228, v228
	v_max_f32_e32 v229, v229, v229
	v_max_f32_e32 v230, v230, v230
	v_max_f32_e32 v231, v231, v231
	v_max_f32_e32 v232, v232, v232
	v_max_f32_e32 v233, v233, v233
	v_max_f32_e32 v234, v234, v234
	v_max_f32_e32 v235, v235, v235
	v_max_f32_e32 v236, v236, v236
	v_max_f32_e32 v237, v237, v237
	v_max_f32_e32 v238, v238, v238
	v_max_f32_e32 v239, v239, v239
	v_max_f32_e32 v240, v240, v240
	v_max_f32_e32 v241, v241, v241
	v_med3_f32 v226, v226, s62, v95
	v_med3_f32 v227, v227, s62, v95
	v_med3_f32 v228, v228, s62, v95
	v_med3_f32 v229, v229, s62, v95
	v_med3_f32 v230, v230, s62, v95
	v_med3_f32 v231, v231, s62, v95
	v_med3_f32 v232, v232, s62, v95
	v_med3_f32 v233, v233, s62, v95
	v_med3_f32 v234, v234, s62, v95
	v_med3_f32 v235, v235, s62, v95
	v_med3_f32 v236, v236, s62, v95
	v_med3_f32 v237, v237, s62, v95
	v_med3_f32 v238, v238, s62, v95
	v_med3_f32 v239, v239, s62, v95
	v_med3_f32 v240, v240, s62, v95
	v_med3_f32 v241, v241, s62, v95
	v_mov_b32_e32 v242, 0
	v_mov_b32_e32 v243, 0
	v_mov_b32_e32 v244, 0
	v_mov_b32_e32 v245, 0
	v_cvt_pk_fp8_f32 v242, v226, v227
	v_cvt_pk_fp8_f32 v243, v230, v231
	v_cvt_pk_fp8_f32 v244, v234, v235
	v_cvt_pk_fp8_f32 v245, v238, v239
	v_cvt_pk_fp8_f32 v242, v228, v229 op_sel:[0,0,1]
	v_cvt_pk_fp8_f32 v243, v232, v233 op_sel:[0,0,1]
	v_cvt_pk_fp8_f32 v244, v236, v237 op_sel:[0,0,1]
	v_cvt_pk_fp8_f32 v245, v240, v241 op_sel:[0,0,1]
	s_nop 0
	global_store_dwordx4 v78, v[242:245], s[6:7]
	s_waitcnt vmcnt(12)
	v_mul_f32_e32 v176, v34, v176
	v_mul_f32_e32 v177, v34, v177
	v_mul_f32_e32 v178, v34, v178
	v_mul_f32_e32 v179, v34, v179
	ds_write_b128 v210, v[176:179]
	v_mul_f32_e32 v180, v35, v180
	v_mul_f32_e32 v181, v35, v181
	v_mul_f32_e32 v182, v35, v182
	v_mul_f32_e32 v183, v35, v183
	ds_write_b128 v210, v[180:183] offset:1024
	v_mul_f32_e32 v184, v36, v184
	v_mul_f32_e32 v185, v36, v185
	v_mul_f32_e32 v186, v36, v186
	v_mul_f32_e32 v187, v36, v187
	ds_write_b128 v210, v[184:187] offset:2048
	v_mul_f32_e32 v188, v37, v188
	v_mul_f32_e32 v189, v37, v189
	v_mul_f32_e32 v190, v37, v190
	v_mul_f32_e32 v191, v37, v191
	ds_write_b128 v210, v[188:191] offset:3072
	v_mul_f32_e32 v192, v38, v192
	v_mul_f32_e32 v193, v38, v193
	v_mul_f32_e32 v194, v38, v194
	v_mul_f32_e32 v195, v38, v195
	ds_write_b128 v210, v[192:195] offset:4096
	v_mul_f32_e32 v196, v39, v196
	v_mul_f32_e32 v197, v39, v197
	v_mul_f32_e32 v198, v39, v198
	v_mul_f32_e32 v199, v39, v199
	ds_write_b128 v210, v[196:199] offset:5120
	v_mul_f32_e32 v200, v40, v200
	v_mul_f32_e32 v201, v40, v201
	v_mul_f32_e32 v202, v40, v202
	v_mul_f32_e32 v203, v40, v203
	ds_write_b128 v210, v[200:203] offset:6144
	v_mul_f32_e32 v204, v41, v204
	v_mul_f32_e32 v205, v41, v205
	v_mul_f32_e32 v206, v41, v206
	v_mul_f32_e32 v207, v41, v207
	ds_write_b128 v210, v[204:207] offset:7168
	s_waitcnt lgkmcnt(0)
	s_barrier
; #define GAS __attribute__((address_space(1)))
; #define LAS __attribute__((address_space(3)))
; #define LDS_WAIT() asm volatile("s_waitcnt lgkmcnt(0)" ::: "memory")
; __device__ __forceinline__ unsigned pk4_fp8(float a, float b, float c, float d) {
;     a = fminf(fmaxf(a, -448.f), 448.f); b = fminf(fmaxf(b, -448.f), 448.f); c = fminf(fmaxf(c, -448.f), 448.f); d = fminf(fmaxf(d, -448.f), 448.f);
;     int w = __builtin_amdgcn_cvt_pk_fp8_f32(a, b, 0, false); w = __builtin_amdgcn_cvt_pk_fp8_f32(c, d, w, true); return (unsigned)w; }
;     ...
;     for (int i = 0; i < 32; ++i) v[i] = sc >= 0 ? W[(size_t)(k0 + 2 * i + (lane >> 5)) * Nsrc + sc] : 0.f;
; #pragma unroll
;     for (int i = 0; i < 32; ++i) { const int k = k0 + 2 * i + (lane >> 5); float x = v[i] * wscale; if (KS) x *= (k < ksplit ? ksA[k] : ksB[k - ksplit]); scr[(2 * i + (lane >> 5)) * 33 + (lane & 31)] = x; }
;     LDS_WAIT(); asm volatile("" ::: "memory");
;     const int c = lane & 7;
; #pragma unroll
;     for (int j = 0; j < 4; ++j) { const int n = (lane >> 3) + 8 * j; const LAS float* s = scr + (8 * c) * 33 + n;
;         const unsigned long long o = (unsigned long long)pg8::pk4_fp8(s[0 * 33], s[1 * 33], s[2 * 33], s[3 * 33]) | ((unsigned long long)pg8::pk4_fp8(s[4 * 33], s[5 * 33], s[6 * 33], s[7 * 33]) << 32);
;         *(GAS unsigned long long*)(WT + (size_t)(n0 + n) * K + k0 + 8 * c) = o; }
	s_add_u32 s8, s34, 0xb000
	s_addc_u32 s9, s35, 0
	global_load_dwordx4 v[176:179], v74, s[8:9]
	s_add_u32 s8, s8, 0x20000
	s_addc_u32 s9, s9, 0
	global_load_dwordx4 v[180:183], v74, s[8:9]
	s_add_u32 s8, s8, 0x20000
	s_addc_u32 s9, s9, 0
	global_load_dwordx4 v[184:187], v74, s[8:9]
	s_add_u32 s8, s8, 0x20000
	s_addc_u32 s9, s9, 0
	global_load_dwordx4 v[188:191], v74, s[8:9]
	s_add_u32 s8, s8, 0x20000
	s_addc_u32 s9, s9, 0
	global_load_dwordx4 v[192:195], v74, s[8:9]
	s_add_u32 s8, s8, 0x20000
	s_addc_u32 s9, s9, 0
	global_load_dwordx4 v[196:199], v74, s[8:9]
	s_add_u32 s8, s8, 0x20000
	s_addc_u32 s9, s9, 0
	global_load_dwordx4 v[200:203], v74, s[8:9]
	s_add_u32 s8, s8, 0x20000
	s_addc_u32 s9, s9, 0
	global_load_dwordx4 v[204:207], v74, s[8:9]
	s_add_u32 s6, s36, 0x2400000
	s_addc_u32 s7, s37, 0
	ds_read_b32 v226, v212
	ds_read_b32 v227, v212 offset:512
	ds_read_b32 v228, v212 offset:1024
	ds_read_b32 v229, v212 offset:1536
	ds_read_b32 v230, v212 offset:2048
	ds_read_b32 v231, v212 offset:2560
	ds_read_b32 v232, v212 offset:3072
	ds_read_b32 v233, v212 offset:3584
	ds_read_b32 v234, v212 offset:4096
	ds_read_b32 v235, v212 offset:4608
	ds_read_b32 v236, v212 offset:5120
	ds_read_b32 v237, v212 offset:5632
	ds_read_b32 v238, v212 offset:6144
	ds_read_b32 v239, v212 offset:6656
	ds_read_b32 v240, v212 offset:7168
	ds_read_b32 v241, v212 offset:7680
	s_waitcnt lgkmcnt(0)
	v_max_f32_e32 v226, v226, v226
	v_max_f32_e32 v227, v227, v227
	v_max_f32_e32 v228, v228, v228
	v_max_f32_e32 v229, v229, v229
	v_max_f32_e32 v230, v230, v230
	v_max_f32_e32 v231, v231, v231
	v_max_f32_e32 v232, v232, v232
	v_max_f32_e32 v233, v233, v233
	v_max_f32_e32 v234, v234, v234
	v_max_f32_e32 v235, v235, v235
	v_max_f32_e32 v236, v236, v236
	v_max_f32_e32 v237, v237, v237
	v_max_f32_e32 v238, v238, v238
	v_max_f32_e32 v239, v239, v239
	v_max_f32_e32 v240, v240, v240
	v_max_f32_e32 v241, v241, v241
	v_med3_f32 v226, v226, s62, v95
	v_med3_f32 v227, v227, s62, v95
	v_med3_f32 v228, v228, s62, v95
	v_med3_f32 v229, v229, s62, v95
	v_med3_f32 v230, v230, s62, v95
	v_med3_f32 v231, v231, s62, v95
	v_med3_f32 v232, v232, s62, v95
	v_med3_f32 v233, v233, s62, v95
	v_med3_f32 v234, v234, s62, v95
	v_med3_f32 v235, v235, s62, v95
	v_med3_f32 v236, v236, s62, v95
	v_med3_f32 v237, v237, s62, v95
	v_med3_f32 v238, v238, s62, v95
	v_med3_f32 v239, v239, s62, v95
	v_med3_f32 v240, v240, s62, v95
	v_med3_f32 v241, v241, s62, v95
	v_mov_b32_e32 v242, 0
	v_mov_b32_e32 v243, 0
	v_mov_b32_e32 v244, 0
	v_mov_b32_e32 v245, 0
	v_cvt_pk_fp8_f32 v242, v226, v227
	v_cvt_pk_fp8_f32 v243, v230, v231
	v_cvt_pk_fp8_f32 v244, v234, v235
	v_cvt_pk_fp8_f32 v245, v238, v239
	v_cvt_pk_fp8_f32 v242, v228, v229 op_sel:[0,0,1]
	v_cvt_pk_fp8_f32 v243, v232, v233 op_sel:[0,0,1]
	v_cvt_pk_fp8_f32 v244, v236, v237 op_sel:[0,0,1]
	v_cvt_pk_fp8_f32 v245, v240, v241 op_sel:[0,0,1]
	s_nop 0
	global_store_dwordx4 v77, v[242:245], s[6:7]
	ds_read_b32 v226, v214
	ds_read_b32 v227, v214 offset:512
	ds_read_b32 v228, v214 offset:1024
	ds_read_b32 v229, v214 offset:1536
	ds_read_b32 v230, v214 offset:2048
	ds_read_b32 v231, v214 offset:2560
	ds_read_b32 v232, v214 offset:3072
	ds_read_b32 v233, v214 offset:3584
	ds_read_b32 v234, v214 offset:4096
	ds_read_b32 v235, v214 offset:4608
	ds_read_b32 v236, v214 offset:5120
	ds_read_b32 v237, v214 offset:5632
	ds_read_b32 v238, v214 offset:6144
	ds_read_b32 v239, v214 offset:6656
	ds_read_b32 v240, v214 offset:7168
	ds_read_b32 v241, v214 offset:7680
	s_waitcnt lgkmcnt(0)
	v_max_f32_e32 v226, v226, v226
	v_max_f32_e32 v227, v227, v227
	v_max_f32_e32 v228, v228, v228
	v_max_f32_e32 v229, v229, v229
	v_max_f32_e32 v230, v230, v230
	v_max_f32_e32 v231, v231, v231
	v_max_f32_e32 v232, v232, v232
	v_max_f32_e32 v233, v233, v233
	v_max_f32_e32 v234, v234, v234
	v_max_f32_e32 v235, v235, v235
	v_max_f32_e32 v236, v236, v236
	v_max_f32_e32 v237, v237, v237
	v_max_f32_e32 v238, v238, v238
	v_max_f32_e32 v239, v239, v239
	v_max_f32_e32 v240, v240, v240
	v_max_f32_e32 v241, v241, v241
	v_med3_f32 v226, v226, s62, v95
	v_med3_f32 v227, v227, s62, v95
	v_med3_f32 v228, v228, s62, v95
	v_med3_f32 v229, v229, s62, v95
	v_med3_f32 v230, v230, s62, v95
	v_med3_f32 v231, v231, s62, v95
	v_med3_f32 v232, v232, s62, v95
	v_med3_f32 v233, v233, s62, v95
	v_med3_f32 v234, v234, s62, v95
	v_med3_f32 v235, v235, s62, v95
	v_med3_f32 v236, v236, s62, v95
	v_med3_f32 v237, v237, s62, v95
	v_med3_f32 v238, v238, s62, v95
	v_med3_f32 v239, v239, s62, v95
	v_med3_f32 v240, v240, s62, v95
	v_med3_f32 v241, v241, s62, v95
	v_mov_b32_e32 v242, 0
	v_mov_b32_e32 v243, 0
	v_mov_b32_e32 v244, 0
	v_mov_b32_e32 v245, 0
	v_cvt_pk_fp8_f32 v242, v226, v227
	v_cvt_pk_fp8_f32 v243, v230, v231
	v_cvt_pk_fp8_f32 v244, v234, v235
	v_cvt_pk_fp8_f32 v245, v238, v239
	v_cvt_pk_fp8_f32 v242, v228, v229 op_sel:[0,0,1]
	v_cvt_pk_fp8_f32 v243, v232, v233 op_sel:[0,0,1]
	v_cvt_pk_fp8_f32 v244, v236, v237 op_sel:[0,0,1]
	v_cvt_pk_fp8_f32 v245, v240, v241 op_sel:[0,0,1]
	s_nop 0
	global_store_dwordx4 v78, v[242:245], s[6:7]
	s_waitcnt vmcnt(12)
	v_mul_f32_e32 v144, v34, v144
	v_mul_f32_e32 v145, v34, v145
	v_mul_f32_e32 v146, v34, v146
	v_mul_f32_e32 v147, v34, v147
	ds_write_b128 v209, v[144:147]
	v_mul_f32_e32 v148, v35, v148
	v_mul_f32_e32 v149, v35, v149
	v_mul_f32_e32 v150, v35, v150
	v_mul_f32_e32 v151, v35, v151
	ds_write_b128 v209, v[148:151] offset:1024
	v_mul_f32_e32 v152, v36, v152
	v_mul_f32_e32 v153, v36, v153
	v_mul_f32_e32 v154, v36, v154
	v_mul_f32_e32 v155, v36, v155
	ds_write_b128 v209, v[152:155] offset:2048
	v_mul_f32_e32 v156, v37, v156
	v_mul_f32_e32 v157, v37, v157
	v_mul_f32_e32 v158, v37, v158
	v_mul_f32_e32 v159, v37, v159
	ds_write_b128 v209, v[156:159] offset:3072
	v_mul_f32_e32 v160, v38, v160
	v_mul_f32_e32 v161, v38, v161
	v_mul_f32_e32 v162, v38, v162
	v_mul_f32_e32 v163, v38, v163
	ds_write_b128 v209, v[160:163] offset:4096
	v_mul_f32_e32 v164, v39, v164
	v_mul_f32_e32 v165, v39, v165
	v_mul_f32_e32 v166, v39, v166
	v_mul_f32_e32 v167, v39, v167
	ds_write_b128 v209, v[164:167] offset:5120
	v_mul_f32_e32 v168, v40, v168
	v_mul_f32_e32 v169, v40, v169
	v_mul_f32_e32 v170, v40, v170
	v_mul_f32_e32 v171, v40, v171
	ds_write_b128 v209, v[168:171] offset:6144
	v_mul_f32_e32 v172, v41, v172
	v_mul_f32_e32 v173, v41, v173
	v_mul_f32_e32 v174, v41, v174
	v_mul_f32_e32 v175, v41, v175
	ds_write_b128 v209, v[172:175] offset:7168
	s_waitcnt lgkmcnt(0)
	s_barrier
; #define GAS __attribute__((address_space(1)))
; #define LAS __attribute__((address_space(3)))
; #define LDS_WAIT() asm volatile("s_waitcnt lgkmcnt(0)" ::: "memory")
; __device__ __forceinline__ unsigned pk4_fp8(float a, float b, float c, float d) {
;     a = fminf(fmaxf(a, -448.f), 448.f); b = fminf(fmaxf(b, -448.f), 448.f); c = fminf(fmaxf(c, -448.f), 448.f); d = fminf(fmaxf(d, -448.f), 448.f);
;     int w = __builtin_amdgcn_cvt_pk_fp8_f32(a, b, 0, false); w = __builtin_amdgcn_cvt_pk_fp8_f32(c, d, w, true); return (unsigned)w; }
;     ...
;     for (int i = 0; i < 32; ++i) v[i] = sc >= 0 ? W[(size_t)(k0 + 2 * i + (lane >> 5)) * Nsrc + sc] : 0.f;
; #pragma unroll
;     for (int i = 0; i < 32; ++i) { const int k = k0 + 2 * i + (lane >> 5); float x = v[i] * wscale; if (KS) x *= (k < ksplit ? ksA[k] : ksB[k - ksplit]); scr[(2 * i + (lane >> 5)) * 33 + (lane & 31)] = x; }
;     LDS_WAIT(); asm volatile("" ::: "memory");
;     const int c = lane & 7;
; #pragma unroll
;     for (int j = 0; j < 4; ++j) { const int n = (lane >> 3) + 8 * j; const LAS float* s = scr + (8 * c) * 33 + n;
;         const unsigned long long o = (unsigned long long)pg8::pk4_fp8(s[0 * 33], s[1 * 33], s[2 * 33], s[3 * 33]) | ((unsigned long long)pg8::pk4_fp8(s[4 * 33], s[5 * 33], s[6 * 33], s[7 * 33]) << 32);
;         *(GAS unsigned long long*)(WT + (size_t)(n0 + n) * K + k0 + 8 * c) = o; }
	s_add_u32 s8, s34, 0xc000
	s_addc_u32 s9, s35, 0
	global_load_dwordx4 v[144:147], v74, s[8:9]
	s_add_u32 s8, s8, 0x20000
	s_addc_u32 s9, s9, 0
	global_load_dwordx4 v[148:151], v74, s[8:9]
	s_add_u32 s8, s8, 0x20000
	s_addc_u32 s9, s9, 0
	global_load_dwordx4 v[152:155], v74, s[8:9]
	s_add_u32 s8, s8, 0x20000
	s_addc_u32 s9, s9, 0
	global_load_dwordx4 v[156:159], v74, s[8:9]
	s_add_u32 s8, s8, 0x20000
	s_addc_u32 s9, s9, 0
	global_load_dwordx4 v[160:163], v74, s[8:9]
	s_add_u32 s8, s8, 0x20000
	s_addc_u32 s9, s9, 0
	global_load_dwordx4 v[164:167], v74, s[8:9]
	s_add_u32 s8, s8, 0x20000
	s_addc_u32 s9, s9, 0
	global_load_dwordx4 v[168:171], v74, s[8:9]
	s_add_u32 s8, s8, 0x20000
	s_addc_u32 s9, s9, 0
	global_load_dwordx4 v[172:175], v74, s[8:9]
	s_add_u32 s6, s36, 0x2800000
	s_addc_u32 s7, s37, 0
	ds_read_b32 v226, v211
	ds_read_b32 v227, v211 offset:512
	ds_read_b32 v228, v211 offset:1024
	ds_read_b32 v229, v211 offset:1536
	ds_read_b32 v230, v211 offset:2048
	ds_read_b32 v231, v211 offset:2560
	ds_read_b32 v232, v211 offset:3072
	ds_read_b32 v233, v211 offset:3584
	ds_read_b32 v234, v211 offset:4096
	ds_read_b32 v235, v211 offset:4608
	ds_read_b32 v236, v211 offset:5120
	ds_read_b32 v237, v211 offset:5632
	ds_read_b32 v238, v211 offset:6144
	ds_read_b32 v239, v211 offset:6656
	ds_read_b32 v240, v211 offset:7168
	ds_read_b32 v241, v211 offset:7680
	s_waitcnt lgkmcnt(0)
	v_max_f32_e32 v226, v226, v226
	v_max_f32_e32 v227, v227, v227
	v_max_f32_e32 v228, v228, v228
	v_max_f32_e32 v229, v229, v229
	v_max_f32_e32 v230, v230, v230
	v_max_f32_e32 v231, v231, v231
	v_max_f32_e32 v232, v232, v232
	v_max_f32_e32 v233, v233, v233
	v_max_f32_e32 v234, v234, v234
	v_max_f32_e32 v235, v235, v235
	v_max_f32_e32 v236, v236, v236
	v_max_f32_e32 v237, v237, v237
	v_max_f32_e32 v238, v238, v238
	v_max_f32_e32 v239, v239, v239
	v_max_f32_e32 v240, v240, v240
	v_max_f32_e32 v241, v241, v241
	v_med3_f32 v226, v226, s62, v95
	v_med3_f32 v227, v227, s62, v95
	v_med3_f32 v228, v228, s62, v95
	v_med3_f32 v229, v229, s62, v95
	v_med3_f32 v230, v230, s62, v95
	v_med3_f32 v231, v231, s62, v95
	v_med3_f32 v232, v232, s62, v95
	v_med3_f32 v233, v233, s62, v95
	v_med3_f32 v234, v234, s62, v95
	v_med3_f32 v235, v235, s62, v95
	v_med3_f32 v236, v236, s62, v95
	v_med3_f32 v237, v237, s62, v95
	v_med3_f32 v238, v238, s62, v95
	v_med3_f32 v239, v239, s62, v95
	v_med3_f32 v240, v240, s62, v95
	v_med3_f32 v241, v241, s62, v95
	v_mov_b32_e32 v242, 0
	v_mov_b32_e32 v243, 0
	v_mov_b32_e32 v244, 0
	v_mov_b32_e32 v245, 0
	v_cvt_pk_fp8_f32 v242, v226, v227
	v_cvt_pk_fp8_f32 v243, v230, v231
	v_cvt_pk_fp8_f32 v244, v234, v235
	v_cvt_pk_fp8_f32 v245, v238, v239
	v_cvt_pk_fp8_f32 v242, v228, v229 op_sel:[0,0,1]
	v_cvt_pk_fp8_f32 v243, v232, v233 op_sel:[0,0,1]
	v_cvt_pk_fp8_f32 v244, v236, v237 op_sel:[0,0,1]
	v_cvt_pk_fp8_f32 v245, v240, v241 op_sel:[0,0,1]
	s_nop 0
	global_store_dwordx4 v77, v[242:245], s[6:7]
	ds_read_b32 v226, v213
	ds_read_b32 v227, v213 offset:512
	ds_read_b32 v228, v213 offset:1024
	ds_read_b32 v229, v213 offset:1536
	ds_read_b32 v230, v213 offset:2048
	ds_read_b32 v231, v213 offset:2560
	ds_read_b32 v232, v213 offset:3072
	ds_read_b32 v233, v213 offset:3584
	ds_read_b32 v234, v213 offset:4096
	ds_read_b32 v235, v213 offset:4608
	ds_read_b32 v236, v213 offset:5120
	ds_read_b32 v237, v213 offset:5632
	ds_read_b32 v238, v213 offset:6144
	ds_read_b32 v239, v213 offset:6656
	ds_read_b32 v240, v213 offset:7168
	ds_read_b32 v241, v213 offset:7680
	s_waitcnt lgkmcnt(0)
	v_max_f32_e32 v226, v226, v226
	v_max_f32_e32 v227, v227, v227
	v_max_f32_e32 v228, v228, v228
	v_max_f32_e32 v229, v229, v229
	v_max_f32_e32 v230, v230, v230
	v_max_f32_e32 v231, v231, v231
	v_max_f32_e32 v232, v232, v232
	v_max_f32_e32 v233, v233, v233
	v_max_f32_e32 v234, v234, v234
	v_max_f32_e32 v235, v235, v235
	v_max_f32_e32 v236, v236, v236
	v_max_f32_e32 v237, v237, v237
	v_max_f32_e32 v238, v238, v238
	v_max_f32_e32 v239, v239, v239
	v_max_f32_e32 v240, v240, v240
	v_max_f32_e32 v241, v241, v241
	v_med3_f32 v226, v226, s62, v95
	v_med3_f32 v227, v227, s62, v95
	v_med3_f32 v228, v228, s62, v95
	v_med3_f32 v229, v229, s62, v95
	v_med3_f32 v230, v230, s62, v95
	v_med3_f32 v231, v231, s62, v95
	v_med3_f32 v232, v232, s62, v95
	v_med3_f32 v233, v233, s62, v95
	v_med3_f32 v234, v234, s62, v95
	v_med3_f32 v235, v235, s62, v95
	v_med3_f32 v236, v236, s62, v95
	v_med3_f32 v237, v237, s62, v95
	v_med3_f32 v238, v238, s62, v95
	v_med3_f32 v239, v239, s62, v95
	v_med3_f32 v240, v240, s62, v95
	v_med3_f32 v241, v241, s62, v95
	v_mov_b32_e32 v242, 0
	v_mov_b32_e32 v243, 0
	v_mov_b32_e32 v244, 0
	v_mov_b32_e32 v245, 0
	v_cvt_pk_fp8_f32 v242, v226, v227
	v_cvt_pk_fp8_f32 v243, v230, v231
	v_cvt_pk_fp8_f32 v244, v234, v235
	v_cvt_pk_fp8_f32 v245, v238, v239
	v_cvt_pk_fp8_f32 v242, v228, v229 op_sel:[0,0,1]
	v_cvt_pk_fp8_f32 v243, v232, v233 op_sel:[0,0,1]
	v_cvt_pk_fp8_f32 v244, v236, v237 op_sel:[0,0,1]
	v_cvt_pk_fp8_f32 v245, v240, v241 op_sel:[0,0,1]
	s_nop 0
	global_store_dwordx4 v78, v[242:245], s[6:7]
	s_waitcnt vmcnt(12)
	v_mul_f32_e32 v176, v34, v176
	v_mul_f32_e32 v177, v34, v177
	v_mul_f32_e32 v178, v34, v178
	v_mul_f32_e32 v179, v34, v179
	ds_write_b128 v210, v[176:179]
	v_mul_f32_e32 v180, v35, v180
	v_mul_f32_e32 v181, v35, v181
	v_mul_f32_e32 v182, v35, v182
	v_mul_f32_e32 v183, v35, v183
	ds_write_b128 v210, v[180:183] offset:1024
	v_mul_f32_e32 v184, v36, v184
	v_mul_f32_e32 v185, v36, v185
	v_mul_f32_e32 v186, v36, v186
	v_mul_f32_e32 v187, v36, v187
	ds_write_b128 v210, v[184:187] offset:2048
	v_mul_f32_e32 v188, v37, v188
	v_mul_f32_e32 v189, v37, v189
	v_mul_f32_e32 v190, v37, v190
	v_mul_f32_e32 v191, v37, v191
	ds_write_b128 v210, v[188:191] offset:3072
	v_mul_f32_e32 v192, v38, v192
	v_mul_f32_e32 v193, v38, v193
	v_mul_f32_e32 v194, v38, v194
	v_mul_f32_e32 v195, v38, v195
	ds_write_b128 v210, v[192:195] offset:4096
	v_mul_f32_e32 v196, v39, v196
	v_mul_f32_e32 v197, v39, v197
	v_mul_f32_e32 v198, v39, v198
	v_mul_f32_e32 v199, v39, v199
	ds_write_b128 v210, v[196:199] offset:5120
	v_mul_f32_e32 v200, v40, v200
	v_mul_f32_e32 v201, v40, v201
	v_mul_f32_e32 v202, v40, v202
	v_mul_f32_e32 v203, v40, v203
	ds_write_b128 v210, v[200:203] offset:6144
	v_mul_f32_e32 v204, v41, v204
	v_mul_f32_e32 v205, v41, v205
	v_mul_f32_e32 v206, v41, v206
	v_mul_f32_e32 v207, v41, v207
	ds_write_b128 v210, v[204:207] offset:7168
	s_waitcnt lgkmcnt(0)
	s_barrier
; #define GAS __attribute__((address_space(1)))
; #define LAS __attribute__((address_space(3)))
; #define LDS_WAIT() asm volatile("s_waitcnt lgkmcnt(0)" ::: "memory")
; __device__ __forceinline__ unsigned pk4_fp8(float a, float b, float c, float d) {
;     a = fminf(fmaxf(a, -448.f), 448.f); b = fminf(fmaxf(b, -448.f), 448.f); c = fminf(fmaxf(c, -448.f), 448.f); d = fminf(fmaxf(d, -448.f), 448.f);
;     int w = __builtin_amdgcn_cvt_pk_fp8_f32(a, b, 0, false); w = __builtin_amdgcn_cvt_pk_fp8_f32(c, d, w, true); return (unsigned)w; }
;     ...
;     for (int i = 0; i < 32; ++i) v[i] = sc >= 0 ? W[(size_t)(k0 + 2 * i + (lane >> 5)) * Nsrc + sc] : 0.f;
; #pragma unroll
;     for (int i = 0; i < 32; ++i) { const int k = k0 + 2 * i + (lane >> 5); float x = v[i] * wscale; if (KS) x *= (k < ksplit ? ksA[k] : ksB[k - ksplit]); scr[(2 * i + (lane >> 5)) * 33 + (lane & 31)] = x; }
;     LDS_WAIT(); asm volatile("" ::: "memory");
;     const int c = lane & 7;
; #pragma unroll
;     for (int j = 0; j < 4; ++j) { const int n = (lane >> 3) + 8 * j; const LAS float* s = scr + (8 * c) * 33 + n;
;         const unsigned long long o = (unsigned long long)pg8::pk4_fp8(s[0 * 33], s[1 * 33], s[2 * 33], s[3 * 33]) | ((unsigned long long)pg8::pk4_fp8(s[4 * 33], s[5 * 33], s[6 * 33], s[7 * 33]) << 32);
;         *(GAS unsigned long long*)(WT + (size_t)(n0 + n) * K + k0 + 8 * c) = o; }
	s_add_u32 s8, s34, 0xd000
	s_addc_u32 s9, s35, 0
	global_load_dwordx4 v[176:179], v74, s[8:9]
	s_add_u32 s8, s8, 0x20000
	s_addc_u32 s9, s9, 0
	global_load_dwordx4 v[180:183], v74, s[8:9]
	s_add_u32 s8, s8, 0x20000
	s_addc_u32 s9, s9, 0
	global_load_dwordx4 v[184:187], v74, s[8:9]
	s_add_u32 s8, s8, 0x20000
	s_addc_u32 s9, s9, 0
	global_load_dwordx4 v[188:191], v74, s[8:9]
	s_add_u32 s8, s8, 0x20000
	s_addc_u32 s9, s9, 0
	global_load_dwordx4 v[192:195], v74, s[8:9]
	s_add_u32 s8, s8, 0x20000
	s_addc_u32 s9, s9, 0
	global_load_dwordx4 v[196:199], v74, s[8:9]
	s_add_u32 s8, s8, 0x20000
	s_addc_u32 s9, s9, 0
	global_load_dwordx4 v[200:203], v74, s[8:9]
	s_add_u32 s8, s8, 0x20000
	s_addc_u32 s9, s9, 0
	global_load_dwordx4 v[204:207], v74, s[8:9]
	s_add_u32 s6, s36, 0x2c00000
	s_addc_u32 s7, s37, 0
	ds_read_b32 v226, v212
	ds_read_b32 v227, v212 offset:512
	ds_read_b32 v228, v212 offset:1024
	ds_read_b32 v229, v212 offset:1536
	ds_read_b32 v230, v212 offset:2048
	ds_read_b32 v231, v212 offset:2560
	ds_read_b32 v232, v212 offset:3072
	ds_read_b32 v233, v212 offset:3584
	ds_read_b32 v234, v212 offset:4096
	ds_read_b32 v235, v212 offset:4608
	ds_read_b32 v236, v212 offset:5120
	ds_read_b32 v237, v212 offset:5632
	ds_read_b32 v238, v212 offset:6144
	ds_read_b32 v239, v212 offset:6656
	ds_read_b32 v240, v212 offset:7168
	ds_read_b32 v241, v212 offset:7680
	s_waitcnt lgkmcnt(0)
	v_max_f32_e32 v226, v226, v226
	v_max_f32_e32 v227, v227, v227
	v_max_f32_e32 v228, v228, v228
	v_max_f32_e32 v229, v229, v229
	v_max_f32_e32 v230, v230, v230
	v_max_f32_e32 v231, v231, v231
	v_max_f32_e32 v232, v232, v232
	v_max_f32_e32 v233, v233, v233
	v_max_f32_e32 v234, v234, v234
	v_max_f32_e32 v235, v235, v235
	v_max_f32_e32 v236, v236, v236
	v_max_f32_e32 v237, v237, v237
	v_max_f32_e32 v238, v238, v238
	v_max_f32_e32 v239, v239, v239
	v_max_f32_e32 v240, v240, v240
	v_max_f32_e32 v241, v241, v241
	v_med3_f32 v226, v226, s62, v95
	v_med3_f32 v227, v227, s62, v95
	v_med3_f32 v228, v228, s62, v95
	v_med3_f32 v229, v229, s62, v95
	v_med3_f32 v230, v230, s62, v95
	v_med3_f32 v231, v231, s62, v95
	v_med3_f32 v232, v232, s62, v95
	v_med3_f32 v233, v233, s62, v95
	v_med3_f32 v234, v234, s62, v95
	v_med3_f32 v235, v235, s62, v95
	v_med3_f32 v236, v236, s62, v95
	v_med3_f32 v237, v237, s62, v95
	v_med3_f32 v238, v238, s62, v95
	v_med3_f32 v239, v239, s62, v95
	v_med3_f32 v240, v240, s62, v95
	v_med3_f32 v241, v241, s62, v95
	v_mov_b32_e32 v242, 0
	v_mov_b32_e32 v243, 0
	v_mov_b32_e32 v244, 0
	v_mov_b32_e32 v245, 0
	v_cvt_pk_fp8_f32 v242, v226, v227
	v_cvt_pk_fp8_f32 v243, v230, v231
	v_cvt_pk_fp8_f32 v244, v234, v235
	v_cvt_pk_fp8_f32 v245, v238, v239
	v_cvt_pk_fp8_f32 v242, v228, v229 op_sel:[0,0,1]
	v_cvt_pk_fp8_f32 v243, v232, v233 op_sel:[0,0,1]
	v_cvt_pk_fp8_f32 v244, v236, v237 op_sel:[0,0,1]
	v_cvt_pk_fp8_f32 v245, v240, v241 op_sel:[0,0,1]
	s_nop 0
	global_store_dwordx4 v77, v[242:245], s[6:7]
	ds_read_b32 v226, v214
	ds_read_b32 v227, v214 offset:512
	ds_read_b32 v228, v214 offset:1024
	ds_read_b32 v229, v214 offset:1536
	ds_read_b32 v230, v214 offset:2048
	ds_read_b32 v231, v214 offset:2560
	ds_read_b32 v232, v214 offset:3072
	ds_read_b32 v233, v214 offset:3584
	ds_read_b32 v234, v214 offset:4096
	ds_read_b32 v235, v214 offset:4608
	ds_read_b32 v236, v214 offset:5120
	ds_read_b32 v237, v214 offset:5632
	ds_read_b32 v238, v214 offset:6144
	ds_read_b32 v239, v214 offset:6656
	ds_read_b32 v240, v214 offset:7168
	ds_read_b32 v241, v214 offset:7680
	s_waitcnt lgkmcnt(0)
	v_max_f32_e32 v226, v226, v226
	v_max_f32_e32 v227, v227, v227
	v_max_f32_e32 v228, v228, v228
	v_max_f32_e32 v229, v229, v229
	v_max_f32_e32 v230, v230, v230
	v_max_f32_e32 v231, v231, v231
	v_max_f32_e32 v232, v232, v232
	v_max_f32_e32 v233, v233, v233
	v_max_f32_e32 v234, v234, v234
	v_max_f32_e32 v235, v235, v235
	v_max_f32_e32 v236, v236, v236
	v_max_f32_e32 v237, v237, v237
	v_max_f32_e32 v238, v238, v238
	v_max_f32_e32 v239, v239, v239
	v_max_f32_e32 v240, v240, v240
	v_max_f32_e32 v241, v241, v241
	v_med3_f32 v226, v226, s62, v95
	v_med3_f32 v227, v227, s62, v95
	v_med3_f32 v228, v228, s62, v95
	v_med3_f32 v229, v229, s62, v95
	v_med3_f32 v230, v230, s62, v95
	v_med3_f32 v231, v231, s62, v95
	v_med3_f32 v232, v232, s62, v95
	v_med3_f32 v233, v233, s62, v95
	v_med3_f32 v234, v234, s62, v95
	v_med3_f32 v235, v235, s62, v95
	v_med3_f32 v236, v236, s62, v95
	v_med3_f32 v237, v237, s62, v95
	v_med3_f32 v238, v238, s62, v95
	v_med3_f32 v239, v239, s62, v95
	v_med3_f32 v240, v240, s62, v95
	v_med3_f32 v241, v241, s62, v95
	v_mov_b32_e32 v242, 0
	v_mov_b32_e32 v243, 0
	v_mov_b32_e32 v244, 0
	v_mov_b32_e32 v245, 0
	v_cvt_pk_fp8_f32 v242, v226, v227
	v_cvt_pk_fp8_f32 v243, v230, v231
	v_cvt_pk_fp8_f32 v244, v234, v235
	v_cvt_pk_fp8_f32 v245, v238, v239
	v_cvt_pk_fp8_f32 v242, v228, v229 op_sel:[0,0,1]
	v_cvt_pk_fp8_f32 v243, v232, v233 op_sel:[0,0,1]
	v_cvt_pk_fp8_f32 v244, v236, v237 op_sel:[0,0,1]
	v_cvt_pk_fp8_f32 v245, v240, v241 op_sel:[0,0,1]
	s_nop 0
	global_store_dwordx4 v78, v[242:245], s[6:7]
	s_waitcnt vmcnt(12)
	v_mul_f32_e32 v144, v34, v144
	v_mul_f32_e32 v145, v34, v145
	v_mul_f32_e32 v146, v34, v146
	v_mul_f32_e32 v147, v34, v147
	ds_write_b128 v209, v[144:147]
	v_mul_f32_e32 v148, v35, v148
	v_mul_f32_e32 v149, v35, v149
	v_mul_f32_e32 v150, v35, v150
	v_mul_f32_e32 v151, v35, v151
	ds_write_b128 v209, v[148:151] offset:1024
	v_mul_f32_e32 v152, v36, v152
	v_mul_f32_e32 v153, v36, v153
	v_mul_f32_e32 v154, v36, v154
	v_mul_f32_e32 v155, v36, v155
	ds_write_b128 v209, v[152:155] offset:2048
	v_mul_f32_e32 v156, v37, v156
	v_mul_f32_e32 v157, v37, v157
	v_mul_f32_e32 v158, v37, v158
	v_mul_f32_e32 v159, v37, v159
	ds_write_b128 v209, v[156:159] offset:3072
	v_mul_f32_e32 v160, v38, v160
	v_mul_f32_e32 v161, v38, v161
	v_mul_f32_e32 v162, v38, v162
	v_mul_f32_e32 v163, v38, v163
	ds_write_b128 v209, v[160:163] offset:4096
	v_mul_f32_e32 v164, v39, v164
	v_mul_f32_e32 v165, v39, v165
	v_mul_f32_e32 v166, v39, v166
	v_mul_f32_e32 v167, v39, v167
	ds_write_b128 v209, v[164:167] offset:5120
	v_mul_f32_e32 v168, v40, v168
	v_mul_f32_e32 v169, v40, v169
	v_mul_f32_e32 v170, v40, v170
	v_mul_f32_e32 v171, v40, v171
	ds_write_b128 v209, v[168:171] offset:6144
	v_mul_f32_e32 v172, v41, v172
	v_mul_f32_e32 v173, v41, v173
	v_mul_f32_e32 v174, v41, v174
	v_mul_f32_e32 v175, v41, v175
	ds_write_b128 v209, v[172:175] offset:7168
	s_waitcnt lgkmcnt(0)
	s_barrier
; #define GAS __attribute__((address_space(1)))
; #define LAS __attribute__((address_space(3)))
; #define LDS_WAIT() asm volatile("s_waitcnt lgkmcnt(0)" ::: "memory")
; __device__ __forceinline__ unsigned pk4_fp8(float a, float b, float c, float d) {
;     a = fminf(fmaxf(a, -448.f), 448.f); b = fminf(fmaxf(b, -448.f), 448.f); c = fminf(fmaxf(c, -448.f), 448.f); d = fminf(fmaxf(d, -448.f), 448.f);
;     int w = __builtin_amdgcn_cvt_pk_fp8_f32(a, b, 0, false); w = __builtin_amdgcn_cvt_pk_fp8_f32(c, d, w, true); return (unsigned)w; }
;     ...
;     for (int i = 0; i < 32; ++i) v[i] = sc >= 0 ? W[(size_t)(k0 + 2 * i + (lane >> 5)) * Nsrc + sc] : 0.f;
; #pragma unroll
;     for (int i = 0; i < 32; ++i) { const int k = k0 + 2 * i + (lane >> 5); float x = v[i] * wscale; if (KS) x *= (k < ksplit ? ksA[k] : ksB[k - ksplit]); scr[(2 * i + (lane >> 5)) * 33 + (lane & 31)] = x; }
;     LDS_WAIT(); asm volatile("" ::: "memory");
;     const int c = lane & 7;
; #pragma unroll
;     for (int j = 0; j < 4; ++j) { const int n = (lane >> 3) + 8 * j; const LAS float* s = scr + (8 * c) * 33 + n;
;         const unsigned long long o = (unsigned long long)pg8::pk4_fp8(s[0 * 33], s[1 * 33], s[2 * 33], s[3 * 33]) | ((unsigned long long)pg8::pk4_fp8(s[4 * 33], s[5 * 33], s[6 * 33], s[7 * 33]) << 32);
;         *(GAS unsigned long long*)(WT + (size_t)(n0 + n) * K + k0 + 8 * c) = o; }
	s_add_u32 s8, s34, 0xe000
	s_addc_u32 s9, s35, 0
	global_load_dwordx4 v[144:147], v74, s[8:9]
	s_add_u32 s8, s8, 0x20000
	s_addc_u32 s9, s9, 0
	global_load_dwordx4 v[148:151], v74, s[8:9]
	s_add_u32 s8, s8, 0x20000
	s_addc_u32 s9, s9, 0
	global_load_dwordx4 v[152:155], v74, s[8:9]
	s_add_u32 s8, s8, 0x20000
	s_addc_u32 s9, s9, 0
	global_load_dwordx4 v[156:159], v74, s[8:9]
	s_add_u32 s8, s8, 0x20000
	s_addc_u32 s9, s9, 0
	global_load_dwordx4 v[160:163], v74, s[8:9]
	s_add_u32 s8, s8, 0x20000
	s_addc_u32 s9, s9, 0
	global_load_dwordx4 v[164:167], v74, s[8:9]
	s_add_u32 s8, s8, 0x20000
	s_addc_u32 s9, s9, 0
	global_load_dwordx4 v[168:171], v74, s[8:9]
	s_add_u32 s8, s8, 0x20000
	s_addc_u32 s9, s9, 0
	global_load_dwordx4 v[172:175], v74, s[8:9]
	s_add_u32 s6, s36, 0x3000000
	s_addc_u32 s7, s37, 0
	ds_read_b32 v226, v211
	ds_read_b32 v227, v211 offset:512
	ds_read_b32 v228, v211 offset:1024
	ds_read_b32 v229, v211 offset:1536
	ds_read_b32 v230, v211 offset:2048
	ds_read_b32 v231, v211 offset:2560
	ds_read_b32 v232, v211 offset:3072
	ds_read_b32 v233, v211 offset:3584
	ds_read_b32 v234, v211 offset:4096
	ds_read_b32 v235, v211 offset:4608
	ds_read_b32 v236, v211 offset:5120
	ds_read_b32 v237, v211 offset:5632
	ds_read_b32 v238, v211 offset:6144
	ds_read_b32 v239, v211 offset:6656
	ds_read_b32 v240, v211 offset:7168
	ds_read_b32 v241, v211 offset:7680
	s_waitcnt lgkmcnt(0)
	v_max_f32_e32 v226, v226, v226
	v_max_f32_e32 v227, v227, v227
	v_max_f32_e32 v228, v228, v228
	v_max_f32_e32 v229, v229, v229
	v_max_f32_e32 v230, v230, v230
	v_max_f32_e32 v231, v231, v231
	v_max_f32_e32 v232, v232, v232
	v_max_f32_e32 v233, v233, v233
	v_max_f32_e32 v234, v234, v234
	v_max_f32_e32 v235, v235, v235
	v_max_f32_e32 v236, v236, v236
	v_max_f32_e32 v237, v237, v237
	v_max_f32_e32 v238, v238, v238
	v_max_f32_e32 v239, v239, v239
	v_max_f32_e32 v240, v240, v240
	v_max_f32_e32 v241, v241, v241
	v_med3_f32 v226, v226, s62, v95
	v_med3_f32 v227, v227, s62, v95
	v_med3_f32 v228, v228, s62, v95
	v_med3_f32 v229, v229, s62, v95
	v_med3_f32 v230, v230, s62, v95
	v_med3_f32 v231, v231, s62, v95
	v_med3_f32 v232, v232, s62, v95
	v_med3_f32 v233, v233, s62, v95
	v_med3_f32 v234, v234, s62, v95
	v_med3_f32 v235, v235, s62, v95
	v_med3_f32 v236, v236, s62, v95
	v_med3_f32 v237, v237, s62, v95
	v_med3_f32 v238, v238, s62, v95
	v_med3_f32 v239, v239, s62, v95
	v_med3_f32 v240, v240, s62, v95
	v_med3_f32 v241, v241, s62, v95
	v_mov_b32_e32 v242, 0
	v_mov_b32_e32 v243, 0
	v_mov_b32_e32 v244, 0
	v_mov_b32_e32 v245, 0
	v_cvt_pk_fp8_f32 v242, v226, v227
	v_cvt_pk_fp8_f32 v243, v230, v231
	v_cvt_pk_fp8_f32 v244, v234, v235
	v_cvt_pk_fp8_f32 v245, v238, v239
	v_cvt_pk_fp8_f32 v242, v228, v229 op_sel:[0,0,1]
	v_cvt_pk_fp8_f32 v243, v232, v233 op_sel:[0,0,1]
	v_cvt_pk_fp8_f32 v244, v236, v237 op_sel:[0,0,1]
	v_cvt_pk_fp8_f32 v245, v240, v241 op_sel:[0,0,1]
	s_nop 0
	global_store_dwordx4 v77, v[242:245], s[6:7]
	ds_read_b32 v226, v213
	ds_read_b32 v227, v213 offset:512
	ds_read_b32 v228, v213 offset:1024
	ds_read_b32 v229, v213 offset:1536
	ds_read_b32 v230, v213 offset:2048
	ds_read_b32 v231, v213 offset:2560
	ds_read_b32 v232, v213 offset:3072
	ds_read_b32 v233, v213 offset:3584
	ds_read_b32 v234, v213 offset:4096
	ds_read_b32 v235, v213 offset:4608
	ds_read_b32 v236, v213 offset:5120
	ds_read_b32 v237, v213 offset:5632
	ds_read_b32 v238, v213 offset:6144
	ds_read_b32 v239, v213 offset:6656
	ds_read_b32 v240, v213 offset:7168
	ds_read_b32 v241, v213 offset:7680
	s_waitcnt lgkmcnt(0)
	v_max_f32_e32 v226, v226, v226
	v_max_f32_e32 v227, v227, v227
	v_max_f32_e32 v228, v228, v228
	v_max_f32_e32 v229, v229, v229
	v_max_f32_e32 v230, v230, v230
	v_max_f32_e32 v231, v231, v231
	v_max_f32_e32 v232, v232, v232
	v_max_f32_e32 v233, v233, v233
	v_max_f32_e32 v234, v234, v234
	v_max_f32_e32 v235, v235, v235
	v_max_f32_e32 v236, v236, v236
	v_max_f32_e32 v237, v237, v237
	v_max_f32_e32 v238, v238, v238
	v_max_f32_e32 v239, v239, v239
	v_max_f32_e32 v240, v240, v240
	v_max_f32_e32 v241, v241, v241
	v_med3_f32 v226, v226, s62, v95
	v_med3_f32 v227, v227, s62, v95
	v_med3_f32 v228, v228, s62, v95
	v_med3_f32 v229, v229, s62, v95
	v_med3_f32 v230, v230, s62, v95
	v_med3_f32 v231, v231, s62, v95
	v_med3_f32 v232, v232, s62, v95
	v_med3_f32 v233, v233, s62, v95
	v_med3_f32 v234, v234, s62, v95
	v_med3_f32 v235, v235, s62, v95
	v_med3_f32 v236, v236, s62, v95
	v_med3_f32 v237, v237, s62, v95
	v_med3_f32 v238, v238, s62, v95
	v_med3_f32 v239, v239, s62, v95
	v_med3_f32 v240, v240, s62, v95
	v_med3_f32 v241, v241, s62, v95
	v_mov_b32_e32 v242, 0
	v_mov_b32_e32 v243, 0
	v_mov_b32_e32 v244, 0
	v_mov_b32_e32 v245, 0
	v_cvt_pk_fp8_f32 v242, v226, v227
	v_cvt_pk_fp8_f32 v243, v230, v231
	v_cvt_pk_fp8_f32 v244, v234, v235
	v_cvt_pk_fp8_f32 v245, v238, v239
	v_cvt_pk_fp8_f32 v242, v228, v229 op_sel:[0,0,1]
	v_cvt_pk_fp8_f32 v243, v232, v233 op_sel:[0,0,1]
	v_cvt_pk_fp8_f32 v244, v236, v237 op_sel:[0,0,1]
	v_cvt_pk_fp8_f32 v245, v240, v241 op_sel:[0,0,1]
	s_nop 0
	global_store_dwordx4 v78, v[242:245], s[6:7]
	s_waitcnt vmcnt(12)
	v_mul_f32_e32 v176, v34, v176
	v_mul_f32_e32 v177, v34, v177
	v_mul_f32_e32 v178, v34, v178
	v_mul_f32_e32 v179, v34, v179
	ds_write_b128 v210, v[176:179]
	v_mul_f32_e32 v180, v35, v180
	v_mul_f32_e32 v181, v35, v181
	v_mul_f32_e32 v182, v35, v182
	v_mul_f32_e32 v183, v35, v183
	ds_write_b128 v210, v[180:183] offset:1024
	v_mul_f32_e32 v184, v36, v184
	v_mul_f32_e32 v185, v36, v185
	v_mul_f32_e32 v186, v36, v186
	v_mul_f32_e32 v187, v36, v187
	ds_write_b128 v210, v[184:187] offset:2048
	v_mul_f32_e32 v188, v37, v188
	v_mul_f32_e32 v189, v37, v189
	v_mul_f32_e32 v190, v37, v190
	v_mul_f32_e32 v191, v37, v191
	ds_write_b128 v210, v[188:191] offset:3072
	v_mul_f32_e32 v192, v38, v192
	v_mul_f32_e32 v193, v38, v193
	v_mul_f32_e32 v194, v38, v194
	v_mul_f32_e32 v195, v38, v195
	ds_write_b128 v210, v[192:195] offset:4096
	v_mul_f32_e32 v196, v39, v196
	v_mul_f32_e32 v197, v39, v197
	v_mul_f32_e32 v198, v39, v198
	v_mul_f32_e32 v199, v39, v199
	ds_write_b128 v210, v[196:199] offset:5120
	v_mul_f32_e32 v200, v40, v200
	v_mul_f32_e32 v201, v40, v201
	v_mul_f32_e32 v202, v40, v202
	v_mul_f32_e32 v203, v40, v203
	ds_write_b128 v210, v[200:203] offset:6144
	v_mul_f32_e32 v204, v41, v204
	v_mul_f32_e32 v205, v41, v205
	v_mul_f32_e32 v206, v41, v206
	v_mul_f32_e32 v207, v41, v207
	ds_write_b128 v210, v[204:207] offset:7168
	s_waitcnt lgkmcnt(0)
	s_barrier
; #define GAS __attribute__((address_space(1)))
; #define LAS __attribute__((address_space(3)))
; #define LDS_WAIT() asm volatile("s_waitcnt lgkmcnt(0)" ::: "memory")
; __device__ __forceinline__ unsigned pk4_fp8(float a, float b, float c, float d) {
;     a = fminf(fmaxf(a, -448.f), 448.f); b = fminf(fmaxf(b, -448.f), 448.f); c = fminf(fmaxf(c, -448.f), 448.f); d = fminf(fmaxf(d, -448.f), 448.f);
;     int w = __builtin_amdgcn_cvt_pk_fp8_f32(a, b, 0, false); w = __builtin_amdgcn_cvt_pk_fp8_f32(c, d, w, true); return (unsigned)w; }
;     ...
;     for (int i = 0; i < 32; ++i) v[i] = sc >= 0 ? W[(size_t)(k0 + 2 * i + (lane >> 5)) * Nsrc + sc] : 0.f;
; #pragma unroll
;     for (int i = 0; i < 32; ++i) { const int k = k0 + 2 * i + (lane >> 5); float x = v[i] * wscale; if (KS) x *= (k < ksplit ? ksA[k] : ksB[k - ksplit]); scr[(2 * i + (lane >> 5)) * 33 + (lane & 31)] = x; }
;     LDS_WAIT(); asm volatile("" ::: "memory");
;     const int c = lane & 7;
; #pragma unroll
;     for (int j = 0; j < 4; ++j) { const int n = (lane >> 3) + 8 * j; const LAS float* s = scr + (8 * c) * 33 + n;
;         const unsigned long long o = (unsigned long long)pg8::pk4_fp8(s[0 * 33], s[1 * 33], s[2 * 33], s[3 * 33]) | ((unsigned long long)pg8::pk4_fp8(s[4 * 33], s[5 * 33], s[6 * 33], s[7 * 33]) << 32);
;         *(GAS unsigned long long*)(WT + (size_t)(n0 + n) * K + k0 + 8 * c) = o; }
	s_add_u32 s8, s34, 0xf000
	s_addc_u32 s9, s35, 0
	global_load_dwordx4 v[176:179], v74, s[8:9]
	s_add_u32 s8, s8, 0x20000
	s_addc_u32 s9, s9, 0
	global_load_dwordx4 v[180:183], v74, s[8:9]
	s_add_u32 s8, s8, 0x20000
	s_addc_u32 s9, s9, 0
	global_load_dwordx4 v[184:187], v74, s[8:9]
	s_add_u32 s8, s8, 0x20000
	s_addc_u32 s9, s9, 0
	global_load_dwordx4 v[188:191], v74, s[8:9]
	s_add_u32 s8, s8, 0x20000
	s_addc_u32 s9, s9, 0
	global_load_dwordx4 v[192:195], v74, s[8:9]
	s_add_u32 s8, s8, 0x20000
	s_addc_u32 s9, s9, 0
	global_load_dwordx4 v[196:199], v74, s[8:9]
	s_add_u32 s8, s8, 0x20000
	s_addc_u32 s9, s9, 0
	global_load_dwordx4 v[200:203], v74, s[8:9]
	s_add_u32 s8, s8, 0x20000
	s_addc_u32 s9, s9, 0
	global_load_dwordx4 v[204:207], v74, s[8:9]
	s_add_u32 s6, s36, 0x3400000
	s_addc_u32 s7, s37, 0
	ds_read_b32 v226, v212
	ds_read_b32 v227, v212 offset:512
	ds_read_b32 v228, v212 offset:1024
	ds_read_b32 v229, v212 offset:1536
	ds_read_b32 v230, v212 offset:2048
	ds_read_b32 v231, v212 offset:2560
	ds_read_b32 v232, v212 offset:3072
	ds_read_b32 v233, v212 offset:3584
	ds_read_b32 v234, v212 offset:4096
	ds_read_b32 v235, v212 offset:4608
	ds_read_b32 v236, v212 offset:5120
	ds_read_b32 v237, v212 offset:5632
	ds_read_b32 v238, v212 offset:6144
	ds_read_b32 v239, v212 offset:6656
	ds_read_b32 v240, v212 offset:7168
	ds_read_b32 v241, v212 offset:7680
	s_waitcnt lgkmcnt(0)
	v_max_f32_e32 v226, v226, v226
	v_max_f32_e32 v227, v227, v227
	v_max_f32_e32 v228, v228, v228
	v_max_f32_e32 v229, v229, v229
	v_max_f32_e32 v230, v230, v230
	v_max_f32_e32 v231, v231, v231
	v_max_f32_e32 v232, v232, v232
	v_max_f32_e32 v233, v233, v233
	v_max_f32_e32 v234, v234, v234
	v_max_f32_e32 v235, v235, v235
	v_max_f32_e32 v236, v236, v236
	v_max_f32_e32 v237, v237, v237
	v_max_f32_e32 v238, v238, v238
	v_max_f32_e32 v239, v239, v239
	v_max_f32_e32 v240, v240, v240
	v_max_f32_e32 v241, v241, v241
	v_med3_f32 v226, v226, s62, v95
	v_med3_f32 v227, v227, s62, v95
	v_med3_f32 v228, v228, s62, v95
	v_med3_f32 v229, v229, s62, v95
	v_med3_f32 v230, v230, s62, v95
	v_med3_f32 v231, v231, s62, v95
	v_med3_f32 v232, v232, s62, v95
	v_med3_f32 v233, v233, s62, v95
	v_med3_f32 v234, v234, s62, v95
	v_med3_f32 v235, v235, s62, v95
	v_med3_f32 v236, v236, s62, v95
	v_med3_f32 v237, v237, s62, v95
	v_med3_f32 v238, v238, s62, v95
	v_med3_f32 v239, v239, s62, v95
	v_med3_f32 v240, v240, s62, v95
	v_med3_f32 v241, v241, s62, v95
	v_mov_b32_e32 v242, 0
	v_mov_b32_e32 v243, 0
	v_mov_b32_e32 v244, 0
	v_mov_b32_e32 v245, 0
	v_cvt_pk_fp8_f32 v242, v226, v227
	v_cvt_pk_fp8_f32 v243, v230, v231
	v_cvt_pk_fp8_f32 v244, v234, v235
	v_cvt_pk_fp8_f32 v245, v238, v239
	v_cvt_pk_fp8_f32 v242, v228, v229 op_sel:[0,0,1]
	v_cvt_pk_fp8_f32 v243, v232, v233 op_sel:[0,0,1]
	v_cvt_pk_fp8_f32 v244, v236, v237 op_sel:[0,0,1]
	v_cvt_pk_fp8_f32 v245, v240, v241 op_sel:[0,0,1]
	s_nop 0
	global_store_dwordx4 v77, v[242:245], s[6:7]
	ds_read_b32 v226, v214
	ds_read_b32 v227, v214 offset:512
	ds_read_b32 v228, v214 offset:1024
	ds_read_b32 v229, v214 offset:1536
	ds_read_b32 v230, v214 offset:2048
	ds_read_b32 v231, v214 offset:2560
	ds_read_b32 v232, v214 offset:3072
	ds_read_b32 v233, v214 offset:3584
	ds_read_b32 v234, v214 offset:4096
	ds_read_b32 v235, v214 offset:4608
	ds_read_b32 v236, v214 offset:5120
	ds_read_b32 v237, v214 offset:5632
	ds_read_b32 v238, v214 offset:6144
	ds_read_b32 v239, v214 offset:6656
	ds_read_b32 v240, v214 offset:7168
	ds_read_b32 v241, v214 offset:7680
	s_waitcnt lgkmcnt(0)
	v_max_f32_e32 v226, v226, v226
	v_max_f32_e32 v227, v227, v227
	v_max_f32_e32 v228, v228, v228
	v_max_f32_e32 v229, v229, v229
	v_max_f32_e32 v230, v230, v230
	v_max_f32_e32 v231, v231, v231
	v_max_f32_e32 v232, v232, v232
	v_max_f32_e32 v233, v233, v233
	v_max_f32_e32 v234, v234, v234
	v_max_f32_e32 v235, v235, v235
	v_max_f32_e32 v236, v236, v236
	v_max_f32_e32 v237, v237, v237
	v_max_f32_e32 v238, v238, v238
	v_max_f32_e32 v239, v239, v239
	v_max_f32_e32 v240, v240, v240
	v_max_f32_e32 v241, v241, v241
	v_med3_f32 v226, v226, s62, v95
	v_med3_f32 v227, v227, s62, v95
	v_med3_f32 v228, v228, s62, v95
	v_med3_f32 v229, v229, s62, v95
	v_med3_f32 v230, v230, s62, v95
	v_med3_f32 v231, v231, s62, v95
	v_med3_f32 v232, v232, s62, v95
	v_med3_f32 v233, v233, s62, v95
	v_med3_f32 v234, v234, s62, v95
	v_med3_f32 v235, v235, s62, v95
	v_med3_f32 v236, v236, s62, v95
	v_med3_f32 v237, v237, s62, v95
	v_med3_f32 v238, v238, s62, v95
	v_med3_f32 v239, v239, s62, v95
	v_med3_f32 v240, v240, s62, v95
	v_med3_f32 v241, v241, s62, v95
	v_mov_b32_e32 v242, 0
	v_mov_b32_e32 v243, 0
	v_mov_b32_e32 v244, 0
	v_mov_b32_e32 v245, 0
	v_cvt_pk_fp8_f32 v242, v226, v227
	v_cvt_pk_fp8_f32 v243, v230, v231
	v_cvt_pk_fp8_f32 v244, v234, v235
	v_cvt_pk_fp8_f32 v245, v238, v239
	v_cvt_pk_fp8_f32 v242, v228, v229 op_sel:[0,0,1]
	v_cvt_pk_fp8_f32 v243, v232, v233 op_sel:[0,0,1]
	v_cvt_pk_fp8_f32 v244, v236, v237 op_sel:[0,0,1]
	v_cvt_pk_fp8_f32 v245, v240, v241 op_sel:[0,0,1]
	s_nop 0
	global_store_dwordx4 v78, v[242:245], s[6:7]
	s_waitcnt vmcnt(12)
	v_mul_f32_e32 v144, v34, v144
	v_mul_f32_e32 v145, v34, v145
	v_mul_f32_e32 v146, v34, v146
	v_mul_f32_e32 v147, v34, v147
	ds_write_b128 v209, v[144:147]
	v_mul_f32_e32 v148, v35, v148
	v_mul_f32_e32 v149, v35, v149
	v_mul_f32_e32 v150, v35, v150
	v_mul_f32_e32 v151, v35, v151
	ds_write_b128 v209, v[148:151] offset:1024
	v_mul_f32_e32 v152, v36, v152
	v_mul_f32_e32 v153, v36, v153
	v_mul_f32_e32 v154, v36, v154
	v_mul_f32_e32 v155, v36, v155
	ds_write_b128 v209, v[152:155] offset:2048
	v_mul_f32_e32 v156, v37, v156
	v_mul_f32_e32 v157, v37, v157
	v_mul_f32_e32 v158, v37, v158
	v_mul_f32_e32 v159, v37, v159
	ds_write_b128 v209, v[156:159] offset:3072
	v_mul_f32_e32 v160, v38, v160
	v_mul_f32_e32 v161, v38, v161
	v_mul_f32_e32 v162, v38, v162
	v_mul_f32_e32 v163, v38, v163
	ds_write_b128 v209, v[160:163] offset:4096
	v_mul_f32_e32 v164, v39, v164
	v_mul_f32_e32 v165, v39, v165
	v_mul_f32_e32 v166, v39, v166
	v_mul_f32_e32 v167, v39, v167
	ds_write_b128 v209, v[164:167] offset:5120
	v_mul_f32_e32 v168, v40, v168
	v_mul_f32_e32 v169, v40, v169
	v_mul_f32_e32 v170, v40, v170
	v_mul_f32_e32 v171, v40, v171
	ds_write_b128 v209, v[168:171] offset:6144
	v_mul_f32_e32 v172, v41, v172
	v_mul_f32_e32 v173, v41, v173
	v_mul_f32_e32 v174, v41, v174
	v_mul_f32_e32 v175, v41, v175
	ds_write_b128 v209, v[172:175] offset:7168
	s_waitcnt lgkmcnt(0)
	s_barrier
; #define GAS __attribute__((address_space(1)))
; #define LAS __attribute__((address_space(3)))
; #define LDS_WAIT() asm volatile("s_waitcnt lgkmcnt(0)" ::: "memory")
; __device__ __forceinline__ unsigned pk4_fp8(float a, float b, float c, float d) {
;     a = fminf(fmaxf(a, -448.f), 448.f); b = fminf(fmaxf(b, -448.f), 448.f); c = fminf(fmaxf(c, -448.f), 448.f); d = fminf(fmaxf(d, -448.f), 448.f);
;     int w = __builtin_amdgcn_cvt_pk_fp8_f32(a, b, 0, false); w = __builtin_amdgcn_cvt_pk_fp8_f32(c, d, w, true); return (unsigned)w; }
;     ...
;     for (int i = 0; i < 32; ++i) v[i] = sc >= 0 ? W[(size_t)(k0 + 2 * i + (lane >> 5)) * Nsrc + sc] : 0.f;
; #pragma unroll
;     for (int i = 0; i < 32; ++i) { const int k = k0 + 2 * i + (lane >> 5); float x = v[i] * wscale; if (KS) x *= (k < ksplit ? ksA[k] : ksB[k - ksplit]); scr[(2 * i + (lane >> 5)) * 33 + (lane & 31)] = x; }
;     LDS_WAIT(); asm volatile("" ::: "memory");
;     const int c = lane & 7;
; #pragma unroll
;     for (int j = 0; j < 4; ++j) { const int n = (lane >> 3) + 8 * j; const LAS float* s = scr + (8 * c) * 33 + n;
;         const unsigned long long o = (unsigned long long)pg8::pk4_fp8(s[0 * 33], s[1 * 33], s[2 * 33], s[3 * 33]) | ((unsigned long long)pg8::pk4_fp8(s[4 * 33], s[5 * 33], s[6 * 33], s[7 * 33]) << 32);
;         *(GAS unsigned long long*)(WT + (size_t)(n0 + n) * K + k0 + 8 * c) = o; }
	s_mov_b64 s[8:9], s[38:39]
	global_load_dwordx4 v[144:147], v75, s[8:9]
	s_add_u32 s8, s8, 0x8000
	s_addc_u32 s9, s9, 0
	global_load_dwordx4 v[148:151], v75, s[8:9]
	s_add_u32 s8, s8, 0x8000
	s_addc_u32 s9, s9, 0
	global_load_dwordx4 v[152:155], v75, s[8:9]
	s_add_u32 s8, s8, 0x8000
	s_addc_u32 s9, s9, 0
	global_load_dwordx4 v[156:159], v75, s[8:9]
	s_add_u32 s8, s8, 0x8000
	s_addc_u32 s9, s9, 0
	global_load_dwordx4 v[160:163], v75, s[8:9]
	s_add_u32 s8, s8, 0x8000
	s_addc_u32 s9, s9, 0
	global_load_dwordx4 v[164:167], v75, s[8:9]
	s_add_u32 s8, s8, 0x8000
	s_addc_u32 s9, s9, 0
	global_load_dwordx4 v[168:171], v75, s[8:9]
	s_add_u32 s8, s8, 0x8000
	s_addc_u32 s9, s9, 0
	global_load_dwordx4 v[172:175], v75, s[8:9]
	s_add_u32 s6, s36, 0x3800000
	s_addc_u32 s7, s37, 0
	ds_read_b32 v226, v211
	ds_read_b32 v227, v211 offset:512
	ds_read_b32 v228, v211 offset:1024
	ds_read_b32 v229, v211 offset:1536
	ds_read_b32 v230, v211 offset:2048
	ds_read_b32 v231, v211 offset:2560
	ds_read_b32 v232, v211 offset:3072
	ds_read_b32 v233, v211 offset:3584
	ds_read_b32 v234, v211 offset:4096
	ds_read_b32 v235, v211 offset:4608
	ds_read_b32 v236, v211 offset:5120
	ds_read_b32 v237, v211 offset:5632
	ds_read_b32 v238, v211 offset:6144
	ds_read_b32 v239, v211 offset:6656
	ds_read_b32 v240, v211 offset:7168
	ds_read_b32 v241, v211 offset:7680
	s_waitcnt lgkmcnt(0)
	v_max_f32_e32 v226, v226, v226
	v_max_f32_e32 v227, v227, v227
	v_max_f32_e32 v228, v228, v228
	v_max_f32_e32 v229, v229, v229
	v_max_f32_e32 v230, v230, v230
	v_max_f32_e32 v231, v231, v231
	v_max_f32_e32 v232, v232, v232
	v_max_f32_e32 v233, v233, v233
	v_max_f32_e32 v234, v234, v234
	v_max_f32_e32 v235, v235, v235
	v_max_f32_e32 v236, v236, v236
	v_max_f32_e32 v237, v237, v237
	v_max_f32_e32 v238, v238, v238
	v_max_f32_e32 v239, v239, v239
	v_max_f32_e32 v240, v240, v240
	v_max_f32_e32 v241, v241, v241
	v_med3_f32 v226, v226, s62, v95
	v_med3_f32 v227, v227, s62, v95
	v_med3_f32 v228, v228, s62, v95
	v_med3_f32 v229, v229, s62, v95
	v_med3_f32 v230, v230, s62, v95
	v_med3_f32 v231, v231, s62, v95
	v_med3_f32 v232, v232, s62, v95
	v_med3_f32 v233, v233, s62, v95
	v_med3_f32 v234, v234, s62, v95
	v_med3_f32 v235, v235, s62, v95
	v_med3_f32 v236, v236, s62, v95
	v_med3_f32 v237, v237, s62, v95
	v_med3_f32 v238, v238, s62, v95
	v_med3_f32 v239, v239, s62, v95
	v_med3_f32 v240, v240, s62, v95
	v_med3_f32 v241, v241, s62, v95
	v_mov_b32_e32 v242, 0
	v_mov_b32_e32 v243, 0
	v_mov_b32_e32 v244, 0
	v_mov_b32_e32 v245, 0
	v_cvt_pk_fp8_f32 v242, v226, v227
	v_cvt_pk_fp8_f32 v243, v230, v231
	v_cvt_pk_fp8_f32 v244, v234, v235
	v_cvt_pk_fp8_f32 v245, v238, v239
	v_cvt_pk_fp8_f32 v242, v228, v229 op_sel:[0,0,1]
	v_cvt_pk_fp8_f32 v243, v232, v233 op_sel:[0,0,1]
	v_cvt_pk_fp8_f32 v244, v236, v237 op_sel:[0,0,1]
	v_cvt_pk_fp8_f32 v245, v240, v241 op_sel:[0,0,1]
	s_nop 0
	global_store_dwordx4 v77, v[242:245], s[6:7]
	ds_read_b32 v226, v213
	ds_read_b32 v227, v213 offset:512
	ds_read_b32 v228, v213 offset:1024
	ds_read_b32 v229, v213 offset:1536
	ds_read_b32 v230, v213 offset:2048
	ds_read_b32 v231, v213 offset:2560
	ds_read_b32 v232, v213 offset:3072
	ds_read_b32 v233, v213 offset:3584
	ds_read_b32 v234, v213 offset:4096
	ds_read_b32 v235, v213 offset:4608
	ds_read_b32 v236, v213 offset:5120
	ds_read_b32 v237, v213 offset:5632
	ds_read_b32 v238, v213 offset:6144
	ds_read_b32 v239, v213 offset:6656
	ds_read_b32 v240, v213 offset:7168
	ds_read_b32 v241, v213 offset:7680
	s_waitcnt lgkmcnt(0)
	v_max_f32_e32 v226, v226, v226
	v_max_f32_e32 v227, v227, v227
	v_max_f32_e32 v228, v228, v228
	v_max_f32_e32 v229, v229, v229
	v_max_f32_e32 v230, v230, v230
	v_max_f32_e32 v231, v231, v231
	v_max_f32_e32 v232, v232, v232
	v_max_f32_e32 v233, v233, v233
	v_max_f32_e32 v234, v234, v234
	v_max_f32_e32 v235, v235, v235
	v_max_f32_e32 v236, v236, v236
	v_max_f32_e32 v237, v237, v237
	v_max_f32_e32 v238, v238, v238
	v_max_f32_e32 v239, v239, v239
	v_max_f32_e32 v240, v240, v240
	v_max_f32_e32 v241, v241, v241
	v_med3_f32 v226, v226, s62, v95
	v_med3_f32 v227, v227, s62, v95
	v_med3_f32 v228, v228, s62, v95
	v_med3_f32 v229, v229, s62, v95
	v_med3_f32 v230, v230, s62, v95
	v_med3_f32 v231, v231, s62, v95
	v_med3_f32 v232, v232, s62, v95
	v_med3_f32 v233, v233, s62, v95
	v_med3_f32 v234, v234, s62, v95
	v_med3_f32 v235, v235, s62, v95
	v_med3_f32 v236, v236, s62, v95
	v_med3_f32 v237, v237, s62, v95
	v_med3_f32 v238, v238, s62, v95
	v_med3_f32 v239, v239, s62, v95
	v_med3_f32 v240, v240, s62, v95
	v_med3_f32 v241, v241, s62, v95
	v_mov_b32_e32 v242, 0
	v_mov_b32_e32 v243, 0
	v_mov_b32_e32 v244, 0
	v_mov_b32_e32 v245, 0
	v_cvt_pk_fp8_f32 v242, v226, v227
	v_cvt_pk_fp8_f32 v243, v230, v231
	v_cvt_pk_fp8_f32 v244, v234, v235
	v_cvt_pk_fp8_f32 v245, v238, v239
	v_cvt_pk_fp8_f32 v242, v228, v229 op_sel:[0,0,1]
	v_cvt_pk_fp8_f32 v243, v232, v233 op_sel:[0,0,1]
	v_cvt_pk_fp8_f32 v244, v236, v237 op_sel:[0,0,1]
	v_cvt_pk_fp8_f32 v245, v240, v241 op_sel:[0,0,1]
	s_nop 0
	global_store_dwordx4 v78, v[242:245], s[6:7]
	s_waitcnt vmcnt(12)
	v_mul_f32_e32 v176, v34, v176
	v_mul_f32_e32 v177, v34, v177
	v_mul_f32_e32 v178, v34, v178
	v_mul_f32_e32 v179, v34, v179
	ds_write_b128 v210, v[176:179]
	v_mul_f32_e32 v180, v35, v180
	v_mul_f32_e32 v181, v35, v181
	v_mul_f32_e32 v182, v35, v182
	v_mul_f32_e32 v183, v35, v183
	ds_write_b128 v210, v[180:183] offset:1024
	v_mul_f32_e32 v184, v36, v184
	v_mul_f32_e32 v185, v36, v185
	v_mul_f32_e32 v186, v36, v186
	v_mul_f32_e32 v187, v36, v187
	ds_write_b128 v210, v[184:187] offset:2048
	v_mul_f32_e32 v188, v37, v188
	v_mul_f32_e32 v189, v37, v189
	v_mul_f32_e32 v190, v37, v190
	v_mul_f32_e32 v191, v37, v191
	ds_write_b128 v210, v[188:191] offset:3072
	v_mul_f32_e32 v192, v38, v192
	v_mul_f32_e32 v193, v38, v193
	v_mul_f32_e32 v194, v38, v194
	v_mul_f32_e32 v195, v38, v195
	ds_write_b128 v210, v[192:195] offset:4096
	v_mul_f32_e32 v196, v39, v196
	v_mul_f32_e32 v197, v39, v197
	v_mul_f32_e32 v198, v39, v198
	v_mul_f32_e32 v199, v39, v199
	ds_write_b128 v210, v[196:199] offset:5120
	v_mul_f32_e32 v200, v40, v200
	v_mul_f32_e32 v201, v40, v201
	v_mul_f32_e32 v202, v40, v202
	v_mul_f32_e32 v203, v40, v203
	ds_write_b128 v210, v[200:203] offset:6144
	v_mul_f32_e32 v204, v41, v204
	v_mul_f32_e32 v205, v41, v205
	v_mul_f32_e32 v206, v41, v206
	v_mul_f32_e32 v207, v41, v207
	ds_write_b128 v210, v[204:207] offset:7168
	s_waitcnt lgkmcnt(0)
	s_barrier
; #define GAS __attribute__((address_space(1)))
; #define LAS __attribute__((address_space(3)))
; #define LDS_WAIT() asm volatile("s_waitcnt lgkmcnt(0)" ::: "memory")
; __device__ __forceinline__ unsigned pk4_fp8(float a, float b, float c, float d) {
;     a = fminf(fmaxf(a, -448.f), 448.f); b = fminf(fmaxf(b, -448.f), 448.f); c = fminf(fmaxf(c, -448.f), 448.f); d = fminf(fmaxf(d, -448.f), 448.f);
;     int w = __builtin_amdgcn_cvt_pk_fp8_f32(a, b, 0, false); w = __builtin_amdgcn_cvt_pk_fp8_f32(c, d, w, true); return (unsigned)w; }
;     ...
;     for (int i = 0; i < 32; ++i) v[i] = sc >= 0 ? W[(size_t)(k0 + 2 * i + (lane >> 5)) * Nsrc + sc] : 0.f;
; #pragma unroll
;     for (int i = 0; i < 32; ++i) { const int k = k0 + 2 * i + (lane >> 5); float x = v[i] * wscale; if (KS) x *= (k < ksplit ? ksA[k] : ksB[k - ksplit]); scr[(2 * i + (lane >> 5)) * 33 + (lane & 31)] = x; }
;     LDS_WAIT(); asm volatile("" ::: "memory");
;     const int c = lane & 7;
; #pragma unroll
;     for (int j = 0; j < 4; ++j) { const int n = (lane >> 3) + 8 * j; const LAS float* s = scr + (8 * c) * 33 + n;
;         const unsigned long long o = (unsigned long long)pg8::pk4_fp8(s[0 * 33], s[1 * 33], s[2 * 33], s[3 * 33]) | ((unsigned long long)pg8::pk4_fp8(s[4 * 33], s[5 * 33], s[6 * 33], s[7 * 33]) << 32);
;         *(GAS unsigned long long*)(WT + (size_t)(n0 + n) * K + k0 + 8 * c) = o; }
	s_add_u32 s8, s38, 0x1000
	s_addc_u32 s9, s39, 0
	global_load_dwordx4 v[176:179], v75, s[8:9]
	s_add_u32 s8, s8, 0x8000
	s_addc_u32 s9, s9, 0
	global_load_dwordx4 v[180:183], v75, s[8:9]
	s_add_u32 s8, s8, 0x8000
	s_addc_u32 s9, s9, 0
	global_load_dwordx4 v[184:187], v75, s[8:9]
	s_add_u32 s8, s8, 0x8000
	s_addc_u32 s9, s9, 0
	global_load_dwordx4 v[188:191], v75, s[8:9]
	s_add_u32 s8, s8, 0x8000
	s_addc_u32 s9, s9, 0
	global_load_dwordx4 v[192:195], v75, s[8:9]
	s_add_u32 s8, s8, 0x8000
	s_addc_u32 s9, s9, 0
	global_load_dwordx4 v[196:199], v75, s[8:9]
	s_add_u32 s8, s8, 0x8000
	s_addc_u32 s9, s9, 0
	global_load_dwordx4 v[200:203], v75, s[8:9]
	s_add_u32 s8, s8, 0x8000
	s_addc_u32 s9, s9, 0
	global_load_dwordx4 v[204:207], v75, s[8:9]
	s_add_u32 s6, s36, 0x3c00000
	s_addc_u32 s7, s37, 0
	ds_read_b32 v226, v212
	ds_read_b32 v227, v212 offset:512
	ds_read_b32 v228, v212 offset:1024
	ds_read_b32 v229, v212 offset:1536
	ds_read_b32 v230, v212 offset:2048
	ds_read_b32 v231, v212 offset:2560
	ds_read_b32 v232, v212 offset:3072
	ds_read_b32 v233, v212 offset:3584
	ds_read_b32 v234, v212 offset:4096
	ds_read_b32 v235, v212 offset:4608
	ds_read_b32 v236, v212 offset:5120
	ds_read_b32 v237, v212 offset:5632
	ds_read_b32 v238, v212 offset:6144
	ds_read_b32 v239, v212 offset:6656
	ds_read_b32 v240, v212 offset:7168
	ds_read_b32 v241, v212 offset:7680
	s_waitcnt lgkmcnt(0)
	v_max_f32_e32 v226, v226, v226
	v_max_f32_e32 v227, v227, v227
	v_max_f32_e32 v228, v228, v228
	v_max_f32_e32 v229, v229, v229
	v_max_f32_e32 v230, v230, v230
	v_max_f32_e32 v231, v231, v231
	v_max_f32_e32 v232, v232, v232
	v_max_f32_e32 v233, v233, v233
	v_max_f32_e32 v234, v234, v234
	v_max_f32_e32 v235, v235, v235
	v_max_f32_e32 v236, v236, v236
	v_max_f32_e32 v237, v237, v237
	v_max_f32_e32 v238, v238, v238
	v_max_f32_e32 v239, v239, v239
	v_max_f32_e32 v240, v240, v240
	v_max_f32_e32 v241, v241, v241
	v_med3_f32 v226, v226, s62, v95
	v_med3_f32 v227, v227, s62, v95
	v_med3_f32 v228, v228, s62, v95
	v_med3_f32 v229, v229, s62, v95
	v_med3_f32 v230, v230, s62, v95
	v_med3_f32 v231, v231, s62, v95
	v_med3_f32 v232, v232, s62, v95
	v_med3_f32 v233, v233, s62, v95
	v_med3_f32 v234, v234, s62, v95
	v_med3_f32 v235, v235, s62, v95
	v_med3_f32 v236, v236, s62, v95
	v_med3_f32 v237, v237, s62, v95
	v_med3_f32 v238, v238, s62, v95
	v_med3_f32 v239, v239, s62, v95
	v_med3_f32 v240, v240, s62, v95
	v_med3_f32 v241, v241, s62, v95
	v_mov_b32_e32 v242, 0
	v_mov_b32_e32 v243, 0
	v_mov_b32_e32 v244, 0
	v_mov_b32_e32 v245, 0
	v_cvt_pk_fp8_f32 v242, v226, v227
	v_cvt_pk_fp8_f32 v243, v230, v231
	v_cvt_pk_fp8_f32 v244, v234, v235
	v_cvt_pk_fp8_f32 v245, v238, v239
	v_cvt_pk_fp8_f32 v242, v228, v229 op_sel:[0,0,1]
	v_cvt_pk_fp8_f32 v243, v232, v233 op_sel:[0,0,1]
	v_cvt_pk_fp8_f32 v244, v236, v237 op_sel:[0,0,1]
	v_cvt_pk_fp8_f32 v245, v240, v241 op_sel:[0,0,1]
	s_nop 0
	global_store_dwordx4 v77, v[242:245], s[6:7]
	ds_read_b32 v226, v214
	ds_read_b32 v227, v214 offset:512
	ds_read_b32 v228, v214 offset:1024
	ds_read_b32 v229, v214 offset:1536
	ds_read_b32 v230, v214 offset:2048
	ds_read_b32 v231, v214 offset:2560
	ds_read_b32 v232, v214 offset:3072
	ds_read_b32 v233, v214 offset:3584
	ds_read_b32 v234, v214 offset:4096
	ds_read_b32 v235, v214 offset:4608
	ds_read_b32 v236, v214 offset:5120
	ds_read_b32 v237, v214 offset:5632
	ds_read_b32 v238, v214 offset:6144
	ds_read_b32 v239, v214 offset:6656
	ds_read_b32 v240, v214 offset:7168
	ds_read_b32 v241, v214 offset:7680
	s_waitcnt lgkmcnt(0)
	v_max_f32_e32 v226, v226, v226
	v_max_f32_e32 v227, v227, v227
	v_max_f32_e32 v228, v228, v228
	v_max_f32_e32 v229, v229, v229
	v_max_f32_e32 v230, v230, v230
	v_max_f32_e32 v231, v231, v231
	v_max_f32_e32 v232, v232, v232
	v_max_f32_e32 v233, v233, v233
	v_max_f32_e32 v234, v234, v234
	v_max_f32_e32 v235, v235, v235
	v_max_f32_e32 v236, v236, v236
	v_max_f32_e32 v237, v237, v237
	v_max_f32_e32 v238, v238, v238
	v_max_f32_e32 v239, v239, v239
	v_max_f32_e32 v240, v240, v240
	v_max_f32_e32 v241, v241, v241
	v_med3_f32 v226, v226, s62, v95
	v_med3_f32 v227, v227, s62, v95
	v_med3_f32 v228, v228, s62, v95
	v_med3_f32 v229, v229, s62, v95
	v_med3_f32 v230, v230, s62, v95
	v_med3_f32 v231, v231, s62, v95
	v_med3_f32 v232, v232, s62, v95
	v_med3_f32 v233, v233, s62, v95
	v_med3_f32 v234, v234, s62, v95
	v_med3_f32 v235, v235, s62, v95
	v_med3_f32 v236, v236, s62, v95
	v_med3_f32 v237, v237, s62, v95
	v_med3_f32 v238, v238, s62, v95
	v_med3_f32 v239, v239, s62, v95
	v_med3_f32 v240, v240, s62, v95
	v_med3_f32 v241, v241, s62, v95
	v_mov_b32_e32 v242, 0
	v_mov_b32_e32 v243, 0
	v_mov_b32_e32 v244, 0
	v_mov_b32_e32 v245, 0
	v_cvt_pk_fp8_f32 v242, v226, v227
	v_cvt_pk_fp8_f32 v243, v230, v231
	v_cvt_pk_fp8_f32 v244, v234, v235
	v_cvt_pk_fp8_f32 v245, v238, v239
	v_cvt_pk_fp8_f32 v242, v228, v229 op_sel:[0,0,1]
	v_cvt_pk_fp8_f32 v243, v232, v233 op_sel:[0,0,1]
	v_cvt_pk_fp8_f32 v244, v236, v237 op_sel:[0,0,1]
	v_cvt_pk_fp8_f32 v245, v240, v241 op_sel:[0,0,1]
	s_nop 0
	global_store_dwordx4 v78, v[242:245], s[6:7]
	s_waitcnt vmcnt(12)
	v_mul_f32_e32 v144, 0x43000000, v144
	v_mul_f32_e32 v145, 0x43000000, v145
	v_mul_f32_e32 v146, 0x43000000, v146
	v_mul_f32_e32 v147, 0x43000000, v147
	ds_write_b128 v209, v[144:147]
	v_mul_f32_e32 v148, 0x43000000, v148
	v_mul_f32_e32 v149, 0x43000000, v149
	v_mul_f32_e32 v150, 0x43000000, v150
	v_mul_f32_e32 v151, 0x43000000, v151
	ds_write_b128 v209, v[148:151] offset:1024
	v_mul_f32_e32 v152, 0x43000000, v152
	v_mul_f32_e32 v153, 0x43000000, v153
	v_mul_f32_e32 v154, 0x43000000, v154
	v_mul_f32_e32 v155, 0x43000000, v155
	ds_write_b128 v209, v[152:155] offset:2048
	v_mul_f32_e32 v156, 0x43000000, v156
	v_mul_f32_e32 v157, 0x43000000, v157
	v_mul_f32_e32 v158, 0x43000000, v158
	v_mul_f32_e32 v159, 0x43000000, v159
	ds_write_b128 v209, v[156:159] offset:3072
	v_mul_f32_e32 v160, 0x43000000, v160
	v_mul_f32_e32 v161, 0x43000000, v161
	v_mul_f32_e32 v162, 0x43000000, v162
	v_mul_f32_e32 v163, 0x43000000, v163
	ds_write_b128 v209, v[160:163] offset:4096
	v_mul_f32_e32 v164, 0x43000000, v164
	v_mul_f32_e32 v165, 0x43000000, v165
	v_mul_f32_e32 v166, 0x43000000, v166
	v_mul_f32_e32 v167, 0x43000000, v167
	ds_write_b128 v209, v[164:167] offset:5120
	v_mul_f32_e32 v168, 0x43000000, v168
	v_mul_f32_e32 v169, 0x43000000, v169
	v_mul_f32_e32 v170, 0x43000000, v170
	v_mul_f32_e32 v171, 0x43000000, v171
	ds_write_b128 v209, v[168:171] offset:6144
	v_mul_f32_e32 v172, 0x43000000, v172
	v_mul_f32_e32 v173, 0x43000000, v173
	v_mul_f32_e32 v174, 0x43000000, v174
	v_mul_f32_e32 v175, 0x43000000, v175
	ds_write_b128 v209, v[172:175] offset:7168
	s_waitcnt lgkmcnt(0)
	s_barrier
; #define GAS __attribute__((address_space(1)))
; #define LAS __attribute__((address_space(3)))
; #define LDS_WAIT() asm volatile("s_waitcnt lgkmcnt(0)" ::: "memory")
; __device__ __forceinline__ unsigned pk4_fp8(float a, float b, float c, float d) {
;     a = fminf(fmaxf(a, -448.f), 448.f); b = fminf(fmaxf(b, -448.f), 448.f); c = fminf(fmaxf(c, -448.f), 448.f); d = fminf(fmaxf(d, -448.f), 448.f);
;     int w = __builtin_amdgcn_cvt_pk_fp8_f32(a, b, 0, false); w = __builtin_amdgcn_cvt_pk_fp8_f32(c, d, w, true); return (unsigned)w; }
;     ...
;     for (int i = 0; i < 32; ++i) v[i] = sc >= 0 ? W[(size_t)(k0 + 2 * i + (lane >> 5)) * Nsrc + sc] : 0.f;
; #pragma unroll
;     for (int i = 0; i < 32; ++i) { const int k = k0 + 2 * i + (lane >> 5); float x = v[i] * wscale; if (KS) x *= (k < ksplit ? ksA[k] : ksB[k - ksplit]); scr[(2 * i + (lane >> 5)) * 33 + (lane & 31)] = x; }
;     LDS_WAIT(); asm volatile("" ::: "memory");
;     const int c = lane & 7;
; #pragma unroll
;     for (int j = 0; j < 4; ++j) { const int n = (lane >> 3) + 8 * j; const LAS float* s = scr + (8 * c) * 33 + n;
;         const unsigned long long o = (unsigned long long)pg8::pk4_fp8(s[0 * 33], s[1 * 33], s[2 * 33], s[3 * 33]) | ((unsigned long long)pg8::pk4_fp8(s[4 * 33], s[5 * 33], s[6 * 33], s[7 * 33]) << 32);
;         *(GAS unsigned long long*)(WT + (size_t)(n0 + n) * K + k0 + 8 * c) = o; }
	s_add_u32 s8, s38, 0x2000
	s_addc_u32 s9, s39, 0
	global_load_dwordx4 v[144:147], v75, s[8:9]
	s_add_u32 s8, s8, 0x8000
	s_addc_u32 s9, s9, 0
	global_load_dwordx4 v[148:151], v75, s[8:9]
	s_add_u32 s8, s8, 0x8000
	s_addc_u32 s9, s9, 0
	global_load_dwordx4 v[152:155], v75, s[8:9]
	s_add_u32 s8, s8, 0x8000
	s_addc_u32 s9, s9, 0
	global_load_dwordx4 v[156:159], v75, s[8:9]
	s_add_u32 s8, s8, 0x8000
	s_addc_u32 s9, s9, 0
	global_load_dwordx4 v[160:163], v75, s[8:9]
	s_add_u32 s8, s8, 0x8000
	s_addc_u32 s9, s9, 0
	global_load_dwordx4 v[164:167], v75, s[8:9]
	s_add_u32 s8, s8, 0x8000
	s_addc_u32 s9, s9, 0
	global_load_dwordx4 v[168:171], v75, s[8:9]
	s_add_u32 s8, s8, 0x8000
	s_addc_u32 s9, s9, 0
	global_load_dwordx4 v[172:175], v75, s[8:9]
	s_mov_b64 s[6:7], s[40:41]
	ds_read_b32 v226, v211
	ds_read_b32 v227, v211 offset:512
	ds_read_b32 v228, v211 offset:1024
	ds_read_b32 v229, v211 offset:1536
	ds_read_b32 v230, v211 offset:2048
	ds_read_b32 v231, v211 offset:2560
	ds_read_b32 v232, v211 offset:3072
	ds_read_b32 v233, v211 offset:3584
	ds_read_b32 v234, v211 offset:4096
	ds_read_b32 v235, v211 offset:4608
	ds_read_b32 v236, v211 offset:5120
	ds_read_b32 v237, v211 offset:5632
	ds_read_b32 v238, v211 offset:6144
	ds_read_b32 v239, v211 offset:6656
	ds_read_b32 v240, v211 offset:7168
	ds_read_b32 v241, v211 offset:7680
	s_waitcnt lgkmcnt(0)
	v_max_f32_e32 v226, v226, v226
	v_max_f32_e32 v227, v227, v227
	v_max_f32_e32 v228, v228, v228
	v_max_f32_e32 v229, v229, v229
	v_max_f32_e32 v230, v230, v230
	v_max_f32_e32 v231, v231, v231
	v_max_f32_e32 v232, v232, v232
	v_max_f32_e32 v233, v233, v233
	v_max_f32_e32 v234, v234, v234
	v_max_f32_e32 v235, v235, v235
	v_max_f32_e32 v236, v236, v236
	v_max_f32_e32 v237, v237, v237
	v_max_f32_e32 v238, v238, v238
	v_max_f32_e32 v239, v239, v239
	v_max_f32_e32 v240, v240, v240
	v_max_f32_e32 v241, v241, v241
	v_med3_f32 v226, v226, s62, v95
	v_med3_f32 v227, v227, s62, v95
	v_med3_f32 v228, v228, s62, v95
	v_med3_f32 v229, v229, s62, v95
	v_med3_f32 v230, v230, s62, v95
	v_med3_f32 v231, v231, s62, v95
	v_med3_f32 v232, v232, s62, v95
	v_med3_f32 v233, v233, s62, v95
	v_med3_f32 v234, v234, s62, v95
	v_med3_f32 v235, v235, s62, v95
	v_med3_f32 v236, v236, s62, v95
	v_med3_f32 v237, v237, s62, v95
	v_med3_f32 v238, v238, s62, v95
	v_med3_f32 v239, v239, s62, v95
	v_med3_f32 v240, v240, s62, v95
	v_med3_f32 v241, v241, s62, v95
	v_mov_b32_e32 v242, 0
	v_mov_b32_e32 v243, 0
	v_mov_b32_e32 v244, 0
	v_mov_b32_e32 v245, 0
	v_cvt_pk_fp8_f32 v242, v226, v227
	v_cvt_pk_fp8_f32 v243, v230, v231
	v_cvt_pk_fp8_f32 v244, v234, v235
	v_cvt_pk_fp8_f32 v245, v238, v239
	v_cvt_pk_fp8_f32 v242, v228, v229 op_sel:[0,0,1]
	v_cvt_pk_fp8_f32 v243, v232, v233 op_sel:[0,0,1]
	v_cvt_pk_fp8_f32 v244, v236, v237 op_sel:[0,0,1]
	v_cvt_pk_fp8_f32 v245, v240, v241 op_sel:[0,0,1]
	s_nop 0
	global_store_dwordx4 v79, v[242:245], s[6:7]
	ds_read_b32 v226, v213
	ds_read_b32 v227, v213 offset:512
	ds_read_b32 v228, v213 offset:1024
	ds_read_b32 v229, v213 offset:1536
	ds_read_b32 v230, v213 offset:2048
	ds_read_b32 v231, v213 offset:2560
	ds_read_b32 v232, v213 offset:3072
	ds_read_b32 v233, v213 offset:3584
	ds_read_b32 v234, v213 offset:4096
	ds_read_b32 v235, v213 offset:4608
	ds_read_b32 v236, v213 offset:5120
	ds_read_b32 v237, v213 offset:5632
	ds_read_b32 v238, v213 offset:6144
	ds_read_b32 v239, v213 offset:6656
	ds_read_b32 v240, v213 offset:7168
	ds_read_b32 v241, v213 offset:7680
	s_waitcnt lgkmcnt(0)
	v_max_f32_e32 v226, v226, v226
	v_max_f32_e32 v227, v227, v227
	v_max_f32_e32 v228, v228, v228
	v_max_f32_e32 v229, v229, v229
	v_max_f32_e32 v230, v230, v230
	v_max_f32_e32 v231, v231, v231
	v_max_f32_e32 v232, v232, v232
	v_max_f32_e32 v233, v233, v233
	v_max_f32_e32 v234, v234, v234
	v_max_f32_e32 v235, v235, v235
	v_max_f32_e32 v236, v236, v236
	v_max_f32_e32 v237, v237, v237
	v_max_f32_e32 v238, v238, v238
	v_max_f32_e32 v239, v239, v239
	v_max_f32_e32 v240, v240, v240
	v_max_f32_e32 v241, v241, v241
	v_med3_f32 v226, v226, s62, v95
	v_med3_f32 v227, v227, s62, v95
	v_med3_f32 v228, v228, s62, v95
	v_med3_f32 v229, v229, s62, v95
	v_med3_f32 v230, v230, s62, v95
	v_med3_f32 v231, v231, s62, v95
	v_med3_f32 v232, v232, s62, v95
	v_med3_f32 v233, v233, s62, v95
	v_med3_f32 v234, v234, s62, v95
	v_med3_f32 v235, v235, s62, v95
	v_med3_f32 v236, v236, s62, v95
	v_med3_f32 v237, v237, s62, v95
	v_med3_f32 v238, v238, s62, v95
	v_med3_f32 v239, v239, s62, v95
	v_med3_f32 v240, v240, s62, v95
	v_med3_f32 v241, v241, s62, v95
	v_mov_b32_e32 v242, 0
	v_mov_b32_e32 v243, 0
	v_mov_b32_e32 v244, 0
	v_mov_b32_e32 v245, 0
	v_cvt_pk_fp8_f32 v242, v226, v227
	v_cvt_pk_fp8_f32 v243, v230, v231
	v_cvt_pk_fp8_f32 v244, v234, v235
	v_cvt_pk_fp8_f32 v245, v238, v239
	v_cvt_pk_fp8_f32 v242, v228, v229 op_sel:[0,0,1]
	v_cvt_pk_fp8_f32 v243, v232, v233 op_sel:[0,0,1]
	v_cvt_pk_fp8_f32 v244, v236, v237 op_sel:[0,0,1]
	v_cvt_pk_fp8_f32 v245, v240, v241 op_sel:[0,0,1]
	s_nop 0
	global_store_dwordx4 v80, v[242:245], s[6:7]
	s_waitcnt vmcnt(12)
	v_mul_f32_e32 v176, 0x43000000, v176
	v_mul_f32_e32 v177, 0x43000000, v177
	v_mul_f32_e32 v178, 0x43000000, v178
	v_mul_f32_e32 v179, 0x43000000, v179
	ds_write_b128 v210, v[176:179]
	v_mul_f32_e32 v180, 0x43000000, v180
	v_mul_f32_e32 v181, 0x43000000, v181
	v_mul_f32_e32 v182, 0x43000000, v182
	v_mul_f32_e32 v183, 0x43000000, v183
	ds_write_b128 v210, v[180:183] offset:1024
	v_mul_f32_e32 v184, 0x43000000, v184
	v_mul_f32_e32 v185, 0x43000000, v185
	v_mul_f32_e32 v186, 0x43000000, v186
	v_mul_f32_e32 v187, 0x43000000, v187
	ds_write_b128 v210, v[184:187] offset:2048
	v_mul_f32_e32 v188, 0x43000000, v188
	v_mul_f32_e32 v189, 0x43000000, v189
	v_mul_f32_e32 v190, 0x43000000, v190
	v_mul_f32_e32 v191, 0x43000000, v191
	ds_write_b128 v210, v[188:191] offset:3072
	v_mul_f32_e32 v192, 0x43000000, v192
	v_mul_f32_e32 v193, 0x43000000, v193
	v_mul_f32_e32 v194, 0x43000000, v194
	v_mul_f32_e32 v195, 0x43000000, v195
	ds_write_b128 v210, v[192:195] offset:4096
	v_mul_f32_e32 v196, 0x43000000, v196
	v_mul_f32_e32 v197, 0x43000000, v197
	v_mul_f32_e32 v198, 0x43000000, v198
	v_mul_f32_e32 v199, 0x43000000, v199
	ds_write_b128 v210, v[196:199] offset:5120
	v_mul_f32_e32 v200, 0x43000000, v200
	v_mul_f32_e32 v201, 0x43000000, v201
	v_mul_f32_e32 v202, 0x43000000, v202
	v_mul_f32_e32 v203, 0x43000000, v203
	ds_write_b128 v210, v[200:203] offset:6144
	v_mul_f32_e32 v204, 0x43000000, v204
	v_mul_f32_e32 v205, 0x43000000, v205
	v_mul_f32_e32 v206, 0x43000000, v206
	v_mul_f32_e32 v207, 0x43000000, v207
	ds_write_b128 v210, v[204:207] offset:7168
	s_waitcnt lgkmcnt(0)
	s_barrier
; #define GAS __attribute__((address_space(1)))
; #define LAS __attribute__((address_space(3)))
; #define LDS_WAIT() asm volatile("s_waitcnt lgkmcnt(0)" ::: "memory")
; __device__ __forceinline__ unsigned pk4_fp8(float a, float b, float c, float d) {
;     a = fminf(fmaxf(a, -448.f), 448.f); b = fminf(fmaxf(b, -448.f), 448.f); c = fminf(fmaxf(c, -448.f), 448.f); d = fminf(fmaxf(d, -448.f), 448.f);
;     int w = __builtin_amdgcn_cvt_pk_fp8_f32(a, b, 0, false); w = __builtin_amdgcn_cvt_pk_fp8_f32(c, d, w, true); return (unsigned)w; }
;     ...
;     for (int i = 0; i < 32; ++i) v[i] = sc >= 0 ? W[(size_t)(k0 + 2 * i + (lane >> 5)) * Nsrc + sc] : 0.f;
; #pragma unroll
;     for (int i = 0; i < 32; ++i) { const int k = k0 + 2 * i + (lane >> 5); float x = v[i] * wscale; if (KS) x *= (k < ksplit ? ksA[k] : ksB[k - ksplit]); scr[(2 * i + (lane >> 5)) * 33 + (lane & 31)] = x; }
;     LDS_WAIT(); asm volatile("" ::: "memory");
;     const int c = lane & 7;
; #pragma unroll
;     for (int j = 0; j < 4; ++j) { const int n = (lane >> 3) + 8 * j; const LAS float* s = scr + (8 * c) * 33 + n;
;         const unsigned long long o = (unsigned long long)pg8::pk4_fp8(s[0 * 33], s[1 * 33], s[2 * 33], s[3 * 33]) | ((unsigned long long)pg8::pk4_fp8(s[4 * 33], s[5 * 33], s[6 * 33], s[7 * 33]) << 32);
;         *(GAS unsigned long long*)(WT + (size_t)(n0 + n) * K + k0 + 8 * c) = o; }
	s_add_u32 s8, s38, 0x3000
	s_addc_u32 s9, s39, 0
	global_load_dwordx4 v[176:179], v75, s[8:9]
	s_add_u32 s8, s8, 0x8000
	s_addc_u32 s9, s9, 0
	global_load_dwordx4 v[180:183], v75, s[8:9]
	s_add_u32 s8, s8, 0x8000
	s_addc_u32 s9, s9, 0
	global_load_dwordx4 v[184:187], v75, s[8:9]
	s_add_u32 s8, s8, 0x8000
	s_addc_u32 s9, s9, 0
	global_load_dwordx4 v[188:191], v75, s[8:9]
	s_add_u32 s8, s8, 0x8000
	s_addc_u32 s9, s9, 0
	global_load_dwordx4 v[192:195], v75, s[8:9]
	s_add_u32 s8, s8, 0x8000
	s_addc_u32 s9, s9, 0
	global_load_dwordx4 v[196:199], v75, s[8:9]
	s_add_u32 s8, s8, 0x8000
	s_addc_u32 s9, s9, 0
	global_load_dwordx4 v[200:203], v75, s[8:9]
	s_add_u32 s8, s8, 0x8000
	s_addc_u32 s9, s9, 0
	global_load_dwordx4 v[204:207], v75, s[8:9]
	s_add_u32 s6, s40, 0x1000000
	s_addc_u32 s7, s41, 0
	ds_read_b32 v226, v212
	ds_read_b32 v227, v212 offset:512
	ds_read_b32 v228, v212 offset:1024
	ds_read_b32 v229, v212 offset:1536
	ds_read_b32 v230, v212 offset:2048
	ds_read_b32 v231, v212 offset:2560
	ds_read_b32 v232, v212 offset:3072
	ds_read_b32 v233, v212 offset:3584
	ds_read_b32 v234, v212 offset:4096
	ds_read_b32 v235, v212 offset:4608
	ds_read_b32 v236, v212 offset:5120
	ds_read_b32 v237, v212 offset:5632
	ds_read_b32 v238, v212 offset:6144
	ds_read_b32 v239, v212 offset:6656
	ds_read_b32 v240, v212 offset:7168
	ds_read_b32 v241, v212 offset:7680
	s_waitcnt lgkmcnt(0)
	v_max_f32_e32 v226, v226, v226
	v_max_f32_e32 v227, v227, v227
	v_max_f32_e32 v228, v228, v228
	v_max_f32_e32 v229, v229, v229
	v_max_f32_e32 v230, v230, v230
	v_max_f32_e32 v231, v231, v231
	v_max_f32_e32 v232, v232, v232
	v_max_f32_e32 v233, v233, v233
	v_max_f32_e32 v234, v234, v234
	v_max_f32_e32 v235, v235, v235
	v_max_f32_e32 v236, v236, v236
	v_max_f32_e32 v237, v237, v237
	v_max_f32_e32 v238, v238, v238
	v_max_f32_e32 v239, v239, v239
	v_max_f32_e32 v240, v240, v240
	v_max_f32_e32 v241, v241, v241
	v_med3_f32 v226, v226, s62, v95
	v_med3_f32 v227, v227, s62, v95
	v_med3_f32 v228, v228, s62, v95
	v_med3_f32 v229, v229, s62, v95
	v_med3_f32 v230, v230, s62, v95
	v_med3_f32 v231, v231, s62, v95
	v_med3_f32 v232, v232, s62, v95
	v_med3_f32 v233, v233, s62, v95
	v_med3_f32 v234, v234, s62, v95
	v_med3_f32 v235, v235, s62, v95
	v_med3_f32 v236, v236, s62, v95
	v_med3_f32 v237, v237, s62, v95
	v_med3_f32 v238, v238, s62, v95
	v_med3_f32 v239, v239, s62, v95
	v_med3_f32 v240, v240, s62, v95
	v_med3_f32 v241, v241, s62, v95
	v_mov_b32_e32 v242, 0
	v_mov_b32_e32 v243, 0
	v_mov_b32_e32 v244, 0
	v_mov_b32_e32 v245, 0
	v_cvt_pk_fp8_f32 v242, v226, v227
	v_cvt_pk_fp8_f32 v243, v230, v231
	v_cvt_pk_fp8_f32 v244, v234, v235
	v_cvt_pk_fp8_f32 v245, v238, v239
	v_cvt_pk_fp8_f32 v242, v228, v229 op_sel:[0,0,1]
	v_cvt_pk_fp8_f32 v243, v232, v233 op_sel:[0,0,1]
	v_cvt_pk_fp8_f32 v244, v236, v237 op_sel:[0,0,1]
	v_cvt_pk_fp8_f32 v245, v240, v241 op_sel:[0,0,1]
	s_nop 0
	global_store_dwordx4 v79, v[242:245], s[6:7]
	ds_read_b32 v226, v214
	ds_read_b32 v227, v214 offset:512
	ds_read_b32 v228, v214 offset:1024
	ds_read_b32 v229, v214 offset:1536
	ds_read_b32 v230, v214 offset:2048
	ds_read_b32 v231, v214 offset:2560
	ds_read_b32 v232, v214 offset:3072
	ds_read_b32 v233, v214 offset:3584
	ds_read_b32 v234, v214 offset:4096
	ds_read_b32 v235, v214 offset:4608
	ds_read_b32 v236, v214 offset:5120
	ds_read_b32 v237, v214 offset:5632
	ds_read_b32 v238, v214 offset:6144
	ds_read_b32 v239, v214 offset:6656
	ds_read_b32 v240, v214 offset:7168
	ds_read_b32 v241, v214 offset:7680
	s_waitcnt lgkmcnt(0)
	v_max_f32_e32 v226, v226, v226
	v_max_f32_e32 v227, v227, v227
	v_max_f32_e32 v228, v228, v228
	v_max_f32_e32 v229, v229, v229
	v_max_f32_e32 v230, v230, v230
	v_max_f32_e32 v231, v231, v231
	v_max_f32_e32 v232, v232, v232
	v_max_f32_e32 v233, v233, v233
	v_max_f32_e32 v234, v234, v234
	v_max_f32_e32 v235, v235, v235
	v_max_f32_e32 v236, v236, v236
	v_max_f32_e32 v237, v237, v237
	v_max_f32_e32 v238, v238, v238
	v_max_f32_e32 v239, v239, v239
	v_max_f32_e32 v240, v240, v240
	v_max_f32_e32 v241, v241, v241
	v_med3_f32 v226, v226, s62, v95
	v_med3_f32 v227, v227, s62, v95
	v_med3_f32 v228, v228, s62, v95
	v_med3_f32 v229, v229, s62, v95
	v_med3_f32 v230, v230, s62, v95
	v_med3_f32 v231, v231, s62, v95
	v_med3_f32 v232, v232, s62, v95
	v_med3_f32 v233, v233, s62, v95
	v_med3_f32 v234, v234, s62, v95
	v_med3_f32 v235, v235, s62, v95
	v_med3_f32 v236, v236, s62, v95
	v_med3_f32 v237, v237, s62, v95
	v_med3_f32 v238, v238, s62, v95
	v_med3_f32 v239, v239, s62, v95
	v_med3_f32 v240, v240, s62, v95
	v_med3_f32 v241, v241, s62, v95
	v_mov_b32_e32 v242, 0
	v_mov_b32_e32 v243, 0
	v_mov_b32_e32 v244, 0
	v_mov_b32_e32 v245, 0
	v_cvt_pk_fp8_f32 v242, v226, v227
	v_cvt_pk_fp8_f32 v243, v230, v231
	v_cvt_pk_fp8_f32 v244, v234, v235
	v_cvt_pk_fp8_f32 v245, v238, v239
	v_cvt_pk_fp8_f32 v242, v228, v229 op_sel:[0,0,1]
	v_cvt_pk_fp8_f32 v243, v232, v233 op_sel:[0,0,1]
	v_cvt_pk_fp8_f32 v244, v236, v237 op_sel:[0,0,1]
	v_cvt_pk_fp8_f32 v245, v240, v241 op_sel:[0,0,1]
	s_nop 0
	global_store_dwordx4 v80, v[242:245], s[6:7]
	s_waitcnt vmcnt(12)
	v_mul_f32_e32 v144, 0x43000000, v144
	v_mul_f32_e32 v145, 0x43000000, v145
	v_mul_f32_e32 v146, 0x43000000, v146
	v_mul_f32_e32 v147, 0x43000000, v147
	ds_write_b128 v209, v[144:147]
	v_mul_f32_e32 v148, 0x43000000, v148
	v_mul_f32_e32 v149, 0x43000000, v149
	v_mul_f32_e32 v150, 0x43000000, v150
	v_mul_f32_e32 v151, 0x43000000, v151
	ds_write_b128 v209, v[148:151] offset:1024
	v_mul_f32_e32 v152, 0x43000000, v152
	v_mul_f32_e32 v153, 0x43000000, v153
	v_mul_f32_e32 v154, 0x43000000, v154
	v_mul_f32_e32 v155, 0x43000000, v155
	ds_write_b128 v209, v[152:155] offset:2048
	v_mul_f32_e32 v156, 0x43000000, v156
	v_mul_f32_e32 v157, 0x43000000, v157
	v_mul_f32_e32 v158, 0x43000000, v158
	v_mul_f32_e32 v159, 0x43000000, v159
	ds_write_b128 v209, v[156:159] offset:3072
	v_mul_f32_e32 v160, 0x43000000, v160
	v_mul_f32_e32 v161, 0x43000000, v161
	v_mul_f32_e32 v162, 0x43000000, v162
	v_mul_f32_e32 v163, 0x43000000, v163
	ds_write_b128 v209, v[160:163] offset:4096
	v_mul_f32_e32 v164, 0x43000000, v164
	v_mul_f32_e32 v165, 0x43000000, v165
	v_mul_f32_e32 v166, 0x43000000, v166
	v_mul_f32_e32 v167, 0x43000000, v167
	ds_write_b128 v209, v[164:167] offset:5120
	v_mul_f32_e32 v168, 0x43000000, v168
	v_mul_f32_e32 v169, 0x43000000, v169
	v_mul_f32_e32 v170, 0x43000000, v170
	v_mul_f32_e32 v171, 0x43000000, v171
	ds_write_b128 v209, v[168:171] offset:6144
	v_mul_f32_e32 v172, 0x43000000, v172
	v_mul_f32_e32 v173, 0x43000000, v173
	v_mul_f32_e32 v174, 0x43000000, v174
	v_mul_f32_e32 v175, 0x43000000, v175
	ds_write_b128 v209, v[172:175] offset:7168
	s_waitcnt lgkmcnt(0)
	s_barrier
; #define GAS __attribute__((address_space(1)))
; #define LAS __attribute__((address_space(3)))
; #define LDS_WAIT() asm volatile("s_waitcnt lgkmcnt(0)" ::: "memory")
; __device__ __forceinline__ unsigned pk4_fp8(float a, float b, float c, float d) {
;     a = fminf(fmaxf(a, -448.f), 448.f); b = fminf(fmaxf(b, -448.f), 448.f); c = fminf(fmaxf(c, -448.f), 448.f); d = fminf(fmaxf(d, -448.f), 448.f);
;     int w = __builtin_amdgcn_cvt_pk_fp8_f32(a, b, 0, false); w = __builtin_amdgcn_cvt_pk_fp8_f32(c, d, w, true); return (unsigned)w; }
;     ...
;     for (int i = 0; i < 32; ++i) v[i] = sc >= 0 ? W[(size_t)(k0 + 2 * i + (lane >> 5)) * Nsrc + sc] : 0.f;
; #pragma unroll
;     for (int i = 0; i < 32; ++i) { const int k = k0 + 2 * i + (lane >> 5); float x = v[i] * wscale; if (KS) x *= (k < ksplit ? ksA[k] : ksB[k - ksplit]); scr[(2 * i + (lane >> 5)) * 33 + (lane & 31)] = x; }
;     LDS_WAIT(); asm volatile("" ::: "memory");
;     const int c = lane & 7;
; #pragma unroll
;     for (int j = 0; j < 4; ++j) { const int n = (lane >> 3) + 8 * j; const LAS float* s = scr + (8 * c) * 33 + n;
;         const unsigned long long o = (unsigned long long)pg8::pk4_fp8(s[0 * 33], s[1 * 33], s[2 * 33], s[3 * 33]) | ((unsigned long long)pg8::pk4_fp8(s[4 * 33], s[5 * 33], s[6 * 33], s[7 * 33]) << 32);
;         *(GAS unsigned long long*)(WT + (size_t)(n0 + n) * K + k0 + 8 * c) = o; }
	s_add_u32 s8, s38, 0x4000000
	s_addc_u32 s9, s39, 0
	global_load_dwordx4 v[144:147], v75, s[8:9]
	s_add_u32 s8, s8, 0x8000
	s_addc_u32 s9, s9, 0
	global_load_dwordx4 v[148:151], v75, s[8:9]
	s_add_u32 s8, s8, 0x8000
	s_addc_u32 s9, s9, 0
	global_load_dwordx4 v[152:155], v75, s[8:9]
	s_add_u32 s8, s8, 0x8000
	s_addc_u32 s9, s9, 0
	global_load_dwordx4 v[156:159], v75, s[8:9]
	s_add_u32 s8, s8, 0x8000
	s_addc_u32 s9, s9, 0
	global_load_dwordx4 v[160:163], v75, s[8:9]
	s_add_u32 s8, s8, 0x8000
	s_addc_u32 s9, s9, 0
	global_load_dwordx4 v[164:167], v75, s[8:9]
	s_add_u32 s8, s8, 0x8000
	s_addc_u32 s9, s9, 0
	global_load_dwordx4 v[168:171], v75, s[8:9]
	s_add_u32 s8, s8, 0x8000
	s_addc_u32 s9, s9, 0
	global_load_dwordx4 v[172:175], v75, s[8:9]
	s_add_u32 s6, s40, 0x2000000
	s_addc_u32 s7, s41, 0
	ds_read_b32 v226, v211
	ds_read_b32 v227, v211 offset:512
	ds_read_b32 v228, v211 offset:1024
	ds_read_b32 v229, v211 offset:1536
	ds_read_b32 v230, v211 offset:2048
	ds_read_b32 v231, v211 offset:2560
	ds_read_b32 v232, v211 offset:3072
	ds_read_b32 v233, v211 offset:3584
	ds_read_b32 v234, v211 offset:4096
	ds_read_b32 v235, v211 offset:4608
	ds_read_b32 v236, v211 offset:5120
	ds_read_b32 v237, v211 offset:5632
	ds_read_b32 v238, v211 offset:6144
	ds_read_b32 v239, v211 offset:6656
	ds_read_b32 v240, v211 offset:7168
	ds_read_b32 v241, v211 offset:7680
	s_waitcnt lgkmcnt(0)
	v_max_f32_e32 v226, v226, v226
	v_max_f32_e32 v227, v227, v227
	v_max_f32_e32 v228, v228, v228
	v_max_f32_e32 v229, v229, v229
	v_max_f32_e32 v230, v230, v230
	v_max_f32_e32 v231, v231, v231
	v_max_f32_e32 v232, v232, v232
	v_max_f32_e32 v233, v233, v233
	v_max_f32_e32 v234, v234, v234
	v_max_f32_e32 v235, v235, v235
	v_max_f32_e32 v236, v236, v236
	v_max_f32_e32 v237, v237, v237
	v_max_f32_e32 v238, v238, v238
	v_max_f32_e32 v239, v239, v239
	v_max_f32_e32 v240, v240, v240
	v_max_f32_e32 v241, v241, v241
	v_med3_f32 v226, v226, s62, v95
	v_med3_f32 v227, v227, s62, v95
	v_med3_f32 v228, v228, s62, v95
	v_med3_f32 v229, v229, s62, v95
	v_med3_f32 v230, v230, s62, v95
	v_med3_f32 v231, v231, s62, v95
	v_med3_f32 v232, v232, s62, v95
	v_med3_f32 v233, v233, s62, v95
	v_med3_f32 v234, v234, s62, v95
	v_med3_f32 v235, v235, s62, v95
	v_med3_f32 v236, v236, s62, v95
	v_med3_f32 v237, v237, s62, v95
	v_med3_f32 v238, v238, s62, v95
	v_med3_f32 v239, v239, s62, v95
	v_med3_f32 v240, v240, s62, v95
	v_med3_f32 v241, v241, s62, v95
	v_mov_b32_e32 v242, 0
	v_mov_b32_e32 v243, 0
	v_mov_b32_e32 v244, 0
	v_mov_b32_e32 v245, 0
	v_cvt_pk_fp8_f32 v242, v226, v227
	v_cvt_pk_fp8_f32 v243, v230, v231
	v_cvt_pk_fp8_f32 v244, v234, v235
	v_cvt_pk_fp8_f32 v245, v238, v239
	v_cvt_pk_fp8_f32 v242, v228, v229 op_sel:[0,0,1]
	v_cvt_pk_fp8_f32 v243, v232, v233 op_sel:[0,0,1]
	v_cvt_pk_fp8_f32 v244, v236, v237 op_sel:[0,0,1]
	v_cvt_pk_fp8_f32 v245, v240, v241 op_sel:[0,0,1]
	s_nop 0
	global_store_dwordx4 v79, v[242:245], s[6:7]
	ds_read_b32 v226, v213
	ds_read_b32 v227, v213 offset:512
	ds_read_b32 v228, v213 offset:1024
	ds_read_b32 v229, v213 offset:1536
	ds_read_b32 v230, v213 offset:2048
	ds_read_b32 v231, v213 offset:2560
	ds_read_b32 v232, v213 offset:3072
	ds_read_b32 v233, v213 offset:3584
	ds_read_b32 v234, v213 offset:4096
	ds_read_b32 v235, v213 offset:4608
	ds_read_b32 v236, v213 offset:5120
	ds_read_b32 v237, v213 offset:5632
	ds_read_b32 v238, v213 offset:6144
	ds_read_b32 v239, v213 offset:6656
	ds_read_b32 v240, v213 offset:7168
	ds_read_b32 v241, v213 offset:7680
	s_waitcnt lgkmcnt(0)
	v_max_f32_e32 v226, v226, v226
	v_max_f32_e32 v227, v227, v227
	v_max_f32_e32 v228, v228, v228
	v_max_f32_e32 v229, v229, v229
	v_max_f32_e32 v230, v230, v230
	v_max_f32_e32 v231, v231, v231
	v_max_f32_e32 v232, v232, v232
	v_max_f32_e32 v233, v233, v233
	v_max_f32_e32 v234, v234, v234
	v_max_f32_e32 v235, v235, v235
	v_max_f32_e32 v236, v236, v236
	v_max_f32_e32 v237, v237, v237
	v_max_f32_e32 v238, v238, v238
	v_max_f32_e32 v239, v239, v239
	v_max_f32_e32 v240, v240, v240
	v_max_f32_e32 v241, v241, v241
	v_med3_f32 v226, v226, s62, v95
	v_med3_f32 v227, v227, s62, v95
	v_med3_f32 v228, v228, s62, v95
	v_med3_f32 v229, v229, s62, v95
	v_med3_f32 v230, v230, s62, v95
	v_med3_f32 v231, v231, s62, v95
	v_med3_f32 v232, v232, s62, v95
	v_med3_f32 v233, v233, s62, v95
	v_med3_f32 v234, v234, s62, v95
	v_med3_f32 v235, v235, s62, v95
	v_med3_f32 v236, v236, s62, v95
	v_med3_f32 v237, v237, s62, v95
	v_med3_f32 v238, v238, s62, v95
	v_med3_f32 v239, v239, s62, v95
	v_med3_f32 v240, v240, s62, v95
	v_med3_f32 v241, v241, s62, v95
	v_mov_b32_e32 v242, 0
	v_mov_b32_e32 v243, 0
	v_mov_b32_e32 v244, 0
	v_mov_b32_e32 v245, 0
	v_cvt_pk_fp8_f32 v242, v226, v227
	v_cvt_pk_fp8_f32 v243, v230, v231
	v_cvt_pk_fp8_f32 v244, v234, v235
	v_cvt_pk_fp8_f32 v245, v238, v239
	v_cvt_pk_fp8_f32 v242, v228, v229 op_sel:[0,0,1]
	v_cvt_pk_fp8_f32 v243, v232, v233 op_sel:[0,0,1]
	v_cvt_pk_fp8_f32 v244, v236, v237 op_sel:[0,0,1]
	v_cvt_pk_fp8_f32 v245, v240, v241 op_sel:[0,0,1]
	s_nop 0
	global_store_dwordx4 v80, v[242:245], s[6:7]
	s_waitcnt vmcnt(12)
	v_mul_f32_e32 v176, 0x43000000, v176
	v_mul_f32_e32 v177, 0x43000000, v177
	v_mul_f32_e32 v178, 0x43000000, v178
	v_mul_f32_e32 v179, 0x43000000, v179
	ds_write_b128 v210, v[176:179]
	v_mul_f32_e32 v180, 0x43000000, v180
	v_mul_f32_e32 v181, 0x43000000, v181
	v_mul_f32_e32 v182, 0x43000000, v182
	v_mul_f32_e32 v183, 0x43000000, v183
	ds_write_b128 v210, v[180:183] offset:1024
	v_mul_f32_e32 v184, 0x43000000, v184
	v_mul_f32_e32 v185, 0x43000000, v185
	v_mul_f32_e32 v186, 0x43000000, v186
	v_mul_f32_e32 v187, 0x43000000, v187
	ds_write_b128 v210, v[184:187] offset:2048
	v_mul_f32_e32 v188, 0x43000000, v188
	v_mul_f32_e32 v189, 0x43000000, v189
	v_mul_f32_e32 v190, 0x43000000, v190
	v_mul_f32_e32 v191, 0x43000000, v191
	ds_write_b128 v210, v[188:191] offset:3072
	v_mul_f32_e32 v192, 0x43000000, v192
	v_mul_f32_e32 v193, 0x43000000, v193
	v_mul_f32_e32 v194, 0x43000000, v194
	v_mul_f32_e32 v195, 0x43000000, v195
	ds_write_b128 v210, v[192:195] offset:4096
	v_mul_f32_e32 v196, 0x43000000, v196
	v_mul_f32_e32 v197, 0x43000000, v197
	v_mul_f32_e32 v198, 0x43000000, v198
	v_mul_f32_e32 v199, 0x43000000, v199
	ds_write_b128 v210, v[196:199] offset:5120
	v_mul_f32_e32 v200, 0x43000000, v200
	v_mul_f32_e32 v201, 0x43000000, v201
	v_mul_f32_e32 v202, 0x43000000, v202
	v_mul_f32_e32 v203, 0x43000000, v203
	ds_write_b128 v210, v[200:203] offset:6144
	v_mul_f32_e32 v204, 0x43000000, v204
	v_mul_f32_e32 v205, 0x43000000, v205
	v_mul_f32_e32 v206, 0x43000000, v206
	v_mul_f32_e32 v207, 0x43000000, v207
	ds_write_b128 v210, v[204:207] offset:7168
	s_waitcnt lgkmcnt(0)
	s_barrier
; #define GAS __attribute__((address_space(1)))
; #define LAS __attribute__((address_space(3)))
; #define LDS_WAIT() asm volatile("s_waitcnt lgkmcnt(0)" ::: "memory")
; __device__ __forceinline__ unsigned pk4_fp8(float a, float b, float c, float d) {
;     a = fminf(fmaxf(a, -448.f), 448.f); b = fminf(fmaxf(b, -448.f), 448.f); c = fminf(fmaxf(c, -448.f), 448.f); d = fminf(fmaxf(d, -448.f), 448.f);
;     int w = __builtin_amdgcn_cvt_pk_fp8_f32(a, b, 0, false); w = __builtin_amdgcn_cvt_pk_fp8_f32(c, d, w, true); return (unsigned)w; }
;     ...
;     for (int i = 0; i < 32; ++i) v[i] = sc >= 0 ? W[(size_t)(k0 + 2 * i + (lane >> 5)) * Nsrc + sc] : 0.f;
; #pragma unroll
;     for (int i = 0; i < 32; ++i) { const int k = k0 + 2 * i + (lane >> 5); float x = v[i] * wscale; if (KS) x *= (k < ksplit ? ksA[k] : ksB[k - ksplit]); scr[(2 * i + (lane >> 5)) * 33 + (lane & 31)] = x; }
;     LDS_WAIT(); asm volatile("" ::: "memory");
;     const int c = lane & 7;
; #pragma unroll
;     for (int j = 0; j < 4; ++j) { const int n = (lane >> 3) + 8 * j; const LAS float* s = scr + (8 * c) * 33 + n;
;         const unsigned long long o = (unsigned long long)pg8::pk4_fp8(s[0 * 33], s[1 * 33], s[2 * 33], s[3 * 33]) | ((unsigned long long)pg8::pk4_fp8(s[4 * 33], s[5 * 33], s[6 * 33], s[7 * 33]) << 32);
;         *(GAS unsigned long long*)(WT + (size_t)(n0 + n) * K + k0 + 8 * c) = o; }
	s_add_u32 s8, s38, 0x4001000
	s_addc_u32 s9, s39, 0
	global_load_dwordx4 v[176:179], v75, s[8:9]
	s_add_u32 s8, s8, 0x8000
	s_addc_u32 s9, s9, 0
	global_load_dwordx4 v[180:183], v75, s[8:9]
	s_add_u32 s8, s8, 0x8000
	s_addc_u32 s9, s9, 0
	global_load_dwordx4 v[184:187], v75, s[8:9]
	s_add_u32 s8, s8, 0x8000
	s_addc_u32 s9, s9, 0
	global_load_dwordx4 v[188:191], v75, s[8:9]
	s_add_u32 s8, s8, 0x8000
	s_addc_u32 s9, s9, 0
	global_load_dwordx4 v[192:195], v75, s[8:9]
	s_add_u32 s8, s8, 0x8000
	s_addc_u32 s9, s9, 0
	global_load_dwordx4 v[196:199], v75, s[8:9]
	s_add_u32 s8, s8, 0x8000
	s_addc_u32 s9, s9, 0
	global_load_dwordx4 v[200:203], v75, s[8:9]
	s_add_u32 s8, s8, 0x8000
	s_addc_u32 s9, s9, 0
	global_load_dwordx4 v[204:207], v75, s[8:9]
	s_add_u32 s6, s40, 0x3000000
	s_addc_u32 s7, s41, 0
	ds_read_b32 v226, v212
	ds_read_b32 v227, v212 offset:512
	ds_read_b32 v228, v212 offset:1024
	ds_read_b32 v229, v212 offset:1536
	ds_read_b32 v230, v212 offset:2048
	ds_read_b32 v231, v212 offset:2560
	ds_read_b32 v232, v212 offset:3072
	ds_read_b32 v233, v212 offset:3584
	ds_read_b32 v234, v212 offset:4096
	ds_read_b32 v235, v212 offset:4608
	ds_read_b32 v236, v212 offset:5120
	ds_read_b32 v237, v212 offset:5632
	ds_read_b32 v238, v212 offset:6144
	ds_read_b32 v239, v212 offset:6656
	ds_read_b32 v240, v212 offset:7168
	ds_read_b32 v241, v212 offset:7680
	s_waitcnt lgkmcnt(0)
	v_max_f32_e32 v226, v226, v226
	v_max_f32_e32 v227, v227, v227
	v_max_f32_e32 v228, v228, v228
	v_max_f32_e32 v229, v229, v229
	v_max_f32_e32 v230, v230, v230
	v_max_f32_e32 v231, v231, v231
	v_max_f32_e32 v232, v232, v232
	v_max_f32_e32 v233, v233, v233
	v_max_f32_e32 v234, v234, v234
	v_max_f32_e32 v235, v235, v235
	v_max_f32_e32 v236, v236, v236
	v_max_f32_e32 v237, v237, v237
	v_max_f32_e32 v238, v238, v238
	v_max_f32_e32 v239, v239, v239
	v_max_f32_e32 v240, v240, v240
	v_max_f32_e32 v241, v241, v241
	v_med3_f32 v226, v226, s62, v95
	v_med3_f32 v227, v227, s62, v95
	v_med3_f32 v228, v228, s62, v95
	v_med3_f32 v229, v229, s62, v95
	v_med3_f32 v230, v230, s62, v95
	v_med3_f32 v231, v231, s62, v95
	v_med3_f32 v232, v232, s62, v95
	v_med3_f32 v233, v233, s62, v95
	v_med3_f32 v234, v234, s62, v95
	v_med3_f32 v235, v235, s62, v95
	v_med3_f32 v236, v236, s62, v95
	v_med3_f32 v237, v237, s62, v95
	v_med3_f32 v238, v238, s62, v95
	v_med3_f32 v239, v239, s62, v95
	v_med3_f32 v240, v240, s62, v95
	v_med3_f32 v241, v241, s62, v95
	v_mov_b32_e32 v242, 0
	v_mov_b32_e32 v243, 0
	v_mov_b32_e32 v244, 0
	v_mov_b32_e32 v245, 0
	v_cvt_pk_fp8_f32 v242, v226, v227
	v_cvt_pk_fp8_f32 v243, v230, v231
	v_cvt_pk_fp8_f32 v244, v234, v235
	v_cvt_pk_fp8_f32 v245, v238, v239
	v_cvt_pk_fp8_f32 v242, v228, v229 op_sel:[0,0,1]
	v_cvt_pk_fp8_f32 v243, v232, v233 op_sel:[0,0,1]
	v_cvt_pk_fp8_f32 v244, v236, v237 op_sel:[0,0,1]
	v_cvt_pk_fp8_f32 v245, v240, v241 op_sel:[0,0,1]
	s_nop 0
	global_store_dwordx4 v79, v[242:245], s[6:7]
	ds_read_b32 v226, v214
	ds_read_b32 v227, v214 offset:512
	ds_read_b32 v228, v214 offset:1024
	ds_read_b32 v229, v214 offset:1536
	ds_read_b32 v230, v214 offset:2048
	ds_read_b32 v231, v214 offset:2560
	ds_read_b32 v232, v214 offset:3072
	ds_read_b32 v233, v214 offset:3584
	ds_read_b32 v234, v214 offset:4096
	ds_read_b32 v235, v214 offset:4608
	ds_read_b32 v236, v214 offset:5120
	ds_read_b32 v237, v214 offset:5632
	ds_read_b32 v238, v214 offset:6144
	ds_read_b32 v239, v214 offset:6656
	ds_read_b32 v240, v214 offset:7168
	ds_read_b32 v241, v214 offset:7680
	s_waitcnt lgkmcnt(0)
	v_max_f32_e32 v226, v226, v226
	v_max_f32_e32 v227, v227, v227
	v_max_f32_e32 v228, v228, v228
	v_max_f32_e32 v229, v229, v229
	v_max_f32_e32 v230, v230, v230
	v_max_f32_e32 v231, v231, v231
	v_max_f32_e32 v232, v232, v232
	v_max_f32_e32 v233, v233, v233
	v_max_f32_e32 v234, v234, v234
	v_max_f32_e32 v235, v235, v235
	v_max_f32_e32 v236, v236, v236
	v_max_f32_e32 v237, v237, v237
	v_max_f32_e32 v238, v238, v238
	v_max_f32_e32 v239, v239, v239
	v_max_f32_e32 v240, v240, v240
	v_max_f32_e32 v241, v241, v241
	v_med3_f32 v226, v226, s62, v95
	v_med3_f32 v227, v227, s62, v95
	v_med3_f32 v228, v228, s62, v95
	v_med3_f32 v229, v229, s62, v95
	v_med3_f32 v230, v230, s62, v95
	v_med3_f32 v231, v231, s62, v95
	v_med3_f32 v232, v232, s62, v95
	v_med3_f32 v233, v233, s62, v95
	v_med3_f32 v234, v234, s62, v95
	v_med3_f32 v235, v235, s62, v95
	v_med3_f32 v236, v236, s62, v95
	v_med3_f32 v237, v237, s62, v95
	v_med3_f32 v238, v238, s62, v95
	v_med3_f32 v239, v239, s62, v95
	v_med3_f32 v240, v240, s62, v95
	v_med3_f32 v241, v241, s62, v95
	v_mov_b32_e32 v242, 0
	v_mov_b32_e32 v243, 0
	v_mov_b32_e32 v244, 0
	v_mov_b32_e32 v245, 0
	v_cvt_pk_fp8_f32 v242, v226, v227
	v_cvt_pk_fp8_f32 v243, v230, v231
	v_cvt_pk_fp8_f32 v244, v234, v235
	v_cvt_pk_fp8_f32 v245, v238, v239
	v_cvt_pk_fp8_f32 v242, v228, v229 op_sel:[0,0,1]
	v_cvt_pk_fp8_f32 v243, v232, v233 op_sel:[0,0,1]
	v_cvt_pk_fp8_f32 v244, v236, v237 op_sel:[0,0,1]
	v_cvt_pk_fp8_f32 v245, v240, v241 op_sel:[0,0,1]
	s_nop 0
	global_store_dwordx4 v80, v[242:245], s[6:7]
	s_waitcnt vmcnt(12)
	v_mul_f32_e32 v144, 0x43000000, v144
	v_mul_f32_e32 v145, 0x43000000, v145
	v_mul_f32_e32 v146, 0x43000000, v146
	v_mul_f32_e32 v147, 0x43000000, v147
	ds_write_b128 v209, v[144:147]
	v_mul_f32_e32 v148, 0x43000000, v148
	v_mul_f32_e32 v149, 0x43000000, v149
	v_mul_f32_e32 v150, 0x43000000, v150
	v_mul_f32_e32 v151, 0x43000000, v151
	ds_write_b128 v209, v[148:151] offset:1024
	v_mul_f32_e32 v152, 0x43000000, v152
	v_mul_f32_e32 v153, 0x43000000, v153
	v_mul_f32_e32 v154, 0x43000000, v154
	v_mul_f32_e32 v155, 0x43000000, v155
	ds_write_b128 v209, v[152:155] offset:2048
	v_mul_f32_e32 v156, 0x43000000, v156
	v_mul_f32_e32 v157, 0x43000000, v157
	v_mul_f32_e32 v158, 0x43000000, v158
	v_mul_f32_e32 v159, 0x43000000, v159
	ds_write_b128 v209, v[156:159] offset:3072
	v_mul_f32_e32 v160, 0x43000000, v160
	v_mul_f32_e32 v161, 0x43000000, v161
	v_mul_f32_e32 v162, 0x43000000, v162
	v_mul_f32_e32 v163, 0x43000000, v163
	ds_write_b128 v209, v[160:163] offset:4096
	v_mul_f32_e32 v164, 0x43000000, v164
	v_mul_f32_e32 v165, 0x43000000, v165
	v_mul_f32_e32 v166, 0x43000000, v166
	v_mul_f32_e32 v167, 0x43000000, v167
	ds_write_b128 v209, v[164:167] offset:5120
	v_mul_f32_e32 v168, 0x43000000, v168
	v_mul_f32_e32 v169, 0x43000000, v169
	v_mul_f32_e32 v170, 0x43000000, v170
	v_mul_f32_e32 v171, 0x43000000, v171
	ds_write_b128 v209, v[168:171] offset:6144
	v_mul_f32_e32 v172, 0x43000000, v172
	v_mul_f32_e32 v173, 0x43000000, v173
	v_mul_f32_e32 v174, 0x43000000, v174
	v_mul_f32_e32 v175, 0x43000000, v175
	ds_write_b128 v209, v[172:175] offset:7168
	s_waitcnt lgkmcnt(0)
	s_barrier
; #define GAS __attribute__((address_space(1)))
; #define LAS __attribute__((address_space(3)))
; #define LDS_WAIT() asm volatile("s_waitcnt lgkmcnt(0)" ::: "memory")
; __device__ __forceinline__ unsigned pk4_fp8(float a, float b, float c, float d) {
;     a = fminf(fmaxf(a, -448.f), 448.f); b = fminf(fmaxf(b, -448.f), 448.f); c = fminf(fmaxf(c, -448.f), 448.f); d = fminf(fmaxf(d, -448.f), 448.f);
;     int w = __builtin_amdgcn_cvt_pk_fp8_f32(a, b, 0, false); w = __builtin_amdgcn_cvt_pk_fp8_f32(c, d, w, true); return (unsigned)w; }
;     ...
;     for (int i = 0; i < 32; ++i) v[i] = sc >= 0 ? W[(size_t)(k0 + 2 * i + (lane >> 5)) * Nsrc + sc] : 0.f;
; #pragma unroll
;     for (int i = 0; i < 32; ++i) { const int k = k0 + 2 * i + (lane >> 5); float x = v[i] * wscale; if (KS) x *= (k < ksplit ? ksA[k] : ksB[k - ksplit]); scr[(2 * i + (lane >> 5)) * 33 + (lane & 31)] = x; }
;     LDS_WAIT(); asm volatile("" ::: "memory");
;     const int c = lane & 7;
; #pragma unroll
;     for (int j = 0; j < 4; ++j) { const int n = (lane >> 3) + 8 * j; const LAS float* s = scr + (8 * c) * 33 + n;
;         const unsigned long long o = (unsigned long long)pg8::pk4_fp8(s[0 * 33], s[1 * 33], s[2 * 33], s[3 * 33]) | ((unsigned long long)pg8::pk4_fp8(s[4 * 33], s[5 * 33], s[6 * 33], s[7 * 33]) << 32);
;         *(GAS unsigned long long*)(WT + (size_t)(n0 + n) * K + k0 + 8 * c) = o; }
	s_add_u32 s8, s38, 0x4002000
	s_addc_u32 s9, s39, 0
	global_load_dwordx4 v[144:147], v75, s[8:9]
	s_add_u32 s8, s8, 0x8000
	s_addc_u32 s9, s9, 0
	global_load_dwordx4 v[148:151], v75, s[8:9]
	s_add_u32 s8, s8, 0x8000
	s_addc_u32 s9, s9, 0
	global_load_dwordx4 v[152:155], v75, s[8:9]
	s_add_u32 s8, s8, 0x8000
	s_addc_u32 s9, s9, 0
	global_load_dwordx4 v[156:159], v75, s[8:9]
	s_add_u32 s8, s8, 0x8000
	s_addc_u32 s9, s9, 0
	global_load_dwordx4 v[160:163], v75, s[8:9]
	s_add_u32 s8, s8, 0x8000
	s_addc_u32 s9, s9, 0
	global_load_dwordx4 v[164:167], v75, s[8:9]
	s_add_u32 s8, s8, 0x8000
	s_addc_u32 s9, s9, 0
	global_load_dwordx4 v[168:171], v75, s[8:9]
	s_add_u32 s8, s8, 0x8000
	s_addc_u32 s9, s9, 0
	global_load_dwordx4 v[172:175], v75, s[8:9]
	s_add_u32 s6, s40, 0x1000
	s_addc_u32 s7, s41, 0
	ds_read_b32 v226, v211
	ds_read_b32 v227, v211 offset:512
	ds_read_b32 v228, v211 offset:1024
	ds_read_b32 v229, v211 offset:1536
	ds_read_b32 v230, v211 offset:2048
	ds_read_b32 v231, v211 offset:2560
	ds_read_b32 v232, v211 offset:3072
	ds_read_b32 v233, v211 offset:3584
	ds_read_b32 v234, v211 offset:4096
	ds_read_b32 v235, v211 offset:4608
	ds_read_b32 v236, v211 offset:5120
	ds_read_b32 v237, v211 offset:5632
	ds_read_b32 v238, v211 offset:6144
	ds_read_b32 v239, v211 offset:6656
	ds_read_b32 v240, v211 offset:7168
	ds_read_b32 v241, v211 offset:7680
	s_waitcnt lgkmcnt(0)
	v_max_f32_e32 v226, v226, v226
	v_max_f32_e32 v227, v227, v227
	v_max_f32_e32 v228, v228, v228
	v_max_f32_e32 v229, v229, v229
	v_max_f32_e32 v230, v230, v230
	v_max_f32_e32 v231, v231, v231
	v_max_f32_e32 v232, v232, v232
	v_max_f32_e32 v233, v233, v233
	v_max_f32_e32 v234, v234, v234
	v_max_f32_e32 v235, v235, v235
	v_max_f32_e32 v236, v236, v236
	v_max_f32_e32 v237, v237, v237
	v_max_f32_e32 v238, v238, v238
	v_max_f32_e32 v239, v239, v239
	v_max_f32_e32 v240, v240, v240
	v_max_f32_e32 v241, v241, v241
	v_med3_f32 v226, v226, s62, v95
	v_med3_f32 v227, v227, s62, v95
	v_med3_f32 v228, v228, s62, v95
	v_med3_f32 v229, v229, s62, v95
	v_med3_f32 v230, v230, s62, v95
	v_med3_f32 v231, v231, s62, v95
	v_med3_f32 v232, v232, s62, v95
	v_med3_f32 v233, v233, s62, v95
	v_med3_f32 v234, v234, s62, v95
	v_med3_f32 v235, v235, s62, v95
	v_med3_f32 v236, v236, s62, v95
	v_med3_f32 v237, v237, s62, v95
	v_med3_f32 v238, v238, s62, v95
	v_med3_f32 v239, v239, s62, v95
	v_med3_f32 v240, v240, s62, v95
	v_med3_f32 v241, v241, s62, v95
	v_mov_b32_e32 v242, 0
	v_mov_b32_e32 v243, 0
	v_mov_b32_e32 v244, 0
	v_mov_b32_e32 v245, 0
	v_cvt_pk_fp8_f32 v242, v226, v227
	v_cvt_pk_fp8_f32 v243, v230, v231
	v_cvt_pk_fp8_f32 v244, v234, v235
	v_cvt_pk_fp8_f32 v245, v238, v239
	v_cvt_pk_fp8_f32 v242, v228, v229 op_sel:[0,0,1]
	v_cvt_pk_fp8_f32 v243, v232, v233 op_sel:[0,0,1]
	v_cvt_pk_fp8_f32 v244, v236, v237 op_sel:[0,0,1]
	v_cvt_pk_fp8_f32 v245, v240, v241 op_sel:[0,0,1]
	s_nop 0
	global_store_dwordx4 v79, v[242:245], s[6:7]
	ds_read_b32 v226, v213
	ds_read_b32 v227, v213 offset:512
	ds_read_b32 v228, v213 offset:1024
	ds_read_b32 v229, v213 offset:1536
	ds_read_b32 v230, v213 offset:2048
	ds_read_b32 v231, v213 offset:2560
	ds_read_b32 v232, v213 offset:3072
	ds_read_b32 v233, v213 offset:3584
	ds_read_b32 v234, v213 offset:4096
	ds_read_b32 v235, v213 offset:4608
	ds_read_b32 v236, v213 offset:5120
	ds_read_b32 v237, v213 offset:5632
	ds_read_b32 v238, v213 offset:6144
	ds_read_b32 v239, v213 offset:6656
	ds_read_b32 v240, v213 offset:7168
	ds_read_b32 v241, v213 offset:7680
	s_waitcnt lgkmcnt(0)
	v_max_f32_e32 v226, v226, v226
	v_max_f32_e32 v227, v227, v227
	v_max_f32_e32 v228, v228, v228
	v_max_f32_e32 v229, v229, v229
	v_max_f32_e32 v230, v230, v230
	v_max_f32_e32 v231, v231, v231
	v_max_f32_e32 v232, v232, v232
	v_max_f32_e32 v233, v233, v233
	v_max_f32_e32 v234, v234, v234
	v_max_f32_e32 v235, v235, v235
	v_max_f32_e32 v236, v236, v236
	v_max_f32_e32 v237, v237, v237
	v_max_f32_e32 v238, v238, v238
	v_max_f32_e32 v239, v239, v239
	v_max_f32_e32 v240, v240, v240
	v_max_f32_e32 v241, v241, v241
	v_med3_f32 v226, v226, s62, v95
	v_med3_f32 v227, v227, s62, v95
	v_med3_f32 v228, v228, s62, v95
	v_med3_f32 v229, v229, s62, v95
	v_med3_f32 v230, v230, s62, v95
	v_med3_f32 v231, v231, s62, v95
	v_med3_f32 v232, v232, s62, v95
	v_med3_f32 v233, v233, s62, v95
	v_med3_f32 v234, v234, s62, v95
	v_med3_f32 v235, v235, s62, v95
	v_med3_f32 v236, v236, s62, v95
	v_med3_f32 v237, v237, s62, v95
	v_med3_f32 v238, v238, s62, v95
	v_med3_f32 v239, v239, s62, v95
	v_med3_f32 v240, v240, s62, v95
	v_med3_f32 v241, v241, s62, v95
	v_mov_b32_e32 v242, 0
	v_mov_b32_e32 v243, 0
	v_mov_b32_e32 v244, 0
	v_mov_b32_e32 v245, 0
	v_cvt_pk_fp8_f32 v242, v226, v227
	v_cvt_pk_fp8_f32 v243, v230, v231
	v_cvt_pk_fp8_f32 v244, v234, v235
	v_cvt_pk_fp8_f32 v245, v238, v239
	v_cvt_pk_fp8_f32 v242, v228, v229 op_sel:[0,0,1]
	v_cvt_pk_fp8_f32 v243, v232, v233 op_sel:[0,0,1]
	v_cvt_pk_fp8_f32 v244, v236, v237 op_sel:[0,0,1]
	v_cvt_pk_fp8_f32 v245, v240, v241 op_sel:[0,0,1]
	s_nop 0
	global_store_dwordx4 v80, v[242:245], s[6:7]
	s_waitcnt vmcnt(12)
	v_mul_f32_e32 v176, 0x43000000, v176
	v_mul_f32_e32 v177, 0x43000000, v177
	v_mul_f32_e32 v178, 0x43000000, v178
	v_mul_f32_e32 v179, 0x43000000, v179
	ds_write_b128 v210, v[176:179]
	v_mul_f32_e32 v180, 0x43000000, v180
	v_mul_f32_e32 v181, 0x43000000, v181
	v_mul_f32_e32 v182, 0x43000000, v182
	v_mul_f32_e32 v183, 0x43000000, v183
	ds_write_b128 v210, v[180:183] offset:1024
	v_mul_f32_e32 v184, 0x43000000, v184
	v_mul_f32_e32 v185, 0x43000000, v185
	v_mul_f32_e32 v186, 0x43000000, v186
	v_mul_f32_e32 v187, 0x43000000, v187
	ds_write_b128 v210, v[184:187] offset:2048
	v_mul_f32_e32 v188, 0x43000000, v188
	v_mul_f32_e32 v189, 0x43000000, v189
	v_mul_f32_e32 v190, 0x43000000, v190
	v_mul_f32_e32 v191, 0x43000000, v191
	ds_write_b128 v210, v[188:191] offset:3072
	v_mul_f32_e32 v192, 0x43000000, v192
	v_mul_f32_e32 v193, 0x43000000, v193
	v_mul_f32_e32 v194, 0x43000000, v194
	v_mul_f32_e32 v195, 0x43000000, v195
	ds_write_b128 v210, v[192:195] offset:4096
	v_mul_f32_e32 v196, 0x43000000, v196
	v_mul_f32_e32 v197, 0x43000000, v197
	v_mul_f32_e32 v198, 0x43000000, v198
	v_mul_f32_e32 v199, 0x43000000, v199
	ds_write_b128 v210, v[196:199] offset:5120
	v_mul_f32_e32 v200, 0x43000000, v200
	v_mul_f32_e32 v201, 0x43000000, v201
	v_mul_f32_e32 v202, 0x43000000, v202
	v_mul_f32_e32 v203, 0x43000000, v203
	ds_write_b128 v210, v[200:203] offset:6144
	v_mul_f32_e32 v204, 0x43000000, v204
	v_mul_f32_e32 v205, 0x43000000, v205
	v_mul_f32_e32 v206, 0x43000000, v206
	v_mul_f32_e32 v207, 0x43000000, v207
	ds_write_b128 v210, v[204:207] offset:7168
	s_waitcnt lgkmcnt(0)
	s_barrier
; #define GAS __attribute__((address_space(1)))
; #define LAS __attribute__((address_space(3)))
; #define LDS_WAIT() asm volatile("s_waitcnt lgkmcnt(0)" ::: "memory")
; __device__ __forceinline__ unsigned pk4_fp8(float a, float b, float c, float d) {
;     a = fminf(fmaxf(a, -448.f), 448.f); b = fminf(fmaxf(b, -448.f), 448.f); c = fminf(fmaxf(c, -448.f), 448.f); d = fminf(fmaxf(d, -448.f), 448.f);
;     int w = __builtin_amdgcn_cvt_pk_fp8_f32(a, b, 0, false); w = __builtin_amdgcn_cvt_pk_fp8_f32(c, d, w, true); return (unsigned)w; }
;     ...
;     for (int i = 0; i < 32; ++i) v[i] = sc >= 0 ? W[(size_t)(k0 + 2 * i + (lane >> 5)) * Nsrc + sc] : 0.f;
; #pragma unroll
;     for (int i = 0; i < 32; ++i) { const int k = k0 + 2 * i + (lane >> 5); float x = v[i] * wscale; if (KS) x *= (k < ksplit ? ksA[k] : ksB[k - ksplit]); scr[(2 * i + (lane >> 5)) * 33 + (lane & 31)] = x; }
;     LDS_WAIT(); asm volatile("" ::: "memory");
;     const int c = lane & 7;
; #pragma unroll
;     for (int j = 0; j < 4; ++j) { const int n = (lane >> 3) + 8 * j; const LAS float* s = scr + (8 * c) * 33 + n;
;         const unsigned long long o = (unsigned long long)pg8::pk4_fp8(s[0 * 33], s[1 * 33], s[2 * 33], s[3 * 33]) | ((unsigned long long)pg8::pk4_fp8(s[4 * 33], s[5 * 33], s[6 * 33], s[7 * 33]) << 32);
;         *(GAS unsigned long long*)(WT + (size_t)(n0 + n) * K + k0 + 8 * c) = o; }
	s_add_u32 s8, s38, 0x4003000
	s_addc_u32 s9, s39, 0
	global_load_dwordx4 v[176:179], v75, s[8:9]
	s_add_u32 s8, s8, 0x8000
	s_addc_u32 s9, s9, 0
	global_load_dwordx4 v[180:183], v75, s[8:9]
	s_add_u32 s8, s8, 0x8000
	s_addc_u32 s9, s9, 0
	global_load_dwordx4 v[184:187], v75, s[8:9]
	s_add_u32 s8, s8, 0x8000
	s_addc_u32 s9, s9, 0
	global_load_dwordx4 v[188:191], v75, s[8:9]
	s_add_u32 s8, s8, 0x8000
	s_addc_u32 s9, s9, 0
	global_load_dwordx4 v[192:195], v75, s[8:9]
	s_add_u32 s8, s8, 0x8000
	s_addc_u32 s9, s9, 0
	global_load_dwordx4 v[196:199], v75, s[8:9]
	s_add_u32 s8, s8, 0x8000
	s_addc_u32 s9, s9, 0
	global_load_dwordx4 v[200:203], v75, s[8:9]
	s_add_u32 s8, s8, 0x8000
	s_addc_u32 s9, s9, 0
	global_load_dwordx4 v[204:207], v75, s[8:9]
	s_add_u32 s6, s40, 0x1001000
	s_addc_u32 s7, s41, 0
	ds_read_b32 v226, v212
	ds_read_b32 v227, v212 offset:512
	ds_read_b32 v228, v212 offset:1024
	ds_read_b32 v229, v212 offset:1536
	ds_read_b32 v230, v212 offset:2048
	ds_read_b32 v231, v212 offset:2560
	ds_read_b32 v232, v212 offset:3072
	ds_read_b32 v233, v212 offset:3584
	ds_read_b32 v234, v212 offset:4096
	ds_read_b32 v235, v212 offset:4608
	ds_read_b32 v236, v212 offset:5120
	ds_read_b32 v237, v212 offset:5632
	ds_read_b32 v238, v212 offset:6144
	ds_read_b32 v239, v212 offset:6656
	ds_read_b32 v240, v212 offset:7168
	ds_read_b32 v241, v212 offset:7680
	s_waitcnt lgkmcnt(0)
	v_max_f32_e32 v226, v226, v226
	v_max_f32_e32 v227, v227, v227
	v_max_f32_e32 v228, v228, v228
	v_max_f32_e32 v229, v229, v229
	v_max_f32_e32 v230, v230, v230
	v_max_f32_e32 v231, v231, v231
	v_max_f32_e32 v232, v232, v232
	v_max_f32_e32 v233, v233, v233
	v_max_f32_e32 v234, v234, v234
	v_max_f32_e32 v235, v235, v235
	v_max_f32_e32 v236, v236, v236
	v_max_f32_e32 v237, v237, v237
	v_max_f32_e32 v238, v238, v238
	v_max_f32_e32 v239, v239, v239
	v_max_f32_e32 v240, v240, v240
	v_max_f32_e32 v241, v241, v241
	v_med3_f32 v226, v226, s62, v95
	v_med3_f32 v227, v227, s62, v95
	v_med3_f32 v228, v228, s62, v95
	v_med3_f32 v229, v229, s62, v95
	v_med3_f32 v230, v230, s62, v95
	v_med3_f32 v231, v231, s62, v95
	v_med3_f32 v232, v232, s62, v95
	v_med3_f32 v233, v233, s62, v95
	v_med3_f32 v234, v234, s62, v95
	v_med3_f32 v235, v235, s62, v95
	v_med3_f32 v236, v236, s62, v95
	v_med3_f32 v237, v237, s62, v95
	v_med3_f32 v238, v238, s62, v95
	v_med3_f32 v239, v239, s62, v95
	v_med3_f32 v240, v240, s62, v95
	v_med3_f32 v241, v241, s62, v95
	v_mov_b32_e32 v242, 0
	v_mov_b32_e32 v243, 0
	v_mov_b32_e32 v244, 0
	v_mov_b32_e32 v245, 0
	v_cvt_pk_fp8_f32 v242, v226, v227
	v_cvt_pk_fp8_f32 v243, v230, v231
	v_cvt_pk_fp8_f32 v244, v234, v235
	v_cvt_pk_fp8_f32 v245, v238, v239
	v_cvt_pk_fp8_f32 v242, v228, v229 op_sel:[0,0,1]
	v_cvt_pk_fp8_f32 v243, v232, v233 op_sel:[0,0,1]
	v_cvt_pk_fp8_f32 v244, v236, v237 op_sel:[0,0,1]
	v_cvt_pk_fp8_f32 v245, v240, v241 op_sel:[0,0,1]
	s_nop 0
	global_store_dwordx4 v79, v[242:245], s[6:7]
	ds_read_b32 v226, v214
	ds_read_b32 v227, v214 offset:512
	ds_read_b32 v228, v214 offset:1024
	ds_read_b32 v229, v214 offset:1536
	ds_read_b32 v230, v214 offset:2048
	ds_read_b32 v231, v214 offset:2560
	ds_read_b32 v232, v214 offset:3072
	ds_read_b32 v233, v214 offset:3584
	ds_read_b32 v234, v214 offset:4096
	ds_read_b32 v235, v214 offset:4608
	ds_read_b32 v236, v214 offset:5120
	ds_read_b32 v237, v214 offset:5632
	ds_read_b32 v238, v214 offset:6144
	ds_read_b32 v239, v214 offset:6656
	ds_read_b32 v240, v214 offset:7168
	ds_read_b32 v241, v214 offset:7680
	s_waitcnt lgkmcnt(0)
	v_max_f32_e32 v226, v226, v226
	v_max_f32_e32 v227, v227, v227
	v_max_f32_e32 v228, v228, v228
	v_max_f32_e32 v229, v229, v229
	v_max_f32_e32 v230, v230, v230
	v_max_f32_e32 v231, v231, v231
	v_max_f32_e32 v232, v232, v232
	v_max_f32_e32 v233, v233, v233
	v_max_f32_e32 v234, v234, v234
	v_max_f32_e32 v235, v235, v235
	v_max_f32_e32 v236, v236, v236
	v_max_f32_e32 v237, v237, v237
	v_max_f32_e32 v238, v238, v238
	v_max_f32_e32 v239, v239, v239
	v_max_f32_e32 v240, v240, v240
	v_max_f32_e32 v241, v241, v241
	v_med3_f32 v226, v226, s62, v95
	v_med3_f32 v227, v227, s62, v95
	v_med3_f32 v228, v228, s62, v95
	v_med3_f32 v229, v229, s62, v95
	v_med3_f32 v230, v230, s62, v95
	v_med3_f32 v231, v231, s62, v95
	v_med3_f32 v232, v232, s62, v95
	v_med3_f32 v233, v233, s62, v95
	v_med3_f32 v234, v234, s62, v95
	v_med3_f32 v235, v235, s62, v95
	v_med3_f32 v236, v236, s62, v95
	v_med3_f32 v237, v237, s62, v95
	v_med3_f32 v238, v238, s62, v95
	v_med3_f32 v239, v239, s62, v95
	v_med3_f32 v240, v240, s62, v95
	v_med3_f32 v241, v241, s62, v95
	v_mov_b32_e32 v242, 0
	v_mov_b32_e32 v243, 0
	v_mov_b32_e32 v244, 0
	v_mov_b32_e32 v245, 0
	v_cvt_pk_fp8_f32 v242, v226, v227
	v_cvt_pk_fp8_f32 v243, v230, v231
	v_cvt_pk_fp8_f32 v244, v234, v235
	v_cvt_pk_fp8_f32 v245, v238, v239
	v_cvt_pk_fp8_f32 v242, v228, v229 op_sel:[0,0,1]
	v_cvt_pk_fp8_f32 v243, v232, v233 op_sel:[0,0,1]
	v_cvt_pk_fp8_f32 v244, v236, v237 op_sel:[0,0,1]
	v_cvt_pk_fp8_f32 v245, v240, v241 op_sel:[0,0,1]
	s_nop 0
	global_store_dwordx4 v80, v[242:245], s[6:7]
	s_waitcnt vmcnt(12)
	v_mul_f32_e32 v144, 0x43000000, v144
	v_mul_f32_e32 v145, 0x43000000, v145
	v_mul_f32_e32 v146, 0x43000000, v146
	v_mul_f32_e32 v147, 0x43000000, v147
	ds_write_b128 v209, v[144:147]
	v_mul_f32_e32 v148, 0x43000000, v148
	v_mul_f32_e32 v149, 0x43000000, v149
	v_mul_f32_e32 v150, 0x43000000, v150
	v_mul_f32_e32 v151, 0x43000000, v151
	ds_write_b128 v209, v[148:151] offset:1024
	v_mul_f32_e32 v152, 0x43000000, v152
	v_mul_f32_e32 v153, 0x43000000, v153
	v_mul_f32_e32 v154, 0x43000000, v154
	v_mul_f32_e32 v155, 0x43000000, v155
	ds_write_b128 v209, v[152:155] offset:2048
	v_mul_f32_e32 v156, 0x43000000, v156
	v_mul_f32_e32 v157, 0x43000000, v157
	v_mul_f32_e32 v158, 0x43000000, v158
	v_mul_f32_e32 v159, 0x43000000, v159
	ds_write_b128 v209, v[156:159] offset:3072
	v_mul_f32_e32 v160, 0x43000000, v160
	v_mul_f32_e32 v161, 0x43000000, v161
	v_mul_f32_e32 v162, 0x43000000, v162
	v_mul_f32_e32 v163, 0x43000000, v163
	ds_write_b128 v209, v[160:163] offset:4096
	v_mul_f32_e32 v164, 0x43000000, v164
	v_mul_f32_e32 v165, 0x43000000, v165
	v_mul_f32_e32 v166, 0x43000000, v166
	v_mul_f32_e32 v167, 0x43000000, v167
	ds_write_b128 v209, v[164:167] offset:5120
	v_mul_f32_e32 v168, 0x43000000, v168
	v_mul_f32_e32 v169, 0x43000000, v169
	v_mul_f32_e32 v170, 0x43000000, v170
	v_mul_f32_e32 v171, 0x43000000, v171
	ds_write_b128 v209, v[168:171] offset:6144
	v_mul_f32_e32 v172, 0x43000000, v172
	v_mul_f32_e32 v173, 0x43000000, v173
	v_mul_f32_e32 v174, 0x43000000, v174
	v_mul_f32_e32 v175, 0x43000000, v175
	ds_write_b128 v209, v[172:175] offset:7168
	s_waitcnt lgkmcnt(0)
	s_barrier
; #define GAS __attribute__((address_space(1)))
; #define LAS __attribute__((address_space(3)))
; #define LDS_WAIT() asm volatile("s_waitcnt lgkmcnt(0)" ::: "memory")
; __device__ __forceinline__ unsigned pk4_fp8(float a, float b, float c, float d) {
;     a = fminf(fmaxf(a, -448.f), 448.f); b = fminf(fmaxf(b, -448.f), 448.f); c = fminf(fmaxf(c, -448.f), 448.f); d = fminf(fmaxf(d, -448.f), 448.f);
;     int w = __builtin_amdgcn_cvt_pk_fp8_f32(a, b, 0, false); w = __builtin_amdgcn_cvt_pk_fp8_f32(c, d, w, true); return (unsigned)w; }
;     ...
;     for (int i = 0; i < 32; ++i) v[i] = sc >= 0 ? W[(size_t)(k0 + 2 * i + (lane >> 5)) * Nsrc + sc] : 0.f;
; #pragma unroll
;     for (int i = 0; i < 32; ++i) { const int k = k0 + 2 * i + (lane >> 5); float x = v[i] * wscale; if (KS) x *= (k < ksplit ? ksA[k] : ksB[k - ksplit]); scr[(2 * i + (lane >> 5)) * 33 + (lane & 31)] = x; }
;     LDS_WAIT(); asm volatile("" ::: "memory");
;     const int c = lane & 7;
; #pragma unroll
;     for (int j = 0; j < 4; ++j) { const int n = (lane >> 3) + 8 * j; const LAS float* s = scr + (8 * c) * 33 + n;
;         const unsigned long long o = (unsigned long long)pg8::pk4_fp8(s[0 * 33], s[1 * 33], s[2 * 33], s[3 * 33]) | ((unsigned long long)pg8::pk4_fp8(s[4 * 33], s[5 * 33], s[6 * 33], s[7 * 33]) << 32);
;         *(GAS unsigned long long*)(WT + (size_t)(n0 + n) * K + k0 + 8 * c) = o; }
	s_add_u32 s8, s38, 0x8000000
	s_addc_u32 s9, s39, 0
	global_load_dwordx4 v[144:147], v75, s[8:9]
	s_add_u32 s8, s8, 0x8000
	s_addc_u32 s9, s9, 0
	global_load_dwordx4 v[148:151], v75, s[8:9]
	s_add_u32 s8, s8, 0x8000
	s_addc_u32 s9, s9, 0
	global_load_dwordx4 v[152:155], v75, s[8:9]
	s_add_u32 s8, s8, 0x8000
	s_addc_u32 s9, s9, 0
	global_load_dwordx4 v[156:159], v75, s[8:9]
	s_add_u32 s8, s8, 0x8000
	s_addc_u32 s9, s9, 0
	global_load_dwordx4 v[160:163], v75, s[8:9]
	s_add_u32 s8, s8, 0x8000
	s_addc_u32 s9, s9, 0
	global_load_dwordx4 v[164:167], v75, s[8:9]
	s_add_u32 s8, s8, 0x8000
	s_addc_u32 s9, s9, 0
	global_load_dwordx4 v[168:171], v75, s[8:9]
	s_add_u32 s8, s8, 0x8000
	s_addc_u32 s9, s9, 0
	global_load_dwordx4 v[172:175], v75, s[8:9]
	s_add_u32 s6, s40, 0x2001000
	s_addc_u32 s7, s41, 0
	ds_read_b32 v226, v211
	ds_read_b32 v227, v211 offset:512
	ds_read_b32 v228, v211 offset:1024
	ds_read_b32 v229, v211 offset:1536
	ds_read_b32 v230, v211 offset:2048
	ds_read_b32 v231, v211 offset:2560
	ds_read_b32 v232, v211 offset:3072
	ds_read_b32 v233, v211 offset:3584
	ds_read_b32 v234, v211 offset:4096
	ds_read_b32 v235, v211 offset:4608
	ds_read_b32 v236, v211 offset:5120
	ds_read_b32 v237, v211 offset:5632
	ds_read_b32 v238, v211 offset:6144
	ds_read_b32 v239, v211 offset:6656
	ds_read_b32 v240, v211 offset:7168
	ds_read_b32 v241, v211 offset:7680
	s_waitcnt lgkmcnt(0)
	v_max_f32_e32 v226, v226, v226
	v_max_f32_e32 v227, v227, v227
	v_max_f32_e32 v228, v228, v228
	v_max_f32_e32 v229, v229, v229
	v_max_f32_e32 v230, v230, v230
	v_max_f32_e32 v231, v231, v231
	v_max_f32_e32 v232, v232, v232
	v_max_f32_e32 v233, v233, v233
	v_max_f32_e32 v234, v234, v234
	v_max_f32_e32 v235, v235, v235
	v_max_f32_e32 v236, v236, v236
	v_max_f32_e32 v237, v237, v237
	v_max_f32_e32 v238, v238, v238
	v_max_f32_e32 v239, v239, v239
	v_max_f32_e32 v240, v240, v240
	v_max_f32_e32 v241, v241, v241
	v_med3_f32 v226, v226, s62, v95
	v_med3_f32 v227, v227, s62, v95
	v_med3_f32 v228, v228, s62, v95
	v_med3_f32 v229, v229, s62, v95
	v_med3_f32 v230, v230, s62, v95
	v_med3_f32 v231, v231, s62, v95
	v_med3_f32 v232, v232, s62, v95
	v_med3_f32 v233, v233, s62, v95
	v_med3_f32 v234, v234, s62, v95
	v_med3_f32 v235, v235, s62, v95
	v_med3_f32 v236, v236, s62, v95
	v_med3_f32 v237, v237, s62, v95
	v_med3_f32 v238, v238, s62, v95
	v_med3_f32 v239, v239, s62, v95
	v_med3_f32 v240, v240, s62, v95
	v_med3_f32 v241, v241, s62, v95
	v_mov_b32_e32 v242, 0
	v_mov_b32_e32 v243, 0
	v_mov_b32_e32 v244, 0
	v_mov_b32_e32 v245, 0
	v_cvt_pk_fp8_f32 v242, v226, v227
	v_cvt_pk_fp8_f32 v243, v230, v231
	v_cvt_pk_fp8_f32 v244, v234, v235
	v_cvt_pk_fp8_f32 v245, v238, v239
	v_cvt_pk_fp8_f32 v242, v228, v229 op_sel:[0,0,1]
	v_cvt_pk_fp8_f32 v243, v232, v233 op_sel:[0,0,1]
	v_cvt_pk_fp8_f32 v244, v236, v237 op_sel:[0,0,1]
	v_cvt_pk_fp8_f32 v245, v240, v241 op_sel:[0,0,1]
	s_nop 0
	global_store_dwordx4 v79, v[242:245], s[6:7]
	ds_read_b32 v226, v213
	ds_read_b32 v227, v213 offset:512
	ds_read_b32 v228, v213 offset:1024
	ds_read_b32 v229, v213 offset:1536
	ds_read_b32 v230, v213 offset:2048
	ds_read_b32 v231, v213 offset:2560
	ds_read_b32 v232, v213 offset:3072
	ds_read_b32 v233, v213 offset:3584
	ds_read_b32 v234, v213 offset:4096
	ds_read_b32 v235, v213 offset:4608
	ds_read_b32 v236, v213 offset:5120
	ds_read_b32 v237, v213 offset:5632
	ds_read_b32 v238, v213 offset:6144
	ds_read_b32 v239, v213 offset:6656
	ds_read_b32 v240, v213 offset:7168
	ds_read_b32 v241, v213 offset:7680
	s_waitcnt lgkmcnt(0)
	v_max_f32_e32 v226, v226, v226
	v_max_f32_e32 v227, v227, v227
	v_max_f32_e32 v228, v228, v228
	v_max_f32_e32 v229, v229, v229
	v_max_f32_e32 v230, v230, v230
	v_max_f32_e32 v231, v231, v231
	v_max_f32_e32 v232, v232, v232
	v_max_f32_e32 v233, v233, v233
	v_max_f32_e32 v234, v234, v234
	v_max_f32_e32 v235, v235, v235
	v_max_f32_e32 v236, v236, v236
	v_max_f32_e32 v237, v237, v237
	v_max_f32_e32 v238, v238, v238
	v_max_f32_e32 v239, v239, v239
	v_max_f32_e32 v240, v240, v240
	v_max_f32_e32 v241, v241, v241
	v_med3_f32 v226, v226, s62, v95
	v_med3_f32 v227, v227, s62, v95
	v_med3_f32 v228, v228, s62, v95
	v_med3_f32 v229, v229, s62, v95
	v_med3_f32 v230, v230, s62, v95
	v_med3_f32 v231, v231, s62, v95
	v_med3_f32 v232, v232, s62, v95
	v_med3_f32 v233, v233, s62, v95
	v_med3_f32 v234, v234, s62, v95
	v_med3_f32 v235, v235, s62, v95
	v_med3_f32 v236, v236, s62, v95
	v_med3_f32 v237, v237, s62, v95
	v_med3_f32 v238, v238, s62, v95
	v_med3_f32 v239, v239, s62, v95
	v_med3_f32 v240, v240, s62, v95
	v_med3_f32 v241, v241, s62, v95
	v_mov_b32_e32 v242, 0
	v_mov_b32_e32 v243, 0
	v_mov_b32_e32 v244, 0
	v_mov_b32_e32 v245, 0
	v_cvt_pk_fp8_f32 v242, v226, v227
	v_cvt_pk_fp8_f32 v243, v230, v231
	v_cvt_pk_fp8_f32 v244, v234, v235
	v_cvt_pk_fp8_f32 v245, v238, v239
	v_cvt_pk_fp8_f32 v242, v228, v229 op_sel:[0,0,1]
	v_cvt_pk_fp8_f32 v243, v232, v233 op_sel:[0,0,1]
	v_cvt_pk_fp8_f32 v244, v236, v237 op_sel:[0,0,1]
	v_cvt_pk_fp8_f32 v245, v240, v241 op_sel:[0,0,1]
	s_nop 0
	global_store_dwordx4 v80, v[242:245], s[6:7]
	s_waitcnt vmcnt(12)
	v_mul_f32_e32 v176, 0x43000000, v176
	v_mul_f32_e32 v177, 0x43000000, v177
	v_mul_f32_e32 v178, 0x43000000, v178
	v_mul_f32_e32 v179, 0x43000000, v179
	ds_write_b128 v210, v[176:179]
	v_mul_f32_e32 v180, 0x43000000, v180
	v_mul_f32_e32 v181, 0x43000000, v181
	v_mul_f32_e32 v182, 0x43000000, v182
	v_mul_f32_e32 v183, 0x43000000, v183
	ds_write_b128 v210, v[180:183] offset:1024
	v_mul_f32_e32 v184, 0x43000000, v184
	v_mul_f32_e32 v185, 0x43000000, v185
	v_mul_f32_e32 v186, 0x43000000, v186
	v_mul_f32_e32 v187, 0x43000000, v187
	ds_write_b128 v210, v[184:187] offset:2048
	v_mul_f32_e32 v188, 0x43000000, v188
	v_mul_f32_e32 v189, 0x43000000, v189
	v_mul_f32_e32 v190, 0x43000000, v190
	v_mul_f32_e32 v191, 0x43000000, v191
	ds_write_b128 v210, v[188:191] offset:3072
	v_mul_f32_e32 v192, 0x43000000, v192
	v_mul_f32_e32 v193, 0x43000000, v193
	v_mul_f32_e32 v194, 0x43000000, v194
	v_mul_f32_e32 v195, 0x43000000, v195
	ds_write_b128 v210, v[192:195] offset:4096
	v_mul_f32_e32 v196, 0x43000000, v196
	v_mul_f32_e32 v197, 0x43000000, v197
	v_mul_f32_e32 v198, 0x43000000, v198
	v_mul_f32_e32 v199, 0x43000000, v199
	ds_write_b128 v210, v[196:199] offset:5120
	v_mul_f32_e32 v200, 0x43000000, v200
	v_mul_f32_e32 v201, 0x43000000, v201
	v_mul_f32_e32 v202, 0x43000000, v202
	v_mul_f32_e32 v203, 0x43000000, v203
	ds_write_b128 v210, v[200:203] offset:6144
	v_mul_f32_e32 v204, 0x43000000, v204
	v_mul_f32_e32 v205, 0x43000000, v205
	v_mul_f32_e32 v206, 0x43000000, v206
	v_mul_f32_e32 v207, 0x43000000, v207
	ds_write_b128 v210, v[204:207] offset:7168
	s_waitcnt lgkmcnt(0)
	s_barrier
; #define GAS __attribute__((address_space(1)))
; #define LAS __attribute__((address_space(3)))
; #define LDS_WAIT() asm volatile("s_waitcnt lgkmcnt(0)" ::: "memory")
; __device__ __forceinline__ unsigned pk4_fp8(float a, float b, float c, float d) {
;     a = fminf(fmaxf(a, -448.f), 448.f); b = fminf(fmaxf(b, -448.f), 448.f); c = fminf(fmaxf(c, -448.f), 448.f); d = fminf(fmaxf(d, -448.f), 448.f);
;     int w = __builtin_amdgcn_cvt_pk_fp8_f32(a, b, 0, false); w = __builtin_amdgcn_cvt_pk_fp8_f32(c, d, w, true); return (unsigned)w; }
;     ...
;     for (int i = 0; i < 32; ++i) v[i] = sc >= 0 ? W[(size_t)(k0 + 2 * i + (lane >> 5)) * Nsrc + sc] : 0.f;
; #pragma unroll
;     for (int i = 0; i < 32; ++i) { const int k = k0 + 2 * i + (lane >> 5); float x = v[i] * wscale; if (KS) x *= (k < ksplit ? ksA[k] : ksB[k - ksplit]); scr[(2 * i + (lane >> 5)) * 33 + (lane & 31)] = x; }
;     LDS_WAIT(); asm volatile("" ::: "memory");
;     const int c = lane & 7;
; #pragma unroll
;     for (int j = 0; j < 4; ++j) { const int n = (lane >> 3) + 8 * j; const LAS float* s = scr + (8 * c) * 33 + n;
;         const unsigned long long o = (unsigned long long)pg8::pk4_fp8(s[0 * 33], s[1 * 33], s[2 * 33], s[3 * 33]) | ((unsigned long long)pg8::pk4_fp8(s[4 * 33], s[5 * 33], s[6 * 33], s[7 * 33]) << 32);
;         *(GAS unsigned long long*)(WT + (size_t)(n0 + n) * K + k0 + 8 * c) = o; }
	s_add_u32 s8, s38, 0x8001000
	s_addc_u32 s9, s39, 0
	global_load_dwordx4 v[176:179], v75, s[8:9]
	s_add_u32 s8, s8, 0x8000
	s_addc_u32 s9, s9, 0
	global_load_dwordx4 v[180:183], v75, s[8:9]
	s_add_u32 s8, s8, 0x8000
	s_addc_u32 s9, s9, 0
	global_load_dwordx4 v[184:187], v75, s[8:9]
	s_add_u32 s8, s8, 0x8000
	s_addc_u32 s9, s9, 0
	global_load_dwordx4 v[188:191], v75, s[8:9]
	s_add_u32 s8, s8, 0x8000
	s_addc_u32 s9, s9, 0
	global_load_dwordx4 v[192:195], v75, s[8:9]
	s_add_u32 s8, s8, 0x8000
	s_addc_u32 s9, s9, 0
	global_load_dwordx4 v[196:199], v75, s[8:9]
	s_add_u32 s8, s8, 0x8000
	s_addc_u32 s9, s9, 0
	global_load_dwordx4 v[200:203], v75, s[8:9]
	s_add_u32 s8, s8, 0x8000
	s_addc_u32 s9, s9, 0
	global_load_dwordx4 v[204:207], v75, s[8:9]
	s_add_u32 s6, s40, 0x3001000
	s_addc_u32 s7, s41, 0
	ds_read_b32 v226, v212
	ds_read_b32 v227, v212 offset:512
	ds_read_b32 v228, v212 offset:1024
	ds_read_b32 v229, v212 offset:1536
	ds_read_b32 v230, v212 offset:2048
	ds_read_b32 v231, v212 offset:2560
	ds_read_b32 v232, v212 offset:3072
	ds_read_b32 v233, v212 offset:3584
	ds_read_b32 v234, v212 offset:4096
	ds_read_b32 v235, v212 offset:4608
	ds_read_b32 v236, v212 offset:5120
	ds_read_b32 v237, v212 offset:5632
	ds_read_b32 v238, v212 offset:6144
	ds_read_b32 v239, v212 offset:6656
	ds_read_b32 v240, v212 offset:7168
	ds_read_b32 v241, v212 offset:7680
	s_waitcnt lgkmcnt(0)
	v_max_f32_e32 v226, v226, v226
	v_max_f32_e32 v227, v227, v227
	v_max_f32_e32 v228, v228, v228
	v_max_f32_e32 v229, v229, v229
	v_max_f32_e32 v230, v230, v230
	v_max_f32_e32 v231, v231, v231
	v_max_f32_e32 v232, v232, v232
	v_max_f32_e32 v233, v233, v233
	v_max_f32_e32 v234, v234, v234
	v_max_f32_e32 v235, v235, v235
	v_max_f32_e32 v236, v236, v236
	v_max_f32_e32 v237, v237, v237
	v_max_f32_e32 v238, v238, v238
	v_max_f32_e32 v239, v239, v239
	v_max_f32_e32 v240, v240, v240
	v_max_f32_e32 v241, v241, v241
	v_med3_f32 v226, v226, s62, v95
	v_med3_f32 v227, v227, s62, v95
	v_med3_f32 v228, v228, s62, v95
	v_med3_f32 v229, v229, s62, v95
	v_med3_f32 v230, v230, s62, v95
	v_med3_f32 v231, v231, s62, v95
	v_med3_f32 v232, v232, s62, v95
	v_med3_f32 v233, v233, s62, v95
	v_med3_f32 v234, v234, s62, v95
	v_med3_f32 v235, v235, s62, v95
	v_med3_f32 v236, v236, s62, v95
	v_med3_f32 v237, v237, s62, v95
	v_med3_f32 v238, v238, s62, v95
	v_med3_f32 v239, v239, s62, v95
	v_med3_f32 v240, v240, s62, v95
	v_med3_f32 v241, v241, s62, v95
	v_mov_b32_e32 v242, 0
	v_mov_b32_e32 v243, 0
	v_mov_b32_e32 v244, 0
	v_mov_b32_e32 v245, 0
	v_cvt_pk_fp8_f32 v242, v226, v227
	v_cvt_pk_fp8_f32 v243, v230, v231
	v_cvt_pk_fp8_f32 v244, v234, v235
	v_cvt_pk_fp8_f32 v245, v238, v239
	v_cvt_pk_fp8_f32 v242, v228, v229 op_sel:[0,0,1]
	v_cvt_pk_fp8_f32 v243, v232, v233 op_sel:[0,0,1]
	v_cvt_pk_fp8_f32 v244, v236, v237 op_sel:[0,0,1]
	v_cvt_pk_fp8_f32 v245, v240, v241 op_sel:[0,0,1]
	s_nop 0
	global_store_dwordx4 v79, v[242:245], s[6:7]
	ds_read_b32 v226, v214
	ds_read_b32 v227, v214 offset:512
	ds_read_b32 v228, v214 offset:1024
	ds_read_b32 v229, v214 offset:1536
	ds_read_b32 v230, v214 offset:2048
	ds_read_b32 v231, v214 offset:2560
	ds_read_b32 v232, v214 offset:3072
	ds_read_b32 v233, v214 offset:3584
	ds_read_b32 v234, v214 offset:4096
	ds_read_b32 v235, v214 offset:4608
	ds_read_b32 v236, v214 offset:5120
	ds_read_b32 v237, v214 offset:5632
	ds_read_b32 v238, v214 offset:6144
	ds_read_b32 v239, v214 offset:6656
	ds_read_b32 v240, v214 offset:7168
	ds_read_b32 v241, v214 offset:7680
	s_waitcnt lgkmcnt(0)
	v_max_f32_e32 v226, v226, v226
	v_max_f32_e32 v227, v227, v227
	v_max_f32_e32 v228, v228, v228
	v_max_f32_e32 v229, v229, v229
	v_max_f32_e32 v230, v230, v230
	v_max_f32_e32 v231, v231, v231
	v_max_f32_e32 v232, v232, v232
	v_max_f32_e32 v233, v233, v233
	v_max_f32_e32 v234, v234, v234
	v_max_f32_e32 v235, v235, v235
	v_max_f32_e32 v236, v236, v236
	v_max_f32_e32 v237, v237, v237
	v_max_f32_e32 v238, v238, v238
	v_max_f32_e32 v239, v239, v239
	v_max_f32_e32 v240, v240, v240
	v_max_f32_e32 v241, v241, v241
	v_med3_f32 v226, v226, s62, v95
	v_med3_f32 v227, v227, s62, v95
	v_med3_f32 v228, v228, s62, v95
	v_med3_f32 v229, v229, s62, v95
	v_med3_f32 v230, v230, s62, v95
	v_med3_f32 v231, v231, s62, v95
	v_med3_f32 v232, v232, s62, v95
	v_med3_f32 v233, v233, s62, v95
	v_med3_f32 v234, v234, s62, v95
	v_med3_f32 v235, v235, s62, v95
	v_med3_f32 v236, v236, s62, v95
	v_med3_f32 v237, v237, s62, v95
	v_med3_f32 v238, v238, s62, v95
	v_med3_f32 v239, v239, s62, v95
	v_med3_f32 v240, v240, s62, v95
	v_med3_f32 v241, v241, s62, v95
	v_mov_b32_e32 v242, 0
	v_mov_b32_e32 v243, 0
	v_mov_b32_e32 v244, 0
	v_mov_b32_e32 v245, 0
	v_cvt_pk_fp8_f32 v242, v226, v227
	v_cvt_pk_fp8_f32 v243, v230, v231
	v_cvt_pk_fp8_f32 v244, v234, v235
	v_cvt_pk_fp8_f32 v245, v238, v239
	v_cvt_pk_fp8_f32 v242, v228, v229 op_sel:[0,0,1]
	v_cvt_pk_fp8_f32 v243, v232, v233 op_sel:[0,0,1]
	v_cvt_pk_fp8_f32 v244, v236, v237 op_sel:[0,0,1]
	v_cvt_pk_fp8_f32 v245, v240, v241 op_sel:[0,0,1]
	s_nop 0
	global_store_dwordx4 v80, v[242:245], s[6:7]
	s_waitcnt vmcnt(12)
	v_mul_f32_e32 v144, 0x43000000, v144
	v_mul_f32_e32 v145, 0x43000000, v145
	v_mul_f32_e32 v146, 0x43000000, v146
	v_mul_f32_e32 v147, 0x43000000, v147
	ds_write_b128 v209, v[144:147]
	v_mul_f32_e32 v148, 0x43000000, v148
	v_mul_f32_e32 v149, 0x43000000, v149
	v_mul_f32_e32 v150, 0x43000000, v150
	v_mul_f32_e32 v151, 0x43000000, v151
	ds_write_b128 v209, v[148:151] offset:1024
	v_mul_f32_e32 v152, 0x43000000, v152
	v_mul_f32_e32 v153, 0x43000000, v153
	v_mul_f32_e32 v154, 0x43000000, v154
	v_mul_f32_e32 v155, 0x43000000, v155
	ds_write_b128 v209, v[152:155] offset:2048
	v_mul_f32_e32 v156, 0x43000000, v156
	v_mul_f32_e32 v157, 0x43000000, v157
	v_mul_f32_e32 v158, 0x43000000, v158
	v_mul_f32_e32 v159, 0x43000000, v159
	ds_write_b128 v209, v[156:159] offset:3072
	v_mul_f32_e32 v160, 0x43000000, v160
	v_mul_f32_e32 v161, 0x43000000, v161
	v_mul_f32_e32 v162, 0x43000000, v162
	v_mul_f32_e32 v163, 0x43000000, v163
	ds_write_b128 v209, v[160:163] offset:4096
	v_mul_f32_e32 v164, 0x43000000, v164
	v_mul_f32_e32 v165, 0x43000000, v165
	v_mul_f32_e32 v166, 0x43000000, v166
	v_mul_f32_e32 v167, 0x43000000, v167
	ds_write_b128 v209, v[164:167] offset:5120
	v_mul_f32_e32 v168, 0x43000000, v168
	v_mul_f32_e32 v169, 0x43000000, v169
	v_mul_f32_e32 v170, 0x43000000, v170
	v_mul_f32_e32 v171, 0x43000000, v171
	ds_write_b128 v209, v[168:171] offset:6144
	v_mul_f32_e32 v172, 0x43000000, v172
	v_mul_f32_e32 v173, 0x43000000, v173
	v_mul_f32_e32 v174, 0x43000000, v174
	v_mul_f32_e32 v175, 0x43000000, v175
	ds_write_b128 v209, v[172:175] offset:7168
	s_waitcnt lgkmcnt(0)
	s_barrier
; #define GAS __attribute__((address_space(1)))
; #define LAS __attribute__((address_space(3)))
; #define LDS_WAIT() asm volatile("s_waitcnt lgkmcnt(0)" ::: "memory")
; __device__ __forceinline__ unsigned pk4_fp8(float a, float b, float c, float d) {
;     a = fminf(fmaxf(a, -448.f), 448.f); b = fminf(fmaxf(b, -448.f), 448.f); c = fminf(fmaxf(c, -448.f), 448.f); d = fminf(fmaxf(d, -448.f), 448.f);
;     int w = __builtin_amdgcn_cvt_pk_fp8_f32(a, b, 0, false); w = __builtin_amdgcn_cvt_pk_fp8_f32(c, d, w, true); return (unsigned)w; }
;     ...
;     for (int i = 0; i < 32; ++i) v[i] = sc >= 0 ? W[(size_t)(k0 + 2 * i + (lane >> 5)) * Nsrc + sc] : 0.f;
; #pragma unroll
;     for (int i = 0; i < 32; ++i) { const int k = k0 + 2 * i + (lane >> 5); float x = v[i] * wscale; if (KS) x *= (k < ksplit ? ksA[k] : ksB[k - ksplit]); scr[(2 * i + (lane >> 5)) * 33 + (lane & 31)] = x; }
;     LDS_WAIT(); asm volatile("" ::: "memory");
;     const int c = lane & 7;
; #pragma unroll
;     for (int j = 0; j < 4; ++j) { const int n = (lane >> 3) + 8 * j; const LAS float* s = scr + (8 * c) * 33 + n;
;         const unsigned long long o = (unsigned long long)pg8::pk4_fp8(s[0 * 33], s[1 * 33], s[2 * 33], s[3 * 33]) | ((unsigned long long)pg8::pk4_fp8(s[4 * 33], s[5 * 33], s[6 * 33], s[7 * 33]) << 32);
;         *(GAS unsigned long long*)(WT + (size_t)(n0 + n) * K + k0 + 8 * c) = o; }
	s_add_u32 s8, s38, 0x8002000
	s_addc_u32 s9, s39, 0
	global_load_dwordx4 v[144:147], v75, s[8:9]
	s_add_u32 s8, s8, 0x8000
	s_addc_u32 s9, s9, 0
	global_load_dwordx4 v[148:151], v75, s[8:9]
	s_add_u32 s8, s8, 0x8000
	s_addc_u32 s9, s9, 0
	global_load_dwordx4 v[152:155], v75, s[8:9]
	s_add_u32 s8, s8, 0x8000
	s_addc_u32 s9, s9, 0
	global_load_dwordx4 v[156:159], v75, s[8:9]
	s_add_u32 s8, s8, 0x8000
	s_addc_u32 s9, s9, 0
	global_load_dwordx4 v[160:163], v75, s[8:9]
	s_add_u32 s8, s8, 0x8000
	s_addc_u32 s9, s9, 0
	global_load_dwordx4 v[164:167], v75, s[8:9]
	s_add_u32 s8, s8, 0x8000
	s_addc_u32 s9, s9, 0
	global_load_dwordx4 v[168:171], v75, s[8:9]
	s_add_u32 s8, s8, 0x8000
	s_addc_u32 s9, s9, 0
	global_load_dwordx4 v[172:175], v75, s[8:9]
	s_add_u32 s6, s40, 0x2000
	s_addc_u32 s7, s41, 0
	ds_read_b32 v226, v211
	ds_read_b32 v227, v211 offset:512
	ds_read_b32 v228, v211 offset:1024
	ds_read_b32 v229, v211 offset:1536
	ds_read_b32 v230, v211 offset:2048
	ds_read_b32 v231, v211 offset:2560
	ds_read_b32 v232, v211 offset:3072
	ds_read_b32 v233, v211 offset:3584
	ds_read_b32 v234, v211 offset:4096
	ds_read_b32 v235, v211 offset:4608
	ds_read_b32 v236, v211 offset:5120
	ds_read_b32 v237, v211 offset:5632
	ds_read_b32 v238, v211 offset:6144
	ds_read_b32 v239, v211 offset:6656
	ds_read_b32 v240, v211 offset:7168
	ds_read_b32 v241, v211 offset:7680
	s_waitcnt lgkmcnt(0)
	v_max_f32_e32 v226, v226, v226
	v_max_f32_e32 v227, v227, v227
	v_max_f32_e32 v228, v228, v228
	v_max_f32_e32 v229, v229, v229
	v_max_f32_e32 v230, v230, v230
	v_max_f32_e32 v231, v231, v231
	v_max_f32_e32 v232, v232, v232
	v_max_f32_e32 v233, v233, v233
	v_max_f32_e32 v234, v234, v234
	v_max_f32_e32 v235, v235, v235
	v_max_f32_e32 v236, v236, v236
	v_max_f32_e32 v237, v237, v237
	v_max_f32_e32 v238, v238, v238
	v_max_f32_e32 v239, v239, v239
	v_max_f32_e32 v240, v240, v240
	v_max_f32_e32 v241, v241, v241
	v_med3_f32 v226, v226, s62, v95
	v_med3_f32 v227, v227, s62, v95
	v_med3_f32 v228, v228, s62, v95
	v_med3_f32 v229, v229, s62, v95
	v_med3_f32 v230, v230, s62, v95
	v_med3_f32 v231, v231, s62, v95
	v_med3_f32 v232, v232, s62, v95
	v_med3_f32 v233, v233, s62, v95
	v_med3_f32 v234, v234, s62, v95
	v_med3_f32 v235, v235, s62, v95
	v_med3_f32 v236, v236, s62, v95
	v_med3_f32 v237, v237, s62, v95
	v_med3_f32 v238, v238, s62, v95
	v_med3_f32 v239, v239, s62, v95
	v_med3_f32 v240, v240, s62, v95
	v_med3_f32 v241, v241, s62, v95
	v_mov_b32_e32 v242, 0
	v_mov_b32_e32 v243, 0
	v_mov_b32_e32 v244, 0
	v_mov_b32_e32 v245, 0
	v_cvt_pk_fp8_f32 v242, v226, v227
	v_cvt_pk_fp8_f32 v243, v230, v231
	v_cvt_pk_fp8_f32 v244, v234, v235
	v_cvt_pk_fp8_f32 v245, v238, v239
	v_cvt_pk_fp8_f32 v242, v228, v229 op_sel:[0,0,1]
	v_cvt_pk_fp8_f32 v243, v232, v233 op_sel:[0,0,1]
	v_cvt_pk_fp8_f32 v244, v236, v237 op_sel:[0,0,1]
	v_cvt_pk_fp8_f32 v245, v240, v241 op_sel:[0,0,1]
	s_nop 0
	global_store_dwordx4 v79, v[242:245], s[6:7]
	ds_read_b32 v226, v213
	ds_read_b32 v227, v213 offset:512
	ds_read_b32 v228, v213 offset:1024
	ds_read_b32 v229, v213 offset:1536
	ds_read_b32 v230, v213 offset:2048
	ds_read_b32 v231, v213 offset:2560
	ds_read_b32 v232, v213 offset:3072
	ds_read_b32 v233, v213 offset:3584
	ds_read_b32 v234, v213 offset:4096
	ds_read_b32 v235, v213 offset:4608
	ds_read_b32 v236, v213 offset:5120
	ds_read_b32 v237, v213 offset:5632
	ds_read_b32 v238, v213 offset:6144
	ds_read_b32 v239, v213 offset:6656
	ds_read_b32 v240, v213 offset:7168
	ds_read_b32 v241, v213 offset:7680
	s_waitcnt lgkmcnt(0)
	v_max_f32_e32 v226, v226, v226
	v_max_f32_e32 v227, v227, v227
	v_max_f32_e32 v228, v228, v228
	v_max_f32_e32 v229, v229, v229
	v_max_f32_e32 v230, v230, v230
	v_max_f32_e32 v231, v231, v231
	v_max_f32_e32 v232, v232, v232
	v_max_f32_e32 v233, v233, v233
	v_max_f32_e32 v234, v234, v234
	v_max_f32_e32 v235, v235, v235
	v_max_f32_e32 v236, v236, v236
	v_max_f32_e32 v237, v237, v237
	v_max_f32_e32 v238, v238, v238
	v_max_f32_e32 v239, v239, v239
	v_max_f32_e32 v240, v240, v240
	v_max_f32_e32 v241, v241, v241
	v_med3_f32 v226, v226, s62, v95
	v_med3_f32 v227, v227, s62, v95
	v_med3_f32 v228, v228, s62, v95
	v_med3_f32 v229, v229, s62, v95
	v_med3_f32 v230, v230, s62, v95
	v_med3_f32 v231, v231, s62, v95
	v_med3_f32 v232, v232, s62, v95
	v_med3_f32 v233, v233, s62, v95
	v_med3_f32 v234, v234, s62, v95
	v_med3_f32 v235, v235, s62, v95
	v_med3_f32 v236, v236, s62, v95
	v_med3_f32 v237, v237, s62, v95
	v_med3_f32 v238, v238, s62, v95
	v_med3_f32 v239, v239, s62, v95
	v_med3_f32 v240, v240, s62, v95
	v_med3_f32 v241, v241, s62, v95
	v_mov_b32_e32 v242, 0
	v_mov_b32_e32 v243, 0
	v_mov_b32_e32 v244, 0
	v_mov_b32_e32 v245, 0
	v_cvt_pk_fp8_f32 v242, v226, v227
	v_cvt_pk_fp8_f32 v243, v230, v231
	v_cvt_pk_fp8_f32 v244, v234, v235
	v_cvt_pk_fp8_f32 v245, v238, v239
	v_cvt_pk_fp8_f32 v242, v228, v229 op_sel:[0,0,1]
	v_cvt_pk_fp8_f32 v243, v232, v233 op_sel:[0,0,1]
	v_cvt_pk_fp8_f32 v244, v236, v237 op_sel:[0,0,1]
	v_cvt_pk_fp8_f32 v245, v240, v241 op_sel:[0,0,1]
	s_nop 0
	global_store_dwordx4 v80, v[242:245], s[6:7]
	s_branch .Lco3_hop_skip

; #define GAS __attribute__((address_space(1)))
; #define LAS __attribute__((address_space(3)))
; #define LDS_WAIT() asm volatile("s_waitcnt lgkmcnt(0)" ::: "memory")
; __device__ __forceinline__ unsigned pk4_fp8(float a, float b, float c, float d) {
;     a = fminf(fmaxf(a, -448.f), 448.f); b = fminf(fmaxf(b, -448.f), 448.f); c = fminf(fmaxf(c, -448.f), 448.f); d = fminf(fmaxf(d, -448.f), 448.f);
;     int w = __builtin_amdgcn_cvt_pk_fp8_f32(a, b, 0, false); w = __builtin_amdgcn_cvt_pk_fp8_f32(c, d, w, true); return (unsigned)w; }
;     ...
;     for (int i = 0; i < 32; ++i) v[i] = sc >= 0 ? W[(size_t)(k0 + 2 * i + (lane >> 5)) * Nsrc + sc] : 0.f;
; #pragma unroll
;     for (int i = 0; i < 32; ++i) { const int k = k0 + 2 * i + (lane >> 5); float x = v[i] * wscale; if (KS) x *= (k < ksplit ? ksA[k] : ksB[k - ksplit]); scr[(2 * i + (lane >> 5)) * 33 + (lane & 31)] = x; }
;     LDS_WAIT(); asm volatile("" ::: "memory");
;     const int c = lane & 7;
; #pragma unroll
;     for (int j = 0; j < 4; ++j) { const int n = (lane >> 3) + 8 * j; const LAS float* s = scr + (8 * c) * 33 + n;
;         const unsigned long long o = (unsigned long long)pg8::pk4_fp8(s[0 * 33], s[1 * 33], s[2 * 33], s[3 * 33]) | ((unsigned long long)pg8::pk4_fp8(s[4 * 33], s[5 * 33], s[6 * 33], s[7 * 33]) << 32);
;         *(GAS unsigned long long*)(WT + (size_t)(n0 + n) * K + k0 + 8 * c) = o; }
.Lco3_hop_skip:
	s_waitcnt vmcnt(12)
	v_mul_f32_e32 v176, 0x43000000, v176
	v_mul_f32_e32 v177, 0x43000000, v177
	v_mul_f32_e32 v178, 0x43000000, v178
	v_mul_f32_e32 v179, 0x43000000, v179
	ds_write_b128 v210, v[176:179]
	v_mul_f32_e32 v180, 0x43000000, v180
	v_mul_f32_e32 v181, 0x43000000, v181
	v_mul_f32_e32 v182, 0x43000000, v182
	v_mul_f32_e32 v183, 0x43000000, v183
	ds_write_b128 v210, v[180:183] offset:1024
	v_mul_f32_e32 v184, 0x43000000, v184
	v_mul_f32_e32 v185, 0x43000000, v185
	v_mul_f32_e32 v186, 0x43000000, v186
	v_mul_f32_e32 v187, 0x43000000, v187
	ds_write_b128 v210, v[184:187] offset:2048
	v_mul_f32_e32 v188, 0x43000000, v188
	v_mul_f32_e32 v189, 0x43000000, v189
	v_mul_f32_e32 v190, 0x43000000, v190
	v_mul_f32_e32 v191, 0x43000000, v191
	ds_write_b128 v210, v[188:191] offset:3072
	v_mul_f32_e32 v192, 0x43000000, v192
	v_mul_f32_e32 v193, 0x43000000, v193
	v_mul_f32_e32 v194, 0x43000000, v194
	v_mul_f32_e32 v195, 0x43000000, v195
	ds_write_b128 v210, v[192:195] offset:4096
	v_mul_f32_e32 v196, 0x43000000, v196
	v_mul_f32_e32 v197, 0x43000000, v197
	v_mul_f32_e32 v198, 0x43000000, v198
	v_mul_f32_e32 v199, 0x43000000, v199
	ds_write_b128 v210, v[196:199] offset:5120
	v_mul_f32_e32 v200, 0x43000000, v200
	v_mul_f32_e32 v201, 0x43000000, v201
	v_mul_f32_e32 v202, 0x43000000, v202
	v_mul_f32_e32 v203, 0x43000000, v203
	ds_write_b128 v210, v[200:203] offset:6144
	v_mul_f32_e32 v204, 0x43000000, v204
	v_mul_f32_e32 v205, 0x43000000, v205
	v_mul_f32_e32 v206, 0x43000000, v206
	v_mul_f32_e32 v207, 0x43000000, v207
	ds_write_b128 v210, v[204:207] offset:7168
	s_waitcnt lgkmcnt(0)
	s_barrier
	s_add_u32 s8, s38, 0x8003000
	s_addc_u32 s9, s39, 0
	global_load_dwordx4 v[176:179], v75, s[8:9]
	s_add_u32 s8, s8, 0x8000
	s_addc_u32 s9, s9, 0
	global_load_dwordx4 v[180:183], v75, s[8:9]
	s_add_u32 s8, s8, 0x8000
	s_addc_u32 s9, s9, 0
	global_load_dwordx4 v[184:187], v75, s[8:9]
	s_add_u32 s8, s8, 0x8000
	s_addc_u32 s9, s9, 0
	global_load_dwordx4 v[188:191], v75, s[8:9]
	s_add_u32 s8, s8, 0x8000
	s_addc_u32 s9, s9, 0
	global_load_dwordx4 v[192:195], v75, s[8:9]
	s_add_u32 s8, s8, 0x8000
	s_addc_u32 s9, s9, 0
	global_load_dwordx4 v[196:199], v75, s[8:9]
	s_add_u32 s8, s8, 0x8000
	s_addc_u32 s9, s9, 0
	global_load_dwordx4 v[200:203], v75, s[8:9]
	s_add_u32 s8, s8, 0x8000
	s_addc_u32 s9, s9, 0
	global_load_dwordx4 v[204:207], v75, s[8:9]
	s_add_u32 s6, s40, 0x1002000
	s_addc_u32 s7, s41, 0
	ds_read_b32 v226, v212
	ds_read_b32 v227, v212 offset:512
	ds_read_b32 v228, v212 offset:1024
	ds_read_b32 v229, v212 offset:1536
	ds_read_b32 v230, v212 offset:2048
	ds_read_b32 v231, v212 offset:2560
	ds_read_b32 v232, v212 offset:3072
	ds_read_b32 v233, v212 offset:3584
	ds_read_b32 v234, v212 offset:4096
	ds_read_b32 v235, v212 offset:4608
	ds_read_b32 v236, v212 offset:5120
	ds_read_b32 v237, v212 offset:5632
	ds_read_b32 v238, v212 offset:6144
	ds_read_b32 v239, v212 offset:6656
	ds_read_b32 v240, v212 offset:7168
	ds_read_b32 v241, v212 offset:7680
	s_waitcnt lgkmcnt(0)
	v_max_f32_e32 v226, v226, v226
	v_max_f32_e32 v227, v227, v227
	v_max_f32_e32 v228, v228, v228
	v_max_f32_e32 v229, v229, v229
	v_max_f32_e32 v230, v230, v230
	v_max_f32_e32 v231, v231, v231
	v_max_f32_e32 v232, v232, v232
	v_max_f32_e32 v233, v233, v233
	v_max_f32_e32 v234, v234, v234
	v_max_f32_e32 v235, v235, v235
	v_max_f32_e32 v236, v236, v236
	v_max_f32_e32 v237, v237, v237
	v_max_f32_e32 v238, v238, v238
	v_max_f32_e32 v239, v239, v239
	v_max_f32_e32 v240, v240, v240
	v_max_f32_e32 v241, v241, v241
	v_med3_f32 v226, v226, s62, v95
	v_med3_f32 v227, v227, s62, v95
	v_med3_f32 v228, v228, s62, v95
	v_med3_f32 v229, v229, s62, v95
	v_med3_f32 v230, v230, s62, v95
	v_med3_f32 v231, v231, s62, v95
	v_med3_f32 v232, v232, s62, v95
	v_med3_f32 v233, v233, s62, v95
	v_med3_f32 v234, v234, s62, v95
	v_med3_f32 v235, v235, s62, v95
	v_med3_f32 v236, v236, s62, v95
	v_med3_f32 v237, v237, s62, v95
	v_med3_f32 v238, v238, s62, v95
	v_med3_f32 v239, v239, s62, v95
	v_med3_f32 v240, v240, s62, v95
	v_med3_f32 v241, v241, s62, v95
	v_mov_b32_e32 v242, 0
	v_mov_b32_e32 v243, 0
	v_mov_b32_e32 v244, 0
	v_mov_b32_e32 v245, 0
	v_cvt_pk_fp8_f32 v242, v226, v227
	v_cvt_pk_fp8_f32 v243, v230, v231
	v_cvt_pk_fp8_f32 v244, v234, v235
	v_cvt_pk_fp8_f32 v245, v238, v239
	v_cvt_pk_fp8_f32 v242, v228, v229 op_sel:[0,0,1]
	v_cvt_pk_fp8_f32 v243, v232, v233 op_sel:[0,0,1]
	v_cvt_pk_fp8_f32 v244, v236, v237 op_sel:[0,0,1]
	v_cvt_pk_fp8_f32 v245, v240, v241 op_sel:[0,0,1]
	s_nop 0
	global_store_dwordx4 v79, v[242:245], s[6:7]
	ds_read_b32 v226, v214
	ds_read_b32 v227, v214 offset:512
	ds_read_b32 v228, v214 offset:1024
	ds_read_b32 v229, v214 offset:1536
	ds_read_b32 v230, v214 offset:2048
	ds_read_b32 v231, v214 offset:2560
	ds_read_b32 v232, v214 offset:3072
	ds_read_b32 v233, v214 offset:3584
	ds_read_b32 v234, v214 offset:4096
	ds_read_b32 v235, v214 offset:4608
	ds_read_b32 v236, v214 offset:5120
	ds_read_b32 v237, v214 offset:5632
	ds_read_b32 v238, v214 offset:6144
	ds_read_b32 v239, v214 offset:6656
	ds_read_b32 v240, v214 offset:7168
	ds_read_b32 v241, v214 offset:7680
	s_waitcnt lgkmcnt(0)
; #define GAS __attribute__((address_space(1)))
; #define LAS __attribute__((address_space(3)))
; #define LDS_WAIT() asm volatile("s_waitcnt lgkmcnt(0)" ::: "memory")
; __device__ __forceinline__ unsigned pk4_fp8(float a, float b, float c, float d) {
;     a = fminf(fmaxf(a, -448.f), 448.f); b = fminf(fmaxf(b, -448.f), 448.f); c = fminf(fmaxf(c, -448.f), 448.f); d = fminf(fmaxf(d, -448.f), 448.f);
;     int w = __builtin_amdgcn_cvt_pk_fp8_f32(a, b, 0, false); w = __builtin_amdgcn_cvt_pk_fp8_f32(c, d, w, true); return (unsigned)w; }
;     ...
;     for (int i = 0; i < 32; ++i) v[i] = sc >= 0 ? W[(size_t)(k0 + 2 * i + (lane >> 5)) * Nsrc + sc] : 0.f;
; #pragma unroll
;     for (int i = 0; i < 32; ++i) { const int k = k0 + 2 * i + (lane >> 5); float x = v[i] * wscale; if (KS) x *= (k < ksplit ? ksA[k] : ksB[k - ksplit]); scr[(2 * i + (lane >> 5)) * 33 + (lane & 31)] = x; }
;     LDS_WAIT(); asm volatile("" ::: "memory");
;     const int c = lane & 7;
; #pragma unroll
;     for (int j = 0; j < 4; ++j) { const int n = (lane >> 3) + 8 * j; const LAS float* s = scr + (8 * c) * 33 + n;
;         const unsigned long long o = (unsigned long long)pg8::pk4_fp8(s[0 * 33], s[1 * 33], s[2 * 33], s[3 * 33]) | ((unsigned long long)pg8::pk4_fp8(s[4 * 33], s[5 * 33], s[6 * 33], s[7 * 33]) << 32);
;         *(GAS unsigned long long*)(WT + (size_t)(n0 + n) * K + k0 + 8 * c) = o; }
	v_max_f32_e32 v226, v226, v226
	v_max_f32_e32 v227, v227, v227
	v_max_f32_e32 v228, v228, v228
	v_max_f32_e32 v229, v229, v229
	v_max_f32_e32 v230, v230, v230
	v_max_f32_e32 v231, v231, v231
	v_max_f32_e32 v232, v232, v232
	v_max_f32_e32 v233, v233, v233
	v_max_f32_e32 v234, v234, v234
	v_max_f32_e32 v235, v235, v235
	v_max_f32_e32 v236, v236, v236
	v_max_f32_e32 v237, v237, v237
	v_max_f32_e32 v238, v238, v238
	v_max_f32_e32 v239, v239, v239
	v_max_f32_e32 v240, v240, v240
	v_max_f32_e32 v241, v241, v241
	v_med3_f32 v226, v226, s62, v95
	v_med3_f32 v227, v227, s62, v95
	v_med3_f32 v228, v228, s62, v95
	v_med3_f32 v229, v229, s62, v95
	v_med3_f32 v230, v230, s62, v95
	v_med3_f32 v231, v231, s62, v95
	v_med3_f32 v232, v232, s62, v95
	v_med3_f32 v233, v233, s62, v95
	v_med3_f32 v234, v234, s62, v95
	v_med3_f32 v235, v235, s62, v95
	v_med3_f32 v236, v236, s62, v95
	v_med3_f32 v237, v237, s62, v95
	v_med3_f32 v238, v238, s62, v95
	v_med3_f32 v239, v239, s62, v95
	v_med3_f32 v240, v240, s62, v95
	v_med3_f32 v241, v241, s62, v95
	v_mov_b32_e32 v242, 0
	v_mov_b32_e32 v243, 0
	v_mov_b32_e32 v244, 0
	v_mov_b32_e32 v245, 0
	v_cvt_pk_fp8_f32 v242, v226, v227
	v_cvt_pk_fp8_f32 v243, v230, v231
	v_cvt_pk_fp8_f32 v244, v234, v235
	v_cvt_pk_fp8_f32 v245, v238, v239
	v_cvt_pk_fp8_f32 v242, v228, v229 op_sel:[0,0,1]
	v_cvt_pk_fp8_f32 v243, v232, v233 op_sel:[0,0,1]
	v_cvt_pk_fp8_f32 v244, v236, v237 op_sel:[0,0,1]
	v_cvt_pk_fp8_f32 v245, v240, v241 op_sel:[0,0,1]
	s_nop 0
	global_store_dwordx4 v80, v[242:245], s[6:7]
	s_waitcnt vmcnt(12)
	v_mul_f32_e32 v144, 0x43000000, v144
	v_mul_f32_e32 v145, 0x43000000, v145
	v_mul_f32_e32 v146, 0x43000000, v146
	v_mul_f32_e32 v147, 0x43000000, v147
	ds_write_b128 v209, v[144:147]
	v_mul_f32_e32 v148, 0x43000000, v148
	v_mul_f32_e32 v149, 0x43000000, v149
	v_mul_f32_e32 v150, 0x43000000, v150
	v_mul_f32_e32 v151, 0x43000000, v151
	ds_write_b128 v209, v[148:151] offset:1024
	v_mul_f32_e32 v152, 0x43000000, v152
	v_mul_f32_e32 v153, 0x43000000, v153
	v_mul_f32_e32 v154, 0x43000000, v154
	v_mul_f32_e32 v155, 0x43000000, v155
	ds_write_b128 v209, v[152:155] offset:2048
	v_mul_f32_e32 v156, 0x43000000, v156
	v_mul_f32_e32 v157, 0x43000000, v157
	v_mul_f32_e32 v158, 0x43000000, v158
	v_mul_f32_e32 v159, 0x43000000, v159
	ds_write_b128 v209, v[156:159] offset:3072
	v_mul_f32_e32 v160, 0x43000000, v160
	v_mul_f32_e32 v161, 0x43000000, v161
	v_mul_f32_e32 v162, 0x43000000, v162
	v_mul_f32_e32 v163, 0x43000000, v163
	ds_write_b128 v209, v[160:163] offset:4096
	v_mul_f32_e32 v164, 0x43000000, v164
	v_mul_f32_e32 v165, 0x43000000, v165
	v_mul_f32_e32 v166, 0x43000000, v166
	v_mul_f32_e32 v167, 0x43000000, v167
	ds_write_b128 v209, v[164:167] offset:5120
	v_mul_f32_e32 v168, 0x43000000, v168
	v_mul_f32_e32 v169, 0x43000000, v169
	v_mul_f32_e32 v170, 0x43000000, v170
	v_mul_f32_e32 v171, 0x43000000, v171
	ds_write_b128 v209, v[168:171] offset:6144
	v_mul_f32_e32 v172, 0x43000000, v172
	v_mul_f32_e32 v173, 0x43000000, v173
	v_mul_f32_e32 v174, 0x43000000, v174
	v_mul_f32_e32 v175, 0x43000000, v175
	ds_write_b128 v209, v[172:175] offset:7168
	s_waitcnt lgkmcnt(0)
	s_barrier
	s_add_u32 s8, s38, 0xc000000
	s_addc_u32 s9, s39, 0
	global_load_dwordx4 v[144:147], v75, s[8:9]
	s_add_u32 s8, s8, 0x8000
	s_addc_u32 s9, s9, 0
	global_load_dwordx4 v[148:151], v75, s[8:9]
	s_add_u32 s8, s8, 0x8000
	s_addc_u32 s9, s9, 0
	global_load_dwordx4 v[152:155], v75, s[8:9]
	s_add_u32 s8, s8, 0x8000
	s_addc_u32 s9, s9, 0
	global_load_dwordx4 v[156:159], v75, s[8:9]
	s_add_u32 s8, s8, 0x8000
	s_addc_u32 s9, s9, 0
	global_load_dwordx4 v[160:163], v75, s[8:9]
	s_add_u32 s8, s8, 0x8000
	s_addc_u32 s9, s9, 0
	global_load_dwordx4 v[164:167], v75, s[8:9]
	s_add_u32 s8, s8, 0x8000
	s_addc_u32 s9, s9, 0
	global_load_dwordx4 v[168:171], v75, s[8:9]
	s_add_u32 s8, s8, 0x8000
	s_addc_u32 s9, s9, 0
	global_load_dwordx4 v[172:175], v75, s[8:9]
	s_add_u32 s6, s40, 0x2002000
	s_addc_u32 s7, s41, 0
	ds_read_b32 v226, v211
	ds_read_b32 v227, v211 offset:512
	ds_read_b32 v228, v211 offset:1024
	ds_read_b32 v229, v211 offset:1536
	ds_read_b32 v230, v211 offset:2048
	ds_read_b32 v231, v211 offset:2560
	ds_read_b32 v232, v211 offset:3072
	ds_read_b32 v233, v211 offset:3584
	ds_read_b32 v234, v211 offset:4096
	ds_read_b32 v235, v211 offset:4608
	ds_read_b32 v236, v211 offset:5120
	ds_read_b32 v237, v211 offset:5632
	ds_read_b32 v238, v211 offset:6144
	ds_read_b32 v239, v211 offset:6656
	ds_read_b32 v240, v211 offset:7168
	ds_read_b32 v241, v211 offset:7680
	s_waitcnt lgkmcnt(0)
	v_max_f32_e32 v226, v226, v226
	v_max_f32_e32 v227, v227, v227
	v_max_f32_e32 v228, v228, v228
	v_max_f32_e32 v229, v229, v229
	v_max_f32_e32 v230, v230, v230
	v_max_f32_e32 v231, v231, v231
	v_max_f32_e32 v232, v232, v232
	v_max_f32_e32 v233, v233, v233
	v_max_f32_e32 v234, v234, v234
	v_max_f32_e32 v235, v235, v235
	v_max_f32_e32 v236, v236, v236
	v_max_f32_e32 v237, v237, v237
	v_max_f32_e32 v238, v238, v238
	v_max_f32_e32 v239, v239, v239
	v_max_f32_e32 v240, v240, v240
	v_max_f32_e32 v241, v241, v241
	v_med3_f32 v226, v226, s62, v95
	v_med3_f32 v227, v227, s62, v95
	v_med3_f32 v228, v228, s62, v95
	v_med3_f32 v229, v229, s62, v95
	v_med3_f32 v230, v230, s62, v95
	v_med3_f32 v231, v231, s62, v95
	v_med3_f32 v232, v232, s62, v95
	v_med3_f32 v233, v233, s62, v95
	v_med3_f32 v234, v234, s62, v95
	v_med3_f32 v235, v235, s62, v95
	v_med3_f32 v236, v236, s62, v95
	v_med3_f32 v237, v237, s62, v95
	v_med3_f32 v238, v238, s62, v95
	v_med3_f32 v239, v239, s62, v95
	v_med3_f32 v240, v240, s62, v95
	v_med3_f32 v241, v241, s62, v95
	v_mov_b32_e32 v242, 0
	v_mov_b32_e32 v243, 0
	v_mov_b32_e32 v244, 0
	v_mov_b32_e32 v245, 0
	v_cvt_pk_fp8_f32 v242, v226, v227
	v_cvt_pk_fp8_f32 v243, v230, v231
	v_cvt_pk_fp8_f32 v244, v234, v235
	v_cvt_pk_fp8_f32 v245, v238, v239
	v_cvt_pk_fp8_f32 v242, v228, v229 op_sel:[0,0,1]
	v_cvt_pk_fp8_f32 v243, v232, v233 op_sel:[0,0,1]
	v_cvt_pk_fp8_f32 v244, v236, v237 op_sel:[0,0,1]
	v_cvt_pk_fp8_f32 v245, v240, v241 op_sel:[0,0,1]
	s_nop 0
	global_store_dwordx4 v79, v[242:245], s[6:7]
	ds_read_b32 v226, v213
	ds_read_b32 v227, v213 offset:512
	ds_read_b32 v228, v213 offset:1024
	ds_read_b32 v229, v213 offset:1536
	ds_read_b32 v230, v213 offset:2048
	ds_read_b32 v231, v213 offset:2560
	ds_read_b32 v232, v213 offset:3072
	ds_read_b32 v233, v213 offset:3584
	ds_read_b32 v234, v213 offset:4096
	ds_read_b32 v235, v213 offset:4608
	ds_read_b32 v236, v213 offset:5120
	ds_read_b32 v237, v213 offset:5632
	ds_read_b32 v238, v213 offset:6144
	ds_read_b32 v239, v213 offset:6656
	ds_read_b32 v240, v213 offset:7168
	ds_read_b32 v241, v213 offset:7680
	s_waitcnt lgkmcnt(0)
; #define GAS __attribute__((address_space(1)))
; #define LAS __attribute__((address_space(3)))
; #define LDS_WAIT() asm volatile("s_waitcnt lgkmcnt(0)" ::: "memory")
;     ...
;     for (int i = 0; i < 32; ++i) v[i] = sc >= 0 ? W[(size_t)(k0 + 2 * i + (lane >> 5)) * Nsrc + sc] : 0.f;
; #pragma unroll
;     for (int i = 0; i < 32; ++i) { const int k = k0 + 2 * i + (lane >> 5); float x = v[i] * wscale; if (KS) x *= (k < ksplit ? ksA[k] : ksB[k - ksplit]); scr[(2 * i + (lane >> 5)) * 33 + (lane & 31)] = x; }
;     LDS_WAIT(); asm volatile("" ::: "memory");
;     const int c = lane & 7;
; #pragma unroll
;     for (int j = 0; j < 4; ++j) { const int n = (lane >> 3) + 8 * j; const LAS float* s = scr + (8 * c) * 33 + n;
;         const unsigned long long o = (unsigned long long)pg8::pk4_fp8(s[0 * 33], s[1 * 33], s[2 * 33], s[3 * 33]) | ((unsigned long long)pg8::pk4_fp8(s[4 * 33], s[5 * 33], s[6 * 33], s[7 * 33]) << 32);
;         *(GAS unsigned long long*)(WT + (size_t)(n0 + n) * K + k0 + 8 * c) = o; }
	v_max_f32_e32 v226, v226, v226
	v_max_f32_e32 v227, v227, v227
	v_max_f32_e32 v228, v228, v228
	v_max_f32_e32 v229, v229, v229
	v_max_f32_e32 v230, v230, v230
	v_max_f32_e32 v231, v231, v231
	v_max_f32_e32 v232, v232, v232
	v_max_f32_e32 v233, v233, v233
	v_max_f32_e32 v234, v234, v234
	v_max_f32_e32 v235, v235, v235
	v_max_f32_e32 v236, v236, v236
	v_max_f32_e32 v237, v237, v237
	v_max_f32_e32 v238, v238, v238
	v_max_f32_e32 v239, v239, v239
	v_max_f32_e32 v240, v240, v240
	v_max_f32_e32 v241, v241, v241
	v_med3_f32 v226, v226, s62, v95
	v_med3_f32 v227, v227, s62, v95
	v_med3_f32 v228, v228, s62, v95
	v_med3_f32 v229, v229, s62, v95
	v_med3_f32 v230, v230, s62, v95
	v_med3_f32 v231, v231, s62, v95
	v_med3_f32 v232, v232, s62, v95
	v_med3_f32 v233, v233, s62, v95
	v_med3_f32 v234, v234, s62, v95
	v_med3_f32 v235, v235, s62, v95
	v_med3_f32 v236, v236, s62, v95
	v_med3_f32 v237, v237, s62, v95
	v_med3_f32 v238, v238, s62, v95
	v_med3_f32 v239, v239, s62, v95
	v_med3_f32 v240, v240, s62, v95
	v_med3_f32 v241, v241, s62, v95
	v_mov_b32_e32 v242, 0
	v_mov_b32_e32 v243, 0
	v_mov_b32_e32 v244, 0
	v_mov_b32_e32 v245, 0
	v_cvt_pk_fp8_f32 v242, v226, v227
	v_cvt_pk_fp8_f32 v243, v230, v231
	v_cvt_pk_fp8_f32 v244, v234, v235
	v_cvt_pk_fp8_f32 v245, v238, v239
	v_cvt_pk_fp8_f32 v242, v228, v229 op_sel:[0,0,1]
	v_cvt_pk_fp8_f32 v243, v232, v233 op_sel:[0,0,1]
	v_cvt_pk_fp8_f32 v244, v236, v237 op_sel:[0,0,1]
	v_cvt_pk_fp8_f32 v245, v240, v241 op_sel:[0,0,1]
	s_nop 0
	global_store_dwordx4 v80, v[242:245], s[6:7]
	s_waitcnt vmcnt(12)
	v_mul_f32_e32 v176, 0x43000000, v176
	v_mul_f32_e32 v177, 0x43000000, v177
	v_mul_f32_e32 v178, 0x43000000, v178
	v_mul_f32_e32 v179, 0x43000000, v179
	ds_write_b128 v210, v[176:179]
	v_mul_f32_e32 v180, 0x43000000, v180
	v_mul_f32_e32 v181, 0x43000000, v181
	v_mul_f32_e32 v182, 0x43000000, v182
	v_mul_f32_e32 v183, 0x43000000, v183
	ds_write_b128 v210, v[180:183] offset:1024
	v_mul_f32_e32 v184, 0x43000000, v184
	v_mul_f32_e32 v185, 0x43000000, v185
	v_mul_f32_e32 v186, 0x43000000, v186
	v_mul_f32_e32 v187, 0x43000000, v187
	ds_write_b128 v210, v[184:187] offset:2048
	v_mul_f32_e32 v188, 0x43000000, v188
	v_mul_f32_e32 v189, 0x43000000, v189
	v_mul_f32_e32 v190, 0x43000000, v190
	v_mul_f32_e32 v191, 0x43000000, v191
	ds_write_b128 v210, v[188:191] offset:3072
	v_mul_f32_e32 v192, 0x43000000, v192
	v_mul_f32_e32 v193, 0x43000000, v193
	v_mul_f32_e32 v194, 0x43000000, v194
	v_mul_f32_e32 v195, 0x43000000, v195
	ds_write_b128 v210, v[192:195] offset:4096
	v_mul_f32_e32 v196, 0x43000000, v196
	v_mul_f32_e32 v197, 0x43000000, v197
	v_mul_f32_e32 v198, 0x43000000, v198
	v_mul_f32_e32 v199, 0x43000000, v199
	ds_write_b128 v210, v[196:199] offset:5120
	v_mul_f32_e32 v200, 0x43000000, v200
	v_mul_f32_e32 v201, 0x43000000, v201
	v_mul_f32_e32 v202, 0x43000000, v202
	v_mul_f32_e32 v203, 0x43000000, v203
	ds_write_b128 v210, v[200:203] offset:6144
	v_mul_f32_e32 v204, 0x43000000, v204
	v_mul_f32_e32 v205, 0x43000000, v205
	v_mul_f32_e32 v206, 0x43000000, v206
	v_mul_f32_e32 v207, 0x43000000, v207
	ds_write_b128 v210, v[204:207] offset:7168
	s_waitcnt lgkmcnt(0)
	s_barrier
	s_add_u32 s8, s38, 0xc001000
	s_addc_u32 s9, s39, 0
	global_load_dwordx4 v[176:179], v75, s[8:9]
	s_add_u32 s8, s8, 0x8000
	s_addc_u32 s9, s9, 0
	global_load_dwordx4 v[180:183], v75, s[8:9]
	s_add_u32 s8, s8, 0x8000
	s_addc_u32 s9, s9, 0
	global_load_dwordx4 v[184:187], v75, s[8:9]
	s_add_u32 s8, s8, 0x8000
	s_addc_u32 s9, s9, 0
	global_load_dwordx4 v[188:191], v75, s[8:9]
	s_add_u32 s8, s8, 0x8000
	s_addc_u32 s9, s9, 0
	global_load_dwordx4 v[192:195], v75, s[8:9]
	s_add_u32 s8, s8, 0x8000
	s_addc_u32 s9, s9, 0
	global_load_dwordx4 v[196:199], v75, s[8:9]
	s_add_u32 s8, s8, 0x8000
	s_addc_u32 s9, s9, 0
	global_load_dwordx4 v[200:203], v75, s[8:9]
	s_add_u32 s8, s8, 0x8000
	s_addc_u32 s9, s9, 0
	global_load_dwordx4 v[204:207], v75, s[8:9]
	s_add_u32 s6, s40, 0x3002000
	s_addc_u32 s7, s41, 0
	ds_read_b32 v226, v212
	ds_read_b32 v227, v212 offset:512
	ds_read_b32 v228, v212 offset:1024
	ds_read_b32 v229, v212 offset:1536
	ds_read_b32 v230, v212 offset:2048
	ds_read_b32 v231, v212 offset:2560
	ds_read_b32 v232, v212 offset:3072
	ds_read_b32 v233, v212 offset:3584
	ds_read_b32 v234, v212 offset:4096
	ds_read_b32 v235, v212 offset:4608
	ds_read_b32 v236, v212 offset:5120
	ds_read_b32 v237, v212 offset:5632
	ds_read_b32 v238, v212 offset:6144
	ds_read_b32 v239, v212 offset:6656
	ds_read_b32 v240, v212 offset:7168
	ds_read_b32 v241, v212 offset:7680
	s_waitcnt lgkmcnt(0)
	v_max_f32_e32 v226, v226, v226
	v_max_f32_e32 v227, v227, v227
	v_max_f32_e32 v228, v228, v228
	v_max_f32_e32 v229, v229, v229
	v_max_f32_e32 v230, v230, v230
	v_max_f32_e32 v231, v231, v231
	v_max_f32_e32 v232, v232, v232
	v_max_f32_e32 v233, v233, v233
	v_max_f32_e32 v234, v234, v234
	v_max_f32_e32 v235, v235, v235
	v_max_f32_e32 v236, v236, v236
	v_max_f32_e32 v237, v237, v237
	v_max_f32_e32 v238, v238, v238
	v_max_f32_e32 v239, v239, v239
	v_max_f32_e32 v240, v240, v240
	v_max_f32_e32 v241, v241, v241
	v_med3_f32 v226, v226, s62, v95
	v_med3_f32 v227, v227, s62, v95
	v_med3_f32 v228, v228, s62, v95
	v_med3_f32 v229, v229, s62, v95
	v_med3_f32 v230, v230, s62, v95
	v_med3_f32 v231, v231, s62, v95
	v_med3_f32 v232, v232, s62, v95
	v_med3_f32 v233, v233, s62, v95
	v_med3_f32 v234, v234, s62, v95
	v_med3_f32 v235, v235, s62, v95
	v_med3_f32 v236, v236, s62, v95
	v_med3_f32 v237, v237, s62, v95
	v_med3_f32 v238, v238, s62, v95
	v_med3_f32 v239, v239, s62, v95
	v_med3_f32 v240, v240, s62, v95
	v_med3_f32 v241, v241, s62, v95
	v_mov_b32_e32 v242, 0
	v_mov_b32_e32 v243, 0
	v_mov_b32_e32 v244, 0
	v_mov_b32_e32 v245, 0
	v_cvt_pk_fp8_f32 v242, v226, v227
	v_cvt_pk_fp8_f32 v243, v230, v231
	v_cvt_pk_fp8_f32 v244, v234, v235
	v_cvt_pk_fp8_f32 v245, v238, v239
	v_cvt_pk_fp8_f32 v242, v228, v229 op_sel:[0,0,1]
	v_cvt_pk_fp8_f32 v243, v232, v233 op_sel:[0,0,1]
	v_cvt_pk_fp8_f32 v244, v236, v237 op_sel:[0,0,1]
	v_cvt_pk_fp8_f32 v245, v240, v241 op_sel:[0,0,1]
	s_nop 0
	global_store_dwordx4 v79, v[242:245], s[6:7]
	ds_read_b32 v226, v214
	ds_read_b32 v227, v214 offset:512
	ds_read_b32 v228, v214 offset:1024
	ds_read_b32 v229, v214 offset:1536
	ds_read_b32 v230, v214 offset:2048
	ds_read_b32 v231, v214 offset:2560
	ds_read_b32 v232, v214 offset:3072
	ds_read_b32 v233, v214 offset:3584
	ds_read_b32 v234, v214 offset:4096
	ds_read_b32 v235, v214 offset:4608
	ds_read_b32 v236, v214 offset:5120
	ds_read_b32 v237, v214 offset:5632
	ds_read_b32 v238, v214 offset:6144
	ds_read_b32 v239, v214 offset:6656
	ds_read_b32 v240, v214 offset:7168
	ds_read_b32 v241, v214 offset:7680
	s_waitcnt lgkmcnt(0)
; #define GAS __attribute__((address_space(1)))
; #define LAS __attribute__((address_space(3)))
; #define LDS_WAIT() asm volatile("s_waitcnt lgkmcnt(0)" ::: "memory")
;     ...
;     for (int i = 0; i < 32; ++i) v[i] = sc >= 0 ? W[(size_t)(k0 + 2 * i + (lane >> 5)) * Nsrc + sc] : 0.f;
; #pragma unroll
;     for (int i = 0; i < 32; ++i) { const int k = k0 + 2 * i + (lane >> 5); float x = v[i] * wscale; if (KS) x *= (k < ksplit ? ksA[k] : ksB[k - ksplit]); scr[(2 * i + (lane >> 5)) * 33 + (lane & 31)] = x; }
;     LDS_WAIT(); asm volatile("" ::: "memory");
;     const int c = lane & 7;
; #pragma unroll
;     for (int j = 0; j < 4; ++j) { const int n = (lane >> 3) + 8 * j; const LAS float* s = scr + (8 * c) * 33 + n;
;         const unsigned long long o = (unsigned long long)pg8::pk4_fp8(s[0 * 33], s[1 * 33], s[2 * 33], s[3 * 33]) | ((unsigned long long)pg8::pk4_fp8(s[4 * 33], s[5 * 33], s[6 * 33], s[7 * 33]) << 32);
;         *(GAS unsigned long long*)(WT + (size_t)(n0 + n) * K + k0 + 8 * c) = o; }
	v_max_f32_e32 v226, v226, v226
	v_max_f32_e32 v227, v227, v227
	v_max_f32_e32 v228, v228, v228
	v_max_f32_e32 v229, v229, v229
	v_max_f32_e32 v230, v230, v230
	v_max_f32_e32 v231, v231, v231
	v_max_f32_e32 v232, v232, v232
	v_max_f32_e32 v233, v233, v233
	v_max_f32_e32 v234, v234, v234
	v_max_f32_e32 v235, v235, v235
	v_max_f32_e32 v236, v236, v236
	v_max_f32_e32 v237, v237, v237
	v_max_f32_e32 v238, v238, v238
	v_max_f32_e32 v239, v239, v239
	v_max_f32_e32 v240, v240, v240
	v_max_f32_e32 v241, v241, v241
	v_med3_f32 v226, v226, s62, v95
	v_med3_f32 v227, v227, s62, v95
	v_med3_f32 v228, v228, s62, v95
	v_med3_f32 v229, v229, s62, v95
	v_med3_f32 v230, v230, s62, v95
	v_med3_f32 v231, v231, s62, v95
	v_med3_f32 v232, v232, s62, v95
	v_med3_f32 v233, v233, s62, v95
	v_med3_f32 v234, v234, s62, v95
	v_med3_f32 v235, v235, s62, v95
	v_med3_f32 v236, v236, s62, v95
	v_med3_f32 v237, v237, s62, v95
	v_med3_f32 v238, v238, s62, v95
	v_med3_f32 v239, v239, s62, v95
	v_med3_f32 v240, v240, s62, v95
	v_med3_f32 v241, v241, s62, v95
	v_mov_b32_e32 v242, 0
	v_mov_b32_e32 v243, 0
	v_mov_b32_e32 v244, 0
	v_mov_b32_e32 v245, 0
	v_cvt_pk_fp8_f32 v242, v226, v227
	v_cvt_pk_fp8_f32 v243, v230, v231
	v_cvt_pk_fp8_f32 v244, v234, v235
	v_cvt_pk_fp8_f32 v245, v238, v239
	v_cvt_pk_fp8_f32 v242, v228, v229 op_sel:[0,0,1]
	v_cvt_pk_fp8_f32 v243, v232, v233 op_sel:[0,0,1]
	v_cvt_pk_fp8_f32 v244, v236, v237 op_sel:[0,0,1]
	v_cvt_pk_fp8_f32 v245, v240, v241 op_sel:[0,0,1]
	s_nop 0
	global_store_dwordx4 v80, v[242:245], s[6:7]
	s_waitcnt vmcnt(12)
	v_mul_f32_e32 v144, 0x43000000, v144
	v_mul_f32_e32 v145, 0x43000000, v145
	v_mul_f32_e32 v146, 0x43000000, v146
	v_mul_f32_e32 v147, 0x43000000, v147
	ds_write_b128 v209, v[144:147]
	v_mul_f32_e32 v148, 0x43000000, v148
	v_mul_f32_e32 v149, 0x43000000, v149
	v_mul_f32_e32 v150, 0x43000000, v150
	v_mul_f32_e32 v151, 0x43000000, v151
	ds_write_b128 v209, v[148:151] offset:1024
	v_mul_f32_e32 v152, 0x43000000, v152
	v_mul_f32_e32 v153, 0x43000000, v153
	v_mul_f32_e32 v154, 0x43000000, v154
	v_mul_f32_e32 v155, 0x43000000, v155
	ds_write_b128 v209, v[152:155] offset:2048
	v_mul_f32_e32 v156, 0x43000000, v156
	v_mul_f32_e32 v157, 0x43000000, v157
	v_mul_f32_e32 v158, 0x43000000, v158
	v_mul_f32_e32 v159, 0x43000000, v159
	ds_write_b128 v209, v[156:159] offset:3072
	v_mul_f32_e32 v160, 0x43000000, v160
	v_mul_f32_e32 v161, 0x43000000, v161
	v_mul_f32_e32 v162, 0x43000000, v162
	v_mul_f32_e32 v163, 0x43000000, v163
	ds_write_b128 v209, v[160:163] offset:4096
	v_mul_f32_e32 v164, 0x43000000, v164
	v_mul_f32_e32 v165, 0x43000000, v165
	v_mul_f32_e32 v166, 0x43000000, v166
	v_mul_f32_e32 v167, 0x43000000, v167
	ds_write_b128 v209, v[164:167] offset:5120
	v_mul_f32_e32 v168, 0x43000000, v168
	v_mul_f32_e32 v169, 0x43000000, v169
	v_mul_f32_e32 v170, 0x43000000, v170
	v_mul_f32_e32 v171, 0x43000000, v171
	ds_write_b128 v209, v[168:171] offset:6144
	v_mul_f32_e32 v172, 0x43000000, v172
	v_mul_f32_e32 v173, 0x43000000, v173
	v_mul_f32_e32 v174, 0x43000000, v174
	v_mul_f32_e32 v175, 0x43000000, v175
	ds_write_b128 v209, v[172:175] offset:7168
	s_waitcnt lgkmcnt(0)
	s_barrier
	s_add_u32 s8, s38, 0xc002000
	s_addc_u32 s9, s39, 0
	global_load_dwordx4 v[144:147], v75, s[8:9]
	s_add_u32 s8, s8, 0x8000
	s_addc_u32 s9, s9, 0
	global_load_dwordx4 v[148:151], v75, s[8:9]
	s_add_u32 s8, s8, 0x8000
	s_addc_u32 s9, s9, 0
	global_load_dwordx4 v[152:155], v75, s[8:9]
	s_add_u32 s8, s8, 0x8000
	s_addc_u32 s9, s9, 0
	global_load_dwordx4 v[156:159], v75, s[8:9]
	s_add_u32 s8, s8, 0x8000
	s_addc_u32 s9, s9, 0
	global_load_dwordx4 v[160:163], v75, s[8:9]
	s_add_u32 s8, s8, 0x8000
	s_addc_u32 s9, s9, 0
	global_load_dwordx4 v[164:167], v75, s[8:9]
	s_add_u32 s8, s8, 0x8000
	s_addc_u32 s9, s9, 0
	global_load_dwordx4 v[168:171], v75, s[8:9]
	s_add_u32 s8, s8, 0x8000
	s_addc_u32 s9, s9, 0
	global_load_dwordx4 v[172:175], v75, s[8:9]
	s_add_u32 s6, s40, 0x3000
	s_addc_u32 s7, s41, 0
	ds_read_b32 v226, v211
	ds_read_b32 v227, v211 offset:512
	ds_read_b32 v228, v211 offset:1024
	ds_read_b32 v229, v211 offset:1536
	ds_read_b32 v230, v211 offset:2048
	ds_read_b32 v231, v211 offset:2560
	ds_read_b32 v232, v211 offset:3072
	ds_read_b32 v233, v211 offset:3584
	ds_read_b32 v234, v211 offset:4096
	ds_read_b32 v235, v211 offset:4608
	ds_read_b32 v236, v211 offset:5120
	ds_read_b32 v237, v211 offset:5632
	ds_read_b32 v238, v211 offset:6144
	ds_read_b32 v239, v211 offset:6656
	ds_read_b32 v240, v211 offset:7168
	ds_read_b32 v241, v211 offset:7680
	s_waitcnt lgkmcnt(0)
	v_max_f32_e32 v226, v226, v226
	v_max_f32_e32 v227, v227, v227
	v_max_f32_e32 v228, v228, v228
	v_max_f32_e32 v229, v229, v229
	v_max_f32_e32 v230, v230, v230
	v_max_f32_e32 v231, v231, v231
	v_max_f32_e32 v232, v232, v232
	v_max_f32_e32 v233, v233, v233
	v_max_f32_e32 v234, v234, v234
	v_max_f32_e32 v235, v235, v235
	v_max_f32_e32 v236, v236, v236
	v_max_f32_e32 v237, v237, v237
	v_max_f32_e32 v238, v238, v238
	v_max_f32_e32 v239, v239, v239
	v_max_f32_e32 v240, v240, v240
	v_max_f32_e32 v241, v241, v241
	v_med3_f32 v226, v226, s62, v95
	v_med3_f32 v227, v227, s62, v95
	v_med3_f32 v228, v228, s62, v95
	v_med3_f32 v229, v229, s62, v95
	v_med3_f32 v230, v230, s62, v95
	v_med3_f32 v231, v231, s62, v95
	v_med3_f32 v232, v232, s62, v95
	v_med3_f32 v233, v233, s62, v95
	v_med3_f32 v234, v234, s62, v95
	v_med3_f32 v235, v235, s62, v95
	v_med3_f32 v236, v236, s62, v95
	v_med3_f32 v237, v237, s62, v95
	v_med3_f32 v238, v238, s62, v95
	v_med3_f32 v239, v239, s62, v95
	v_med3_f32 v240, v240, s62, v95
	v_med3_f32 v241, v241, s62, v95
	v_mov_b32_e32 v242, 0
	v_mov_b32_e32 v243, 0
	v_mov_b32_e32 v244, 0
	v_mov_b32_e32 v245, 0
	v_cvt_pk_fp8_f32 v242, v226, v227
	v_cvt_pk_fp8_f32 v243, v230, v231
	v_cvt_pk_fp8_f32 v244, v234, v235
	v_cvt_pk_fp8_f32 v245, v238, v239
	v_cvt_pk_fp8_f32 v242, v228, v229 op_sel:[0,0,1]
	v_cvt_pk_fp8_f32 v243, v232, v233 op_sel:[0,0,1]
	v_cvt_pk_fp8_f32 v244, v236, v237 op_sel:[0,0,1]
	v_cvt_pk_fp8_f32 v245, v240, v241 op_sel:[0,0,1]
	s_nop 0
	global_store_dwordx4 v79, v[242:245], s[6:7]
	ds_read_b32 v226, v213
	ds_read_b32 v227, v213 offset:512
	ds_read_b32 v228, v213 offset:1024
	ds_read_b32 v229, v213 offset:1536
	ds_read_b32 v230, v213 offset:2048
	ds_read_b32 v231, v213 offset:2560
	ds_read_b32 v232, v213 offset:3072
	ds_read_b32 v233, v213 offset:3584
	ds_read_b32 v234, v213 offset:4096
	ds_read_b32 v235, v213 offset:4608
	ds_read_b32 v236, v213 offset:5120
	ds_read_b32 v237, v213 offset:5632
	ds_read_b32 v238, v213 offset:6144
	ds_read_b32 v239, v213 offset:6656
	ds_read_b32 v240, v213 offset:7168
	ds_read_b32 v241, v213 offset:7680
	s_waitcnt lgkmcnt(0)
; #define GAS __attribute__((address_space(1)))
; #define LAS __attribute__((address_space(3)))
; #define LDS_WAIT() asm volatile("s_waitcnt lgkmcnt(0)" ::: "memory")
;     ...
;     for (int i = 0; i < 32; ++i) v[i] = sc >= 0 ? W[(size_t)(k0 + 2 * i + (lane >> 5)) * Nsrc + sc] : 0.f;
; #pragma unroll
;     for (int i = 0; i < 32; ++i) { const int k = k0 + 2 * i + (lane >> 5); float x = v[i] * wscale; if (KS) x *= (k < ksplit ? ksA[k] : ksB[k - ksplit]); scr[(2 * i + (lane >> 5)) * 33 + (lane & 31)] = x; }
;     LDS_WAIT(); asm volatile("" ::: "memory");
;     const int c = lane & 7;
; #pragma unroll
;     for (int j = 0; j < 4; ++j) { const int n = (lane >> 3) + 8 * j; const LAS float* s = scr + (8 * c) * 33 + n;
;         const unsigned long long o = (unsigned long long)pg8::pk4_fp8(s[0 * 33], s[1 * 33], s[2 * 33], s[3 * 33]) | ((unsigned long long)pg8::pk4_fp8(s[4 * 33], s[5 * 33], s[6 * 33], s[7 * 33]) << 32);
;         *(GAS unsigned long long*)(WT + (size_t)(n0 + n) * K + k0 + 8 * c) = o; }
	v_max_f32_e32 v226, v226, v226
	v_max_f32_e32 v227, v227, v227
	v_max_f32_e32 v228, v228, v228
	v_max_f32_e32 v229, v229, v229
	v_max_f32_e32 v230, v230, v230
	v_max_f32_e32 v231, v231, v231
	v_max_f32_e32 v232, v232, v232
	v_max_f32_e32 v233, v233, v233
	v_max_f32_e32 v234, v234, v234
	v_max_f32_e32 v235, v235, v235
	v_max_f32_e32 v236, v236, v236
	v_max_f32_e32 v237, v237, v237
	v_max_f32_e32 v238, v238, v238
	v_max_f32_e32 v239, v239, v239
	v_max_f32_e32 v240, v240, v240
	v_max_f32_e32 v241, v241, v241
	v_med3_f32 v226, v226, s62, v95
	v_med3_f32 v227, v227, s62, v95
	v_med3_f32 v228, v228, s62, v95
	v_med3_f32 v229, v229, s62, v95
	v_med3_f32 v230, v230, s62, v95
	v_med3_f32 v231, v231, s62, v95
	v_med3_f32 v232, v232, s62, v95
	v_med3_f32 v233, v233, s62, v95
	v_med3_f32 v234, v234, s62, v95
	v_med3_f32 v235, v235, s62, v95
	v_med3_f32 v236, v236, s62, v95
	v_med3_f32 v237, v237, s62, v95
	v_med3_f32 v238, v238, s62, v95
	v_med3_f32 v239, v239, s62, v95
	v_med3_f32 v240, v240, s62, v95
	v_med3_f32 v241, v241, s62, v95
	v_mov_b32_e32 v242, 0
	v_mov_b32_e32 v243, 0
	v_mov_b32_e32 v244, 0
	v_mov_b32_e32 v245, 0
	v_cvt_pk_fp8_f32 v242, v226, v227
	v_cvt_pk_fp8_f32 v243, v230, v231
	v_cvt_pk_fp8_f32 v244, v234, v235
	v_cvt_pk_fp8_f32 v245, v238, v239
	v_cvt_pk_fp8_f32 v242, v228, v229 op_sel:[0,0,1]
	v_cvt_pk_fp8_f32 v243, v232, v233 op_sel:[0,0,1]
	v_cvt_pk_fp8_f32 v244, v236, v237 op_sel:[0,0,1]
	v_cvt_pk_fp8_f32 v245, v240, v241 op_sel:[0,0,1]
	s_nop 0
	global_store_dwordx4 v80, v[242:245], s[6:7]
	s_waitcnt vmcnt(12)
	v_mul_f32_e32 v176, 0x43000000, v176
	v_mul_f32_e32 v177, 0x43000000, v177
	v_mul_f32_e32 v178, 0x43000000, v178
	v_mul_f32_e32 v179, 0x43000000, v179
	ds_write_b128 v210, v[176:179]
	v_mul_f32_e32 v180, 0x43000000, v180
	v_mul_f32_e32 v181, 0x43000000, v181
	v_mul_f32_e32 v182, 0x43000000, v182
	v_mul_f32_e32 v183, 0x43000000, v183
	ds_write_b128 v210, v[180:183] offset:1024
	v_mul_f32_e32 v184, 0x43000000, v184
	v_mul_f32_e32 v185, 0x43000000, v185
	v_mul_f32_e32 v186, 0x43000000, v186
	v_mul_f32_e32 v187, 0x43000000, v187
	ds_write_b128 v210, v[184:187] offset:2048
	v_mul_f32_e32 v188, 0x43000000, v188
	v_mul_f32_e32 v189, 0x43000000, v189
	v_mul_f32_e32 v190, 0x43000000, v190
	v_mul_f32_e32 v191, 0x43000000, v191
	ds_write_b128 v210, v[188:191] offset:3072
	v_mul_f32_e32 v192, 0x43000000, v192
	v_mul_f32_e32 v193, 0x43000000, v193
	v_mul_f32_e32 v194, 0x43000000, v194
	v_mul_f32_e32 v195, 0x43000000, v195
	ds_write_b128 v210, v[192:195] offset:4096
	v_mul_f32_e32 v196, 0x43000000, v196
	v_mul_f32_e32 v197, 0x43000000, v197
	v_mul_f32_e32 v198, 0x43000000, v198
	v_mul_f32_e32 v199, 0x43000000, v199
	ds_write_b128 v210, v[196:199] offset:5120
	v_mul_f32_e32 v200, 0x43000000, v200
	v_mul_f32_e32 v201, 0x43000000, v201
	v_mul_f32_e32 v202, 0x43000000, v202
	v_mul_f32_e32 v203, 0x43000000, v203
	ds_write_b128 v210, v[200:203] offset:6144
	v_mul_f32_e32 v204, 0x43000000, v204
	v_mul_f32_e32 v205, 0x43000000, v205
	v_mul_f32_e32 v206, 0x43000000, v206
	v_mul_f32_e32 v207, 0x43000000, v207
	ds_write_b128 v210, v[204:207] offset:7168
	s_waitcnt lgkmcnt(0)
	s_barrier
	s_add_u32 s8, s38, 0xc003000
	s_addc_u32 s9, s39, 0
	global_load_dwordx4 v[176:179], v75, s[8:9]
	s_add_u32 s8, s8, 0x8000
	s_addc_u32 s9, s9, 0
	global_load_dwordx4 v[180:183], v75, s[8:9]
	s_add_u32 s8, s8, 0x8000
	s_addc_u32 s9, s9, 0
	global_load_dwordx4 v[184:187], v75, s[8:9]
	s_add_u32 s8, s8, 0x8000
	s_addc_u32 s9, s9, 0
	global_load_dwordx4 v[188:191], v75, s[8:9]
	s_add_u32 s8, s8, 0x8000
	s_addc_u32 s9, s9, 0
	global_load_dwordx4 v[192:195], v75, s[8:9]
	s_add_u32 s8, s8, 0x8000
	s_addc_u32 s9, s9, 0
	global_load_dwordx4 v[196:199], v75, s[8:9]
	s_add_u32 s8, s8, 0x8000
	s_addc_u32 s9, s9, 0
	global_load_dwordx4 v[200:203], v75, s[8:9]
	s_add_u32 s8, s8, 0x8000
	s_addc_u32 s9, s9, 0
	global_load_dwordx4 v[204:207], v75, s[8:9]
	s_add_u32 s6, s40, 0x1003000
	s_addc_u32 s7, s41, 0
	ds_read_b32 v226, v212
	ds_read_b32 v227, v212 offset:512
	ds_read_b32 v228, v212 offset:1024
	ds_read_b32 v229, v212 offset:1536
	ds_read_b32 v230, v212 offset:2048
	ds_read_b32 v231, v212 offset:2560
	ds_read_b32 v232, v212 offset:3072
	ds_read_b32 v233, v212 offset:3584
	ds_read_b32 v234, v212 offset:4096
	ds_read_b32 v235, v212 offset:4608
	ds_read_b32 v236, v212 offset:5120
	ds_read_b32 v237, v212 offset:5632
	ds_read_b32 v238, v212 offset:6144
	ds_read_b32 v239, v212 offset:6656
	ds_read_b32 v240, v212 offset:7168
	ds_read_b32 v241, v212 offset:7680
	s_waitcnt lgkmcnt(0)
	v_max_f32_e32 v226, v226, v226
	v_max_f32_e32 v227, v227, v227
	v_max_f32_e32 v228, v228, v228
	v_max_f32_e32 v229, v229, v229
	v_max_f32_e32 v230, v230, v230
	v_max_f32_e32 v231, v231, v231
	v_max_f32_e32 v232, v232, v232
	v_max_f32_e32 v233, v233, v233
	v_max_f32_e32 v234, v234, v234
	v_max_f32_e32 v235, v235, v235
	v_max_f32_e32 v236, v236, v236
	v_max_f32_e32 v237, v237, v237
	v_max_f32_e32 v238, v238, v238
	v_max_f32_e32 v239, v239, v239
	v_max_f32_e32 v240, v240, v240
	v_max_f32_e32 v241, v241, v241
	v_med3_f32 v226, v226, s62, v95
	v_med3_f32 v227, v227, s62, v95
	v_med3_f32 v228, v228, s62, v95
	v_med3_f32 v229, v229, s62, v95
	v_med3_f32 v230, v230, s62, v95
	v_med3_f32 v231, v231, s62, v95
	v_med3_f32 v232, v232, s62, v95
	v_med3_f32 v233, v233, s62, v95
	v_med3_f32 v234, v234, s62, v95
	v_med3_f32 v235, v235, s62, v95
	v_med3_f32 v236, v236, s62, v95
	v_med3_f32 v237, v237, s62, v95
	v_med3_f32 v238, v238, s62, v95
	v_med3_f32 v239, v239, s62, v95
	v_med3_f32 v240, v240, s62, v95
	v_med3_f32 v241, v241, s62, v95
	v_mov_b32_e32 v242, 0
	v_mov_b32_e32 v243, 0
	v_mov_b32_e32 v244, 0
	v_mov_b32_e32 v245, 0
	v_cvt_pk_fp8_f32 v242, v226, v227
	v_cvt_pk_fp8_f32 v243, v230, v231
	v_cvt_pk_fp8_f32 v244, v234, v235
	v_cvt_pk_fp8_f32 v245, v238, v239
	v_cvt_pk_fp8_f32 v242, v228, v229 op_sel:[0,0,1]
	v_cvt_pk_fp8_f32 v243, v232, v233 op_sel:[0,0,1]
	v_cvt_pk_fp8_f32 v244, v236, v237 op_sel:[0,0,1]
	v_cvt_pk_fp8_f32 v245, v240, v241 op_sel:[0,0,1]
	s_nop 0
	global_store_dwordx4 v79, v[242:245], s[6:7]
	ds_read_b32 v226, v214
	ds_read_b32 v227, v214 offset:512
	ds_read_b32 v228, v214 offset:1024
	ds_read_b32 v229, v214 offset:1536
	ds_read_b32 v230, v214 offset:2048
	ds_read_b32 v231, v214 offset:2560
	ds_read_b32 v232, v214 offset:3072
	ds_read_b32 v233, v214 offset:3584
	ds_read_b32 v234, v214 offset:4096
	ds_read_b32 v235, v214 offset:4608
	ds_read_b32 v236, v214 offset:5120
	ds_read_b32 v237, v214 offset:5632
	ds_read_b32 v238, v214 offset:6144
	ds_read_b32 v239, v214 offset:6656
	ds_read_b32 v240, v214 offset:7168
	ds_read_b32 v241, v214 offset:7680
	s_waitcnt lgkmcnt(0)
; #define GAS __attribute__((address_space(1)))
; #define LAS __attribute__((address_space(3)))
; #define LDS_WAIT() asm volatile("s_waitcnt lgkmcnt(0)" ::: "memory")
;     ...
;     for (int i = 0; i < 32; ++i) v[i] = sc >= 0 ? W[(size_t)(k0 + 2 * i + (lane >> 5)) * Nsrc + sc] : 0.f;
; #pragma unroll
;     for (int i = 0; i < 32; ++i) { const int k = k0 + 2 * i + (lane >> 5); float x = v[i] * wscale; if (KS) x *= (k < ksplit ? ksA[k] : ksB[k - ksplit]); scr[(2 * i + (lane >> 5)) * 33 + (lane & 31)] = x; }
;     LDS_WAIT(); asm volatile("" ::: "memory");
;     const int c = lane & 7;
; #pragma unroll
;     for (int j = 0; j < 4; ++j) { const int n = (lane >> 3) + 8 * j; const LAS float* s = scr + (8 * c) * 33 + n;
;         const unsigned long long o = (unsigned long long)pg8::pk4_fp8(s[0 * 33], s[1 * 33], s[2 * 33], s[3 * 33]) | ((unsigned long long)pg8::pk4_fp8(s[4 * 33], s[5 * 33], s[6 * 33], s[7 * 33]) << 32);
;         *(GAS unsigned long long*)(WT + (size_t)(n0 + n) * K + k0 + 8 * c) = o; }
	v_max_f32_e32 v226, v226, v226
	v_max_f32_e32 v227, v227, v227
	v_max_f32_e32 v228, v228, v228
	v_max_f32_e32 v229, v229, v229
	v_max_f32_e32 v230, v230, v230
	v_max_f32_e32 v231, v231, v231
	v_max_f32_e32 v232, v232, v232
	v_max_f32_e32 v233, v233, v233
	v_max_f32_e32 v234, v234, v234
	v_max_f32_e32 v235, v235, v235
	v_max_f32_e32 v236, v236, v236
	v_max_f32_e32 v237, v237, v237
	v_max_f32_e32 v238, v238, v238
	v_max_f32_e32 v239, v239, v239
	v_max_f32_e32 v240, v240, v240
	v_max_f32_e32 v241, v241, v241
	v_med3_f32 v226, v226, s62, v95
	v_med3_f32 v227, v227, s62, v95
	v_med3_f32 v228, v228, s62, v95
	v_med3_f32 v229, v229, s62, v95
	v_med3_f32 v230, v230, s62, v95
	v_med3_f32 v231, v231, s62, v95
	v_med3_f32 v232, v232, s62, v95
	v_med3_f32 v233, v233, s62, v95
	v_med3_f32 v234, v234, s62, v95
	v_med3_f32 v235, v235, s62, v95
	v_med3_f32 v236, v236, s62, v95
	v_med3_f32 v237, v237, s62, v95
	v_med3_f32 v238, v238, s62, v95
	v_med3_f32 v239, v239, s62, v95
	v_med3_f32 v240, v240, s62, v95
	v_med3_f32 v241, v241, s62, v95
	v_mov_b32_e32 v242, 0
	v_mov_b32_e32 v243, 0
	v_mov_b32_e32 v244, 0
	v_mov_b32_e32 v245, 0
	v_cvt_pk_fp8_f32 v242, v226, v227
	v_cvt_pk_fp8_f32 v243, v230, v231
	v_cvt_pk_fp8_f32 v244, v234, v235
	v_cvt_pk_fp8_f32 v245, v238, v239
	v_cvt_pk_fp8_f32 v242, v228, v229 op_sel:[0,0,1]
	v_cvt_pk_fp8_f32 v243, v232, v233 op_sel:[0,0,1]
	v_cvt_pk_fp8_f32 v244, v236, v237 op_sel:[0,0,1]
	v_cvt_pk_fp8_f32 v245, v240, v241 op_sel:[0,0,1]
	s_nop 0
	global_store_dwordx4 v80, v[242:245], s[6:7]
	s_waitcnt vmcnt(12)
	v_mul_f32_e32 v144, 0x43000000, v144
	v_mul_f32_e32 v145, 0x43000000, v145
	v_mul_f32_e32 v146, 0x43000000, v146
	v_mul_f32_e32 v147, 0x43000000, v147
	ds_write_b128 v209, v[144:147]
	v_mul_f32_e32 v148, 0x43000000, v148
	v_mul_f32_e32 v149, 0x43000000, v149
	v_mul_f32_e32 v150, 0x43000000, v150
	v_mul_f32_e32 v151, 0x43000000, v151
	ds_write_b128 v209, v[148:151] offset:1024
	v_mul_f32_e32 v152, 0x43000000, v152
	v_mul_f32_e32 v153, 0x43000000, v153
	v_mul_f32_e32 v154, 0x43000000, v154
	v_mul_f32_e32 v155, 0x43000000, v155
	ds_write_b128 v209, v[152:155] offset:2048
	v_mul_f32_e32 v156, 0x43000000, v156
	v_mul_f32_e32 v157, 0x43000000, v157
	v_mul_f32_e32 v158, 0x43000000, v158
	v_mul_f32_e32 v159, 0x43000000, v159
	ds_write_b128 v209, v[156:159] offset:3072
	v_mul_f32_e32 v160, 0x43000000, v160
	v_mul_f32_e32 v161, 0x43000000, v161
	v_mul_f32_e32 v162, 0x43000000, v162
	v_mul_f32_e32 v163, 0x43000000, v163
	ds_write_b128 v209, v[160:163] offset:4096
	v_mul_f32_e32 v164, 0x43000000, v164
	v_mul_f32_e32 v165, 0x43000000, v165
	v_mul_f32_e32 v166, 0x43000000, v166
	v_mul_f32_e32 v167, 0x43000000, v167
	ds_write_b128 v209, v[164:167] offset:5120
	v_mul_f32_e32 v168, 0x43000000, v168
	v_mul_f32_e32 v169, 0x43000000, v169
	v_mul_f32_e32 v170, 0x43000000, v170
	v_mul_f32_e32 v171, 0x43000000, v171
	ds_write_b128 v209, v[168:171] offset:6144
	v_mul_f32_e32 v172, 0x43000000, v172
	v_mul_f32_e32 v173, 0x43000000, v173
	v_mul_f32_e32 v174, 0x43000000, v174
	v_mul_f32_e32 v175, 0x43000000, v175
	ds_write_b128 v209, v[172:175] offset:7168
	s_waitcnt lgkmcnt(0)
	s_barrier
	s_mov_b64 s[8:9], s[42:43]
	global_load_dwordx4 v[144:147], v75, s[8:9]
	s_add_u32 s8, s8, 0x8000
	s_addc_u32 s9, s9, 0
	global_load_dwordx4 v[148:151], v75, s[8:9]
	s_add_u32 s8, s8, 0x8000
	s_addc_u32 s9, s9, 0
	global_load_dwordx4 v[152:155], v75, s[8:9]
	s_add_u32 s8, s8, 0x8000
	s_addc_u32 s9, s9, 0
	global_load_dwordx4 v[156:159], v75, s[8:9]
	s_add_u32 s8, s8, 0x8000
	s_addc_u32 s9, s9, 0
	global_load_dwordx4 v[160:163], v75, s[8:9]
	s_add_u32 s8, s8, 0x8000
	s_addc_u32 s9, s9, 0
	global_load_dwordx4 v[164:167], v75, s[8:9]
	s_add_u32 s8, s8, 0x8000
	s_addc_u32 s9, s9, 0
	global_load_dwordx4 v[168:171], v75, s[8:9]
	s_add_u32 s8, s8, 0x8000
	s_addc_u32 s9, s9, 0
	global_load_dwordx4 v[172:175], v75, s[8:9]
	s_add_u32 s6, s40, 0x2003000
	s_addc_u32 s7, s41, 0
	ds_read_b32 v226, v211
	ds_read_b32 v227, v211 offset:512
	ds_read_b32 v228, v211 offset:1024
	ds_read_b32 v229, v211 offset:1536
	ds_read_b32 v230, v211 offset:2048
	ds_read_b32 v231, v211 offset:2560
	ds_read_b32 v232, v211 offset:3072
	ds_read_b32 v233, v211 offset:3584
	ds_read_b32 v234, v211 offset:4096
	ds_read_b32 v235, v211 offset:4608
	ds_read_b32 v236, v211 offset:5120
	ds_read_b32 v237, v211 offset:5632
	ds_read_b32 v238, v211 offset:6144
	ds_read_b32 v239, v211 offset:6656
	ds_read_b32 v240, v211 offset:7168
	ds_read_b32 v241, v211 offset:7680
	s_waitcnt lgkmcnt(0)
	v_max_f32_e32 v226, v226, v226
	v_max_f32_e32 v227, v227, v227
	v_max_f32_e32 v228, v228, v228
	v_max_f32_e32 v229, v229, v229
	v_max_f32_e32 v230, v230, v230
	v_max_f32_e32 v231, v231, v231
	v_max_f32_e32 v232, v232, v232
	v_max_f32_e32 v233, v233, v233
	v_max_f32_e32 v234, v234, v234
	v_max_f32_e32 v235, v235, v235
	v_max_f32_e32 v236, v236, v236
	v_max_f32_e32 v237, v237, v237
	v_max_f32_e32 v238, v238, v238
	v_max_f32_e32 v239, v239, v239
	v_max_f32_e32 v240, v240, v240
	v_max_f32_e32 v241, v241, v241
	v_med3_f32 v226, v226, s62, v95
	v_med3_f32 v227, v227, s62, v95
	v_med3_f32 v228, v228, s62, v95
	v_med3_f32 v229, v229, s62, v95
	v_med3_f32 v230, v230, s62, v95
	v_med3_f32 v231, v231, s62, v95
	v_med3_f32 v232, v232, s62, v95
	v_med3_f32 v233, v233, s62, v95
	v_med3_f32 v234, v234, s62, v95
	v_med3_f32 v235, v235, s62, v95
	v_med3_f32 v236, v236, s62, v95
	v_med3_f32 v237, v237, s62, v95
	v_med3_f32 v238, v238, s62, v95
	v_med3_f32 v239, v239, s62, v95
	v_med3_f32 v240, v240, s62, v95
	v_med3_f32 v241, v241, s62, v95
	v_mov_b32_e32 v242, 0
	v_mov_b32_e32 v243, 0
	v_mov_b32_e32 v244, 0
	v_mov_b32_e32 v245, 0
	v_cvt_pk_fp8_f32 v242, v226, v227
	v_cvt_pk_fp8_f32 v243, v230, v231
	v_cvt_pk_fp8_f32 v244, v234, v235
	v_cvt_pk_fp8_f32 v245, v238, v239
	v_cvt_pk_fp8_f32 v242, v228, v229 op_sel:[0,0,1]
	v_cvt_pk_fp8_f32 v243, v232, v233 op_sel:[0,0,1]
	v_cvt_pk_fp8_f32 v244, v236, v237 op_sel:[0,0,1]
	v_cvt_pk_fp8_f32 v245, v240, v241 op_sel:[0,0,1]
	s_nop 0
	global_store_dwordx4 v79, v[242:245], s[6:7]
	ds_read_b32 v226, v213
	ds_read_b32 v227, v213 offset:512
	ds_read_b32 v228, v213 offset:1024
	ds_read_b32 v229, v213 offset:1536
	ds_read_b32 v230, v213 offset:2048
	ds_read_b32 v231, v213 offset:2560
	ds_read_b32 v232, v213 offset:3072
	ds_read_b32 v233, v213 offset:3584
	ds_read_b32 v234, v213 offset:4096
	ds_read_b32 v235, v213 offset:4608
	ds_read_b32 v236, v213 offset:5120
	ds_read_b32 v237, v213 offset:5632
	ds_read_b32 v238, v213 offset:6144
	ds_read_b32 v239, v213 offset:6656
	ds_read_b32 v240, v213 offset:7168
	ds_read_b32 v241, v213 offset:7680
	s_waitcnt lgkmcnt(0)
; #define GAS __attribute__((address_space(1)))
; #define LAS __attribute__((address_space(3)))
; #define LDS_WAIT() asm volatile("s_waitcnt lgkmcnt(0)" ::: "memory")
;     ...
;     for (int i = 0; i < 32; ++i) v[i] = sc >= 0 ? W[(size_t)(k0 + 2 * i + (lane >> 5)) * Nsrc + sc] : 0.f;
; #pragma unroll
;     for (int i = 0; i < 32; ++i) { const int k = k0 + 2 * i + (lane >> 5); float x = v[i] * wscale; if (KS) x *= (k < ksplit ? ksA[k] : ksB[k - ksplit]); scr[(2 * i + (lane >> 5)) * 33 + (lane & 31)] = x; }
;     LDS_WAIT(); asm volatile("" ::: "memory");
;     const int c = lane & 7;
; #pragma unroll
;     for (int j = 0; j < 4; ++j) { const int n = (lane >> 3) + 8 * j; const LAS float* s = scr + (8 * c) * 33 + n;
;         const unsigned long long o = (unsigned long long)pg8::pk4_fp8(s[0 * 33], s[1 * 33], s[2 * 33], s[3 * 33]) | ((unsigned long long)pg8::pk4_fp8(s[4 * 33], s[5 * 33], s[6 * 33], s[7 * 33]) << 32);
;         *(GAS unsigned long long*)(WT + (size_t)(n0 + n) * K + k0 + 8 * c) = o; }
	v_max_f32_e32 v226, v226, v226
	v_max_f32_e32 v227, v227, v227
	v_max_f32_e32 v228, v228, v228
	v_max_f32_e32 v229, v229, v229
	v_max_f32_e32 v230, v230, v230
	v_max_f32_e32 v231, v231, v231
	v_max_f32_e32 v232, v232, v232
	v_max_f32_e32 v233, v233, v233
	v_max_f32_e32 v234, v234, v234
	v_max_f32_e32 v235, v235, v235
	v_max_f32_e32 v236, v236, v236
	v_max_f32_e32 v237, v237, v237
	v_max_f32_e32 v238, v238, v238
	v_max_f32_e32 v239, v239, v239
	v_max_f32_e32 v240, v240, v240
	v_max_f32_e32 v241, v241, v241
	v_med3_f32 v226, v226, s62, v95
	v_med3_f32 v227, v227, s62, v95
	v_med3_f32 v228, v228, s62, v95
	v_med3_f32 v229, v229, s62, v95
	v_med3_f32 v230, v230, s62, v95
	v_med3_f32 v231, v231, s62, v95
	v_med3_f32 v232, v232, s62, v95
	v_med3_f32 v233, v233, s62, v95
	v_med3_f32 v234, v234, s62, v95
	v_med3_f32 v235, v235, s62, v95
	v_med3_f32 v236, v236, s62, v95
	v_med3_f32 v237, v237, s62, v95
	v_med3_f32 v238, v238, s62, v95
	v_med3_f32 v239, v239, s62, v95
	v_med3_f32 v240, v240, s62, v95
	v_med3_f32 v241, v241, s62, v95
	v_mov_b32_e32 v242, 0
	v_mov_b32_e32 v243, 0
	v_mov_b32_e32 v244, 0
	v_mov_b32_e32 v245, 0
	v_cvt_pk_fp8_f32 v242, v226, v227
	v_cvt_pk_fp8_f32 v243, v230, v231
	v_cvt_pk_fp8_f32 v244, v234, v235
	v_cvt_pk_fp8_f32 v245, v238, v239
	v_cvt_pk_fp8_f32 v242, v228, v229 op_sel:[0,0,1]
	v_cvt_pk_fp8_f32 v243, v232, v233 op_sel:[0,0,1]
	v_cvt_pk_fp8_f32 v244, v236, v237 op_sel:[0,0,1]
	v_cvt_pk_fp8_f32 v245, v240, v241 op_sel:[0,0,1]
	s_nop 0
	global_store_dwordx4 v80, v[242:245], s[6:7]
	s_waitcnt vmcnt(12)
	v_mul_f32_e32 v176, 0x43000000, v176
	v_mul_f32_e32 v177, 0x43000000, v177
	v_mul_f32_e32 v178, 0x43000000, v178
	v_mul_f32_e32 v179, 0x43000000, v179
	ds_write_b128 v210, v[176:179]
	v_mul_f32_e32 v180, 0x43000000, v180
	v_mul_f32_e32 v181, 0x43000000, v181
	v_mul_f32_e32 v182, 0x43000000, v182
	v_mul_f32_e32 v183, 0x43000000, v183
	ds_write_b128 v210, v[180:183] offset:1024
	v_mul_f32_e32 v184, 0x43000000, v184
	v_mul_f32_e32 v185, 0x43000000, v185
	v_mul_f32_e32 v186, 0x43000000, v186
	v_mul_f32_e32 v187, 0x43000000, v187
	ds_write_b128 v210, v[184:187] offset:2048
	v_mul_f32_e32 v188, 0x43000000, v188
	v_mul_f32_e32 v189, 0x43000000, v189
	v_mul_f32_e32 v190, 0x43000000, v190
	v_mul_f32_e32 v191, 0x43000000, v191
	ds_write_b128 v210, v[188:191] offset:3072
	v_mul_f32_e32 v192, 0x43000000, v192
	v_mul_f32_e32 v193, 0x43000000, v193
	v_mul_f32_e32 v194, 0x43000000, v194
	v_mul_f32_e32 v195, 0x43000000, v195
	ds_write_b128 v210, v[192:195] offset:4096
	v_mul_f32_e32 v196, 0x43000000, v196
	v_mul_f32_e32 v197, 0x43000000, v197
	v_mul_f32_e32 v198, 0x43000000, v198
	v_mul_f32_e32 v199, 0x43000000, v199
	ds_write_b128 v210, v[196:199] offset:5120
	v_mul_f32_e32 v200, 0x43000000, v200
	v_mul_f32_e32 v201, 0x43000000, v201
	v_mul_f32_e32 v202, 0x43000000, v202
	v_mul_f32_e32 v203, 0x43000000, v203
	ds_write_b128 v210, v[200:203] offset:6144
	v_mul_f32_e32 v204, 0x43000000, v204
	v_mul_f32_e32 v205, 0x43000000, v205
	v_mul_f32_e32 v206, 0x43000000, v206
	v_mul_f32_e32 v207, 0x43000000, v207
	ds_write_b128 v210, v[204:207] offset:7168
	s_waitcnt lgkmcnt(0)
	s_barrier
	s_add_u32 s8, s42, 0x1000
	s_addc_u32 s9, s43, 0
	global_load_dwordx4 v[176:179], v75, s[8:9]
	s_add_u32 s8, s8, 0x8000
	s_addc_u32 s9, s9, 0
	global_load_dwordx4 v[180:183], v75, s[8:9]
	s_add_u32 s8, s8, 0x8000
	s_addc_u32 s9, s9, 0
	global_load_dwordx4 v[184:187], v75, s[8:9]
	s_add_u32 s8, s8, 0x8000
	s_addc_u32 s9, s9, 0
	global_load_dwordx4 v[188:191], v75, s[8:9]
	s_add_u32 s8, s8, 0x8000
	s_addc_u32 s9, s9, 0
	global_load_dwordx4 v[192:195], v75, s[8:9]
	s_add_u32 s8, s8, 0x8000
	s_addc_u32 s9, s9, 0
	global_load_dwordx4 v[196:199], v75, s[8:9]
	s_add_u32 s8, s8, 0x8000
	s_addc_u32 s9, s9, 0
	global_load_dwordx4 v[200:203], v75, s[8:9]
	s_add_u32 s8, s8, 0x8000
	s_addc_u32 s9, s9, 0
	global_load_dwordx4 v[204:207], v75, s[8:9]
	s_add_u32 s6, s40, 0x3003000
	s_addc_u32 s7, s41, 0
	ds_read_b32 v226, v212
	ds_read_b32 v227, v212 offset:512
	ds_read_b32 v228, v212 offset:1024
	ds_read_b32 v229, v212 offset:1536
	ds_read_b32 v230, v212 offset:2048
	ds_read_b32 v231, v212 offset:2560
	ds_read_b32 v232, v212 offset:3072
	ds_read_b32 v233, v212 offset:3584
	ds_read_b32 v234, v212 offset:4096
	ds_read_b32 v235, v212 offset:4608
	ds_read_b32 v236, v212 offset:5120
	ds_read_b32 v237, v212 offset:5632
	ds_read_b32 v238, v212 offset:6144
	ds_read_b32 v239, v212 offset:6656
	ds_read_b32 v240, v212 offset:7168
	ds_read_b32 v241, v212 offset:7680
	s_waitcnt lgkmcnt(0)
	v_max_f32_e32 v226, v226, v226
	v_max_f32_e32 v227, v227, v227
	v_max_f32_e32 v228, v228, v228
	v_max_f32_e32 v229, v229, v229
	v_max_f32_e32 v230, v230, v230
	v_max_f32_e32 v231, v231, v231
	v_max_f32_e32 v232, v232, v232
	v_max_f32_e32 v233, v233, v233
	v_max_f32_e32 v234, v234, v234
	v_max_f32_e32 v235, v235, v235
	v_max_f32_e32 v236, v236, v236
	v_max_f32_e32 v237, v237, v237
	v_max_f32_e32 v238, v238, v238
	v_max_f32_e32 v239, v239, v239
	v_max_f32_e32 v240, v240, v240
	v_max_f32_e32 v241, v241, v241
	v_med3_f32 v226, v226, s62, v95
	v_med3_f32 v227, v227, s62, v95
	v_med3_f32 v228, v228, s62, v95
	v_med3_f32 v229, v229, s62, v95
	v_med3_f32 v230, v230, s62, v95
	v_med3_f32 v231, v231, s62, v95
	v_med3_f32 v232, v232, s62, v95
	v_med3_f32 v233, v233, s62, v95
	v_med3_f32 v234, v234, s62, v95
	v_med3_f32 v235, v235, s62, v95
	v_med3_f32 v236, v236, s62, v95
	v_med3_f32 v237, v237, s62, v95
	v_med3_f32 v238, v238, s62, v95
	v_med3_f32 v239, v239, s62, v95
	v_med3_f32 v240, v240, s62, v95
	v_med3_f32 v241, v241, s62, v95
	v_mov_b32_e32 v242, 0
	v_mov_b32_e32 v243, 0
	v_mov_b32_e32 v244, 0
	v_mov_b32_e32 v245, 0
	v_cvt_pk_fp8_f32 v242, v226, v227
	v_cvt_pk_fp8_f32 v243, v230, v231
	v_cvt_pk_fp8_f32 v244, v234, v235
	v_cvt_pk_fp8_f32 v245, v238, v239
	v_cvt_pk_fp8_f32 v242, v228, v229 op_sel:[0,0,1]
	v_cvt_pk_fp8_f32 v243, v232, v233 op_sel:[0,0,1]
	v_cvt_pk_fp8_f32 v244, v236, v237 op_sel:[0,0,1]
	v_cvt_pk_fp8_f32 v245, v240, v241 op_sel:[0,0,1]
	s_nop 0
	global_store_dwordx4 v79, v[242:245], s[6:7]
	ds_read_b32 v226, v214
	ds_read_b32 v227, v214 offset:512
	ds_read_b32 v228, v214 offset:1024
	ds_read_b32 v229, v214 offset:1536
	ds_read_b32 v230, v214 offset:2048
	ds_read_b32 v231, v214 offset:2560
	ds_read_b32 v232, v214 offset:3072
	ds_read_b32 v233, v214 offset:3584
	ds_read_b32 v234, v214 offset:4096
	ds_read_b32 v235, v214 offset:4608
	ds_read_b32 v236, v214 offset:5120
	ds_read_b32 v237, v214 offset:5632
	ds_read_b32 v238, v214 offset:6144
	ds_read_b32 v239, v214 offset:6656
	ds_read_b32 v240, v214 offset:7168
	ds_read_b32 v241, v214 offset:7680
	s_waitcnt lgkmcnt(0)
; #define GAS __attribute__((address_space(1)))
; #define LAS __attribute__((address_space(3)))
; #define LDS_WAIT() asm volatile("s_waitcnt lgkmcnt(0)" ::: "memory")
;     ...
;     for (int i = 0; i < 32; ++i) v[i] = sc >= 0 ? W[(size_t)(k0 + 2 * i + (lane >> 5)) * Nsrc + sc] : 0.f;
; #pragma unroll
;     for (int i = 0; i < 32; ++i) { const int k = k0 + 2 * i + (lane >> 5); float x = v[i] * wscale; if (KS) x *= (k < ksplit ? ksA[k] : ksB[k - ksplit]); scr[(2 * i + (lane >> 5)) * 33 + (lane & 31)] = x; }
;     LDS_WAIT(); asm volatile("" ::: "memory");
;     const int c = lane & 7;
; #pragma unroll
;     for (int j = 0; j < 4; ++j) { const int n = (lane >> 3) + 8 * j; const LAS float* s = scr + (8 * c) * 33 + n;
;         const unsigned long long o = (unsigned long long)pg8::pk4_fp8(s[0 * 33], s[1 * 33], s[2 * 33], s[3 * 33]) | ((unsigned long long)pg8::pk4_fp8(s[4 * 33], s[5 * 33], s[6 * 33], s[7 * 33]) << 32);
;         *(GAS unsigned long long*)(WT + (size_t)(n0 + n) * K + k0 + 8 * c) = o; }
	v_max_f32_e32 v226, v226, v226
	v_max_f32_e32 v227, v227, v227
	v_max_f32_e32 v228, v228, v228
	v_max_f32_e32 v229, v229, v229
	v_max_f32_e32 v230, v230, v230
	v_max_f32_e32 v231, v231, v231
	v_max_f32_e32 v232, v232, v232
	v_max_f32_e32 v233, v233, v233
	v_max_f32_e32 v234, v234, v234
	v_max_f32_e32 v235, v235, v235
	v_max_f32_e32 v236, v236, v236
	v_max_f32_e32 v237, v237, v237
	v_max_f32_e32 v238, v238, v238
	v_max_f32_e32 v239, v239, v239
	v_max_f32_e32 v240, v240, v240
	v_max_f32_e32 v241, v241, v241
	v_med3_f32 v226, v226, s62, v95
	v_med3_f32 v227, v227, s62, v95
	v_med3_f32 v228, v228, s62, v95
	v_med3_f32 v229, v229, s62, v95
	v_med3_f32 v230, v230, s62, v95
	v_med3_f32 v231, v231, s62, v95
	v_med3_f32 v232, v232, s62, v95
	v_med3_f32 v233, v233, s62, v95
	v_med3_f32 v234, v234, s62, v95
	v_med3_f32 v235, v235, s62, v95
	v_med3_f32 v236, v236, s62, v95
	v_med3_f32 v237, v237, s62, v95
	v_med3_f32 v238, v238, s62, v95
	v_med3_f32 v239, v239, s62, v95
	v_med3_f32 v240, v240, s62, v95
	v_med3_f32 v241, v241, s62, v95
	v_mov_b32_e32 v242, 0
	v_mov_b32_e32 v243, 0
	v_mov_b32_e32 v244, 0
	v_mov_b32_e32 v245, 0
	v_cvt_pk_fp8_f32 v242, v226, v227
	v_cvt_pk_fp8_f32 v243, v230, v231
	v_cvt_pk_fp8_f32 v244, v234, v235
	v_cvt_pk_fp8_f32 v245, v238, v239
	v_cvt_pk_fp8_f32 v242, v228, v229 op_sel:[0,0,1]
	v_cvt_pk_fp8_f32 v243, v232, v233 op_sel:[0,0,1]
	v_cvt_pk_fp8_f32 v244, v236, v237 op_sel:[0,0,1]
	v_cvt_pk_fp8_f32 v245, v240, v241 op_sel:[0,0,1]
	s_nop 0
	global_store_dwordx4 v80, v[242:245], s[6:7]
	s_waitcnt vmcnt(12)
	v_mul_f32_e32 v144, 0x43000000, v144
	v_mul_f32_e32 v145, 0x43000000, v145
	v_mul_f32_e32 v146, 0x43000000, v146
	v_mul_f32_e32 v147, 0x43000000, v147
	ds_write_b128 v209, v[144:147]
	v_mul_f32_e32 v148, 0x43000000, v148
	v_mul_f32_e32 v149, 0x43000000, v149
	v_mul_f32_e32 v150, 0x43000000, v150
	v_mul_f32_e32 v151, 0x43000000, v151
	ds_write_b128 v209, v[148:151] offset:1024
	v_mul_f32_e32 v152, 0x43000000, v152
	v_mul_f32_e32 v153, 0x43000000, v153
	v_mul_f32_e32 v154, 0x43000000, v154
	v_mul_f32_e32 v155, 0x43000000, v155
	ds_write_b128 v209, v[152:155] offset:2048
	v_mul_f32_e32 v156, 0x43000000, v156
	v_mul_f32_e32 v157, 0x43000000, v157
	v_mul_f32_e32 v158, 0x43000000, v158
	v_mul_f32_e32 v159, 0x43000000, v159
	ds_write_b128 v209, v[156:159] offset:3072
	v_mul_f32_e32 v160, 0x43000000, v160
	v_mul_f32_e32 v161, 0x43000000, v161
	v_mul_f32_e32 v162, 0x43000000, v162
	v_mul_f32_e32 v163, 0x43000000, v163
	ds_write_b128 v209, v[160:163] offset:4096
	v_mul_f32_e32 v164, 0x43000000, v164
	v_mul_f32_e32 v165, 0x43000000, v165
	v_mul_f32_e32 v166, 0x43000000, v166
	v_mul_f32_e32 v167, 0x43000000, v167
	ds_write_b128 v209, v[164:167] offset:5120
	v_mul_f32_e32 v168, 0x43000000, v168
	v_mul_f32_e32 v169, 0x43000000, v169
	v_mul_f32_e32 v170, 0x43000000, v170
	v_mul_f32_e32 v171, 0x43000000, v171
	ds_write_b128 v209, v[168:171] offset:6144
	v_mul_f32_e32 v172, 0x43000000, v172
	v_mul_f32_e32 v173, 0x43000000, v173
	v_mul_f32_e32 v174, 0x43000000, v174
	v_mul_f32_e32 v175, 0x43000000, v175
	ds_write_b128 v209, v[172:175] offset:7168
	s_waitcnt lgkmcnt(0)
	s_barrier
	s_add_u32 s8, s42, 0x2000
	s_addc_u32 s9, s43, 0
	global_load_dwordx4 v[144:147], v75, s[8:9]
	s_add_u32 s8, s8, 0x8000
	s_addc_u32 s9, s9, 0
	global_load_dwordx4 v[148:151], v75, s[8:9]
	s_add_u32 s8, s8, 0x8000
	s_addc_u32 s9, s9, 0
	global_load_dwordx4 v[152:155], v75, s[8:9]
	s_add_u32 s8, s8, 0x8000
	s_addc_u32 s9, s9, 0
	global_load_dwordx4 v[156:159], v75, s[8:9]
	s_add_u32 s8, s8, 0x8000
	s_addc_u32 s9, s9, 0
	global_load_dwordx4 v[160:163], v75, s[8:9]
	s_add_u32 s8, s8, 0x8000
	s_addc_u32 s9, s9, 0
	global_load_dwordx4 v[164:167], v75, s[8:9]
	s_add_u32 s8, s8, 0x8000
	s_addc_u32 s9, s9, 0
	global_load_dwordx4 v[168:171], v75, s[8:9]
	s_add_u32 s8, s8, 0x8000
	s_addc_u32 s9, s9, 0
	global_load_dwordx4 v[172:175], v75, s[8:9]
	s_mov_b64 s[6:7], s[44:45]
	ds_read_b32 v226, v211
	ds_read_b32 v227, v211 offset:512
	ds_read_b32 v228, v211 offset:1024
	ds_read_b32 v229, v211 offset:1536
	ds_read_b32 v230, v211 offset:2048
	ds_read_b32 v231, v211 offset:2560
	ds_read_b32 v232, v211 offset:3072
	ds_read_b32 v233, v211 offset:3584
	ds_read_b32 v234, v211 offset:4096
	ds_read_b32 v235, v211 offset:4608
	ds_read_b32 v236, v211 offset:5120
	ds_read_b32 v237, v211 offset:5632
	ds_read_b32 v238, v211 offset:6144
	ds_read_b32 v239, v211 offset:6656
	ds_read_b32 v240, v211 offset:7168
	ds_read_b32 v241, v211 offset:7680
	s_waitcnt lgkmcnt(0)
	v_max_f32_e32 v226, v226, v226
	v_max_f32_e32 v227, v227, v227
	v_max_f32_e32 v228, v228, v228
	v_max_f32_e32 v229, v229, v229
	v_max_f32_e32 v230, v230, v230
	v_max_f32_e32 v231, v231, v231
	v_max_f32_e32 v232, v232, v232
	v_max_f32_e32 v233, v233, v233
	v_max_f32_e32 v234, v234, v234
	v_max_f32_e32 v235, v235, v235
	v_max_f32_e32 v236, v236, v236
	v_max_f32_e32 v237, v237, v237
	v_max_f32_e32 v238, v238, v238
	v_max_f32_e32 v239, v239, v239
	v_max_f32_e32 v240, v240, v240
	v_max_f32_e32 v241, v241, v241
	v_med3_f32 v226, v226, s62, v95
	v_med3_f32 v227, v227, s62, v95
	v_med3_f32 v228, v228, s62, v95
	v_med3_f32 v229, v229, s62, v95
	v_med3_f32 v230, v230, s62, v95
	v_med3_f32 v231, v231, s62, v95
	v_med3_f32 v232, v232, s62, v95
	v_med3_f32 v233, v233, s62, v95
	v_med3_f32 v234, v234, s62, v95
	v_med3_f32 v235, v235, s62, v95
	v_med3_f32 v236, v236, s62, v95
	v_med3_f32 v237, v237, s62, v95
	v_med3_f32 v238, v238, s62, v95
	v_med3_f32 v239, v239, s62, v95
	v_med3_f32 v240, v240, s62, v95
	v_med3_f32 v241, v241, s62, v95
	v_mov_b32_e32 v242, 0
	v_mov_b32_e32 v243, 0
	v_mov_b32_e32 v244, 0
	v_mov_b32_e32 v245, 0
	v_cvt_pk_fp8_f32 v242, v226, v227
	v_cvt_pk_fp8_f32 v243, v230, v231
	v_cvt_pk_fp8_f32 v244, v234, v235
	v_cvt_pk_fp8_f32 v245, v238, v239
	v_cvt_pk_fp8_f32 v242, v228, v229 op_sel:[0,0,1]
	v_cvt_pk_fp8_f32 v243, v232, v233 op_sel:[0,0,1]
	v_cvt_pk_fp8_f32 v244, v236, v237 op_sel:[0,0,1]
	v_cvt_pk_fp8_f32 v245, v240, v241 op_sel:[0,0,1]
	s_nop 0
	global_store_dwordx4 v79, v[242:245], s[6:7]
	ds_read_b32 v226, v213
	ds_read_b32 v227, v213 offset:512
	ds_read_b32 v228, v213 offset:1024
	ds_read_b32 v229, v213 offset:1536
	ds_read_b32 v230, v213 offset:2048
	ds_read_b32 v231, v213 offset:2560
	ds_read_b32 v232, v213 offset:3072
	ds_read_b32 v233, v213 offset:3584
	ds_read_b32 v234, v213 offset:4096
	ds_read_b32 v235, v213 offset:4608
	ds_read_b32 v236, v213 offset:5120
	ds_read_b32 v237, v213 offset:5632
	ds_read_b32 v238, v213 offset:6144
	ds_read_b32 v239, v213 offset:6656
	ds_read_b32 v240, v213 offset:7168
	ds_read_b32 v241, v213 offset:7680
	s_waitcnt lgkmcnt(0)
; #define GAS __attribute__((address_space(1)))
; #define LAS __attribute__((address_space(3)))
; #define LDS_WAIT() asm volatile("s_waitcnt lgkmcnt(0)" ::: "memory")
;     ...
;     for (int i = 0; i < 32; ++i) v[i] = sc >= 0 ? W[(size_t)(k0 + 2 * i + (lane >> 5)) * Nsrc + sc] : 0.f;
; #pragma unroll
;     for (int i = 0; i < 32; ++i) { const int k = k0 + 2 * i + (lane >> 5); float x = v[i] * wscale; if (KS) x *= (k < ksplit ? ksA[k] : ksB[k - ksplit]); scr[(2 * i + (lane >> 5)) * 33 + (lane & 31)] = x; }
;     LDS_WAIT(); asm volatile("" ::: "memory");
;     const int c = lane & 7;
; #pragma unroll
;     for (int j = 0; j < 4; ++j) { const int n = (lane >> 3) + 8 * j; const LAS float* s = scr + (8 * c) * 33 + n;
;         const unsigned long long o = (unsigned long long)pg8::pk4_fp8(s[0 * 33], s[1 * 33], s[2 * 33], s[3 * 33]) | ((unsigned long long)pg8::pk4_fp8(s[4 * 33], s[5 * 33], s[6 * 33], s[7 * 33]) << 32);
;         *(GAS unsigned long long*)(WT + (size_t)(n0 + n) * K + k0 + 8 * c) = o; }
	v_max_f32_e32 v226, v226, v226
	v_max_f32_e32 v227, v227, v227
	v_max_f32_e32 v228, v228, v228
	v_max_f32_e32 v229, v229, v229
	v_max_f32_e32 v230, v230, v230
	v_max_f32_e32 v231, v231, v231
	v_max_f32_e32 v232, v232, v232
	v_max_f32_e32 v233, v233, v233
	v_max_f32_e32 v234, v234, v234
	v_max_f32_e32 v235, v235, v235
	v_max_f32_e32 v236, v236, v236
	v_max_f32_e32 v237, v237, v237
	v_max_f32_e32 v238, v238, v238
	v_max_f32_e32 v239, v239, v239
	v_max_f32_e32 v240, v240, v240
	v_max_f32_e32 v241, v241, v241
	v_med3_f32 v226, v226, s62, v95
	v_med3_f32 v227, v227, s62, v95
	v_med3_f32 v228, v228, s62, v95
	v_med3_f32 v229, v229, s62, v95
	v_med3_f32 v230, v230, s62, v95
	v_med3_f32 v231, v231, s62, v95
	v_med3_f32 v232, v232, s62, v95
	v_med3_f32 v233, v233, s62, v95
	v_med3_f32 v234, v234, s62, v95
	v_med3_f32 v235, v235, s62, v95
	v_med3_f32 v236, v236, s62, v95
	v_med3_f32 v237, v237, s62, v95
	v_med3_f32 v238, v238, s62, v95
	v_med3_f32 v239, v239, s62, v95
	v_med3_f32 v240, v240, s62, v95
	v_med3_f32 v241, v241, s62, v95
	v_mov_b32_e32 v242, 0
	v_mov_b32_e32 v243, 0
	v_mov_b32_e32 v244, 0
	v_mov_b32_e32 v245, 0
	v_cvt_pk_fp8_f32 v242, v226, v227
	v_cvt_pk_fp8_f32 v243, v230, v231
	v_cvt_pk_fp8_f32 v244, v234, v235
	v_cvt_pk_fp8_f32 v245, v238, v239
	v_cvt_pk_fp8_f32 v242, v228, v229 op_sel:[0,0,1]
	v_cvt_pk_fp8_f32 v243, v232, v233 op_sel:[0,0,1]
	v_cvt_pk_fp8_f32 v244, v236, v237 op_sel:[0,0,1]
	v_cvt_pk_fp8_f32 v245, v240, v241 op_sel:[0,0,1]
	s_nop 0
	global_store_dwordx4 v80, v[242:245], s[6:7]
	s_waitcnt vmcnt(12)
	v_mul_f32_e32 v176, 0x43000000, v176
	v_mul_f32_e32 v177, 0x43000000, v177
	v_mul_f32_e32 v178, 0x43000000, v178
	v_mul_f32_e32 v179, 0x43000000, v179
	ds_write_b128 v210, v[176:179]
	v_mul_f32_e32 v180, 0x43000000, v180
	v_mul_f32_e32 v181, 0x43000000, v181
	v_mul_f32_e32 v182, 0x43000000, v182
	v_mul_f32_e32 v183, 0x43000000, v183
	ds_write_b128 v210, v[180:183] offset:1024
	v_mul_f32_e32 v184, 0x43000000, v184
	v_mul_f32_e32 v185, 0x43000000, v185
	v_mul_f32_e32 v186, 0x43000000, v186
	v_mul_f32_e32 v187, 0x43000000, v187
	ds_write_b128 v210, v[184:187] offset:2048
	v_mul_f32_e32 v188, 0x43000000, v188
	v_mul_f32_e32 v189, 0x43000000, v189
	v_mul_f32_e32 v190, 0x43000000, v190
	v_mul_f32_e32 v191, 0x43000000, v191
	ds_write_b128 v210, v[188:191] offset:3072
	v_mul_f32_e32 v192, 0x43000000, v192
	v_mul_f32_e32 v193, 0x43000000, v193
	v_mul_f32_e32 v194, 0x43000000, v194
	v_mul_f32_e32 v195, 0x43000000, v195
	ds_write_b128 v210, v[192:195] offset:4096
	v_mul_f32_e32 v196, 0x43000000, v196
	v_mul_f32_e32 v197, 0x43000000, v197
	v_mul_f32_e32 v198, 0x43000000, v198
	v_mul_f32_e32 v199, 0x43000000, v199
	ds_write_b128 v210, v[196:199] offset:5120
	v_mul_f32_e32 v200, 0x43000000, v200
	v_mul_f32_e32 v201, 0x43000000, v201
	v_mul_f32_e32 v202, 0x43000000, v202
	v_mul_f32_e32 v203, 0x43000000, v203
	ds_write_b128 v210, v[200:203] offset:6144
	v_mul_f32_e32 v204, 0x43000000, v204
	v_mul_f32_e32 v205, 0x43000000, v205
	v_mul_f32_e32 v206, 0x43000000, v206
	v_mul_f32_e32 v207, 0x43000000, v207
	ds_write_b128 v210, v[204:207] offset:7168
	s_waitcnt lgkmcnt(0)
	s_barrier
	s_add_u32 s8, s42, 0x3000
	s_addc_u32 s9, s43, 0
	global_load_dwordx4 v[176:179], v75, s[8:9]
	s_add_u32 s8, s8, 0x8000
	s_addc_u32 s9, s9, 0
	global_load_dwordx4 v[180:183], v75, s[8:9]
	s_add_u32 s8, s8, 0x8000
	s_addc_u32 s9, s9, 0
	global_load_dwordx4 v[184:187], v75, s[8:9]
	s_add_u32 s8, s8, 0x8000
	s_addc_u32 s9, s9, 0
	global_load_dwordx4 v[188:191], v75, s[8:9]
	s_add_u32 s8, s8, 0x8000
	s_addc_u32 s9, s9, 0
	global_load_dwordx4 v[192:195], v75, s[8:9]
	s_add_u32 s8, s8, 0x8000
	s_addc_u32 s9, s9, 0
	global_load_dwordx4 v[196:199], v75, s[8:9]
	s_add_u32 s8, s8, 0x8000
	s_addc_u32 s9, s9, 0
	global_load_dwordx4 v[200:203], v75, s[8:9]
	s_add_u32 s8, s8, 0x8000
	s_addc_u32 s9, s9, 0
	global_load_dwordx4 v[204:207], v75, s[8:9]
	s_add_u32 s6, s44, 0x1000000
	s_addc_u32 s7, s45, 0
	ds_read_b32 v226, v212
	ds_read_b32 v227, v212 offset:512
	ds_read_b32 v228, v212 offset:1024
	ds_read_b32 v229, v212 offset:1536
	ds_read_b32 v230, v212 offset:2048
	ds_read_b32 v231, v212 offset:2560
	ds_read_b32 v232, v212 offset:3072
	ds_read_b32 v233, v212 offset:3584
	ds_read_b32 v234, v212 offset:4096
	ds_read_b32 v235, v212 offset:4608
	ds_read_b32 v236, v212 offset:5120
	ds_read_b32 v237, v212 offset:5632
	ds_read_b32 v238, v212 offset:6144
	ds_read_b32 v239, v212 offset:6656
	ds_read_b32 v240, v212 offset:7168
	ds_read_b32 v241, v212 offset:7680
	s_waitcnt lgkmcnt(0)
	v_max_f32_e32 v226, v226, v226
	v_max_f32_e32 v227, v227, v227
	v_max_f32_e32 v228, v228, v228
	v_max_f32_e32 v229, v229, v229
	v_max_f32_e32 v230, v230, v230
	v_max_f32_e32 v231, v231, v231
	v_max_f32_e32 v232, v232, v232
	v_max_f32_e32 v233, v233, v233
	v_max_f32_e32 v234, v234, v234
	v_max_f32_e32 v235, v235, v235
	v_max_f32_e32 v236, v236, v236
	v_max_f32_e32 v237, v237, v237
	v_max_f32_e32 v238, v238, v238
	v_max_f32_e32 v239, v239, v239
	v_max_f32_e32 v240, v240, v240
	v_max_f32_e32 v241, v241, v241
	v_med3_f32 v226, v226, s62, v95
	v_med3_f32 v227, v227, s62, v95
	v_med3_f32 v228, v228, s62, v95
	v_med3_f32 v229, v229, s62, v95
	v_med3_f32 v230, v230, s62, v95
	v_med3_f32 v231, v231, s62, v95
	v_med3_f32 v232, v232, s62, v95
	v_med3_f32 v233, v233, s62, v95
	v_med3_f32 v234, v234, s62, v95
	v_med3_f32 v235, v235, s62, v95
	v_med3_f32 v236, v236, s62, v95
	v_med3_f32 v237, v237, s62, v95
	v_med3_f32 v238, v238, s62, v95
	v_med3_f32 v239, v239, s62, v95
	v_med3_f32 v240, v240, s62, v95
	v_med3_f32 v241, v241, s62, v95
	v_mov_b32_e32 v242, 0
	v_mov_b32_e32 v243, 0
	v_mov_b32_e32 v244, 0
	v_mov_b32_e32 v245, 0
	v_cvt_pk_fp8_f32 v242, v226, v227
	v_cvt_pk_fp8_f32 v243, v230, v231
	v_cvt_pk_fp8_f32 v244, v234, v235
	v_cvt_pk_fp8_f32 v245, v238, v239
	v_cvt_pk_fp8_f32 v242, v228, v229 op_sel:[0,0,1]
	v_cvt_pk_fp8_f32 v243, v232, v233 op_sel:[0,0,1]
	v_cvt_pk_fp8_f32 v244, v236, v237 op_sel:[0,0,1]
	v_cvt_pk_fp8_f32 v245, v240, v241 op_sel:[0,0,1]
	s_nop 0
	global_store_dwordx4 v79, v[242:245], s[6:7]
	ds_read_b32 v226, v214
	ds_read_b32 v227, v214 offset:512
	ds_read_b32 v228, v214 offset:1024
	ds_read_b32 v229, v214 offset:1536
	ds_read_b32 v230, v214 offset:2048
	ds_read_b32 v231, v214 offset:2560
	ds_read_b32 v232, v214 offset:3072
	ds_read_b32 v233, v214 offset:3584
	ds_read_b32 v234, v214 offset:4096
	ds_read_b32 v235, v214 offset:4608
	ds_read_b32 v236, v214 offset:5120
	ds_read_b32 v237, v214 offset:5632
	ds_read_b32 v238, v214 offset:6144
	ds_read_b32 v239, v214 offset:6656
	ds_read_b32 v240, v214 offset:7168
	ds_read_b32 v241, v214 offset:7680
	s_waitcnt lgkmcnt(0)
; #define GAS __attribute__((address_space(1)))
; #define LAS __attribute__((address_space(3)))
; #define LDS_WAIT() asm volatile("s_waitcnt lgkmcnt(0)" ::: "memory")
; __device__ __forceinline__ unsigned pk2(float lo, float hi) { return f2bf(lo) | (f2bf(hi) << 16); }
; __device__ __forceinline__ int nat_dim(int p) { return (p >> 1) + 64 * (p & 1); }
; template <int MAP, bool KS, bool KPERM = false>
; __device__ __forceinline__ void p0_transpose_item(const float* W, int K, int Nsrc, int nblk, bf16* WT, const float* ksA, const float* ksB, int ksplit, LAS float* scr, int item, int lane) {
;     ...
;     for (int i = 0; i < 32; ++i) { const int k = k0 + 2 * i + (lane >> 5); const int ksrc = KPERM ? ((k & ~127) + nat_dim(k & 127)) : k;
;         v[i] = sc >= 0 ? W[(size_t)ksrc * Nsrc + sc] : 0.f; }
; #pragma unroll
;     for (int i = 0; i < 32; ++i) { const int kk = 2 * i + (lane >> 5); const int k = k0 + kk;
;         if (KS) v[i] *= (k < ksplit ? ksA[k] : ksB[k - ksplit]);
;         scr[kk * 33 + (lane & 31)] = v[i]; }
;     LDS_WAIT(); asm volatile("" ::: "memory");
;     const int c = lane & 7;
; #pragma unroll
;     for (int j = 0; j < 4; ++j) { const int n = (lane >> 3) + 8 * j; const LAS float* s = scr + (8 * c) * 33 + n;
;         v4u o; o.x = pk2(s[0 * 33], s[1 * 33]); o.y = pk2(s[2 * 33], s[3 * 33]); o.z = pk2(s[4 * 33], s[5 * 33]); o.w = pk2(s[6 * 33], s[7 * 33]);
;         *(GAS v4u*)(WT + (size_t)(n0 + n) * K + k0 + 8 * c) = o; }
;     ...
;     for (int i = 0; i < 32; ++i) v[i] = sc >= 0 ? W[(size_t)(k0 + 2 * i + (lane >> 5)) * Nsrc + sc] : 0.f;
; #pragma unroll
;     for (int i = 0; i < 32; ++i) { const int k = k0 + 2 * i + (lane >> 5); float x = v[i] * wscale; if (KS) x *= (k < ksplit ? ksA[k] : ksB[k - ksplit]); scr[(2 * i + (lane >> 5)) * 33 + (lane & 31)] = x; }
;     LDS_WAIT(); asm volatile("" ::: "memory");
;     const int c = lane & 7;
; #pragma unroll
;     for (int j = 0; j < 4; ++j) { const int n = (lane >> 3) + 8 * j; const LAS float* s = scr + (8 * c) * 33 + n;
;         const unsigned long long o = (unsigned long long)pg8::pk4_fp8(s[0 * 33], s[1 * 33], s[2 * 33], s[3 * 33]) | ((unsigned long long)pg8::pk4_fp8(s[4 * 33], s[5 * 33], s[6 * 33], s[7 * 33]) << 32);
;         *(GAS unsigned long long*)(WT + (size_t)(n0 + n) * K + k0 + 8 * c) = o; }
	v_max_f32_e32 v226, v226, v226
	v_max_f32_e32 v227, v227, v227
	v_max_f32_e32 v228, v228, v228
	v_max_f32_e32 v229, v229, v229
	v_max_f32_e32 v230, v230, v230
	v_max_f32_e32 v231, v231, v231
	v_max_f32_e32 v232, v232, v232
	v_max_f32_e32 v233, v233, v233
	v_max_f32_e32 v234, v234, v234
	v_max_f32_e32 v235, v235, v235
	v_max_f32_e32 v236, v236, v236
	v_max_f32_e32 v237, v237, v237
	v_max_f32_e32 v238, v238, v238
	v_max_f32_e32 v239, v239, v239
	v_max_f32_e32 v240, v240, v240
	v_max_f32_e32 v241, v241, v241
	v_med3_f32 v226, v226, s62, v95
	v_med3_f32 v227, v227, s62, v95
	v_med3_f32 v228, v228, s62, v95
	v_med3_f32 v229, v229, s62, v95
	v_med3_f32 v230, v230, s62, v95
	v_med3_f32 v231, v231, s62, v95
	v_med3_f32 v232, v232, s62, v95
	v_med3_f32 v233, v233, s62, v95
	v_med3_f32 v234, v234, s62, v95
	v_med3_f32 v235, v235, s62, v95
	v_med3_f32 v236, v236, s62, v95
	v_med3_f32 v237, v237, s62, v95
	v_med3_f32 v238, v238, s62, v95
	v_med3_f32 v239, v239, s62, v95
	v_med3_f32 v240, v240, s62, v95
	v_med3_f32 v241, v241, s62, v95
	v_mov_b32_e32 v242, 0
	v_mov_b32_e32 v243, 0
	v_mov_b32_e32 v244, 0
	v_mov_b32_e32 v245, 0
	v_cvt_pk_fp8_f32 v242, v226, v227
	v_cvt_pk_fp8_f32 v243, v230, v231
	v_cvt_pk_fp8_f32 v244, v234, v235
	v_cvt_pk_fp8_f32 v245, v238, v239
	v_cvt_pk_fp8_f32 v242, v228, v229 op_sel:[0,0,1]
	v_cvt_pk_fp8_f32 v243, v232, v233 op_sel:[0,0,1]
	v_cvt_pk_fp8_f32 v244, v236, v237 op_sel:[0,0,1]
	v_cvt_pk_fp8_f32 v245, v240, v241 op_sel:[0,0,1]
	s_nop 0
	global_store_dwordx4 v80, v[242:245], s[6:7]
	s_waitcnt vmcnt(12)
	v_mul_f32_e32 v144, 0x43000000, v144
	v_mul_f32_e32 v145, 0x43000000, v145
	v_mul_f32_e32 v146, 0x43000000, v146
	v_mul_f32_e32 v147, 0x43000000, v147
	ds_write_b128 v209, v[144:147]
	v_mul_f32_e32 v148, 0x43000000, v148
	v_mul_f32_e32 v149, 0x43000000, v149
	v_mul_f32_e32 v150, 0x43000000, v150
	v_mul_f32_e32 v151, 0x43000000, v151
	ds_write_b128 v209, v[148:151] offset:1024
	v_mul_f32_e32 v152, 0x43000000, v152
	v_mul_f32_e32 v153, 0x43000000, v153
	v_mul_f32_e32 v154, 0x43000000, v154
	v_mul_f32_e32 v155, 0x43000000, v155
	ds_write_b128 v209, v[152:155] offset:2048
	v_mul_f32_e32 v156, 0x43000000, v156
	v_mul_f32_e32 v157, 0x43000000, v157
	v_mul_f32_e32 v158, 0x43000000, v158
	v_mul_f32_e32 v159, 0x43000000, v159
	ds_write_b128 v209, v[156:159] offset:3072
	v_mul_f32_e32 v160, 0x43000000, v160
	v_mul_f32_e32 v161, 0x43000000, v161
	v_mul_f32_e32 v162, 0x43000000, v162
	v_mul_f32_e32 v163, 0x43000000, v163
	ds_write_b128 v209, v[160:163] offset:4096
	v_mul_f32_e32 v164, 0x43000000, v164
	v_mul_f32_e32 v165, 0x43000000, v165
	v_mul_f32_e32 v166, 0x43000000, v166
	v_mul_f32_e32 v167, 0x43000000, v167
	ds_write_b128 v209, v[164:167] offset:5120
	v_mul_f32_e32 v168, 0x43000000, v168
	v_mul_f32_e32 v169, 0x43000000, v169
	v_mul_f32_e32 v170, 0x43000000, v170
	v_mul_f32_e32 v171, 0x43000000, v171
	ds_write_b128 v209, v[168:171] offset:6144
	v_mul_f32_e32 v172, 0x43000000, v172
	v_mul_f32_e32 v173, 0x43000000, v173
	v_mul_f32_e32 v174, 0x43000000, v174
	v_mul_f32_e32 v175, 0x43000000, v175
	ds_write_b128 v209, v[172:175] offset:7168
	s_waitcnt lgkmcnt(0)
	s_barrier
	s_add_i32 s24, s23, 0
	s_lshl_b32 s20, s24, 7
	s_cmp_lt_u32 s24, 40
	s_cselect_b32 s21, 0, 0x830
	s_cmp_lt_u32 s24, 72
	s_cselect_b32 s21, s21, 0xfffff030
	s_add_i32 s20, s20, s21
	s_lshl_b32 s20, s20, 2
	s_add_u32 s8, s46, s20
	s_addc_u32 s9, s47, 0
	global_load_dwordx4 v[144:147], v76, s[8:9]
	s_add_u32 s8, s8, 0x16280
	s_addc_u32 s9, s9, 0
	global_load_dwordx4 v[148:151], v76, s[8:9]
	s_add_u32 s8, s8, 0x16280
	s_addc_u32 s9, s9, 0
	global_load_dwordx4 v[152:155], v76, s[8:9]
	s_add_u32 s8, s8, 0x16280
	s_addc_u32 s9, s9, 0
	global_load_dwordx4 v[156:159], v76, s[8:9]
	s_add_u32 s8, s8, 0x16280
	s_addc_u32 s9, s9, 0
	global_load_dwordx4 v[160:163], v76, s[8:9]
	s_add_u32 s8, s8, 0x16280
	s_addc_u32 s9, s9, 0
	global_load_dwordx4 v[164:167], v76, s[8:9]
	s_add_u32 s8, s8, 0x16280
	s_addc_u32 s9, s9, 0
	global_load_dwordx4 v[168:171], v76, s[8:9]
	s_add_u32 s8, s8, 0x16280
	s_addc_u32 s9, s9, 0
	global_load_dwordx4 v[172:175], v76, s[8:9]
	s_add_u32 s6, s44, 0x2000000
	s_addc_u32 s7, s45, 0
	ds_read_b32 v226, v211
	ds_read_b32 v227, v211 offset:512
	ds_read_b32 v228, v211 offset:1024
	ds_read_b32 v229, v211 offset:1536
	ds_read_b32 v230, v211 offset:2048
	ds_read_b32 v231, v211 offset:2560
	ds_read_b32 v232, v211 offset:3072
	ds_read_b32 v233, v211 offset:3584
	ds_read_b32 v234, v211 offset:4096
	ds_read_b32 v235, v211 offset:4608
	ds_read_b32 v236, v211 offset:5120
	ds_read_b32 v237, v211 offset:5632
	ds_read_b32 v238, v211 offset:6144
	ds_read_b32 v239, v211 offset:6656
	ds_read_b32 v240, v211 offset:7168
	ds_read_b32 v241, v211 offset:7680
	s_waitcnt lgkmcnt(0)
; #define GAS __attribute__((address_space(1)))
; #define LAS __attribute__((address_space(3)))
; #define LDS_WAIT() asm volatile("s_waitcnt lgkmcnt(0)" ::: "memory")
;     ...
;     for (int i = 0; i < 32; ++i) v[i] = sc >= 0 ? W[(size_t)(k0 + 2 * i + (lane >> 5)) * Nsrc + sc] : 0.f;
; #pragma unroll
;     for (int i = 0; i < 32; ++i) { const int k = k0 + 2 * i + (lane >> 5); float x = v[i] * wscale; if (KS) x *= (k < ksplit ? ksA[k] : ksB[k - ksplit]); scr[(2 * i + (lane >> 5)) * 33 + (lane & 31)] = x; }
;     LDS_WAIT(); asm volatile("" ::: "memory");
;     const int c = lane & 7;
; #pragma unroll
;     for (int j = 0; j < 4; ++j) { const int n = (lane >> 3) + 8 * j; const LAS float* s = scr + (8 * c) * 33 + n;
;         const unsigned long long o = (unsigned long long)pg8::pk4_fp8(s[0 * 33], s[1 * 33], s[2 * 33], s[3 * 33]) | ((unsigned long long)pg8::pk4_fp8(s[4 * 33], s[5 * 33], s[6 * 33], s[7 * 33]) << 32);
;         *(GAS unsigned long long*)(WT + (size_t)(n0 + n) * K + k0 + 8 * c) = o; }
	v_max_f32_e32 v226, v226, v226
	v_max_f32_e32 v227, v227, v227
	v_max_f32_e32 v228, v228, v228
	v_max_f32_e32 v229, v229, v229
	v_max_f32_e32 v230, v230, v230
	v_max_f32_e32 v231, v231, v231
	v_max_f32_e32 v232, v232, v232
	v_max_f32_e32 v233, v233, v233
	v_max_f32_e32 v234, v234, v234
	v_max_f32_e32 v235, v235, v235
	v_max_f32_e32 v236, v236, v236
	v_max_f32_e32 v237, v237, v237
	v_max_f32_e32 v238, v238, v238
	v_max_f32_e32 v239, v239, v239
	v_max_f32_e32 v240, v240, v240
	v_max_f32_e32 v241, v241, v241
	v_med3_f32 v226, v226, s62, v95
	v_med3_f32 v227, v227, s62, v95
	v_med3_f32 v228, v228, s62, v95
	v_med3_f32 v229, v229, s62, v95
	v_med3_f32 v230, v230, s62, v95
	v_med3_f32 v231, v231, s62, v95
	v_med3_f32 v232, v232, s62, v95
	v_med3_f32 v233, v233, s62, v95
	v_med3_f32 v234, v234, s62, v95
	v_med3_f32 v235, v235, s62, v95
	v_med3_f32 v236, v236, s62, v95
	v_med3_f32 v237, v237, s62, v95
	v_med3_f32 v238, v238, s62, v95
	v_med3_f32 v239, v239, s62, v95
	v_med3_f32 v240, v240, s62, v95
	v_med3_f32 v241, v241, s62, v95
	v_mov_b32_e32 v242, 0
	v_mov_b32_e32 v243, 0
	v_mov_b32_e32 v244, 0
	v_mov_b32_e32 v245, 0
	v_cvt_pk_fp8_f32 v242, v226, v227
	v_cvt_pk_fp8_f32 v243, v230, v231
	v_cvt_pk_fp8_f32 v244, v234, v235
	v_cvt_pk_fp8_f32 v245, v238, v239
	v_cvt_pk_fp8_f32 v242, v228, v229 op_sel:[0,0,1]
	v_cvt_pk_fp8_f32 v243, v232, v233 op_sel:[0,0,1]
	v_cvt_pk_fp8_f32 v244, v236, v237 op_sel:[0,0,1]
	v_cvt_pk_fp8_f32 v245, v240, v241 op_sel:[0,0,1]
	s_nop 0
	global_store_dwordx4 v79, v[242:245], s[6:7]
	ds_read_b32 v226, v213
	ds_read_b32 v227, v213 offset:512
	ds_read_b32 v228, v213 offset:1024
	ds_read_b32 v229, v213 offset:1536
	ds_read_b32 v230, v213 offset:2048
	ds_read_b32 v231, v213 offset:2560
	ds_read_b32 v232, v213 offset:3072
	ds_read_b32 v233, v213 offset:3584
	ds_read_b32 v234, v213 offset:4096
	ds_read_b32 v235, v213 offset:4608
	ds_read_b32 v236, v213 offset:5120
	ds_read_b32 v237, v213 offset:5632
	ds_read_b32 v238, v213 offset:6144
	ds_read_b32 v239, v213 offset:6656
	ds_read_b32 v240, v213 offset:7168
	ds_read_b32 v241, v213 offset:7680
	s_waitcnt lgkmcnt(0)
	v_max_f32_e32 v226, v226, v226
	v_max_f32_e32 v227, v227, v227
	v_max_f32_e32 v228, v228, v228
	v_max_f32_e32 v229, v229, v229
	v_max_f32_e32 v230, v230, v230
	v_max_f32_e32 v231, v231, v231
	v_max_f32_e32 v232, v232, v232
	v_max_f32_e32 v233, v233, v233
	v_max_f32_e32 v234, v234, v234
	v_max_f32_e32 v235, v235, v235
	v_max_f32_e32 v236, v236, v236
	v_max_f32_e32 v237, v237, v237
	v_max_f32_e32 v238, v238, v238
	v_max_f32_e32 v239, v239, v239
	v_max_f32_e32 v240, v240, v240
	v_max_f32_e32 v241, v241, v241
	v_med3_f32 v226, v226, s62, v95
	v_med3_f32 v227, v227, s62, v95
	v_med3_f32 v228, v228, s62, v95
	v_med3_f32 v229, v229, s62, v95
	v_med3_f32 v230, v230, s62, v95
	v_med3_f32 v231, v231, s62, v95
	v_med3_f32 v232, v232, s62, v95
	v_med3_f32 v233, v233, s62, v95
	v_med3_f32 v234, v234, s62, v95
	v_med3_f32 v235, v235, s62, v95
	v_med3_f32 v236, v236, s62, v95
	v_med3_f32 v237, v237, s62, v95
	v_med3_f32 v238, v238, s62, v95
	v_med3_f32 v239, v239, s62, v95
	v_med3_f32 v240, v240, s62, v95
	v_med3_f32 v241, v241, s62, v95
	v_mov_b32_e32 v242, 0
	v_mov_b32_e32 v243, 0
	v_mov_b32_e32 v244, 0
	v_mov_b32_e32 v245, 0
	v_cvt_pk_fp8_f32 v242, v226, v227
	v_cvt_pk_fp8_f32 v243, v230, v231
	v_cvt_pk_fp8_f32 v244, v234, v235
	v_cvt_pk_fp8_f32 v245, v238, v239
	v_cvt_pk_fp8_f32 v242, v228, v229 op_sel:[0,0,1]
	v_cvt_pk_fp8_f32 v243, v232, v233 op_sel:[0,0,1]
	v_cvt_pk_fp8_f32 v244, v236, v237 op_sel:[0,0,1]
	v_cvt_pk_fp8_f32 v245, v240, v241 op_sel:[0,0,1]
	s_nop 0
	global_store_dwordx4 v80, v[242:245], s[6:7]
	s_waitcnt vmcnt(12)
	v_mul_f32_e32 v176, 0x43000000, v176
	v_mul_f32_e32 v177, 0x43000000, v177
	v_mul_f32_e32 v178, 0x43000000, v178
	v_mul_f32_e32 v179, 0x43000000, v179
	ds_write_b128 v210, v[176:179]
	v_mul_f32_e32 v180, 0x43000000, v180
	v_mul_f32_e32 v181, 0x43000000, v181
	v_mul_f32_e32 v182, 0x43000000, v182
	v_mul_f32_e32 v183, 0x43000000, v183
	ds_write_b128 v210, v[180:183] offset:1024
	v_mul_f32_e32 v184, 0x43000000, v184
	v_mul_f32_e32 v185, 0x43000000, v185
	v_mul_f32_e32 v186, 0x43000000, v186
	v_mul_f32_e32 v187, 0x43000000, v187
	ds_write_b128 v210, v[184:187] offset:2048
	v_mul_f32_e32 v188, 0x43000000, v188
	v_mul_f32_e32 v189, 0x43000000, v189
	v_mul_f32_e32 v190, 0x43000000, v190
	v_mul_f32_e32 v191, 0x43000000, v191
	ds_write_b128 v210, v[188:191] offset:3072
	v_mul_f32_e32 v192, 0x43000000, v192
	v_mul_f32_e32 v193, 0x43000000, v193
	v_mul_f32_e32 v194, 0x43000000, v194
	v_mul_f32_e32 v195, 0x43000000, v195
	ds_write_b128 v210, v[192:195] offset:4096
	v_mul_f32_e32 v196, 0x43000000, v196
	v_mul_f32_e32 v197, 0x43000000, v197
	v_mul_f32_e32 v198, 0x43000000, v198
	v_mul_f32_e32 v199, 0x43000000, v199
	ds_write_b128 v210, v[196:199] offset:5120
	v_mul_f32_e32 v200, 0x43000000, v200
	v_mul_f32_e32 v201, 0x43000000, v201
	v_mul_f32_e32 v202, 0x43000000, v202
	v_mul_f32_e32 v203, 0x43000000, v203
	ds_write_b128 v210, v[200:203] offset:6144
	v_mul_f32_e32 v204, 0x43000000, v204
	v_mul_f32_e32 v205, 0x43000000, v205
	v_mul_f32_e32 v206, 0x43000000, v206
	v_mul_f32_e32 v207, 0x43000000, v207
	ds_write_b128 v210, v[204:207] offset:7168
	s_waitcnt lgkmcnt(0)
	s_barrier
; #define GAS __attribute__((address_space(1)))
; #define LAS __attribute__((address_space(3)))
; #define LDS_WAIT() asm volatile("s_waitcnt lgkmcnt(0)" ::: "memory")
; __device__ __forceinline__ unsigned pk2(float lo, float hi) { return f2bf(lo) | (f2bf(hi) << 16); }
; __device__ __forceinline__ int nat_dim(int p) { return (p >> 1) + 64 * (p & 1); }
; template <int MAP, bool KS, bool KPERM = false>
; __device__ __forceinline__ void p0_transpose_item(const float* W, int K, int Nsrc, int nblk, bf16* WT, const float* ksA, const float* ksB, int ksplit, LAS float* scr, int item, int lane) {
;     ...
;     for (int i = 0; i < 32; ++i) { const int k = k0 + 2 * i + (lane >> 5); const int ksrc = KPERM ? ((k & ~127) + nat_dim(k & 127)) : k;
;         v[i] = sc >= 0 ? W[(size_t)ksrc * Nsrc + sc] : 0.f; }
; #pragma unroll
;     for (int i = 0; i < 32; ++i) { const int kk = 2 * i + (lane >> 5); const int k = k0 + kk;
;         if (KS) v[i] *= (k < ksplit ? ksA[k] : ksB[k - ksplit]);
;         scr[kk * 33 + (lane & 31)] = v[i]; }
;     LDS_WAIT(); asm volatile("" ::: "memory");
;     const int c = lane & 7;
; #pragma unroll
;     for (int j = 0; j < 4; ++j) { const int n = (lane >> 3) + 8 * j; const LAS float* s = scr + (8 * c) * 33 + n;
;         v4u o; o.x = pk2(s[0 * 33], s[1 * 33]); o.y = pk2(s[2 * 33], s[3 * 33]); o.z = pk2(s[4 * 33], s[5 * 33]); o.w = pk2(s[6 * 33], s[7 * 33]);
;         *(GAS v4u*)(WT + (size_t)(n0 + n) * K + k0 + 8 * c) = o; }
;     ...
;     for (int i = 0; i < 32; ++i) v[i] = sc >= 0 ? W[(size_t)(k0 + 2 * i + (lane >> 5)) * Nsrc + sc] : 0.f;
; #pragma unroll
;     for (int i = 0; i < 32; ++i) { const int k = k0 + 2 * i + (lane >> 5); float x = v[i] * wscale; if (KS) x *= (k < ksplit ? ksA[k] : ksB[k - ksplit]); scr[(2 * i + (lane >> 5)) * 33 + (lane & 31)] = x; }
;     LDS_WAIT(); asm volatile("" ::: "memory");
;     const int c = lane & 7;
; #pragma unroll
;     for (int j = 0; j < 4; ++j) { const int n = (lane >> 3) + 8 * j; const LAS float* s = scr + (8 * c) * 33 + n;
;         const unsigned long long o = (unsigned long long)pg8::pk4_fp8(s[0 * 33], s[1 * 33], s[2 * 33], s[3 * 33]) | ((unsigned long long)pg8::pk4_fp8(s[4 * 33], s[5 * 33], s[6 * 33], s[7 * 33]) << 32);
;         *(GAS unsigned long long*)(WT + (size_t)(n0 + n) * K + k0 + 8 * c) = o; }
	s_add_i32 s24, s23, 8
	s_lshl_b32 s20, s24, 7
	s_cmp_lt_u32 s24, 40
	s_cselect_b32 s21, 0, 0x830
	s_cmp_lt_u32 s24, 72
	s_cselect_b32 s21, s21, 0xfffff030
	s_add_i32 s20, s20, s21
	s_lshl_b32 s20, s20, 2
	s_add_u32 s8, s46, s20
	s_addc_u32 s9, s47, 0
	global_load_dwordx4 v[176:179], v76, s[8:9]
	s_add_u32 s8, s8, 0x16280
	s_addc_u32 s9, s9, 0
	global_load_dwordx4 v[180:183], v76, s[8:9]
	s_add_u32 s8, s8, 0x16280
	s_addc_u32 s9, s9, 0
	global_load_dwordx4 v[184:187], v76, s[8:9]
	s_add_u32 s8, s8, 0x16280
	s_addc_u32 s9, s9, 0
	global_load_dwordx4 v[188:191], v76, s[8:9]
	s_add_u32 s8, s8, 0x16280
	s_addc_u32 s9, s9, 0
	global_load_dwordx4 v[192:195], v76, s[8:9]
	s_add_u32 s8, s8, 0x16280
	s_addc_u32 s9, s9, 0
	global_load_dwordx4 v[196:199], v76, s[8:9]
	s_add_u32 s8, s8, 0x16280
	s_addc_u32 s9, s9, 0
	global_load_dwordx4 v[200:203], v76, s[8:9]
	s_add_u32 s8, s8, 0x16280
	s_addc_u32 s9, s9, 0
	global_load_dwordx4 v[204:207], v76, s[8:9]
	s_add_u32 s6, s44, 0x3000000
	s_addc_u32 s7, s45, 0
	ds_read_b32 v226, v212
	ds_read_b32 v227, v212 offset:512
	ds_read_b32 v228, v212 offset:1024
	ds_read_b32 v229, v212 offset:1536
	ds_read_b32 v230, v212 offset:2048
	ds_read_b32 v231, v212 offset:2560
	ds_read_b32 v232, v212 offset:3072
	ds_read_b32 v233, v212 offset:3584
	ds_read_b32 v234, v212 offset:4096
	ds_read_b32 v235, v212 offset:4608
	ds_read_b32 v236, v212 offset:5120
	ds_read_b32 v237, v212 offset:5632
	ds_read_b32 v238, v212 offset:6144
	ds_read_b32 v239, v212 offset:6656
	ds_read_b32 v240, v212 offset:7168
	ds_read_b32 v241, v212 offset:7680
	s_waitcnt lgkmcnt(0)
	v_max_f32_e32 v226, v226, v226
	v_max_f32_e32 v227, v227, v227
	v_max_f32_e32 v228, v228, v228
	v_max_f32_e32 v229, v229, v229
	v_max_f32_e32 v230, v230, v230
	v_max_f32_e32 v231, v231, v231
	v_max_f32_e32 v232, v232, v232
	v_max_f32_e32 v233, v233, v233
	v_max_f32_e32 v234, v234, v234
	v_max_f32_e32 v235, v235, v235
	v_max_f32_e32 v236, v236, v236
	v_max_f32_e32 v237, v237, v237
	v_max_f32_e32 v238, v238, v238
	v_max_f32_e32 v239, v239, v239
	v_max_f32_e32 v240, v240, v240
	v_max_f32_e32 v241, v241, v241
	v_med3_f32 v226, v226, s62, v95
	v_med3_f32 v227, v227, s62, v95
	v_med3_f32 v228, v228, s62, v95
	v_med3_f32 v229, v229, s62, v95
	v_med3_f32 v230, v230, s62, v95
	v_med3_f32 v231, v231, s62, v95
	v_med3_f32 v232, v232, s62, v95
	v_med3_f32 v233, v233, s62, v95
	v_med3_f32 v234, v234, s62, v95
	v_med3_f32 v235, v235, s62, v95
	v_med3_f32 v236, v236, s62, v95
	v_med3_f32 v237, v237, s62, v95
	v_med3_f32 v238, v238, s62, v95
	v_med3_f32 v239, v239, s62, v95
	v_med3_f32 v240, v240, s62, v95
	v_med3_f32 v241, v241, s62, v95
	v_mov_b32_e32 v242, 0
	v_mov_b32_e32 v243, 0
	v_mov_b32_e32 v244, 0
	v_mov_b32_e32 v245, 0
	v_cvt_pk_fp8_f32 v242, v226, v227
	v_cvt_pk_fp8_f32 v243, v230, v231
	v_cvt_pk_fp8_f32 v244, v234, v235
	v_cvt_pk_fp8_f32 v245, v238, v239
	v_cvt_pk_fp8_f32 v242, v228, v229 op_sel:[0,0,1]
	v_cvt_pk_fp8_f32 v243, v232, v233 op_sel:[0,0,1]
	v_cvt_pk_fp8_f32 v244, v236, v237 op_sel:[0,0,1]
	v_cvt_pk_fp8_f32 v245, v240, v241 op_sel:[0,0,1]
	s_nop 0
	global_store_dwordx4 v79, v[242:245], s[6:7]
	ds_read_b32 v226, v214
	ds_read_b32 v227, v214 offset:512
	ds_read_b32 v228, v214 offset:1024
	ds_read_b32 v229, v214 offset:1536
	ds_read_b32 v230, v214 offset:2048
	ds_read_b32 v231, v214 offset:2560
	ds_read_b32 v232, v214 offset:3072
	ds_read_b32 v233, v214 offset:3584
	ds_read_b32 v234, v214 offset:4096
	ds_read_b32 v235, v214 offset:4608
	ds_read_b32 v236, v214 offset:5120
	ds_read_b32 v237, v214 offset:5632
	ds_read_b32 v238, v214 offset:6144
	ds_read_b32 v239, v214 offset:6656
	ds_read_b32 v240, v214 offset:7168
	ds_read_b32 v241, v214 offset:7680
	s_waitcnt lgkmcnt(0)
	v_max_f32_e32 v226, v226, v226
	v_max_f32_e32 v227, v227, v227
	v_max_f32_e32 v228, v228, v228
	v_max_f32_e32 v229, v229, v229
	v_max_f32_e32 v230, v230, v230
	v_max_f32_e32 v231, v231, v231
	v_max_f32_e32 v232, v232, v232
	v_max_f32_e32 v233, v233, v233
	v_max_f32_e32 v234, v234, v234
	v_max_f32_e32 v235, v235, v235
	v_max_f32_e32 v236, v236, v236
	v_max_f32_e32 v237, v237, v237
	v_max_f32_e32 v238, v238, v238
	v_max_f32_e32 v239, v239, v239
	v_max_f32_e32 v240, v240, v240
	v_max_f32_e32 v241, v241, v241
	v_med3_f32 v226, v226, s62, v95
	v_med3_f32 v227, v227, s62, v95
	v_med3_f32 v228, v228, s62, v95
	v_med3_f32 v229, v229, s62, v95
	v_med3_f32 v230, v230, s62, v95
	v_med3_f32 v231, v231, s62, v95
	v_med3_f32 v232, v232, s62, v95
	v_med3_f32 v233, v233, s62, v95
	v_med3_f32 v234, v234, s62, v95
	v_med3_f32 v235, v235, s62, v95
	v_med3_f32 v236, v236, s62, v95
	v_med3_f32 v237, v237, s62, v95
	v_med3_f32 v238, v238, s62, v95
	v_med3_f32 v239, v239, s62, v95
	v_med3_f32 v240, v240, s62, v95
	v_med3_f32 v241, v241, s62, v95
	v_mov_b32_e32 v242, 0
	v_mov_b32_e32 v243, 0
	v_mov_b32_e32 v244, 0
	v_mov_b32_e32 v245, 0
	v_cvt_pk_fp8_f32 v242, v226, v227
	v_cvt_pk_fp8_f32 v243, v230, v231
	v_cvt_pk_fp8_f32 v244, v234, v235
	v_cvt_pk_fp8_f32 v245, v238, v239
	v_cvt_pk_fp8_f32 v242, v228, v229 op_sel:[0,0,1]
	v_cvt_pk_fp8_f32 v243, v232, v233 op_sel:[0,0,1]
	v_cvt_pk_fp8_f32 v244, v236, v237 op_sel:[0,0,1]
	v_cvt_pk_fp8_f32 v245, v240, v241 op_sel:[0,0,1]
	s_nop 0
	global_store_dwordx4 v80, v[242:245], s[6:7]
	s_waitcnt vmcnt(12)
	v_mul_f32_e32 v144, v42, v144
	v_mul_f32_e32 v145, v42, v145
	v_mul_f32_e32 v146, v42, v146
	v_mul_f32_e32 v147, v42, v147
	ds_write_b128 v209, v[144:147]
	v_mul_f32_e32 v148, v43, v148
	v_mul_f32_e32 v149, v43, v149
	v_mul_f32_e32 v150, v43, v150
	v_mul_f32_e32 v151, v43, v151
	ds_write_b128 v209, v[148:151] offset:1024
	v_mul_f32_e32 v152, v44, v152
	v_mul_f32_e32 v153, v44, v153
	v_mul_f32_e32 v154, v44, v154
	v_mul_f32_e32 v155, v44, v155
	ds_write_b128 v209, v[152:155] offset:2048
	v_mul_f32_e32 v156, v45, v156
	v_mul_f32_e32 v157, v45, v157
	v_mul_f32_e32 v158, v45, v158
	v_mul_f32_e32 v159, v45, v159
	ds_write_b128 v209, v[156:159] offset:3072
	v_mul_f32_e32 v160, v46, v160
	v_mul_f32_e32 v161, v46, v161
	v_mul_f32_e32 v162, v46, v162
	v_mul_f32_e32 v163, v46, v163
	ds_write_b128 v209, v[160:163] offset:4096
	v_mul_f32_e32 v164, v47, v164
	v_mul_f32_e32 v165, v47, v165
	v_mul_f32_e32 v166, v47, v166
	v_mul_f32_e32 v167, v47, v167
	ds_write_b128 v209, v[164:167] offset:5120
	v_mul_f32_e32 v168, v48, v168
	v_mul_f32_e32 v169, v48, v169
	v_mul_f32_e32 v170, v48, v170
	v_mul_f32_e32 v171, v48, v171
	ds_write_b128 v209, v[168:171] offset:6144
	v_mul_f32_e32 v172, v49, v172
	v_mul_f32_e32 v173, v49, v173
	v_mul_f32_e32 v174, v49, v174
	v_mul_f32_e32 v175, v49, v175
	ds_write_b128 v209, v[172:175] offset:7168
	s_waitcnt lgkmcnt(0)
	s_barrier
; #define GAS __attribute__((address_space(1)))
; #define LAS __attribute__((address_space(3)))
; #define LDS_WAIT() asm volatile("s_waitcnt lgkmcnt(0)" ::: "memory")
; __device__ __forceinline__ unsigned pk2(float lo, float hi) { return f2bf(lo) | (f2bf(hi) << 16); }
; __device__ __forceinline__ int nat_dim(int p) { return (p >> 1) + 64 * (p & 1); }
; template <int MAP, bool KS, bool KPERM = false>
; __device__ __forceinline__ void p0_transpose_item(const float* W, int K, int Nsrc, int nblk, bf16* WT, const float* ksA, const float* ksB, int ksplit, LAS float* scr, int item, int lane) {
;     ...
;     const int nr = n0 + (lane & 31); const int sc = MAP == 1 ? src_col_in(nr) : (MAP == 2 ? nat_dim(nr) : nr);
;     float v[32];
; #pragma unroll
;     for (int i = 0; i < 32; ++i) { const int k = k0 + 2 * i + (lane >> 5); const int ksrc = KPERM ? ((k & ~127) + nat_dim(k & 127)) : k;
;         v[i] = sc >= 0 ? W[(size_t)ksrc * Nsrc + sc] : 0.f; }
; #pragma unroll
;     for (int i = 0; i < 32; ++i) { const int kk = 2 * i + (lane >> 5); const int k = k0 + kk;
;         if (KS) v[i] *= (k < ksplit ? ksA[k] : ksB[k - ksplit]);
;         scr[kk * 33 + (lane & 31)] = v[i]; }
;     LDS_WAIT(); asm volatile("" ::: "memory");
;     const int c = lane & 7;
; #pragma unroll
;     for (int j = 0; j < 4; ++j) { const int n = (lane >> 3) + 8 * j; const LAS float* s = scr + (8 * c) * 33 + n;
;         v4u o; o.x = pk2(s[0 * 33], s[1 * 33]); o.y = pk2(s[2 * 33], s[3 * 33]); o.z = pk2(s[4 * 33], s[5 * 33]); o.w = pk2(s[6 * 33], s[7 * 33]);
;         *(GAS v4u*)(WT + (size_t)(n0 + n) * K + k0 + 8 * c) = o; }
	s_add_i32 s24, s23, 16
	s_lshl_b32 s20, s24, 7
	s_cmp_lt_u32 s24, 40
	s_cselect_b32 s21, 0, 0x830
	s_cmp_lt_u32 s24, 72
	s_cselect_b32 s21, s21, 0xfffff030
	s_add_i32 s20, s20, s21
	s_lshl_b32 s20, s20, 2
	s_add_u32 s8, s46, s20
	s_addc_u32 s9, s47, 0
	global_load_dwordx4 v[144:147], v76, s[8:9]
	s_add_u32 s8, s8, 0x16280
	s_addc_u32 s9, s9, 0
	global_load_dwordx4 v[148:151], v76, s[8:9]
	s_add_u32 s8, s8, 0x16280
	s_addc_u32 s9, s9, 0
	global_load_dwordx4 v[152:155], v76, s[8:9]
	s_add_u32 s8, s8, 0x16280
	s_addc_u32 s9, s9, 0
	global_load_dwordx4 v[156:159], v76, s[8:9]
	s_add_u32 s8, s8, 0x16280
	s_addc_u32 s9, s9, 0
	global_load_dwordx4 v[160:163], v76, s[8:9]
	s_add_u32 s8, s8, 0x16280
	s_addc_u32 s9, s9, 0
	global_load_dwordx4 v[164:167], v76, s[8:9]
	s_add_u32 s8, s8, 0x16280
	s_addc_u32 s9, s9, 0
	global_load_dwordx4 v[168:171], v76, s[8:9]
	s_add_u32 s8, s8, 0x16280
	s_addc_u32 s9, s9, 0
	global_load_dwordx4 v[172:175], v76, s[8:9]
	s_add_i32 s24, s23, 0
	s_mul_i32 s20, s24, 0x100000
	s_add_u32 s6, s48, s20
	s_addc_u32 s7, s49, 0
	s_cmp_lt_u32 s24, 16
	s_cselect_b32 s20, 1, 0
	s_sub_i32 s21, s24, 16
	s_bitcmp0_b32 s21, 2
	s_cselect_b32 s21, 1, 0
	s_cmp_lt_u32 s24, 40
	s_cselect_b32 s21, s21, 0
	s_or_b32 s20, s20, s21
	s_cmp_lg_u32 s20, 0
	s_cselect_b64 s[20:21], -1, 0
	v_cndmask_b32_e64 v91, v83, v87, s[20:21]
	v_cndmask_b32_e64 v92, v84, v88, s[20:21]
	v_cndmask_b32_e64 v93, v85, v89, s[20:21]
	v_cndmask_b32_e64 v94, v86, v90, s[20:21]
	ds_read_b32 v226, v112
	ds_read_b32 v227, v112 offset:512
	ds_read_b32 v228, v112 offset:1024
	ds_read_b32 v229, v112 offset:1536
	ds_read_b32 v230, v112 offset:2048
	ds_read_b32 v231, v112 offset:2560
	ds_read_b32 v232, v112 offset:3072
	ds_read_b32 v233, v112 offset:3584
	s_waitcnt lgkmcnt(0)
	v_bfe_u32 v120, v226, 16, 1
	v_bfe_u32 v121, v227, 16, 1
	v_bfe_u32 v122, v228, 16, 1
	v_bfe_u32 v123, v229, 16, 1
	v_bfe_u32 v124, v230, 16, 1
	v_bfe_u32 v125, v231, 16, 1
	v_bfe_u32 v126, v232, 16, 1
	v_bfe_u32 v127, v233, 16, 1
	v_add3_u32 v226, v226, v120, s63
	v_add3_u32 v227, v227, v121, s63
	v_add3_u32 v228, v228, v122, s63
	v_add3_u32 v229, v229, v123, s63
	v_add3_u32 v230, v230, v124, s63
	v_add3_u32 v231, v231, v125, s63
	v_add3_u32 v232, v232, v126, s63
	v_add3_u32 v233, v233, v127, s63
	v_perm_b32 v242, v227, v226, s64
	v_perm_b32 v243, v229, v228, s64
	v_perm_b32 v244, v231, v230, s64
	v_perm_b32 v245, v233, v232, s64
	s_nop 0
	global_store_dwordx4 v91, v[242:245], s[6:7]
	ds_read_b32 v226, v114
	ds_read_b32 v227, v114 offset:512
	ds_read_b32 v228, v114 offset:1024
	ds_read_b32 v229, v114 offset:1536
	ds_read_b32 v230, v114 offset:2048
	ds_read_b32 v231, v114 offset:2560
	ds_read_b32 v232, v114 offset:3072
	ds_read_b32 v233, v114 offset:3584
	s_waitcnt lgkmcnt(0)
	v_bfe_u32 v120, v226, 16, 1
	v_bfe_u32 v121, v227, 16, 1
	v_bfe_u32 v122, v228, 16, 1
	v_bfe_u32 v123, v229, 16, 1
	v_bfe_u32 v124, v230, 16, 1
	v_bfe_u32 v125, v231, 16, 1
	v_bfe_u32 v126, v232, 16, 1
	v_bfe_u32 v127, v233, 16, 1
	v_add3_u32 v226, v226, v120, s63
	v_add3_u32 v227, v227, v121, s63
	v_add3_u32 v228, v228, v122, s63
	v_add3_u32 v229, v229, v123, s63
	v_add3_u32 v230, v230, v124, s63
	v_add3_u32 v231, v231, v125, s63
	v_add3_u32 v232, v232, v126, s63
	v_add3_u32 v233, v233, v127, s63
	v_perm_b32 v242, v227, v226, s64
	v_perm_b32 v243, v229, v228, s64
	v_perm_b32 v244, v231, v230, s64
	v_perm_b32 v245, v233, v232, s64
	s_nop 0
	global_store_dwordx4 v92, v[242:245], s[6:7]
	ds_read_b32 v226, v116
	ds_read_b32 v227, v116 offset:512
	ds_read_b32 v228, v116 offset:1024
	ds_read_b32 v229, v116 offset:1536
	ds_read_b32 v230, v116 offset:2048
	ds_read_b32 v231, v116 offset:2560
	ds_read_b32 v232, v116 offset:3072
	ds_read_b32 v233, v116 offset:3584
	s_waitcnt lgkmcnt(0)
	v_bfe_u32 v120, v226, 16, 1
	v_bfe_u32 v121, v227, 16, 1
	v_bfe_u32 v122, v228, 16, 1
	v_bfe_u32 v123, v229, 16, 1
	v_bfe_u32 v124, v230, 16, 1
	v_bfe_u32 v125, v231, 16, 1
	v_bfe_u32 v126, v232, 16, 1
	v_bfe_u32 v127, v233, 16, 1
	v_add3_u32 v226, v226, v120, s63
	v_add3_u32 v227, v227, v121, s63
	v_add3_u32 v228, v228, v122, s63
	v_add3_u32 v229, v229, v123, s63
	v_add3_u32 v230, v230, v124, s63
	v_add3_u32 v231, v231, v125, s63
	v_add3_u32 v232, v232, v126, s63
	v_add3_u32 v233, v233, v127, s63
	v_perm_b32 v242, v227, v226, s64
	v_perm_b32 v243, v229, v228, s64
	v_perm_b32 v244, v231, v230, s64
	v_perm_b32 v245, v233, v232, s64
	s_nop 0
	global_store_dwordx4 v93, v[242:245], s[6:7]
	ds_read_b32 v226, v118
	ds_read_b32 v227, v118 offset:512
	ds_read_b32 v228, v118 offset:1024
	ds_read_b32 v229, v118 offset:1536
	ds_read_b32 v230, v118 offset:2048
	ds_read_b32 v231, v118 offset:2560
	ds_read_b32 v232, v118 offset:3072
	ds_read_b32 v233, v118 offset:3584
	s_waitcnt lgkmcnt(0)
	v_bfe_u32 v120, v226, 16, 1
	v_bfe_u32 v121, v227, 16, 1
	v_bfe_u32 v122, v228, 16, 1
	v_bfe_u32 v123, v229, 16, 1
	v_bfe_u32 v124, v230, 16, 1
	v_bfe_u32 v125, v231, 16, 1
	v_bfe_u32 v126, v232, 16, 1
	v_bfe_u32 v127, v233, 16, 1
	v_add3_u32 v226, v226, v120, s63
	v_add3_u32 v227, v227, v121, s63
	v_add3_u32 v228, v228, v122, s63
	v_add3_u32 v229, v229, v123, s63
	v_add3_u32 v230, v230, v124, s63
	v_add3_u32 v231, v231, v125, s63
	v_add3_u32 v232, v232, v126, s63
	v_add3_u32 v233, v233, v127, s63
	v_perm_b32 v242, v227, v226, s64
	v_perm_b32 v243, v229, v228, s64
	v_perm_b32 v244, v231, v230, s64
	v_perm_b32 v245, v233, v232, s64
	s_nop 0
	global_store_dwordx4 v94, v[242:245], s[6:7]
	s_waitcnt vmcnt(14)
	v_mul_f32_e32 v176, v42, v176
	v_mul_f32_e32 v177, v42, v177
	v_mul_f32_e32 v178, v42, v178
	v_mul_f32_e32 v179, v42, v179
	ds_write_b128 v210, v[176:179]
	v_mul_f32_e32 v180, v43, v180
	v_mul_f32_e32 v181, v43, v181
	v_mul_f32_e32 v182, v43, v182
	v_mul_f32_e32 v183, v43, v183
	ds_write_b128 v210, v[180:183] offset:1024
	v_mul_f32_e32 v184, v44, v184
	v_mul_f32_e32 v185, v44, v185
	v_mul_f32_e32 v186, v44, v186
	v_mul_f32_e32 v187, v44, v187
	ds_write_b128 v210, v[184:187] offset:2048
	v_mul_f32_e32 v188, v45, v188
	v_mul_f32_e32 v189, v45, v189
	v_mul_f32_e32 v190, v45, v190
	v_mul_f32_e32 v191, v45, v191
	ds_write_b128 v210, v[188:191] offset:3072
	v_mul_f32_e32 v192, v46, v192
	v_mul_f32_e32 v193, v46, v193
	v_mul_f32_e32 v194, v46, v194
	v_mul_f32_e32 v195, v46, v195
	ds_write_b128 v210, v[192:195] offset:4096
	v_mul_f32_e32 v196, v47, v196
	v_mul_f32_e32 v197, v47, v197
	v_mul_f32_e32 v198, v47, v198
	v_mul_f32_e32 v199, v47, v199
	ds_write_b128 v210, v[196:199] offset:5120
	v_mul_f32_e32 v200, v48, v200
	v_mul_f32_e32 v201, v48, v201
	v_mul_f32_e32 v202, v48, v202
	v_mul_f32_e32 v203, v48, v203
	ds_write_b128 v210, v[200:203] offset:6144
	v_mul_f32_e32 v204, v49, v204
	v_mul_f32_e32 v205, v49, v205
	v_mul_f32_e32 v206, v49, v206
	v_mul_f32_e32 v207, v49, v207
	ds_write_b128 v210, v[204:207] offset:7168
	s_waitcnt lgkmcnt(0)
	s_barrier
; #define GAS __attribute__((address_space(1)))
; #define LAS __attribute__((address_space(3)))
; #define LDS_WAIT() asm volatile("s_waitcnt lgkmcnt(0)" ::: "memory")
; __device__ __forceinline__ unsigned pk2(float lo, float hi) { return f2bf(lo) | (f2bf(hi) << 16); }
; __device__ __forceinline__ int nat_dim(int p) { return (p >> 1) + 64 * (p & 1); }
; template <int MAP, bool KS, bool KPERM = false>
; __device__ __forceinline__ void p0_transpose_item(const float* W, int K, int Nsrc, int nblk, bf16* WT, const float* ksA, const float* ksB, int ksplit, LAS float* scr, int item, int lane) {
;     ...
;     const int nr = n0 + (lane & 31); const int sc = MAP == 1 ? src_col_in(nr) : (MAP == 2 ? nat_dim(nr) : nr);
;     float v[32];
; #pragma unroll
;     for (int i = 0; i < 32; ++i) { const int k = k0 + 2 * i + (lane >> 5); const int ksrc = KPERM ? ((k & ~127) + nat_dim(k & 127)) : k;
;         v[i] = sc >= 0 ? W[(size_t)ksrc * Nsrc + sc] : 0.f; }
; #pragma unroll
;     for (int i = 0; i < 32; ++i) { const int kk = 2 * i + (lane >> 5); const int k = k0 + kk;
;         if (KS) v[i] *= (k < ksplit ? ksA[k] : ksB[k - ksplit]);
;         scr[kk * 33 + (lane & 31)] = v[i]; }
;     LDS_WAIT(); asm volatile("" ::: "memory");
;     const int c = lane & 7;
; #pragma unroll
;     for (int j = 0; j < 4; ++j) { const int n = (lane >> 3) + 8 * j; const LAS float* s = scr + (8 * c) * 33 + n;
;         v4u o; o.x = pk2(s[0 * 33], s[1 * 33]); o.y = pk2(s[2 * 33], s[3 * 33]); o.z = pk2(s[4 * 33], s[5 * 33]); o.w = pk2(s[6 * 33], s[7 * 33]);
;         *(GAS v4u*)(WT + (size_t)(n0 + n) * K + k0 + 8 * c) = o; }
	s_add_i32 s24, s23, 24
	s_lshl_b32 s20, s24, 7
	s_cmp_lt_u32 s24, 40
	s_cselect_b32 s21, 0, 0x830
	s_cmp_lt_u32 s24, 72
	s_cselect_b32 s21, s21, 0xfffff030
	s_add_i32 s20, s20, s21
	s_lshl_b32 s20, s20, 2
	s_add_u32 s8, s46, s20
	s_addc_u32 s9, s47, 0
	global_load_dwordx4 v[176:179], v76, s[8:9]
	s_add_u32 s8, s8, 0x16280
	s_addc_u32 s9, s9, 0
	global_load_dwordx4 v[180:183], v76, s[8:9]
	s_add_u32 s8, s8, 0x16280
	s_addc_u32 s9, s9, 0
	global_load_dwordx4 v[184:187], v76, s[8:9]
	s_add_u32 s8, s8, 0x16280
	s_addc_u32 s9, s9, 0
	global_load_dwordx4 v[188:191], v76, s[8:9]
	s_add_u32 s8, s8, 0x16280
	s_addc_u32 s9, s9, 0
	global_load_dwordx4 v[192:195], v76, s[8:9]
	s_add_u32 s8, s8, 0x16280
	s_addc_u32 s9, s9, 0
	global_load_dwordx4 v[196:199], v76, s[8:9]
	s_add_u32 s8, s8, 0x16280
	s_addc_u32 s9, s9, 0
	global_load_dwordx4 v[200:203], v76, s[8:9]
	s_add_u32 s8, s8, 0x16280
	s_addc_u32 s9, s9, 0
	global_load_dwordx4 v[204:207], v76, s[8:9]
	s_add_i32 s24, s23, 8
	s_mul_i32 s20, s24, 0x100000
	s_add_u32 s6, s48, s20
	s_addc_u32 s7, s49, 0
	s_cmp_lt_u32 s24, 16
	s_cselect_b32 s20, 1, 0
	s_sub_i32 s21, s24, 16
	s_bitcmp0_b32 s21, 2
	s_cselect_b32 s21, 1, 0
	s_cmp_lt_u32 s24, 40
	s_cselect_b32 s21, s21, 0
	s_or_b32 s20, s20, s21
	s_cmp_lg_u32 s20, 0
	s_cselect_b64 s[20:21], -1, 0
	v_cndmask_b32_e64 v91, v83, v87, s[20:21]
	v_cndmask_b32_e64 v92, v84, v88, s[20:21]
	v_cndmask_b32_e64 v93, v85, v89, s[20:21]
	v_cndmask_b32_e64 v94, v86, v90, s[20:21]
	ds_read_b32 v226, v113
	ds_read_b32 v227, v113 offset:512
	ds_read_b32 v228, v113 offset:1024
	ds_read_b32 v229, v113 offset:1536
	ds_read_b32 v230, v113 offset:2048
	ds_read_b32 v231, v113 offset:2560
	ds_read_b32 v232, v113 offset:3072
	ds_read_b32 v233, v113 offset:3584
	s_waitcnt lgkmcnt(0)
	v_bfe_u32 v120, v226, 16, 1
	v_bfe_u32 v121, v227, 16, 1
	v_bfe_u32 v122, v228, 16, 1
	v_bfe_u32 v123, v229, 16, 1
	v_bfe_u32 v124, v230, 16, 1
	v_bfe_u32 v125, v231, 16, 1
	v_bfe_u32 v126, v232, 16, 1
	v_bfe_u32 v127, v233, 16, 1
	v_add3_u32 v226, v226, v120, s63
	v_add3_u32 v227, v227, v121, s63
	v_add3_u32 v228, v228, v122, s63
	v_add3_u32 v229, v229, v123, s63
	v_add3_u32 v230, v230, v124, s63
	v_add3_u32 v231, v231, v125, s63
	v_add3_u32 v232, v232, v126, s63
	v_add3_u32 v233, v233, v127, s63
	v_perm_b32 v242, v227, v226, s64
	v_perm_b32 v243, v229, v228, s64
	v_perm_b32 v244, v231, v230, s64
	v_perm_b32 v245, v233, v232, s64
	s_nop 0
	global_store_dwordx4 v91, v[242:245], s[6:7]
	ds_read_b32 v226, v115
	ds_read_b32 v227, v115 offset:512
	ds_read_b32 v228, v115 offset:1024
	ds_read_b32 v229, v115 offset:1536
	ds_read_b32 v230, v115 offset:2048
	ds_read_b32 v231, v115 offset:2560
	ds_read_b32 v232, v115 offset:3072
	ds_read_b32 v233, v115 offset:3584
	s_waitcnt lgkmcnt(0)
	v_bfe_u32 v120, v226, 16, 1
	v_bfe_u32 v121, v227, 16, 1
	v_bfe_u32 v122, v228, 16, 1
	v_bfe_u32 v123, v229, 16, 1
	v_bfe_u32 v124, v230, 16, 1
	v_bfe_u32 v125, v231, 16, 1
	v_bfe_u32 v126, v232, 16, 1
	v_bfe_u32 v127, v233, 16, 1
	v_add3_u32 v226, v226, v120, s63
	v_add3_u32 v227, v227, v121, s63
	v_add3_u32 v228, v228, v122, s63
	v_add3_u32 v229, v229, v123, s63
	v_add3_u32 v230, v230, v124, s63
	v_add3_u32 v231, v231, v125, s63
	v_add3_u32 v232, v232, v126, s63
	v_add3_u32 v233, v233, v127, s63
	v_perm_b32 v242, v227, v226, s64
	v_perm_b32 v243, v229, v228, s64
	v_perm_b32 v244, v231, v230, s64
	v_perm_b32 v245, v233, v232, s64
	s_nop 0
	global_store_dwordx4 v92, v[242:245], s[6:7]
	ds_read_b32 v226, v117
	ds_read_b32 v227, v117 offset:512
	ds_read_b32 v228, v117 offset:1024
	ds_read_b32 v229, v117 offset:1536
	ds_read_b32 v230, v117 offset:2048
	ds_read_b32 v231, v117 offset:2560
	ds_read_b32 v232, v117 offset:3072
	ds_read_b32 v233, v117 offset:3584
	s_waitcnt lgkmcnt(0)
	v_bfe_u32 v120, v226, 16, 1
	v_bfe_u32 v121, v227, 16, 1
	v_bfe_u32 v122, v228, 16, 1
	v_bfe_u32 v123, v229, 16, 1
	v_bfe_u32 v124, v230, 16, 1
	v_bfe_u32 v125, v231, 16, 1
	v_bfe_u32 v126, v232, 16, 1
	v_bfe_u32 v127, v233, 16, 1
	v_add3_u32 v226, v226, v120, s63
	v_add3_u32 v227, v227, v121, s63
	v_add3_u32 v228, v228, v122, s63
	v_add3_u32 v229, v229, v123, s63
	v_add3_u32 v230, v230, v124, s63
	v_add3_u32 v231, v231, v125, s63
	v_add3_u32 v232, v232, v126, s63
	v_add3_u32 v233, v233, v127, s63
	v_perm_b32 v242, v227, v226, s64
	v_perm_b32 v243, v229, v228, s64
	v_perm_b32 v244, v231, v230, s64
	v_perm_b32 v245, v233, v232, s64
	s_nop 0
	global_store_dwordx4 v93, v[242:245], s[6:7]
	ds_read_b32 v226, v119
	ds_read_b32 v227, v119 offset:512
	ds_read_b32 v228, v119 offset:1024
	ds_read_b32 v229, v119 offset:1536
	ds_read_b32 v230, v119 offset:2048
	ds_read_b32 v231, v119 offset:2560
	ds_read_b32 v232, v119 offset:3072
	ds_read_b32 v233, v119 offset:3584
	s_waitcnt lgkmcnt(0)
	v_bfe_u32 v120, v226, 16, 1
	v_bfe_u32 v121, v227, 16, 1
	v_bfe_u32 v122, v228, 16, 1
	v_bfe_u32 v123, v229, 16, 1
	v_bfe_u32 v124, v230, 16, 1
	v_bfe_u32 v125, v231, 16, 1
	v_bfe_u32 v126, v232, 16, 1
	v_bfe_u32 v127, v233, 16, 1
	v_add3_u32 v226, v226, v120, s63
	v_add3_u32 v227, v227, v121, s63
	v_add3_u32 v228, v228, v122, s63
	v_add3_u32 v229, v229, v123, s63
	v_add3_u32 v230, v230, v124, s63
	v_add3_u32 v231, v231, v125, s63
	v_add3_u32 v232, v232, v126, s63
	v_add3_u32 v233, v233, v127, s63
	v_perm_b32 v242, v227, v226, s64
	v_perm_b32 v243, v229, v228, s64
	v_perm_b32 v244, v231, v230, s64
	v_perm_b32 v245, v233, v232, s64
	s_nop 0
	global_store_dwordx4 v94, v[242:245], s[6:7]
	s_waitcnt vmcnt(16)
	v_mul_f32_e32 v144, v42, v144
	v_mul_f32_e32 v145, v42, v145
	v_mul_f32_e32 v146, v42, v146
	v_mul_f32_e32 v147, v42, v147
	ds_write_b128 v209, v[144:147]
	v_mul_f32_e32 v148, v43, v148
	v_mul_f32_e32 v149, v43, v149
	v_mul_f32_e32 v150, v43, v150
	v_mul_f32_e32 v151, v43, v151
	ds_write_b128 v209, v[148:151] offset:1024
	v_mul_f32_e32 v152, v44, v152
	v_mul_f32_e32 v153, v44, v153
	v_mul_f32_e32 v154, v44, v154
	v_mul_f32_e32 v155, v44, v155
	ds_write_b128 v209, v[152:155] offset:2048
	v_mul_f32_e32 v156, v45, v156
	v_mul_f32_e32 v157, v45, v157
	v_mul_f32_e32 v158, v45, v158
	v_mul_f32_e32 v159, v45, v159
	ds_write_b128 v209, v[156:159] offset:3072
	v_mul_f32_e32 v160, v46, v160
	v_mul_f32_e32 v161, v46, v161
	v_mul_f32_e32 v162, v46, v162
	v_mul_f32_e32 v163, v46, v163
	ds_write_b128 v209, v[160:163] offset:4096
	v_mul_f32_e32 v164, v47, v164
	v_mul_f32_e32 v165, v47, v165
	v_mul_f32_e32 v166, v47, v166
	v_mul_f32_e32 v167, v47, v167
	ds_write_b128 v209, v[164:167] offset:5120
	v_mul_f32_e32 v168, v48, v168
	v_mul_f32_e32 v169, v48, v169
	v_mul_f32_e32 v170, v48, v170
	v_mul_f32_e32 v171, v48, v171
	ds_write_b128 v209, v[168:171] offset:6144
	v_mul_f32_e32 v172, v49, v172
	v_mul_f32_e32 v173, v49, v173
	v_mul_f32_e32 v174, v49, v174
	v_mul_f32_e32 v175, v49, v175
	ds_write_b128 v209, v[172:175] offset:7168
	s_waitcnt lgkmcnt(0)
	s_barrier
; #define GAS __attribute__((address_space(1)))
; #define LAS __attribute__((address_space(3)))
; #define LDS_WAIT() asm volatile("s_waitcnt lgkmcnt(0)" ::: "memory")
; __device__ __forceinline__ unsigned pk2(float lo, float hi) { return f2bf(lo) | (f2bf(hi) << 16); }
; __device__ __forceinline__ int nat_dim(int p) { return (p >> 1) + 64 * (p & 1); }
; template <int MAP, bool KS, bool KPERM = false>
; __device__ __forceinline__ void p0_transpose_item(const float* W, int K, int Nsrc, int nblk, bf16* WT, const float* ksA, const float* ksB, int ksplit, LAS float* scr, int item, int lane) {
;     ...
;     const int nr = n0 + (lane & 31); const int sc = MAP == 1 ? src_col_in(nr) : (MAP == 2 ? nat_dim(nr) : nr);
;     float v[32];
; #pragma unroll
;     for (int i = 0; i < 32; ++i) { const int k = k0 + 2 * i + (lane >> 5); const int ksrc = KPERM ? ((k & ~127) + nat_dim(k & 127)) : k;
;         v[i] = sc >= 0 ? W[(size_t)ksrc * Nsrc + sc] : 0.f; }
; #pragma unroll
;     for (int i = 0; i < 32; ++i) { const int kk = 2 * i + (lane >> 5); const int k = k0 + kk;
;         if (KS) v[i] *= (k < ksplit ? ksA[k] : ksB[k - ksplit]);
;         scr[kk * 33 + (lane & 31)] = v[i]; }
;     LDS_WAIT(); asm volatile("" ::: "memory");
;     const int c = lane & 7;
; #pragma unroll
;     for (int j = 0; j < 4; ++j) { const int n = (lane >> 3) + 8 * j; const LAS float* s = scr + (8 * c) * 33 + n;
;         v4u o; o.x = pk2(s[0 * 33], s[1 * 33]); o.y = pk2(s[2 * 33], s[3 * 33]); o.z = pk2(s[4 * 33], s[5 * 33]); o.w = pk2(s[6 * 33], s[7 * 33]);
;         *(GAS v4u*)(WT + (size_t)(n0 + n) * K + k0 + 8 * c) = o; }
	s_add_i32 s24, s23, 32
	s_lshl_b32 s20, s24, 7
	s_cmp_lt_u32 s24, 40
	s_cselect_b32 s21, 0, 0x830
	s_cmp_lt_u32 s24, 72
	s_cselect_b32 s21, s21, 0xfffff030
	s_add_i32 s20, s20, s21
	s_lshl_b32 s20, s20, 2
	s_add_u32 s8, s46, s20
	s_addc_u32 s9, s47, 0
	global_load_dwordx4 v[144:147], v76, s[8:9]
	s_add_u32 s8, s8, 0x16280
	s_addc_u32 s9, s9, 0
	global_load_dwordx4 v[148:151], v76, s[8:9]
	s_add_u32 s8, s8, 0x16280
	s_addc_u32 s9, s9, 0
	global_load_dwordx4 v[152:155], v76, s[8:9]
	s_add_u32 s8, s8, 0x16280
	s_addc_u32 s9, s9, 0
	global_load_dwordx4 v[156:159], v76, s[8:9]
	s_add_u32 s8, s8, 0x16280
	s_addc_u32 s9, s9, 0
	global_load_dwordx4 v[160:163], v76, s[8:9]
	s_add_u32 s8, s8, 0x16280
	s_addc_u32 s9, s9, 0
	global_load_dwordx4 v[164:167], v76, s[8:9]
	s_add_u32 s8, s8, 0x16280
	s_addc_u32 s9, s9, 0
	global_load_dwordx4 v[168:171], v76, s[8:9]
	s_add_u32 s8, s8, 0x16280
	s_addc_u32 s9, s9, 0
	global_load_dwordx4 v[172:175], v76, s[8:9]
	s_add_i32 s24, s23, 16
	s_mul_i32 s20, s24, 0x100000
	s_add_u32 s6, s48, s20
	s_addc_u32 s7, s49, 0
	s_cmp_lt_u32 s24, 16
	s_cselect_b32 s20, 1, 0
	s_sub_i32 s21, s24, 16
	s_bitcmp0_b32 s21, 2
	s_cselect_b32 s21, 1, 0
	s_cmp_lt_u32 s24, 40
	s_cselect_b32 s21, s21, 0
	s_or_b32 s20, s20, s21
	s_cmp_lg_u32 s20, 0
	s_cselect_b64 s[20:21], -1, 0
	v_cndmask_b32_e64 v91, v83, v87, s[20:21]
	v_cndmask_b32_e64 v92, v84, v88, s[20:21]
	v_cndmask_b32_e64 v93, v85, v89, s[20:21]
	v_cndmask_b32_e64 v94, v86, v90, s[20:21]
	ds_read_b32 v226, v112
	ds_read_b32 v227, v112 offset:512
	ds_read_b32 v228, v112 offset:1024
	ds_read_b32 v229, v112 offset:1536
	ds_read_b32 v230, v112 offset:2048
	ds_read_b32 v231, v112 offset:2560
	ds_read_b32 v232, v112 offset:3072
	ds_read_b32 v233, v112 offset:3584
	s_waitcnt lgkmcnt(0)
	v_bfe_u32 v120, v226, 16, 1
	v_bfe_u32 v121, v227, 16, 1
	v_bfe_u32 v122, v228, 16, 1
	v_bfe_u32 v123, v229, 16, 1
	v_bfe_u32 v124, v230, 16, 1
	v_bfe_u32 v125, v231, 16, 1
	v_bfe_u32 v126, v232, 16, 1
	v_bfe_u32 v127, v233, 16, 1
	v_add3_u32 v226, v226, v120, s63
	v_add3_u32 v227, v227, v121, s63
	v_add3_u32 v228, v228, v122, s63
	v_add3_u32 v229, v229, v123, s63
	v_add3_u32 v230, v230, v124, s63
	v_add3_u32 v231, v231, v125, s63
	v_add3_u32 v232, v232, v126, s63
	v_add3_u32 v233, v233, v127, s63
	v_perm_b32 v242, v227, v226, s64
	v_perm_b32 v243, v229, v228, s64
	v_perm_b32 v244, v231, v230, s64
	v_perm_b32 v245, v233, v232, s64
	s_nop 0
	global_store_dwordx4 v91, v[242:245], s[6:7]
	ds_read_b32 v226, v114
	ds_read_b32 v227, v114 offset:512
	ds_read_b32 v228, v114 offset:1024
	ds_read_b32 v229, v114 offset:1536
	ds_read_b32 v230, v114 offset:2048
	ds_read_b32 v231, v114 offset:2560
	ds_read_b32 v232, v114 offset:3072
	ds_read_b32 v233, v114 offset:3584
	s_waitcnt lgkmcnt(0)
	v_bfe_u32 v120, v226, 16, 1
	v_bfe_u32 v121, v227, 16, 1
	v_bfe_u32 v122, v228, 16, 1
	v_bfe_u32 v123, v229, 16, 1
	v_bfe_u32 v124, v230, 16, 1
	v_bfe_u32 v125, v231, 16, 1
	v_bfe_u32 v126, v232, 16, 1
	v_bfe_u32 v127, v233, 16, 1
	v_add3_u32 v226, v226, v120, s63
	v_add3_u32 v227, v227, v121, s63
	v_add3_u32 v228, v228, v122, s63
	v_add3_u32 v229, v229, v123, s63
	v_add3_u32 v230, v230, v124, s63
	v_add3_u32 v231, v231, v125, s63
	v_add3_u32 v232, v232, v126, s63
	v_add3_u32 v233, v233, v127, s63
	v_perm_b32 v242, v227, v226, s64
	v_perm_b32 v243, v229, v228, s64
	v_perm_b32 v244, v231, v230, s64
	v_perm_b32 v245, v233, v232, s64
	s_nop 0
	global_store_dwordx4 v92, v[242:245], s[6:7]
	ds_read_b32 v226, v116
	ds_read_b32 v227, v116 offset:512
	ds_read_b32 v228, v116 offset:1024
	ds_read_b32 v229, v116 offset:1536
	ds_read_b32 v230, v116 offset:2048
	ds_read_b32 v231, v116 offset:2560
	ds_read_b32 v232, v116 offset:3072
	ds_read_b32 v233, v116 offset:3584
	s_waitcnt lgkmcnt(0)
	v_bfe_u32 v120, v226, 16, 1
	v_bfe_u32 v121, v227, 16, 1
	v_bfe_u32 v122, v228, 16, 1
	v_bfe_u32 v123, v229, 16, 1
	v_bfe_u32 v124, v230, 16, 1
	v_bfe_u32 v125, v231, 16, 1
	v_bfe_u32 v126, v232, 16, 1
	v_bfe_u32 v127, v233, 16, 1
	v_add3_u32 v226, v226, v120, s63
	v_add3_u32 v227, v227, v121, s63
	v_add3_u32 v228, v228, v122, s63
	v_add3_u32 v229, v229, v123, s63
	v_add3_u32 v230, v230, v124, s63
	v_add3_u32 v231, v231, v125, s63
	v_add3_u32 v232, v232, v126, s63
	v_add3_u32 v233, v233, v127, s63
	v_perm_b32 v242, v227, v226, s64
	v_perm_b32 v243, v229, v228, s64
	v_perm_b32 v244, v231, v230, s64
	v_perm_b32 v245, v233, v232, s64
	s_nop 0
	global_store_dwordx4 v93, v[242:245], s[6:7]
	ds_read_b32 v226, v118
	ds_read_b32 v227, v118 offset:512
	ds_read_b32 v228, v118 offset:1024
	ds_read_b32 v229, v118 offset:1536
	ds_read_b32 v230, v118 offset:2048
	ds_read_b32 v231, v118 offset:2560
	ds_read_b32 v232, v118 offset:3072
	ds_read_b32 v233, v118 offset:3584
	s_waitcnt lgkmcnt(0)
	v_bfe_u32 v120, v226, 16, 1
	v_bfe_u32 v121, v227, 16, 1
	v_bfe_u32 v122, v228, 16, 1
	v_bfe_u32 v123, v229, 16, 1
	v_bfe_u32 v124, v230, 16, 1
	v_bfe_u32 v125, v231, 16, 1
	v_bfe_u32 v126, v232, 16, 1
	v_bfe_u32 v127, v233, 16, 1
	v_add3_u32 v226, v226, v120, s63
	v_add3_u32 v227, v227, v121, s63
	v_add3_u32 v228, v228, v122, s63
	v_add3_u32 v229, v229, v123, s63
	v_add3_u32 v230, v230, v124, s63
	v_add3_u32 v231, v231, v125, s63
	v_add3_u32 v232, v232, v126, s63
	v_add3_u32 v233, v233, v127, s63
	v_perm_b32 v242, v227, v226, s64
	v_perm_b32 v243, v229, v228, s64
	v_perm_b32 v244, v231, v230, s64
	v_perm_b32 v245, v233, v232, s64
	s_nop 0
	global_store_dwordx4 v94, v[242:245], s[6:7]
	s_waitcnt vmcnt(16)
	v_mul_f32_e32 v176, v42, v176
	v_mul_f32_e32 v177, v42, v177
	v_mul_f32_e32 v178, v42, v178
	v_mul_f32_e32 v179, v42, v179
	ds_write_b128 v210, v[176:179]
	v_mul_f32_e32 v180, v43, v180
	v_mul_f32_e32 v181, v43, v181
	v_mul_f32_e32 v182, v43, v182
	v_mul_f32_e32 v183, v43, v183
	ds_write_b128 v210, v[180:183] offset:1024
	v_mul_f32_e32 v184, v44, v184
	v_mul_f32_e32 v185, v44, v185
	v_mul_f32_e32 v186, v44, v186
	v_mul_f32_e32 v187, v44, v187
	ds_write_b128 v210, v[184:187] offset:2048
	v_mul_f32_e32 v188, v45, v188
	v_mul_f32_e32 v189, v45, v189
	v_mul_f32_e32 v190, v45, v190
	v_mul_f32_e32 v191, v45, v191
	ds_write_b128 v210, v[188:191] offset:3072
	v_mul_f32_e32 v192, v46, v192
	v_mul_f32_e32 v193, v46, v193
	v_mul_f32_e32 v194, v46, v194
	v_mul_f32_e32 v195, v46, v195
	ds_write_b128 v210, v[192:195] offset:4096
	v_mul_f32_e32 v196, v47, v196
	v_mul_f32_e32 v197, v47, v197
	v_mul_f32_e32 v198, v47, v198
	v_mul_f32_e32 v199, v47, v199
	ds_write_b128 v210, v[196:199] offset:5120
	v_mul_f32_e32 v200, v48, v200
	v_mul_f32_e32 v201, v48, v201
	v_mul_f32_e32 v202, v48, v202
	v_mul_f32_e32 v203, v48, v203
	ds_write_b128 v210, v[200:203] offset:6144
	v_mul_f32_e32 v204, v49, v204
	v_mul_f32_e32 v205, v49, v205
	v_mul_f32_e32 v206, v49, v206
	v_mul_f32_e32 v207, v49, v207
	ds_write_b128 v210, v[204:207] offset:7168
	s_waitcnt lgkmcnt(0)
	s_barrier
; #define GAS __attribute__((address_space(1)))
; #define LAS __attribute__((address_space(3)))
; #define LDS_WAIT() asm volatile("s_waitcnt lgkmcnt(0)" ::: "memory")
; __device__ __forceinline__ unsigned pk2(float lo, float hi) { return f2bf(lo) | (f2bf(hi) << 16); }
; __device__ __forceinline__ int nat_dim(int p) { return (p >> 1) + 64 * (p & 1); }
; template <int MAP, bool KS, bool KPERM = false>
; __device__ __forceinline__ void p0_transpose_item(const float* W, int K, int Nsrc, int nblk, bf16* WT, const float* ksA, const float* ksB, int ksplit, LAS float* scr, int item, int lane) {
;     ...
;     const int nr = n0 + (lane & 31); const int sc = MAP == 1 ? src_col_in(nr) : (MAP == 2 ? nat_dim(nr) : nr);
;     float v[32];
; #pragma unroll
;     for (int i = 0; i < 32; ++i) { const int k = k0 + 2 * i + (lane >> 5); const int ksrc = KPERM ? ((k & ~127) + nat_dim(k & 127)) : k;
;         v[i] = sc >= 0 ? W[(size_t)ksrc * Nsrc + sc] : 0.f; }
; #pragma unroll
;     for (int i = 0; i < 32; ++i) { const int kk = 2 * i + (lane >> 5); const int k = k0 + kk;
;         if (KS) v[i] *= (k < ksplit ? ksA[k] : ksB[k - ksplit]);
;         scr[kk * 33 + (lane & 31)] = v[i]; }
;     LDS_WAIT(); asm volatile("" ::: "memory");
;     const int c = lane & 7;
; #pragma unroll
;     for (int j = 0; j < 4; ++j) { const int n = (lane >> 3) + 8 * j; const LAS float* s = scr + (8 * c) * 33 + n;
;         v4u o; o.x = pk2(s[0 * 33], s[1 * 33]); o.y = pk2(s[2 * 33], s[3 * 33]); o.z = pk2(s[4 * 33], s[5 * 33]); o.w = pk2(s[6 * 33], s[7 * 33]);
;         *(GAS v4u*)(WT + (size_t)(n0 + n) * K + k0 + 8 * c) = o; }
	s_add_i32 s24, s23, 40
	s_lshl_b32 s20, s24, 7
	s_cmp_lt_u32 s24, 40
	s_cselect_b32 s21, 0, 0x830
	s_cmp_lt_u32 s24, 72
	s_cselect_b32 s21, s21, 0xfffff030
	s_add_i32 s20, s20, s21
	s_lshl_b32 s20, s20, 2
	s_add_u32 s8, s46, s20
	s_addc_u32 s9, s47, 0
	global_load_dwordx4 v[176:179], v76, s[8:9]
	s_add_u32 s8, s8, 0x16280
	s_addc_u32 s9, s9, 0
	global_load_dwordx4 v[180:183], v76, s[8:9]
	s_add_u32 s8, s8, 0x16280
	s_addc_u32 s9, s9, 0
	global_load_dwordx4 v[184:187], v76, s[8:9]
	s_add_u32 s8, s8, 0x16280
	s_addc_u32 s9, s9, 0
	global_load_dwordx4 v[188:191], v76, s[8:9]
	s_add_u32 s8, s8, 0x16280
	s_addc_u32 s9, s9, 0
	global_load_dwordx4 v[192:195], v76, s[8:9]
	s_add_u32 s8, s8, 0x16280
	s_addc_u32 s9, s9, 0
	global_load_dwordx4 v[196:199], v76, s[8:9]
	s_add_u32 s8, s8, 0x16280
	s_addc_u32 s9, s9, 0
	global_load_dwordx4 v[200:203], v76, s[8:9]
	s_add_u32 s8, s8, 0x16280
	s_addc_u32 s9, s9, 0
	global_load_dwordx4 v[204:207], v76, s[8:9]
	s_add_i32 s24, s23, 24
	s_mul_i32 s20, s24, 0x100000
	s_add_u32 s6, s48, s20
	s_addc_u32 s7, s49, 0
	s_cmp_lt_u32 s24, 16
	s_cselect_b32 s20, 1, 0
	s_sub_i32 s21, s24, 16
	s_bitcmp0_b32 s21, 2
	s_cselect_b32 s21, 1, 0
	s_cmp_lt_u32 s24, 40
	s_cselect_b32 s21, s21, 0
	s_or_b32 s20, s20, s21
	s_cmp_lg_u32 s20, 0
	s_cselect_b64 s[20:21], -1, 0
	v_cndmask_b32_e64 v91, v83, v87, s[20:21]
	v_cndmask_b32_e64 v92, v84, v88, s[20:21]
	v_cndmask_b32_e64 v93, v85, v89, s[20:21]
	v_cndmask_b32_e64 v94, v86, v90, s[20:21]
	ds_read_b32 v226, v113
	ds_read_b32 v227, v113 offset:512
	ds_read_b32 v228, v113 offset:1024
	ds_read_b32 v229, v113 offset:1536
	ds_read_b32 v230, v113 offset:2048
	ds_read_b32 v231, v113 offset:2560
	ds_read_b32 v232, v113 offset:3072
	ds_read_b32 v233, v113 offset:3584
	s_waitcnt lgkmcnt(0)
	v_bfe_u32 v120, v226, 16, 1
	v_bfe_u32 v121, v227, 16, 1
	v_bfe_u32 v122, v228, 16, 1
	v_bfe_u32 v123, v229, 16, 1
	v_bfe_u32 v124, v230, 16, 1
	v_bfe_u32 v125, v231, 16, 1
	v_bfe_u32 v126, v232, 16, 1
	v_bfe_u32 v127, v233, 16, 1
	v_add3_u32 v226, v226, v120, s63
	v_add3_u32 v227, v227, v121, s63
	v_add3_u32 v228, v228, v122, s63
	v_add3_u32 v229, v229, v123, s63
	v_add3_u32 v230, v230, v124, s63
	v_add3_u32 v231, v231, v125, s63
	v_add3_u32 v232, v232, v126, s63
	v_add3_u32 v233, v233, v127, s63
	v_perm_b32 v242, v227, v226, s64
	v_perm_b32 v243, v229, v228, s64
	v_perm_b32 v244, v231, v230, s64
	v_perm_b32 v245, v233, v232, s64
	s_nop 0
	global_store_dwordx4 v91, v[242:245], s[6:7]
	ds_read_b32 v226, v115
	ds_read_b32 v227, v115 offset:512
	ds_read_b32 v228, v115 offset:1024
	ds_read_b32 v229, v115 offset:1536
	ds_read_b32 v230, v115 offset:2048
	ds_read_b32 v231, v115 offset:2560
	ds_read_b32 v232, v115 offset:3072
	ds_read_b32 v233, v115 offset:3584
	s_waitcnt lgkmcnt(0)
	v_bfe_u32 v120, v226, 16, 1
	v_bfe_u32 v121, v227, 16, 1
	v_bfe_u32 v122, v228, 16, 1
	v_bfe_u32 v123, v229, 16, 1
	v_bfe_u32 v124, v230, 16, 1
	v_bfe_u32 v125, v231, 16, 1
	v_bfe_u32 v126, v232, 16, 1
	v_bfe_u32 v127, v233, 16, 1
	v_add3_u32 v226, v226, v120, s63
	v_add3_u32 v227, v227, v121, s63
	v_add3_u32 v228, v228, v122, s63
	v_add3_u32 v229, v229, v123, s63
	v_add3_u32 v230, v230, v124, s63
	v_add3_u32 v231, v231, v125, s63
	v_add3_u32 v232, v232, v126, s63
	v_add3_u32 v233, v233, v127, s63
	v_perm_b32 v242, v227, v226, s64
	v_perm_b32 v243, v229, v228, s64
	v_perm_b32 v244, v231, v230, s64
	v_perm_b32 v245, v233, v232, s64
	s_nop 0
	global_store_dwordx4 v92, v[242:245], s[6:7]
	ds_read_b32 v226, v117
	ds_read_b32 v227, v117 offset:512
	ds_read_b32 v228, v117 offset:1024
	ds_read_b32 v229, v117 offset:1536
	ds_read_b32 v230, v117 offset:2048
	ds_read_b32 v231, v117 offset:2560
	ds_read_b32 v232, v117 offset:3072
	ds_read_b32 v233, v117 offset:3584
	s_waitcnt lgkmcnt(0)
	v_bfe_u32 v120, v226, 16, 1
	v_bfe_u32 v121, v227, 16, 1
	v_bfe_u32 v122, v228, 16, 1
	v_bfe_u32 v123, v229, 16, 1
	v_bfe_u32 v124, v230, 16, 1
	v_bfe_u32 v125, v231, 16, 1
	v_bfe_u32 v126, v232, 16, 1
	v_bfe_u32 v127, v233, 16, 1
	v_add3_u32 v226, v226, v120, s63
	v_add3_u32 v227, v227, v121, s63
	v_add3_u32 v228, v228, v122, s63
	v_add3_u32 v229, v229, v123, s63
	v_add3_u32 v230, v230, v124, s63
	v_add3_u32 v231, v231, v125, s63
	v_add3_u32 v232, v232, v126, s63
	v_add3_u32 v233, v233, v127, s63
	v_perm_b32 v242, v227, v226, s64
	v_perm_b32 v243, v229, v228, s64
	v_perm_b32 v244, v231, v230, s64
	v_perm_b32 v245, v233, v232, s64
	s_nop 0
	global_store_dwordx4 v93, v[242:245], s[6:7]
	ds_read_b32 v226, v119
	ds_read_b32 v227, v119 offset:512
	ds_read_b32 v228, v119 offset:1024
	ds_read_b32 v229, v119 offset:1536
	ds_read_b32 v230, v119 offset:2048
	ds_read_b32 v231, v119 offset:2560
	ds_read_b32 v232, v119 offset:3072
	ds_read_b32 v233, v119 offset:3584
	s_waitcnt lgkmcnt(0)
	v_bfe_u32 v120, v226, 16, 1
	v_bfe_u32 v121, v227, 16, 1
	v_bfe_u32 v122, v228, 16, 1
	v_bfe_u32 v123, v229, 16, 1
	v_bfe_u32 v124, v230, 16, 1
	v_bfe_u32 v125, v231, 16, 1
	v_bfe_u32 v126, v232, 16, 1
	v_bfe_u32 v127, v233, 16, 1
	v_add3_u32 v226, v226, v120, s63
	v_add3_u32 v227, v227, v121, s63
	v_add3_u32 v228, v228, v122, s63
	v_add3_u32 v229, v229, v123, s63
	v_add3_u32 v230, v230, v124, s63
	v_add3_u32 v231, v231, v125, s63
	v_add3_u32 v232, v232, v126, s63
	v_add3_u32 v233, v233, v127, s63
	v_perm_b32 v242, v227, v226, s64
	v_perm_b32 v243, v229, v228, s64
	v_perm_b32 v244, v231, v230, s64
	v_perm_b32 v245, v233, v232, s64
	s_nop 0
	global_store_dwordx4 v94, v[242:245], s[6:7]
	s_waitcnt vmcnt(16)
	v_mul_f32_e32 v144, v42, v144
	v_mul_f32_e32 v145, v42, v145
	v_mul_f32_e32 v146, v42, v146
	v_mul_f32_e32 v147, v42, v147
	ds_write_b128 v209, v[144:147]
	v_mul_f32_e32 v148, v43, v148
	v_mul_f32_e32 v149, v43, v149
	v_mul_f32_e32 v150, v43, v150
	v_mul_f32_e32 v151, v43, v151
	ds_write_b128 v209, v[148:151] offset:1024
	v_mul_f32_e32 v152, v44, v152
	v_mul_f32_e32 v153, v44, v153
	v_mul_f32_e32 v154, v44, v154
	v_mul_f32_e32 v155, v44, v155
	ds_write_b128 v209, v[152:155] offset:2048
	v_mul_f32_e32 v156, v45, v156
	v_mul_f32_e32 v157, v45, v157
	v_mul_f32_e32 v158, v45, v158
	v_mul_f32_e32 v159, v45, v159
	ds_write_b128 v209, v[156:159] offset:3072
	v_mul_f32_e32 v160, v46, v160
	v_mul_f32_e32 v161, v46, v161
	v_mul_f32_e32 v162, v46, v162
	v_mul_f32_e32 v163, v46, v163
	ds_write_b128 v209, v[160:163] offset:4096
	v_mul_f32_e32 v164, v47, v164
	v_mul_f32_e32 v165, v47, v165
	v_mul_f32_e32 v166, v47, v166
	v_mul_f32_e32 v167, v47, v167
	ds_write_b128 v209, v[164:167] offset:5120
	v_mul_f32_e32 v168, v48, v168
	v_mul_f32_e32 v169, v48, v169
	v_mul_f32_e32 v170, v48, v170
	v_mul_f32_e32 v171, v48, v171
	ds_write_b128 v209, v[168:171] offset:6144
	v_mul_f32_e32 v172, v49, v172
	v_mul_f32_e32 v173, v49, v173
	v_mul_f32_e32 v174, v49, v174
	v_mul_f32_e32 v175, v49, v175
	ds_write_b128 v209, v[172:175] offset:7168
	s_waitcnt lgkmcnt(0)
	s_barrier
; #define GAS __attribute__((address_space(1)))
; #define LAS __attribute__((address_space(3)))
; #define LDS_WAIT() asm volatile("s_waitcnt lgkmcnt(0)" ::: "memory")
; __device__ __forceinline__ unsigned pk2(float lo, float hi) { return f2bf(lo) | (f2bf(hi) << 16); }
; __device__ __forceinline__ int nat_dim(int p) { return (p >> 1) + 64 * (p & 1); }
; template <int MAP, bool KS, bool KPERM = false>
; __device__ __forceinline__ void p0_transpose_item(const float* W, int K, int Nsrc, int nblk, bf16* WT, const float* ksA, const float* ksB, int ksplit, LAS float* scr, int item, int lane) {
;     ...
;     const int nr = n0 + (lane & 31); const int sc = MAP == 1 ? src_col_in(nr) : (MAP == 2 ? nat_dim(nr) : nr);
;     float v[32];
; #pragma unroll
;     for (int i = 0; i < 32; ++i) { const int k = k0 + 2 * i + (lane >> 5); const int ksrc = KPERM ? ((k & ~127) + nat_dim(k & 127)) : k;
;         v[i] = sc >= 0 ? W[(size_t)ksrc * Nsrc + sc] : 0.f; }
; #pragma unroll
;     for (int i = 0; i < 32; ++i) { const int kk = 2 * i + (lane >> 5); const int k = k0 + kk;
;         if (KS) v[i] *= (k < ksplit ? ksA[k] : ksB[k - ksplit]);
;         scr[kk * 33 + (lane & 31)] = v[i]; }
;     LDS_WAIT(); asm volatile("" ::: "memory");
;     const int c = lane & 7;
; #pragma unroll
;     for (int j = 0; j < 4; ++j) { const int n = (lane >> 3) + 8 * j; const LAS float* s = scr + (8 * c) * 33 + n;
;         v4u o; o.x = pk2(s[0 * 33], s[1 * 33]); o.y = pk2(s[2 * 33], s[3 * 33]); o.z = pk2(s[4 * 33], s[5 * 33]); o.w = pk2(s[6 * 33], s[7 * 33]);
;         *(GAS v4u*)(WT + (size_t)(n0 + n) * K + k0 + 8 * c) = o; }
	s_add_i32 s24, s23, 48
	s_lshl_b32 s20, s24, 7
	s_cmp_lt_u32 s24, 40
	s_cselect_b32 s21, 0, 0x830
	s_cmp_lt_u32 s24, 72
	s_cselect_b32 s21, s21, 0xfffff030
	s_add_i32 s20, s20, s21
	s_lshl_b32 s20, s20, 2
	s_add_u32 s8, s46, s20
	s_addc_u32 s9, s47, 0
	global_load_dwordx4 v[144:147], v76, s[8:9]
	s_add_u32 s8, s8, 0x16280
	s_addc_u32 s9, s9, 0
	global_load_dwordx4 v[148:151], v76, s[8:9]
	s_add_u32 s8, s8, 0x16280
	s_addc_u32 s9, s9, 0
	global_load_dwordx4 v[152:155], v76, s[8:9]
	s_add_u32 s8, s8, 0x16280
	s_addc_u32 s9, s9, 0
	global_load_dwordx4 v[156:159], v76, s[8:9]
	s_add_u32 s8, s8, 0x16280
	s_addc_u32 s9, s9, 0
	global_load_dwordx4 v[160:163], v76, s[8:9]
	s_add_u32 s8, s8, 0x16280
	s_addc_u32 s9, s9, 0
	global_load_dwordx4 v[164:167], v76, s[8:9]
	s_add_u32 s8, s8, 0x16280
	s_addc_u32 s9, s9, 0
	global_load_dwordx4 v[168:171], v76, s[8:9]
	s_add_u32 s8, s8, 0x16280
	s_addc_u32 s9, s9, 0
	global_load_dwordx4 v[172:175], v76, s[8:9]
	s_add_i32 s24, s23, 32
	s_mul_i32 s20, s24, 0x100000
	s_add_u32 s6, s48, s20
	s_addc_u32 s7, s49, 0
	s_cmp_lt_u32 s24, 16
	s_cselect_b32 s20, 1, 0
	s_sub_i32 s21, s24, 16
	s_bitcmp0_b32 s21, 2
	s_cselect_b32 s21, 1, 0
	s_cmp_lt_u32 s24, 40
	s_cselect_b32 s21, s21, 0
	s_or_b32 s20, s20, s21
	s_cmp_lg_u32 s20, 0
	s_cselect_b64 s[20:21], -1, 0
	v_cndmask_b32_e64 v91, v83, v87, s[20:21]
	v_cndmask_b32_e64 v92, v84, v88, s[20:21]
	v_cndmask_b32_e64 v93, v85, v89, s[20:21]
	v_cndmask_b32_e64 v94, v86, v90, s[20:21]
	ds_read_b32 v226, v112
	ds_read_b32 v227, v112 offset:512
	ds_read_b32 v228, v112 offset:1024
	ds_read_b32 v229, v112 offset:1536
	ds_read_b32 v230, v112 offset:2048
	ds_read_b32 v231, v112 offset:2560
	ds_read_b32 v232, v112 offset:3072
	ds_read_b32 v233, v112 offset:3584
	s_waitcnt lgkmcnt(0)
	v_bfe_u32 v120, v226, 16, 1
	v_bfe_u32 v121, v227, 16, 1
	v_bfe_u32 v122, v228, 16, 1
	v_bfe_u32 v123, v229, 16, 1
	v_bfe_u32 v124, v230, 16, 1
	v_bfe_u32 v125, v231, 16, 1
	v_bfe_u32 v126, v232, 16, 1
	v_bfe_u32 v127, v233, 16, 1
	v_add3_u32 v226, v226, v120, s63
	v_add3_u32 v227, v227, v121, s63
	v_add3_u32 v228, v228, v122, s63
	v_add3_u32 v229, v229, v123, s63
	v_add3_u32 v230, v230, v124, s63
	v_add3_u32 v231, v231, v125, s63
	v_add3_u32 v232, v232, v126, s63
	v_add3_u32 v233, v233, v127, s63
	v_perm_b32 v242, v227, v226, s64
	v_perm_b32 v243, v229, v228, s64
	v_perm_b32 v244, v231, v230, s64
	v_perm_b32 v245, v233, v232, s64
	s_nop 0
	global_store_dwordx4 v91, v[242:245], s[6:7]
	ds_read_b32 v226, v114
	ds_read_b32 v227, v114 offset:512
	ds_read_b32 v228, v114 offset:1024
	ds_read_b32 v229, v114 offset:1536
	ds_read_b32 v230, v114 offset:2048
	ds_read_b32 v231, v114 offset:2560
	ds_read_b32 v232, v114 offset:3072
	ds_read_b32 v233, v114 offset:3584
	s_waitcnt lgkmcnt(0)
	v_bfe_u32 v120, v226, 16, 1
	v_bfe_u32 v121, v227, 16, 1
	v_bfe_u32 v122, v228, 16, 1
	v_bfe_u32 v123, v229, 16, 1
	v_bfe_u32 v124, v230, 16, 1
	v_bfe_u32 v125, v231, 16, 1
	v_bfe_u32 v126, v232, 16, 1
	v_bfe_u32 v127, v233, 16, 1
	v_add3_u32 v226, v226, v120, s63
	v_add3_u32 v227, v227, v121, s63
	v_add3_u32 v228, v228, v122, s63
	v_add3_u32 v229, v229, v123, s63
	v_add3_u32 v230, v230, v124, s63
	v_add3_u32 v231, v231, v125, s63
	v_add3_u32 v232, v232, v126, s63
	v_add3_u32 v233, v233, v127, s63
	v_perm_b32 v242, v227, v226, s64
	v_perm_b32 v243, v229, v228, s64
	v_perm_b32 v244, v231, v230, s64
	v_perm_b32 v245, v233, v232, s64
	s_nop 0
	global_store_dwordx4 v92, v[242:245], s[6:7]
	ds_read_b32 v226, v116
	ds_read_b32 v227, v116 offset:512
	ds_read_b32 v228, v116 offset:1024
	ds_read_b32 v229, v116 offset:1536
	ds_read_b32 v230, v116 offset:2048
	ds_read_b32 v231, v116 offset:2560
	ds_read_b32 v232, v116 offset:3072
	ds_read_b32 v233, v116 offset:3584
	s_waitcnt lgkmcnt(0)
	v_bfe_u32 v120, v226, 16, 1
	v_bfe_u32 v121, v227, 16, 1
	v_bfe_u32 v122, v228, 16, 1
	v_bfe_u32 v123, v229, 16, 1
	v_bfe_u32 v124, v230, 16, 1
	v_bfe_u32 v125, v231, 16, 1
	v_bfe_u32 v126, v232, 16, 1
	v_bfe_u32 v127, v233, 16, 1
	v_add3_u32 v226, v226, v120, s63
	v_add3_u32 v227, v227, v121, s63
	v_add3_u32 v228, v228, v122, s63
	v_add3_u32 v229, v229, v123, s63
	v_add3_u32 v230, v230, v124, s63
	v_add3_u32 v231, v231, v125, s63
	v_add3_u32 v232, v232, v126, s63
	v_add3_u32 v233, v233, v127, s63
	v_perm_b32 v242, v227, v226, s64
	v_perm_b32 v243, v229, v228, s64
	v_perm_b32 v244, v231, v230, s64
	v_perm_b32 v245, v233, v232, s64
	s_nop 0
	global_store_dwordx4 v93, v[242:245], s[6:7]
	ds_read_b32 v226, v118
	ds_read_b32 v227, v118 offset:512
	ds_read_b32 v228, v118 offset:1024
	ds_read_b32 v229, v118 offset:1536
	ds_read_b32 v230, v118 offset:2048
	ds_read_b32 v231, v118 offset:2560
	ds_read_b32 v232, v118 offset:3072
	ds_read_b32 v233, v118 offset:3584
	s_waitcnt lgkmcnt(0)
	v_bfe_u32 v120, v226, 16, 1
	v_bfe_u32 v121, v227, 16, 1
	v_bfe_u32 v122, v228, 16, 1
	v_bfe_u32 v123, v229, 16, 1
	v_bfe_u32 v124, v230, 16, 1
	v_bfe_u32 v125, v231, 16, 1
	v_bfe_u32 v126, v232, 16, 1
	v_bfe_u32 v127, v233, 16, 1
	v_add3_u32 v226, v226, v120, s63
	v_add3_u32 v227, v227, v121, s63
	v_add3_u32 v228, v228, v122, s63
	v_add3_u32 v229, v229, v123, s63
	v_add3_u32 v230, v230, v124, s63
	v_add3_u32 v231, v231, v125, s63
	v_add3_u32 v232, v232, v126, s63
	v_add3_u32 v233, v233, v127, s63
	v_perm_b32 v242, v227, v226, s64
	v_perm_b32 v243, v229, v228, s64
	v_perm_b32 v244, v231, v230, s64
	v_perm_b32 v245, v233, v232, s64
	s_nop 0
	global_store_dwordx4 v94, v[242:245], s[6:7]
	s_waitcnt vmcnt(16)
	v_mul_f32_e32 v176, v42, v176
	v_mul_f32_e32 v177, v42, v177
	v_mul_f32_e32 v178, v42, v178
	v_mul_f32_e32 v179, v42, v179
	ds_write_b128 v210, v[176:179]
	v_mul_f32_e32 v180, v43, v180
	v_mul_f32_e32 v181, v43, v181
	v_mul_f32_e32 v182, v43, v182
	v_mul_f32_e32 v183, v43, v183
	ds_write_b128 v210, v[180:183] offset:1024
	v_mul_f32_e32 v184, v44, v184
	v_mul_f32_e32 v185, v44, v185
	v_mul_f32_e32 v186, v44, v186
	v_mul_f32_e32 v187, v44, v187
	ds_write_b128 v210, v[184:187] offset:2048
	v_mul_f32_e32 v188, v45, v188
	v_mul_f32_e32 v189, v45, v189
	v_mul_f32_e32 v190, v45, v190
	v_mul_f32_e32 v191, v45, v191
	ds_write_b128 v210, v[188:191] offset:3072
	v_mul_f32_e32 v192, v46, v192
	v_mul_f32_e32 v193, v46, v193
	v_mul_f32_e32 v194, v46, v194
	v_mul_f32_e32 v195, v46, v195
	ds_write_b128 v210, v[192:195] offset:4096
	v_mul_f32_e32 v196, v47, v196
	v_mul_f32_e32 v197, v47, v197
	v_mul_f32_e32 v198, v47, v198
	v_mul_f32_e32 v199, v47, v199
	ds_write_b128 v210, v[196:199] offset:5120
	v_mul_f32_e32 v200, v48, v200
	v_mul_f32_e32 v201, v48, v201
	v_mul_f32_e32 v202, v48, v202
	v_mul_f32_e32 v203, v48, v203
	ds_write_b128 v210, v[200:203] offset:6144
	v_mul_f32_e32 v204, v49, v204
	v_mul_f32_e32 v205, v49, v205
	v_mul_f32_e32 v206, v49, v206
	v_mul_f32_e32 v207, v49, v207
	ds_write_b128 v210, v[204:207] offset:7168
	s_waitcnt lgkmcnt(0)
	s_barrier
; #define GAS __attribute__((address_space(1)))
; #define LAS __attribute__((address_space(3)))
; #define LDS_WAIT() asm volatile("s_waitcnt lgkmcnt(0)" ::: "memory")
; __device__ __forceinline__ unsigned pk2(float lo, float hi) { return f2bf(lo) | (f2bf(hi) << 16); }
; __device__ __forceinline__ int nat_dim(int p) { return (p >> 1) + 64 * (p & 1); }
; template <int MAP, bool KS, bool KPERM = false>
; __device__ __forceinline__ void p0_transpose_item(const float* W, int K, int Nsrc, int nblk, bf16* WT, const float* ksA, const float* ksB, int ksplit, LAS float* scr, int item, int lane) {
;     ...
;     const int nr = n0 + (lane & 31); const int sc = MAP == 1 ? src_col_in(nr) : (MAP == 2 ? nat_dim(nr) : nr);
;     float v[32];
; #pragma unroll
;     for (int i = 0; i < 32; ++i) { const int k = k0 + 2 * i + (lane >> 5); const int ksrc = KPERM ? ((k & ~127) + nat_dim(k & 127)) : k;
;         v[i] = sc >= 0 ? W[(size_t)ksrc * Nsrc + sc] : 0.f; }
; #pragma unroll
;     for (int i = 0; i < 32; ++i) { const int kk = 2 * i + (lane >> 5); const int k = k0 + kk;
;         if (KS) v[i] *= (k < ksplit ? ksA[k] : ksB[k - ksplit]);
;         scr[kk * 33 + (lane & 31)] = v[i]; }
;     LDS_WAIT(); asm volatile("" ::: "memory");
;     const int c = lane & 7;
; #pragma unroll
;     for (int j = 0; j < 4; ++j) { const int n = (lane >> 3) + 8 * j; const LAS float* s = scr + (8 * c) * 33 + n;
;         v4u o; o.x = pk2(s[0 * 33], s[1 * 33]); o.y = pk2(s[2 * 33], s[3 * 33]); o.z = pk2(s[4 * 33], s[5 * 33]); o.w = pk2(s[6 * 33], s[7 * 33]);
;         *(GAS v4u*)(WT + (size_t)(n0 + n) * K + k0 + 8 * c) = o; }
	s_add_i32 s24, s23, 56
	s_lshl_b32 s20, s24, 7
	s_cmp_lt_u32 s24, 40
	s_cselect_b32 s21, 0, 0x830
	s_cmp_lt_u32 s24, 72
	s_cselect_b32 s21, s21, 0xfffff030
	s_add_i32 s20, s20, s21
	s_lshl_b32 s20, s20, 2
	s_add_u32 s8, s46, s20
	s_addc_u32 s9, s47, 0
	global_load_dwordx4 v[176:179], v76, s[8:9]
	s_add_u32 s8, s8, 0x16280
	s_addc_u32 s9, s9, 0
	global_load_dwordx4 v[180:183], v76, s[8:9]
	s_add_u32 s8, s8, 0x16280
	s_addc_u32 s9, s9, 0
	global_load_dwordx4 v[184:187], v76, s[8:9]
	s_add_u32 s8, s8, 0x16280
	s_addc_u32 s9, s9, 0
	global_load_dwordx4 v[188:191], v76, s[8:9]
	s_add_u32 s8, s8, 0x16280
	s_addc_u32 s9, s9, 0
	global_load_dwordx4 v[192:195], v76, s[8:9]
	s_add_u32 s8, s8, 0x16280
	s_addc_u32 s9, s9, 0
	global_load_dwordx4 v[196:199], v76, s[8:9]
	s_add_u32 s8, s8, 0x16280
	s_addc_u32 s9, s9, 0
	global_load_dwordx4 v[200:203], v76, s[8:9]
	s_add_u32 s8, s8, 0x16280
	s_addc_u32 s9, s9, 0
	global_load_dwordx4 v[204:207], v76, s[8:9]
	s_add_i32 s24, s23, 40
	s_mul_i32 s20, s24, 0x100000
	s_add_u32 s6, s48, s20
	s_addc_u32 s7, s49, 0
	s_cmp_lt_u32 s24, 16
	s_cselect_b32 s20, 1, 0
	s_sub_i32 s21, s24, 16
	s_bitcmp0_b32 s21, 2
	s_cselect_b32 s21, 1, 0
	s_cmp_lt_u32 s24, 40
	s_cselect_b32 s21, s21, 0
	s_or_b32 s20, s20, s21
	s_cmp_lg_u32 s20, 0
	s_cselect_b64 s[20:21], -1, 0
	v_cndmask_b32_e64 v91, v83, v87, s[20:21]
	v_cndmask_b32_e64 v92, v84, v88, s[20:21]
	v_cndmask_b32_e64 v93, v85, v89, s[20:21]
	v_cndmask_b32_e64 v94, v86, v90, s[20:21]
	ds_read_b32 v226, v113
	ds_read_b32 v227, v113 offset:512
	ds_read_b32 v228, v113 offset:1024
	ds_read_b32 v229, v113 offset:1536
	ds_read_b32 v230, v113 offset:2048
	ds_read_b32 v231, v113 offset:2560
	ds_read_b32 v232, v113 offset:3072
	ds_read_b32 v233, v113 offset:3584
	s_waitcnt lgkmcnt(0)
	v_bfe_u32 v120, v226, 16, 1
	v_bfe_u32 v121, v227, 16, 1
	v_bfe_u32 v122, v228, 16, 1
	v_bfe_u32 v123, v229, 16, 1
	v_bfe_u32 v124, v230, 16, 1
	v_bfe_u32 v125, v231, 16, 1
	v_bfe_u32 v126, v232, 16, 1
	v_bfe_u32 v127, v233, 16, 1
	v_add3_u32 v226, v226, v120, s63
	v_add3_u32 v227, v227, v121, s63
	v_add3_u32 v228, v228, v122, s63
	v_add3_u32 v229, v229, v123, s63
	v_add3_u32 v230, v230, v124, s63
	v_add3_u32 v231, v231, v125, s63
	v_add3_u32 v232, v232, v126, s63
	v_add3_u32 v233, v233, v127, s63
	v_perm_b32 v242, v227, v226, s64
	v_perm_b32 v243, v229, v228, s64
	v_perm_b32 v244, v231, v230, s64
	v_perm_b32 v245, v233, v232, s64
	s_nop 0
	global_store_dwordx4 v91, v[242:245], s[6:7]
	ds_read_b32 v226, v115
	ds_read_b32 v227, v115 offset:512
	ds_read_b32 v228, v115 offset:1024
	ds_read_b32 v229, v115 offset:1536
	ds_read_b32 v230, v115 offset:2048
	ds_read_b32 v231, v115 offset:2560
	ds_read_b32 v232, v115 offset:3072
	ds_read_b32 v233, v115 offset:3584
	s_waitcnt lgkmcnt(0)
	v_bfe_u32 v120, v226, 16, 1
	v_bfe_u32 v121, v227, 16, 1
	v_bfe_u32 v122, v228, 16, 1
	v_bfe_u32 v123, v229, 16, 1
	v_bfe_u32 v124, v230, 16, 1
	v_bfe_u32 v125, v231, 16, 1
	v_bfe_u32 v126, v232, 16, 1
	v_bfe_u32 v127, v233, 16, 1
	v_add3_u32 v226, v226, v120, s63
	v_add3_u32 v227, v227, v121, s63
	v_add3_u32 v228, v228, v122, s63
	v_add3_u32 v229, v229, v123, s63
	v_add3_u32 v230, v230, v124, s63
	v_add3_u32 v231, v231, v125, s63
	v_add3_u32 v232, v232, v126, s63
	v_add3_u32 v233, v233, v127, s63
	v_perm_b32 v242, v227, v226, s64
	v_perm_b32 v243, v229, v228, s64
	v_perm_b32 v244, v231, v230, s64
	v_perm_b32 v245, v233, v232, s64
	s_nop 0
	global_store_dwordx4 v92, v[242:245], s[6:7]
	ds_read_b32 v226, v117
	ds_read_b32 v227, v117 offset:512
	ds_read_b32 v228, v117 offset:1024
	ds_read_b32 v229, v117 offset:1536
	ds_read_b32 v230, v117 offset:2048
	ds_read_b32 v231, v117 offset:2560
	ds_read_b32 v232, v117 offset:3072
	ds_read_b32 v233, v117 offset:3584
	s_waitcnt lgkmcnt(0)
	v_bfe_u32 v120, v226, 16, 1
	v_bfe_u32 v121, v227, 16, 1
	v_bfe_u32 v122, v228, 16, 1
	v_bfe_u32 v123, v229, 16, 1
	v_bfe_u32 v124, v230, 16, 1
	v_bfe_u32 v125, v231, 16, 1
	v_bfe_u32 v126, v232, 16, 1
	v_bfe_u32 v127, v233, 16, 1
	v_add3_u32 v226, v226, v120, s63
	v_add3_u32 v227, v227, v121, s63
	v_add3_u32 v228, v228, v122, s63
	v_add3_u32 v229, v229, v123, s63
	v_add3_u32 v230, v230, v124, s63
	v_add3_u32 v231, v231, v125, s63
	v_add3_u32 v232, v232, v126, s63
	v_add3_u32 v233, v233, v127, s63
	v_perm_b32 v242, v227, v226, s64
	v_perm_b32 v243, v229, v228, s64
	v_perm_b32 v244, v231, v230, s64
	v_perm_b32 v245, v233, v232, s64
	s_nop 0
	global_store_dwordx4 v93, v[242:245], s[6:7]
	ds_read_b32 v226, v119
	ds_read_b32 v227, v119 offset:512
	ds_read_b32 v228, v119 offset:1024
	ds_read_b32 v229, v119 offset:1536
	ds_read_b32 v230, v119 offset:2048
	ds_read_b32 v231, v119 offset:2560
	ds_read_b32 v232, v119 offset:3072
	ds_read_b32 v233, v119 offset:3584
	s_waitcnt lgkmcnt(0)
	v_bfe_u32 v120, v226, 16, 1
	v_bfe_u32 v121, v227, 16, 1
	v_bfe_u32 v122, v228, 16, 1
	v_bfe_u32 v123, v229, 16, 1
	v_bfe_u32 v124, v230, 16, 1
	v_bfe_u32 v125, v231, 16, 1
	v_bfe_u32 v126, v232, 16, 1
	v_bfe_u32 v127, v233, 16, 1
	v_add3_u32 v226, v226, v120, s63
	v_add3_u32 v227, v227, v121, s63
	v_add3_u32 v228, v228, v122, s63
	v_add3_u32 v229, v229, v123, s63
	v_add3_u32 v230, v230, v124, s63
	v_add3_u32 v231, v231, v125, s63
	v_add3_u32 v232, v232, v126, s63
	v_add3_u32 v233, v233, v127, s63
	v_perm_b32 v242, v227, v226, s64
	v_perm_b32 v243, v229, v228, s64
	v_perm_b32 v244, v231, v230, s64
	v_perm_b32 v245, v233, v232, s64
	s_nop 0
	global_store_dwordx4 v94, v[242:245], s[6:7]
	s_waitcnt vmcnt(16)
	v_mul_f32_e32 v144, v42, v144
	v_mul_f32_e32 v145, v42, v145
	v_mul_f32_e32 v146, v42, v146
	v_mul_f32_e32 v147, v42, v147
	ds_write_b128 v209, v[144:147]
	v_mul_f32_e32 v148, v43, v148
	v_mul_f32_e32 v149, v43, v149
	v_mul_f32_e32 v150, v43, v150
	v_mul_f32_e32 v151, v43, v151
	ds_write_b128 v209, v[148:151] offset:1024
	v_mul_f32_e32 v152, v44, v152
	v_mul_f32_e32 v153, v44, v153
	v_mul_f32_e32 v154, v44, v154
	v_mul_f32_e32 v155, v44, v155
	ds_write_b128 v209, v[152:155] offset:2048
	v_mul_f32_e32 v156, v45, v156
	v_mul_f32_e32 v157, v45, v157
	v_mul_f32_e32 v158, v45, v158
	v_mul_f32_e32 v159, v45, v159
	ds_write_b128 v209, v[156:159] offset:3072
	v_mul_f32_e32 v160, v46, v160
	v_mul_f32_e32 v161, v46, v161
	v_mul_f32_e32 v162, v46, v162
	v_mul_f32_e32 v163, v46, v163
	ds_write_b128 v209, v[160:163] offset:4096
	v_mul_f32_e32 v164, v47, v164
	v_mul_f32_e32 v165, v47, v165
	v_mul_f32_e32 v166, v47, v166
	v_mul_f32_e32 v167, v47, v167
	ds_write_b128 v209, v[164:167] offset:5120
	v_mul_f32_e32 v168, v48, v168
	v_mul_f32_e32 v169, v48, v169
	v_mul_f32_e32 v170, v48, v170
	v_mul_f32_e32 v171, v48, v171
	ds_write_b128 v209, v[168:171] offset:6144
	v_mul_f32_e32 v172, v49, v172
	v_mul_f32_e32 v173, v49, v173
	v_mul_f32_e32 v174, v49, v174
	v_mul_f32_e32 v175, v49, v175
	ds_write_b128 v209, v[172:175] offset:7168
	s_waitcnt lgkmcnt(0)
	s_barrier
; #define GAS __attribute__((address_space(1)))
; #define LAS __attribute__((address_space(3)))
; #define LDS_WAIT() asm volatile("s_waitcnt lgkmcnt(0)" ::: "memory")
; __device__ __forceinline__ unsigned pk2(float lo, float hi) { return f2bf(lo) | (f2bf(hi) << 16); }
; __device__ __forceinline__ int nat_dim(int p) { return (p >> 1) + 64 * (p & 1); }
; template <int MAP, bool KS, bool KPERM = false>
; __device__ __forceinline__ void p0_transpose_item(const float* W, int K, int Nsrc, int nblk, bf16* WT, const float* ksA, const float* ksB, int ksplit, LAS float* scr, int item, int lane) {
;     ...
;     const int nr = n0 + (lane & 31); const int sc = MAP == 1 ? src_col_in(nr) : (MAP == 2 ? nat_dim(nr) : nr);
;     float v[32];
; #pragma unroll
;     for (int i = 0; i < 32; ++i) { const int k = k0 + 2 * i + (lane >> 5); const int ksrc = KPERM ? ((k & ~127) + nat_dim(k & 127)) : k;
;         v[i] = sc >= 0 ? W[(size_t)ksrc * Nsrc + sc] : 0.f; }
; #pragma unroll
;     for (int i = 0; i < 32; ++i) { const int kk = 2 * i + (lane >> 5); const int k = k0 + kk;
;         if (KS) v[i] *= (k < ksplit ? ksA[k] : ksB[k - ksplit]);
;         scr[kk * 33 + (lane & 31)] = v[i]; }
;     LDS_WAIT(); asm volatile("" ::: "memory");
;     const int c = lane & 7;
; #pragma unroll
;     for (int j = 0; j < 4; ++j) { const int n = (lane >> 3) + 8 * j; const LAS float* s = scr + (8 * c) * 33 + n;
;         v4u o; o.x = pk2(s[0 * 33], s[1 * 33]); o.y = pk2(s[2 * 33], s[3 * 33]); o.z = pk2(s[4 * 33], s[5 * 33]); o.w = pk2(s[6 * 33], s[7 * 33]);
;         *(GAS v4u*)(WT + (size_t)(n0 + n) * K + k0 + 8 * c) = o; }
	s_add_i32 s24, s23, 64
	s_lshl_b32 s20, s24, 7
	s_cmp_lt_u32 s24, 40
	s_cselect_b32 s21, 0, 0x830
	s_cmp_lt_u32 s24, 72
	s_cselect_b32 s21, s21, 0xfffff030
	s_add_i32 s20, s20, s21
	s_lshl_b32 s20, s20, 2
	s_add_u32 s8, s46, s20
	s_addc_u32 s9, s47, 0
	global_load_dwordx4 v[144:147], v76, s[8:9]
	s_add_u32 s8, s8, 0x16280
	s_addc_u32 s9, s9, 0
	global_load_dwordx4 v[148:151], v76, s[8:9]
	s_add_u32 s8, s8, 0x16280
	s_addc_u32 s9, s9, 0
	global_load_dwordx4 v[152:155], v76, s[8:9]
	s_add_u32 s8, s8, 0x16280
	s_addc_u32 s9, s9, 0
	global_load_dwordx4 v[156:159], v76, s[8:9]
	s_add_u32 s8, s8, 0x16280
	s_addc_u32 s9, s9, 0
	global_load_dwordx4 v[160:163], v76, s[8:9]
	s_add_u32 s8, s8, 0x16280
	s_addc_u32 s9, s9, 0
	global_load_dwordx4 v[164:167], v76, s[8:9]
	s_add_u32 s8, s8, 0x16280
	s_addc_u32 s9, s9, 0
	global_load_dwordx4 v[168:171], v76, s[8:9]
	s_add_u32 s8, s8, 0x16280
	s_addc_u32 s9, s9, 0
	global_load_dwordx4 v[172:175], v76, s[8:9]
	s_add_i32 s24, s23, 48
	s_mul_i32 s20, s24, 0x100000
	s_add_u32 s6, s48, s20
	s_addc_u32 s7, s49, 0
	s_cmp_lt_u32 s24, 16
	s_cselect_b32 s20, 1, 0
	s_sub_i32 s21, s24, 16
	s_bitcmp0_b32 s21, 2
	s_cselect_b32 s21, 1, 0
	s_cmp_lt_u32 s24, 40
	s_cselect_b32 s21, s21, 0
	s_or_b32 s20, s20, s21
	s_cmp_lg_u32 s20, 0
	s_cselect_b64 s[20:21], -1, 0
	v_cndmask_b32_e64 v91, v83, v87, s[20:21]
	v_cndmask_b32_e64 v92, v84, v88, s[20:21]
	v_cndmask_b32_e64 v93, v85, v89, s[20:21]
	v_cndmask_b32_e64 v94, v86, v90, s[20:21]
	ds_read_b32 v226, v112
	ds_read_b32 v227, v112 offset:512
	ds_read_b32 v228, v112 offset:1024
	ds_read_b32 v229, v112 offset:1536
	ds_read_b32 v230, v112 offset:2048
	ds_read_b32 v231, v112 offset:2560
	ds_read_b32 v232, v112 offset:3072
	ds_read_b32 v233, v112 offset:3584
	s_waitcnt lgkmcnt(0)
	v_bfe_u32 v120, v226, 16, 1
	v_bfe_u32 v121, v227, 16, 1
	v_bfe_u32 v122, v228, 16, 1
	v_bfe_u32 v123, v229, 16, 1
	v_bfe_u32 v124, v230, 16, 1
	v_bfe_u32 v125, v231, 16, 1
	v_bfe_u32 v126, v232, 16, 1
	v_bfe_u32 v127, v233, 16, 1
	v_add3_u32 v226, v226, v120, s63
	v_add3_u32 v227, v227, v121, s63
	v_add3_u32 v228, v228, v122, s63
	v_add3_u32 v229, v229, v123, s63
	v_add3_u32 v230, v230, v124, s63
	v_add3_u32 v231, v231, v125, s63
	v_add3_u32 v232, v232, v126, s63
	v_add3_u32 v233, v233, v127, s63
	v_perm_b32 v242, v227, v226, s64
	v_perm_b32 v243, v229, v228, s64
	v_perm_b32 v244, v231, v230, s64
	v_perm_b32 v245, v233, v232, s64
	s_nop 0
	global_store_dwordx4 v91, v[242:245], s[6:7]
	ds_read_b32 v226, v114
	ds_read_b32 v227, v114 offset:512
	ds_read_b32 v228, v114 offset:1024
	ds_read_b32 v229, v114 offset:1536
	ds_read_b32 v230, v114 offset:2048
	ds_read_b32 v231, v114 offset:2560
	ds_read_b32 v232, v114 offset:3072
	ds_read_b32 v233, v114 offset:3584
	s_waitcnt lgkmcnt(0)
	v_bfe_u32 v120, v226, 16, 1
	v_bfe_u32 v121, v227, 16, 1
	v_bfe_u32 v122, v228, 16, 1
	v_bfe_u32 v123, v229, 16, 1
	v_bfe_u32 v124, v230, 16, 1
	v_bfe_u32 v125, v231, 16, 1
	v_bfe_u32 v126, v232, 16, 1
	v_bfe_u32 v127, v233, 16, 1
	v_add3_u32 v226, v226, v120, s63
	v_add3_u32 v227, v227, v121, s63
	v_add3_u32 v228, v228, v122, s63
	v_add3_u32 v229, v229, v123, s63
	v_add3_u32 v230, v230, v124, s63
	v_add3_u32 v231, v231, v125, s63
	v_add3_u32 v232, v232, v126, s63
	v_add3_u32 v233, v233, v127, s63
	v_perm_b32 v242, v227, v226, s64
	v_perm_b32 v243, v229, v228, s64
	v_perm_b32 v244, v231, v230, s64
	v_perm_b32 v245, v233, v232, s64
	s_nop 0
	global_store_dwordx4 v92, v[242:245], s[6:7]
	ds_read_b32 v226, v116
	ds_read_b32 v227, v116 offset:512
	ds_read_b32 v228, v116 offset:1024
	ds_read_b32 v229, v116 offset:1536
	ds_read_b32 v230, v116 offset:2048
	ds_read_b32 v231, v116 offset:2560
	ds_read_b32 v232, v116 offset:3072
	ds_read_b32 v233, v116 offset:3584
	s_waitcnt lgkmcnt(0)
	v_bfe_u32 v120, v226, 16, 1
	v_bfe_u32 v121, v227, 16, 1
	v_bfe_u32 v122, v228, 16, 1
	v_bfe_u32 v123, v229, 16, 1
	v_bfe_u32 v124, v230, 16, 1
	v_bfe_u32 v125, v231, 16, 1
	v_bfe_u32 v126, v232, 16, 1
	v_bfe_u32 v127, v233, 16, 1
	v_add3_u32 v226, v226, v120, s63
	v_add3_u32 v227, v227, v121, s63
	v_add3_u32 v228, v228, v122, s63
	v_add3_u32 v229, v229, v123, s63
	v_add3_u32 v230, v230, v124, s63
	v_add3_u32 v231, v231, v125, s63
	v_add3_u32 v232, v232, v126, s63
	v_add3_u32 v233, v233, v127, s63
	v_perm_b32 v242, v227, v226, s64
	v_perm_b32 v243, v229, v228, s64
	v_perm_b32 v244, v231, v230, s64
	v_perm_b32 v245, v233, v232, s64
	s_nop 0
	global_store_dwordx4 v93, v[242:245], s[6:7]
	ds_read_b32 v226, v118
	ds_read_b32 v227, v118 offset:512
	ds_read_b32 v228, v118 offset:1024
	ds_read_b32 v229, v118 offset:1536
	ds_read_b32 v230, v118 offset:2048
	ds_read_b32 v231, v118 offset:2560
	ds_read_b32 v232, v118 offset:3072
	ds_read_b32 v233, v118 offset:3584
	s_waitcnt lgkmcnt(0)
	v_bfe_u32 v120, v226, 16, 1
	v_bfe_u32 v121, v227, 16, 1
	v_bfe_u32 v122, v228, 16, 1
	v_bfe_u32 v123, v229, 16, 1
	v_bfe_u32 v124, v230, 16, 1
	v_bfe_u32 v125, v231, 16, 1
	v_bfe_u32 v126, v232, 16, 1
	v_bfe_u32 v127, v233, 16, 1
	v_add3_u32 v226, v226, v120, s63
	v_add3_u32 v227, v227, v121, s63
	v_add3_u32 v228, v228, v122, s63
	v_add3_u32 v229, v229, v123, s63
	v_add3_u32 v230, v230, v124, s63
	v_add3_u32 v231, v231, v125, s63
	v_add3_u32 v232, v232, v126, s63
	v_add3_u32 v233, v233, v127, s63
	v_perm_b32 v242, v227, v226, s64
	v_perm_b32 v243, v229, v228, s64
	v_perm_b32 v244, v231, v230, s64
	v_perm_b32 v245, v233, v232, s64
	s_nop 0
	global_store_dwordx4 v94, v[242:245], s[6:7]
	s_waitcnt vmcnt(16)
	v_mul_f32_e32 v176, v42, v176
	v_mul_f32_e32 v177, v42, v177
	v_mul_f32_e32 v178, v42, v178
	v_mul_f32_e32 v179, v42, v179
	ds_write_b128 v210, v[176:179]
	v_mul_f32_e32 v180, v43, v180
	v_mul_f32_e32 v181, v43, v181
	v_mul_f32_e32 v182, v43, v182
	v_mul_f32_e32 v183, v43, v183
	ds_write_b128 v210, v[180:183] offset:1024
	v_mul_f32_e32 v184, v44, v184
	v_mul_f32_e32 v185, v44, v185
	v_mul_f32_e32 v186, v44, v186
	v_mul_f32_e32 v187, v44, v187
	ds_write_b128 v210, v[184:187] offset:2048
	v_mul_f32_e32 v188, v45, v188
	v_mul_f32_e32 v189, v45, v189
	v_mul_f32_e32 v190, v45, v190
	v_mul_f32_e32 v191, v45, v191
	ds_write_b128 v210, v[188:191] offset:3072
	v_mul_f32_e32 v192, v46, v192
	v_mul_f32_e32 v193, v46, v193
	v_mul_f32_e32 v194, v46, v194
	v_mul_f32_e32 v195, v46, v195
	ds_write_b128 v210, v[192:195] offset:4096
	v_mul_f32_e32 v196, v47, v196
	v_mul_f32_e32 v197, v47, v197
	v_mul_f32_e32 v198, v47, v198
	v_mul_f32_e32 v199, v47, v199
	ds_write_b128 v210, v[196:199] offset:5120
	v_mul_f32_e32 v200, v48, v200
	v_mul_f32_e32 v201, v48, v201
	v_mul_f32_e32 v202, v48, v202
	v_mul_f32_e32 v203, v48, v203
	ds_write_b128 v210, v[200:203] offset:6144
	v_mul_f32_e32 v204, v49, v204
	v_mul_f32_e32 v205, v49, v205
	v_mul_f32_e32 v206, v49, v206
	v_mul_f32_e32 v207, v49, v207
	ds_write_b128 v210, v[204:207] offset:7168
	s_waitcnt lgkmcnt(0)
	s_barrier
; #define GAS __attribute__((address_space(1)))
; #define LAS __attribute__((address_space(3)))
; #define LDS_WAIT() asm volatile("s_waitcnt lgkmcnt(0)" ::: "memory")
; __device__ __forceinline__ unsigned pk2(float lo, float hi) { return f2bf(lo) | (f2bf(hi) << 16); }
; __device__ __forceinline__ int nat_dim(int p) { return (p >> 1) + 64 * (p & 1); }
; template <int MAP, bool KS, bool KPERM = false>
; __device__ __forceinline__ void p0_transpose_item(const float* W, int K, int Nsrc, int nblk, bf16* WT, const float* ksA, const float* ksB, int ksplit, LAS float* scr, int item, int lane) {
;     ...
;     const int nr = n0 + (lane & 31); const int sc = MAP == 1 ? src_col_in(nr) : (MAP == 2 ? nat_dim(nr) : nr);
;     float v[32];
; #pragma unroll
;     for (int i = 0; i < 32; ++i) { const int k = k0 + 2 * i + (lane >> 5); const int ksrc = KPERM ? ((k & ~127) + nat_dim(k & 127)) : k;
;         v[i] = sc >= 0 ? W[(size_t)ksrc * Nsrc + sc] : 0.f; }
; #pragma unroll
;     for (int i = 0; i < 32; ++i) { const int kk = 2 * i + (lane >> 5); const int k = k0 + kk;
;         if (KS) v[i] *= (k < ksplit ? ksA[k] : ksB[k - ksplit]);
;         scr[kk * 33 + (lane & 31)] = v[i]; }
;     LDS_WAIT(); asm volatile("" ::: "memory");
;     const int c = lane & 7;
; #pragma unroll
;     for (int j = 0; j < 4; ++j) { const int n = (lane >> 3) + 8 * j; const LAS float* s = scr + (8 * c) * 33 + n;
;         v4u o; o.x = pk2(s[0 * 33], s[1 * 33]); o.y = pk2(s[2 * 33], s[3 * 33]); o.z = pk2(s[4 * 33], s[5 * 33]); o.w = pk2(s[6 * 33], s[7 * 33]);
;         *(GAS v4u*)(WT + (size_t)(n0 + n) * K + k0 + 8 * c) = o; }
	s_add_i32 s24, s23, 72
	s_lshl_b32 s20, s24, 7
	s_cmp_lt_u32 s24, 40
	s_cselect_b32 s21, 0, 0x830
	s_cmp_lt_u32 s24, 72
	s_cselect_b32 s21, s21, 0xfffff030
	s_add_i32 s20, s20, s21
	s_lshl_b32 s20, s20, 2
	s_add_u32 s8, s46, s20
	s_addc_u32 s9, s47, 0
	global_load_dwordx4 v[176:179], v76, s[8:9]
	s_add_u32 s8, s8, 0x16280
	s_addc_u32 s9, s9, 0
	global_load_dwordx4 v[180:183], v76, s[8:9]
	s_add_u32 s8, s8, 0x16280
	s_addc_u32 s9, s9, 0
	global_load_dwordx4 v[184:187], v76, s[8:9]
	s_add_u32 s8, s8, 0x16280
	s_addc_u32 s9, s9, 0
	global_load_dwordx4 v[188:191], v76, s[8:9]
	s_add_u32 s8, s8, 0x16280
	s_addc_u32 s9, s9, 0
	global_load_dwordx4 v[192:195], v76, s[8:9]
	s_add_u32 s8, s8, 0x16280
	s_addc_u32 s9, s9, 0
	global_load_dwordx4 v[196:199], v76, s[8:9]
	s_add_u32 s8, s8, 0x16280
	s_addc_u32 s9, s9, 0
	global_load_dwordx4 v[200:203], v76, s[8:9]
	s_add_u32 s8, s8, 0x16280
	s_addc_u32 s9, s9, 0
	global_load_dwordx4 v[204:207], v76, s[8:9]
	s_add_i32 s24, s23, 56
	s_mul_i32 s20, s24, 0x100000
	s_add_u32 s6, s48, s20
	s_addc_u32 s7, s49, 0
	s_cmp_lt_u32 s24, 16
	s_cselect_b32 s20, 1, 0
	s_sub_i32 s21, s24, 16
	s_bitcmp0_b32 s21, 2
	s_cselect_b32 s21, 1, 0
	s_cmp_lt_u32 s24, 40
	s_cselect_b32 s21, s21, 0
	s_or_b32 s20, s20, s21
	s_cmp_lg_u32 s20, 0
	s_cselect_b64 s[20:21], -1, 0
	v_cndmask_b32_e64 v91, v83, v87, s[20:21]
	v_cndmask_b32_e64 v92, v84, v88, s[20:21]
	v_cndmask_b32_e64 v93, v85, v89, s[20:21]
	v_cndmask_b32_e64 v94, v86, v90, s[20:21]
	ds_read_b32 v226, v113
	ds_read_b32 v227, v113 offset:512
	ds_read_b32 v228, v113 offset:1024
	ds_read_b32 v229, v113 offset:1536
	ds_read_b32 v230, v113 offset:2048
	ds_read_b32 v231, v113 offset:2560
	ds_read_b32 v232, v113 offset:3072
	ds_read_b32 v233, v113 offset:3584
	s_waitcnt lgkmcnt(0)
	v_bfe_u32 v120, v226, 16, 1
	v_bfe_u32 v121, v227, 16, 1
	v_bfe_u32 v122, v228, 16, 1
	v_bfe_u32 v123, v229, 16, 1
	v_bfe_u32 v124, v230, 16, 1
	v_bfe_u32 v125, v231, 16, 1
	v_bfe_u32 v126, v232, 16, 1
	v_bfe_u32 v127, v233, 16, 1
	v_add3_u32 v226, v226, v120, s63
	v_add3_u32 v227, v227, v121, s63
	v_add3_u32 v228, v228, v122, s63
	v_add3_u32 v229, v229, v123, s63
	v_add3_u32 v230, v230, v124, s63
	v_add3_u32 v231, v231, v125, s63
	v_add3_u32 v232, v232, v126, s63
	v_add3_u32 v233, v233, v127, s63
	v_perm_b32 v242, v227, v226, s64
	v_perm_b32 v243, v229, v228, s64
	v_perm_b32 v244, v231, v230, s64
	v_perm_b32 v245, v233, v232, s64
	s_nop 0
	global_store_dwordx4 v91, v[242:245], s[6:7]
	ds_read_b32 v226, v115
	ds_read_b32 v227, v115 offset:512
	ds_read_b32 v228, v115 offset:1024
	ds_read_b32 v229, v115 offset:1536
	ds_read_b32 v230, v115 offset:2048
	ds_read_b32 v231, v115 offset:2560
	ds_read_b32 v232, v115 offset:3072
	ds_read_b32 v233, v115 offset:3584
	s_waitcnt lgkmcnt(0)
	v_bfe_u32 v120, v226, 16, 1
	v_bfe_u32 v121, v227, 16, 1
	v_bfe_u32 v122, v228, 16, 1
	v_bfe_u32 v123, v229, 16, 1
	v_bfe_u32 v124, v230, 16, 1
	v_bfe_u32 v125, v231, 16, 1
	v_bfe_u32 v126, v232, 16, 1
	v_bfe_u32 v127, v233, 16, 1
	v_add3_u32 v226, v226, v120, s63
	v_add3_u32 v227, v227, v121, s63
	v_add3_u32 v228, v228, v122, s63
	v_add3_u32 v229, v229, v123, s63
	v_add3_u32 v230, v230, v124, s63
	v_add3_u32 v231, v231, v125, s63
	v_add3_u32 v232, v232, v126, s63
	v_add3_u32 v233, v233, v127, s63
	v_perm_b32 v242, v227, v226, s64
	v_perm_b32 v243, v229, v228, s64
	v_perm_b32 v244, v231, v230, s64
	v_perm_b32 v245, v233, v232, s64
	s_nop 0
	global_store_dwordx4 v92, v[242:245], s[6:7]
	ds_read_b32 v226, v117
	ds_read_b32 v227, v117 offset:512
	ds_read_b32 v228, v117 offset:1024
	ds_read_b32 v229, v117 offset:1536
	ds_read_b32 v230, v117 offset:2048
	ds_read_b32 v231, v117 offset:2560
	ds_read_b32 v232, v117 offset:3072
	ds_read_b32 v233, v117 offset:3584
	s_waitcnt lgkmcnt(0)
	v_bfe_u32 v120, v226, 16, 1
	v_bfe_u32 v121, v227, 16, 1
	v_bfe_u32 v122, v228, 16, 1
	v_bfe_u32 v123, v229, 16, 1
	v_bfe_u32 v124, v230, 16, 1
	v_bfe_u32 v125, v231, 16, 1
	v_bfe_u32 v126, v232, 16, 1
	v_bfe_u32 v127, v233, 16, 1
	v_add3_u32 v226, v226, v120, s63
	v_add3_u32 v227, v227, v121, s63
	v_add3_u32 v228, v228, v122, s63
	v_add3_u32 v229, v229, v123, s63
	v_add3_u32 v230, v230, v124, s63
	v_add3_u32 v231, v231, v125, s63
	v_add3_u32 v232, v232, v126, s63
	v_add3_u32 v233, v233, v127, s63
	v_perm_b32 v242, v227, v226, s64
	v_perm_b32 v243, v229, v228, s64
	v_perm_b32 v244, v231, v230, s64
	v_perm_b32 v245, v233, v232, s64
	s_nop 0
	global_store_dwordx4 v93, v[242:245], s[6:7]
	ds_read_b32 v226, v119
	ds_read_b32 v227, v119 offset:512
	ds_read_b32 v228, v119 offset:1024
	ds_read_b32 v229, v119 offset:1536
	ds_read_b32 v230, v119 offset:2048
	ds_read_b32 v231, v119 offset:2560
	ds_read_b32 v232, v119 offset:3072
	ds_read_b32 v233, v119 offset:3584
	s_waitcnt lgkmcnt(0)
	v_bfe_u32 v120, v226, 16, 1
	v_bfe_u32 v121, v227, 16, 1
	v_bfe_u32 v122, v228, 16, 1
	v_bfe_u32 v123, v229, 16, 1
	v_bfe_u32 v124, v230, 16, 1
	v_bfe_u32 v125, v231, 16, 1
	v_bfe_u32 v126, v232, 16, 1
	v_bfe_u32 v127, v233, 16, 1
	v_add3_u32 v226, v226, v120, s63
	v_add3_u32 v227, v227, v121, s63
	v_add3_u32 v228, v228, v122, s63
	v_add3_u32 v229, v229, v123, s63
	v_add3_u32 v230, v230, v124, s63
	v_add3_u32 v231, v231, v125, s63
	v_add3_u32 v232, v232, v126, s63
	v_add3_u32 v233, v233, v127, s63
	v_perm_b32 v242, v227, v226, s64
	v_perm_b32 v243, v229, v228, s64
	v_perm_b32 v244, v231, v230, s64
	v_perm_b32 v245, v233, v232, s64
	s_nop 0
	global_store_dwordx4 v94, v[242:245], s[6:7]
	s_waitcnt vmcnt(16)
	v_mul_f32_e32 v144, v42, v144
	v_mul_f32_e32 v145, v42, v145
	v_mul_f32_e32 v146, v42, v146
	v_mul_f32_e32 v147, v42, v147
	ds_write_b128 v209, v[144:147]
	v_mul_f32_e32 v148, v43, v148
	v_mul_f32_e32 v149, v43, v149
	v_mul_f32_e32 v150, v43, v150
	v_mul_f32_e32 v151, v43, v151
	ds_write_b128 v209, v[148:151] offset:1024
	v_mul_f32_e32 v152, v44, v152
	v_mul_f32_e32 v153, v44, v153
	v_mul_f32_e32 v154, v44, v154
	v_mul_f32_e32 v155, v44, v155
	ds_write_b128 v209, v[152:155] offset:2048
	v_mul_f32_e32 v156, v45, v156
	v_mul_f32_e32 v157, v45, v157
	v_mul_f32_e32 v158, v45, v158
	v_mul_f32_e32 v159, v45, v159
	ds_write_b128 v209, v[156:159] offset:3072
	v_mul_f32_e32 v160, v46, v160
	v_mul_f32_e32 v161, v46, v161
	v_mul_f32_e32 v162, v46, v162
	v_mul_f32_e32 v163, v46, v163
	ds_write_b128 v209, v[160:163] offset:4096
	v_mul_f32_e32 v164, v47, v164
	v_mul_f32_e32 v165, v47, v165
	v_mul_f32_e32 v166, v47, v166
	v_mul_f32_e32 v167, v47, v167
	ds_write_b128 v209, v[164:167] offset:5120
	v_mul_f32_e32 v168, v48, v168
	v_mul_f32_e32 v169, v48, v169
	v_mul_f32_e32 v170, v48, v170
	v_mul_f32_e32 v171, v48, v171
	ds_write_b128 v209, v[168:171] offset:6144
	v_mul_f32_e32 v172, v49, v172
	v_mul_f32_e32 v173, v49, v173
	v_mul_f32_e32 v174, v49, v174
	v_mul_f32_e32 v175, v49, v175
	ds_write_b128 v209, v[172:175] offset:7168
	s_waitcnt lgkmcnt(0)
	s_barrier
; #define GAS __attribute__((address_space(1)))
; #define LAS __attribute__((address_space(3)))
; #define LDS_WAIT() asm volatile("s_waitcnt lgkmcnt(0)" ::: "memory")
; __device__ __forceinline__ unsigned pk2(float lo, float hi) { return f2bf(lo) | (f2bf(hi) << 16); }
; __device__ __forceinline__ int nat_dim(int p) { return (p >> 1) + 64 * (p & 1); }
; template <int MAP, bool KS, bool KPERM = false>
; __device__ __forceinline__ void p0_transpose_item(const float* W, int K, int Nsrc, int nblk, bf16* WT, const float* ksA, const float* ksB, int ksplit, LAS float* scr, int item, int lane) {
;     const int kb = item / nblk, nb = item % nblk, k0 = 64 * kb, n0 = 32 * nb;
;     const int nr = n0 + (lane & 31); const int sc = MAP == 1 ? src_col_in(nr) : (MAP == 2 ? nat_dim(nr) : nr);
;     float v[32];
; #pragma unroll
;     for (int i = 0; i < 32; ++i) { const int k = k0 + 2 * i + (lane >> 5); const int ksrc = KPERM ? ((k & ~127) + nat_dim(k & 127)) : k;
;         v[i] = sc >= 0 ? W[(size_t)ksrc * Nsrc + sc] : 0.f; }
; #pragma unroll
;     for (int i = 0; i < 32; ++i) { const int kk = 2 * i + (lane >> 5); const int k = k0 + kk;
;         if (KS) v[i] *= (k < ksplit ? ksA[k] : ksB[k - ksplit]);
;         scr[kk * 33 + (lane & 31)] = v[i]; }
;     LDS_WAIT(); asm volatile("" ::: "memory");
;     const int c = lane & 7;
; #pragma unroll
;     for (int j = 0; j < 4; ++j) { const int n = (lane >> 3) + 8 * j; const LAS float* s = scr + (8 * c) * 33 + n;
;         v4u o; o.x = pk2(s[0 * 33], s[1 * 33]); o.y = pk2(s[2 * 33], s[3 * 33]); o.z = pk2(s[4 * 33], s[5 * 33]); o.w = pk2(s[6 * 33], s[7 * 33]);
;         *(GAS v4u*)(WT + (size_t)(n0 + n) * K + k0 + 8 * c) = o; }
;     LDS_WAIT(); asm volatile("" ::: "memory");
; __global__ void __launch_bounds__(NWAVES * 64, 2) hybrid_fwd(Args args) {
;     ...
;             if (r < I_IN) { if (l >= PROJ_F8_FROM) p0_transpose_item_f8<true, 1>(args.in[2] + (size_t)l * DM * NSRC, DM, NSRC, NPROJ / 32, (unsigned char*)(ws + WS_WIN + l * SZ_WIN), WUP8_SCALE, args.in[1] + l * DM, args.in[1] + l * DM, DM, scr, r, lane);
;                 else p0_transpose_item<1, true>(args.in[2] + (size_t)l * DM * NSRC, DM, NSRC, NPROJ / 32, (bf16*)(ws + WS_WIN + l * SZ_WIN), args.in[1] + l * DM, args.in[1] + l * DM, DM, scr, r, lane); continue; } r -= I_IN;
	s_add_i32 s24, s23, 80
	s_lshl_b32 s20, s24, 7
	s_cmp_lt_u32 s24, 40
	s_cselect_b32 s21, 0, 0x830
	s_cmp_lt_u32 s24, 72
	s_cselect_b32 s21, s21, 0xfffff030
	s_add_i32 s20, s20, s21
	s_lshl_b32 s20, s20, 2
	s_add_u32 s8, s46, s20
	s_addc_u32 s9, s47, 0
	global_load_dwordx4 v[144:147], v76, s[8:9]
	s_add_u32 s8, s8, 0x16280
	s_addc_u32 s9, s9, 0
	global_load_dwordx4 v[148:151], v76, s[8:9]
	s_add_u32 s8, s8, 0x16280
	s_addc_u32 s9, s9, 0
	global_load_dwordx4 v[152:155], v76, s[8:9]
	s_add_u32 s8, s8, 0x16280
	s_addc_u32 s9, s9, 0
	global_load_dwordx4 v[156:159], v76, s[8:9]
	s_add_u32 s8, s8, 0x16280
	s_addc_u32 s9, s9, 0
	global_load_dwordx4 v[160:163], v76, s[8:9]
	s_add_u32 s8, s8, 0x16280
	s_addc_u32 s9, s9, 0
	global_load_dwordx4 v[164:167], v76, s[8:9]
	s_add_u32 s8, s8, 0x16280
	s_addc_u32 s9, s9, 0
	global_load_dwordx4 v[168:171], v76, s[8:9]
	s_add_u32 s8, s8, 0x16280
	s_addc_u32 s9, s9, 0
	global_load_dwordx4 v[172:175], v76, s[8:9]
	s_add_i32 s24, s23, 64
	s_mul_i32 s20, s24, 0x100000
	s_add_u32 s6, s48, s20
	s_addc_u32 s7, s49, 0
	s_cmp_lt_u32 s24, 16
	s_cselect_b32 s20, 1, 0
	s_sub_i32 s21, s24, 16
	s_bitcmp0_b32 s21, 2
	s_cselect_b32 s21, 1, 0
	s_cmp_lt_u32 s24, 40
	s_cselect_b32 s21, s21, 0
	s_or_b32 s20, s20, s21
	s_cmp_lg_u32 s20, 0
	s_cselect_b64 s[20:21], -1, 0
	v_cndmask_b32_e64 v91, v83, v87, s[20:21]
	v_cndmask_b32_e64 v92, v84, v88, s[20:21]
	v_cndmask_b32_e64 v93, v85, v89, s[20:21]
	v_cndmask_b32_e64 v94, v86, v90, s[20:21]
	ds_read_b32 v226, v112
	ds_read_b32 v227, v112 offset:512
	ds_read_b32 v228, v112 offset:1024
	ds_read_b32 v229, v112 offset:1536
	ds_read_b32 v230, v112 offset:2048
	ds_read_b32 v231, v112 offset:2560
	ds_read_b32 v232, v112 offset:3072
	ds_read_b32 v233, v112 offset:3584
	s_waitcnt lgkmcnt(0)
	v_bfe_u32 v120, v226, 16, 1
	v_bfe_u32 v121, v227, 16, 1
	v_bfe_u32 v122, v228, 16, 1
	v_bfe_u32 v123, v229, 16, 1
	v_bfe_u32 v124, v230, 16, 1
	v_bfe_u32 v125, v231, 16, 1
	v_bfe_u32 v126, v232, 16, 1
	v_bfe_u32 v127, v233, 16, 1
	v_add3_u32 v226, v226, v120, s63
	v_add3_u32 v227, v227, v121, s63
	v_add3_u32 v228, v228, v122, s63
	v_add3_u32 v229, v229, v123, s63
	v_add3_u32 v230, v230, v124, s63
	v_add3_u32 v231, v231, v125, s63
	v_add3_u32 v232, v232, v126, s63
	v_add3_u32 v233, v233, v127, s63
	v_perm_b32 v242, v227, v226, s64
	v_perm_b32 v243, v229, v228, s64
	v_perm_b32 v244, v231, v230, s64
	v_perm_b32 v245, v233, v232, s64
	s_nop 0
	global_store_dwordx4 v91, v[242:245], s[6:7]
	ds_read_b32 v226, v114
	ds_read_b32 v227, v114 offset:512
	ds_read_b32 v228, v114 offset:1024
	ds_read_b32 v229, v114 offset:1536
	ds_read_b32 v230, v114 offset:2048
	ds_read_b32 v231, v114 offset:2560
	ds_read_b32 v232, v114 offset:3072
	ds_read_b32 v233, v114 offset:3584
	s_waitcnt lgkmcnt(0)
	v_bfe_u32 v120, v226, 16, 1
	v_bfe_u32 v121, v227, 16, 1
	v_bfe_u32 v122, v228, 16, 1
	v_bfe_u32 v123, v229, 16, 1
	v_bfe_u32 v124, v230, 16, 1
	v_bfe_u32 v125, v231, 16, 1
	v_bfe_u32 v126, v232, 16, 1
	v_bfe_u32 v127, v233, 16, 1
	v_add3_u32 v226, v226, v120, s63
	v_add3_u32 v227, v227, v121, s63
	v_add3_u32 v228, v228, v122, s63
	v_add3_u32 v229, v229, v123, s63
	v_add3_u32 v230, v230, v124, s63
	v_add3_u32 v231, v231, v125, s63
	v_add3_u32 v232, v232, v126, s63
	v_add3_u32 v233, v233, v127, s63
	v_perm_b32 v242, v227, v226, s64
	v_perm_b32 v243, v229, v228, s64
	v_perm_b32 v244, v231, v230, s64
	v_perm_b32 v245, v233, v232, s64
	s_nop 0
	global_store_dwordx4 v92, v[242:245], s[6:7]
	ds_read_b32 v226, v116
	ds_read_b32 v227, v116 offset:512
	ds_read_b32 v228, v116 offset:1024
	ds_read_b32 v229, v116 offset:1536
	ds_read_b32 v230, v116 offset:2048
	ds_read_b32 v231, v116 offset:2560
	ds_read_b32 v232, v116 offset:3072
	ds_read_b32 v233, v116 offset:3584
	s_waitcnt lgkmcnt(0)
	v_bfe_u32 v120, v226, 16, 1
	v_bfe_u32 v121, v227, 16, 1
	v_bfe_u32 v122, v228, 16, 1
	v_bfe_u32 v123, v229, 16, 1
	v_bfe_u32 v124, v230, 16, 1
	v_bfe_u32 v125, v231, 16, 1
	v_bfe_u32 v126, v232, 16, 1
	v_bfe_u32 v127, v233, 16, 1
	v_add3_u32 v226, v226, v120, s63
	v_add3_u32 v227, v227, v121, s63
	v_add3_u32 v228, v228, v122, s63
	v_add3_u32 v229, v229, v123, s63
	v_add3_u32 v230, v230, v124, s63
	v_add3_u32 v231, v231, v125, s63
	v_add3_u32 v232, v232, v126, s63
	v_add3_u32 v233, v233, v127, s63
	v_perm_b32 v242, v227, v226, s64
	v_perm_b32 v243, v229, v228, s64
	v_perm_b32 v244, v231, v230, s64
	v_perm_b32 v245, v233, v232, s64
	s_nop 0
	global_store_dwordx4 v93, v[242:245], s[6:7]
	ds_read_b32 v226, v118
	ds_read_b32 v227, v118 offset:512
	ds_read_b32 v228, v118 offset:1024
	ds_read_b32 v229, v118 offset:1536
	ds_read_b32 v230, v118 offset:2048
	ds_read_b32 v231, v118 offset:2560
	ds_read_b32 v232, v118 offset:3072
	ds_read_b32 v233, v118 offset:3584
	s_waitcnt lgkmcnt(0)
	v_bfe_u32 v120, v226, 16, 1
	v_bfe_u32 v121, v227, 16, 1
	v_bfe_u32 v122, v228, 16, 1
	v_bfe_u32 v123, v229, 16, 1
	v_bfe_u32 v124, v230, 16, 1
	v_bfe_u32 v125, v231, 16, 1
	v_bfe_u32 v126, v232, 16, 1
	v_bfe_u32 v127, v233, 16, 1
	v_add3_u32 v226, v226, v120, s63
	v_add3_u32 v227, v227, v121, s63
	v_add3_u32 v228, v228, v122, s63
	v_add3_u32 v229, v229, v123, s63
	v_add3_u32 v230, v230, v124, s63
	v_add3_u32 v231, v231, v125, s63
	v_add3_u32 v232, v232, v126, s63
	v_add3_u32 v233, v233, v127, s63
	v_perm_b32 v242, v227, v226, s64
	v_perm_b32 v243, v229, v228, s64
	v_perm_b32 v244, v231, v230, s64
	v_perm_b32 v245, v233, v232, s64
	s_nop 0
	global_store_dwordx4 v94, v[242:245], s[6:7]
	s_waitcnt vmcnt(16)
	v_mul_f32_e32 v176, v42, v176
	v_mul_f32_e32 v177, v42, v177
	v_mul_f32_e32 v178, v42, v178
	v_mul_f32_e32 v179, v42, v179
	ds_write_b128 v210, v[176:179]
	v_mul_f32_e32 v180, v43, v180
	v_mul_f32_e32 v181, v43, v181
	v_mul_f32_e32 v182, v43, v182
	v_mul_f32_e32 v183, v43, v183
	ds_write_b128 v210, v[180:183] offset:1024
	v_mul_f32_e32 v184, v44, v184
	v_mul_f32_e32 v185, v44, v185
	v_mul_f32_e32 v186, v44, v186
	v_mul_f32_e32 v187, v44, v187
	ds_write_b128 v210, v[184:187] offset:2048
	v_mul_f32_e32 v188, v45, v188
	v_mul_f32_e32 v189, v45, v189
	v_mul_f32_e32 v190, v45, v190
	v_mul_f32_e32 v191, v45, v191
	ds_write_b128 v210, v[188:191] offset:3072
	v_mul_f32_e32 v192, v46, v192
	v_mul_f32_e32 v193, v46, v193
	v_mul_f32_e32 v194, v46, v194
	v_mul_f32_e32 v195, v46, v195
	ds_write_b128 v210, v[192:195] offset:4096
	v_mul_f32_e32 v196, v47, v196
	v_mul_f32_e32 v197, v47, v197
	v_mul_f32_e32 v198, v47, v198
	v_mul_f32_e32 v199, v47, v199
	ds_write_b128 v210, v[196:199] offset:5120
	v_mul_f32_e32 v200, v48, v200
	v_mul_f32_e32 v201, v48, v201
	v_mul_f32_e32 v202, v48, v202
	v_mul_f32_e32 v203, v48, v203
	ds_write_b128 v210, v[200:203] offset:6144
	v_mul_f32_e32 v204, v49, v204
	v_mul_f32_e32 v205, v49, v205
	v_mul_f32_e32 v206, v49, v206
	v_mul_f32_e32 v207, v49, v207
	ds_write_b128 v210, v[204:207] offset:7168
	s_waitcnt lgkmcnt(0)
	s_barrier
; #define GAS __attribute__((address_space(1)))
; #define LAS __attribute__((address_space(3)))
; #define LDS_WAIT() asm volatile("s_waitcnt lgkmcnt(0)" ::: "memory")
; __device__ __forceinline__ unsigned pk2(float lo, float hi) { return f2bf(lo) | (f2bf(hi) << 16); }
; __device__ __forceinline__ int nat_dim(int p) { return (p >> 1) + 64 * (p & 1); }
; template <int MAP, bool KS, bool KPERM = false>
; __device__ __forceinline__ void p0_transpose_item(const float* W, int K, int Nsrc, int nblk, bf16* WT, const float* ksA, const float* ksB, int ksplit, LAS float* scr, int item, int lane) {
;     const int kb = item / nblk, nb = item % nblk, k0 = 64 * kb, n0 = 32 * nb;
;     const int nr = n0 + (lane & 31); const int sc = MAP == 1 ? src_col_in(nr) : (MAP == 2 ? nat_dim(nr) : nr);
;     float v[32];
; #pragma unroll
;     for (int i = 0; i < 32; ++i) { const int k = k0 + 2 * i + (lane >> 5); const int ksrc = KPERM ? ((k & ~127) + nat_dim(k & 127)) : k;
;         v[i] = sc >= 0 ? W[(size_t)ksrc * Nsrc + sc] : 0.f; }
; #pragma unroll
;     for (int i = 0; i < 32; ++i) { const int kk = 2 * i + (lane >> 5); const int k = k0 + kk;
;         if (KS) v[i] *= (k < ksplit ? ksA[k] : ksB[k - ksplit]);
;         scr[kk * 33 + (lane & 31)] = v[i]; }
;     LDS_WAIT(); asm volatile("" ::: "memory");
;     const int c = lane & 7;
; #pragma unroll
;     for (int j = 0; j < 4; ++j) { const int n = (lane >> 3) + 8 * j; const LAS float* s = scr + (8 * c) * 33 + n;
;         v4u o; o.x = pk2(s[0 * 33], s[1 * 33]); o.y = pk2(s[2 * 33], s[3 * 33]); o.z = pk2(s[4 * 33], s[5 * 33]); o.w = pk2(s[6 * 33], s[7 * 33]);
;         *(GAS v4u*)(WT + (size_t)(n0 + n) * K + k0 + 8 * c) = o; }
;     LDS_WAIT(); asm volatile("" ::: "memory");
; __global__ void __launch_bounds__(NWAVES * 64, 2) hybrid_fwd(Args args) {
;     ...
;             if (r < I_IN) { if (l >= PROJ_F8_FROM) p0_transpose_item_f8<true, 1>(args.in[2] + (size_t)l * DM * NSRC, DM, NSRC, NPROJ / 32, (unsigned char*)(ws + WS_WIN + l * SZ_WIN), WUP8_SCALE, args.in[1] + l * DM, args.in[1] + l * DM, DM, scr, r, lane);
;                 else p0_transpose_item<1, true>(args.in[2] + (size_t)l * DM * NSRC, DM, NSRC, NPROJ / 32, (bf16*)(ws + WS_WIN + l * SZ_WIN), args.in[1] + l * DM, args.in[1] + l * DM, DM, scr, r, lane); continue; } r -= I_IN;
	s_add_i32 s24, s23, 0
	s_lshl_b32 s20, s24, 7
	s_cmp_lt_u32 s24, 40
	s_cselect_b32 s21, 0, 0x830
	s_cmp_lt_u32 s24, 72
	s_cselect_b32 s21, s21, 0xfffff030
	s_add_i32 s20, s20, s21
	s_lshl_b32 s20, s20, 2
	s_add_u32 s8, s50, s20
	s_addc_u32 s9, s51, 0
	global_load_dwordx4 v[176:179], v76, s[8:9]
	s_add_u32 s8, s8, 0x16280
	s_addc_u32 s9, s9, 0
	global_load_dwordx4 v[180:183], v76, s[8:9]
	s_add_u32 s8, s8, 0x16280
	s_addc_u32 s9, s9, 0
	global_load_dwordx4 v[184:187], v76, s[8:9]
	s_add_u32 s8, s8, 0x16280
	s_addc_u32 s9, s9, 0
	global_load_dwordx4 v[188:191], v76, s[8:9]
	s_add_u32 s8, s8, 0x16280
	s_addc_u32 s9, s9, 0
	global_load_dwordx4 v[192:195], v76, s[8:9]
	s_add_u32 s8, s8, 0x16280
	s_addc_u32 s9, s9, 0
	global_load_dwordx4 v[196:199], v76, s[8:9]
	s_add_u32 s8, s8, 0x16280
	s_addc_u32 s9, s9, 0
	global_load_dwordx4 v[200:203], v76, s[8:9]
	s_add_u32 s8, s8, 0x16280
	s_addc_u32 s9, s9, 0
	global_load_dwordx4 v[204:207], v76, s[8:9]
	s_add_i32 s24, s23, 72
	s_mul_i32 s20, s24, 0x100000
	s_add_u32 s6, s48, s20
	s_addc_u32 s7, s49, 0
	s_cmp_lt_u32 s24, 16
	s_cselect_b32 s20, 1, 0
	s_sub_i32 s21, s24, 16
	s_bitcmp0_b32 s21, 2
	s_cselect_b32 s21, 1, 0
	s_cmp_lt_u32 s24, 40
	s_cselect_b32 s21, s21, 0
	s_or_b32 s20, s20, s21
	s_cmp_lg_u32 s20, 0
	s_cselect_b64 s[20:21], -1, 0
	v_cndmask_b32_e64 v91, v83, v87, s[20:21]
	v_cndmask_b32_e64 v92, v84, v88, s[20:21]
	v_cndmask_b32_e64 v93, v85, v89, s[20:21]
	v_cndmask_b32_e64 v94, v86, v90, s[20:21]
	ds_read_b32 v226, v113
	ds_read_b32 v227, v113 offset:512
	ds_read_b32 v228, v113 offset:1024
	ds_read_b32 v229, v113 offset:1536
	ds_read_b32 v230, v113 offset:2048
	ds_read_b32 v231, v113 offset:2560
	ds_read_b32 v232, v113 offset:3072
	ds_read_b32 v233, v113 offset:3584
	s_waitcnt lgkmcnt(0)
	v_bfe_u32 v120, v226, 16, 1
	v_bfe_u32 v121, v227, 16, 1
	v_bfe_u32 v122, v228, 16, 1
	v_bfe_u32 v123, v229, 16, 1
	v_bfe_u32 v124, v230, 16, 1
	v_bfe_u32 v125, v231, 16, 1
	v_bfe_u32 v126, v232, 16, 1
	v_bfe_u32 v127, v233, 16, 1
	v_add3_u32 v226, v226, v120, s63
	v_add3_u32 v227, v227, v121, s63
	v_add3_u32 v228, v228, v122, s63
	v_add3_u32 v229, v229, v123, s63
	v_add3_u32 v230, v230, v124, s63
	v_add3_u32 v231, v231, v125, s63
	v_add3_u32 v232, v232, v126, s63
	v_add3_u32 v233, v233, v127, s63
	v_perm_b32 v242, v227, v226, s64
	v_perm_b32 v243, v229, v228, s64
	v_perm_b32 v244, v231, v230, s64
	v_perm_b32 v245, v233, v232, s64
	s_nop 0
	global_store_dwordx4 v91, v[242:245], s[6:7]
	ds_read_b32 v226, v115
	ds_read_b32 v227, v115 offset:512
	ds_read_b32 v228, v115 offset:1024
	ds_read_b32 v229, v115 offset:1536
	ds_read_b32 v230, v115 offset:2048
	ds_read_b32 v231, v115 offset:2560
	ds_read_b32 v232, v115 offset:3072
	ds_read_b32 v233, v115 offset:3584
	s_waitcnt lgkmcnt(0)
	v_bfe_u32 v120, v226, 16, 1
	v_bfe_u32 v121, v227, 16, 1
	v_bfe_u32 v122, v228, 16, 1
	v_bfe_u32 v123, v229, 16, 1
	v_bfe_u32 v124, v230, 16, 1
	v_bfe_u32 v125, v231, 16, 1
	v_bfe_u32 v126, v232, 16, 1
	v_bfe_u32 v127, v233, 16, 1
	v_add3_u32 v226, v226, v120, s63
	v_add3_u32 v227, v227, v121, s63
	v_add3_u32 v228, v228, v122, s63
	v_add3_u32 v229, v229, v123, s63
	v_add3_u32 v230, v230, v124, s63
	v_add3_u32 v231, v231, v125, s63
	v_add3_u32 v232, v232, v126, s63
	v_add3_u32 v233, v233, v127, s63
	v_perm_b32 v242, v227, v226, s64
	v_perm_b32 v243, v229, v228, s64
	v_perm_b32 v244, v231, v230, s64
	v_perm_b32 v245, v233, v232, s64
	s_nop 0
	global_store_dwordx4 v92, v[242:245], s[6:7]
	ds_read_b32 v226, v117
	ds_read_b32 v227, v117 offset:512
	ds_read_b32 v228, v117 offset:1024
	ds_read_b32 v229, v117 offset:1536
	ds_read_b32 v230, v117 offset:2048
	ds_read_b32 v231, v117 offset:2560
	ds_read_b32 v232, v117 offset:3072
	ds_read_b32 v233, v117 offset:3584
	s_waitcnt lgkmcnt(0)
	v_bfe_u32 v120, v226, 16, 1
	v_bfe_u32 v121, v227, 16, 1
	v_bfe_u32 v122, v228, 16, 1
	v_bfe_u32 v123, v229, 16, 1
	v_bfe_u32 v124, v230, 16, 1
	v_bfe_u32 v125, v231, 16, 1
	v_bfe_u32 v126, v232, 16, 1
	v_bfe_u32 v127, v233, 16, 1
	v_add3_u32 v226, v226, v120, s63
	v_add3_u32 v227, v227, v121, s63
	v_add3_u32 v228, v228, v122, s63
	v_add3_u32 v229, v229, v123, s63
	v_add3_u32 v230, v230, v124, s63
	v_add3_u32 v231, v231, v125, s63
	v_add3_u32 v232, v232, v126, s63
	v_add3_u32 v233, v233, v127, s63
	v_perm_b32 v242, v227, v226, s64
	v_perm_b32 v243, v229, v228, s64
	v_perm_b32 v244, v231, v230, s64
	v_perm_b32 v245, v233, v232, s64
	s_nop 0
	global_store_dwordx4 v93, v[242:245], s[6:7]
	ds_read_b32 v226, v119
	ds_read_b32 v227, v119 offset:512
	ds_read_b32 v228, v119 offset:1024
	ds_read_b32 v229, v119 offset:1536
	ds_read_b32 v230, v119 offset:2048
	ds_read_b32 v231, v119 offset:2560
	ds_read_b32 v232, v119 offset:3072
	ds_read_b32 v233, v119 offset:3584
	s_waitcnt lgkmcnt(0)
	v_bfe_u32 v120, v226, 16, 1
	v_bfe_u32 v121, v227, 16, 1
	v_bfe_u32 v122, v228, 16, 1
	v_bfe_u32 v123, v229, 16, 1
	v_bfe_u32 v124, v230, 16, 1
	v_bfe_u32 v125, v231, 16, 1
	v_bfe_u32 v126, v232, 16, 1
	v_bfe_u32 v127, v233, 16, 1
	v_add3_u32 v226, v226, v120, s63
	v_add3_u32 v227, v227, v121, s63
	v_add3_u32 v228, v228, v122, s63
	v_add3_u32 v229, v229, v123, s63
	v_add3_u32 v230, v230, v124, s63
	v_add3_u32 v231, v231, v125, s63
	v_add3_u32 v232, v232, v126, s63
	v_add3_u32 v233, v233, v127, s63
	v_perm_b32 v242, v227, v226, s64
	v_perm_b32 v243, v229, v228, s64
	v_perm_b32 v244, v231, v230, s64
	v_perm_b32 v245, v233, v232, s64
	s_nop 0
	global_store_dwordx4 v94, v[242:245], s[6:7]
	s_waitcnt vmcnt(16)
	v_mul_f32_e32 v144, v42, v144
	v_mul_f32_e32 v145, v42, v145
	v_mul_f32_e32 v146, v42, v146
	v_mul_f32_e32 v147, v42, v147
	ds_write_b128 v209, v[144:147]
	v_mul_f32_e32 v148, v43, v148
	v_mul_f32_e32 v149, v43, v149
	v_mul_f32_e32 v150, v43, v150
	v_mul_f32_e32 v151, v43, v151
	ds_write_b128 v209, v[148:151] offset:1024
	v_mul_f32_e32 v152, v44, v152
	v_mul_f32_e32 v153, v44, v153
	v_mul_f32_e32 v154, v44, v154
	v_mul_f32_e32 v155, v44, v155
	ds_write_b128 v209, v[152:155] offset:2048
	v_mul_f32_e32 v156, v45, v156
	v_mul_f32_e32 v157, v45, v157
	v_mul_f32_e32 v158, v45, v158
	v_mul_f32_e32 v159, v45, v159
	ds_write_b128 v209, v[156:159] offset:3072
	v_mul_f32_e32 v160, v46, v160
	v_mul_f32_e32 v161, v46, v161
	v_mul_f32_e32 v162, v46, v162
	v_mul_f32_e32 v163, v46, v163
	ds_write_b128 v209, v[160:163] offset:4096
	v_mul_f32_e32 v164, v47, v164
	v_mul_f32_e32 v165, v47, v165
	v_mul_f32_e32 v166, v47, v166
	v_mul_f32_e32 v167, v47, v167
	ds_write_b128 v209, v[164:167] offset:5120
	v_mul_f32_e32 v168, v48, v168
	v_mul_f32_e32 v169, v48, v169
	v_mul_f32_e32 v170, v48, v170
	v_mul_f32_e32 v171, v48, v171
	ds_write_b128 v209, v[168:171] offset:6144
	v_mul_f32_e32 v172, v49, v172
	v_mul_f32_e32 v173, v49, v173
	v_mul_f32_e32 v174, v49, v174
	v_mul_f32_e32 v175, v49, v175
	ds_write_b128 v209, v[172:175] offset:7168
	s_waitcnt lgkmcnt(0)
	s_barrier
; #define GAS __attribute__((address_space(1)))
; #define LAS __attribute__((address_space(3)))
; #define LDS_WAIT() asm volatile("s_waitcnt lgkmcnt(0)" ::: "memory")
; __device__ __forceinline__ unsigned pk2(float lo, float hi) { return f2bf(lo) | (f2bf(hi) << 16); }
; __device__ __forceinline__ int nat_dim(int p) { return (p >> 1) + 64 * (p & 1); }
; template <int MAP, bool KS, bool KPERM = false>
; __device__ __forceinline__ void p0_transpose_item(const float* W, int K, int Nsrc, int nblk, bf16* WT, const float* ksA, const float* ksB, int ksplit, LAS float* scr, int item, int lane) {
;     const int kb = item / nblk, nb = item % nblk, k0 = 64 * kb, n0 = 32 * nb;
;     const int nr = n0 + (lane & 31); const int sc = MAP == 1 ? src_col_in(nr) : (MAP == 2 ? nat_dim(nr) : nr);
;     float v[32];
; #pragma unroll
;     for (int i = 0; i < 32; ++i) { const int k = k0 + 2 * i + (lane >> 5); const int ksrc = KPERM ? ((k & ~127) + nat_dim(k & 127)) : k;
;         v[i] = sc >= 0 ? W[(size_t)ksrc * Nsrc + sc] : 0.f; }
; #pragma unroll
;     for (int i = 0; i < 32; ++i) { const int kk = 2 * i + (lane >> 5); const int k = k0 + kk;
;         if (KS) v[i] *= (k < ksplit ? ksA[k] : ksB[k - ksplit]);
;         scr[kk * 33 + (lane & 31)] = v[i]; }
;     LDS_WAIT(); asm volatile("" ::: "memory");
;     const int c = lane & 7;
; #pragma unroll
;     for (int j = 0; j < 4; ++j) { const int n = (lane >> 3) + 8 * j; const LAS float* s = scr + (8 * c) * 33 + n;
;         v4u o; o.x = pk2(s[0 * 33], s[1 * 33]); o.y = pk2(s[2 * 33], s[3 * 33]); o.z = pk2(s[4 * 33], s[5 * 33]); o.w = pk2(s[6 * 33], s[7 * 33]);
;         *(GAS v4u*)(WT + (size_t)(n0 + n) * K + k0 + 8 * c) = o; }
;     LDS_WAIT(); asm volatile("" ::: "memory");
; __global__ void __launch_bounds__(NWAVES * 64, 2) hybrid_fwd(Args args) {
;     ...
;             if (r < I_IN) { if (l >= PROJ_F8_FROM) p0_transpose_item_f8<true, 1>(args.in[2] + (size_t)l * DM * NSRC, DM, NSRC, NPROJ / 32, (unsigned char*)(ws + WS_WIN + l * SZ_WIN), WUP8_SCALE, args.in[1] + l * DM, args.in[1] + l * DM, DM, scr, r, lane);
;                 else p0_transpose_item<1, true>(args.in[2] + (size_t)l * DM * NSRC, DM, NSRC, NPROJ / 32, (bf16*)(ws + WS_WIN + l * SZ_WIN), args.in[1] + l * DM, args.in[1] + l * DM, DM, scr, r, lane); continue; } r -= I_IN;
	s_add_i32 s24, s23, 8
	s_lshl_b32 s20, s24, 7
	s_cmp_lt_u32 s24, 40
	s_cselect_b32 s21, 0, 0x830
	s_cmp_lt_u32 s24, 72
	s_cselect_b32 s21, s21, 0xfffff030
	s_add_i32 s20, s20, s21
	s_lshl_b32 s20, s20, 2
	s_add_u32 s8, s50, s20
	s_addc_u32 s9, s51, 0
	global_load_dwordx4 v[144:147], v76, s[8:9]
	s_add_u32 s8, s8, 0x16280
	s_addc_u32 s9, s9, 0
	global_load_dwordx4 v[148:151], v76, s[8:9]
	s_add_u32 s8, s8, 0x16280
	s_addc_u32 s9, s9, 0
	global_load_dwordx4 v[152:155], v76, s[8:9]
	s_add_u32 s8, s8, 0x16280
	s_addc_u32 s9, s9, 0
	global_load_dwordx4 v[156:159], v76, s[8:9]
	s_add_u32 s8, s8, 0x16280
	s_addc_u32 s9, s9, 0
	global_load_dwordx4 v[160:163], v76, s[8:9]
	s_add_u32 s8, s8, 0x16280
	s_addc_u32 s9, s9, 0
	global_load_dwordx4 v[164:167], v76, s[8:9]
	s_add_u32 s8, s8, 0x16280
	s_addc_u32 s9, s9, 0
	global_load_dwordx4 v[168:171], v76, s[8:9]
	s_add_u32 s8, s8, 0x16280
	s_addc_u32 s9, s9, 0
	global_load_dwordx4 v[172:175], v76, s[8:9]
	s_add_i32 s24, s23, 80
	s_mul_i32 s20, s24, 0x100000
	s_add_u32 s6, s48, s20
	s_addc_u32 s7, s49, 0
	s_cmp_lt_u32 s24, 16
	s_cselect_b32 s20, 1, 0
	s_sub_i32 s21, s24, 16
	s_bitcmp0_b32 s21, 2
	s_cselect_b32 s21, 1, 0
	s_cmp_lt_u32 s24, 40
	s_cselect_b32 s21, s21, 0
	s_or_b32 s20, s20, s21
	s_cmp_lg_u32 s20, 0
	s_cselect_b64 s[20:21], -1, 0
	v_cndmask_b32_e64 v91, v83, v87, s[20:21]
	v_cndmask_b32_e64 v92, v84, v88, s[20:21]
	v_cndmask_b32_e64 v93, v85, v89, s[20:21]
	v_cndmask_b32_e64 v94, v86, v90, s[20:21]
	ds_read_b32 v226, v112
	ds_read_b32 v227, v112 offset:512
	ds_read_b32 v228, v112 offset:1024
	ds_read_b32 v229, v112 offset:1536
	ds_read_b32 v230, v112 offset:2048
	ds_read_b32 v231, v112 offset:2560
	ds_read_b32 v232, v112 offset:3072
	ds_read_b32 v233, v112 offset:3584
	s_waitcnt lgkmcnt(0)
	v_bfe_u32 v120, v226, 16, 1
	v_bfe_u32 v121, v227, 16, 1
	v_bfe_u32 v122, v228, 16, 1
	v_bfe_u32 v123, v229, 16, 1
	v_bfe_u32 v124, v230, 16, 1
	v_bfe_u32 v125, v231, 16, 1
	v_bfe_u32 v126, v232, 16, 1
	v_bfe_u32 v127, v233, 16, 1
	v_add3_u32 v226, v226, v120, s63
	v_add3_u32 v227, v227, v121, s63
	v_add3_u32 v228, v228, v122, s63
	v_add3_u32 v229, v229, v123, s63
	v_add3_u32 v230, v230, v124, s63
	v_add3_u32 v231, v231, v125, s63
	v_add3_u32 v232, v232, v126, s63
	v_add3_u32 v233, v233, v127, s63
	v_perm_b32 v242, v227, v226, s64
	v_perm_b32 v243, v229, v228, s64
	v_perm_b32 v244, v231, v230, s64
	v_perm_b32 v245, v233, v232, s64
	s_nop 0
	global_store_dwordx4 v91, v[242:245], s[6:7]
	ds_read_b32 v226, v114
	ds_read_b32 v227, v114 offset:512
	ds_read_b32 v228, v114 offset:1024
	ds_read_b32 v229, v114 offset:1536
	ds_read_b32 v230, v114 offset:2048
	ds_read_b32 v231, v114 offset:2560
	ds_read_b32 v232, v114 offset:3072
	ds_read_b32 v233, v114 offset:3584
	s_waitcnt lgkmcnt(0)
	v_bfe_u32 v120, v226, 16, 1
	v_bfe_u32 v121, v227, 16, 1
	v_bfe_u32 v122, v228, 16, 1
	v_bfe_u32 v123, v229, 16, 1
	v_bfe_u32 v124, v230, 16, 1
	v_bfe_u32 v125, v231, 16, 1
	v_bfe_u32 v126, v232, 16, 1
	v_bfe_u32 v127, v233, 16, 1
	v_add3_u32 v226, v226, v120, s63
	v_add3_u32 v227, v227, v121, s63
	v_add3_u32 v228, v228, v122, s63
	v_add3_u32 v229, v229, v123, s63
	v_add3_u32 v230, v230, v124, s63
	v_add3_u32 v231, v231, v125, s63
	v_add3_u32 v232, v232, v126, s63
	v_add3_u32 v233, v233, v127, s63
	v_perm_b32 v242, v227, v226, s64
	v_perm_b32 v243, v229, v228, s64
	v_perm_b32 v244, v231, v230, s64
	v_perm_b32 v245, v233, v232, s64
	s_nop 0
	global_store_dwordx4 v92, v[242:245], s[6:7]
	ds_read_b32 v226, v116
	ds_read_b32 v227, v116 offset:512
	ds_read_b32 v228, v116 offset:1024
	ds_read_b32 v229, v116 offset:1536
	ds_read_b32 v230, v116 offset:2048
	ds_read_b32 v231, v116 offset:2560
	ds_read_b32 v232, v116 offset:3072
	ds_read_b32 v233, v116 offset:3584
	s_waitcnt lgkmcnt(0)
	v_bfe_u32 v120, v226, 16, 1
	v_bfe_u32 v121, v227, 16, 1
	v_bfe_u32 v122, v228, 16, 1
	v_bfe_u32 v123, v229, 16, 1
	v_bfe_u32 v124, v230, 16, 1
	v_bfe_u32 v125, v231, 16, 1
	v_bfe_u32 v126, v232, 16, 1
	v_bfe_u32 v127, v233, 16, 1
	v_add3_u32 v226, v226, v120, s63
	v_add3_u32 v227, v227, v121, s63
	v_add3_u32 v228, v228, v122, s63
	v_add3_u32 v229, v229, v123, s63
	v_add3_u32 v230, v230, v124, s63
	v_add3_u32 v231, v231, v125, s63
	v_add3_u32 v232, v232, v126, s63
	v_add3_u32 v233, v233, v127, s63
	v_perm_b32 v242, v227, v226, s64
	v_perm_b32 v243, v229, v228, s64
	v_perm_b32 v244, v231, v230, s64
	v_perm_b32 v245, v233, v232, s64
	s_nop 0
	global_store_dwordx4 v93, v[242:245], s[6:7]
	ds_read_b32 v226, v118
	ds_read_b32 v227, v118 offset:512
	ds_read_b32 v228, v118 offset:1024
	ds_read_b32 v229, v118 offset:1536
	ds_read_b32 v230, v118 offset:2048
	ds_read_b32 v231, v118 offset:2560
	ds_read_b32 v232, v118 offset:3072
	ds_read_b32 v233, v118 offset:3584
	s_waitcnt lgkmcnt(0)
	v_bfe_u32 v120, v226, 16, 1
	v_bfe_u32 v121, v227, 16, 1
	v_bfe_u32 v122, v228, 16, 1
	v_bfe_u32 v123, v229, 16, 1
	v_bfe_u32 v124, v230, 16, 1
	v_bfe_u32 v125, v231, 16, 1
	v_bfe_u32 v126, v232, 16, 1
	v_bfe_u32 v127, v233, 16, 1
	v_add3_u32 v226, v226, v120, s63
	v_add3_u32 v227, v227, v121, s63
	v_add3_u32 v228, v228, v122, s63
	v_add3_u32 v229, v229, v123, s63
	v_add3_u32 v230, v230, v124, s63
	v_add3_u32 v231, v231, v125, s63
	v_add3_u32 v232, v232, v126, s63
	v_add3_u32 v233, v233, v127, s63
	v_perm_b32 v242, v227, v226, s64
	v_perm_b32 v243, v229, v228, s64
	v_perm_b32 v244, v231, v230, s64
	v_perm_b32 v245, v233, v232, s64
	s_nop 0
	global_store_dwordx4 v94, v[242:245], s[6:7]
	s_waitcnt vmcnt(16)
	v_mul_f32_e32 v176, v50, v176
	v_mul_f32_e32 v177, v50, v177
	v_mul_f32_e32 v178, v50, v178
	v_mul_f32_e32 v179, v50, v179
	ds_write_b128 v210, v[176:179]
	v_mul_f32_e32 v180, v51, v180
	v_mul_f32_e32 v181, v51, v181
	v_mul_f32_e32 v182, v51, v182
	v_mul_f32_e32 v183, v51, v183
	ds_write_b128 v210, v[180:183] offset:1024
	v_mul_f32_e32 v184, v52, v184
	v_mul_f32_e32 v185, v52, v185
	v_mul_f32_e32 v186, v52, v186
	v_mul_f32_e32 v187, v52, v187
	ds_write_b128 v210, v[184:187] offset:2048
	v_mul_f32_e32 v188, v53, v188
	v_mul_f32_e32 v189, v53, v189
	v_mul_f32_e32 v190, v53, v190
	v_mul_f32_e32 v191, v53, v191
	ds_write_b128 v210, v[188:191] offset:3072
	v_mul_f32_e32 v192, v54, v192
	v_mul_f32_e32 v193, v54, v193
	v_mul_f32_e32 v194, v54, v194
	v_mul_f32_e32 v195, v54, v195
	ds_write_b128 v210, v[192:195] offset:4096
	v_mul_f32_e32 v196, v55, v196
	v_mul_f32_e32 v197, v55, v197
	v_mul_f32_e32 v198, v55, v198
	v_mul_f32_e32 v199, v55, v199
	ds_write_b128 v210, v[196:199] offset:5120
	v_mul_f32_e32 v200, v56, v200
	v_mul_f32_e32 v201, v56, v201
	v_mul_f32_e32 v202, v56, v202
	v_mul_f32_e32 v203, v56, v203
	ds_write_b128 v210, v[200:203] offset:6144
	v_mul_f32_e32 v204, v57, v204
	v_mul_f32_e32 v205, v57, v205
	v_mul_f32_e32 v206, v57, v206
	v_mul_f32_e32 v207, v57, v207
	ds_write_b128 v210, v[204:207] offset:7168
	s_waitcnt lgkmcnt(0)
	s_barrier
; #define GAS __attribute__((address_space(1)))
; #define LAS __attribute__((address_space(3)))
; #define LDS_WAIT() asm volatile("s_waitcnt lgkmcnt(0)" ::: "memory")
;     const int pr = item >> 1, kb = 2 * (pr / nblk) + (item & 1), nb = pr % nblk, k0 = 64 * kb, n0 = 32 * nb;
;     const int nr = n0 + (lane & 31); const int sc = MAP == 1 ? src_col_in(nr) : nr;
;     float v[32];
; #pragma unroll
;     for (int i = 0; i < 32; ++i) v[i] = sc >= 0 ? W[(size_t)(k0 + 2 * i + (lane >> 5)) * Nsrc + sc] : 0.f;
; #pragma unroll
;     for (int i = 0; i < 32; ++i) { const int k = k0 + 2 * i + (lane >> 5); float x = v[i] * wscale; if (KS) x *= (k < ksplit ? ksA[k] : ksB[k - ksplit]); scr[(2 * i + (lane >> 5)) * 33 + (lane & 31)] = x; }
;     LDS_WAIT(); asm volatile("" ::: "memory");
;     const int c = lane & 7;
; #pragma unroll
;     for (int j = 0; j < 4; ++j) { const int n = (lane >> 3) + 8 * j; const LAS float* s = scr + (8 * c) * 33 + n;
;         const unsigned long long o = (unsigned long long)pg8::pk4_fp8(s[0 * 33], s[1 * 33], s[2 * 33], s[3 * 33]) | ((unsigned long long)pg8::pk4_fp8(s[4 * 33], s[5 * 33], s[6 * 33], s[7 * 33]) << 32);
;         *(GAS unsigned long long*)(WT + (size_t)(n0 + n) * K + k0 + 8 * c) = o; }
;     LDS_WAIT(); asm volatile("" ::: "memory");
; __global__ void __launch_bounds__(NWAVES * 64, 2) hybrid_fwd(Args args) {
;     ...
;             if (r < I_IN) { if (l >= PROJ_F8_FROM) p0_transpose_item_f8<true, 1>(args.in[2] + (size_t)l * DM * NSRC, DM, NSRC, NPROJ / 32, (unsigned char*)(ws + WS_WIN + l * SZ_WIN), WUP8_SCALE, args.in[1] + l * DM, args.in[1] + l * DM, DM, scr, r, lane);
	s_add_i32 s24, s23, 16
	s_lshl_b32 s20, s24, 7
	s_cmp_lt_u32 s24, 40
	s_cselect_b32 s21, 0, 0x830
	s_cmp_lt_u32 s24, 72
	s_cselect_b32 s21, s21, 0xfffff030
	s_add_i32 s20, s20, s21
	s_lshl_b32 s20, s20, 2
	s_add_u32 s8, s50, s20
	s_addc_u32 s9, s51, 0
	global_load_dwordx4 v[176:179], v76, s[8:9]
	s_add_u32 s8, s8, 0x16280
	s_addc_u32 s9, s9, 0
	global_load_dwordx4 v[180:183], v76, s[8:9]
	s_add_u32 s8, s8, 0x16280
	s_addc_u32 s9, s9, 0
	global_load_dwordx4 v[184:187], v76, s[8:9]
	s_add_u32 s8, s8, 0x16280
	s_addc_u32 s9, s9, 0
	global_load_dwordx4 v[188:191], v76, s[8:9]
	s_add_u32 s8, s8, 0x16280
	s_addc_u32 s9, s9, 0
	global_load_dwordx4 v[192:195], v76, s[8:9]
	s_add_u32 s8, s8, 0x16280
	s_addc_u32 s9, s9, 0
	global_load_dwordx4 v[196:199], v76, s[8:9]
	s_add_u32 s8, s8, 0x16280
	s_addc_u32 s9, s9, 0
	global_load_dwordx4 v[200:203], v76, s[8:9]
	s_add_u32 s8, s8, 0x16280
	s_addc_u32 s9, s9, 0
	global_load_dwordx4 v[204:207], v76, s[8:9]
	s_add_i32 s24, s23, 0
	s_mul_i32 s20, s24, 0x80000
	s_add_u32 s6, s52, s20
	s_addc_u32 s7, s53, 0
	s_cmp_lt_u32 s24, 16
	s_cselect_b32 s20, 1, 0
	s_sub_i32 s21, s24, 16
	s_bitcmp0_b32 s21, 2
	s_cselect_b32 s21, 1, 0
	s_cmp_lt_u32 s24, 40
	s_cselect_b32 s21, s21, 0
	s_or_b32 s20, s20, s21
	s_cmp_lg_u32 s20, 0
	s_cselect_b64 s[20:21], -1, 0
	v_cndmask_b32_e64 v91, v77, v81, s[20:21]
	v_cndmask_b32_e64 v92, v78, v82, s[20:21]
	ds_read_b32 v226, v212
	ds_read_b32 v227, v212 offset:512
	ds_read_b32 v228, v212 offset:1024
	ds_read_b32 v229, v212 offset:1536
	ds_read_b32 v230, v212 offset:2048
	ds_read_b32 v231, v212 offset:2560
	ds_read_b32 v232, v212 offset:3072
	ds_read_b32 v233, v212 offset:3584
	ds_read_b32 v234, v212 offset:4096
	ds_read_b32 v235, v212 offset:4608
	ds_read_b32 v236, v212 offset:5120
	ds_read_b32 v237, v212 offset:5632
	ds_read_b32 v238, v212 offset:6144
	ds_read_b32 v239, v212 offset:6656
	ds_read_b32 v240, v212 offset:7168
	ds_read_b32 v241, v212 offset:7680
	s_waitcnt lgkmcnt(0)
	v_max_f32_e32 v226, v226, v226
	v_max_f32_e32 v227, v227, v227
	v_max_f32_e32 v228, v228, v228
	v_max_f32_e32 v229, v229, v229
	v_max_f32_e32 v230, v230, v230
	v_max_f32_e32 v231, v231, v231
	v_max_f32_e32 v232, v232, v232
	v_max_f32_e32 v233, v233, v233
	v_max_f32_e32 v234, v234, v234
	v_max_f32_e32 v235, v235, v235
	v_max_f32_e32 v236, v236, v236
	v_max_f32_e32 v237, v237, v237
	v_max_f32_e32 v238, v238, v238
	v_max_f32_e32 v239, v239, v239
	v_max_f32_e32 v240, v240, v240
	v_max_f32_e32 v241, v241, v241
	v_med3_f32 v226, v226, s62, v95
	v_med3_f32 v227, v227, s62, v95
	v_med3_f32 v228, v228, s62, v95
	v_med3_f32 v229, v229, s62, v95
	v_med3_f32 v230, v230, s62, v95
	v_med3_f32 v231, v231, s62, v95
	v_med3_f32 v232, v232, s62, v95
	v_med3_f32 v233, v233, s62, v95
	v_med3_f32 v234, v234, s62, v95
	v_med3_f32 v235, v235, s62, v95
	v_med3_f32 v236, v236, s62, v95
	v_med3_f32 v237, v237, s62, v95
	v_med3_f32 v238, v238, s62, v95
	v_med3_f32 v239, v239, s62, v95
	v_med3_f32 v240, v240, s62, v95
	v_med3_f32 v241, v241, s62, v95
	v_mov_b32_e32 v242, 0
	v_mov_b32_e32 v243, 0
	v_mov_b32_e32 v244, 0
	v_mov_b32_e32 v245, 0
	v_cvt_pk_fp8_f32 v242, v226, v227
	v_cvt_pk_fp8_f32 v243, v230, v231
	v_cvt_pk_fp8_f32 v244, v234, v235
	v_cvt_pk_fp8_f32 v245, v238, v239
	v_cvt_pk_fp8_f32 v242, v228, v229 op_sel:[0,0,1]
	v_cvt_pk_fp8_f32 v243, v232, v233 op_sel:[0,0,1]
	v_cvt_pk_fp8_f32 v244, v236, v237 op_sel:[0,0,1]
	v_cvt_pk_fp8_f32 v245, v240, v241 op_sel:[0,0,1]
	s_nop 0
	global_store_dwordx4 v91, v[242:245], s[6:7]
	ds_read_b32 v226, v214
	ds_read_b32 v227, v214 offset:512
	ds_read_b32 v228, v214 offset:1024
	ds_read_b32 v229, v214 offset:1536
	ds_read_b32 v230, v214 offset:2048
	ds_read_b32 v231, v214 offset:2560
	ds_read_b32 v232, v214 offset:3072
	ds_read_b32 v233, v214 offset:3584
	ds_read_b32 v234, v214 offset:4096
	ds_read_b32 v235, v214 offset:4608
	ds_read_b32 v236, v214 offset:5120
	ds_read_b32 v237, v214 offset:5632
	ds_read_b32 v238, v214 offset:6144
	ds_read_b32 v239, v214 offset:6656
	ds_read_b32 v240, v214 offset:7168
	ds_read_b32 v241, v214 offset:7680
	s_waitcnt lgkmcnt(0)
	v_max_f32_e32 v226, v226, v226
	v_max_f32_e32 v227, v227, v227
	v_max_f32_e32 v228, v228, v228
	v_max_f32_e32 v229, v229, v229
	v_max_f32_e32 v230, v230, v230
	v_max_f32_e32 v231, v231, v231
	v_max_f32_e32 v232, v232, v232
	v_max_f32_e32 v233, v233, v233
	v_max_f32_e32 v234, v234, v234
	v_max_f32_e32 v235, v235, v235
	v_max_f32_e32 v236, v236, v236
	v_max_f32_e32 v237, v237, v237
	v_max_f32_e32 v238, v238, v238
	v_max_f32_e32 v239, v239, v239
	v_max_f32_e32 v240, v240, v240
	v_max_f32_e32 v241, v241, v241
	v_med3_f32 v226, v226, s62, v95
	v_med3_f32 v227, v227, s62, v95
	v_med3_f32 v228, v228, s62, v95
	v_med3_f32 v229, v229, s62, v95
	v_med3_f32 v230, v230, s62, v95
	v_med3_f32 v231, v231, s62, v95
	v_med3_f32 v232, v232, s62, v95
	v_med3_f32 v233, v233, s62, v95
	v_med3_f32 v234, v234, s62, v95
	v_med3_f32 v235, v235, s62, v95
	v_med3_f32 v236, v236, s62, v95
	v_med3_f32 v237, v237, s62, v95
	v_med3_f32 v238, v238, s62, v95
	v_med3_f32 v239, v239, s62, v95
	v_med3_f32 v240, v240, s62, v95
	v_med3_f32 v241, v241, s62, v95
	v_mov_b32_e32 v242, 0
	v_mov_b32_e32 v243, 0
	v_mov_b32_e32 v244, 0
	v_mov_b32_e32 v245, 0
	v_cvt_pk_fp8_f32 v242, v226, v227
	v_cvt_pk_fp8_f32 v243, v230, v231
	v_cvt_pk_fp8_f32 v244, v234, v235
	v_cvt_pk_fp8_f32 v245, v238, v239
	v_cvt_pk_fp8_f32 v242, v228, v229 op_sel:[0,0,1]
	v_cvt_pk_fp8_f32 v243, v232, v233 op_sel:[0,0,1]
	v_cvt_pk_fp8_f32 v244, v236, v237 op_sel:[0,0,1]
	v_cvt_pk_fp8_f32 v245, v240, v241 op_sel:[0,0,1]
	s_nop 0
	global_store_dwordx4 v92, v[242:245], s[6:7]
	s_waitcnt vmcnt(14)
	v_mul_f32_e32 v144, v50, v144
	v_mul_f32_e32 v145, v50, v145
	v_mul_f32_e32 v146, v50, v146
	v_mul_f32_e32 v147, v50, v147
	ds_write_b128 v209, v[144:147]
	v_mul_f32_e32 v148, v51, v148
	v_mul_f32_e32 v149, v51, v149
	v_mul_f32_e32 v150, v51, v150
	v_mul_f32_e32 v151, v51, v151
	ds_write_b128 v209, v[148:151] offset:1024
	v_mul_f32_e32 v152, v52, v152
	v_mul_f32_e32 v153, v52, v153
	v_mul_f32_e32 v154, v52, v154
	v_mul_f32_e32 v155, v52, v155
	ds_write_b128 v209, v[152:155] offset:2048
	v_mul_f32_e32 v156, v53, v156
	v_mul_f32_e32 v157, v53, v157
	v_mul_f32_e32 v158, v53, v158
	v_mul_f32_e32 v159, v53, v159
	ds_write_b128 v209, v[156:159] offset:3072
	v_mul_f32_e32 v160, v54, v160
	v_mul_f32_e32 v161, v54, v161
	v_mul_f32_e32 v162, v54, v162
	v_mul_f32_e32 v163, v54, v163
	ds_write_b128 v209, v[160:163] offset:4096
	v_mul_f32_e32 v164, v55, v164
	v_mul_f32_e32 v165, v55, v165
	v_mul_f32_e32 v166, v55, v166
	v_mul_f32_e32 v167, v55, v167
	ds_write_b128 v209, v[164:167] offset:5120
	v_mul_f32_e32 v168, v56, v168
	v_mul_f32_e32 v169, v56, v169
	v_mul_f32_e32 v170, v56, v170
	v_mul_f32_e32 v171, v56, v171
	ds_write_b128 v209, v[168:171] offset:6144
	v_mul_f32_e32 v172, v57, v172
	v_mul_f32_e32 v173, v57, v173
	v_mul_f32_e32 v174, v57, v174
	v_mul_f32_e32 v175, v57, v175
	ds_write_b128 v209, v[172:175] offset:7168
	s_waitcnt lgkmcnt(0)
	s_barrier
; #define GAS __attribute__((address_space(1)))
; #define LAS __attribute__((address_space(3)))
; #define LDS_WAIT() asm volatile("s_waitcnt lgkmcnt(0)" ::: "memory")
;     const int pr = item >> 1, kb = 2 * (pr / nblk) + (item & 1), nb = pr % nblk, k0 = 64 * kb, n0 = 32 * nb;
;     const int nr = n0 + (lane & 31); const int sc = MAP == 1 ? src_col_in(nr) : nr;
;     float v[32];
; #pragma unroll
;     for (int i = 0; i < 32; ++i) v[i] = sc >= 0 ? W[(size_t)(k0 + 2 * i + (lane >> 5)) * Nsrc + sc] : 0.f;
; #pragma unroll
;     for (int i = 0; i < 32; ++i) { const int k = k0 + 2 * i + (lane >> 5); float x = v[i] * wscale; if (KS) x *= (k < ksplit ? ksA[k] : ksB[k - ksplit]); scr[(2 * i + (lane >> 5)) * 33 + (lane & 31)] = x; }
;     LDS_WAIT(); asm volatile("" ::: "memory");
;     const int c = lane & 7;
; #pragma unroll
;     for (int j = 0; j < 4; ++j) { const int n = (lane >> 3) + 8 * j; const LAS float* s = scr + (8 * c) * 33 + n;
;         const unsigned long long o = (unsigned long long)pg8::pk4_fp8(s[0 * 33], s[1 * 33], s[2 * 33], s[3 * 33]) | ((unsigned long long)pg8::pk4_fp8(s[4 * 33], s[5 * 33], s[6 * 33], s[7 * 33]) << 32);
;         *(GAS unsigned long long*)(WT + (size_t)(n0 + n) * K + k0 + 8 * c) = o; }
;     LDS_WAIT(); asm volatile("" ::: "memory");
; __global__ void __launch_bounds__(NWAVES * 64, 2) hybrid_fwd(Args args) {
;     ...
;             if (r < I_IN) { if (l >= PROJ_F8_FROM) p0_transpose_item_f8<true, 1>(args.in[2] + (size_t)l * DM * NSRC, DM, NSRC, NPROJ / 32, (unsigned char*)(ws + WS_WIN + l * SZ_WIN), WUP8_SCALE, args.in[1] + l * DM, args.in[1] + l * DM, DM, scr, r, lane);
	s_add_i32 s24, s23, 24
	s_lshl_b32 s20, s24, 7
	s_cmp_lt_u32 s24, 40
	s_cselect_b32 s21, 0, 0x830
	s_cmp_lt_u32 s24, 72
	s_cselect_b32 s21, s21, 0xfffff030
	s_add_i32 s20, s20, s21
	s_lshl_b32 s20, s20, 2
	s_add_u32 s8, s50, s20
	s_addc_u32 s9, s51, 0
	global_load_dwordx4 v[144:147], v76, s[8:9]
	s_add_u32 s8, s8, 0x16280
	s_addc_u32 s9, s9, 0
	global_load_dwordx4 v[148:151], v76, s[8:9]
	s_add_u32 s8, s8, 0x16280
	s_addc_u32 s9, s9, 0
	global_load_dwordx4 v[152:155], v76, s[8:9]
	s_add_u32 s8, s8, 0x16280
	s_addc_u32 s9, s9, 0
	global_load_dwordx4 v[156:159], v76, s[8:9]
	s_add_u32 s8, s8, 0x16280
	s_addc_u32 s9, s9, 0
	global_load_dwordx4 v[160:163], v76, s[8:9]
	s_add_u32 s8, s8, 0x16280
	s_addc_u32 s9, s9, 0
	global_load_dwordx4 v[164:167], v76, s[8:9]
	s_add_u32 s8, s8, 0x16280
	s_addc_u32 s9, s9, 0
	global_load_dwordx4 v[168:171], v76, s[8:9]
	s_add_u32 s8, s8, 0x16280
	s_addc_u32 s9, s9, 0
	global_load_dwordx4 v[172:175], v76, s[8:9]
	s_add_i32 s24, s23, 8
	s_mul_i32 s20, s24, 0x80000
	s_add_u32 s6, s52, s20
	s_addc_u32 s7, s53, 0
	s_cmp_lt_u32 s24, 16
	s_cselect_b32 s20, 1, 0
	s_sub_i32 s21, s24, 16
	s_bitcmp0_b32 s21, 2
	s_cselect_b32 s21, 1, 0
	s_cmp_lt_u32 s24, 40
	s_cselect_b32 s21, s21, 0
	s_or_b32 s20, s20, s21
	s_cmp_lg_u32 s20, 0
	s_cselect_b64 s[20:21], -1, 0
	v_cndmask_b32_e64 v91, v77, v81, s[20:21]
	v_cndmask_b32_e64 v92, v78, v82, s[20:21]
	ds_read_b32 v226, v211
	ds_read_b32 v227, v211 offset:512
	ds_read_b32 v228, v211 offset:1024
	ds_read_b32 v229, v211 offset:1536
	ds_read_b32 v230, v211 offset:2048
	ds_read_b32 v231, v211 offset:2560
	ds_read_b32 v232, v211 offset:3072
	ds_read_b32 v233, v211 offset:3584
	ds_read_b32 v234, v211 offset:4096
	ds_read_b32 v235, v211 offset:4608
	ds_read_b32 v236, v211 offset:5120
	ds_read_b32 v237, v211 offset:5632
	ds_read_b32 v238, v211 offset:6144
	ds_read_b32 v239, v211 offset:6656
	ds_read_b32 v240, v211 offset:7168
	ds_read_b32 v241, v211 offset:7680
	s_waitcnt lgkmcnt(0)
	v_max_f32_e32 v226, v226, v226
	v_max_f32_e32 v227, v227, v227
	v_max_f32_e32 v228, v228, v228
	v_max_f32_e32 v229, v229, v229
	v_max_f32_e32 v230, v230, v230
	v_max_f32_e32 v231, v231, v231
	v_max_f32_e32 v232, v232, v232
	v_max_f32_e32 v233, v233, v233
	v_max_f32_e32 v234, v234, v234
	v_max_f32_e32 v235, v235, v235
	v_max_f32_e32 v236, v236, v236
	v_max_f32_e32 v237, v237, v237
	v_max_f32_e32 v238, v238, v238
	v_max_f32_e32 v239, v239, v239
	v_max_f32_e32 v240, v240, v240
	v_max_f32_e32 v241, v241, v241
	v_med3_f32 v226, v226, s62, v95
	v_med3_f32 v227, v227, s62, v95
	v_med3_f32 v228, v228, s62, v95
	v_med3_f32 v229, v229, s62, v95
	v_med3_f32 v230, v230, s62, v95
	v_med3_f32 v231, v231, s62, v95
	v_med3_f32 v232, v232, s62, v95
	v_med3_f32 v233, v233, s62, v95
	v_med3_f32 v234, v234, s62, v95
	v_med3_f32 v235, v235, s62, v95
	v_med3_f32 v236, v236, s62, v95
	v_med3_f32 v237, v237, s62, v95
	v_med3_f32 v238, v238, s62, v95
	v_med3_f32 v239, v239, s62, v95
	v_med3_f32 v240, v240, s62, v95
	v_med3_f32 v241, v241, s62, v95
	v_mov_b32_e32 v242, 0
	v_mov_b32_e32 v243, 0
	v_mov_b32_e32 v244, 0
	v_mov_b32_e32 v245, 0
	v_cvt_pk_fp8_f32 v242, v226, v227
	v_cvt_pk_fp8_f32 v243, v230, v231
	v_cvt_pk_fp8_f32 v244, v234, v235
	v_cvt_pk_fp8_f32 v245, v238, v239
	v_cvt_pk_fp8_f32 v242, v228, v229 op_sel:[0,0,1]
	v_cvt_pk_fp8_f32 v243, v232, v233 op_sel:[0,0,1]
	v_cvt_pk_fp8_f32 v244, v236, v237 op_sel:[0,0,1]
	v_cvt_pk_fp8_f32 v245, v240, v241 op_sel:[0,0,1]
	s_nop 0
	global_store_dwordx4 v91, v[242:245], s[6:7]
	ds_read_b32 v226, v213
	ds_read_b32 v227, v213 offset:512
	ds_read_b32 v228, v213 offset:1024
	ds_read_b32 v229, v213 offset:1536
	ds_read_b32 v230, v213 offset:2048
	ds_read_b32 v231, v213 offset:2560
	ds_read_b32 v232, v213 offset:3072
	ds_read_b32 v233, v213 offset:3584
	ds_read_b32 v234, v213 offset:4096
	ds_read_b32 v235, v213 offset:4608
	ds_read_b32 v236, v213 offset:5120
	ds_read_b32 v237, v213 offset:5632
	ds_read_b32 v238, v213 offset:6144
	ds_read_b32 v239, v213 offset:6656
	ds_read_b32 v240, v213 offset:7168
	ds_read_b32 v241, v213 offset:7680
	s_waitcnt lgkmcnt(0)
	v_max_f32_e32 v226, v226, v226
	v_max_f32_e32 v227, v227, v227
	v_max_f32_e32 v228, v228, v228
	v_max_f32_e32 v229, v229, v229
	v_max_f32_e32 v230, v230, v230
	v_max_f32_e32 v231, v231, v231
	v_max_f32_e32 v232, v232, v232
	v_max_f32_e32 v233, v233, v233
	v_max_f32_e32 v234, v234, v234
	v_max_f32_e32 v235, v235, v235
	v_max_f32_e32 v236, v236, v236
	v_max_f32_e32 v237, v237, v237
	v_max_f32_e32 v238, v238, v238
	v_max_f32_e32 v239, v239, v239
	v_max_f32_e32 v240, v240, v240
	v_max_f32_e32 v241, v241, v241
	v_med3_f32 v226, v226, s62, v95
	v_med3_f32 v227, v227, s62, v95
	v_med3_f32 v228, v228, s62, v95
	v_med3_f32 v229, v229, s62, v95
	v_med3_f32 v230, v230, s62, v95
	v_med3_f32 v231, v231, s62, v95
	v_med3_f32 v232, v232, s62, v95
	v_med3_f32 v233, v233, s62, v95
	v_med3_f32 v234, v234, s62, v95
	v_med3_f32 v235, v235, s62, v95
	v_med3_f32 v236, v236, s62, v95
	v_med3_f32 v237, v237, s62, v95
	v_med3_f32 v238, v238, s62, v95
	v_med3_f32 v239, v239, s62, v95
	v_med3_f32 v240, v240, s62, v95
	v_med3_f32 v241, v241, s62, v95
	v_mov_b32_e32 v242, 0
	v_mov_b32_e32 v243, 0
	v_mov_b32_e32 v244, 0
	v_mov_b32_e32 v245, 0
	v_cvt_pk_fp8_f32 v242, v226, v227
	v_cvt_pk_fp8_f32 v243, v230, v231
	v_cvt_pk_fp8_f32 v244, v234, v235
	v_cvt_pk_fp8_f32 v245, v238, v239
	v_cvt_pk_fp8_f32 v242, v228, v229 op_sel:[0,0,1]
	v_cvt_pk_fp8_f32 v243, v232, v233 op_sel:[0,0,1]
	v_cvt_pk_fp8_f32 v244, v236, v237 op_sel:[0,0,1]
	v_cvt_pk_fp8_f32 v245, v240, v241 op_sel:[0,0,1]
	s_nop 0
	global_store_dwordx4 v92, v[242:245], s[6:7]
	s_waitcnt vmcnt(12)
	v_mul_f32_e32 v176, v50, v176
	v_mul_f32_e32 v177, v50, v177
	v_mul_f32_e32 v178, v50, v178
	v_mul_f32_e32 v179, v50, v179
	ds_write_b128 v210, v[176:179]
	v_mul_f32_e32 v180, v51, v180
	v_mul_f32_e32 v181, v51, v181
	v_mul_f32_e32 v182, v51, v182
	v_mul_f32_e32 v183, v51, v183
	ds_write_b128 v210, v[180:183] offset:1024
	v_mul_f32_e32 v184, v52, v184
	v_mul_f32_e32 v185, v52, v185
	v_mul_f32_e32 v186, v52, v186
	v_mul_f32_e32 v187, v52, v187
	ds_write_b128 v210, v[184:187] offset:2048
	v_mul_f32_e32 v188, v53, v188
	v_mul_f32_e32 v189, v53, v189
	v_mul_f32_e32 v190, v53, v190
	v_mul_f32_e32 v191, v53, v191
	ds_write_b128 v210, v[188:191] offset:3072
	v_mul_f32_e32 v192, v54, v192
	v_mul_f32_e32 v193, v54, v193
	v_mul_f32_e32 v194, v54, v194
	v_mul_f32_e32 v195, v54, v195
	ds_write_b128 v210, v[192:195] offset:4096
	v_mul_f32_e32 v196, v55, v196
	v_mul_f32_e32 v197, v55, v197
	v_mul_f32_e32 v198, v55, v198
	v_mul_f32_e32 v199, v55, v199
	ds_write_b128 v210, v[196:199] offset:5120
	v_mul_f32_e32 v200, v56, v200
	v_mul_f32_e32 v201, v56, v201
	v_mul_f32_e32 v202, v56, v202
	v_mul_f32_e32 v203, v56, v203
	ds_write_b128 v210, v[200:203] offset:6144
	v_mul_f32_e32 v204, v57, v204
	v_mul_f32_e32 v205, v57, v205
	v_mul_f32_e32 v206, v57, v206
	v_mul_f32_e32 v207, v57, v207
	ds_write_b128 v210, v[204:207] offset:7168
	s_waitcnt lgkmcnt(0)
	s_barrier
; #define GAS __attribute__((address_space(1)))
; #define LAS __attribute__((address_space(3)))
; #define LDS_WAIT() asm volatile("s_waitcnt lgkmcnt(0)" ::: "memory")
;     const int pr = item >> 1, kb = 2 * (pr / nblk) + (item & 1), nb = pr % nblk, k0 = 64 * kb, n0 = 32 * nb;
;     const int nr = n0 + (lane & 31); const int sc = MAP == 1 ? src_col_in(nr) : nr;
;     float v[32];
; #pragma unroll
;     for (int i = 0; i < 32; ++i) v[i] = sc >= 0 ? W[(size_t)(k0 + 2 * i + (lane >> 5)) * Nsrc + sc] : 0.f;
; #pragma unroll
;     for (int i = 0; i < 32; ++i) { const int k = k0 + 2 * i + (lane >> 5); float x = v[i] * wscale; if (KS) x *= (k < ksplit ? ksA[k] : ksB[k - ksplit]); scr[(2 * i + (lane >> 5)) * 33 + (lane & 31)] = x; }
;     LDS_WAIT(); asm volatile("" ::: "memory");
;     const int c = lane & 7;
; #pragma unroll
;     for (int j = 0; j < 4; ++j) { const int n = (lane >> 3) + 8 * j; const LAS float* s = scr + (8 * c) * 33 + n;
;         const unsigned long long o = (unsigned long long)pg8::pk4_fp8(s[0 * 33], s[1 * 33], s[2 * 33], s[3 * 33]) | ((unsigned long long)pg8::pk4_fp8(s[4 * 33], s[5 * 33], s[6 * 33], s[7 * 33]) << 32);
;         *(GAS unsigned long long*)(WT + (size_t)(n0 + n) * K + k0 + 8 * c) = o; }
;     LDS_WAIT(); asm volatile("" ::: "memory");
; __global__ void __launch_bounds__(NWAVES * 64, 2) hybrid_fwd(Args args) {
;     ...
;             if (r < I_IN) { if (l >= PROJ_F8_FROM) p0_transpose_item_f8<true, 1>(args.in[2] + (size_t)l * DM * NSRC, DM, NSRC, NPROJ / 32, (unsigned char*)(ws + WS_WIN + l * SZ_WIN), WUP8_SCALE, args.in[1] + l * DM, args.in[1] + l * DM, DM, scr, r, lane);
	s_add_i32 s24, s23, 32
	s_lshl_b32 s20, s24, 7
	s_cmp_lt_u32 s24, 40
	s_cselect_b32 s21, 0, 0x830
	s_cmp_lt_u32 s24, 72
	s_cselect_b32 s21, s21, 0xfffff030
	s_add_i32 s20, s20, s21
	s_lshl_b32 s20, s20, 2
	s_add_u32 s8, s50, s20
	s_addc_u32 s9, s51, 0
	global_load_dwordx4 v[176:179], v76, s[8:9]
	s_add_u32 s8, s8, 0x16280
	s_addc_u32 s9, s9, 0
	global_load_dwordx4 v[180:183], v76, s[8:9]
	s_add_u32 s8, s8, 0x16280
	s_addc_u32 s9, s9, 0
	global_load_dwordx4 v[184:187], v76, s[8:9]
	s_add_u32 s8, s8, 0x16280
	s_addc_u32 s9, s9, 0
	global_load_dwordx4 v[188:191], v76, s[8:9]
	s_add_u32 s8, s8, 0x16280
	s_addc_u32 s9, s9, 0
	global_load_dwordx4 v[192:195], v76, s[8:9]
	s_add_u32 s8, s8, 0x16280
	s_addc_u32 s9, s9, 0
	global_load_dwordx4 v[196:199], v76, s[8:9]
	s_add_u32 s8, s8, 0x16280
	s_addc_u32 s9, s9, 0
	global_load_dwordx4 v[200:203], v76, s[8:9]
	s_add_u32 s8, s8, 0x16280
	s_addc_u32 s9, s9, 0
	global_load_dwordx4 v[204:207], v76, s[8:9]
	s_add_i32 s24, s23, 16
	s_mul_i32 s20, s24, 0x80000
	s_add_u32 s6, s52, s20
	s_addc_u32 s7, s53, 0
	s_cmp_lt_u32 s24, 16
	s_cselect_b32 s20, 1, 0
	s_sub_i32 s21, s24, 16
	s_bitcmp0_b32 s21, 2
	s_cselect_b32 s21, 1, 0
	s_cmp_lt_u32 s24, 40
	s_cselect_b32 s21, s21, 0
	s_or_b32 s20, s20, s21
	s_cmp_lg_u32 s20, 0
	s_cselect_b64 s[20:21], -1, 0
	v_cndmask_b32_e64 v91, v77, v81, s[20:21]
	v_cndmask_b32_e64 v92, v78, v82, s[20:21]
	ds_read_b32 v226, v212
	ds_read_b32 v227, v212 offset:512
	ds_read_b32 v228, v212 offset:1024
	ds_read_b32 v229, v212 offset:1536
	ds_read_b32 v230, v212 offset:2048
	ds_read_b32 v231, v212 offset:2560
	ds_read_b32 v232, v212 offset:3072
	ds_read_b32 v233, v212 offset:3584
	ds_read_b32 v234, v212 offset:4096
	ds_read_b32 v235, v212 offset:4608
	ds_read_b32 v236, v212 offset:5120
	ds_read_b32 v237, v212 offset:5632
	ds_read_b32 v238, v212 offset:6144
	ds_read_b32 v239, v212 offset:6656
	ds_read_b32 v240, v212 offset:7168
	ds_read_b32 v241, v212 offset:7680
	s_waitcnt lgkmcnt(0)
	v_max_f32_e32 v226, v226, v226
	v_max_f32_e32 v227, v227, v227
	v_max_f32_e32 v228, v228, v228
	v_max_f32_e32 v229, v229, v229
	v_max_f32_e32 v230, v230, v230
	v_max_f32_e32 v231, v231, v231
	v_max_f32_e32 v232, v232, v232
	v_max_f32_e32 v233, v233, v233
	v_max_f32_e32 v234, v234, v234
	v_max_f32_e32 v235, v235, v235
	v_max_f32_e32 v236, v236, v236
	v_max_f32_e32 v237, v237, v237
	v_max_f32_e32 v238, v238, v238
	v_max_f32_e32 v239, v239, v239
	v_max_f32_e32 v240, v240, v240
	v_max_f32_e32 v241, v241, v241
	v_med3_f32 v226, v226, s62, v95
	v_med3_f32 v227, v227, s62, v95
	v_med3_f32 v228, v228, s62, v95
	v_med3_f32 v229, v229, s62, v95
	v_med3_f32 v230, v230, s62, v95
	v_med3_f32 v231, v231, s62, v95
	v_med3_f32 v232, v232, s62, v95
	v_med3_f32 v233, v233, s62, v95
	v_med3_f32 v234, v234, s62, v95
	v_med3_f32 v235, v235, s62, v95
	v_med3_f32 v236, v236, s62, v95
	v_med3_f32 v237, v237, s62, v95
	v_med3_f32 v238, v238, s62, v95
	v_med3_f32 v239, v239, s62, v95
	v_med3_f32 v240, v240, s62, v95
	v_med3_f32 v241, v241, s62, v95
	v_mov_b32_e32 v242, 0
	v_mov_b32_e32 v243, 0
	v_mov_b32_e32 v244, 0
	v_mov_b32_e32 v245, 0
	v_cvt_pk_fp8_f32 v242, v226, v227
	v_cvt_pk_fp8_f32 v243, v230, v231
	v_cvt_pk_fp8_f32 v244, v234, v235
	v_cvt_pk_fp8_f32 v245, v238, v239
	v_cvt_pk_fp8_f32 v242, v228, v229 op_sel:[0,0,1]
	v_cvt_pk_fp8_f32 v243, v232, v233 op_sel:[0,0,1]
	v_cvt_pk_fp8_f32 v244, v236, v237 op_sel:[0,0,1]
	v_cvt_pk_fp8_f32 v245, v240, v241 op_sel:[0,0,1]
	s_nop 0
	global_store_dwordx4 v91, v[242:245], s[6:7]
	ds_read_b32 v226, v214
	ds_read_b32 v227, v214 offset:512
	ds_read_b32 v228, v214 offset:1024
	ds_read_b32 v229, v214 offset:1536
	ds_read_b32 v230, v214 offset:2048
	ds_read_b32 v231, v214 offset:2560
	ds_read_b32 v232, v214 offset:3072
	ds_read_b32 v233, v214 offset:3584
	ds_read_b32 v234, v214 offset:4096
	ds_read_b32 v235, v214 offset:4608
	ds_read_b32 v236, v214 offset:5120
	ds_read_b32 v237, v214 offset:5632
	ds_read_b32 v238, v214 offset:6144
	ds_read_b32 v239, v214 offset:6656
	ds_read_b32 v240, v214 offset:7168
	ds_read_b32 v241, v214 offset:7680
	s_waitcnt lgkmcnt(0)
	v_max_f32_e32 v226, v226, v226
	v_max_f32_e32 v227, v227, v227
	v_max_f32_e32 v228, v228, v228
	v_max_f32_e32 v229, v229, v229
	v_max_f32_e32 v230, v230, v230
	v_max_f32_e32 v231, v231, v231
	v_max_f32_e32 v232, v232, v232
	v_max_f32_e32 v233, v233, v233
	v_max_f32_e32 v234, v234, v234
	v_max_f32_e32 v235, v235, v235
	v_max_f32_e32 v236, v236, v236
	v_max_f32_e32 v237, v237, v237
	v_max_f32_e32 v238, v238, v238
	v_max_f32_e32 v239, v239, v239
	v_max_f32_e32 v240, v240, v240
	v_max_f32_e32 v241, v241, v241
	v_med3_f32 v226, v226, s62, v95
	v_med3_f32 v227, v227, s62, v95
	v_med3_f32 v228, v228, s62, v95
	v_med3_f32 v229, v229, s62, v95
	v_med3_f32 v230, v230, s62, v95
	v_med3_f32 v231, v231, s62, v95
	v_med3_f32 v232, v232, s62, v95
	v_med3_f32 v233, v233, s62, v95
	v_med3_f32 v234, v234, s62, v95
	v_med3_f32 v235, v235, s62, v95
	v_med3_f32 v236, v236, s62, v95
	v_med3_f32 v237, v237, s62, v95
	v_med3_f32 v238, v238, s62, v95
	v_med3_f32 v239, v239, s62, v95
	v_med3_f32 v240, v240, s62, v95
	v_med3_f32 v241, v241, s62, v95
	v_mov_b32_e32 v242, 0
	v_mov_b32_e32 v243, 0
	v_mov_b32_e32 v244, 0
	v_mov_b32_e32 v245, 0
	v_cvt_pk_fp8_f32 v242, v226, v227
	v_cvt_pk_fp8_f32 v243, v230, v231
	v_cvt_pk_fp8_f32 v244, v234, v235
	v_cvt_pk_fp8_f32 v245, v238, v239
	v_cvt_pk_fp8_f32 v242, v228, v229 op_sel:[0,0,1]
	v_cvt_pk_fp8_f32 v243, v232, v233 op_sel:[0,0,1]
	v_cvt_pk_fp8_f32 v244, v236, v237 op_sel:[0,0,1]
	v_cvt_pk_fp8_f32 v245, v240, v241 op_sel:[0,0,1]
	s_nop 0
	global_store_dwordx4 v92, v[242:245], s[6:7]
	s_waitcnt vmcnt(12)
	v_mul_f32_e32 v144, v50, v144
	v_mul_f32_e32 v145, v50, v145
	v_mul_f32_e32 v146, v50, v146
	v_mul_f32_e32 v147, v50, v147
	ds_write_b128 v209, v[144:147]
	v_mul_f32_e32 v148, v51, v148
	v_mul_f32_e32 v149, v51, v149
	v_mul_f32_e32 v150, v51, v150
	v_mul_f32_e32 v151, v51, v151
	ds_write_b128 v209, v[148:151] offset:1024
	v_mul_f32_e32 v152, v52, v152
	v_mul_f32_e32 v153, v52, v153
	v_mul_f32_e32 v154, v52, v154
	v_mul_f32_e32 v155, v52, v155
	ds_write_b128 v209, v[152:155] offset:2048
	v_mul_f32_e32 v156, v53, v156
	v_mul_f32_e32 v157, v53, v157
	v_mul_f32_e32 v158, v53, v158
	v_mul_f32_e32 v159, v53, v159
	ds_write_b128 v209, v[156:159] offset:3072
	v_mul_f32_e32 v160, v54, v160
	v_mul_f32_e32 v161, v54, v161
	v_mul_f32_e32 v162, v54, v162
	v_mul_f32_e32 v163, v54, v163
	ds_write_b128 v209, v[160:163] offset:4096
	v_mul_f32_e32 v164, v55, v164
	v_mul_f32_e32 v165, v55, v165
	v_mul_f32_e32 v166, v55, v166
	v_mul_f32_e32 v167, v55, v167
	ds_write_b128 v209, v[164:167] offset:5120
	v_mul_f32_e32 v168, v56, v168
	v_mul_f32_e32 v169, v56, v169
	v_mul_f32_e32 v170, v56, v170
	v_mul_f32_e32 v171, v56, v171
	ds_write_b128 v209, v[168:171] offset:6144
	v_mul_f32_e32 v172, v57, v172
	v_mul_f32_e32 v173, v57, v173
	v_mul_f32_e32 v174, v57, v174
	v_mul_f32_e32 v175, v57, v175
	ds_write_b128 v209, v[172:175] offset:7168
	s_waitcnt lgkmcnt(0)
	s_barrier
; #define GAS __attribute__((address_space(1)))
; #define LAS __attribute__((address_space(3)))
; #define LDS_WAIT() asm volatile("s_waitcnt lgkmcnt(0)" ::: "memory")
;     const int pr = item >> 1, kb = 2 * (pr / nblk) + (item & 1), nb = pr % nblk, k0 = 64 * kb, n0 = 32 * nb;
;     const int nr = n0 + (lane & 31); const int sc = MAP == 1 ? src_col_in(nr) : nr;
;     float v[32];
; #pragma unroll
;     for (int i = 0; i < 32; ++i) v[i] = sc >= 0 ? W[(size_t)(k0 + 2 * i + (lane >> 5)) * Nsrc + sc] : 0.f;
; #pragma unroll
;     for (int i = 0; i < 32; ++i) { const int k = k0 + 2 * i + (lane >> 5); float x = v[i] * wscale; if (KS) x *= (k < ksplit ? ksA[k] : ksB[k - ksplit]); scr[(2 * i + (lane >> 5)) * 33 + (lane & 31)] = x; }
;     LDS_WAIT(); asm volatile("" ::: "memory");
;     const int c = lane & 7;
; #pragma unroll
;     for (int j = 0; j < 4; ++j) { const int n = (lane >> 3) + 8 * j; const LAS float* s = scr + (8 * c) * 33 + n;
;         const unsigned long long o = (unsigned long long)pg8::pk4_fp8(s[0 * 33], s[1 * 33], s[2 * 33], s[3 * 33]) | ((unsigned long long)pg8::pk4_fp8(s[4 * 33], s[5 * 33], s[6 * 33], s[7 * 33]) << 32);
;         *(GAS unsigned long long*)(WT + (size_t)(n0 + n) * K + k0 + 8 * c) = o; }
;     LDS_WAIT(); asm volatile("" ::: "memory");
; __global__ void __launch_bounds__(NWAVES * 64, 2) hybrid_fwd(Args args) {
;     ...
;             if (r < I_IN) { if (l >= PROJ_F8_FROM) p0_transpose_item_f8<true, 1>(args.in[2] + (size_t)l * DM * NSRC, DM, NSRC, NPROJ / 32, (unsigned char*)(ws + WS_WIN + l * SZ_WIN), WUP8_SCALE, args.in[1] + l * DM, args.in[1] + l * DM, DM, scr, r, lane);
	s_add_i32 s24, s23, 40
	s_lshl_b32 s20, s24, 7
	s_cmp_lt_u32 s24, 40
	s_cselect_b32 s21, 0, 0x830
	s_cmp_lt_u32 s24, 72
	s_cselect_b32 s21, s21, 0xfffff030
	s_add_i32 s20, s20, s21
	s_lshl_b32 s20, s20, 2
	s_add_u32 s8, s50, s20
	s_addc_u32 s9, s51, 0
	global_load_dwordx4 v[144:147], v76, s[8:9]
	s_add_u32 s8, s8, 0x16280
	s_addc_u32 s9, s9, 0
	global_load_dwordx4 v[148:151], v76, s[8:9]
	s_add_u32 s8, s8, 0x16280
	s_addc_u32 s9, s9, 0
	global_load_dwordx4 v[152:155], v76, s[8:9]
	s_add_u32 s8, s8, 0x16280
	s_addc_u32 s9, s9, 0
	global_load_dwordx4 v[156:159], v76, s[8:9]
	s_add_u32 s8, s8, 0x16280
	s_addc_u32 s9, s9, 0
	global_load_dwordx4 v[160:163], v76, s[8:9]
	s_add_u32 s8, s8, 0x16280
	s_addc_u32 s9, s9, 0
	global_load_dwordx4 v[164:167], v76, s[8:9]
	s_add_u32 s8, s8, 0x16280
	s_addc_u32 s9, s9, 0
	global_load_dwordx4 v[168:171], v76, s[8:9]
	s_add_u32 s8, s8, 0x16280
	s_addc_u32 s9, s9, 0
	global_load_dwordx4 v[172:175], v76, s[8:9]
	s_add_i32 s24, s23, 24
	s_mul_i32 s20, s24, 0x80000
	s_add_u32 s6, s52, s20
	s_addc_u32 s7, s53, 0
	s_cmp_lt_u32 s24, 16
	s_cselect_b32 s20, 1, 0
	s_sub_i32 s21, s24, 16
	s_bitcmp0_b32 s21, 2
	s_cselect_b32 s21, 1, 0
	s_cmp_lt_u32 s24, 40
	s_cselect_b32 s21, s21, 0
	s_or_b32 s20, s20, s21
	s_cmp_lg_u32 s20, 0
	s_cselect_b64 s[20:21], -1, 0
	v_cndmask_b32_e64 v91, v77, v81, s[20:21]
	v_cndmask_b32_e64 v92, v78, v82, s[20:21]
	ds_read_b32 v226, v211
	ds_read_b32 v227, v211 offset:512
	ds_read_b32 v228, v211 offset:1024
	ds_read_b32 v229, v211 offset:1536
	ds_read_b32 v230, v211 offset:2048
	ds_read_b32 v231, v211 offset:2560
	ds_read_b32 v232, v211 offset:3072
	ds_read_b32 v233, v211 offset:3584
	ds_read_b32 v234, v211 offset:4096
	ds_read_b32 v235, v211 offset:4608
	ds_read_b32 v236, v211 offset:5120
	ds_read_b32 v237, v211 offset:5632
	ds_read_b32 v238, v211 offset:6144
	ds_read_b32 v239, v211 offset:6656
	ds_read_b32 v240, v211 offset:7168
	ds_read_b32 v241, v211 offset:7680
	s_waitcnt lgkmcnt(0)
	v_max_f32_e32 v226, v226, v226
	v_max_f32_e32 v227, v227, v227
	v_max_f32_e32 v228, v228, v228
	v_max_f32_e32 v229, v229, v229
	v_max_f32_e32 v230, v230, v230
	v_max_f32_e32 v231, v231, v231
	v_max_f32_e32 v232, v232, v232
	v_max_f32_e32 v233, v233, v233
	v_max_f32_e32 v234, v234, v234
	v_max_f32_e32 v235, v235, v235
	v_max_f32_e32 v236, v236, v236
	v_max_f32_e32 v237, v237, v237
	v_max_f32_e32 v238, v238, v238
	v_max_f32_e32 v239, v239, v239
	v_max_f32_e32 v240, v240, v240
	v_max_f32_e32 v241, v241, v241
	v_med3_f32 v226, v226, s62, v95
	v_med3_f32 v227, v227, s62, v95
	v_med3_f32 v228, v228, s62, v95
	v_med3_f32 v229, v229, s62, v95
	v_med3_f32 v230, v230, s62, v95
	v_med3_f32 v231, v231, s62, v95
	v_med3_f32 v232, v232, s62, v95
	v_med3_f32 v233, v233, s62, v95
	v_med3_f32 v234, v234, s62, v95
	v_med3_f32 v235, v235, s62, v95
	v_med3_f32 v236, v236, s62, v95
	v_med3_f32 v237, v237, s62, v95
	v_med3_f32 v238, v238, s62, v95
	v_med3_f32 v239, v239, s62, v95
	v_med3_f32 v240, v240, s62, v95
	v_med3_f32 v241, v241, s62, v95
	v_mov_b32_e32 v242, 0
	v_mov_b32_e32 v243, 0
	v_mov_b32_e32 v244, 0
	v_mov_b32_e32 v245, 0
	v_cvt_pk_fp8_f32 v242, v226, v227
	v_cvt_pk_fp8_f32 v243, v230, v231
	v_cvt_pk_fp8_f32 v244, v234, v235
	v_cvt_pk_fp8_f32 v245, v238, v239
	v_cvt_pk_fp8_f32 v242, v228, v229 op_sel:[0,0,1]
	v_cvt_pk_fp8_f32 v243, v232, v233 op_sel:[0,0,1]
	v_cvt_pk_fp8_f32 v244, v236, v237 op_sel:[0,0,1]
	v_cvt_pk_fp8_f32 v245, v240, v241 op_sel:[0,0,1]
	s_nop 0
	global_store_dwordx4 v91, v[242:245], s[6:7]
	ds_read_b32 v226, v213
	ds_read_b32 v227, v213 offset:512
	ds_read_b32 v228, v213 offset:1024
	ds_read_b32 v229, v213 offset:1536
	ds_read_b32 v230, v213 offset:2048
	ds_read_b32 v231, v213 offset:2560
	ds_read_b32 v232, v213 offset:3072
	ds_read_b32 v233, v213 offset:3584
	ds_read_b32 v234, v213 offset:4096
	ds_read_b32 v235, v213 offset:4608
	ds_read_b32 v236, v213 offset:5120
	ds_read_b32 v237, v213 offset:5632
	ds_read_b32 v238, v213 offset:6144
	ds_read_b32 v239, v213 offset:6656
	ds_read_b32 v240, v213 offset:7168
	ds_read_b32 v241, v213 offset:7680
	s_waitcnt lgkmcnt(0)
	v_max_f32_e32 v226, v226, v226
	v_max_f32_e32 v227, v227, v227
	v_max_f32_e32 v228, v228, v228
	v_max_f32_e32 v229, v229, v229
	v_max_f32_e32 v230, v230, v230
	v_max_f32_e32 v231, v231, v231
	v_max_f32_e32 v232, v232, v232
	v_max_f32_e32 v233, v233, v233
	v_max_f32_e32 v234, v234, v234
	v_max_f32_e32 v235, v235, v235
	v_max_f32_e32 v236, v236, v236
	v_max_f32_e32 v237, v237, v237
	v_max_f32_e32 v238, v238, v238
	v_max_f32_e32 v239, v239, v239
	v_max_f32_e32 v240, v240, v240
	v_max_f32_e32 v241, v241, v241
	v_med3_f32 v226, v226, s62, v95
	v_med3_f32 v227, v227, s62, v95
	v_med3_f32 v228, v228, s62, v95
	v_med3_f32 v229, v229, s62, v95
	v_med3_f32 v230, v230, s62, v95
	v_med3_f32 v231, v231, s62, v95
	v_med3_f32 v232, v232, s62, v95
	v_med3_f32 v233, v233, s62, v95
	v_med3_f32 v234, v234, s62, v95
	v_med3_f32 v235, v235, s62, v95
	v_med3_f32 v236, v236, s62, v95
	v_med3_f32 v237, v237, s62, v95
	v_med3_f32 v238, v238, s62, v95
	v_med3_f32 v239, v239, s62, v95
	v_med3_f32 v240, v240, s62, v95
	v_med3_f32 v241, v241, s62, v95
	v_mov_b32_e32 v242, 0
	v_mov_b32_e32 v243, 0
	v_mov_b32_e32 v244, 0
	v_mov_b32_e32 v245, 0
	v_cvt_pk_fp8_f32 v242, v226, v227
	v_cvt_pk_fp8_f32 v243, v230, v231
	v_cvt_pk_fp8_f32 v244, v234, v235
	v_cvt_pk_fp8_f32 v245, v238, v239
	v_cvt_pk_fp8_f32 v242, v228, v229 op_sel:[0,0,1]
	v_cvt_pk_fp8_f32 v243, v232, v233 op_sel:[0,0,1]
	v_cvt_pk_fp8_f32 v244, v236, v237 op_sel:[0,0,1]
	v_cvt_pk_fp8_f32 v245, v240, v241 op_sel:[0,0,1]
	s_nop 0
	global_store_dwordx4 v92, v[242:245], s[6:7]
	s_waitcnt vmcnt(12)
	v_mul_f32_e32 v176, v50, v176
	v_mul_f32_e32 v177, v50, v177
	v_mul_f32_e32 v178, v50, v178
	v_mul_f32_e32 v179, v50, v179
	ds_write_b128 v210, v[176:179]
	v_mul_f32_e32 v180, v51, v180
	v_mul_f32_e32 v181, v51, v181
	v_mul_f32_e32 v182, v51, v182
	v_mul_f32_e32 v183, v51, v183
	ds_write_b128 v210, v[180:183] offset:1024
	v_mul_f32_e32 v184, v52, v184
	v_mul_f32_e32 v185, v52, v185
	v_mul_f32_e32 v186, v52, v186
	v_mul_f32_e32 v187, v52, v187
	ds_write_b128 v210, v[184:187] offset:2048
	v_mul_f32_e32 v188, v53, v188
	v_mul_f32_e32 v189, v53, v189
	v_mul_f32_e32 v190, v53, v190
	v_mul_f32_e32 v191, v53, v191
	ds_write_b128 v210, v[188:191] offset:3072
	v_mul_f32_e32 v192, v54, v192
	v_mul_f32_e32 v193, v54, v193
	v_mul_f32_e32 v194, v54, v194
	v_mul_f32_e32 v195, v54, v195
	ds_write_b128 v210, v[192:195] offset:4096
	v_mul_f32_e32 v196, v55, v196
	v_mul_f32_e32 v197, v55, v197
	v_mul_f32_e32 v198, v55, v198
	v_mul_f32_e32 v199, v55, v199
	ds_write_b128 v210, v[196:199] offset:5120
	v_mul_f32_e32 v200, v56, v200
	v_mul_f32_e32 v201, v56, v201
	v_mul_f32_e32 v202, v56, v202
	v_mul_f32_e32 v203, v56, v203
	ds_write_b128 v210, v[200:203] offset:6144
	v_mul_f32_e32 v204, v57, v204
	v_mul_f32_e32 v205, v57, v205
	v_mul_f32_e32 v206, v57, v206
	v_mul_f32_e32 v207, v57, v207
	ds_write_b128 v210, v[204:207] offset:7168
	s_waitcnt lgkmcnt(0)
	s_barrier
; #define GAS __attribute__((address_space(1)))
; #define LAS __attribute__((address_space(3)))
; #define LDS_WAIT() asm volatile("s_waitcnt lgkmcnt(0)" ::: "memory")
;     const int pr = item >> 1, kb = 2 * (pr / nblk) + (item & 1), nb = pr % nblk, k0 = 64 * kb, n0 = 32 * nb;
;     const int nr = n0 + (lane & 31); const int sc = MAP == 1 ? src_col_in(nr) : nr;
;     float v[32];
; #pragma unroll
;     for (int i = 0; i < 32; ++i) v[i] = sc >= 0 ? W[(size_t)(k0 + 2 * i + (lane >> 5)) * Nsrc + sc] : 0.f;
; #pragma unroll
;     for (int i = 0; i < 32; ++i) { const int k = k0 + 2 * i + (lane >> 5); float x = v[i] * wscale; if (KS) x *= (k < ksplit ? ksA[k] : ksB[k - ksplit]); scr[(2 * i + (lane >> 5)) * 33 + (lane & 31)] = x; }
;     LDS_WAIT(); asm volatile("" ::: "memory");
;     const int c = lane & 7;
; #pragma unroll
;     for (int j = 0; j < 4; ++j) { const int n = (lane >> 3) + 8 * j; const LAS float* s = scr + (8 * c) * 33 + n;
;         const unsigned long long o = (unsigned long long)pg8::pk4_fp8(s[0 * 33], s[1 * 33], s[2 * 33], s[3 * 33]) | ((unsigned long long)pg8::pk4_fp8(s[4 * 33], s[5 * 33], s[6 * 33], s[7 * 33]) << 32);
;         *(GAS unsigned long long*)(WT + (size_t)(n0 + n) * K + k0 + 8 * c) = o; }
;     LDS_WAIT(); asm volatile("" ::: "memory");
; __global__ void __launch_bounds__(NWAVES * 64, 2) hybrid_fwd(Args args) {
;     ...
;             if (r < I_IN) { if (l >= PROJ_F8_FROM) p0_transpose_item_f8<true, 1>(args.in[2] + (size_t)l * DM * NSRC, DM, NSRC, NPROJ / 32, (unsigned char*)(ws + WS_WIN + l * SZ_WIN), WUP8_SCALE, args.in[1] + l * DM, args.in[1] + l * DM, DM, scr, r, lane);
	s_add_i32 s24, s23, 48
	s_lshl_b32 s20, s24, 7
	s_cmp_lt_u32 s24, 40
	s_cselect_b32 s21, 0, 0x830
	s_cmp_lt_u32 s24, 72
	s_cselect_b32 s21, s21, 0xfffff030
	s_add_i32 s20, s20, s21
	s_lshl_b32 s20, s20, 2
	s_add_u32 s8, s50, s20
	s_addc_u32 s9, s51, 0
	global_load_dwordx4 v[176:179], v76, s[8:9]
	s_add_u32 s8, s8, 0x16280
	s_addc_u32 s9, s9, 0
	global_load_dwordx4 v[180:183], v76, s[8:9]
	s_add_u32 s8, s8, 0x16280
	s_addc_u32 s9, s9, 0
	global_load_dwordx4 v[184:187], v76, s[8:9]
	s_add_u32 s8, s8, 0x16280
	s_addc_u32 s9, s9, 0
	global_load_dwordx4 v[188:191], v76, s[8:9]
	s_add_u32 s8, s8, 0x16280
	s_addc_u32 s9, s9, 0
	global_load_dwordx4 v[192:195], v76, s[8:9]
	s_add_u32 s8, s8, 0x16280
	s_addc_u32 s9, s9, 0
	global_load_dwordx4 v[196:199], v76, s[8:9]
	s_add_u32 s8, s8, 0x16280
	s_addc_u32 s9, s9, 0
	global_load_dwordx4 v[200:203], v76, s[8:9]
	s_add_u32 s8, s8, 0x16280
	s_addc_u32 s9, s9, 0
	global_load_dwordx4 v[204:207], v76, s[8:9]
	s_add_i32 s24, s23, 32
	s_mul_i32 s20, s24, 0x80000
	s_add_u32 s6, s52, s20
	s_addc_u32 s7, s53, 0
	s_cmp_lt_u32 s24, 16
	s_cselect_b32 s20, 1, 0
	s_sub_i32 s21, s24, 16
	s_bitcmp0_b32 s21, 2
	s_cselect_b32 s21, 1, 0
	s_cmp_lt_u32 s24, 40
	s_cselect_b32 s21, s21, 0
	s_or_b32 s20, s20, s21
	s_cmp_lg_u32 s20, 0
	s_cselect_b64 s[20:21], -1, 0
	v_cndmask_b32_e64 v91, v77, v81, s[20:21]
	v_cndmask_b32_e64 v92, v78, v82, s[20:21]
	ds_read_b32 v226, v212
	ds_read_b32 v227, v212 offset:512
	ds_read_b32 v228, v212 offset:1024
	ds_read_b32 v229, v212 offset:1536
	ds_read_b32 v230, v212 offset:2048
	ds_read_b32 v231, v212 offset:2560
	ds_read_b32 v232, v212 offset:3072
	ds_read_b32 v233, v212 offset:3584
	ds_read_b32 v234, v212 offset:4096
	ds_read_b32 v235, v212 offset:4608
	ds_read_b32 v236, v212 offset:5120
	ds_read_b32 v237, v212 offset:5632
	ds_read_b32 v238, v212 offset:6144
	ds_read_b32 v239, v212 offset:6656
	ds_read_b32 v240, v212 offset:7168
	ds_read_b32 v241, v212 offset:7680
	s_waitcnt lgkmcnt(0)
	v_max_f32_e32 v226, v226, v226
	v_max_f32_e32 v227, v227, v227
	v_max_f32_e32 v228, v228, v228
	v_max_f32_e32 v229, v229, v229
	v_max_f32_e32 v230, v230, v230
	v_max_f32_e32 v231, v231, v231
	v_max_f32_e32 v232, v232, v232
	v_max_f32_e32 v233, v233, v233
	v_max_f32_e32 v234, v234, v234
	v_max_f32_e32 v235, v235, v235
	v_max_f32_e32 v236, v236, v236
	v_max_f32_e32 v237, v237, v237
	v_max_f32_e32 v238, v238, v238
	v_max_f32_e32 v239, v239, v239
	v_max_f32_e32 v240, v240, v240
	v_max_f32_e32 v241, v241, v241
	v_med3_f32 v226, v226, s62, v95
	v_med3_f32 v227, v227, s62, v95
	v_med3_f32 v228, v228, s62, v95
	v_med3_f32 v229, v229, s62, v95
	v_med3_f32 v230, v230, s62, v95
	v_med3_f32 v231, v231, s62, v95
	v_med3_f32 v232, v232, s62, v95
	v_med3_f32 v233, v233, s62, v95
	v_med3_f32 v234, v234, s62, v95
	v_med3_f32 v235, v235, s62, v95
	v_med3_f32 v236, v236, s62, v95
	v_med3_f32 v237, v237, s62, v95
	v_med3_f32 v238, v238, s62, v95
	v_med3_f32 v239, v239, s62, v95
	v_med3_f32 v240, v240, s62, v95
	v_med3_f32 v241, v241, s62, v95
	v_mov_b32_e32 v242, 0
	v_mov_b32_e32 v243, 0
	v_mov_b32_e32 v244, 0
	v_mov_b32_e32 v245, 0
	v_cvt_pk_fp8_f32 v242, v226, v227
	v_cvt_pk_fp8_f32 v243, v230, v231
	v_cvt_pk_fp8_f32 v244, v234, v235
	v_cvt_pk_fp8_f32 v245, v238, v239
	v_cvt_pk_fp8_f32 v242, v228, v229 op_sel:[0,0,1]
	v_cvt_pk_fp8_f32 v243, v232, v233 op_sel:[0,0,1]
	v_cvt_pk_fp8_f32 v244, v236, v237 op_sel:[0,0,1]
	v_cvt_pk_fp8_f32 v245, v240, v241 op_sel:[0,0,1]
	s_nop 0
	global_store_dwordx4 v91, v[242:245], s[6:7]
	ds_read_b32 v226, v214
	ds_read_b32 v227, v214 offset:512
	ds_read_b32 v228, v214 offset:1024
	ds_read_b32 v229, v214 offset:1536
	ds_read_b32 v230, v214 offset:2048
	ds_read_b32 v231, v214 offset:2560
	ds_read_b32 v232, v214 offset:3072
	ds_read_b32 v233, v214 offset:3584
	ds_read_b32 v234, v214 offset:4096
	ds_read_b32 v235, v214 offset:4608
	ds_read_b32 v236, v214 offset:5120
	ds_read_b32 v237, v214 offset:5632
	ds_read_b32 v238, v214 offset:6144
	ds_read_b32 v239, v214 offset:6656
	ds_read_b32 v240, v214 offset:7168
	ds_read_b32 v241, v214 offset:7680
	s_waitcnt lgkmcnt(0)
	v_max_f32_e32 v226, v226, v226
	v_max_f32_e32 v227, v227, v227
	v_max_f32_e32 v228, v228, v228
	v_max_f32_e32 v229, v229, v229
	v_max_f32_e32 v230, v230, v230
	v_max_f32_e32 v231, v231, v231
	v_max_f32_e32 v232, v232, v232
	v_max_f32_e32 v233, v233, v233
	v_max_f32_e32 v234, v234, v234
	v_max_f32_e32 v235, v235, v235
	v_max_f32_e32 v236, v236, v236
	v_max_f32_e32 v237, v237, v237
	v_max_f32_e32 v238, v238, v238
	v_max_f32_e32 v239, v239, v239
	v_max_f32_e32 v240, v240, v240
	v_max_f32_e32 v241, v241, v241
	v_med3_f32 v226, v226, s62, v95
	v_med3_f32 v227, v227, s62, v95
	v_med3_f32 v228, v228, s62, v95
	v_med3_f32 v229, v229, s62, v95
	v_med3_f32 v230, v230, s62, v95
	v_med3_f32 v231, v231, s62, v95
	v_med3_f32 v232, v232, s62, v95
	v_med3_f32 v233, v233, s62, v95
	v_med3_f32 v234, v234, s62, v95
	v_med3_f32 v235, v235, s62, v95
	v_med3_f32 v236, v236, s62, v95
	v_med3_f32 v237, v237, s62, v95
	v_med3_f32 v238, v238, s62, v95
	v_med3_f32 v239, v239, s62, v95
	v_med3_f32 v240, v240, s62, v95
	v_med3_f32 v241, v241, s62, v95
	v_mov_b32_e32 v242, 0
	v_mov_b32_e32 v243, 0
	v_mov_b32_e32 v244, 0
	v_mov_b32_e32 v245, 0
	v_cvt_pk_fp8_f32 v242, v226, v227
	v_cvt_pk_fp8_f32 v243, v230, v231
	v_cvt_pk_fp8_f32 v244, v234, v235
	v_cvt_pk_fp8_f32 v245, v238, v239
	v_cvt_pk_fp8_f32 v242, v228, v229 op_sel:[0,0,1]
	v_cvt_pk_fp8_f32 v243, v232, v233 op_sel:[0,0,1]
	v_cvt_pk_fp8_f32 v244, v236, v237 op_sel:[0,0,1]
	v_cvt_pk_fp8_f32 v245, v240, v241 op_sel:[0,0,1]
	s_nop 0
	global_store_dwordx4 v92, v[242:245], s[6:7]
	s_waitcnt vmcnt(12)
	v_mul_f32_e32 v144, v50, v144
	v_mul_f32_e32 v145, v50, v145
	v_mul_f32_e32 v146, v50, v146
	v_mul_f32_e32 v147, v50, v147
	ds_write_b128 v209, v[144:147]
	v_mul_f32_e32 v148, v51, v148
	v_mul_f32_e32 v149, v51, v149
	v_mul_f32_e32 v150, v51, v150
	v_mul_f32_e32 v151, v51, v151
	ds_write_b128 v209, v[148:151] offset:1024
	v_mul_f32_e32 v152, v52, v152
	v_mul_f32_e32 v153, v52, v153
	v_mul_f32_e32 v154, v52, v154
	v_mul_f32_e32 v155, v52, v155
	ds_write_b128 v209, v[152:155] offset:2048
	v_mul_f32_e32 v156, v53, v156
	v_mul_f32_e32 v157, v53, v157
	v_mul_f32_e32 v158, v53, v158
	v_mul_f32_e32 v159, v53, v159
	ds_write_b128 v209, v[156:159] offset:3072
	v_mul_f32_e32 v160, v54, v160
	v_mul_f32_e32 v161, v54, v161
	v_mul_f32_e32 v162, v54, v162
	v_mul_f32_e32 v163, v54, v163
	ds_write_b128 v209, v[160:163] offset:4096
	v_mul_f32_e32 v164, v55, v164
	v_mul_f32_e32 v165, v55, v165
	v_mul_f32_e32 v166, v55, v166
	v_mul_f32_e32 v167, v55, v167
	ds_write_b128 v209, v[164:167] offset:5120
	v_mul_f32_e32 v168, v56, v168
	v_mul_f32_e32 v169, v56, v169
	v_mul_f32_e32 v170, v56, v170
	v_mul_f32_e32 v171, v56, v171
	ds_write_b128 v209, v[168:171] offset:6144
	v_mul_f32_e32 v172, v57, v172
	v_mul_f32_e32 v173, v57, v173
	v_mul_f32_e32 v174, v57, v174
	v_mul_f32_e32 v175, v57, v175
	ds_write_b128 v209, v[172:175] offset:7168
	s_waitcnt lgkmcnt(0)
	s_barrier
; #define GAS __attribute__((address_space(1)))
; #define LAS __attribute__((address_space(3)))
; #define LDS_WAIT() asm volatile("s_waitcnt lgkmcnt(0)" ::: "memory")
;     const int pr = item >> 1, kb = 2 * (pr / nblk) + (item & 1), nb = pr % nblk, k0 = 64 * kb, n0 = 32 * nb;
;     const int nr = n0 + (lane & 31); const int sc = MAP == 1 ? src_col_in(nr) : nr;
;     float v[32];
; #pragma unroll
;     for (int i = 0; i < 32; ++i) v[i] = sc >= 0 ? W[(size_t)(k0 + 2 * i + (lane >> 5)) * Nsrc + sc] : 0.f;
; #pragma unroll
;     for (int i = 0; i < 32; ++i) { const int k = k0 + 2 * i + (lane >> 5); float x = v[i] * wscale; if (KS) x *= (k < ksplit ? ksA[k] : ksB[k - ksplit]); scr[(2 * i + (lane >> 5)) * 33 + (lane & 31)] = x; }
;     LDS_WAIT(); asm volatile("" ::: "memory");
;     const int c = lane & 7;
; #pragma unroll
;     for (int j = 0; j < 4; ++j) { const int n = (lane >> 3) + 8 * j; const LAS float* s = scr + (8 * c) * 33 + n;
;         const unsigned long long o = (unsigned long long)pg8::pk4_fp8(s[0 * 33], s[1 * 33], s[2 * 33], s[3 * 33]) | ((unsigned long long)pg8::pk4_fp8(s[4 * 33], s[5 * 33], s[6 * 33], s[7 * 33]) << 32);
;         *(GAS unsigned long long*)(WT + (size_t)(n0 + n) * K + k0 + 8 * c) = o; }
;     LDS_WAIT(); asm volatile("" ::: "memory");
; __global__ void __launch_bounds__(NWAVES * 64, 2) hybrid_fwd(Args args) {
;     ...
;             if (r < I_IN) { if (l >= PROJ_F8_FROM) p0_transpose_item_f8<true, 1>(args.in[2] + (size_t)l * DM * NSRC, DM, NSRC, NPROJ / 32, (unsigned char*)(ws + WS_WIN + l * SZ_WIN), WUP8_SCALE, args.in[1] + l * DM, args.in[1] + l * DM, DM, scr, r, lane);
	s_add_i32 s24, s23, 56
	s_lshl_b32 s20, s24, 7
	s_cmp_lt_u32 s24, 40
	s_cselect_b32 s21, 0, 0x830
	s_cmp_lt_u32 s24, 72
	s_cselect_b32 s21, s21, 0xfffff030
	s_add_i32 s20, s20, s21
	s_lshl_b32 s20, s20, 2
	s_add_u32 s8, s50, s20
	s_addc_u32 s9, s51, 0
	global_load_dwordx4 v[144:147], v76, s[8:9]
	s_add_u32 s8, s8, 0x16280
	s_addc_u32 s9, s9, 0
	global_load_dwordx4 v[148:151], v76, s[8:9]
	s_add_u32 s8, s8, 0x16280
	s_addc_u32 s9, s9, 0
	global_load_dwordx4 v[152:155], v76, s[8:9]
	s_add_u32 s8, s8, 0x16280
	s_addc_u32 s9, s9, 0
	global_load_dwordx4 v[156:159], v76, s[8:9]
	s_add_u32 s8, s8, 0x16280
	s_addc_u32 s9, s9, 0
	global_load_dwordx4 v[160:163], v76, s[8:9]
	s_add_u32 s8, s8, 0x16280
	s_addc_u32 s9, s9, 0
	global_load_dwordx4 v[164:167], v76, s[8:9]
	s_add_u32 s8, s8, 0x16280
	s_addc_u32 s9, s9, 0
	global_load_dwordx4 v[168:171], v76, s[8:9]
	s_add_u32 s8, s8, 0x16280
	s_addc_u32 s9, s9, 0
	global_load_dwordx4 v[172:175], v76, s[8:9]
	s_add_i32 s24, s23, 40
	s_mul_i32 s20, s24, 0x80000
	s_add_u32 s6, s52, s20
	s_addc_u32 s7, s53, 0
	s_cmp_lt_u32 s24, 16
	s_cselect_b32 s20, 1, 0
	s_sub_i32 s21, s24, 16
	s_bitcmp0_b32 s21, 2
	s_cselect_b32 s21, 1, 0
	s_cmp_lt_u32 s24, 40
	s_cselect_b32 s21, s21, 0
	s_or_b32 s20, s20, s21
	s_cmp_lg_u32 s20, 0
	s_cselect_b64 s[20:21], -1, 0
	v_cndmask_b32_e64 v91, v77, v81, s[20:21]
	v_cndmask_b32_e64 v92, v78, v82, s[20:21]
	ds_read_b32 v226, v211
	ds_read_b32 v227, v211 offset:512
	ds_read_b32 v228, v211 offset:1024
	ds_read_b32 v229, v211 offset:1536
	ds_read_b32 v230, v211 offset:2048
	ds_read_b32 v231, v211 offset:2560
	ds_read_b32 v232, v211 offset:3072
	ds_read_b32 v233, v211 offset:3584
	ds_read_b32 v234, v211 offset:4096
	ds_read_b32 v235, v211 offset:4608
	ds_read_b32 v236, v211 offset:5120
	ds_read_b32 v237, v211 offset:5632
	ds_read_b32 v238, v211 offset:6144
	ds_read_b32 v239, v211 offset:6656
	ds_read_b32 v240, v211 offset:7168
	ds_read_b32 v241, v211 offset:7680
	s_waitcnt lgkmcnt(0)
	v_max_f32_e32 v226, v226, v226
	v_max_f32_e32 v227, v227, v227
	v_max_f32_e32 v228, v228, v228
	v_max_f32_e32 v229, v229, v229
	v_max_f32_e32 v230, v230, v230
	v_max_f32_e32 v231, v231, v231
	v_max_f32_e32 v232, v232, v232
	v_max_f32_e32 v233, v233, v233
	v_max_f32_e32 v234, v234, v234
	v_max_f32_e32 v235, v235, v235
	v_max_f32_e32 v236, v236, v236
	v_max_f32_e32 v237, v237, v237
	v_max_f32_e32 v238, v238, v238
	v_max_f32_e32 v239, v239, v239
	v_max_f32_e32 v240, v240, v240
	v_max_f32_e32 v241, v241, v241
	v_med3_f32 v226, v226, s62, v95
	v_med3_f32 v227, v227, s62, v95
	v_med3_f32 v228, v228, s62, v95
	v_med3_f32 v229, v229, s62, v95
	v_med3_f32 v230, v230, s62, v95
	v_med3_f32 v231, v231, s62, v95
	v_med3_f32 v232, v232, s62, v95
	v_med3_f32 v233, v233, s62, v95
	v_med3_f32 v234, v234, s62, v95
	v_med3_f32 v235, v235, s62, v95
	v_med3_f32 v236, v236, s62, v95
	v_med3_f32 v237, v237, s62, v95
	v_med3_f32 v238, v238, s62, v95
	v_med3_f32 v239, v239, s62, v95
	v_med3_f32 v240, v240, s62, v95
	v_med3_f32 v241, v241, s62, v95
	v_mov_b32_e32 v242, 0
	v_mov_b32_e32 v243, 0
	v_mov_b32_e32 v244, 0
	v_mov_b32_e32 v245, 0
	v_cvt_pk_fp8_f32 v242, v226, v227
	v_cvt_pk_fp8_f32 v243, v230, v231
	v_cvt_pk_fp8_f32 v244, v234, v235
	v_cvt_pk_fp8_f32 v245, v238, v239
	v_cvt_pk_fp8_f32 v242, v228, v229 op_sel:[0,0,1]
	v_cvt_pk_fp8_f32 v243, v232, v233 op_sel:[0,0,1]
	v_cvt_pk_fp8_f32 v244, v236, v237 op_sel:[0,0,1]
	v_cvt_pk_fp8_f32 v245, v240, v241 op_sel:[0,0,1]
	s_nop 0
	global_store_dwordx4 v91, v[242:245], s[6:7]
	ds_read_b32 v226, v213
	ds_read_b32 v227, v213 offset:512
	ds_read_b32 v228, v213 offset:1024
	ds_read_b32 v229, v213 offset:1536
	ds_read_b32 v230, v213 offset:2048
	ds_read_b32 v231, v213 offset:2560
	ds_read_b32 v232, v213 offset:3072
	ds_read_b32 v233, v213 offset:3584
	ds_read_b32 v234, v213 offset:4096
	ds_read_b32 v235, v213 offset:4608
	ds_read_b32 v236, v213 offset:5120
	ds_read_b32 v237, v213 offset:5632
	ds_read_b32 v238, v213 offset:6144
	ds_read_b32 v239, v213 offset:6656
	ds_read_b32 v240, v213 offset:7168
	ds_read_b32 v241, v213 offset:7680
	s_waitcnt lgkmcnt(0)
	v_max_f32_e32 v226, v226, v226
	v_max_f32_e32 v227, v227, v227
	v_max_f32_e32 v228, v228, v228
	v_max_f32_e32 v229, v229, v229
	v_max_f32_e32 v230, v230, v230
	v_max_f32_e32 v231, v231, v231
	v_max_f32_e32 v232, v232, v232
	v_max_f32_e32 v233, v233, v233
	v_max_f32_e32 v234, v234, v234
	v_max_f32_e32 v235, v235, v235
	v_max_f32_e32 v236, v236, v236
	v_max_f32_e32 v237, v237, v237
	v_max_f32_e32 v238, v238, v238
	v_max_f32_e32 v239, v239, v239
	v_max_f32_e32 v240, v240, v240
	v_max_f32_e32 v241, v241, v241
	v_med3_f32 v226, v226, s62, v95
	v_med3_f32 v227, v227, s62, v95
	v_med3_f32 v228, v228, s62, v95
	v_med3_f32 v229, v229, s62, v95
	v_med3_f32 v230, v230, s62, v95
	v_med3_f32 v231, v231, s62, v95
	v_med3_f32 v232, v232, s62, v95
	v_med3_f32 v233, v233, s62, v95
	v_med3_f32 v234, v234, s62, v95
	v_med3_f32 v235, v235, s62, v95
	v_med3_f32 v236, v236, s62, v95
	v_med3_f32 v237, v237, s62, v95
	v_med3_f32 v238, v238, s62, v95
	v_med3_f32 v239, v239, s62, v95
	v_med3_f32 v240, v240, s62, v95
	v_med3_f32 v241, v241, s62, v95
	v_mov_b32_e32 v242, 0
	v_mov_b32_e32 v243, 0
	v_mov_b32_e32 v244, 0
	v_mov_b32_e32 v245, 0
	v_cvt_pk_fp8_f32 v242, v226, v227
	v_cvt_pk_fp8_f32 v243, v230, v231
	v_cvt_pk_fp8_f32 v244, v234, v235
	v_cvt_pk_fp8_f32 v245, v238, v239
	v_cvt_pk_fp8_f32 v242, v228, v229 op_sel:[0,0,1]
	v_cvt_pk_fp8_f32 v243, v232, v233 op_sel:[0,0,1]
	v_cvt_pk_fp8_f32 v244, v236, v237 op_sel:[0,0,1]
	v_cvt_pk_fp8_f32 v245, v240, v241 op_sel:[0,0,1]
	s_nop 0
	global_store_dwordx4 v92, v[242:245], s[6:7]
	s_waitcnt vmcnt(12)
	v_mul_f32_e32 v176, v50, v176
	v_mul_f32_e32 v177, v50, v177
	v_mul_f32_e32 v178, v50, v178
	v_mul_f32_e32 v179, v50, v179
	ds_write_b128 v210, v[176:179]
	v_mul_f32_e32 v180, v51, v180
	v_mul_f32_e32 v181, v51, v181
	v_mul_f32_e32 v182, v51, v182
	v_mul_f32_e32 v183, v51, v183
	ds_write_b128 v210, v[180:183] offset:1024
	v_mul_f32_e32 v184, v52, v184
	v_mul_f32_e32 v185, v52, v185
	v_mul_f32_e32 v186, v52, v186
	v_mul_f32_e32 v187, v52, v187
	ds_write_b128 v210, v[184:187] offset:2048
	v_mul_f32_e32 v188, v53, v188
	v_mul_f32_e32 v189, v53, v189
	v_mul_f32_e32 v190, v53, v190
	v_mul_f32_e32 v191, v53, v191
	ds_write_b128 v210, v[188:191] offset:3072
	v_mul_f32_e32 v192, v54, v192
	v_mul_f32_e32 v193, v54, v193
	v_mul_f32_e32 v194, v54, v194
	v_mul_f32_e32 v195, v54, v195
	ds_write_b128 v210, v[192:195] offset:4096
	v_mul_f32_e32 v196, v55, v196
	v_mul_f32_e32 v197, v55, v197
	v_mul_f32_e32 v198, v55, v198
	v_mul_f32_e32 v199, v55, v199
	ds_write_b128 v210, v[196:199] offset:5120
	v_mul_f32_e32 v200, v56, v200
	v_mul_f32_e32 v201, v56, v201
	v_mul_f32_e32 v202, v56, v202
	v_mul_f32_e32 v203, v56, v203
	ds_write_b128 v210, v[200:203] offset:6144
	v_mul_f32_e32 v204, v57, v204
	v_mul_f32_e32 v205, v57, v205
	v_mul_f32_e32 v206, v57, v206
	v_mul_f32_e32 v207, v57, v207
	ds_write_b128 v210, v[204:207] offset:7168
	s_waitcnt lgkmcnt(0)
	s_barrier
; #define GAS __attribute__((address_space(1)))
; #define LAS __attribute__((address_space(3)))
; #define LDS_WAIT() asm volatile("s_waitcnt lgkmcnt(0)" ::: "memory")
;     const int pr = item >> 1, kb = 2 * (pr / nblk) + (item & 1), nb = pr % nblk, k0 = 64 * kb, n0 = 32 * nb;
;     const int nr = n0 + (lane & 31); const int sc = MAP == 1 ? src_col_in(nr) : nr;
;     float v[32];
; #pragma unroll
;     for (int i = 0; i < 32; ++i) v[i] = sc >= 0 ? W[(size_t)(k0 + 2 * i + (lane >> 5)) * Nsrc + sc] : 0.f;
; #pragma unroll
;     for (int i = 0; i < 32; ++i) { const int k = k0 + 2 * i + (lane >> 5); float x = v[i] * wscale; if (KS) x *= (k < ksplit ? ksA[k] : ksB[k - ksplit]); scr[(2 * i + (lane >> 5)) * 33 + (lane & 31)] = x; }
;     LDS_WAIT(); asm volatile("" ::: "memory");
;     const int c = lane & 7;
; #pragma unroll
;     for (int j = 0; j < 4; ++j) { const int n = (lane >> 3) + 8 * j; const LAS float* s = scr + (8 * c) * 33 + n;
;         const unsigned long long o = (unsigned long long)pg8::pk4_fp8(s[0 * 33], s[1 * 33], s[2 * 33], s[3 * 33]) | ((unsigned long long)pg8::pk4_fp8(s[4 * 33], s[5 * 33], s[6 * 33], s[7 * 33]) << 32);
;         *(GAS unsigned long long*)(WT + (size_t)(n0 + n) * K + k0 + 8 * c) = o; }
;     LDS_WAIT(); asm volatile("" ::: "memory");
; __global__ void __launch_bounds__(NWAVES * 64, 2) hybrid_fwd(Args args) {
;     ...
;             if (r < I_IN) { if (l >= PROJ_F8_FROM) p0_transpose_item_f8<true, 1>(args.in[2] + (size_t)l * DM * NSRC, DM, NSRC, NPROJ / 32, (unsigned char*)(ws + WS_WIN + l * SZ_WIN), WUP8_SCALE, args.in[1] + l * DM, args.in[1] + l * DM, DM, scr, r, lane);
	s_add_i32 s24, s23, 64
	s_lshl_b32 s20, s24, 7
	s_cmp_lt_u32 s24, 40
	s_cselect_b32 s21, 0, 0x830
	s_cmp_lt_u32 s24, 72
	s_cselect_b32 s21, s21, 0xfffff030
	s_add_i32 s20, s20, s21
	s_lshl_b32 s20, s20, 2
	s_add_u32 s8, s50, s20
	s_addc_u32 s9, s51, 0
	global_load_dwordx4 v[176:179], v76, s[8:9]
	s_add_u32 s8, s8, 0x16280
	s_addc_u32 s9, s9, 0
	global_load_dwordx4 v[180:183], v76, s[8:9]
	s_add_u32 s8, s8, 0x16280
	s_addc_u32 s9, s9, 0
	global_load_dwordx4 v[184:187], v76, s[8:9]
	s_add_u32 s8, s8, 0x16280
	s_addc_u32 s9, s9, 0
	global_load_dwordx4 v[188:191], v76, s[8:9]
	s_add_u32 s8, s8, 0x16280
	s_addc_u32 s9, s9, 0
	global_load_dwordx4 v[192:195], v76, s[8:9]
	s_add_u32 s8, s8, 0x16280
	s_addc_u32 s9, s9, 0
	global_load_dwordx4 v[196:199], v76, s[8:9]
	s_add_u32 s8, s8, 0x16280
	s_addc_u32 s9, s9, 0
	global_load_dwordx4 v[200:203], v76, s[8:9]
	s_add_u32 s8, s8, 0x16280
	s_addc_u32 s9, s9, 0
	global_load_dwordx4 v[204:207], v76, s[8:9]
	s_add_i32 s24, s23, 48
	s_mul_i32 s20, s24, 0x80000
	s_add_u32 s6, s52, s20
	s_addc_u32 s7, s53, 0
	s_cmp_lt_u32 s24, 16
	s_cselect_b32 s20, 1, 0
	s_sub_i32 s21, s24, 16
	s_bitcmp0_b32 s21, 2
	s_cselect_b32 s21, 1, 0
	s_cmp_lt_u32 s24, 40
	s_cselect_b32 s21, s21, 0
	s_or_b32 s20, s20, s21
	s_cmp_lg_u32 s20, 0
	s_cselect_b64 s[20:21], -1, 0
	v_cndmask_b32_e64 v91, v77, v81, s[20:21]
	v_cndmask_b32_e64 v92, v78, v82, s[20:21]
	ds_read_b32 v226, v212
	ds_read_b32 v227, v212 offset:512
	ds_read_b32 v228, v212 offset:1024
	ds_read_b32 v229, v212 offset:1536
	ds_read_b32 v230, v212 offset:2048
	ds_read_b32 v231, v212 offset:2560
	ds_read_b32 v232, v212 offset:3072
	ds_read_b32 v233, v212 offset:3584
	ds_read_b32 v234, v212 offset:4096
	ds_read_b32 v235, v212 offset:4608
	ds_read_b32 v236, v212 offset:5120
	ds_read_b32 v237, v212 offset:5632
	ds_read_b32 v238, v212 offset:6144
	ds_read_b32 v239, v212 offset:6656
	ds_read_b32 v240, v212 offset:7168
	ds_read_b32 v241, v212 offset:7680
	s_waitcnt lgkmcnt(0)
	v_max_f32_e32 v226, v226, v226
	v_max_f32_e32 v227, v227, v227
	v_max_f32_e32 v228, v228, v228
	v_max_f32_e32 v229, v229, v229
	v_max_f32_e32 v230, v230, v230
	v_max_f32_e32 v231, v231, v231
	v_max_f32_e32 v232, v232, v232
	v_max_f32_e32 v233, v233, v233
	v_max_f32_e32 v234, v234, v234
	v_max_f32_e32 v235, v235, v235
	v_max_f32_e32 v236, v236, v236
	v_max_f32_e32 v237, v237, v237
	v_max_f32_e32 v238, v238, v238
	v_max_f32_e32 v239, v239, v239
	v_max_f32_e32 v240, v240, v240
	v_max_f32_e32 v241, v241, v241
	v_med3_f32 v226, v226, s62, v95
	v_med3_f32 v227, v227, s62, v95
	v_med3_f32 v228, v228, s62, v95
	v_med3_f32 v229, v229, s62, v95
	v_med3_f32 v230, v230, s62, v95
	v_med3_f32 v231, v231, s62, v95
	v_med3_f32 v232, v232, s62, v95
	v_med3_f32 v233, v233, s62, v95
	v_med3_f32 v234, v234, s62, v95
	v_med3_f32 v235, v235, s62, v95
	v_med3_f32 v236, v236, s62, v95
	v_med3_f32 v237, v237, s62, v95
	v_med3_f32 v238, v238, s62, v95
	v_med3_f32 v239, v239, s62, v95
	v_med3_f32 v240, v240, s62, v95
	v_med3_f32 v241, v241, s62, v95
	v_mov_b32_e32 v242, 0
	v_mov_b32_e32 v243, 0
	v_mov_b32_e32 v244, 0
	v_mov_b32_e32 v245, 0
	v_cvt_pk_fp8_f32 v242, v226, v227
	v_cvt_pk_fp8_f32 v243, v230, v231
	v_cvt_pk_fp8_f32 v244, v234, v235
	v_cvt_pk_fp8_f32 v245, v238, v239
	v_cvt_pk_fp8_f32 v242, v228, v229 op_sel:[0,0,1]
	v_cvt_pk_fp8_f32 v243, v232, v233 op_sel:[0,0,1]
	v_cvt_pk_fp8_f32 v244, v236, v237 op_sel:[0,0,1]
	v_cvt_pk_fp8_f32 v245, v240, v241 op_sel:[0,0,1]
	s_nop 0
	global_store_dwordx4 v91, v[242:245], s[6:7]
	ds_read_b32 v226, v214
	ds_read_b32 v227, v214 offset:512
	ds_read_b32 v228, v214 offset:1024
	ds_read_b32 v229, v214 offset:1536
	ds_read_b32 v230, v214 offset:2048
	ds_read_b32 v231, v214 offset:2560
	ds_read_b32 v232, v214 offset:3072
	ds_read_b32 v233, v214 offset:3584
	ds_read_b32 v234, v214 offset:4096
	ds_read_b32 v235, v214 offset:4608
	ds_read_b32 v236, v214 offset:5120
	ds_read_b32 v237, v214 offset:5632
	ds_read_b32 v238, v214 offset:6144
	ds_read_b32 v239, v214 offset:6656
	ds_read_b32 v240, v214 offset:7168
	ds_read_b32 v241, v214 offset:7680
	s_waitcnt lgkmcnt(0)
	v_max_f32_e32 v226, v226, v226
	v_max_f32_e32 v227, v227, v227
	v_max_f32_e32 v228, v228, v228
	v_max_f32_e32 v229, v229, v229
	v_max_f32_e32 v230, v230, v230
	v_max_f32_e32 v231, v231, v231
	v_max_f32_e32 v232, v232, v232
	v_max_f32_e32 v233, v233, v233
	v_max_f32_e32 v234, v234, v234
	v_max_f32_e32 v235, v235, v235
	v_max_f32_e32 v236, v236, v236
	v_max_f32_e32 v237, v237, v237
	v_max_f32_e32 v238, v238, v238
	v_max_f32_e32 v239, v239, v239
	v_max_f32_e32 v240, v240, v240
	v_max_f32_e32 v241, v241, v241
	v_med3_f32 v226, v226, s62, v95
	v_med3_f32 v227, v227, s62, v95
	v_med3_f32 v228, v228, s62, v95
	v_med3_f32 v229, v229, s62, v95
	v_med3_f32 v230, v230, s62, v95
	v_med3_f32 v231, v231, s62, v95
	v_med3_f32 v232, v232, s62, v95
	v_med3_f32 v233, v233, s62, v95
	v_med3_f32 v234, v234, s62, v95
	v_med3_f32 v235, v235, s62, v95
	v_med3_f32 v236, v236, s62, v95
	v_med3_f32 v237, v237, s62, v95
	v_med3_f32 v238, v238, s62, v95
	v_med3_f32 v239, v239, s62, v95
	v_med3_f32 v240, v240, s62, v95
	v_med3_f32 v241, v241, s62, v95
	v_mov_b32_e32 v242, 0
	v_mov_b32_e32 v243, 0
	v_mov_b32_e32 v244, 0
	v_mov_b32_e32 v245, 0
	v_cvt_pk_fp8_f32 v242, v226, v227
	v_cvt_pk_fp8_f32 v243, v230, v231
	v_cvt_pk_fp8_f32 v244, v234, v235
	v_cvt_pk_fp8_f32 v245, v238, v239
	v_cvt_pk_fp8_f32 v242, v228, v229 op_sel:[0,0,1]
	v_cvt_pk_fp8_f32 v243, v232, v233 op_sel:[0,0,1]
	v_cvt_pk_fp8_f32 v244, v236, v237 op_sel:[0,0,1]
	v_cvt_pk_fp8_f32 v245, v240, v241 op_sel:[0,0,1]
	s_nop 0
	global_store_dwordx4 v92, v[242:245], s[6:7]
	s_waitcnt vmcnt(12)
	v_mul_f32_e32 v144, v50, v144
	v_mul_f32_e32 v145, v50, v145
	v_mul_f32_e32 v146, v50, v146
	v_mul_f32_e32 v147, v50, v147
	ds_write_b128 v209, v[144:147]
	v_mul_f32_e32 v148, v51, v148
	v_mul_f32_e32 v149, v51, v149
	v_mul_f32_e32 v150, v51, v150
	v_mul_f32_e32 v151, v51, v151
	ds_write_b128 v209, v[148:151] offset:1024
	v_mul_f32_e32 v152, v52, v152
	v_mul_f32_e32 v153, v52, v153
	v_mul_f32_e32 v154, v52, v154
	v_mul_f32_e32 v155, v52, v155
	ds_write_b128 v209, v[152:155] offset:2048
	v_mul_f32_e32 v156, v53, v156
	v_mul_f32_e32 v157, v53, v157
	v_mul_f32_e32 v158, v53, v158
	v_mul_f32_e32 v159, v53, v159
	ds_write_b128 v209, v[156:159] offset:3072
	v_mul_f32_e32 v160, v54, v160
	v_mul_f32_e32 v161, v54, v161
	v_mul_f32_e32 v162, v54, v162
	v_mul_f32_e32 v163, v54, v163
	ds_write_b128 v209, v[160:163] offset:4096
	v_mul_f32_e32 v164, v55, v164
	v_mul_f32_e32 v165, v55, v165
	v_mul_f32_e32 v166, v55, v166
	v_mul_f32_e32 v167, v55, v167
	ds_write_b128 v209, v[164:167] offset:5120
	v_mul_f32_e32 v168, v56, v168
	v_mul_f32_e32 v169, v56, v169
	v_mul_f32_e32 v170, v56, v170
	v_mul_f32_e32 v171, v56, v171
	ds_write_b128 v209, v[168:171] offset:6144
	v_mul_f32_e32 v172, v57, v172
	v_mul_f32_e32 v173, v57, v173
	v_mul_f32_e32 v174, v57, v174
	v_mul_f32_e32 v175, v57, v175
	ds_write_b128 v209, v[172:175] offset:7168
	s_waitcnt lgkmcnt(0)
	s_barrier
; #define GAS __attribute__((address_space(1)))
; #define LAS __attribute__((address_space(3)))
; #define LDS_WAIT() asm volatile("s_waitcnt lgkmcnt(0)" ::: "memory")
;     const int pr = item >> 1, kb = 2 * (pr / nblk) + (item & 1), nb = pr % nblk, k0 = 64 * kb, n0 = 32 * nb;
;     const int nr = n0 + (lane & 31); const int sc = MAP == 1 ? src_col_in(nr) : nr;
;     float v[32];
; #pragma unroll
;     for (int i = 0; i < 32; ++i) v[i] = sc >= 0 ? W[(size_t)(k0 + 2 * i + (lane >> 5)) * Nsrc + sc] : 0.f;
; #pragma unroll
;     for (int i = 0; i < 32; ++i) { const int k = k0 + 2 * i + (lane >> 5); float x = v[i] * wscale; if (KS) x *= (k < ksplit ? ksA[k] : ksB[k - ksplit]); scr[(2 * i + (lane >> 5)) * 33 + (lane & 31)] = x; }
;     LDS_WAIT(); asm volatile("" ::: "memory");
;     const int c = lane & 7;
; #pragma unroll
;     for (int j = 0; j < 4; ++j) { const int n = (lane >> 3) + 8 * j; const LAS float* s = scr + (8 * c) * 33 + n;
;         const unsigned long long o = (unsigned long long)pg8::pk4_fp8(s[0 * 33], s[1 * 33], s[2 * 33], s[3 * 33]) | ((unsigned long long)pg8::pk4_fp8(s[4 * 33], s[5 * 33], s[6 * 33], s[7 * 33]) << 32);
;         *(GAS unsigned long long*)(WT + (size_t)(n0 + n) * K + k0 + 8 * c) = o; }
;     LDS_WAIT(); asm volatile("" ::: "memory");
; __global__ void __launch_bounds__(NWAVES * 64, 2) hybrid_fwd(Args args) {
;     ...
;             if (r < I_IN) { if (l >= PROJ_F8_FROM) p0_transpose_item_f8<true, 1>(args.in[2] + (size_t)l * DM * NSRC, DM, NSRC, NPROJ / 32, (unsigned char*)(ws + WS_WIN + l * SZ_WIN), WUP8_SCALE, args.in[1] + l * DM, args.in[1] + l * DM, DM, scr, r, lane);
	s_add_i32 s24, s23, 72
	s_lshl_b32 s20, s24, 7
	s_cmp_lt_u32 s24, 40
	s_cselect_b32 s21, 0, 0x830
	s_cmp_lt_u32 s24, 72
	s_cselect_b32 s21, s21, 0xfffff030
	s_add_i32 s20, s20, s21
	s_lshl_b32 s20, s20, 2
	s_add_u32 s8, s50, s20
	s_addc_u32 s9, s51, 0
	global_load_dwordx4 v[144:147], v76, s[8:9]
	s_add_u32 s8, s8, 0x16280
	s_addc_u32 s9, s9, 0
	global_load_dwordx4 v[148:151], v76, s[8:9]
	s_add_u32 s8, s8, 0x16280
	s_addc_u32 s9, s9, 0
	global_load_dwordx4 v[152:155], v76, s[8:9]
	s_add_u32 s8, s8, 0x16280
	s_addc_u32 s9, s9, 0
	global_load_dwordx4 v[156:159], v76, s[8:9]
	s_add_u32 s8, s8, 0x16280
	s_addc_u32 s9, s9, 0
	global_load_dwordx4 v[160:163], v76, s[8:9]
	s_add_u32 s8, s8, 0x16280
	s_addc_u32 s9, s9, 0
	global_load_dwordx4 v[164:167], v76, s[8:9]
	s_add_u32 s8, s8, 0x16280
	s_addc_u32 s9, s9, 0
	global_load_dwordx4 v[168:171], v76, s[8:9]
	s_add_u32 s8, s8, 0x16280
	s_addc_u32 s9, s9, 0
	global_load_dwordx4 v[172:175], v76, s[8:9]
	s_add_i32 s24, s23, 56
	s_mul_i32 s20, s24, 0x80000
	s_add_u32 s6, s52, s20
	s_addc_u32 s7, s53, 0
	s_cmp_lt_u32 s24, 16
	s_cselect_b32 s20, 1, 0
	s_sub_i32 s21, s24, 16
	s_bitcmp0_b32 s21, 2
	s_cselect_b32 s21, 1, 0
	s_cmp_lt_u32 s24, 40
	s_cselect_b32 s21, s21, 0
	s_or_b32 s20, s20, s21
	s_cmp_lg_u32 s20, 0
	s_cselect_b64 s[20:21], -1, 0
	v_cndmask_b32_e64 v91, v77, v81, s[20:21]
	v_cndmask_b32_e64 v92, v78, v82, s[20:21]
	ds_read_b32 v226, v211
	ds_read_b32 v227, v211 offset:512
	ds_read_b32 v228, v211 offset:1024
	ds_read_b32 v229, v211 offset:1536
	ds_read_b32 v230, v211 offset:2048
	ds_read_b32 v231, v211 offset:2560
	ds_read_b32 v232, v211 offset:3072
	ds_read_b32 v233, v211 offset:3584
	ds_read_b32 v234, v211 offset:4096
	ds_read_b32 v235, v211 offset:4608
	ds_read_b32 v236, v211 offset:5120
	ds_read_b32 v237, v211 offset:5632
	ds_read_b32 v238, v211 offset:6144
	ds_read_b32 v239, v211 offset:6656
	ds_read_b32 v240, v211 offset:7168
	ds_read_b32 v241, v211 offset:7680
	s_waitcnt lgkmcnt(0)
	v_max_f32_e32 v226, v226, v226
	v_max_f32_e32 v227, v227, v227
	v_max_f32_e32 v228, v228, v228
	v_max_f32_e32 v229, v229, v229
	v_max_f32_e32 v230, v230, v230
	v_max_f32_e32 v231, v231, v231
	v_max_f32_e32 v232, v232, v232
	v_max_f32_e32 v233, v233, v233
	v_max_f32_e32 v234, v234, v234
	v_max_f32_e32 v235, v235, v235
	v_max_f32_e32 v236, v236, v236
	v_max_f32_e32 v237, v237, v237
	v_max_f32_e32 v238, v238, v238
	v_max_f32_e32 v239, v239, v239
	v_max_f32_e32 v240, v240, v240
	v_max_f32_e32 v241, v241, v241
	v_med3_f32 v226, v226, s62, v95
	v_med3_f32 v227, v227, s62, v95
	v_med3_f32 v228, v228, s62, v95
	v_med3_f32 v229, v229, s62, v95
	v_med3_f32 v230, v230, s62, v95
	v_med3_f32 v231, v231, s62, v95
	v_med3_f32 v232, v232, s62, v95
	v_med3_f32 v233, v233, s62, v95
	v_med3_f32 v234, v234, s62, v95
	v_med3_f32 v235, v235, s62, v95
	v_med3_f32 v236, v236, s62, v95
	v_med3_f32 v237, v237, s62, v95
	v_med3_f32 v238, v238, s62, v95
	v_med3_f32 v239, v239, s62, v95
	v_med3_f32 v240, v240, s62, v95
	v_med3_f32 v241, v241, s62, v95
	v_mov_b32_e32 v242, 0
	v_mov_b32_e32 v243, 0
	v_mov_b32_e32 v244, 0
	v_mov_b32_e32 v245, 0
	v_cvt_pk_fp8_f32 v242, v226, v227
	v_cvt_pk_fp8_f32 v243, v230, v231
	v_cvt_pk_fp8_f32 v244, v234, v235
	v_cvt_pk_fp8_f32 v245, v238, v239
	v_cvt_pk_fp8_f32 v242, v228, v229 op_sel:[0,0,1]
	v_cvt_pk_fp8_f32 v243, v232, v233 op_sel:[0,0,1]
	v_cvt_pk_fp8_f32 v244, v236, v237 op_sel:[0,0,1]
	v_cvt_pk_fp8_f32 v245, v240, v241 op_sel:[0,0,1]
	s_nop 0
	global_store_dwordx4 v91, v[242:245], s[6:7]
	ds_read_b32 v226, v213
	ds_read_b32 v227, v213 offset:512
	ds_read_b32 v228, v213 offset:1024
	ds_read_b32 v229, v213 offset:1536
	ds_read_b32 v230, v213 offset:2048
	ds_read_b32 v231, v213 offset:2560
	ds_read_b32 v232, v213 offset:3072
	ds_read_b32 v233, v213 offset:3584
	ds_read_b32 v234, v213 offset:4096
	ds_read_b32 v235, v213 offset:4608
	ds_read_b32 v236, v213 offset:5120
	ds_read_b32 v237, v213 offset:5632
	ds_read_b32 v238, v213 offset:6144
	ds_read_b32 v239, v213 offset:6656
	ds_read_b32 v240, v213 offset:7168
	ds_read_b32 v241, v213 offset:7680
	s_waitcnt lgkmcnt(0)
	v_max_f32_e32 v226, v226, v226
	v_max_f32_e32 v227, v227, v227
	v_max_f32_e32 v228, v228, v228
	v_max_f32_e32 v229, v229, v229
	v_max_f32_e32 v230, v230, v230
	v_max_f32_e32 v231, v231, v231
	v_max_f32_e32 v232, v232, v232
	v_max_f32_e32 v233, v233, v233
	v_max_f32_e32 v234, v234, v234
	v_max_f32_e32 v235, v235, v235
	v_max_f32_e32 v236, v236, v236
	v_max_f32_e32 v237, v237, v237
	v_max_f32_e32 v238, v238, v238
	v_max_f32_e32 v239, v239, v239
	v_max_f32_e32 v240, v240, v240
	v_max_f32_e32 v241, v241, v241
	v_med3_f32 v226, v226, s62, v95
	v_med3_f32 v227, v227, s62, v95
	v_med3_f32 v228, v228, s62, v95
	v_med3_f32 v229, v229, s62, v95
	v_med3_f32 v230, v230, s62, v95
	v_med3_f32 v231, v231, s62, v95
	v_med3_f32 v232, v232, s62, v95
	v_med3_f32 v233, v233, s62, v95
	v_med3_f32 v234, v234, s62, v95
	v_med3_f32 v235, v235, s62, v95
	v_med3_f32 v236, v236, s62, v95
	v_med3_f32 v237, v237, s62, v95
	v_med3_f32 v238, v238, s62, v95
	v_med3_f32 v239, v239, s62, v95
	v_med3_f32 v240, v240, s62, v95
	v_med3_f32 v241, v241, s62, v95
	v_mov_b32_e32 v242, 0
	v_mov_b32_e32 v243, 0
	v_mov_b32_e32 v244, 0
	v_mov_b32_e32 v245, 0
	v_cvt_pk_fp8_f32 v242, v226, v227
	v_cvt_pk_fp8_f32 v243, v230, v231
	v_cvt_pk_fp8_f32 v244, v234, v235
	v_cvt_pk_fp8_f32 v245, v238, v239
	v_cvt_pk_fp8_f32 v242, v228, v229 op_sel:[0,0,1]
	v_cvt_pk_fp8_f32 v243, v232, v233 op_sel:[0,0,1]
	v_cvt_pk_fp8_f32 v244, v236, v237 op_sel:[0,0,1]
	v_cvt_pk_fp8_f32 v245, v240, v241 op_sel:[0,0,1]
	s_nop 0
	global_store_dwordx4 v92, v[242:245], s[6:7]
	s_waitcnt vmcnt(12)
	v_mul_f32_e32 v176, v50, v176
	v_mul_f32_e32 v177, v50, v177
	v_mul_f32_e32 v178, v50, v178
	v_mul_f32_e32 v179, v50, v179
	ds_write_b128 v210, v[176:179]
	v_mul_f32_e32 v180, v51, v180
	v_mul_f32_e32 v181, v51, v181
	v_mul_f32_e32 v182, v51, v182
	v_mul_f32_e32 v183, v51, v183
	ds_write_b128 v210, v[180:183] offset:1024
	v_mul_f32_e32 v184, v52, v184
	v_mul_f32_e32 v185, v52, v185
	v_mul_f32_e32 v186, v52, v186
	v_mul_f32_e32 v187, v52, v187
	ds_write_b128 v210, v[184:187] offset:2048
	v_mul_f32_e32 v188, v53, v188
	v_mul_f32_e32 v189, v53, v189
	v_mul_f32_e32 v190, v53, v190
	v_mul_f32_e32 v191, v53, v191
	ds_write_b128 v210, v[188:191] offset:3072
	v_mul_f32_e32 v192, v54, v192
	v_mul_f32_e32 v193, v54, v193
	v_mul_f32_e32 v194, v54, v194
	v_mul_f32_e32 v195, v54, v195
	ds_write_b128 v210, v[192:195] offset:4096
	v_mul_f32_e32 v196, v55, v196
	v_mul_f32_e32 v197, v55, v197
	v_mul_f32_e32 v198, v55, v198
	v_mul_f32_e32 v199, v55, v199
	ds_write_b128 v210, v[196:199] offset:5120
	v_mul_f32_e32 v200, v56, v200
	v_mul_f32_e32 v201, v56, v201
	v_mul_f32_e32 v202, v56, v202
	v_mul_f32_e32 v203, v56, v203
	ds_write_b128 v210, v[200:203] offset:6144
	v_mul_f32_e32 v204, v57, v204
	v_mul_f32_e32 v205, v57, v205
	v_mul_f32_e32 v206, v57, v206
	v_mul_f32_e32 v207, v57, v207
	ds_write_b128 v210, v[204:207] offset:7168
	s_waitcnt lgkmcnt(0)
	s_barrier
; #define GAS __attribute__((address_space(1)))
; #define LAS __attribute__((address_space(3)))
; #define LDS_WAIT() asm volatile("s_waitcnt lgkmcnt(0)" ::: "memory")
;     const int pr = item >> 1, kb = 2 * (pr / nblk) + (item & 1), nb = pr % nblk, k0 = 64 * kb, n0 = 32 * nb;
;     const int nr = n0 + (lane & 31); const int sc = MAP == 1 ? src_col_in(nr) : nr;
;     float v[32];
; #pragma unroll
;     for (int i = 0; i < 32; ++i) v[i] = sc >= 0 ? W[(size_t)(k0 + 2 * i + (lane >> 5)) * Nsrc + sc] : 0.f;
; #pragma unroll
;     for (int i = 0; i < 32; ++i) { const int k = k0 + 2 * i + (lane >> 5); float x = v[i] * wscale; if (KS) x *= (k < ksplit ? ksA[k] : ksB[k - ksplit]); scr[(2 * i + (lane >> 5)) * 33 + (lane & 31)] = x; }
;     LDS_WAIT(); asm volatile("" ::: "memory");
;     const int c = lane & 7;
; #pragma unroll
;     for (int j = 0; j < 4; ++j) { const int n = (lane >> 3) + 8 * j; const LAS float* s = scr + (8 * c) * 33 + n;
;         const unsigned long long o = (unsigned long long)pg8::pk4_fp8(s[0 * 33], s[1 * 33], s[2 * 33], s[3 * 33]) | ((unsigned long long)pg8::pk4_fp8(s[4 * 33], s[5 * 33], s[6 * 33], s[7 * 33]) << 32);
;         *(GAS unsigned long long*)(WT + (size_t)(n0 + n) * K + k0 + 8 * c) = o; }
;     LDS_WAIT(); asm volatile("" ::: "memory");
; __global__ void __launch_bounds__(NWAVES * 64, 2) hybrid_fwd(Args args) {
;     ...
;             if (r < I_IN) { if (l >= PROJ_F8_FROM) p0_transpose_item_f8<true, 1>(args.in[2] + (size_t)l * DM * NSRC, DM, NSRC, NPROJ / 32, (unsigned char*)(ws + WS_WIN + l * SZ_WIN), WUP8_SCALE, args.in[1] + l * DM, args.in[1] + l * DM, DM, scr, r, lane);
	s_add_i32 s24, s23, 80
	s_lshl_b32 s20, s24, 7
	s_cmp_lt_u32 s24, 40
	s_cselect_b32 s21, 0, 0x830
	s_cmp_lt_u32 s24, 72
	s_cselect_b32 s21, s21, 0xfffff030
	s_add_i32 s20, s20, s21
	s_lshl_b32 s20, s20, 2
	s_add_u32 s8, s50, s20
	s_addc_u32 s9, s51, 0
	global_load_dwordx4 v[176:179], v76, s[8:9]
	s_add_u32 s8, s8, 0x16280
	s_addc_u32 s9, s9, 0
	global_load_dwordx4 v[180:183], v76, s[8:9]
	s_add_u32 s8, s8, 0x16280
	s_addc_u32 s9, s9, 0
	global_load_dwordx4 v[184:187], v76, s[8:9]
	s_add_u32 s8, s8, 0x16280
	s_addc_u32 s9, s9, 0
	global_load_dwordx4 v[188:191], v76, s[8:9]
	s_add_u32 s8, s8, 0x16280
	s_addc_u32 s9, s9, 0
	global_load_dwordx4 v[192:195], v76, s[8:9]
	s_add_u32 s8, s8, 0x16280
	s_addc_u32 s9, s9, 0
	global_load_dwordx4 v[196:199], v76, s[8:9]
	s_add_u32 s8, s8, 0x16280
	s_addc_u32 s9, s9, 0
	global_load_dwordx4 v[200:203], v76, s[8:9]
	s_add_u32 s8, s8, 0x16280
	s_addc_u32 s9, s9, 0
	global_load_dwordx4 v[204:207], v76, s[8:9]
	s_add_i32 s24, s23, 64
	s_mul_i32 s20, s24, 0x80000
	s_add_u32 s6, s52, s20
	s_addc_u32 s7, s53, 0
	s_cmp_lt_u32 s24, 16
	s_cselect_b32 s20, 1, 0
	s_sub_i32 s21, s24, 16
	s_bitcmp0_b32 s21, 2
	s_cselect_b32 s21, 1, 0
	s_cmp_lt_u32 s24, 40
	s_cselect_b32 s21, s21, 0
	s_or_b32 s20, s20, s21
	s_cmp_lg_u32 s20, 0
	s_cselect_b64 s[20:21], -1, 0
	v_cndmask_b32_e64 v91, v77, v81, s[20:21]
	v_cndmask_b32_e64 v92, v78, v82, s[20:21]
	ds_read_b32 v226, v212
	ds_read_b32 v227, v212 offset:512
	ds_read_b32 v228, v212 offset:1024
	ds_read_b32 v229, v212 offset:1536
	ds_read_b32 v230, v212 offset:2048
	ds_read_b32 v231, v212 offset:2560
	ds_read_b32 v232, v212 offset:3072
	ds_read_b32 v233, v212 offset:3584
	ds_read_b32 v234, v212 offset:4096
	ds_read_b32 v235, v212 offset:4608
	ds_read_b32 v236, v212 offset:5120
	ds_read_b32 v237, v212 offset:5632
	ds_read_b32 v238, v212 offset:6144
	ds_read_b32 v239, v212 offset:6656
	ds_read_b32 v240, v212 offset:7168
	ds_read_b32 v241, v212 offset:7680
	s_waitcnt lgkmcnt(0)
	v_max_f32_e32 v226, v226, v226
	v_max_f32_e32 v227, v227, v227
	v_max_f32_e32 v228, v228, v228
	v_max_f32_e32 v229, v229, v229
	v_max_f32_e32 v230, v230, v230
	v_max_f32_e32 v231, v231, v231
	v_max_f32_e32 v232, v232, v232
	v_max_f32_e32 v233, v233, v233
	v_max_f32_e32 v234, v234, v234
	v_max_f32_e32 v235, v235, v235
	v_max_f32_e32 v236, v236, v236
	v_max_f32_e32 v237, v237, v237
	v_max_f32_e32 v238, v238, v238
	v_max_f32_e32 v239, v239, v239
	v_max_f32_e32 v240, v240, v240
	v_max_f32_e32 v241, v241, v241
	v_med3_f32 v226, v226, s62, v95
	v_med3_f32 v227, v227, s62, v95
	v_med3_f32 v228, v228, s62, v95
	v_med3_f32 v229, v229, s62, v95
	v_med3_f32 v230, v230, s62, v95
	v_med3_f32 v231, v231, s62, v95
	v_med3_f32 v232, v232, s62, v95
	v_med3_f32 v233, v233, s62, v95
	v_med3_f32 v234, v234, s62, v95
	v_med3_f32 v235, v235, s62, v95
	v_med3_f32 v236, v236, s62, v95
	v_med3_f32 v237, v237, s62, v95
	v_med3_f32 v238, v238, s62, v95
	v_med3_f32 v239, v239, s62, v95
	v_med3_f32 v240, v240, s62, v95
	v_med3_f32 v241, v241, s62, v95
	v_mov_b32_e32 v242, 0
	v_mov_b32_e32 v243, 0
	v_mov_b32_e32 v244, 0
	v_mov_b32_e32 v245, 0
	v_cvt_pk_fp8_f32 v242, v226, v227
	v_cvt_pk_fp8_f32 v243, v230, v231
	v_cvt_pk_fp8_f32 v244, v234, v235
	v_cvt_pk_fp8_f32 v245, v238, v239
	v_cvt_pk_fp8_f32 v242, v228, v229 op_sel:[0,0,1]
	v_cvt_pk_fp8_f32 v243, v232, v233 op_sel:[0,0,1]
	v_cvt_pk_fp8_f32 v244, v236, v237 op_sel:[0,0,1]
	v_cvt_pk_fp8_f32 v245, v240, v241 op_sel:[0,0,1]
	s_nop 0
	global_store_dwordx4 v91, v[242:245], s[6:7]
	ds_read_b32 v226, v214
	ds_read_b32 v227, v214 offset:512
	ds_read_b32 v228, v214 offset:1024
	ds_read_b32 v229, v214 offset:1536
	ds_read_b32 v230, v214 offset:2048
	ds_read_b32 v231, v214 offset:2560
	ds_read_b32 v232, v214 offset:3072
	ds_read_b32 v233, v214 offset:3584
	ds_read_b32 v234, v214 offset:4096
	ds_read_b32 v235, v214 offset:4608
	ds_read_b32 v236, v214 offset:5120
	ds_read_b32 v237, v214 offset:5632
	ds_read_b32 v238, v214 offset:6144
	ds_read_b32 v239, v214 offset:6656
	ds_read_b32 v240, v214 offset:7168
	ds_read_b32 v241, v214 offset:7680
	s_waitcnt lgkmcnt(0)
	v_max_f32_e32 v226, v226, v226
	v_max_f32_e32 v227, v227, v227
	v_max_f32_e32 v228, v228, v228
	v_max_f32_e32 v229, v229, v229
	v_max_f32_e32 v230, v230, v230
	v_max_f32_e32 v231, v231, v231
	v_max_f32_e32 v232, v232, v232
	v_max_f32_e32 v233, v233, v233
	v_max_f32_e32 v234, v234, v234
	v_max_f32_e32 v235, v235, v235
	v_max_f32_e32 v236, v236, v236
	v_max_f32_e32 v237, v237, v237
	v_max_f32_e32 v238, v238, v238
	v_max_f32_e32 v239, v239, v239
	v_max_f32_e32 v240, v240, v240
	v_max_f32_e32 v241, v241, v241
	v_med3_f32 v226, v226, s62, v95
	v_med3_f32 v227, v227, s62, v95
	v_med3_f32 v228, v228, s62, v95
	v_med3_f32 v229, v229, s62, v95
	v_med3_f32 v230, v230, s62, v95
	v_med3_f32 v231, v231, s62, v95
	v_med3_f32 v232, v232, s62, v95
	v_med3_f32 v233, v233, s62, v95
	v_med3_f32 v234, v234, s62, v95
	v_med3_f32 v235, v235, s62, v95
	v_med3_f32 v236, v236, s62, v95
	v_med3_f32 v237, v237, s62, v95
	v_med3_f32 v238, v238, s62, v95
	v_med3_f32 v239, v239, s62, v95
	v_med3_f32 v240, v240, s62, v95
	v_med3_f32 v241, v241, s62, v95
	v_mov_b32_e32 v242, 0
	v_mov_b32_e32 v243, 0
	v_mov_b32_e32 v244, 0
	v_mov_b32_e32 v245, 0
	v_cvt_pk_fp8_f32 v242, v226, v227
	v_cvt_pk_fp8_f32 v243, v230, v231
	v_cvt_pk_fp8_f32 v244, v234, v235
	v_cvt_pk_fp8_f32 v245, v238, v239
	v_cvt_pk_fp8_f32 v242, v228, v229 op_sel:[0,0,1]
	v_cvt_pk_fp8_f32 v243, v232, v233 op_sel:[0,0,1]
	v_cvt_pk_fp8_f32 v244, v236, v237 op_sel:[0,0,1]
	v_cvt_pk_fp8_f32 v245, v240, v241 op_sel:[0,0,1]
	s_nop 0
	global_store_dwordx4 v92, v[242:245], s[6:7]
	s_waitcnt vmcnt(12)
	v_mul_f32_e32 v144, v50, v144
	v_mul_f32_e32 v145, v50, v145
	v_mul_f32_e32 v146, v50, v146
	v_mul_f32_e32 v147, v50, v147
	ds_write_b128 v209, v[144:147]
	v_mul_f32_e32 v148, v51, v148
	v_mul_f32_e32 v149, v51, v149
	v_mul_f32_e32 v150, v51, v150
	v_mul_f32_e32 v151, v51, v151
	ds_write_b128 v209, v[148:151] offset:1024
	v_mul_f32_e32 v152, v52, v152
	v_mul_f32_e32 v153, v52, v153
	v_mul_f32_e32 v154, v52, v154
	v_mul_f32_e32 v155, v52, v155
	ds_write_b128 v209, v[152:155] offset:2048
	v_mul_f32_e32 v156, v53, v156
	v_mul_f32_e32 v157, v53, v157
	v_mul_f32_e32 v158, v53, v158
	v_mul_f32_e32 v159, v53, v159
	ds_write_b128 v209, v[156:159] offset:3072
	v_mul_f32_e32 v160, v54, v160
	v_mul_f32_e32 v161, v54, v161
	v_mul_f32_e32 v162, v54, v162
	v_mul_f32_e32 v163, v54, v163
	ds_write_b128 v209, v[160:163] offset:4096
	v_mul_f32_e32 v164, v55, v164
	v_mul_f32_e32 v165, v55, v165
	v_mul_f32_e32 v166, v55, v166
	v_mul_f32_e32 v167, v55, v167
	ds_write_b128 v209, v[164:167] offset:5120
	v_mul_f32_e32 v168, v56, v168
	v_mul_f32_e32 v169, v56, v169
	v_mul_f32_e32 v170, v56, v170
	v_mul_f32_e32 v171, v56, v171
	ds_write_b128 v209, v[168:171] offset:6144
	v_mul_f32_e32 v172, v57, v172
	v_mul_f32_e32 v173, v57, v173
	v_mul_f32_e32 v174, v57, v174
	v_mul_f32_e32 v175, v57, v175
	ds_write_b128 v209, v[172:175] offset:7168
	s_waitcnt lgkmcnt(0)
	s_barrier
; #define GAS __attribute__((address_space(1)))
; #define LAS __attribute__((address_space(3)))
; #define LDS_WAIT() asm volatile("s_waitcnt lgkmcnt(0)" ::: "memory")
;     const int pr = item >> 1, kb = 2 * (pr / nblk) + (item & 1), nb = pr % nblk, k0 = 64 * kb, n0 = 32 * nb;
;     const int nr = n0 + (lane & 31); const int sc = MAP == 1 ? src_col_in(nr) : nr;
;     float v[32];
; #pragma unroll
;     for (int i = 0; i < 32; ++i) v[i] = sc >= 0 ? W[(size_t)(k0 + 2 * i + (lane >> 5)) * Nsrc + sc] : 0.f;
; #pragma unroll
;     for (int i = 0; i < 32; ++i) { const int k = k0 + 2 * i + (lane >> 5); float x = v[i] * wscale; if (KS) x *= (k < ksplit ? ksA[k] : ksB[k - ksplit]); scr[(2 * i + (lane >> 5)) * 33 + (lane & 31)] = x; }
;     LDS_WAIT(); asm volatile("" ::: "memory");
;     const int c = lane & 7;
; #pragma unroll
;     for (int j = 0; j < 4; ++j) { const int n = (lane >> 3) + 8 * j; const LAS float* s = scr + (8 * c) * 33 + n;
;         const unsigned long long o = (unsigned long long)pg8::pk4_fp8(s[0 * 33], s[1 * 33], s[2 * 33], s[3 * 33]) | ((unsigned long long)pg8::pk4_fp8(s[4 * 33], s[5 * 33], s[6 * 33], s[7 * 33]) << 32);
;         *(GAS unsigned long long*)(WT + (size_t)(n0 + n) * K + k0 + 8 * c) = o; }
;     LDS_WAIT(); asm volatile("" ::: "memory");
; __global__ void __launch_bounds__(NWAVES * 64, 2) hybrid_fwd(Args args) {
;     ...
;             if (r < I_O) { if (l >= WO_F8_FROM) p0_transpose_item_f8<true>(args.in[13] + (size_t)l * DM * DM, DM, DM, DM / 32, (unsigned char*)(ws + WS_WO + l * SZ_WO), 64.f, args.in[6] + l * 2048, args.in[12] + l * 2048, 2048, scr, r, lane);
	s_mov_b64 s[8:9], s[54:55]
	global_load_dwordx4 v[144:147], v75, s[8:9]
	s_add_u32 s8, s8, 0x8000
	s_addc_u32 s9, s9, 0
	global_load_dwordx4 v[148:151], v75, s[8:9]
	s_add_u32 s8, s8, 0x8000
	s_addc_u32 s9, s9, 0
	global_load_dwordx4 v[152:155], v75, s[8:9]
	s_add_u32 s8, s8, 0x8000
	s_addc_u32 s9, s9, 0
	global_load_dwordx4 v[156:159], v75, s[8:9]
	s_add_u32 s8, s8, 0x8000
	s_addc_u32 s9, s9, 0
	global_load_dwordx4 v[160:163], v75, s[8:9]
	s_add_u32 s8, s8, 0x8000
	s_addc_u32 s9, s9, 0
	global_load_dwordx4 v[164:167], v75, s[8:9]
	s_add_u32 s8, s8, 0x8000
	s_addc_u32 s9, s9, 0
	global_load_dwordx4 v[168:171], v75, s[8:9]
	s_add_u32 s8, s8, 0x8000
	s_addc_u32 s9, s9, 0
	global_load_dwordx4 v[172:175], v75, s[8:9]
	s_add_i32 s24, s23, 72
	s_mul_i32 s20, s24, 0x80000
	s_add_u32 s6, s52, s20
	s_addc_u32 s7, s53, 0
	s_cmp_lt_u32 s24, 16
	s_cselect_b32 s20, 1, 0
	s_sub_i32 s21, s24, 16
	s_bitcmp0_b32 s21, 2
	s_cselect_b32 s21, 1, 0
	s_cmp_lt_u32 s24, 40
	s_cselect_b32 s21, s21, 0
	s_or_b32 s20, s20, s21
	s_cmp_lg_u32 s20, 0
	s_cselect_b64 s[20:21], -1, 0
	v_cndmask_b32_e64 v91, v77, v81, s[20:21]
	v_cndmask_b32_e64 v92, v78, v82, s[20:21]
	ds_read_b32 v226, v211
	ds_read_b32 v227, v211 offset:512
	ds_read_b32 v228, v211 offset:1024
	ds_read_b32 v229, v211 offset:1536
	ds_read_b32 v230, v211 offset:2048
	ds_read_b32 v231, v211 offset:2560
	ds_read_b32 v232, v211 offset:3072
	ds_read_b32 v233, v211 offset:3584
	ds_read_b32 v234, v211 offset:4096
	ds_read_b32 v235, v211 offset:4608
	ds_read_b32 v236, v211 offset:5120
	ds_read_b32 v237, v211 offset:5632
	ds_read_b32 v238, v211 offset:6144
	ds_read_b32 v239, v211 offset:6656
	ds_read_b32 v240, v211 offset:7168
	ds_read_b32 v241, v211 offset:7680
	s_waitcnt lgkmcnt(0)
	v_max_f32_e32 v226, v226, v226
	v_max_f32_e32 v227, v227, v227
	v_max_f32_e32 v228, v228, v228
	v_max_f32_e32 v229, v229, v229
	v_max_f32_e32 v230, v230, v230
	v_max_f32_e32 v231, v231, v231
	v_max_f32_e32 v232, v232, v232
	v_max_f32_e32 v233, v233, v233
	v_max_f32_e32 v234, v234, v234
	v_max_f32_e32 v235, v235, v235
	v_max_f32_e32 v236, v236, v236
	v_max_f32_e32 v237, v237, v237
	v_max_f32_e32 v238, v238, v238
	v_max_f32_e32 v239, v239, v239
	v_max_f32_e32 v240, v240, v240
	v_max_f32_e32 v241, v241, v241
	v_med3_f32 v226, v226, s62, v95
	v_med3_f32 v227, v227, s62, v95
	v_med3_f32 v228, v228, s62, v95
	v_med3_f32 v229, v229, s62, v95
	v_med3_f32 v230, v230, s62, v95
	v_med3_f32 v231, v231, s62, v95
	v_med3_f32 v232, v232, s62, v95
	v_med3_f32 v233, v233, s62, v95
	v_med3_f32 v234, v234, s62, v95
	v_med3_f32 v235, v235, s62, v95
	v_med3_f32 v236, v236, s62, v95
	v_med3_f32 v237, v237, s62, v95
	v_med3_f32 v238, v238, s62, v95
	v_med3_f32 v239, v239, s62, v95
	v_med3_f32 v240, v240, s62, v95
	v_med3_f32 v241, v241, s62, v95
	v_mov_b32_e32 v242, 0
	v_mov_b32_e32 v243, 0
	v_mov_b32_e32 v244, 0
	v_mov_b32_e32 v245, 0
	v_cvt_pk_fp8_f32 v242, v226, v227
	v_cvt_pk_fp8_f32 v243, v230, v231
	v_cvt_pk_fp8_f32 v244, v234, v235
	v_cvt_pk_fp8_f32 v245, v238, v239
	v_cvt_pk_fp8_f32 v242, v228, v229 op_sel:[0,0,1]
	v_cvt_pk_fp8_f32 v243, v232, v233 op_sel:[0,0,1]
	v_cvt_pk_fp8_f32 v244, v236, v237 op_sel:[0,0,1]
	v_cvt_pk_fp8_f32 v245, v240, v241 op_sel:[0,0,1]
	s_nop 0
	global_store_dwordx4 v91, v[242:245], s[6:7]
	ds_read_b32 v226, v213
	ds_read_b32 v227, v213 offset:512
	ds_read_b32 v228, v213 offset:1024
	ds_read_b32 v229, v213 offset:1536
	ds_read_b32 v230, v213 offset:2048
	ds_read_b32 v231, v213 offset:2560
	ds_read_b32 v232, v213 offset:3072
	ds_read_b32 v233, v213 offset:3584
	ds_read_b32 v234, v213 offset:4096
	ds_read_b32 v235, v213 offset:4608
	ds_read_b32 v236, v213 offset:5120
	ds_read_b32 v237, v213 offset:5632
	ds_read_b32 v238, v213 offset:6144
	ds_read_b32 v239, v213 offset:6656
	ds_read_b32 v240, v213 offset:7168
	ds_read_b32 v241, v213 offset:7680
	s_waitcnt lgkmcnt(0)
	v_max_f32_e32 v226, v226, v226
	v_max_f32_e32 v227, v227, v227
	v_max_f32_e32 v228, v228, v228
	v_max_f32_e32 v229, v229, v229
	v_max_f32_e32 v230, v230, v230
	v_max_f32_e32 v231, v231, v231
	v_max_f32_e32 v232, v232, v232
	v_max_f32_e32 v233, v233, v233
	v_max_f32_e32 v234, v234, v234
	v_max_f32_e32 v235, v235, v235
	v_max_f32_e32 v236, v236, v236
	v_max_f32_e32 v237, v237, v237
	v_max_f32_e32 v238, v238, v238
	v_max_f32_e32 v239, v239, v239
	v_max_f32_e32 v240, v240, v240
	v_max_f32_e32 v241, v241, v241
	v_med3_f32 v226, v226, s62, v95
	v_med3_f32 v227, v227, s62, v95
	v_med3_f32 v228, v228, s62, v95
	v_med3_f32 v229, v229, s62, v95
	v_med3_f32 v230, v230, s62, v95
	v_med3_f32 v231, v231, s62, v95
	v_med3_f32 v232, v232, s62, v95
	v_med3_f32 v233, v233, s62, v95
	v_med3_f32 v234, v234, s62, v95
	v_med3_f32 v235, v235, s62, v95
	v_med3_f32 v236, v236, s62, v95
	v_med3_f32 v237, v237, s62, v95
	v_med3_f32 v238, v238, s62, v95
	v_med3_f32 v239, v239, s62, v95
	v_med3_f32 v240, v240, s62, v95
	v_med3_f32 v241, v241, s62, v95
	v_mov_b32_e32 v242, 0
	v_mov_b32_e32 v243, 0
	v_mov_b32_e32 v244, 0
	v_mov_b32_e32 v245, 0
	v_cvt_pk_fp8_f32 v242, v226, v227
	v_cvt_pk_fp8_f32 v243, v230, v231
	v_cvt_pk_fp8_f32 v244, v234, v235
	v_cvt_pk_fp8_f32 v245, v238, v239
	v_cvt_pk_fp8_f32 v242, v228, v229 op_sel:[0,0,1]
	v_cvt_pk_fp8_f32 v243, v232, v233 op_sel:[0,0,1]
	v_cvt_pk_fp8_f32 v244, v236, v237 op_sel:[0,0,1]
	v_cvt_pk_fp8_f32 v245, v240, v241 op_sel:[0,0,1]
	s_nop 0
	global_store_dwordx4 v92, v[242:245], s[6:7]
	s_waitcnt vmcnt(12)
	v_mul_f32_e32 v176, v50, v176
	v_mul_f32_e32 v177, v50, v177
	v_mul_f32_e32 v178, v50, v178
	v_mul_f32_e32 v179, v50, v179
	ds_write_b128 v210, v[176:179]
	v_mul_f32_e32 v180, v51, v180
	v_mul_f32_e32 v181, v51, v181
	v_mul_f32_e32 v182, v51, v182
	v_mul_f32_e32 v183, v51, v183
	ds_write_b128 v210, v[180:183] offset:1024
	v_mul_f32_e32 v184, v52, v184
	v_mul_f32_e32 v185, v52, v185
	v_mul_f32_e32 v186, v52, v186
	v_mul_f32_e32 v187, v52, v187
	ds_write_b128 v210, v[184:187] offset:2048
	v_mul_f32_e32 v188, v53, v188
	v_mul_f32_e32 v189, v53, v189
	v_mul_f32_e32 v190, v53, v190
	v_mul_f32_e32 v191, v53, v191
	ds_write_b128 v210, v[188:191] offset:3072
	v_mul_f32_e32 v192, v54, v192
	v_mul_f32_e32 v193, v54, v193
	v_mul_f32_e32 v194, v54, v194
	v_mul_f32_e32 v195, v54, v195
	ds_write_b128 v210, v[192:195] offset:4096
	v_mul_f32_e32 v196, v55, v196
	v_mul_f32_e32 v197, v55, v197
	v_mul_f32_e32 v198, v55, v198
	v_mul_f32_e32 v199, v55, v199
	ds_write_b128 v210, v[196:199] offset:5120
	v_mul_f32_e32 v200, v56, v200
	v_mul_f32_e32 v201, v56, v201
	v_mul_f32_e32 v202, v56, v202
	v_mul_f32_e32 v203, v56, v203
	ds_write_b128 v210, v[200:203] offset:6144
	v_mul_f32_e32 v204, v57, v204
	v_mul_f32_e32 v205, v57, v205
	v_mul_f32_e32 v206, v57, v206
	v_mul_f32_e32 v207, v57, v207
	ds_write_b128 v210, v[204:207] offset:7168
	s_waitcnt lgkmcnt(0)
	s_barrier
; #define GAS __attribute__((address_space(1)))
; #define LAS __attribute__((address_space(3)))
; #define LDS_WAIT() asm volatile("s_waitcnt lgkmcnt(0)" ::: "memory")
;     const int pr = item >> 1, kb = 2 * (pr / nblk) + (item & 1), nb = pr % nblk, k0 = 64 * kb, n0 = 32 * nb;
;     const int nr = n0 + (lane & 31); const int sc = MAP == 1 ? src_col_in(nr) : nr;
;     float v[32];
; #pragma unroll
;     for (int i = 0; i < 32; ++i) v[i] = sc >= 0 ? W[(size_t)(k0 + 2 * i + (lane >> 5)) * Nsrc + sc] : 0.f;
; #pragma unroll
;     for (int i = 0; i < 32; ++i) { const int k = k0 + 2 * i + (lane >> 5); float x = v[i] * wscale; if (KS) x *= (k < ksplit ? ksA[k] : ksB[k - ksplit]); scr[(2 * i + (lane >> 5)) * 33 + (lane & 31)] = x; }
;     LDS_WAIT(); asm volatile("" ::: "memory");
;     const int c = lane & 7;
; #pragma unroll
;     for (int j = 0; j < 4; ++j) { const int n = (lane >> 3) + 8 * j; const LAS float* s = scr + (8 * c) * 33 + n;
;         const unsigned long long o = (unsigned long long)pg8::pk4_fp8(s[0 * 33], s[1 * 33], s[2 * 33], s[3 * 33]) | ((unsigned long long)pg8::pk4_fp8(s[4 * 33], s[5 * 33], s[6 * 33], s[7 * 33]) << 32);
;         *(GAS unsigned long long*)(WT + (size_t)(n0 + n) * K + k0 + 8 * c) = o; }
;     LDS_WAIT(); asm volatile("" ::: "memory");
; __global__ void __launch_bounds__(NWAVES * 64, 2) hybrid_fwd(Args args) {
;     ...
;             if (r < I_O) { if (l >= WO_F8_FROM) p0_transpose_item_f8<true>(args.in[13] + (size_t)l * DM * DM, DM, DM, DM / 32, (unsigned char*)(ws + WS_WO + l * SZ_WO), 64.f, args.in[6] + l * 2048, args.in[12] + l * 2048, 2048, scr, r, lane);
	s_add_u32 s8, s54, 0x1000
	s_addc_u32 s9, s55, 0
	global_load_dwordx4 v[176:179], v75, s[8:9]
	s_add_u32 s8, s8, 0x8000
	s_addc_u32 s9, s9, 0
	global_load_dwordx4 v[180:183], v75, s[8:9]
	s_add_u32 s8, s8, 0x8000
	s_addc_u32 s9, s9, 0
	global_load_dwordx4 v[184:187], v75, s[8:9]
	s_add_u32 s8, s8, 0x8000
	s_addc_u32 s9, s9, 0
	global_load_dwordx4 v[188:191], v75, s[8:9]
	s_add_u32 s8, s8, 0x8000
	s_addc_u32 s9, s9, 0
	global_load_dwordx4 v[192:195], v75, s[8:9]
	s_add_u32 s8, s8, 0x8000
	s_addc_u32 s9, s9, 0
	global_load_dwordx4 v[196:199], v75, s[8:9]
	s_add_u32 s8, s8, 0x8000
	s_addc_u32 s9, s9, 0
	global_load_dwordx4 v[200:203], v75, s[8:9]
	s_add_u32 s8, s8, 0x8000
	s_addc_u32 s9, s9, 0
	global_load_dwordx4 v[204:207], v75, s[8:9]
	s_add_i32 s24, s23, 80
	s_mul_i32 s20, s24, 0x80000
	s_add_u32 s6, s52, s20
	s_addc_u32 s7, s53, 0
	s_cmp_lt_u32 s24, 16
	s_cselect_b32 s20, 1, 0
	s_sub_i32 s21, s24, 16
	s_bitcmp0_b32 s21, 2
	s_cselect_b32 s21, 1, 0
	s_cmp_lt_u32 s24, 40
	s_cselect_b32 s21, s21, 0
	s_or_b32 s20, s20, s21
	s_cmp_lg_u32 s20, 0
	s_cselect_b64 s[20:21], -1, 0
	v_cndmask_b32_e64 v91, v77, v81, s[20:21]
	v_cndmask_b32_e64 v92, v78, v82, s[20:21]
	ds_read_b32 v226, v212
	ds_read_b32 v227, v212 offset:512
	ds_read_b32 v228, v212 offset:1024
	ds_read_b32 v229, v212 offset:1536
	ds_read_b32 v230, v212 offset:2048
	ds_read_b32 v231, v212 offset:2560
	ds_read_b32 v232, v212 offset:3072
	ds_read_b32 v233, v212 offset:3584
	ds_read_b32 v234, v212 offset:4096
	ds_read_b32 v235, v212 offset:4608
	ds_read_b32 v236, v212 offset:5120
	ds_read_b32 v237, v212 offset:5632
	ds_read_b32 v238, v212 offset:6144
	ds_read_b32 v239, v212 offset:6656
	ds_read_b32 v240, v212 offset:7168
	ds_read_b32 v241, v212 offset:7680
	s_waitcnt lgkmcnt(0)
	v_max_f32_e32 v226, v226, v226
	v_max_f32_e32 v227, v227, v227
	v_max_f32_e32 v228, v228, v228
	v_max_f32_e32 v229, v229, v229
	v_max_f32_e32 v230, v230, v230
	v_max_f32_e32 v231, v231, v231
	v_max_f32_e32 v232, v232, v232
	v_max_f32_e32 v233, v233, v233
	v_max_f32_e32 v234, v234, v234
	v_max_f32_e32 v235, v235, v235
	v_max_f32_e32 v236, v236, v236
	v_max_f32_e32 v237, v237, v237
	v_max_f32_e32 v238, v238, v238
	v_max_f32_e32 v239, v239, v239
	v_max_f32_e32 v240, v240, v240
	v_max_f32_e32 v241, v241, v241
	v_med3_f32 v226, v226, s62, v95
	v_med3_f32 v227, v227, s62, v95
	v_med3_f32 v228, v228, s62, v95
	v_med3_f32 v229, v229, s62, v95
	v_med3_f32 v230, v230, s62, v95
	v_med3_f32 v231, v231, s62, v95
	v_med3_f32 v232, v232, s62, v95
	v_med3_f32 v233, v233, s62, v95
	v_med3_f32 v234, v234, s62, v95
	v_med3_f32 v235, v235, s62, v95
	v_med3_f32 v236, v236, s62, v95
	v_med3_f32 v237, v237, s62, v95
	v_med3_f32 v238, v238, s62, v95
	v_med3_f32 v239, v239, s62, v95
	v_med3_f32 v240, v240, s62, v95
	v_med3_f32 v241, v241, s62, v95
	v_mov_b32_e32 v242, 0
	v_mov_b32_e32 v243, 0
	v_mov_b32_e32 v244, 0
	v_mov_b32_e32 v245, 0
	v_cvt_pk_fp8_f32 v242, v226, v227
	v_cvt_pk_fp8_f32 v243, v230, v231
	v_cvt_pk_fp8_f32 v244, v234, v235
	v_cvt_pk_fp8_f32 v245, v238, v239
	v_cvt_pk_fp8_f32 v242, v228, v229 op_sel:[0,0,1]
	v_cvt_pk_fp8_f32 v243, v232, v233 op_sel:[0,0,1]
	v_cvt_pk_fp8_f32 v244, v236, v237 op_sel:[0,0,1]
	v_cvt_pk_fp8_f32 v245, v240, v241 op_sel:[0,0,1]
	s_nop 0
	global_store_dwordx4 v91, v[242:245], s[6:7]
	ds_read_b32 v226, v214
	ds_read_b32 v227, v214 offset:512
	ds_read_b32 v228, v214 offset:1024
	ds_read_b32 v229, v214 offset:1536
	ds_read_b32 v230, v214 offset:2048
	ds_read_b32 v231, v214 offset:2560
	ds_read_b32 v232, v214 offset:3072
	ds_read_b32 v233, v214 offset:3584
	ds_read_b32 v234, v214 offset:4096
	ds_read_b32 v235, v214 offset:4608
	ds_read_b32 v236, v214 offset:5120
	ds_read_b32 v237, v214 offset:5632
	ds_read_b32 v238, v214 offset:6144
	ds_read_b32 v239, v214 offset:6656
	ds_read_b32 v240, v214 offset:7168
	ds_read_b32 v241, v214 offset:7680
	s_waitcnt lgkmcnt(0)
	v_max_f32_e32 v226, v226, v226
	v_max_f32_e32 v227, v227, v227
	v_max_f32_e32 v228, v228, v228
	v_max_f32_e32 v229, v229, v229
	v_max_f32_e32 v230, v230, v230
	v_max_f32_e32 v231, v231, v231
	v_max_f32_e32 v232, v232, v232
	v_max_f32_e32 v233, v233, v233
	v_max_f32_e32 v234, v234, v234
	v_max_f32_e32 v235, v235, v235
	v_max_f32_e32 v236, v236, v236
	v_max_f32_e32 v237, v237, v237
	v_max_f32_e32 v238, v238, v238
	v_max_f32_e32 v239, v239, v239
	v_max_f32_e32 v240, v240, v240
	v_max_f32_e32 v241, v241, v241
	v_med3_f32 v226, v226, s62, v95
	v_med3_f32 v227, v227, s62, v95
	v_med3_f32 v228, v228, s62, v95
	v_med3_f32 v229, v229, s62, v95
	v_med3_f32 v230, v230, s62, v95
	v_med3_f32 v231, v231, s62, v95
	v_med3_f32 v232, v232, s62, v95
	v_med3_f32 v233, v233, s62, v95
	v_med3_f32 v234, v234, s62, v95
	v_med3_f32 v235, v235, s62, v95
	v_med3_f32 v236, v236, s62, v95
	v_med3_f32 v237, v237, s62, v95
	v_med3_f32 v238, v238, s62, v95
	v_med3_f32 v239, v239, s62, v95
	v_med3_f32 v240, v240, s62, v95
	v_med3_f32 v241, v241, s62, v95
	v_mov_b32_e32 v242, 0
	v_mov_b32_e32 v243, 0
	v_mov_b32_e32 v244, 0
	v_mov_b32_e32 v245, 0
	v_cvt_pk_fp8_f32 v242, v226, v227
	v_cvt_pk_fp8_f32 v243, v230, v231
	v_cvt_pk_fp8_f32 v244, v234, v235
	v_cvt_pk_fp8_f32 v245, v238, v239
	v_cvt_pk_fp8_f32 v242, v228, v229 op_sel:[0,0,1]
	v_cvt_pk_fp8_f32 v243, v232, v233 op_sel:[0,0,1]
	v_cvt_pk_fp8_f32 v244, v236, v237 op_sel:[0,0,1]
	v_cvt_pk_fp8_f32 v245, v240, v241 op_sel:[0,0,1]
	s_nop 0
	global_store_dwordx4 v92, v[242:245], s[6:7]
	s_waitcnt vmcnt(12)
	v_mul_f32_e32 v144, v58, v144
	v_mul_f32_e32 v145, v58, v145
	v_mul_f32_e32 v146, v58, v146
	v_mul_f32_e32 v147, v58, v147
	ds_write_b128 v209, v[144:147]
	v_mul_f32_e32 v148, v59, v148
	v_mul_f32_e32 v149, v59, v149
	v_mul_f32_e32 v150, v59, v150
	v_mul_f32_e32 v151, v59, v151
	ds_write_b128 v209, v[148:151] offset:1024
	v_mul_f32_e32 v152, v60, v152
	v_mul_f32_e32 v153, v60, v153
	v_mul_f32_e32 v154, v60, v154
	v_mul_f32_e32 v155, v60, v155
	ds_write_b128 v209, v[152:155] offset:2048
	v_mul_f32_e32 v156, v61, v156
	v_mul_f32_e32 v157, v61, v157
	v_mul_f32_e32 v158, v61, v158
	v_mul_f32_e32 v159, v61, v159
	ds_write_b128 v209, v[156:159] offset:3072
	v_mul_f32_e32 v160, v62, v160
	v_mul_f32_e32 v161, v62, v161
	v_mul_f32_e32 v162, v62, v162
	v_mul_f32_e32 v163, v62, v163
	ds_write_b128 v209, v[160:163] offset:4096
	v_mul_f32_e32 v164, v63, v164
	v_mul_f32_e32 v165, v63, v165
	v_mul_f32_e32 v166, v63, v166
	v_mul_f32_e32 v167, v63, v167
	ds_write_b128 v209, v[164:167] offset:5120
	v_mul_f32_e32 v168, v64, v168
	v_mul_f32_e32 v169, v64, v169
	v_mul_f32_e32 v170, v64, v170
	v_mul_f32_e32 v171, v64, v171
	ds_write_b128 v209, v[168:171] offset:6144
	v_mul_f32_e32 v172, v65, v172
	v_mul_f32_e32 v173, v65, v173
	v_mul_f32_e32 v174, v65, v174
	v_mul_f32_e32 v175, v65, v175
	ds_write_b128 v209, v[172:175] offset:7168
	s_waitcnt lgkmcnt(0)
	s_barrier
; #define GAS __attribute__((address_space(1)))
; #define LAS __attribute__((address_space(3)))
; #define LDS_WAIT() asm volatile("s_waitcnt lgkmcnt(0)" ::: "memory")
; __device__ __forceinline__ unsigned pk2(float lo, float hi) { return f2bf(lo) | (f2bf(hi) << 16); }
; __device__ __forceinline__ int nat_dim(int p) { return (p >> 1) + 64 * (p & 1); }
; template <int MAP, bool KS, bool KPERM = false>
; __device__ __forceinline__ void p0_transpose_item(const float* W, int K, int Nsrc, int nblk, bf16* WT, const float* ksA, const float* ksB, int ksplit, LAS float* scr, int item, int lane) {
;     const int kb = item / nblk, nb = item % nblk, k0 = 64 * kb, n0 = 32 * nb;
;     const int nr = n0 + (lane & 31); const int sc = MAP == 1 ? src_col_in(nr) : (MAP == 2 ? nat_dim(nr) : nr);
;     float v[32];
; #pragma unroll
;     for (int i = 0; i < 32; ++i) { const int k = k0 + 2 * i + (lane >> 5); const int ksrc = KPERM ? ((k & ~127) + nat_dim(k & 127)) : k;
;         v[i] = sc >= 0 ? W[(size_t)ksrc * Nsrc + sc] : 0.f; }
; #pragma unroll
;     for (int i = 0; i < 32; ++i) { const int kk = 2 * i + (lane >> 5); const int k = k0 + kk;
;         if (KS) v[i] *= (k < ksplit ? ksA[k] : ksB[k - ksplit]);
;         scr[kk * 33 + (lane & 31)] = v[i]; }
;     LDS_WAIT(); asm volatile("" ::: "memory");
;     const int c = lane & 7;
; #pragma unroll
;     for (int j = 0; j < 4; ++j) { const int n = (lane >> 3) + 8 * j; const LAS float* s = scr + (8 * c) * 33 + n;
;         v4u o; o.x = pk2(s[0 * 33], s[1 * 33]); o.y = pk2(s[2 * 33], s[3 * 33]); o.z = pk2(s[4 * 33], s[5 * 33]); o.w = pk2(s[6 * 33], s[7 * 33]);
;         *(GAS v4u*)(WT + (size_t)(n0 + n) * K + k0 + 8 * c) = o; }
;     LDS_WAIT(); asm volatile("" ::: "memory");
; __global__ void __launch_bounds__(NWAVES * 64, 2) hybrid_fwd(Args args) {
;     ...
;                 else p0_transpose_item<0, true>(args.in[13] + (size_t)l * DM * DM, DM, DM, DM / 32, (bf16*)(ws + WS_WO + l * SZ_WO), args.in[6] + l * 2048, args.in[12] + l * 2048, 2048, scr, r, lane); continue; } r -= I_O;
	s_add_u32 s8, s54, 0x2000
	s_addc_u32 s9, s55, 0
	global_load_dwordx4 v[144:147], v75, s[8:9]
	s_add_u32 s8, s8, 0x8000
	s_addc_u32 s9, s9, 0
	global_load_dwordx4 v[148:151], v75, s[8:9]
	s_add_u32 s8, s8, 0x8000
	s_addc_u32 s9, s9, 0
	global_load_dwordx4 v[152:155], v75, s[8:9]
	s_add_u32 s8, s8, 0x8000
	s_addc_u32 s9, s9, 0
	global_load_dwordx4 v[156:159], v75, s[8:9]
	s_add_u32 s8, s8, 0x8000
	s_addc_u32 s9, s9, 0
	global_load_dwordx4 v[160:163], v75, s[8:9]
	s_add_u32 s8, s8, 0x8000
	s_addc_u32 s9, s9, 0
	global_load_dwordx4 v[164:167], v75, s[8:9]
	s_add_u32 s8, s8, 0x8000
	s_addc_u32 s9, s9, 0
	global_load_dwordx4 v[168:171], v75, s[8:9]
	s_add_u32 s8, s8, 0x8000
	s_addc_u32 s9, s9, 0
	global_load_dwordx4 v[172:175], v75, s[8:9]
	s_mov_b64 s[6:7], s[56:57]
	ds_read_b32 v226, v112
	ds_read_b32 v227, v112 offset:512
	ds_read_b32 v228, v112 offset:1024
	ds_read_b32 v229, v112 offset:1536
	ds_read_b32 v230, v112 offset:2048
	ds_read_b32 v231, v112 offset:2560
	ds_read_b32 v232, v112 offset:3072
	ds_read_b32 v233, v112 offset:3584
	s_waitcnt lgkmcnt(0)
	v_bfe_u32 v120, v226, 16, 1
	v_bfe_u32 v121, v227, 16, 1
	v_bfe_u32 v122, v228, 16, 1
	v_bfe_u32 v123, v229, 16, 1
	v_bfe_u32 v124, v230, 16, 1
	v_bfe_u32 v125, v231, 16, 1
	v_bfe_u32 v126, v232, 16, 1
	v_bfe_u32 v127, v233, 16, 1
	v_add3_u32 v226, v226, v120, s63
	v_add3_u32 v227, v227, v121, s63
	v_add3_u32 v228, v228, v122, s63
	v_add3_u32 v229, v229, v123, s63
	v_add3_u32 v230, v230, v124, s63
	v_add3_u32 v231, v231, v125, s63
	v_add3_u32 v232, v232, v126, s63
	v_add3_u32 v233, v233, v127, s63
	v_perm_b32 v242, v227, v226, s64
	v_perm_b32 v243, v229, v228, s64
	v_perm_b32 v244, v231, v230, s64
	v_perm_b32 v245, v233, v232, s64
	s_nop 0
	global_store_dwordx4 v83, v[242:245], s[6:7]
	ds_read_b32 v226, v114
	ds_read_b32 v227, v114 offset:512
	ds_read_b32 v228, v114 offset:1024
	ds_read_b32 v229, v114 offset:1536
	ds_read_b32 v230, v114 offset:2048
	ds_read_b32 v231, v114 offset:2560
	ds_read_b32 v232, v114 offset:3072
	ds_read_b32 v233, v114 offset:3584
	s_waitcnt lgkmcnt(0)
	v_bfe_u32 v120, v226, 16, 1
	v_bfe_u32 v121, v227, 16, 1
	v_bfe_u32 v122, v228, 16, 1
	v_bfe_u32 v123, v229, 16, 1
	v_bfe_u32 v124, v230, 16, 1
	v_bfe_u32 v125, v231, 16, 1
	v_bfe_u32 v126, v232, 16, 1
	v_bfe_u32 v127, v233, 16, 1
	v_add3_u32 v226, v226, v120, s63
	v_add3_u32 v227, v227, v121, s63
	v_add3_u32 v228, v228, v122, s63
	v_add3_u32 v229, v229, v123, s63
	v_add3_u32 v230, v230, v124, s63
	v_add3_u32 v231, v231, v125, s63
	v_add3_u32 v232, v232, v126, s63
	v_add3_u32 v233, v233, v127, s63
	v_perm_b32 v242, v227, v226, s64
	v_perm_b32 v243, v229, v228, s64
	v_perm_b32 v244, v231, v230, s64
	v_perm_b32 v245, v233, v232, s64
	s_nop 0
	global_store_dwordx4 v84, v[242:245], s[6:7]
	ds_read_b32 v226, v116
	ds_read_b32 v227, v116 offset:512
	ds_read_b32 v228, v116 offset:1024
	ds_read_b32 v229, v116 offset:1536
	ds_read_b32 v230, v116 offset:2048
	ds_read_b32 v231, v116 offset:2560
	ds_read_b32 v232, v116 offset:3072
	ds_read_b32 v233, v116 offset:3584
	s_waitcnt lgkmcnt(0)
	v_bfe_u32 v120, v226, 16, 1
	v_bfe_u32 v121, v227, 16, 1
	v_bfe_u32 v122, v228, 16, 1
	v_bfe_u32 v123, v229, 16, 1
	v_bfe_u32 v124, v230, 16, 1
	v_bfe_u32 v125, v231, 16, 1
	v_bfe_u32 v126, v232, 16, 1
	v_bfe_u32 v127, v233, 16, 1
	v_add3_u32 v226, v226, v120, s63
	v_add3_u32 v227, v227, v121, s63
	v_add3_u32 v228, v228, v122, s63
	v_add3_u32 v229, v229, v123, s63
	v_add3_u32 v230, v230, v124, s63
	v_add3_u32 v231, v231, v125, s63
	v_add3_u32 v232, v232, v126, s63
	v_add3_u32 v233, v233, v127, s63
	v_perm_b32 v242, v227, v226, s64
	v_perm_b32 v243, v229, v228, s64
	v_perm_b32 v244, v231, v230, s64
	v_perm_b32 v245, v233, v232, s64
	s_nop 0
	global_store_dwordx4 v85, v[242:245], s[6:7]
	ds_read_b32 v226, v118
	ds_read_b32 v227, v118 offset:512
	ds_read_b32 v228, v118 offset:1024
	ds_read_b32 v229, v118 offset:1536
	ds_read_b32 v230, v118 offset:2048
	ds_read_b32 v231, v118 offset:2560
	ds_read_b32 v232, v118 offset:3072
	ds_read_b32 v233, v118 offset:3584
	s_waitcnt lgkmcnt(0)
	v_bfe_u32 v120, v226, 16, 1
	v_bfe_u32 v121, v227, 16, 1
	v_bfe_u32 v122, v228, 16, 1
	v_bfe_u32 v123, v229, 16, 1
	v_bfe_u32 v124, v230, 16, 1
	v_bfe_u32 v125, v231, 16, 1
	v_bfe_u32 v126, v232, 16, 1
	v_bfe_u32 v127, v233, 16, 1
	v_add3_u32 v226, v226, v120, s63
	v_add3_u32 v227, v227, v121, s63
	v_add3_u32 v228, v228, v122, s63
	v_add3_u32 v229, v229, v123, s63
	v_add3_u32 v230, v230, v124, s63
	v_add3_u32 v231, v231, v125, s63
	v_add3_u32 v232, v232, v126, s63
	v_add3_u32 v233, v233, v127, s63
	v_perm_b32 v242, v227, v226, s64
	v_perm_b32 v243, v229, v228, s64
	v_perm_b32 v244, v231, v230, s64
	v_perm_b32 v245, v233, v232, s64
	s_nop 0
	global_store_dwordx4 v86, v[242:245], s[6:7]
	s_waitcnt vmcnt(14)
	v_mul_f32_e32 v176, v58, v176
	v_mul_f32_e32 v177, v58, v177
	v_mul_f32_e32 v178, v58, v178
	v_mul_f32_e32 v179, v58, v179
	ds_write_b128 v210, v[176:179]
	v_mul_f32_e32 v180, v59, v180
	v_mul_f32_e32 v181, v59, v181
	v_mul_f32_e32 v182, v59, v182
	v_mul_f32_e32 v183, v59, v183
	ds_write_b128 v210, v[180:183] offset:1024
	v_mul_f32_e32 v184, v60, v184
	v_mul_f32_e32 v185, v60, v185
	v_mul_f32_e32 v186, v60, v186
	v_mul_f32_e32 v187, v60, v187
	ds_write_b128 v210, v[184:187] offset:2048
	v_mul_f32_e32 v188, v61, v188
	v_mul_f32_e32 v189, v61, v189
	v_mul_f32_e32 v190, v61, v190
	v_mul_f32_e32 v191, v61, v191
	ds_write_b128 v210, v[188:191] offset:3072
	v_mul_f32_e32 v192, v62, v192
	v_mul_f32_e32 v193, v62, v193
	v_mul_f32_e32 v194, v62, v194
	v_mul_f32_e32 v195, v62, v195
	ds_write_b128 v210, v[192:195] offset:4096
	v_mul_f32_e32 v196, v63, v196
	v_mul_f32_e32 v197, v63, v197
	v_mul_f32_e32 v198, v63, v198
	v_mul_f32_e32 v199, v63, v199
	ds_write_b128 v210, v[196:199] offset:5120
	v_mul_f32_e32 v200, v64, v200
	v_mul_f32_e32 v201, v64, v201
	v_mul_f32_e32 v202, v64, v202
	v_mul_f32_e32 v203, v64, v203
	ds_write_b128 v210, v[200:203] offset:6144
	v_mul_f32_e32 v204, v65, v204
	v_mul_f32_e32 v205, v65, v205
	v_mul_f32_e32 v206, v65, v206
	v_mul_f32_e32 v207, v65, v207
	ds_write_b128 v210, v[204:207] offset:7168
	s_waitcnt lgkmcnt(0)
	s_barrier
; #define GAS __attribute__((address_space(1)))
; #define LAS __attribute__((address_space(3)))
; #define LDS_WAIT() asm volatile("s_waitcnt lgkmcnt(0)" ::: "memory")
; __device__ __forceinline__ unsigned pk2(float lo, float hi) { return f2bf(lo) | (f2bf(hi) << 16); }
; __device__ __forceinline__ int nat_dim(int p) { return (p >> 1) + 64 * (p & 1); }
; template <int MAP, bool KS, bool KPERM = false>
; __device__ __forceinline__ void p0_transpose_item(const float* W, int K, int Nsrc, int nblk, bf16* WT, const float* ksA, const float* ksB, int ksplit, LAS float* scr, int item, int lane) {
;     const int kb = item / nblk, nb = item % nblk, k0 = 64 * kb, n0 = 32 * nb;
;     const int nr = n0 + (lane & 31); const int sc = MAP == 1 ? src_col_in(nr) : (MAP == 2 ? nat_dim(nr) : nr);
;     float v[32];
; #pragma unroll
;     for (int i = 0; i < 32; ++i) { const int k = k0 + 2 * i + (lane >> 5); const int ksrc = KPERM ? ((k & ~127) + nat_dim(k & 127)) : k;
;         v[i] = sc >= 0 ? W[(size_t)ksrc * Nsrc + sc] : 0.f; }
; #pragma unroll
;     for (int i = 0; i < 32; ++i) { const int kk = 2 * i + (lane >> 5); const int k = k0 + kk;
;         if (KS) v[i] *= (k < ksplit ? ksA[k] : ksB[k - ksplit]);
;         scr[kk * 33 + (lane & 31)] = v[i]; }
;     LDS_WAIT(); asm volatile("" ::: "memory");
;     const int c = lane & 7;
; #pragma unroll
;     for (int j = 0; j < 4; ++j) { const int n = (lane >> 3) + 8 * j; const LAS float* s = scr + (8 * c) * 33 + n;
;         v4u o; o.x = pk2(s[0 * 33], s[1 * 33]); o.y = pk2(s[2 * 33], s[3 * 33]); o.z = pk2(s[4 * 33], s[5 * 33]); o.w = pk2(s[6 * 33], s[7 * 33]);
;         *(GAS v4u*)(WT + (size_t)(n0 + n) * K + k0 + 8 * c) = o; }
;     LDS_WAIT(); asm volatile("" ::: "memory");
; __global__ void __launch_bounds__(NWAVES * 64, 2) hybrid_fwd(Args args) {
;     ...
;                 else p0_transpose_item<0, true>(args.in[13] + (size_t)l * DM * DM, DM, DM, DM / 32, (bf16*)(ws + WS_WO + l * SZ_WO), args.in[6] + l * 2048, args.in[12] + l * 2048, 2048, scr, r, lane); continue; } r -= I_O;
	s_add_u32 s8, s54, 0x3000
	s_addc_u32 s9, s55, 0
	global_load_dwordx4 v[176:179], v75, s[8:9]
	s_add_u32 s8, s8, 0x8000
	s_addc_u32 s9, s9, 0
	global_load_dwordx4 v[180:183], v75, s[8:9]
	s_add_u32 s8, s8, 0x8000
	s_addc_u32 s9, s9, 0
	global_load_dwordx4 v[184:187], v75, s[8:9]
	s_add_u32 s8, s8, 0x8000
	s_addc_u32 s9, s9, 0
	global_load_dwordx4 v[188:191], v75, s[8:9]
	s_add_u32 s8, s8, 0x8000
	s_addc_u32 s9, s9, 0
	global_load_dwordx4 v[192:195], v75, s[8:9]
	s_add_u32 s8, s8, 0x8000
	s_addc_u32 s9, s9, 0
	global_load_dwordx4 v[196:199], v75, s[8:9]
	s_add_u32 s8, s8, 0x8000
	s_addc_u32 s9, s9, 0
	global_load_dwordx4 v[200:203], v75, s[8:9]
	s_add_u32 s8, s8, 0x8000
	s_addc_u32 s9, s9, 0
	global_load_dwordx4 v[204:207], v75, s[8:9]
	s_add_u32 s6, s56, 0x800000
	s_addc_u32 s7, s57, 0
	ds_read_b32 v226, v113
	ds_read_b32 v227, v113 offset:512
	ds_read_b32 v228, v113 offset:1024
	ds_read_b32 v229, v113 offset:1536
	ds_read_b32 v230, v113 offset:2048
	ds_read_b32 v231, v113 offset:2560
	ds_read_b32 v232, v113 offset:3072
	ds_read_b32 v233, v113 offset:3584
	s_waitcnt lgkmcnt(0)
	v_bfe_u32 v120, v226, 16, 1
	v_bfe_u32 v121, v227, 16, 1
	v_bfe_u32 v122, v228, 16, 1
	v_bfe_u32 v123, v229, 16, 1
	v_bfe_u32 v124, v230, 16, 1
	v_bfe_u32 v125, v231, 16, 1
	v_bfe_u32 v126, v232, 16, 1
	v_bfe_u32 v127, v233, 16, 1
	v_add3_u32 v226, v226, v120, s63
	v_add3_u32 v227, v227, v121, s63
	v_add3_u32 v228, v228, v122, s63
	v_add3_u32 v229, v229, v123, s63
	v_add3_u32 v230, v230, v124, s63
	v_add3_u32 v231, v231, v125, s63
	v_add3_u32 v232, v232, v126, s63
	v_add3_u32 v233, v233, v127, s63
	v_perm_b32 v242, v227, v226, s64
	v_perm_b32 v243, v229, v228, s64
	v_perm_b32 v244, v231, v230, s64
	v_perm_b32 v245, v233, v232, s64
	s_nop 0
	global_store_dwordx4 v83, v[242:245], s[6:7]
	ds_read_b32 v226, v115
	ds_read_b32 v227, v115 offset:512
	ds_read_b32 v228, v115 offset:1024
	ds_read_b32 v229, v115 offset:1536
	ds_read_b32 v230, v115 offset:2048
	ds_read_b32 v231, v115 offset:2560
	ds_read_b32 v232, v115 offset:3072
	ds_read_b32 v233, v115 offset:3584
	s_waitcnt lgkmcnt(0)
	v_bfe_u32 v120, v226, 16, 1
	v_bfe_u32 v121, v227, 16, 1
	v_bfe_u32 v122, v228, 16, 1
	v_bfe_u32 v123, v229, 16, 1
	v_bfe_u32 v124, v230, 16, 1
	v_bfe_u32 v125, v231, 16, 1
	v_bfe_u32 v126, v232, 16, 1
	v_bfe_u32 v127, v233, 16, 1
	v_add3_u32 v226, v226, v120, s63
	v_add3_u32 v227, v227, v121, s63
	v_add3_u32 v228, v228, v122, s63
	v_add3_u32 v229, v229, v123, s63
	v_add3_u32 v230, v230, v124, s63
	v_add3_u32 v231, v231, v125, s63
	v_add3_u32 v232, v232, v126, s63
	v_add3_u32 v233, v233, v127, s63
	v_perm_b32 v242, v227, v226, s64
	v_perm_b32 v243, v229, v228, s64
	v_perm_b32 v244, v231, v230, s64
	v_perm_b32 v245, v233, v232, s64
	s_nop 0
	global_store_dwordx4 v84, v[242:245], s[6:7]
	ds_read_b32 v226, v117
	ds_read_b32 v227, v117 offset:512
	ds_read_b32 v228, v117 offset:1024
	ds_read_b32 v229, v117 offset:1536
	ds_read_b32 v230, v117 offset:2048
	ds_read_b32 v231, v117 offset:2560
	ds_read_b32 v232, v117 offset:3072
	ds_read_b32 v233, v117 offset:3584
	s_waitcnt lgkmcnt(0)
	v_bfe_u32 v120, v226, 16, 1
	v_bfe_u32 v121, v227, 16, 1
	v_bfe_u32 v122, v228, 16, 1
	v_bfe_u32 v123, v229, 16, 1
	v_bfe_u32 v124, v230, 16, 1
	v_bfe_u32 v125, v231, 16, 1
	v_bfe_u32 v126, v232, 16, 1
	v_bfe_u32 v127, v233, 16, 1
	v_add3_u32 v226, v226, v120, s63
	v_add3_u32 v227, v227, v121, s63
	v_add3_u32 v228, v228, v122, s63
	v_add3_u32 v229, v229, v123, s63
	v_add3_u32 v230, v230, v124, s63
	v_add3_u32 v231, v231, v125, s63
	v_add3_u32 v232, v232, v126, s63
	v_add3_u32 v233, v233, v127, s63
	v_perm_b32 v242, v227, v226, s64
	v_perm_b32 v243, v229, v228, s64
	v_perm_b32 v244, v231, v230, s64
	v_perm_b32 v245, v233, v232, s64
	s_nop 0
	global_store_dwordx4 v85, v[242:245], s[6:7]
	ds_read_b32 v226, v119
	ds_read_b32 v227, v119 offset:512
	ds_read_b32 v228, v119 offset:1024
	ds_read_b32 v229, v119 offset:1536
	ds_read_b32 v230, v119 offset:2048
	ds_read_b32 v231, v119 offset:2560
	ds_read_b32 v232, v119 offset:3072
	ds_read_b32 v233, v119 offset:3584
	s_waitcnt lgkmcnt(0)
	v_bfe_u32 v120, v226, 16, 1
	v_bfe_u32 v121, v227, 16, 1
	v_bfe_u32 v122, v228, 16, 1
	v_bfe_u32 v123, v229, 16, 1
	v_bfe_u32 v124, v230, 16, 1
	v_bfe_u32 v125, v231, 16, 1
	v_bfe_u32 v126, v232, 16, 1
	v_bfe_u32 v127, v233, 16, 1
	v_add3_u32 v226, v226, v120, s63
	v_add3_u32 v227, v227, v121, s63
	v_add3_u32 v228, v228, v122, s63
	v_add3_u32 v229, v229, v123, s63
	v_add3_u32 v230, v230, v124, s63
	v_add3_u32 v231, v231, v125, s63
	v_add3_u32 v232, v232, v126, s63
	v_add3_u32 v233, v233, v127, s63
	v_perm_b32 v242, v227, v226, s64
	v_perm_b32 v243, v229, v228, s64
	v_perm_b32 v244, v231, v230, s64
	v_perm_b32 v245, v233, v232, s64
	s_nop 0
	global_store_dwordx4 v86, v[242:245], s[6:7]
	s_waitcnt vmcnt(16)
	v_mul_f32_e32 v144, v58, v144
	v_mul_f32_e32 v145, v58, v145
	v_mul_f32_e32 v146, v58, v146
	v_mul_f32_e32 v147, v58, v147
	ds_write_b128 v209, v[144:147]
	v_mul_f32_e32 v148, v59, v148
	v_mul_f32_e32 v149, v59, v149
	v_mul_f32_e32 v150, v59, v150
	v_mul_f32_e32 v151, v59, v151
	ds_write_b128 v209, v[148:151] offset:1024
	v_mul_f32_e32 v152, v60, v152
	v_mul_f32_e32 v153, v60, v153
	v_mul_f32_e32 v154, v60, v154
	v_mul_f32_e32 v155, v60, v155
	ds_write_b128 v209, v[152:155] offset:2048
	v_mul_f32_e32 v156, v61, v156
	v_mul_f32_e32 v157, v61, v157
	v_mul_f32_e32 v158, v61, v158
	v_mul_f32_e32 v159, v61, v159
	ds_write_b128 v209, v[156:159] offset:3072
	v_mul_f32_e32 v160, v62, v160
	v_mul_f32_e32 v161, v62, v161
	v_mul_f32_e32 v162, v62, v162
	v_mul_f32_e32 v163, v62, v163
	ds_write_b128 v209, v[160:163] offset:4096
	v_mul_f32_e32 v164, v63, v164
	v_mul_f32_e32 v165, v63, v165
	v_mul_f32_e32 v166, v63, v166
	v_mul_f32_e32 v167, v63, v167
	ds_write_b128 v209, v[164:167] offset:5120
	v_mul_f32_e32 v168, v64, v168
	v_mul_f32_e32 v169, v64, v169
	v_mul_f32_e32 v170, v64, v170
	v_mul_f32_e32 v171, v64, v171
	ds_write_b128 v209, v[168:171] offset:6144
	v_mul_f32_e32 v172, v65, v172
	v_mul_f32_e32 v173, v65, v173
	v_mul_f32_e32 v174, v65, v174
	v_mul_f32_e32 v175, v65, v175
	ds_write_b128 v209, v[172:175] offset:7168
	s_waitcnt lgkmcnt(0)
	s_barrier
; #define GAS __attribute__((address_space(1)))
; #define LAS __attribute__((address_space(3)))
; #define LDS_WAIT() asm volatile("s_waitcnt lgkmcnt(0)" ::: "memory")
; __device__ __forceinline__ unsigned pk2(float lo, float hi) { return f2bf(lo) | (f2bf(hi) << 16); }
; __device__ __forceinline__ int nat_dim(int p) { return (p >> 1) + 64 * (p & 1); }
; template <int MAP, bool KS, bool KPERM = false>
; __device__ __forceinline__ void p0_transpose_item(const float* W, int K, int Nsrc, int nblk, bf16* WT, const float* ksA, const float* ksB, int ksplit, LAS float* scr, int item, int lane) {
;     const int kb = item / nblk, nb = item % nblk, k0 = 64 * kb, n0 = 32 * nb;
;     const int nr = n0 + (lane & 31); const int sc = MAP == 1 ? src_col_in(nr) : (MAP == 2 ? nat_dim(nr) : nr);
;     float v[32];
; #pragma unroll
;     for (int i = 0; i < 32; ++i) { const int k = k0 + 2 * i + (lane >> 5); const int ksrc = KPERM ? ((k & ~127) + nat_dim(k & 127)) : k;
;         v[i] = sc >= 0 ? W[(size_t)ksrc * Nsrc + sc] : 0.f; }
; #pragma unroll
;     for (int i = 0; i < 32; ++i) { const int kk = 2 * i + (lane >> 5); const int k = k0 + kk;
;         if (KS) v[i] *= (k < ksplit ? ksA[k] : ksB[k - ksplit]);
;         scr[kk * 33 + (lane & 31)] = v[i]; }
;     LDS_WAIT(); asm volatile("" ::: "memory");
;     const int c = lane & 7;
; #pragma unroll
;     for (int j = 0; j < 4; ++j) { const int n = (lane >> 3) + 8 * j; const LAS float* s = scr + (8 * c) * 33 + n;
;         v4u o; o.x = pk2(s[0 * 33], s[1 * 33]); o.y = pk2(s[2 * 33], s[3 * 33]); o.z = pk2(s[4 * 33], s[5 * 33]); o.w = pk2(s[6 * 33], s[7 * 33]);
;         *(GAS v4u*)(WT + (size_t)(n0 + n) * K + k0 + 8 * c) = o; }
;     LDS_WAIT(); asm volatile("" ::: "memory");
; __global__ void __launch_bounds__(NWAVES * 64, 2) hybrid_fwd(Args args) {
;     ...
;                 else p0_transpose_item<0, true>(args.in[13] + (size_t)l * DM * DM, DM, DM, DM / 32, (bf16*)(ws + WS_WO + l * SZ_WO), args.in[6] + l * 2048, args.in[12] + l * 2048, 2048, scr, r, lane); continue; } r -= I_O;
	s_mov_b64 s[8:9], s[58:59]
	global_load_dwordx4 v[144:147], v75, s[8:9]
	s_add_u32 s8, s8, 0x8000
	s_addc_u32 s9, s9, 0
	global_load_dwordx4 v[148:151], v75, s[8:9]
	s_add_u32 s8, s8, 0x8000
	s_addc_u32 s9, s9, 0
	global_load_dwordx4 v[152:155], v75, s[8:9]
	s_add_u32 s8, s8, 0x8000
	s_addc_u32 s9, s9, 0
	global_load_dwordx4 v[156:159], v75, s[8:9]
	s_add_u32 s8, s8, 0x8000
	s_addc_u32 s9, s9, 0
	global_load_dwordx4 v[160:163], v75, s[8:9]
	s_add_u32 s8, s8, 0x8000
	s_addc_u32 s9, s9, 0
	global_load_dwordx4 v[164:167], v75, s[8:9]
	s_add_u32 s8, s8, 0x8000
	s_addc_u32 s9, s9, 0
	global_load_dwordx4 v[168:171], v75, s[8:9]
	s_add_u32 s8, s8, 0x8000
	s_addc_u32 s9, s9, 0
	global_load_dwordx4 v[172:175], v75, s[8:9]
	s_add_u32 s6, s56, 0x1000000
	s_addc_u32 s7, s57, 0
	ds_read_b32 v226, v112
	ds_read_b32 v227, v112 offset:512
	ds_read_b32 v228, v112 offset:1024
	ds_read_b32 v229, v112 offset:1536
	ds_read_b32 v230, v112 offset:2048
	ds_read_b32 v231, v112 offset:2560
	ds_read_b32 v232, v112 offset:3072
	ds_read_b32 v233, v112 offset:3584
	s_waitcnt lgkmcnt(0)
	v_bfe_u32 v120, v226, 16, 1
	v_bfe_u32 v121, v227, 16, 1
	v_bfe_u32 v122, v228, 16, 1
	v_bfe_u32 v123, v229, 16, 1
	v_bfe_u32 v124, v230, 16, 1
	v_bfe_u32 v125, v231, 16, 1
	v_bfe_u32 v126, v232, 16, 1
	v_bfe_u32 v127, v233, 16, 1
	v_add3_u32 v226, v226, v120, s63
	v_add3_u32 v227, v227, v121, s63
	v_add3_u32 v228, v228, v122, s63
	v_add3_u32 v229, v229, v123, s63
	v_add3_u32 v230, v230, v124, s63
	v_add3_u32 v231, v231, v125, s63
	v_add3_u32 v232, v232, v126, s63
	v_add3_u32 v233, v233, v127, s63
	v_perm_b32 v242, v227, v226, s64
	v_perm_b32 v243, v229, v228, s64
	v_perm_b32 v244, v231, v230, s64
	v_perm_b32 v245, v233, v232, s64
	s_nop 0
	global_store_dwordx4 v83, v[242:245], s[6:7]
	ds_read_b32 v226, v114
	ds_read_b32 v227, v114 offset:512
	ds_read_b32 v228, v114 offset:1024
	ds_read_b32 v229, v114 offset:1536
	ds_read_b32 v230, v114 offset:2048
	ds_read_b32 v231, v114 offset:2560
	ds_read_b32 v232, v114 offset:3072
	ds_read_b32 v233, v114 offset:3584
	s_waitcnt lgkmcnt(0)
	v_bfe_u32 v120, v226, 16, 1
	v_bfe_u32 v121, v227, 16, 1
	v_bfe_u32 v122, v228, 16, 1
	v_bfe_u32 v123, v229, 16, 1
	v_bfe_u32 v124, v230, 16, 1
	v_bfe_u32 v125, v231, 16, 1
	v_bfe_u32 v126, v232, 16, 1
	v_bfe_u32 v127, v233, 16, 1
	v_add3_u32 v226, v226, v120, s63
	v_add3_u32 v227, v227, v121, s63
	v_add3_u32 v228, v228, v122, s63
	v_add3_u32 v229, v229, v123, s63
	v_add3_u32 v230, v230, v124, s63
	v_add3_u32 v231, v231, v125, s63
	v_add3_u32 v232, v232, v126, s63
	v_add3_u32 v233, v233, v127, s63
	v_perm_b32 v242, v227, v226, s64
	v_perm_b32 v243, v229, v228, s64
	v_perm_b32 v244, v231, v230, s64
	v_perm_b32 v245, v233, v232, s64
	s_nop 0
	global_store_dwordx4 v84, v[242:245], s[6:7]
	ds_read_b32 v226, v116
	ds_read_b32 v227, v116 offset:512
	ds_read_b32 v228, v116 offset:1024
	ds_read_b32 v229, v116 offset:1536
	ds_read_b32 v230, v116 offset:2048
	ds_read_b32 v231, v116 offset:2560
	ds_read_b32 v232, v116 offset:3072
	ds_read_b32 v233, v116 offset:3584
	s_waitcnt lgkmcnt(0)
	v_bfe_u32 v120, v226, 16, 1
	v_bfe_u32 v121, v227, 16, 1
	v_bfe_u32 v122, v228, 16, 1
	v_bfe_u32 v123, v229, 16, 1
	v_bfe_u32 v124, v230, 16, 1
	v_bfe_u32 v125, v231, 16, 1
	v_bfe_u32 v126, v232, 16, 1
	v_bfe_u32 v127, v233, 16, 1
	v_add3_u32 v226, v226, v120, s63
	v_add3_u32 v227, v227, v121, s63
	v_add3_u32 v228, v228, v122, s63
	v_add3_u32 v229, v229, v123, s63
	v_add3_u32 v230, v230, v124, s63
	v_add3_u32 v231, v231, v125, s63
	v_add3_u32 v232, v232, v126, s63
	v_add3_u32 v233, v233, v127, s63
	v_perm_b32 v242, v227, v226, s64
	v_perm_b32 v243, v229, v228, s64
	v_perm_b32 v244, v231, v230, s64
	v_perm_b32 v245, v233, v232, s64
	s_nop 0
	global_store_dwordx4 v85, v[242:245], s[6:7]
	ds_read_b32 v226, v118
	ds_read_b32 v227, v118 offset:512
	ds_read_b32 v228, v118 offset:1024
	ds_read_b32 v229, v118 offset:1536
	ds_read_b32 v230, v118 offset:2048
	ds_read_b32 v231, v118 offset:2560
	ds_read_b32 v232, v118 offset:3072
	ds_read_b32 v233, v118 offset:3584
	s_waitcnt lgkmcnt(0)
	v_bfe_u32 v120, v226, 16, 1
	v_bfe_u32 v121, v227, 16, 1
	v_bfe_u32 v122, v228, 16, 1
	v_bfe_u32 v123, v229, 16, 1
	v_bfe_u32 v124, v230, 16, 1
	v_bfe_u32 v125, v231, 16, 1
	v_bfe_u32 v126, v232, 16, 1
	v_bfe_u32 v127, v233, 16, 1
	v_add3_u32 v226, v226, v120, s63
	v_add3_u32 v227, v227, v121, s63
	v_add3_u32 v228, v228, v122, s63
	v_add3_u32 v229, v229, v123, s63
	v_add3_u32 v230, v230, v124, s63
	v_add3_u32 v231, v231, v125, s63
	v_add3_u32 v232, v232, v126, s63
	v_add3_u32 v233, v233, v127, s63
	v_perm_b32 v242, v227, v226, s64
	v_perm_b32 v243, v229, v228, s64
	v_perm_b32 v244, v231, v230, s64
	v_perm_b32 v245, v233, v232, s64
	s_nop 0
	global_store_dwordx4 v86, v[242:245], s[6:7]
	s_waitcnt vmcnt(16)
	v_mul_f32_e32 v176, v58, v176
	v_mul_f32_e32 v177, v58, v177
	v_mul_f32_e32 v178, v58, v178
	v_mul_f32_e32 v179, v58, v179
	ds_write_b128 v210, v[176:179]
	v_mul_f32_e32 v180, v59, v180
	v_mul_f32_e32 v181, v59, v181
	v_mul_f32_e32 v182, v59, v182
	v_mul_f32_e32 v183, v59, v183
	ds_write_b128 v210, v[180:183] offset:1024
	v_mul_f32_e32 v184, v60, v184
	v_mul_f32_e32 v185, v60, v185
	v_mul_f32_e32 v186, v60, v186
	v_mul_f32_e32 v187, v60, v187
	ds_write_b128 v210, v[184:187] offset:2048
	v_mul_f32_e32 v188, v61, v188
	v_mul_f32_e32 v189, v61, v189
	v_mul_f32_e32 v190, v61, v190
	v_mul_f32_e32 v191, v61, v191
	ds_write_b128 v210, v[188:191] offset:3072
	v_mul_f32_e32 v192, v62, v192
	v_mul_f32_e32 v193, v62, v193
	v_mul_f32_e32 v194, v62, v194
	v_mul_f32_e32 v195, v62, v195
	ds_write_b128 v210, v[192:195] offset:4096
	v_mul_f32_e32 v196, v63, v196
	v_mul_f32_e32 v197, v63, v197
	v_mul_f32_e32 v198, v63, v198
	v_mul_f32_e32 v199, v63, v199
	ds_write_b128 v210, v[196:199] offset:5120
	v_mul_f32_e32 v200, v64, v200
	v_mul_f32_e32 v201, v64, v201
	v_mul_f32_e32 v202, v64, v202
	v_mul_f32_e32 v203, v64, v203
	ds_write_b128 v210, v[200:203] offset:6144
	v_mul_f32_e32 v204, v65, v204
	v_mul_f32_e32 v205, v65, v205
	v_mul_f32_e32 v206, v65, v206
	v_mul_f32_e32 v207, v65, v207
	ds_write_b128 v210, v[204:207] offset:7168
	s_waitcnt lgkmcnt(0)
	s_barrier
; #define GAS __attribute__((address_space(1)))
; #define LAS __attribute__((address_space(3)))
; #define LDS_WAIT() asm volatile("s_waitcnt lgkmcnt(0)" ::: "memory")
; __device__ __forceinline__ unsigned pk2(float lo, float hi) { return f2bf(lo) | (f2bf(hi) << 16); }
; __device__ __forceinline__ int nat_dim(int p) { return (p >> 1) + 64 * (p & 1); }
; template <int MAP, bool KS, bool KPERM = false>
; __device__ __forceinline__ void p0_transpose_item(const float* W, int K, int Nsrc, int nblk, bf16* WT, const float* ksA, const float* ksB, int ksplit, LAS float* scr, int item, int lane) {
;     const int kb = item / nblk, nb = item % nblk, k0 = 64 * kb, n0 = 32 * nb;
;     const int nr = n0 + (lane & 31); const int sc = MAP == 1 ? src_col_in(nr) : (MAP == 2 ? nat_dim(nr) : nr);
;     float v[32];
; #pragma unroll
;     for (int i = 0; i < 32; ++i) { const int k = k0 + 2 * i + (lane >> 5); const int ksrc = KPERM ? ((k & ~127) + nat_dim(k & 127)) : k;
;         v[i] = sc >= 0 ? W[(size_t)ksrc * Nsrc + sc] : 0.f; }
; #pragma unroll
;     for (int i = 0; i < 32; ++i) { const int kk = 2 * i + (lane >> 5); const int k = k0 + kk;
;         if (KS) v[i] *= (k < ksplit ? ksA[k] : ksB[k - ksplit]);
;         scr[kk * 33 + (lane & 31)] = v[i]; }
;     LDS_WAIT(); asm volatile("" ::: "memory");
;     const int c = lane & 7;
; #pragma unroll
;     for (int j = 0; j < 4; ++j) { const int n = (lane >> 3) + 8 * j; const LAS float* s = scr + (8 * c) * 33 + n;
;         v4u o; o.x = pk2(s[0 * 33], s[1 * 33]); o.y = pk2(s[2 * 33], s[3 * 33]); o.z = pk2(s[4 * 33], s[5 * 33]); o.w = pk2(s[6 * 33], s[7 * 33]);
;         *(GAS v4u*)(WT + (size_t)(n0 + n) * K + k0 + 8 * c) = o; }
;     LDS_WAIT(); asm volatile("" ::: "memory");
; __global__ void __launch_bounds__(NWAVES * 64, 2) hybrid_fwd(Args args) {
;     ...
;                 else p0_transpose_item<0, true>(args.in[13] + (size_t)l * DM * DM, DM, DM, DM / 32, (bf16*)(ws + WS_WO + l * SZ_WO), args.in[6] + l * 2048, args.in[12] + l * 2048, 2048, scr, r, lane); continue; } r -= I_O;
	s_add_u32 s8, s58, 0x1000
	s_addc_u32 s9, s59, 0
	global_load_dwordx4 v[176:179], v75, s[8:9]
	s_add_u32 s8, s8, 0x8000
	s_addc_u32 s9, s9, 0
	global_load_dwordx4 v[180:183], v75, s[8:9]
	s_add_u32 s8, s8, 0x8000
	s_addc_u32 s9, s9, 0
	global_load_dwordx4 v[184:187], v75, s[8:9]
	s_add_u32 s8, s8, 0x8000
	s_addc_u32 s9, s9, 0
	global_load_dwordx4 v[188:191], v75, s[8:9]
	s_add_u32 s8, s8, 0x8000
	s_addc_u32 s9, s9, 0
	global_load_dwordx4 v[192:195], v75, s[8:9]
	s_add_u32 s8, s8, 0x8000
	s_addc_u32 s9, s9, 0
	global_load_dwordx4 v[196:199], v75, s[8:9]
	s_add_u32 s8, s8, 0x8000
	s_addc_u32 s9, s9, 0
	global_load_dwordx4 v[200:203], v75, s[8:9]
	s_add_u32 s8, s8, 0x8000
	s_addc_u32 s9, s9, 0
	global_load_dwordx4 v[204:207], v75, s[8:9]
	s_add_u32 s6, s56, 0x1800000
	s_addc_u32 s7, s57, 0
	ds_read_b32 v226, v113
	ds_read_b32 v227, v113 offset:512
	ds_read_b32 v228, v113 offset:1024
	ds_read_b32 v229, v113 offset:1536
	ds_read_b32 v230, v113 offset:2048
	ds_read_b32 v231, v113 offset:2560
	ds_read_b32 v232, v113 offset:3072
	ds_read_b32 v233, v113 offset:3584
	s_waitcnt lgkmcnt(0)
	v_bfe_u32 v120, v226, 16, 1
	v_bfe_u32 v121, v227, 16, 1
	v_bfe_u32 v122, v228, 16, 1
	v_bfe_u32 v123, v229, 16, 1
	v_bfe_u32 v124, v230, 16, 1
	v_bfe_u32 v125, v231, 16, 1
	v_bfe_u32 v126, v232, 16, 1
	v_bfe_u32 v127, v233, 16, 1
	v_add3_u32 v226, v226, v120, s63
	v_add3_u32 v227, v227, v121, s63
	v_add3_u32 v228, v228, v122, s63
	v_add3_u32 v229, v229, v123, s63
	v_add3_u32 v230, v230, v124, s63
	v_add3_u32 v231, v231, v125, s63
	v_add3_u32 v232, v232, v126, s63
	v_add3_u32 v233, v233, v127, s63
	v_perm_b32 v242, v227, v226, s64
	v_perm_b32 v243, v229, v228, s64
	v_perm_b32 v244, v231, v230, s64
	v_perm_b32 v245, v233, v232, s64
	s_nop 0
	global_store_dwordx4 v83, v[242:245], s[6:7]
	ds_read_b32 v226, v115
	ds_read_b32 v227, v115 offset:512
	ds_read_b32 v228, v115 offset:1024
	ds_read_b32 v229, v115 offset:1536
	ds_read_b32 v230, v115 offset:2048
	ds_read_b32 v231, v115 offset:2560
	ds_read_b32 v232, v115 offset:3072
	ds_read_b32 v233, v115 offset:3584
	s_waitcnt lgkmcnt(0)
	v_bfe_u32 v120, v226, 16, 1
	v_bfe_u32 v121, v227, 16, 1
	v_bfe_u32 v122, v228, 16, 1
	v_bfe_u32 v123, v229, 16, 1
	v_bfe_u32 v124, v230, 16, 1
	v_bfe_u32 v125, v231, 16, 1
	v_bfe_u32 v126, v232, 16, 1
	v_bfe_u32 v127, v233, 16, 1
	v_add3_u32 v226, v226, v120, s63
	v_add3_u32 v227, v227, v121, s63
	v_add3_u32 v228, v228, v122, s63
	v_add3_u32 v229, v229, v123, s63
	v_add3_u32 v230, v230, v124, s63
	v_add3_u32 v231, v231, v125, s63
	v_add3_u32 v232, v232, v126, s63
	v_add3_u32 v233, v233, v127, s63
	v_perm_b32 v242, v227, v226, s64
	v_perm_b32 v243, v229, v228, s64
	v_perm_b32 v244, v231, v230, s64
	v_perm_b32 v245, v233, v232, s64
	s_nop 0
	global_store_dwordx4 v84, v[242:245], s[6:7]
	ds_read_b32 v226, v117
	ds_read_b32 v227, v117 offset:512
	ds_read_b32 v228, v117 offset:1024
	ds_read_b32 v229, v117 offset:1536
	ds_read_b32 v230, v117 offset:2048
	ds_read_b32 v231, v117 offset:2560
	ds_read_b32 v232, v117 offset:3072
	ds_read_b32 v233, v117 offset:3584
	s_waitcnt lgkmcnt(0)
	v_bfe_u32 v120, v226, 16, 1
	v_bfe_u32 v121, v227, 16, 1
	v_bfe_u32 v122, v228, 16, 1
	v_bfe_u32 v123, v229, 16, 1
	v_bfe_u32 v124, v230, 16, 1
	v_bfe_u32 v125, v231, 16, 1
	v_bfe_u32 v126, v232, 16, 1
	v_bfe_u32 v127, v233, 16, 1
	v_add3_u32 v226, v226, v120, s63
	v_add3_u32 v227, v227, v121, s63
	v_add3_u32 v228, v228, v122, s63
	v_add3_u32 v229, v229, v123, s63
	v_add3_u32 v230, v230, v124, s63
	v_add3_u32 v231, v231, v125, s63
	v_add3_u32 v232, v232, v126, s63
	v_add3_u32 v233, v233, v127, s63
	v_perm_b32 v242, v227, v226, s64
	v_perm_b32 v243, v229, v228, s64
	v_perm_b32 v244, v231, v230, s64
	v_perm_b32 v245, v233, v232, s64
	s_nop 0
	global_store_dwordx4 v85, v[242:245], s[6:7]
	ds_read_b32 v226, v119
	ds_read_b32 v227, v119 offset:512
	ds_read_b32 v228, v119 offset:1024
	ds_read_b32 v229, v119 offset:1536
	ds_read_b32 v230, v119 offset:2048
	ds_read_b32 v231, v119 offset:2560
	ds_read_b32 v232, v119 offset:3072
	ds_read_b32 v233, v119 offset:3584
	s_waitcnt lgkmcnt(0)
	v_bfe_u32 v120, v226, 16, 1
	v_bfe_u32 v121, v227, 16, 1
	v_bfe_u32 v122, v228, 16, 1
	v_bfe_u32 v123, v229, 16, 1
	v_bfe_u32 v124, v230, 16, 1
	v_bfe_u32 v125, v231, 16, 1
	v_bfe_u32 v126, v232, 16, 1
	v_bfe_u32 v127, v233, 16, 1
	v_add3_u32 v226, v226, v120, s63
	v_add3_u32 v227, v227, v121, s63
	v_add3_u32 v228, v228, v122, s63
	v_add3_u32 v229, v229, v123, s63
	v_add3_u32 v230, v230, v124, s63
	v_add3_u32 v231, v231, v125, s63
	v_add3_u32 v232, v232, v126, s63
	v_add3_u32 v233, v233, v127, s63
	v_perm_b32 v242, v227, v226, s64
	v_perm_b32 v243, v229, v228, s64
	v_perm_b32 v244, v231, v230, s64
	v_perm_b32 v245, v233, v232, s64
	s_nop 0
	global_store_dwordx4 v86, v[242:245], s[6:7]
	s_waitcnt vmcnt(16)
	v_mul_f32_e32 v144, v66, v144
	v_mul_f32_e32 v145, v66, v145
	v_mul_f32_e32 v146, v66, v146
	v_mul_f32_e32 v147, v66, v147
	ds_write_b128 v209, v[144:147]
	v_mul_f32_e32 v148, v67, v148
	v_mul_f32_e32 v149, v67, v149
	v_mul_f32_e32 v150, v67, v150
	v_mul_f32_e32 v151, v67, v151
	ds_write_b128 v209, v[148:151] offset:1024
	v_mul_f32_e32 v152, v68, v152
	v_mul_f32_e32 v153, v68, v153
	v_mul_f32_e32 v154, v68, v154
	v_mul_f32_e32 v155, v68, v155
	ds_write_b128 v209, v[152:155] offset:2048
	v_mul_f32_e32 v156, v69, v156
	v_mul_f32_e32 v157, v69, v157
	v_mul_f32_e32 v158, v69, v158
	v_mul_f32_e32 v159, v69, v159
	ds_write_b128 v209, v[156:159] offset:3072
	v_mul_f32_e32 v160, v70, v160
	v_mul_f32_e32 v161, v70, v161
	v_mul_f32_e32 v162, v70, v162
	v_mul_f32_e32 v163, v70, v163
	ds_write_b128 v209, v[160:163] offset:4096
	v_mul_f32_e32 v164, v71, v164
	v_mul_f32_e32 v165, v71, v165
	v_mul_f32_e32 v166, v71, v166
	v_mul_f32_e32 v167, v71, v167
	ds_write_b128 v209, v[164:167] offset:5120
	v_mul_f32_e32 v168, v72, v168
	v_mul_f32_e32 v169, v72, v169
	v_mul_f32_e32 v170, v72, v170
	v_mul_f32_e32 v171, v72, v171
	ds_write_b128 v209, v[168:171] offset:6144
	v_mul_f32_e32 v172, v73, v172
	v_mul_f32_e32 v173, v73, v173
	v_mul_f32_e32 v174, v73, v174
	v_mul_f32_e32 v175, v73, v175
	ds_write_b128 v209, v[172:175] offset:7168
	s_waitcnt lgkmcnt(0)
	s_barrier
; #define GAS __attribute__((address_space(1)))
; #define LAS __attribute__((address_space(3)))
; #define LDS_WAIT() asm volatile("s_waitcnt lgkmcnt(0)" ::: "memory")
;     const int pr = item >> 1, kb = 2 * (pr / nblk) + (item & 1), nb = pr % nblk, k0 = 64 * kb, n0 = 32 * nb;
;     const int nr = n0 + (lane & 31); const int sc = MAP == 1 ? src_col_in(nr) : nr;
;     float v[32];
; #pragma unroll
;     for (int i = 0; i < 32; ++i) v[i] = sc >= 0 ? W[(size_t)(k0 + 2 * i + (lane >> 5)) * Nsrc + sc] : 0.f;
; #pragma unroll
;     for (int i = 0; i < 32; ++i) { const int k = k0 + 2 * i + (lane >> 5); float x = v[i] * wscale; if (KS) x *= (k < ksplit ? ksA[k] : ksB[k - ksplit]); scr[(2 * i + (lane >> 5)) * 33 + (lane & 31)] = x; }
;     LDS_WAIT(); asm volatile("" ::: "memory");
;     const int c = lane & 7;
; #pragma unroll
;     for (int j = 0; j < 4; ++j) { const int n = (lane >> 3) + 8 * j; const LAS float* s = scr + (8 * c) * 33 + n;
;         const unsigned long long o = (unsigned long long)pg8::pk4_fp8(s[0 * 33], s[1 * 33], s[2 * 33], s[3 * 33]) | ((unsigned long long)pg8::pk4_fp8(s[4 * 33], s[5 * 33], s[6 * 33], s[7 * 33]) << 32);
;         *(GAS unsigned long long*)(WT + (size_t)(n0 + n) * K + k0 + 8 * c) = o; }
;     LDS_WAIT(); asm volatile("" ::: "memory");
; }
	s_add_u32 s8, s58, 0x2000
	s_addc_u32 s9, s59, 0
	global_load_dwordx4 v[144:147], v75, s[8:9]
	s_add_u32 s8, s8, 0x8000
	s_addc_u32 s9, s9, 0
	global_load_dwordx4 v[148:151], v75, s[8:9]
	s_add_u32 s8, s8, 0x8000
	s_addc_u32 s9, s9, 0
	global_load_dwordx4 v[152:155], v75, s[8:9]
	s_add_u32 s8, s8, 0x8000
	s_addc_u32 s9, s9, 0
	global_load_dwordx4 v[156:159], v75, s[8:9]
	s_add_u32 s8, s8, 0x8000
	s_addc_u32 s9, s9, 0
	global_load_dwordx4 v[160:163], v75, s[8:9]
	s_add_u32 s8, s8, 0x8000
	s_addc_u32 s9, s9, 0
	global_load_dwordx4 v[164:167], v75, s[8:9]
	s_add_u32 s8, s8, 0x8000
	s_addc_u32 s9, s9, 0
	global_load_dwordx4 v[168:171], v75, s[8:9]
	s_add_u32 s8, s8, 0x8000
	s_addc_u32 s9, s9, 0
	global_load_dwordx4 v[172:175], v75, s[8:9]
	s_mov_b64 s[6:7], s[60:61]
	ds_read_b32 v226, v211
	ds_read_b32 v227, v211 offset:512
	ds_read_b32 v228, v211 offset:1024
	ds_read_b32 v229, v211 offset:1536
	ds_read_b32 v230, v211 offset:2048
	ds_read_b32 v231, v211 offset:2560
	ds_read_b32 v232, v211 offset:3072
	ds_read_b32 v233, v211 offset:3584
	ds_read_b32 v234, v211 offset:4096
	ds_read_b32 v235, v211 offset:4608
	ds_read_b32 v236, v211 offset:5120
	ds_read_b32 v237, v211 offset:5632
	ds_read_b32 v238, v211 offset:6144
	ds_read_b32 v239, v211 offset:6656
	ds_read_b32 v240, v211 offset:7168
	ds_read_b32 v241, v211 offset:7680
	s_waitcnt lgkmcnt(0)
	v_max_f32_e32 v226, v226, v226
	v_max_f32_e32 v227, v227, v227
	v_max_f32_e32 v228, v228, v228
	v_max_f32_e32 v229, v229, v229
	v_max_f32_e32 v230, v230, v230
	v_max_f32_e32 v231, v231, v231
	v_max_f32_e32 v232, v232, v232
	v_max_f32_e32 v233, v233, v233
	v_max_f32_e32 v234, v234, v234
	v_max_f32_e32 v235, v235, v235
	v_max_f32_e32 v236, v236, v236
	v_max_f32_e32 v237, v237, v237
	v_max_f32_e32 v238, v238, v238
	v_max_f32_e32 v239, v239, v239
	v_max_f32_e32 v240, v240, v240
	v_max_f32_e32 v241, v241, v241
	v_med3_f32 v226, v226, s62, v95
	v_med3_f32 v227, v227, s62, v95
	v_med3_f32 v228, v228, s62, v95
	v_med3_f32 v229, v229, s62, v95
	v_med3_f32 v230, v230, s62, v95
	v_med3_f32 v231, v231, s62, v95
	v_med3_f32 v232, v232, s62, v95
	v_med3_f32 v233, v233, s62, v95
	v_med3_f32 v234, v234, s62, v95
	v_med3_f32 v235, v235, s62, v95
	v_med3_f32 v236, v236, s62, v95
	v_med3_f32 v237, v237, s62, v95
	v_med3_f32 v238, v238, s62, v95
	v_med3_f32 v239, v239, s62, v95
	v_med3_f32 v240, v240, s62, v95
	v_med3_f32 v241, v241, s62, v95
	v_mov_b32_e32 v242, 0
	v_mov_b32_e32 v243, 0
	v_mov_b32_e32 v244, 0
	v_mov_b32_e32 v245, 0
	v_cvt_pk_fp8_f32 v242, v226, v227
	v_cvt_pk_fp8_f32 v243, v230, v231
	v_cvt_pk_fp8_f32 v244, v234, v235
	v_cvt_pk_fp8_f32 v245, v238, v239
	v_cvt_pk_fp8_f32 v242, v228, v229 op_sel:[0,0,1]
	v_cvt_pk_fp8_f32 v243, v232, v233 op_sel:[0,0,1]
	v_cvt_pk_fp8_f32 v244, v236, v237 op_sel:[0,0,1]
	v_cvt_pk_fp8_f32 v245, v240, v241 op_sel:[0,0,1]
	s_nop 0
	global_store_dwordx4 v77, v[242:245], s[6:7]
	ds_read_b32 v226, v213
	ds_read_b32 v227, v213 offset:512
	ds_read_b32 v228, v213 offset:1024
	ds_read_b32 v229, v213 offset:1536
	ds_read_b32 v230, v213 offset:2048
	ds_read_b32 v231, v213 offset:2560
	ds_read_b32 v232, v213 offset:3072
	ds_read_b32 v233, v213 offset:3584
	ds_read_b32 v234, v213 offset:4096
	ds_read_b32 v235, v213 offset:4608
	ds_read_b32 v236, v213 offset:5120
	ds_read_b32 v237, v213 offset:5632
	ds_read_b32 v238, v213 offset:6144
	ds_read_b32 v239, v213 offset:6656
	ds_read_b32 v240, v213 offset:7168
	ds_read_b32 v241, v213 offset:7680
	s_waitcnt lgkmcnt(0)
	v_max_f32_e32 v226, v226, v226
	v_max_f32_e32 v227, v227, v227
	v_max_f32_e32 v228, v228, v228
	v_max_f32_e32 v229, v229, v229
	v_max_f32_e32 v230, v230, v230
	v_max_f32_e32 v231, v231, v231
	v_max_f32_e32 v232, v232, v232
	v_max_f32_e32 v233, v233, v233
	v_max_f32_e32 v234, v234, v234
	v_max_f32_e32 v235, v235, v235
	v_max_f32_e32 v236, v236, v236
	v_max_f32_e32 v237, v237, v237
	v_max_f32_e32 v238, v238, v238
	v_max_f32_e32 v239, v239, v239
	v_max_f32_e32 v240, v240, v240
	v_max_f32_e32 v241, v241, v241
	v_med3_f32 v226, v226, s62, v95
	v_med3_f32 v227, v227, s62, v95
	v_med3_f32 v228, v228, s62, v95
	v_med3_f32 v229, v229, s62, v95
	v_med3_f32 v230, v230, s62, v95
	v_med3_f32 v231, v231, s62, v95
	v_med3_f32 v232, v232, s62, v95
	v_med3_f32 v233, v233, s62, v95
	v_med3_f32 v234, v234, s62, v95
	v_med3_f32 v235, v235, s62, v95
	v_med3_f32 v236, v236, s62, v95
	v_med3_f32 v237, v237, s62, v95
	v_med3_f32 v238, v238, s62, v95
	v_med3_f32 v239, v239, s62, v95
	v_med3_f32 v240, v240, s62, v95
	v_med3_f32 v241, v241, s62, v95
	v_mov_b32_e32 v242, 0
	v_mov_b32_e32 v243, 0
	v_mov_b32_e32 v244, 0
	v_mov_b32_e32 v245, 0
	v_cvt_pk_fp8_f32 v242, v226, v227
	v_cvt_pk_fp8_f32 v243, v230, v231
	v_cvt_pk_fp8_f32 v244, v234, v235
	v_cvt_pk_fp8_f32 v245, v238, v239
	v_cvt_pk_fp8_f32 v242, v228, v229 op_sel:[0,0,1]
	v_cvt_pk_fp8_f32 v243, v232, v233 op_sel:[0,0,1]
	v_cvt_pk_fp8_f32 v244, v236, v237 op_sel:[0,0,1]
	v_cvt_pk_fp8_f32 v245, v240, v241 op_sel:[0,0,1]
	s_nop 0
	global_store_dwordx4 v78, v[242:245], s[6:7]
	s_waitcnt vmcnt(14)
	v_mul_f32_e32 v176, v66, v176
	v_mul_f32_e32 v177, v66, v177
	v_mul_f32_e32 v178, v66, v178
	v_mul_f32_e32 v179, v66, v179
	ds_write_b128 v210, v[176:179]
	v_mul_f32_e32 v180, v67, v180
	v_mul_f32_e32 v181, v67, v181
	v_mul_f32_e32 v182, v67, v182
	v_mul_f32_e32 v183, v67, v183
	ds_write_b128 v210, v[180:183] offset:1024
	v_mul_f32_e32 v184, v68, v184
	v_mul_f32_e32 v185, v68, v185
	v_mul_f32_e32 v186, v68, v186
	v_mul_f32_e32 v187, v68, v187
	ds_write_b128 v210, v[184:187] offset:2048
	v_mul_f32_e32 v188, v69, v188
	v_mul_f32_e32 v189, v69, v189
	v_mul_f32_e32 v190, v69, v190
	v_mul_f32_e32 v191, v69, v191
	ds_write_b128 v210, v[188:191] offset:3072
	v_mul_f32_e32 v192, v70, v192
	v_mul_f32_e32 v193, v70, v193
	v_mul_f32_e32 v194, v70, v194
	v_mul_f32_e32 v195, v70, v195
	ds_write_b128 v210, v[192:195] offset:4096
	v_mul_f32_e32 v196, v71, v196
	v_mul_f32_e32 v197, v71, v197
	v_mul_f32_e32 v198, v71, v198
	v_mul_f32_e32 v199, v71, v199
	ds_write_b128 v210, v[196:199] offset:5120
	v_mul_f32_e32 v200, v72, v200
	v_mul_f32_e32 v201, v72, v201
	v_mul_f32_e32 v202, v72, v202
	v_mul_f32_e32 v203, v72, v203
	ds_write_b128 v210, v[200:203] offset:6144
	v_mul_f32_e32 v204, v73, v204
	v_mul_f32_e32 v205, v73, v205
	v_mul_f32_e32 v206, v73, v206
	v_mul_f32_e32 v207, v73, v207
	ds_write_b128 v210, v[204:207] offset:7168
	s_waitcnt lgkmcnt(0)
	s_barrier
; #define GAS __attribute__((address_space(1)))
; #define LAS __attribute__((address_space(3)))
; #define LDS_WAIT() asm volatile("s_waitcnt lgkmcnt(0)" ::: "memory")
;     const int pr = item >> 1, kb = 2 * (pr / nblk) + (item & 1), nb = pr % nblk, k0 = 64 * kb, n0 = 32 * nb;
;     const int nr = n0 + (lane & 31); const int sc = MAP == 1 ? src_col_in(nr) : nr;
;     float v[32];
; #pragma unroll
;     for (int i = 0; i < 32; ++i) v[i] = sc >= 0 ? W[(size_t)(k0 + 2 * i + (lane >> 5)) * Nsrc + sc] : 0.f;
; #pragma unroll
;     for (int i = 0; i < 32; ++i) { const int k = k0 + 2 * i + (lane >> 5); float x = v[i] * wscale; if (KS) x *= (k < ksplit ? ksA[k] : ksB[k - ksplit]); scr[(2 * i + (lane >> 5)) * 33 + (lane & 31)] = x; }
;     LDS_WAIT(); asm volatile("" ::: "memory");
;     const int c = lane & 7;
; #pragma unroll
;     for (int j = 0; j < 4; ++j) { const int n = (lane >> 3) + 8 * j; const LAS float* s = scr + (8 * c) * 33 + n;
;         const unsigned long long o = (unsigned long long)pg8::pk4_fp8(s[0 * 33], s[1 * 33], s[2 * 33], s[3 * 33]) | ((unsigned long long)pg8::pk4_fp8(s[4 * 33], s[5 * 33], s[6 * 33], s[7 * 33]) << 32);
;         *(GAS unsigned long long*)(WT + (size_t)(n0 + n) * K + k0 + 8 * c) = o; }
;     LDS_WAIT(); asm volatile("" ::: "memory");
; }
	s_add_u32 s8, s58, 0x3000
	s_addc_u32 s9, s59, 0
	global_load_dwordx4 v[176:179], v75, s[8:9]
	s_add_u32 s8, s8, 0x8000
	s_addc_u32 s9, s9, 0
	global_load_dwordx4 v[180:183], v75, s[8:9]
	s_add_u32 s8, s8, 0x8000
	s_addc_u32 s9, s9, 0
	global_load_dwordx4 v[184:187], v75, s[8:9]
	s_add_u32 s8, s8, 0x8000
	s_addc_u32 s9, s9, 0
	global_load_dwordx4 v[188:191], v75, s[8:9]
	s_add_u32 s8, s8, 0x8000
	s_addc_u32 s9, s9, 0
	global_load_dwordx4 v[192:195], v75, s[8:9]
	s_add_u32 s8, s8, 0x8000
	s_addc_u32 s9, s9, 0
	global_load_dwordx4 v[196:199], v75, s[8:9]
	s_add_u32 s8, s8, 0x8000
	s_addc_u32 s9, s9, 0
	global_load_dwordx4 v[200:203], v75, s[8:9]
	s_add_u32 s8, s8, 0x8000
	s_addc_u32 s9, s9, 0
	global_load_dwordx4 v[204:207], v75, s[8:9]
	s_add_u32 s6, s60, 0x400000
	s_addc_u32 s7, s61, 0
	ds_read_b32 v226, v212
	ds_read_b32 v227, v212 offset:512
	ds_read_b32 v228, v212 offset:1024
	ds_read_b32 v229, v212 offset:1536
	ds_read_b32 v230, v212 offset:2048
	ds_read_b32 v231, v212 offset:2560
	ds_read_b32 v232, v212 offset:3072
	ds_read_b32 v233, v212 offset:3584
	ds_read_b32 v234, v212 offset:4096
	ds_read_b32 v235, v212 offset:4608
	ds_read_b32 v236, v212 offset:5120
	ds_read_b32 v237, v212 offset:5632
	ds_read_b32 v238, v212 offset:6144
	ds_read_b32 v239, v212 offset:6656
	ds_read_b32 v240, v212 offset:7168
	ds_read_b32 v241, v212 offset:7680
	s_waitcnt lgkmcnt(0)
	v_max_f32_e32 v226, v226, v226
	v_max_f32_e32 v227, v227, v227
	v_max_f32_e32 v228, v228, v228
	v_max_f32_e32 v229, v229, v229
	v_max_f32_e32 v230, v230, v230
	v_max_f32_e32 v231, v231, v231
	v_max_f32_e32 v232, v232, v232
	v_max_f32_e32 v233, v233, v233
	v_max_f32_e32 v234, v234, v234
	v_max_f32_e32 v235, v235, v235
	v_max_f32_e32 v236, v236, v236
	v_max_f32_e32 v237, v237, v237
	v_max_f32_e32 v238, v238, v238
	v_max_f32_e32 v239, v239, v239
	v_max_f32_e32 v240, v240, v240
	v_max_f32_e32 v241, v241, v241
	v_med3_f32 v226, v226, s62, v95
	v_med3_f32 v227, v227, s62, v95
	v_med3_f32 v228, v228, s62, v95
	v_med3_f32 v229, v229, s62, v95
	v_med3_f32 v230, v230, s62, v95
	v_med3_f32 v231, v231, s62, v95
	v_med3_f32 v232, v232, s62, v95
	v_med3_f32 v233, v233, s62, v95
	v_med3_f32 v234, v234, s62, v95
	v_med3_f32 v235, v235, s62, v95
	v_med3_f32 v236, v236, s62, v95
	v_med3_f32 v237, v237, s62, v95
	v_med3_f32 v238, v238, s62, v95
	v_med3_f32 v239, v239, s62, v95
	v_med3_f32 v240, v240, s62, v95
	v_med3_f32 v241, v241, s62, v95
	v_mov_b32_e32 v242, 0
	v_mov_b32_e32 v243, 0
	v_mov_b32_e32 v244, 0
	v_mov_b32_e32 v245, 0
	v_cvt_pk_fp8_f32 v242, v226, v227
	v_cvt_pk_fp8_f32 v243, v230, v231
	v_cvt_pk_fp8_f32 v244, v234, v235
	v_cvt_pk_fp8_f32 v245, v238, v239
	v_cvt_pk_fp8_f32 v242, v228, v229 op_sel:[0,0,1]
	v_cvt_pk_fp8_f32 v243, v232, v233 op_sel:[0,0,1]
	v_cvt_pk_fp8_f32 v244, v236, v237 op_sel:[0,0,1]
	v_cvt_pk_fp8_f32 v245, v240, v241 op_sel:[0,0,1]
	s_nop 0
	global_store_dwordx4 v77, v[242:245], s[6:7]
	ds_read_b32 v226, v214
	ds_read_b32 v227, v214 offset:512
	ds_read_b32 v228, v214 offset:1024
	ds_read_b32 v229, v214 offset:1536
	ds_read_b32 v230, v214 offset:2048
	ds_read_b32 v231, v214 offset:2560
	ds_read_b32 v232, v214 offset:3072
	ds_read_b32 v233, v214 offset:3584
	ds_read_b32 v234, v214 offset:4096
	ds_read_b32 v235, v214 offset:4608
	ds_read_b32 v236, v214 offset:5120
	ds_read_b32 v237, v214 offset:5632
	ds_read_b32 v238, v214 offset:6144
	ds_read_b32 v239, v214 offset:6656
	ds_read_b32 v240, v214 offset:7168
	ds_read_b32 v241, v214 offset:7680
	s_waitcnt lgkmcnt(0)
	v_max_f32_e32 v226, v226, v226
	v_max_f32_e32 v227, v227, v227
	v_max_f32_e32 v228, v228, v228
	v_max_f32_e32 v229, v229, v229
	v_max_f32_e32 v230, v230, v230
	v_max_f32_e32 v231, v231, v231
	v_max_f32_e32 v232, v232, v232
	v_max_f32_e32 v233, v233, v233
	v_max_f32_e32 v234, v234, v234
	v_max_f32_e32 v235, v235, v235
	v_max_f32_e32 v236, v236, v236
	v_max_f32_e32 v237, v237, v237
	v_max_f32_e32 v238, v238, v238
	v_max_f32_e32 v239, v239, v239
	v_max_f32_e32 v240, v240, v240
	v_max_f32_e32 v241, v241, v241
	v_med3_f32 v226, v226, s62, v95
	v_med3_f32 v227, v227, s62, v95
	v_med3_f32 v228, v228, s62, v95
	v_med3_f32 v229, v229, s62, v95
	v_med3_f32 v230, v230, s62, v95
	v_med3_f32 v231, v231, s62, v95
	v_med3_f32 v232, v232, s62, v95
	v_med3_f32 v233, v233, s62, v95
	v_med3_f32 v234, v234, s62, v95
	v_med3_f32 v235, v235, s62, v95
	v_med3_f32 v236, v236, s62, v95
	v_med3_f32 v237, v237, s62, v95
	v_med3_f32 v238, v238, s62, v95
	v_med3_f32 v239, v239, s62, v95
	v_med3_f32 v240, v240, s62, v95
	v_med3_f32 v241, v241, s62, v95
	v_mov_b32_e32 v242, 0
	v_mov_b32_e32 v243, 0
	v_mov_b32_e32 v244, 0
	v_mov_b32_e32 v245, 0
	v_cvt_pk_fp8_f32 v242, v226, v227
	v_cvt_pk_fp8_f32 v243, v230, v231
	v_cvt_pk_fp8_f32 v244, v234, v235
	v_cvt_pk_fp8_f32 v245, v238, v239
	v_cvt_pk_fp8_f32 v242, v228, v229 op_sel:[0,0,1]
	v_cvt_pk_fp8_f32 v243, v232, v233 op_sel:[0,0,1]
	v_cvt_pk_fp8_f32 v244, v236, v237 op_sel:[0,0,1]
	v_cvt_pk_fp8_f32 v245, v240, v241 op_sel:[0,0,1]
	s_nop 0
	global_store_dwordx4 v78, v[242:245], s[6:7]
	s_waitcnt vmcnt(12)
	v_mul_f32_e32 v144, v66, v144
	v_mul_f32_e32 v145, v66, v145
	v_mul_f32_e32 v146, v66, v146
	v_mul_f32_e32 v147, v66, v147
	ds_write_b128 v209, v[144:147]
	v_mul_f32_e32 v148, v67, v148
	v_mul_f32_e32 v149, v67, v149
	v_mul_f32_e32 v150, v67, v150
	v_mul_f32_e32 v151, v67, v151
	ds_write_b128 v209, v[148:151] offset:1024
	v_mul_f32_e32 v152, v68, v152
	v_mul_f32_e32 v153, v68, v153
	v_mul_f32_e32 v154, v68, v154
	v_mul_f32_e32 v155, v68, v155
	ds_write_b128 v209, v[152:155] offset:2048
	v_mul_f32_e32 v156, v69, v156
	v_mul_f32_e32 v157, v69, v157
	v_mul_f32_e32 v158, v69, v158
	v_mul_f32_e32 v159, v69, v159
	ds_write_b128 v209, v[156:159] offset:3072
	v_mul_f32_e32 v160, v70, v160
	v_mul_f32_e32 v161, v70, v161
	v_mul_f32_e32 v162, v70, v162
	v_mul_f32_e32 v163, v70, v163
	ds_write_b128 v209, v[160:163] offset:4096
	v_mul_f32_e32 v164, v71, v164
	v_mul_f32_e32 v165, v71, v165
	v_mul_f32_e32 v166, v71, v166
	v_mul_f32_e32 v167, v71, v167
	ds_write_b128 v209, v[164:167] offset:5120
	v_mul_f32_e32 v168, v72, v168
	v_mul_f32_e32 v169, v72, v169
	v_mul_f32_e32 v170, v72, v170
	v_mul_f32_e32 v171, v72, v171
	ds_write_b128 v209, v[168:171] offset:6144
	v_mul_f32_e32 v172, v73, v172
	v_mul_f32_e32 v173, v73, v173
	v_mul_f32_e32 v174, v73, v174
	v_mul_f32_e32 v175, v73, v175
	ds_write_b128 v209, v[172:175] offset:7168
	s_waitcnt lgkmcnt(0)
	s_barrier
; #define GAS __attribute__((address_space(1)))
; #define LAS __attribute__((address_space(3)))
; #define LDS_WAIT() asm volatile("s_waitcnt lgkmcnt(0)" ::: "memory")
;     const int pr = item >> 1, kb = 2 * (pr / nblk) + (item & 1), nb = pr % nblk, k0 = 64 * kb, n0 = 32 * nb;
;     const int nr = n0 + (lane & 31); const int sc = MAP == 1 ? src_col_in(nr) : nr;
;     float v[32];
; #pragma unroll
;     for (int i = 0; i < 32; ++i) v[i] = sc >= 0 ? W[(size_t)(k0 + 2 * i + (lane >> 5)) * Nsrc + sc] : 0.f;
; #pragma unroll
;     for (int i = 0; i < 32; ++i) { const int k = k0 + 2 * i + (lane >> 5); float x = v[i] * wscale; if (KS) x *= (k < ksplit ? ksA[k] : ksB[k - ksplit]); scr[(2 * i + (lane >> 5)) * 33 + (lane & 31)] = x; }
;     LDS_WAIT(); asm volatile("" ::: "memory");
;     const int c = lane & 7;
; #pragma unroll
;     for (int j = 0; j < 4; ++j) { const int n = (lane >> 3) + 8 * j; const LAS float* s = scr + (8 * c) * 33 + n;
;         const unsigned long long o = (unsigned long long)pg8::pk4_fp8(s[0 * 33], s[1 * 33], s[2 * 33], s[3 * 33]) | ((unsigned long long)pg8::pk4_fp8(s[4 * 33], s[5 * 33], s[6 * 33], s[7 * 33]) << 32);
;         *(GAS unsigned long long*)(WT + (size_t)(n0 + n) * K + k0 + 8 * c) = o; }
;     LDS_WAIT(); asm volatile("" ::: "memory");
; }
	s_add_u32 s6, s60, 0x800000
	s_addc_u32 s7, s61, 0
	ds_read_b32 v226, v211
	ds_read_b32 v227, v211 offset:512
	ds_read_b32 v228, v211 offset:1024
	ds_read_b32 v229, v211 offset:1536
	ds_read_b32 v230, v211 offset:2048
	ds_read_b32 v231, v211 offset:2560
	ds_read_b32 v232, v211 offset:3072
	ds_read_b32 v233, v211 offset:3584
	ds_read_b32 v234, v211 offset:4096
	ds_read_b32 v235, v211 offset:4608
	ds_read_b32 v236, v211 offset:5120
	ds_read_b32 v237, v211 offset:5632
	ds_read_b32 v238, v211 offset:6144
	ds_read_b32 v239, v211 offset:6656
	ds_read_b32 v240, v211 offset:7168
	ds_read_b32 v241, v211 offset:7680
	s_waitcnt lgkmcnt(0)
	v_max_f32_e32 v226, v226, v226
	v_max_f32_e32 v227, v227, v227
	v_max_f32_e32 v228, v228, v228
	v_max_f32_e32 v229, v229, v229
	v_max_f32_e32 v230, v230, v230
	v_max_f32_e32 v231, v231, v231
	v_max_f32_e32 v232, v232, v232
	v_max_f32_e32 v233, v233, v233
	v_max_f32_e32 v234, v234, v234
	v_max_f32_e32 v235, v235, v235
	v_max_f32_e32 v236, v236, v236
	v_max_f32_e32 v237, v237, v237
	v_max_f32_e32 v238, v238, v238
	v_max_f32_e32 v239, v239, v239
	v_max_f32_e32 v240, v240, v240
	v_max_f32_e32 v241, v241, v241
	v_med3_f32 v226, v226, s62, v95
	v_med3_f32 v227, v227, s62, v95
	v_med3_f32 v228, v228, s62, v95
	v_med3_f32 v229, v229, s62, v95
	v_med3_f32 v230, v230, s62, v95
	v_med3_f32 v231, v231, s62, v95
	v_med3_f32 v232, v232, s62, v95
	v_med3_f32 v233, v233, s62, v95
	v_med3_f32 v234, v234, s62, v95
	v_med3_f32 v235, v235, s62, v95
	v_med3_f32 v236, v236, s62, v95
	v_med3_f32 v237, v237, s62, v95
	v_med3_f32 v238, v238, s62, v95
	v_med3_f32 v239, v239, s62, v95
	v_med3_f32 v240, v240, s62, v95
	v_med3_f32 v241, v241, s62, v95
	v_mov_b32_e32 v242, 0
	v_mov_b32_e32 v243, 0
	v_mov_b32_e32 v244, 0
	v_mov_b32_e32 v245, 0
	v_cvt_pk_fp8_f32 v242, v226, v227
	v_cvt_pk_fp8_f32 v243, v230, v231
	v_cvt_pk_fp8_f32 v244, v234, v235
	v_cvt_pk_fp8_f32 v245, v238, v239
	v_cvt_pk_fp8_f32 v242, v228, v229 op_sel:[0,0,1]
	v_cvt_pk_fp8_f32 v243, v232, v233 op_sel:[0,0,1]
	v_cvt_pk_fp8_f32 v244, v236, v237 op_sel:[0,0,1]
	v_cvt_pk_fp8_f32 v245, v240, v241 op_sel:[0,0,1]
	s_nop 0
	global_store_dwordx4 v77, v[242:245], s[6:7]
	ds_read_b32 v226, v213
	ds_read_b32 v227, v213 offset:512
	ds_read_b32 v228, v213 offset:1024
	ds_read_b32 v229, v213 offset:1536
	ds_read_b32 v230, v213 offset:2048
	ds_read_b32 v231, v213 offset:2560
	ds_read_b32 v232, v213 offset:3072
	ds_read_b32 v233, v213 offset:3584
	ds_read_b32 v234, v213 offset:4096
	ds_read_b32 v235, v213 offset:4608
	ds_read_b32 v236, v213 offset:5120
	ds_read_b32 v237, v213 offset:5632
	ds_read_b32 v238, v213 offset:6144
	ds_read_b32 v239, v213 offset:6656
	ds_read_b32 v240, v213 offset:7168
	ds_read_b32 v241, v213 offset:7680
	s_waitcnt lgkmcnt(0)
	v_max_f32_e32 v226, v226, v226
	v_max_f32_e32 v227, v227, v227
	v_max_f32_e32 v228, v228, v228
	v_max_f32_e32 v229, v229, v229
	v_max_f32_e32 v230, v230, v230
	v_max_f32_e32 v231, v231, v231
	v_max_f32_e32 v232, v232, v232
	v_max_f32_e32 v233, v233, v233
	v_max_f32_e32 v234, v234, v234
	v_max_f32_e32 v235, v235, v235
	v_max_f32_e32 v236, v236, v236
	v_max_f32_e32 v237, v237, v237
	v_max_f32_e32 v238, v238, v238
	v_max_f32_e32 v239, v239, v239
	v_max_f32_e32 v240, v240, v240
	v_max_f32_e32 v241, v241, v241
	v_med3_f32 v226, v226, s62, v95
	v_med3_f32 v227, v227, s62, v95
	v_med3_f32 v228, v228, s62, v95
	v_med3_f32 v229, v229, s62, v95
	v_med3_f32 v230, v230, s62, v95
	v_med3_f32 v231, v231, s62, v95
	v_med3_f32 v232, v232, s62, v95
	v_med3_f32 v233, v233, s62, v95
	v_med3_f32 v234, v234, s62, v95
	v_med3_f32 v235, v235, s62, v95
	v_med3_f32 v236, v236, s62, v95
	v_med3_f32 v237, v237, s62, v95
	v_med3_f32 v238, v238, s62, v95
	v_med3_f32 v239, v239, s62, v95
	v_med3_f32 v240, v240, s62, v95
	v_med3_f32 v241, v241, s62, v95
	v_mov_b32_e32 v242, 0
	v_mov_b32_e32 v243, 0
	v_mov_b32_e32 v244, 0
	v_mov_b32_e32 v245, 0
	v_cvt_pk_fp8_f32 v242, v226, v227
	v_cvt_pk_fp8_f32 v243, v230, v231
	v_cvt_pk_fp8_f32 v244, v234, v235
	v_cvt_pk_fp8_f32 v245, v238, v239
	v_cvt_pk_fp8_f32 v242, v228, v229 op_sel:[0,0,1]
	v_cvt_pk_fp8_f32 v243, v232, v233 op_sel:[0,0,1]
	v_cvt_pk_fp8_f32 v244, v236, v237 op_sel:[0,0,1]
	v_cvt_pk_fp8_f32 v245, v240, v241 op_sel:[0,0,1]
	s_nop 0
	global_store_dwordx4 v78, v[242:245], s[6:7]
	s_waitcnt vmcnt(4)
	v_mul_f32_e32 v176, v66, v176
	v_mul_f32_e32 v177, v66, v177
	v_mul_f32_e32 v178, v66, v178
	v_mul_f32_e32 v179, v66, v179
	ds_write_b128 v210, v[176:179]
	v_mul_f32_e32 v180, v67, v180
	v_mul_f32_e32 v181, v67, v181
	v_mul_f32_e32 v182, v67, v182
	v_mul_f32_e32 v183, v67, v183
	ds_write_b128 v210, v[180:183] offset:1024
	v_mul_f32_e32 v184, v68, v184
	v_mul_f32_e32 v185, v68, v185
	v_mul_f32_e32 v186, v68, v186
	v_mul_f32_e32 v187, v68, v187
	ds_write_b128 v210, v[184:187] offset:2048
	v_mul_f32_e32 v188, v69, v188
	v_mul_f32_e32 v189, v69, v189
	v_mul_f32_e32 v190, v69, v190
	v_mul_f32_e32 v191, v69, v191
	ds_write_b128 v210, v[188:191] offset:3072
	v_mul_f32_e32 v192, v70, v192
	v_mul_f32_e32 v193, v70, v193
	v_mul_f32_e32 v194, v70, v194
	v_mul_f32_e32 v195, v70, v195
	ds_write_b128 v210, v[192:195] offset:4096
	v_mul_f32_e32 v196, v71, v196
	v_mul_f32_e32 v197, v71, v197
	v_mul_f32_e32 v198, v71, v198
	v_mul_f32_e32 v199, v71, v199
	ds_write_b128 v210, v[196:199] offset:5120
	v_mul_f32_e32 v200, v72, v200
	v_mul_f32_e32 v201, v72, v201
	v_mul_f32_e32 v202, v72, v202
	v_mul_f32_e32 v203, v72, v203
	ds_write_b128 v210, v[200:203] offset:6144
	v_mul_f32_e32 v204, v73, v204
	v_mul_f32_e32 v205, v73, v205
	v_mul_f32_e32 v206, v73, v206
	v_mul_f32_e32 v207, v73, v207
	ds_write_b128 v210, v[204:207] offset:7168
	s_waitcnt lgkmcnt(0)
	s_barrier
; #define GAS __attribute__((address_space(1)))
; #define LAS __attribute__((address_space(3)))
; #define LDS_WAIT() asm volatile("s_waitcnt lgkmcnt(0)" ::: "memory")
;     const int pr = item >> 1, kb = 2 * (pr / nblk) + (item & 1), nb = pr % nblk, k0 = 64 * kb, n0 = 32 * nb;
;     const int nr = n0 + (lane & 31); const int sc = MAP == 1 ? src_col_in(nr) : nr;
;     float v[32];
; #pragma unroll
;     for (int i = 0; i < 32; ++i) v[i] = sc >= 0 ? W[(size_t)(k0 + 2 * i + (lane >> 5)) * Nsrc + sc] : 0.f;
; #pragma unroll
;     for (int i = 0; i < 32; ++i) { const int k = k0 + 2 * i + (lane >> 5); float x = v[i] * wscale; if (KS) x *= (k < ksplit ? ksA[k] : ksB[k - ksplit]); scr[(2 * i + (lane >> 5)) * 33 + (lane & 31)] = x; }
;     LDS_WAIT(); asm volatile("" ::: "memory");
;     const int c = lane & 7;
; #pragma unroll
;     for (int j = 0; j < 4; ++j) { const int n = (lane >> 3) + 8 * j; const LAS float* s = scr + (8 * c) * 33 + n;
;         const unsigned long long o = (unsigned long long)pg8::pk4_fp8(s[0 * 33], s[1 * 33], s[2 * 33], s[3 * 33]) | ((unsigned long long)pg8::pk4_fp8(s[4 * 33], s[5 * 33], s[6 * 33], s[7 * 33]) << 32);
;         *(GAS unsigned long long*)(WT + (size_t)(n0 + n) * K + k0 + 8 * c) = o; }
;     LDS_WAIT(); asm volatile("" ::: "memory");
; }
	s_add_u32 s6, s60, 0xc00000
	s_addc_u32 s7, s61, 0
	ds_read_b32 v226, v212
	ds_read_b32 v227, v212 offset:512
	ds_read_b32 v228, v212 offset:1024
	ds_read_b32 v229, v212 offset:1536
	ds_read_b32 v230, v212 offset:2048
	ds_read_b32 v231, v212 offset:2560
	ds_read_b32 v232, v212 offset:3072
	ds_read_b32 v233, v212 offset:3584
	ds_read_b32 v234, v212 offset:4096
	ds_read_b32 v235, v212 offset:4608
	ds_read_b32 v236, v212 offset:5120
	ds_read_b32 v237, v212 offset:5632
	ds_read_b32 v238, v212 offset:6144
	ds_read_b32 v239, v212 offset:6656
	ds_read_b32 v240, v212 offset:7168
	ds_read_b32 v241, v212 offset:7680
	s_waitcnt lgkmcnt(0)
	v_max_f32_e32 v226, v226, v226
	v_max_f32_e32 v227, v227, v227
	v_max_f32_e32 v228, v228, v228
	v_max_f32_e32 v229, v229, v229
	v_max_f32_e32 v230, v230, v230
	v_max_f32_e32 v231, v231, v231
	v_max_f32_e32 v232, v232, v232
	v_max_f32_e32 v233, v233, v233
	v_max_f32_e32 v234, v234, v234
	v_max_f32_e32 v235, v235, v235
	v_max_f32_e32 v236, v236, v236
	v_max_f32_e32 v237, v237, v237
	v_max_f32_e32 v238, v238, v238
	v_max_f32_e32 v239, v239, v239
	v_max_f32_e32 v240, v240, v240
	v_max_f32_e32 v241, v241, v241
	v_med3_f32 v226, v226, s62, v95
	v_med3_f32 v227, v227, s62, v95
	v_med3_f32 v228, v228, s62, v95
	v_med3_f32 v229, v229, s62, v95
	v_med3_f32 v230, v230, s62, v95
	v_med3_f32 v231, v231, s62, v95
	v_med3_f32 v232, v232, s62, v95
	v_med3_f32 v233, v233, s62, v95
	v_med3_f32 v234, v234, s62, v95
	v_med3_f32 v235, v235, s62, v95
	v_med3_f32 v236, v236, s62, v95
	v_med3_f32 v237, v237, s62, v95
	v_med3_f32 v238, v238, s62, v95
	v_med3_f32 v239, v239, s62, v95
	v_med3_f32 v240, v240, s62, v95
	v_med3_f32 v241, v241, s62, v95
	v_mov_b32_e32 v242, 0
	v_mov_b32_e32 v243, 0
	v_mov_b32_e32 v244, 0
	v_mov_b32_e32 v245, 0
	v_cvt_pk_fp8_f32 v242, v226, v227
	v_cvt_pk_fp8_f32 v243, v230, v231
	v_cvt_pk_fp8_f32 v244, v234, v235
	v_cvt_pk_fp8_f32 v245, v238, v239
	v_cvt_pk_fp8_f32 v242, v228, v229 op_sel:[0,0,1]
	v_cvt_pk_fp8_f32 v243, v232, v233 op_sel:[0,0,1]
	v_cvt_pk_fp8_f32 v244, v236, v237 op_sel:[0,0,1]
	v_cvt_pk_fp8_f32 v245, v240, v241 op_sel:[0,0,1]
	s_nop 0
	global_store_dwordx4 v77, v[242:245], s[6:7]
	ds_read_b32 v226, v214
	ds_read_b32 v227, v214 offset:512
	ds_read_b32 v228, v214 offset:1024
	ds_read_b32 v229, v214 offset:1536
	ds_read_b32 v230, v214 offset:2048
	ds_read_b32 v231, v214 offset:2560
	ds_read_b32 v232, v214 offset:3072
	ds_read_b32 v233, v214 offset:3584
	ds_read_b32 v234, v214 offset:4096
	ds_read_b32 v235, v214 offset:4608
	ds_read_b32 v236, v214 offset:5120
	ds_read_b32 v237, v214 offset:5632
	ds_read_b32 v238, v214 offset:6144
	ds_read_b32 v239, v214 offset:6656
	ds_read_b32 v240, v214 offset:7168
	ds_read_b32 v241, v214 offset:7680
	s_waitcnt lgkmcnt(0)
	v_max_f32_e32 v226, v226, v226
	v_max_f32_e32 v227, v227, v227
	v_max_f32_e32 v228, v228, v228
	v_max_f32_e32 v229, v229, v229
	v_max_f32_e32 v230, v230, v230
	v_max_f32_e32 v231, v231, v231
	v_max_f32_e32 v232, v232, v232
	v_max_f32_e32 v233, v233, v233
	v_max_f32_e32 v234, v234, v234
	v_max_f32_e32 v235, v235, v235
	v_max_f32_e32 v236, v236, v236
	v_max_f32_e32 v237, v237, v237
	v_max_f32_e32 v238, v238, v238
	v_max_f32_e32 v239, v239, v239
	v_max_f32_e32 v240, v240, v240
	v_max_f32_e32 v241, v241, v241
	v_med3_f32 v226, v226, s62, v95
	v_med3_f32 v227, v227, s62, v95
	v_med3_f32 v228, v228, s62, v95
	v_med3_f32 v229, v229, s62, v95
	v_med3_f32 v230, v230, s62, v95
	v_med3_f32 v231, v231, s62, v95
	v_med3_f32 v232, v232, s62, v95
	v_med3_f32 v233, v233, s62, v95
	v_med3_f32 v234, v234, s62, v95
	v_med3_f32 v235, v235, s62, v95
	v_med3_f32 v236, v236, s62, v95
	v_med3_f32 v237, v237, s62, v95
	v_med3_f32 v238, v238, s62, v95
	v_med3_f32 v239, v239, s62, v95
	v_med3_f32 v240, v240, s62, v95
	v_med3_f32 v241, v241, s62, v95
	v_mov_b32_e32 v242, 0
	v_mov_b32_e32 v243, 0
	v_mov_b32_e32 v244, 0
	v_mov_b32_e32 v245, 0
	v_cvt_pk_fp8_f32 v242, v226, v227
	v_cvt_pk_fp8_f32 v243, v230, v231
	v_cvt_pk_fp8_f32 v244, v234, v235
	v_cvt_pk_fp8_f32 v245, v238, v239
	v_cvt_pk_fp8_f32 v242, v228, v229 op_sel:[0,0,1]
	v_cvt_pk_fp8_f32 v243, v232, v233 op_sel:[0,0,1]
	v_cvt_pk_fp8_f32 v244, v236, v237 op_sel:[0,0,1]
	v_cvt_pk_fp8_f32 v245, v240, v241 op_sel:[0,0,1]
	s_nop 0
	global_store_dwordx4 v78, v[242:245], s[6:7]
	s_waitcnt lgkmcnt(0)
	s_barrier
; __global__ void __launch_bounds__(NWAVES * 64, 2) hybrid_fwd(Args args) {
;     ...
;     for (int L = 0; L < DEPTH; ++L) {
;         { unsigned long long wz = 0; asm volatile("" : "+s"(wz)); ws = args.ws + wz; }
;         bf16* Hres = (bf16*)(ws + WS_H);     static_assert(DEPTH == 2 && WO_F8_FROM == 1 && PROJ_F8_FROM == 1, "the phase instantiations below are written for this precision plan");
;         bf16* XN = (bf16*)(ws + WS_XN); bf16* PROJ = (bf16*)(ws + WS_PROJ); bf16* ACT = (bf16*)(ws + WS_ACT); unsigned char* CAT = (unsigned char*)(ws + WS_CAT);     const bool wo_f8 = L >= WO_F8_FROM;
;         float* ATT = (float*)(ws + WS_ATT); bf16* XBC = (bf16*)(ws + WS_XBC); bf16* Y = (bf16*)(ws + WS_Y);
;         bf16* KC = (bf16*)(ws + WS_KC); bf16* VC = (bf16*)(ws + WS_VC); float* DT = (float*)(ws + WS_DT); float* ADT = (float*)(ws + WS_ADT);
;         float* COS = (float*)(ws + WS_COS); float* SIN = (float*)(ws + WS_SIN); unsigned* BMP = (unsigned*)(ws + WS_BMP);
;         bf16* AO = (bf16*)(ws + WS_ACT);     float* STT = (float*)(ws + WS_ST); bf16* PREVB = (bf16*)(ws + WS_PREV);     float* ACSG = (float*)(ws + WS_ACSG); float* DEC = (float*)(ws + WS_DEC);
	v_readlane_b32 s12, v253, 35
	v_readlane_b32 s18, v253, 41
	v_readlane_b32 s19, v253, 42
	s_add_u32 s81, s18, 0x1f600000
	s_addc_u32 s94, s19, 0
	s_add_u32 s24, s18, 0xf600000
	v_or_b32_e32 v2, 2, v6
	v_mov_b32_e32 v3, 0x630
	v_readlane_b32 s13, v253, 36
	v_readlane_b32 s14, v253, 37
	v_readlane_b32 s15, v253, 38
	s_addc_u32 s25, s19, 0
	v_mad_u32_u24 v58, v2, s0, v3
	v_mov_b32_e32 v3, 0xc60
	s_add_u32 s26, s18, 0xb600000
	v_mad_u32_u24 v59, v2, s0, v3
	v_readlane_b32 s0, v253, 19
	s_addc_u32 s27, s19, 0
	v_readlane_b32 s2, v253, 21
	v_readlane_b32 s10, v253, 29
	v_readlane_b32 s3, v253, 22
	v_readlane_b32 s11, v253, 30
	s_add_u32 s2, s10, 0x4000000
	v_readlane_b32 s40, v253, 3
	s_addc_u32 s3, s11, 0
	v_readlane_b32 s52, v253, 15
	v_readlane_b32 s53, v253, 16
	s_add_u32 s22, s52, 0x2000
	v_readlane_b32 s8, v253, 27
	s_addc_u32 s23, s53, 0
	v_readlane_b32 s9, v253, 28
	s_add_u32 s84, s8, 0x2000
	s_addc_u32 s85, s9, 0
	s_add_u32 s33, s18, 0x200000
	v_readlane_b32 s44, v253, 7
	s_addc_u32 s38, s19, 0
	v_mov_b32_e32 v9, v11
	v_readlane_b32 s1, v253, 20
	v_readlane_b32 s45, v253, 8
	s_add_u32 s86, s44, 0xb140000
	v_mul_u32_u24_e32 v57, 0x84, v2
	v_readlane_b32 s42, v253, 5
	v_lshl_add_u64 v[2:3], s[18:19], 0, v[8:9]
	s_mov_b64 s[0:1], 0xd600000
	s_addc_u32 s87, s45, 0
	v_readlane_b32 s12, v253, 31
	v_readlane_b32 s13, v253, 32
	v_readlane_b32 s14, v253, 33
	v_readlane_b32 s15, v253, 34
	v_readlane_b32 s43, v253, 6
	v_readlane_b32 s54, v253, 17
	v_readlane_b32 s55, v253, 18
	v_lshl_add_u64 v[12:13], v[2:3], 0, s[0:1]
	s_add_u32 s88, s42, 0x4000
	s_mov_b64 s[0:1], 0x5c00000
	v_readlane_b32 s41, v253, 4
	v_readlane_b32 s46, v253, 9
	v_readlane_b32 s47, v253, 10
	v_readlane_b32 s48, v253, 11
	v_readlane_b32 s49, v253, 12
	v_readlane_b32 s50, v253, 13
	s_addc_u32 s89, s43, 0
	v_lshlrev_b32_e32 v4, 6, v18
	v_lshl_add_u64 v[14:15], v[2:3], 0, s[0:1]
	s_lshl_b32 s0, s80, 5
	s_movk_i32 s12, 0xe000
	s_movk_i32 s14, 0xe008
	s_movk_i32 s18, 0xe010
	s_movk_i32 s78, 0xe018
	s_movk_i32 s92, 0xe0d0
	s_movk_i32 s28, 0xe0d8
	s_movk_i32 s34, 0xe0e0
	s_movk_i32 s52, 0xe0e8
	s_movk_i32 s54, 0xe0f0
	s_movk_i32 s56, 0xe0f8
	v_or_b32_e32 v26, 0x2000, v18
	v_or_b32_e32 v27, 0x4000, v18
	v_or_b32_e32 v28, 0x6000, v18
	v_or_b32_e32 v29, 0x8000, v18
	v_or_b32_e32 v30, 0xa000, v18
	v_or_b32_e32 v31, 0xc000, v18
	v_or_b32_e32 v32, 0xe000, v18
	v_or_b32_e32 v33, 0x10000, v18
	v_or_b32_e32 v34, 0x12000, v18
	v_or_b32_e32 v35, 0x14000, v18
	v_or_b32_e32 v36, 0x16000, v18
	v_or_b32_e32 v37, 0x18000, v18
	v_or_b32_e32 v38, 0x1a000, v18
	v_or_b32_e32 v39, 0x1c000, v18
	v_or_b32_e32 v40, 0x1e000, v18
	v_or_b32_e32 v41, 0x20000, v18
	v_or_b32_e32 v42, 0x22000, v18
	v_or_b32_e32 v43, 0x24000, v18
	v_or_b32_e32 v44, 0x26000, v18
	v_or_b32_e32 v45, 0x28000, v18
	v_or_b32_e32 v46, 0x2a000, v18
	v_or_b32_e32 v47, 0x2c000, v18
	v_or_b32_e32 v48, 0x2e000, v18
	v_or_b32_e32 v49, 0x30000, v18
	v_or_b32_e32 v50, 0x32000, v18
	v_or_b32_e32 v51, 0x34000, v18
	v_or_b32_e32 v52, 0x36000, v18
	v_or_b32_e32 v53, 0x38000, v18
	v_or_b32_e32 v54, 0x3a000, v18
	v_or_b32_e32 v55, 0x3c000, v18
	v_or_b32_e32 v56, 0x3e000, v18
	v_and_b32_e32 v60, 64, v4
	v_mov_b32_e32 v7, v11
	s_lshl_b32 s39, s80, 6
	s_add_i32 s40, s0, 0xfff4c000
	s_lshl_b32 s41, s83, 8
	s_lshl_b32 s42, s80, 4
	s_lshl_b32 s43, s83, 7
	s_mov_b32 s91, 0
	s_mov_b32 s44, 0xc3e00000
	s_movk_i32 s45, 0x7fff
	s_mov_b32 s46, 0xffff0000
	s_movk_i32 s47, 0x2c2f
	s_movk_i32 s48, 0x2c50
	s_mov_b32 s49, 0xb140
	v_add_u32_e32 v61, 0x400, v19
	v_add_u32_e32 v62, 0x800, v19
	v_add_u32_e32 v63, 0xc00, v19
	v_mov_b32_e32 v64, 0x43e00000
	s_mov_b32 s50, s80
	s_mov_b32 s13, -1
	s_mov_b32 s15, -1
	s_mov_b32 s19, -1
	s_mov_b32 s79, -1
	s_mov_b32 s93, -1
	s_mov_b32 s29, -1
	s_mov_b32 s35, -1
	s_mov_b32 s53, -1
	s_mov_b32 s55, -1
	s_mov_b32 s57, -1
	v_readlane_b32 s16, v253, 39
	v_readlane_b32 s17, v253, 40
	v_readlane_b32 s4, v253, 23
	v_readlane_b32 s5, v253, 24
	v_readlane_b32 s6, v253, 25
	v_readlane_b32 s7, v253, 26
	v_readlane_b32 s51, v253, 14
	s_branch .LBB0_15

; #define PG8_WAIT_V(n) asm volatile("s_waitcnt vmcnt(" #n ")" ::: "memory")
; #define PG8_BAR __builtin_amdgcn_s_barrier()
; #define GAS __attribute__((address_space(1)))
; #define LAS __attribute__((address_space(3)))
; #define LDS_WAIT() asm volatile("s_waitcnt lgkmcnt(0)" ::: "memory")
; template <class Epi, class Sched, bool ALIGN_EPI = false, bool SP2 = false, bool F8 = false>
; __device__ __forceinline__ void gemm_phase(PG8_LAS unsigned char* lds, const Gemm g, const Sched& S, const Epi& E) {
;     ...
;     PG8_WAIT_V(0);
;     if constexpr (!ALIGN_EPI) { if (wr == 0) PG8_BAR; }
;     PG8_BAR;
;     const int pr = item >> 1, kb = 2 * (pr / nblk) + (item & 1), nb = pr % nblk, k0 = 64 * kb, n0 = 32 * nb;
;     const int nr = n0 + (lane & 31); const int sc = MAP == 1 ? src_col_in(nr) : nr;
;     float v[32];
; #pragma unroll
;     for (int i = 0; i < 32; ++i) v[i] = sc >= 0 ? W[(size_t)(k0 + 2 * i + (lane >> 5)) * Nsrc + sc] : 0.f;
; #pragma unroll
;     for (int i = 0; i < 32; ++i) { const int k = k0 + 2 * i + (lane >> 5); float x = v[i] * wscale; if (KS) x *= (k < ksplit ? ksA[k] : ksB[k - ksplit]); scr[(2 * i + (lane >> 5)) * 33 + (lane & 31)] = x; }
;     LDS_WAIT(); asm volatile("" ::: "memory");
;     const int c = lane & 7;
; #pragma unroll
;     for (int j = 0; j < 4; ++j) { const int n = (lane >> 3) + 8 * j; const LAS float* s = scr + (8 * c) * 33 + n;
;         const unsigned long long o = (unsigned long long)pg8::pk4_fp8(s[0 * 33], s[1 * 33], s[2 * 33], s[3 * 33]) | ((unsigned long long)pg8::pk4_fp8(s[4 * 33], s[5 * 33], s[6 * 33], s[7 * 33]) << 32);
;         *(GAS unsigned long long*)(WT + (size_t)(n0 + n) * K + k0 + 8 * c) = o; }
;     LDS_WAIT(); asm volatile("" ::: "memory");
; }
.LBB0_575:
	s_waitcnt vmcnt(0)
	s_barrier
	s_cmpk_lt_u32 s77, 0xa0
	s_cbranch_scc1 .Llite_skip
	s_sub_i32 s16, s77, 160
	v_and_b32_e32 v133, 63, v0
	v_lshrrev_b32_e32 v134, 6, v0
	v_lshrrev_b32_e32 v130, 5, v133
	v_lshl_add_u32 v131, v134, 4, v130
	v_and_b32_e32 v132, 31, v133
	v_xor_b32_e32 v132, v132, v134
	v_lshlrev_b32_e32 v132, 4, v132
	v_lshl_add_u32 v120, v131, 9, v132
	v_add_u32_e32 v121, 0x10000, v120
	v_and_b32_e32 v132, 31, v133
	v_lshlrev_b32_e32 v132, 4, v132
	s_mov_b32 s21, 0x4000
	v_mad_u32_u24 v126, v131, s21, v132
	v_and_b32_e32 v130, 7, v133
	v_lshrrev_b32_e32 v131, 5, v133
	v_lshl_add_u32 v131, v134, 2, v131
	v_xor_b32_e32 v131, v131, v130
	v_lshlrev_b32_e32 v131, 4, v131
	v_lshl_add_u32 v131, v130, 13, v131
	v_bfe_u32 v132, v133, 3, 2
	v_lshl_add_u32 v122, v132, 2, v131
	v_add_u32_e32 v123, 0x10000, v122
	v_and_b32_e32 v130, 7, v133
	v_lshrrev_b32_e32 v131, 5, v133
	v_lshl_add_u32 v131, v134, 2, v131
	v_add_u32_e32 v131, 2, v131
	v_xor_b32_e32 v131, v131, v130
	v_lshlrev_b32_e32 v131, 4, v131
	v_lshl_add_u32 v131, v130, 13, v131
	v_bfe_u32 v132, v133, 3, 2
	v_lshl_add_u32 v124, v132, 2, v131
	v_add_u32_e32 v125, 0x10000, v124
	v_lshrrev_b32_e32 v130, 3, v133
	v_lshl_add_u32 v130, v134, 4, v130
	v_and_b32_e32 v131, 7, v133
	v_lshlrev_b32_e32 v131, 4, v131
	v_lshl_add_u32 v127, v130, 14, v131
	v_lshrrev_b32_e32 v130, 3, v133
	v_lshl_add_u32 v130, v134, 4, v130
	v_add_u32_e32 v130, 8, v130
	v_and_b32_e32 v131, 7, v133
	v_lshlrev_b32_e32 v131, 4, v131
	v_lshl_add_u32 v128, v130, 14, v131
	v_mov_b32_e32 v129, 0x43e00000
	s_mov_b32 s20, 0xc3e00000
	v_readlane_b32 s2, v253, 35
	v_readlane_b32 s3, v253, 36
	v_readlane_b32 s4, v253, 41
	v_readlane_b32 s5, v253, 42
	s_add_u32 s2, s2, 0x10000000
	s_addc_u32 s3, s3, 0
	s_add_u32 s4, s4, 0x27600000
	s_addc_u32 s5, s5, 0
	s_add_i32 s17, s16, 0
	s_min_u32 s17, s17, 0xbff
	s_lshr_b32 s18, s17, 5
	s_add_i32 s18, s18, 32
	s_and_b32 s19, s17, 31
	s_lshl_b32 s18, s18, 21
	s_lshl_b32 s19, s19, 9
	s_add_u32 s18, s18, s19
	s_add_u32 s12, s2, s18
	s_addc_u32 s13, s3, 0
	global_load_dwordx4 v[36:39], v126, s[12:13]
	s_add_u32 s12, s12, 0x8000
	s_addc_u32 s13, s13, 0
	global_load_dwordx4 v[40:43], v126, s[12:13]
	s_add_u32 s12, s12, 0x8000
	s_addc_u32 s13, s13, 0
	global_load_dwordx4 v[44:47], v126, s[12:13]
	s_add_u32 s12, s12, 0x8000
	s_addc_u32 s13, s13, 0
	global_load_dwordx4 v[48:51], v126, s[12:13]
	s_add_u32 s12, s12, 0x8000
	s_addc_u32 s13, s13, 0
	global_load_dwordx4 v[52:55], v126, s[12:13]
	s_add_u32 s12, s12, 0x8000
	s_addc_u32 s13, s13, 0
	global_load_dwordx4 v[56:59], v126, s[12:13]
	s_add_u32 s12, s12, 0x8000
	s_addc_u32 s13, s13, 0
	global_load_dwordx4 v[60:63], v126, s[12:13]
	s_add_u32 s12, s12, 0x8000
	s_addc_u32 s13, s13, 0
	global_load_dwordx4 v[64:67], v126, s[12:13]
	s_add_i32 s17, s16, 96
	s_min_u32 s17, s17, 0xbff
	s_lshr_b32 s18, s17, 5
	s_add_i32 s18, s18, 32
	s_and_b32 s19, s17, 31
	s_lshl_b32 s18, s18, 21
	s_lshl_b32 s19, s19, 9
	s_add_u32 s18, s18, s19
	s_add_u32 s12, s2, s18
	s_addc_u32 s13, s3, 0
	global_load_dwordx4 v[68:71], v126, s[12:13]
	s_add_u32 s12, s12, 0x8000
	s_addc_u32 s13, s13, 0
	global_load_dwordx4 v[72:75], v126, s[12:13]
	s_add_u32 s12, s12, 0x8000
	s_addc_u32 s13, s13, 0
	global_load_dwordx4 v[76:79], v126, s[12:13]
	s_add_u32 s12, s12, 0x8000
	s_addc_u32 s13, s13, 0
	global_load_dwordx4 v[80:83], v126, s[12:13]
	s_add_u32 s12, s12, 0x8000
	s_addc_u32 s13, s13, 0
	global_load_dwordx4 v[84:87], v126, s[12:13]
	s_add_u32 s12, s12, 0x8000
	s_addc_u32 s13, s13, 0
	global_load_dwordx4 v[88:91], v126, s[12:13]
	s_add_u32 s12, s12, 0x8000
	s_addc_u32 s13, s13, 0
	global_load_dwordx4 v[92:95], v126, s[12:13]
	s_add_u32 s12, s12, 0x8000
	s_addc_u32 s13, s13, 0
	global_load_dwordx4 v[96:99], v126, s[12:13]
	s_waitcnt vmcnt(8)
	v_mul_f32_e32 v36, 0x43000000, v36
	v_mul_f32_e32 v37, 0x43000000, v37
	v_mul_f32_e32 v38, 0x43000000, v38
	v_mul_f32_e32 v39, 0x43000000, v39
	ds_write_b128 v120, v[36:39]
	v_mul_f32_e32 v40, 0x43000000, v40
	v_mul_f32_e32 v41, 0x43000000, v41
	v_mul_f32_e32 v42, 0x43000000, v42
	v_mul_f32_e32 v43, 0x43000000, v43
	ds_write_b128 v120, v[40:43] offset:1024
	v_mul_f32_e32 v44, 0x43000000, v44
	v_mul_f32_e32 v45, 0x43000000, v45
	v_mul_f32_e32 v46, 0x43000000, v46
	v_mul_f32_e32 v47, 0x43000000, v47
	ds_write_b128 v120, v[44:47] offset:2048
	v_mul_f32_e32 v48, 0x43000000, v48
	v_mul_f32_e32 v49, 0x43000000, v49
	v_mul_f32_e32 v50, 0x43000000, v50
	v_mul_f32_e32 v51, 0x43000000, v51
	ds_write_b128 v120, v[48:51] offset:3072
	v_mul_f32_e32 v52, 0x43000000, v52
	v_mul_f32_e32 v53, 0x43000000, v53
	v_mul_f32_e32 v54, 0x43000000, v54
	v_mul_f32_e32 v55, 0x43000000, v55
	ds_write_b128 v120, v[52:55] offset:4096
	v_mul_f32_e32 v56, 0x43000000, v56
	v_mul_f32_e32 v57, 0x43000000, v57
	v_mul_f32_e32 v58, 0x43000000, v58
	v_mul_f32_e32 v59, 0x43000000, v59
	ds_write_b128 v120, v[56:59] offset:5120
	v_mul_f32_e32 v60, 0x43000000, v60
	v_mul_f32_e32 v61, 0x43000000, v61
	v_mul_f32_e32 v62, 0x43000000, v62
	v_mul_f32_e32 v63, 0x43000000, v63
	ds_write_b128 v120, v[60:63] offset:6144
	v_mul_f32_e32 v64, 0x43000000, v64
	v_mul_f32_e32 v65, 0x43000000, v65
	v_mul_f32_e32 v66, 0x43000000, v66
	v_mul_f32_e32 v67, 0x43000000, v67
	ds_write_b128 v120, v[64:67] offset:7168
	s_waitcnt lgkmcnt(0)
	s_barrier
; #define GAS __attribute__((address_space(1)))
; #define LAS __attribute__((address_space(3)))
; #define LDS_WAIT() asm volatile("s_waitcnt lgkmcnt(0)" ::: "memory")
;     const int pr = item >> 1, kb = 2 * (pr / nblk) + (item & 1), nb = pr % nblk, k0 = 64 * kb, n0 = 32 * nb;
;     const int nr = n0 + (lane & 31); const int sc = MAP == 1 ? src_col_in(nr) : nr;
;     float v[32];
; #pragma unroll
;     for (int i = 0; i < 32; ++i) v[i] = sc >= 0 ? W[(size_t)(k0 + 2 * i + (lane >> 5)) * Nsrc + sc] : 0.f;
; #pragma unroll
;     for (int i = 0; i < 32; ++i) { const int k = k0 + 2 * i + (lane >> 5); float x = v[i] * wscale; if (KS) x *= (k < ksplit ? ksA[k] : ksB[k - ksplit]); scr[(2 * i + (lane >> 5)) * 33 + (lane & 31)] = x; }
;     LDS_WAIT(); asm volatile("" ::: "memory");
;     const int c = lane & 7;
; #pragma unroll
;     for (int j = 0; j < 4; ++j) { const int n = (lane >> 3) + 8 * j; const LAS float* s = scr + (8 * c) * 33 + n;
;         const unsigned long long o = (unsigned long long)pg8::pk4_fp8(s[0 * 33], s[1 * 33], s[2 * 33], s[3 * 33]) | ((unsigned long long)pg8::pk4_fp8(s[4 * 33], s[5 * 33], s[6 * 33], s[7 * 33]) << 32);
;         *(GAS unsigned long long*)(WT + (size_t)(n0 + n) * K + k0 + 8 * c) = o; }
;     LDS_WAIT(); asm volatile("" ::: "memory");
; }
; __global__ void __launch_bounds__(NWAVES * 64, 2) hybrid_fwd(Args args) {
;     ...
;             p0_transpose_item_f8<false>(args.in[16] + (size_t)l * FF * DM, FF, DM, DM / 32, (unsigned char*)(ws + WS_WDN + l * SZ_WDN), 128.f, args.in[16], args.in[16], 0, scr, r, lane);
	s_add_i32 s17, s16, 192
	s_min_u32 s17, s17, 0xbff
	s_lshr_b32 s18, s17, 5
	s_add_i32 s18, s18, 32
	s_and_b32 s19, s17, 31
	s_lshl_b32 s18, s18, 21
	s_lshl_b32 s19, s19, 9
	s_add_u32 s18, s18, s19
	s_add_u32 s12, s2, s18
	s_addc_u32 s13, s3, 0
	global_load_dwordx4 v[36:39], v126, s[12:13]
	s_add_u32 s12, s12, 0x8000
	s_addc_u32 s13, s13, 0
	global_load_dwordx4 v[40:43], v126, s[12:13]
	s_add_u32 s12, s12, 0x8000
	s_addc_u32 s13, s13, 0
	global_load_dwordx4 v[44:47], v126, s[12:13]
	s_add_u32 s12, s12, 0x8000
	s_addc_u32 s13, s13, 0
	global_load_dwordx4 v[48:51], v126, s[12:13]
	s_add_u32 s12, s12, 0x8000
	s_addc_u32 s13, s13, 0
	global_load_dwordx4 v[52:55], v126, s[12:13]
	s_add_u32 s12, s12, 0x8000
	s_addc_u32 s13, s13, 0
	global_load_dwordx4 v[56:59], v126, s[12:13]
	s_add_u32 s12, s12, 0x8000
	s_addc_u32 s13, s13, 0
	global_load_dwordx4 v[60:63], v126, s[12:13]
	s_add_u32 s12, s12, 0x8000
	s_addc_u32 s13, s13, 0
	global_load_dwordx4 v[64:67], v126, s[12:13]
	s_add_i32 s17, s16, 0
	s_min_u32 s17, s17, 0xbff
	s_lshr_b32 s18, s17, 5
	s_add_i32 s18, s18, 32
	s_and_b32 s19, s17, 31
	s_lshl_b32 s19, s19, 21
	s_lshl_b32 s18, s18, 7
	s_add_u32 s18, s18, s19
	s_add_u32 s14, s4, s18
	s_addc_u32 s15, s5, 0
	ds_read_b32 v100, v122
	ds_read_b32 v101, v122 offset:512
	ds_read_b32 v102, v122 offset:1024
	ds_read_b32 v103, v122 offset:1536
	ds_read_b32 v104, v122 offset:2048
	ds_read_b32 v105, v122 offset:2560
	ds_read_b32 v106, v122 offset:3072
	ds_read_b32 v107, v122 offset:3584
	ds_read_b32 v108, v122 offset:4096
	ds_read_b32 v109, v122 offset:4608
	ds_read_b32 v110, v122 offset:5120
	ds_read_b32 v111, v122 offset:5632
	ds_read_b32 v112, v122 offset:6144
	ds_read_b32 v113, v122 offset:6656
	ds_read_b32 v114, v122 offset:7168
	ds_read_b32 v115, v122 offset:7680
	s_waitcnt lgkmcnt(0)
	v_max_f32_e32 v100, v100, v100
	v_max_f32_e32 v101, v101, v101
	v_max_f32_e32 v102, v102, v102
	v_max_f32_e32 v103, v103, v103
	v_max_f32_e32 v104, v104, v104
	v_max_f32_e32 v105, v105, v105
	v_max_f32_e32 v106, v106, v106
	v_max_f32_e32 v107, v107, v107
	v_max_f32_e32 v108, v108, v108
	v_max_f32_e32 v109, v109, v109
	v_max_f32_e32 v110, v110, v110
	v_max_f32_e32 v111, v111, v111
	v_max_f32_e32 v112, v112, v112
	v_max_f32_e32 v113, v113, v113
	v_max_f32_e32 v114, v114, v114
	v_max_f32_e32 v115, v115, v115
	v_med3_f32 v100, v100, s20, v129
	v_med3_f32 v101, v101, s20, v129
	v_med3_f32 v102, v102, s20, v129
	v_med3_f32 v103, v103, s20, v129
	v_med3_f32 v104, v104, s20, v129
	v_med3_f32 v105, v105, s20, v129
	v_med3_f32 v106, v106, s20, v129
	v_med3_f32 v107, v107, s20, v129
	v_med3_f32 v108, v108, s20, v129
	v_med3_f32 v109, v109, s20, v129
	v_med3_f32 v110, v110, s20, v129
	v_med3_f32 v111, v111, s20, v129
	v_med3_f32 v112, v112, s20, v129
	v_med3_f32 v113, v113, s20, v129
	v_med3_f32 v114, v114, s20, v129
	v_med3_f32 v115, v115, s20, v129
	v_mov_b32_e32 v116, 0
	v_mov_b32_e32 v117, 0
	v_mov_b32_e32 v118, 0
	v_mov_b32_e32 v119, 0
	v_cvt_pk_fp8_f32 v116, v100, v101
	v_cvt_pk_fp8_f32 v117, v104, v105
	v_cvt_pk_fp8_f32 v118, v108, v109
	v_cvt_pk_fp8_f32 v119, v112, v113
	v_cvt_pk_fp8_f32 v116, v102, v103 op_sel:[0,0,1]
	v_cvt_pk_fp8_f32 v117, v106, v107 op_sel:[0,0,1]
	v_cvt_pk_fp8_f32 v118, v110, v111 op_sel:[0,0,1]
	v_cvt_pk_fp8_f32 v119, v114, v115 op_sel:[0,0,1]
	s_nop 0
	global_store_dwordx4 v127, v[116:119], s[14:15]
	ds_read_b32 v100, v124
	ds_read_b32 v101, v124 offset:512
	ds_read_b32 v102, v124 offset:1024
	ds_read_b32 v103, v124 offset:1536
	ds_read_b32 v104, v124 offset:2048
	ds_read_b32 v105, v124 offset:2560
	ds_read_b32 v106, v124 offset:3072
	ds_read_b32 v107, v124 offset:3584
	ds_read_b32 v108, v124 offset:4096
	ds_read_b32 v109, v124 offset:4608
	ds_read_b32 v110, v124 offset:5120
	ds_read_b32 v111, v124 offset:5632
	ds_read_b32 v112, v124 offset:6144
	ds_read_b32 v113, v124 offset:6656
	ds_read_b32 v114, v124 offset:7168
	ds_read_b32 v115, v124 offset:7680
	s_waitcnt lgkmcnt(0)
	v_max_f32_e32 v100, v100, v100
	v_max_f32_e32 v101, v101, v101
	v_max_f32_e32 v102, v102, v102
	v_max_f32_e32 v103, v103, v103
	v_max_f32_e32 v104, v104, v104
	v_max_f32_e32 v105, v105, v105
	v_max_f32_e32 v106, v106, v106
	v_max_f32_e32 v107, v107, v107
	v_max_f32_e32 v108, v108, v108
	v_max_f32_e32 v109, v109, v109
	v_max_f32_e32 v110, v110, v110
	v_max_f32_e32 v111, v111, v111
	v_max_f32_e32 v112, v112, v112
	v_max_f32_e32 v113, v113, v113
	v_max_f32_e32 v114, v114, v114
	v_max_f32_e32 v115, v115, v115
	v_med3_f32 v100, v100, s20, v129
	v_med3_f32 v101, v101, s20, v129
	v_med3_f32 v102, v102, s20, v129
	v_med3_f32 v103, v103, s20, v129
	v_med3_f32 v104, v104, s20, v129
	v_med3_f32 v105, v105, s20, v129
	v_med3_f32 v106, v106, s20, v129
	v_med3_f32 v107, v107, s20, v129
	v_med3_f32 v108, v108, s20, v129
	v_med3_f32 v109, v109, s20, v129
	v_med3_f32 v110, v110, s20, v129
	v_med3_f32 v111, v111, s20, v129
	v_med3_f32 v112, v112, s20, v129
	v_med3_f32 v113, v113, s20, v129
	v_med3_f32 v114, v114, s20, v129
	v_med3_f32 v115, v115, s20, v129
	v_mov_b32_e32 v116, 0
	v_mov_b32_e32 v117, 0
	v_mov_b32_e32 v118, 0
	v_mov_b32_e32 v119, 0
	v_cvt_pk_fp8_f32 v116, v100, v101
	v_cvt_pk_fp8_f32 v117, v104, v105
	v_cvt_pk_fp8_f32 v118, v108, v109
	v_cvt_pk_fp8_f32 v119, v112, v113
	v_cvt_pk_fp8_f32 v116, v102, v103 op_sel:[0,0,1]
	v_cvt_pk_fp8_f32 v117, v106, v107 op_sel:[0,0,1]
	v_cvt_pk_fp8_f32 v118, v110, v111 op_sel:[0,0,1]
	v_cvt_pk_fp8_f32 v119, v114, v115 op_sel:[0,0,1]
	s_nop 0
	global_store_dwordx4 v128, v[116:119], s[14:15]
	s_waitcnt vmcnt(10)
	v_mul_f32_e32 v68, 0x43000000, v68
	v_mul_f32_e32 v69, 0x43000000, v69
	v_mul_f32_e32 v70, 0x43000000, v70
	v_mul_f32_e32 v71, 0x43000000, v71
	ds_write_b128 v121, v[68:71]
	v_mul_f32_e32 v72, 0x43000000, v72
	v_mul_f32_e32 v73, 0x43000000, v73
	v_mul_f32_e32 v74, 0x43000000, v74
	v_mul_f32_e32 v75, 0x43000000, v75
	ds_write_b128 v121, v[72:75] offset:1024
	v_mul_f32_e32 v76, 0x43000000, v76
	v_mul_f32_e32 v77, 0x43000000, v77
	v_mul_f32_e32 v78, 0x43000000, v78
	v_mul_f32_e32 v79, 0x43000000, v79
	ds_write_b128 v121, v[76:79] offset:2048
	v_mul_f32_e32 v80, 0x43000000, v80
	v_mul_f32_e32 v81, 0x43000000, v81
	v_mul_f32_e32 v82, 0x43000000, v82
	v_mul_f32_e32 v83, 0x43000000, v83
	ds_write_b128 v121, v[80:83] offset:3072
	v_mul_f32_e32 v84, 0x43000000, v84
	v_mul_f32_e32 v85, 0x43000000, v85
	v_mul_f32_e32 v86, 0x43000000, v86
	v_mul_f32_e32 v87, 0x43000000, v87
	ds_write_b128 v121, v[84:87] offset:4096
	v_mul_f32_e32 v88, 0x43000000, v88
	v_mul_f32_e32 v89, 0x43000000, v89
	v_mul_f32_e32 v90, 0x43000000, v90
	v_mul_f32_e32 v91, 0x43000000, v91
	ds_write_b128 v121, v[88:91] offset:5120
	v_mul_f32_e32 v92, 0x43000000, v92
	v_mul_f32_e32 v93, 0x43000000, v93
	v_mul_f32_e32 v94, 0x43000000, v94
	v_mul_f32_e32 v95, 0x43000000, v95
	ds_write_b128 v121, v[92:95] offset:6144
	v_mul_f32_e32 v96, 0x43000000, v96
	v_mul_f32_e32 v97, 0x43000000, v97
	v_mul_f32_e32 v98, 0x43000000, v98
	v_mul_f32_e32 v99, 0x43000000, v99
	ds_write_b128 v121, v[96:99] offset:7168
	s_waitcnt lgkmcnt(0)
	s_barrier
; #define GAS __attribute__((address_space(1)))
; #define LAS __attribute__((address_space(3)))
; #define LDS_WAIT() asm volatile("s_waitcnt lgkmcnt(0)" ::: "memory")
;     const int pr = item >> 1, kb = 2 * (pr / nblk) + (item & 1), nb = pr % nblk, k0 = 64 * kb, n0 = 32 * nb;
;     const int nr = n0 + (lane & 31); const int sc = MAP == 1 ? src_col_in(nr) : nr;
;     float v[32];
; #pragma unroll
;     for (int i = 0; i < 32; ++i) v[i] = sc >= 0 ? W[(size_t)(k0 + 2 * i + (lane >> 5)) * Nsrc + sc] : 0.f;
; #pragma unroll
;     for (int i = 0; i < 32; ++i) { const int k = k0 + 2 * i + (lane >> 5); float x = v[i] * wscale; if (KS) x *= (k < ksplit ? ksA[k] : ksB[k - ksplit]); scr[(2 * i + (lane >> 5)) * 33 + (lane & 31)] = x; }
;     LDS_WAIT(); asm volatile("" ::: "memory");
;     const int c = lane & 7;
; #pragma unroll
;     for (int j = 0; j < 4; ++j) { const int n = (lane >> 3) + 8 * j; const LAS float* s = scr + (8 * c) * 33 + n;
;         const unsigned long long o = (unsigned long long)pg8::pk4_fp8(s[0 * 33], s[1 * 33], s[2 * 33], s[3 * 33]) | ((unsigned long long)pg8::pk4_fp8(s[4 * 33], s[5 * 33], s[6 * 33], s[7 * 33]) << 32);
;         *(GAS unsigned long long*)(WT + (size_t)(n0 + n) * K + k0 + 8 * c) = o; }
;     LDS_WAIT(); asm volatile("" ::: "memory");
; }
; __global__ void __launch_bounds__(NWAVES * 64, 2) hybrid_fwd(Args args) {
;     ...
;             p0_transpose_item_f8<false>(args.in[16] + (size_t)l * FF * DM, FF, DM, DM / 32, (unsigned char*)(ws + WS_WDN + l * SZ_WDN), 128.f, args.in[16], args.in[16], 0, scr, r, lane);
	s_add_i32 s17, s16, 288
	s_min_u32 s17, s17, 0xbff
	s_lshr_b32 s18, s17, 5
	s_add_i32 s18, s18, 32
	s_and_b32 s19, s17, 31
	s_lshl_b32 s18, s18, 21
	s_lshl_b32 s19, s19, 9
	s_add_u32 s18, s18, s19
	s_add_u32 s12, s2, s18
	s_addc_u32 s13, s3, 0
	global_load_dwordx4 v[68:71], v126, s[12:13]
	s_add_u32 s12, s12, 0x8000
	s_addc_u32 s13, s13, 0
	global_load_dwordx4 v[72:75], v126, s[12:13]
	s_add_u32 s12, s12, 0x8000
	s_addc_u32 s13, s13, 0
	global_load_dwordx4 v[76:79], v126, s[12:13]
	s_add_u32 s12, s12, 0x8000
	s_addc_u32 s13, s13, 0
	global_load_dwordx4 v[80:83], v126, s[12:13]
	s_add_u32 s12, s12, 0x8000
	s_addc_u32 s13, s13, 0
	global_load_dwordx4 v[84:87], v126, s[12:13]
	s_add_u32 s12, s12, 0x8000
	s_addc_u32 s13, s13, 0
	global_load_dwordx4 v[88:91], v126, s[12:13]
	s_add_u32 s12, s12, 0x8000
	s_addc_u32 s13, s13, 0
	global_load_dwordx4 v[92:95], v126, s[12:13]
	s_add_u32 s12, s12, 0x8000
	s_addc_u32 s13, s13, 0
	global_load_dwordx4 v[96:99], v126, s[12:13]
	s_add_i32 s17, s16, 96
	s_min_u32 s17, s17, 0xbff
	s_lshr_b32 s18, s17, 5
	s_add_i32 s18, s18, 32
	s_and_b32 s19, s17, 31
	s_lshl_b32 s19, s19, 21
	s_lshl_b32 s18, s18, 7
	s_add_u32 s18, s18, s19
	s_add_u32 s14, s4, s18
	s_addc_u32 s15, s5, 0
	ds_read_b32 v100, v123
	ds_read_b32 v101, v123 offset:512
	ds_read_b32 v102, v123 offset:1024
	ds_read_b32 v103, v123 offset:1536
	ds_read_b32 v104, v123 offset:2048
	ds_read_b32 v105, v123 offset:2560
	ds_read_b32 v106, v123 offset:3072
	ds_read_b32 v107, v123 offset:3584
	ds_read_b32 v108, v123 offset:4096
	ds_read_b32 v109, v123 offset:4608
	ds_read_b32 v110, v123 offset:5120
	ds_read_b32 v111, v123 offset:5632
	ds_read_b32 v112, v123 offset:6144
	ds_read_b32 v113, v123 offset:6656
	ds_read_b32 v114, v123 offset:7168
	ds_read_b32 v115, v123 offset:7680
	s_waitcnt lgkmcnt(0)
	v_max_f32_e32 v100, v100, v100
	v_max_f32_e32 v101, v101, v101
	v_max_f32_e32 v102, v102, v102
	v_max_f32_e32 v103, v103, v103
	v_max_f32_e32 v104, v104, v104
	v_max_f32_e32 v105, v105, v105
	v_max_f32_e32 v106, v106, v106
	v_max_f32_e32 v107, v107, v107
	v_max_f32_e32 v108, v108, v108
	v_max_f32_e32 v109, v109, v109
	v_max_f32_e32 v110, v110, v110
	v_max_f32_e32 v111, v111, v111
	v_max_f32_e32 v112, v112, v112
	v_max_f32_e32 v113, v113, v113
	v_max_f32_e32 v114, v114, v114
	v_max_f32_e32 v115, v115, v115
	v_med3_f32 v100, v100, s20, v129
	v_med3_f32 v101, v101, s20, v129
	v_med3_f32 v102, v102, s20, v129
	v_med3_f32 v103, v103, s20, v129
	v_med3_f32 v104, v104, s20, v129
	v_med3_f32 v105, v105, s20, v129
	v_med3_f32 v106, v106, s20, v129
	v_med3_f32 v107, v107, s20, v129
	v_med3_f32 v108, v108, s20, v129
	v_med3_f32 v109, v109, s20, v129
	v_med3_f32 v110, v110, s20, v129
	v_med3_f32 v111, v111, s20, v129
	v_med3_f32 v112, v112, s20, v129
	v_med3_f32 v113, v113, s20, v129
	v_med3_f32 v114, v114, s20, v129
	v_med3_f32 v115, v115, s20, v129
	v_mov_b32_e32 v116, 0
	v_mov_b32_e32 v117, 0
	v_mov_b32_e32 v118, 0
	v_mov_b32_e32 v119, 0
	v_cvt_pk_fp8_f32 v116, v100, v101
	v_cvt_pk_fp8_f32 v117, v104, v105
	v_cvt_pk_fp8_f32 v118, v108, v109
	v_cvt_pk_fp8_f32 v119, v112, v113
	v_cvt_pk_fp8_f32 v116, v102, v103 op_sel:[0,0,1]
	v_cvt_pk_fp8_f32 v117, v106, v107 op_sel:[0,0,1]
	v_cvt_pk_fp8_f32 v118, v110, v111 op_sel:[0,0,1]
	v_cvt_pk_fp8_f32 v119, v114, v115 op_sel:[0,0,1]
	s_nop 0
	global_store_dwordx4 v127, v[116:119], s[14:15]
	ds_read_b32 v100, v125
	ds_read_b32 v101, v125 offset:512
	ds_read_b32 v102, v125 offset:1024
	ds_read_b32 v103, v125 offset:1536
	ds_read_b32 v104, v125 offset:2048
	ds_read_b32 v105, v125 offset:2560
	ds_read_b32 v106, v125 offset:3072
	ds_read_b32 v107, v125 offset:3584
	ds_read_b32 v108, v125 offset:4096
	ds_read_b32 v109, v125 offset:4608
	ds_read_b32 v110, v125 offset:5120
	ds_read_b32 v111, v125 offset:5632
	ds_read_b32 v112, v125 offset:6144
	ds_read_b32 v113, v125 offset:6656
	ds_read_b32 v114, v125 offset:7168
	ds_read_b32 v115, v125 offset:7680
	s_waitcnt lgkmcnt(0)
	v_max_f32_e32 v100, v100, v100
	v_max_f32_e32 v101, v101, v101
	v_max_f32_e32 v102, v102, v102
	v_max_f32_e32 v103, v103, v103
	v_max_f32_e32 v104, v104, v104
	v_max_f32_e32 v105, v105, v105
	v_max_f32_e32 v106, v106, v106
	v_max_f32_e32 v107, v107, v107
	v_max_f32_e32 v108, v108, v108
	v_max_f32_e32 v109, v109, v109
	v_max_f32_e32 v110, v110, v110
	v_max_f32_e32 v111, v111, v111
	v_max_f32_e32 v112, v112, v112
	v_max_f32_e32 v113, v113, v113
	v_max_f32_e32 v114, v114, v114
	v_max_f32_e32 v115, v115, v115
	v_med3_f32 v100, v100, s20, v129
	v_med3_f32 v101, v101, s20, v129
	v_med3_f32 v102, v102, s20, v129
	v_med3_f32 v103, v103, s20, v129
	v_med3_f32 v104, v104, s20, v129
	v_med3_f32 v105, v105, s20, v129
	v_med3_f32 v106, v106, s20, v129
	v_med3_f32 v107, v107, s20, v129
	v_med3_f32 v108, v108, s20, v129
	v_med3_f32 v109, v109, s20, v129
	v_med3_f32 v110, v110, s20, v129
	v_med3_f32 v111, v111, s20, v129
	v_med3_f32 v112, v112, s20, v129
	v_med3_f32 v113, v113, s20, v129
	v_med3_f32 v114, v114, s20, v129
	v_med3_f32 v115, v115, s20, v129
	v_mov_b32_e32 v116, 0
	v_mov_b32_e32 v117, 0
	v_mov_b32_e32 v118, 0
	v_mov_b32_e32 v119, 0
	v_cvt_pk_fp8_f32 v116, v100, v101
	v_cvt_pk_fp8_f32 v117, v104, v105
	v_cvt_pk_fp8_f32 v118, v108, v109
	v_cvt_pk_fp8_f32 v119, v112, v113
	v_cvt_pk_fp8_f32 v116, v102, v103 op_sel:[0,0,1]
	v_cvt_pk_fp8_f32 v117, v106, v107 op_sel:[0,0,1]
	v_cvt_pk_fp8_f32 v118, v110, v111 op_sel:[0,0,1]
	v_cvt_pk_fp8_f32 v119, v114, v115 op_sel:[0,0,1]
	s_nop 0
	global_store_dwordx4 v128, v[116:119], s[14:15]
	s_waitcnt vmcnt(12)
	v_mul_f32_e32 v36, 0x43000000, v36
	v_mul_f32_e32 v37, 0x43000000, v37
	v_mul_f32_e32 v38, 0x43000000, v38
	v_mul_f32_e32 v39, 0x43000000, v39
	ds_write_b128 v120, v[36:39]
	v_mul_f32_e32 v40, 0x43000000, v40
	v_mul_f32_e32 v41, 0x43000000, v41
	v_mul_f32_e32 v42, 0x43000000, v42
	v_mul_f32_e32 v43, 0x43000000, v43
	ds_write_b128 v120, v[40:43] offset:1024
	v_mul_f32_e32 v44, 0x43000000, v44
	v_mul_f32_e32 v45, 0x43000000, v45
	v_mul_f32_e32 v46, 0x43000000, v46
	v_mul_f32_e32 v47, 0x43000000, v47
	ds_write_b128 v120, v[44:47] offset:2048
	v_mul_f32_e32 v48, 0x43000000, v48
	v_mul_f32_e32 v49, 0x43000000, v49
	v_mul_f32_e32 v50, 0x43000000, v50
	v_mul_f32_e32 v51, 0x43000000, v51
	ds_write_b128 v120, v[48:51] offset:3072
	v_mul_f32_e32 v52, 0x43000000, v52
	v_mul_f32_e32 v53, 0x43000000, v53
	v_mul_f32_e32 v54, 0x43000000, v54
	v_mul_f32_e32 v55, 0x43000000, v55
	ds_write_b128 v120, v[52:55] offset:4096
	v_mul_f32_e32 v56, 0x43000000, v56
	v_mul_f32_e32 v57, 0x43000000, v57
	v_mul_f32_e32 v58, 0x43000000, v58
	v_mul_f32_e32 v59, 0x43000000, v59
	ds_write_b128 v120, v[56:59] offset:5120
	v_mul_f32_e32 v60, 0x43000000, v60
	v_mul_f32_e32 v61, 0x43000000, v61
	v_mul_f32_e32 v62, 0x43000000, v62
	v_mul_f32_e32 v63, 0x43000000, v63
	ds_write_b128 v120, v[60:63] offset:6144
	v_mul_f32_e32 v64, 0x43000000, v64
	v_mul_f32_e32 v65, 0x43000000, v65
	v_mul_f32_e32 v66, 0x43000000, v66
	v_mul_f32_e32 v67, 0x43000000, v67
	ds_write_b128 v120, v[64:67] offset:7168
	s_waitcnt lgkmcnt(0)
	s_barrier
; #define GAS __attribute__((address_space(1)))
; #define LAS __attribute__((address_space(3)))
; #define LDS_WAIT() asm volatile("s_waitcnt lgkmcnt(0)" ::: "memory")
;     const int pr = item >> 1, kb = 2 * (pr / nblk) + (item & 1), nb = pr % nblk, k0 = 64 * kb, n0 = 32 * nb;
;     const int nr = n0 + (lane & 31); const int sc = MAP == 1 ? src_col_in(nr) : nr;
;     float v[32];
; #pragma unroll
;     for (int i = 0; i < 32; ++i) v[i] = sc >= 0 ? W[(size_t)(k0 + 2 * i + (lane >> 5)) * Nsrc + sc] : 0.f;
; #pragma unroll
;     for (int i = 0; i < 32; ++i) { const int k = k0 + 2 * i + (lane >> 5); float x = v[i] * wscale; if (KS) x *= (k < ksplit ? ksA[k] : ksB[k - ksplit]); scr[(2 * i + (lane >> 5)) * 33 + (lane & 31)] = x; }
;     LDS_WAIT(); asm volatile("" ::: "memory");
;     const int c = lane & 7;
; #pragma unroll
;     for (int j = 0; j < 4; ++j) { const int n = (lane >> 3) + 8 * j; const LAS float* s = scr + (8 * c) * 33 + n;
;         const unsigned long long o = (unsigned long long)pg8::pk4_fp8(s[0 * 33], s[1 * 33], s[2 * 33], s[3 * 33]) | ((unsigned long long)pg8::pk4_fp8(s[4 * 33], s[5 * 33], s[6 * 33], s[7 * 33]) << 32);
;         *(GAS unsigned long long*)(WT + (size_t)(n0 + n) * K + k0 + 8 * c) = o; }
;     LDS_WAIT(); asm volatile("" ::: "memory");
; }
; __global__ void __launch_bounds__(NWAVES * 64, 2) hybrid_fwd(Args args) {
;     ...
;             p0_transpose_item_f8<false>(args.in[16] + (size_t)l * FF * DM, FF, DM, DM / 32, (unsigned char*)(ws + WS_WDN + l * SZ_WDN), 128.f, args.in[16], args.in[16], 0, scr, r, lane);
	s_add_i32 s17, s16, 384
	s_min_u32 s17, s17, 0xbff
	s_lshr_b32 s18, s17, 5
	s_add_i32 s18, s18, 32
	s_and_b32 s19, s17, 31
	s_lshl_b32 s18, s18, 21
	s_lshl_b32 s19, s19, 9
	s_add_u32 s18, s18, s19
	s_add_u32 s12, s2, s18
	s_addc_u32 s13, s3, 0
	global_load_dwordx4 v[36:39], v126, s[12:13]
	s_add_u32 s12, s12, 0x8000
	s_addc_u32 s13, s13, 0
	global_load_dwordx4 v[40:43], v126, s[12:13]
	s_add_u32 s12, s12, 0x8000
	s_addc_u32 s13, s13, 0
	global_load_dwordx4 v[44:47], v126, s[12:13]
	s_add_u32 s12, s12, 0x8000
	s_addc_u32 s13, s13, 0
	global_load_dwordx4 v[48:51], v126, s[12:13]
	s_add_u32 s12, s12, 0x8000
	s_addc_u32 s13, s13, 0
	global_load_dwordx4 v[52:55], v126, s[12:13]
	s_add_u32 s12, s12, 0x8000
	s_addc_u32 s13, s13, 0
	global_load_dwordx4 v[56:59], v126, s[12:13]
	s_add_u32 s12, s12, 0x8000
	s_addc_u32 s13, s13, 0
	global_load_dwordx4 v[60:63], v126, s[12:13]
	s_add_u32 s12, s12, 0x8000
	s_addc_u32 s13, s13, 0
	global_load_dwordx4 v[64:67], v126, s[12:13]
	s_add_i32 s17, s16, 192
	s_min_u32 s17, s17, 0xbff
	s_lshr_b32 s18, s17, 5
	s_add_i32 s18, s18, 32
	s_and_b32 s19, s17, 31
	s_lshl_b32 s19, s19, 21
	s_lshl_b32 s18, s18, 7
	s_add_u32 s18, s18, s19
	s_add_u32 s14, s4, s18
	s_addc_u32 s15, s5, 0
	ds_read_b32 v100, v122
	ds_read_b32 v101, v122 offset:512
	ds_read_b32 v102, v122 offset:1024
	ds_read_b32 v103, v122 offset:1536
	ds_read_b32 v104, v122 offset:2048
	ds_read_b32 v105, v122 offset:2560
	ds_read_b32 v106, v122 offset:3072
	ds_read_b32 v107, v122 offset:3584
	ds_read_b32 v108, v122 offset:4096
	ds_read_b32 v109, v122 offset:4608
	ds_read_b32 v110, v122 offset:5120
	ds_read_b32 v111, v122 offset:5632
	ds_read_b32 v112, v122 offset:6144
	ds_read_b32 v113, v122 offset:6656
	ds_read_b32 v114, v122 offset:7168
	ds_read_b32 v115, v122 offset:7680
	s_waitcnt lgkmcnt(0)
	v_max_f32_e32 v100, v100, v100
	v_max_f32_e32 v101, v101, v101
	v_max_f32_e32 v102, v102, v102
	v_max_f32_e32 v103, v103, v103
	v_max_f32_e32 v104, v104, v104
	v_max_f32_e32 v105, v105, v105
	v_max_f32_e32 v106, v106, v106
	v_max_f32_e32 v107, v107, v107
	v_max_f32_e32 v108, v108, v108
	v_max_f32_e32 v109, v109, v109
	v_max_f32_e32 v110, v110, v110
	v_max_f32_e32 v111, v111, v111
	v_max_f32_e32 v112, v112, v112
	v_max_f32_e32 v113, v113, v113
	v_max_f32_e32 v114, v114, v114
	v_max_f32_e32 v115, v115, v115
	v_med3_f32 v100, v100, s20, v129
	v_med3_f32 v101, v101, s20, v129
	v_med3_f32 v102, v102, s20, v129
	v_med3_f32 v103, v103, s20, v129
	v_med3_f32 v104, v104, s20, v129
	v_med3_f32 v105, v105, s20, v129
	v_med3_f32 v106, v106, s20, v129
	v_med3_f32 v107, v107, s20, v129
	v_med3_f32 v108, v108, s20, v129
	v_med3_f32 v109, v109, s20, v129
	v_med3_f32 v110, v110, s20, v129
	v_med3_f32 v111, v111, s20, v129
	v_med3_f32 v112, v112, s20, v129
	v_med3_f32 v113, v113, s20, v129
	v_med3_f32 v114, v114, s20, v129
	v_med3_f32 v115, v115, s20, v129
	v_mov_b32_e32 v116, 0
	v_mov_b32_e32 v117, 0
	v_mov_b32_e32 v118, 0
	v_mov_b32_e32 v119, 0
	v_cvt_pk_fp8_f32 v116, v100, v101
	v_cvt_pk_fp8_f32 v117, v104, v105
	v_cvt_pk_fp8_f32 v118, v108, v109
	v_cvt_pk_fp8_f32 v119, v112, v113
	v_cvt_pk_fp8_f32 v116, v102, v103 op_sel:[0,0,1]
	v_cvt_pk_fp8_f32 v117, v106, v107 op_sel:[0,0,1]
	v_cvt_pk_fp8_f32 v118, v110, v111 op_sel:[0,0,1]
	v_cvt_pk_fp8_f32 v119, v114, v115 op_sel:[0,0,1]
	s_nop 0
	global_store_dwordx4 v127, v[116:119], s[14:15]
	ds_read_b32 v100, v124
	ds_read_b32 v101, v124 offset:512
	ds_read_b32 v102, v124 offset:1024
	ds_read_b32 v103, v124 offset:1536
	ds_read_b32 v104, v124 offset:2048
	ds_read_b32 v105, v124 offset:2560
	ds_read_b32 v106, v124 offset:3072
	ds_read_b32 v107, v124 offset:3584
	ds_read_b32 v108, v124 offset:4096
	ds_read_b32 v109, v124 offset:4608
	ds_read_b32 v110, v124 offset:5120
	ds_read_b32 v111, v124 offset:5632
	ds_read_b32 v112, v124 offset:6144
	ds_read_b32 v113, v124 offset:6656
	ds_read_b32 v114, v124 offset:7168
	ds_read_b32 v115, v124 offset:7680
	s_waitcnt lgkmcnt(0)
	v_max_f32_e32 v100, v100, v100
	v_max_f32_e32 v101, v101, v101
	v_max_f32_e32 v102, v102, v102
	v_max_f32_e32 v103, v103, v103
	v_max_f32_e32 v104, v104, v104
	v_max_f32_e32 v105, v105, v105
	v_max_f32_e32 v106, v106, v106
	v_max_f32_e32 v107, v107, v107
	v_max_f32_e32 v108, v108, v108
	v_max_f32_e32 v109, v109, v109
	v_max_f32_e32 v110, v110, v110
	v_max_f32_e32 v111, v111, v111
	v_max_f32_e32 v112, v112, v112
	v_max_f32_e32 v113, v113, v113
	v_max_f32_e32 v114, v114, v114
	v_max_f32_e32 v115, v115, v115
	v_med3_f32 v100, v100, s20, v129
	v_med3_f32 v101, v101, s20, v129
	v_med3_f32 v102, v102, s20, v129
	v_med3_f32 v103, v103, s20, v129
	v_med3_f32 v104, v104, s20, v129
	v_med3_f32 v105, v105, s20, v129
	v_med3_f32 v106, v106, s20, v129
	v_med3_f32 v107, v107, s20, v129
	v_med3_f32 v108, v108, s20, v129
	v_med3_f32 v109, v109, s20, v129
	v_med3_f32 v110, v110, s20, v129
	v_med3_f32 v111, v111, s20, v129
	v_med3_f32 v112, v112, s20, v129
	v_med3_f32 v113, v113, s20, v129
	v_med3_f32 v114, v114, s20, v129
	v_med3_f32 v115, v115, s20, v129
	v_mov_b32_e32 v116, 0
	v_mov_b32_e32 v117, 0
	v_mov_b32_e32 v118, 0
	v_mov_b32_e32 v119, 0
	v_cvt_pk_fp8_f32 v116, v100, v101
	v_cvt_pk_fp8_f32 v117, v104, v105
	v_cvt_pk_fp8_f32 v118, v108, v109
	v_cvt_pk_fp8_f32 v119, v112, v113
	v_cvt_pk_fp8_f32 v116, v102, v103 op_sel:[0,0,1]
	v_cvt_pk_fp8_f32 v117, v106, v107 op_sel:[0,0,1]
	v_cvt_pk_fp8_f32 v118, v110, v111 op_sel:[0,0,1]
	v_cvt_pk_fp8_f32 v119, v114, v115 op_sel:[0,0,1]
	s_nop 0
	global_store_dwordx4 v128, v[116:119], s[14:15]
	s_waitcnt vmcnt(12)
	v_mul_f32_e32 v68, 0x43000000, v68
	v_mul_f32_e32 v69, 0x43000000, v69
	v_mul_f32_e32 v70, 0x43000000, v70
	v_mul_f32_e32 v71, 0x43000000, v71
	ds_write_b128 v121, v[68:71]
	v_mul_f32_e32 v72, 0x43000000, v72
	v_mul_f32_e32 v73, 0x43000000, v73
	v_mul_f32_e32 v74, 0x43000000, v74
	v_mul_f32_e32 v75, 0x43000000, v75
	ds_write_b128 v121, v[72:75] offset:1024
	v_mul_f32_e32 v76, 0x43000000, v76
	v_mul_f32_e32 v77, 0x43000000, v77
	v_mul_f32_e32 v78, 0x43000000, v78
	v_mul_f32_e32 v79, 0x43000000, v79
	ds_write_b128 v121, v[76:79] offset:2048
	v_mul_f32_e32 v80, 0x43000000, v80
	v_mul_f32_e32 v81, 0x43000000, v81
	v_mul_f32_e32 v82, 0x43000000, v82
	v_mul_f32_e32 v83, 0x43000000, v83
	ds_write_b128 v121, v[80:83] offset:3072
	v_mul_f32_e32 v84, 0x43000000, v84
	v_mul_f32_e32 v85, 0x43000000, v85
	v_mul_f32_e32 v86, 0x43000000, v86
	v_mul_f32_e32 v87, 0x43000000, v87
	ds_write_b128 v121, v[84:87] offset:4096
	v_mul_f32_e32 v88, 0x43000000, v88
	v_mul_f32_e32 v89, 0x43000000, v89
	v_mul_f32_e32 v90, 0x43000000, v90
	v_mul_f32_e32 v91, 0x43000000, v91
	ds_write_b128 v121, v[88:91] offset:5120
	v_mul_f32_e32 v92, 0x43000000, v92
	v_mul_f32_e32 v93, 0x43000000, v93
	v_mul_f32_e32 v94, 0x43000000, v94
	v_mul_f32_e32 v95, 0x43000000, v95
	ds_write_b128 v121, v[92:95] offset:6144
	v_mul_f32_e32 v96, 0x43000000, v96
	v_mul_f32_e32 v97, 0x43000000, v97
	v_mul_f32_e32 v98, 0x43000000, v98
	v_mul_f32_e32 v99, 0x43000000, v99
	ds_write_b128 v121, v[96:99] offset:7168
	s_waitcnt lgkmcnt(0)
	s_barrier
; #define GAS __attribute__((address_space(1)))
; #define LAS __attribute__((address_space(3)))
; #define LDS_WAIT() asm volatile("s_waitcnt lgkmcnt(0)" ::: "memory")
;     const int pr = item >> 1, kb = 2 * (pr / nblk) + (item & 1), nb = pr % nblk, k0 = 64 * kb, n0 = 32 * nb;
;     const int nr = n0 + (lane & 31); const int sc = MAP == 1 ? src_col_in(nr) : nr;
;     float v[32];
; #pragma unroll
;     for (int i = 0; i < 32; ++i) v[i] = sc >= 0 ? W[(size_t)(k0 + 2 * i + (lane >> 5)) * Nsrc + sc] : 0.f;
; #pragma unroll
;     for (int i = 0; i < 32; ++i) { const int k = k0 + 2 * i + (lane >> 5); float x = v[i] * wscale; if (KS) x *= (k < ksplit ? ksA[k] : ksB[k - ksplit]); scr[(2 * i + (lane >> 5)) * 33 + (lane & 31)] = x; }
;     LDS_WAIT(); asm volatile("" ::: "memory");
;     const int c = lane & 7;
; #pragma unroll
;     for (int j = 0; j < 4; ++j) { const int n = (lane >> 3) + 8 * j; const LAS float* s = scr + (8 * c) * 33 + n;
;         const unsigned long long o = (unsigned long long)pg8::pk4_fp8(s[0 * 33], s[1 * 33], s[2 * 33], s[3 * 33]) | ((unsigned long long)pg8::pk4_fp8(s[4 * 33], s[5 * 33], s[6 * 33], s[7 * 33]) << 32);
;         *(GAS unsigned long long*)(WT + (size_t)(n0 + n) * K + k0 + 8 * c) = o; }
;     LDS_WAIT(); asm volatile("" ::: "memory");
; }
; __global__ void __launch_bounds__(NWAVES * 64, 2) hybrid_fwd(Args args) {
;     ...
;             p0_transpose_item_f8<false>(args.in[16] + (size_t)l * FF * DM, FF, DM, DM / 32, (unsigned char*)(ws + WS_WDN + l * SZ_WDN), 128.f, args.in[16], args.in[16], 0, scr, r, lane);
	s_add_i32 s17, s16, 480
	s_min_u32 s17, s17, 0xbff
	s_lshr_b32 s18, s17, 5
	s_add_i32 s18, s18, 32
	s_and_b32 s19, s17, 31
	s_lshl_b32 s18, s18, 21
	s_lshl_b32 s19, s19, 9
	s_add_u32 s18, s18, s19
	s_add_u32 s12, s2, s18
	s_addc_u32 s13, s3, 0
	global_load_dwordx4 v[68:71], v126, s[12:13]
	s_add_u32 s12, s12, 0x8000
	s_addc_u32 s13, s13, 0
	global_load_dwordx4 v[72:75], v126, s[12:13]
	s_add_u32 s12, s12, 0x8000
	s_addc_u32 s13, s13, 0
	global_load_dwordx4 v[76:79], v126, s[12:13]
	s_add_u32 s12, s12, 0x8000
	s_addc_u32 s13, s13, 0
	global_load_dwordx4 v[80:83], v126, s[12:13]
	s_add_u32 s12, s12, 0x8000
	s_addc_u32 s13, s13, 0
	global_load_dwordx4 v[84:87], v126, s[12:13]
	s_add_u32 s12, s12, 0x8000
	s_addc_u32 s13, s13, 0
	global_load_dwordx4 v[88:91], v126, s[12:13]
	s_add_u32 s12, s12, 0x8000
	s_addc_u32 s13, s13, 0
	global_load_dwordx4 v[92:95], v126, s[12:13]
	s_add_u32 s12, s12, 0x8000
	s_addc_u32 s13, s13, 0
	global_load_dwordx4 v[96:99], v126, s[12:13]
	s_add_i32 s17, s16, 288
	s_min_u32 s17, s17, 0xbff
	s_lshr_b32 s18, s17, 5
	s_add_i32 s18, s18, 32
	s_and_b32 s19, s17, 31
	s_lshl_b32 s19, s19, 21
	s_lshl_b32 s18, s18, 7
	s_add_u32 s18, s18, s19
	s_add_u32 s14, s4, s18
	s_addc_u32 s15, s5, 0
	ds_read_b32 v100, v123
	ds_read_b32 v101, v123 offset:512
	ds_read_b32 v102, v123 offset:1024
	ds_read_b32 v103, v123 offset:1536
	ds_read_b32 v104, v123 offset:2048
	ds_read_b32 v105, v123 offset:2560
	ds_read_b32 v106, v123 offset:3072
	ds_read_b32 v107, v123 offset:3584
	ds_read_b32 v108, v123 offset:4096
	ds_read_b32 v109, v123 offset:4608
	ds_read_b32 v110, v123 offset:5120
	ds_read_b32 v111, v123 offset:5632
	ds_read_b32 v112, v123 offset:6144
	ds_read_b32 v113, v123 offset:6656
	ds_read_b32 v114, v123 offset:7168
	ds_read_b32 v115, v123 offset:7680
	s_waitcnt lgkmcnt(0)
	v_max_f32_e32 v100, v100, v100
	v_max_f32_e32 v101, v101, v101
	v_max_f32_e32 v102, v102, v102
	v_max_f32_e32 v103, v103, v103
	v_max_f32_e32 v104, v104, v104
	v_max_f32_e32 v105, v105, v105
	v_max_f32_e32 v106, v106, v106
	v_max_f32_e32 v107, v107, v107
	v_max_f32_e32 v108, v108, v108
	v_max_f32_e32 v109, v109, v109
	v_max_f32_e32 v110, v110, v110
	v_max_f32_e32 v111, v111, v111
	v_max_f32_e32 v112, v112, v112
	v_max_f32_e32 v113, v113, v113
	v_max_f32_e32 v114, v114, v114
	v_max_f32_e32 v115, v115, v115
	v_med3_f32 v100, v100, s20, v129
	v_med3_f32 v101, v101, s20, v129
	v_med3_f32 v102, v102, s20, v129
	v_med3_f32 v103, v103, s20, v129
	v_med3_f32 v104, v104, s20, v129
	v_med3_f32 v105, v105, s20, v129
	v_med3_f32 v106, v106, s20, v129
	v_med3_f32 v107, v107, s20, v129
	v_med3_f32 v108, v108, s20, v129
	v_med3_f32 v109, v109, s20, v129
	v_med3_f32 v110, v110, s20, v129
	v_med3_f32 v111, v111, s20, v129
	v_med3_f32 v112, v112, s20, v129
	v_med3_f32 v113, v113, s20, v129
	v_med3_f32 v114, v114, s20, v129
	v_med3_f32 v115, v115, s20, v129
	v_mov_b32_e32 v116, 0
	v_mov_b32_e32 v117, 0
	v_mov_b32_e32 v118, 0
	v_mov_b32_e32 v119, 0
	v_cvt_pk_fp8_f32 v116, v100, v101
	v_cvt_pk_fp8_f32 v117, v104, v105
	v_cvt_pk_fp8_f32 v118, v108, v109
	v_cvt_pk_fp8_f32 v119, v112, v113
	v_cvt_pk_fp8_f32 v116, v102, v103 op_sel:[0,0,1]
	v_cvt_pk_fp8_f32 v117, v106, v107 op_sel:[0,0,1]
	v_cvt_pk_fp8_f32 v118, v110, v111 op_sel:[0,0,1]
	v_cvt_pk_fp8_f32 v119, v114, v115 op_sel:[0,0,1]
	s_nop 0
	global_store_dwordx4 v127, v[116:119], s[14:15]
	ds_read_b32 v100, v125
	ds_read_b32 v101, v125 offset:512
	ds_read_b32 v102, v125 offset:1024
	ds_read_b32 v103, v125 offset:1536
	ds_read_b32 v104, v125 offset:2048
	ds_read_b32 v105, v125 offset:2560
	ds_read_b32 v106, v125 offset:3072
	ds_read_b32 v107, v125 offset:3584
	ds_read_b32 v108, v125 offset:4096
	ds_read_b32 v109, v125 offset:4608
	ds_read_b32 v110, v125 offset:5120
	ds_read_b32 v111, v125 offset:5632
	ds_read_b32 v112, v125 offset:6144
	ds_read_b32 v113, v125 offset:6656
	ds_read_b32 v114, v125 offset:7168
	ds_read_b32 v115, v125 offset:7680
	s_waitcnt lgkmcnt(0)
	v_max_f32_e32 v100, v100, v100
	v_max_f32_e32 v101, v101, v101
	v_max_f32_e32 v102, v102, v102
	v_max_f32_e32 v103, v103, v103
	v_max_f32_e32 v104, v104, v104
	v_max_f32_e32 v105, v105, v105
	v_max_f32_e32 v106, v106, v106
	v_max_f32_e32 v107, v107, v107
	v_max_f32_e32 v108, v108, v108
	v_max_f32_e32 v109, v109, v109
	v_max_f32_e32 v110, v110, v110
	v_max_f32_e32 v111, v111, v111
	v_max_f32_e32 v112, v112, v112
	v_max_f32_e32 v113, v113, v113
	v_max_f32_e32 v114, v114, v114
	v_max_f32_e32 v115, v115, v115
	v_med3_f32 v100, v100, s20, v129
	v_med3_f32 v101, v101, s20, v129
	v_med3_f32 v102, v102, s20, v129
	v_med3_f32 v103, v103, s20, v129
	v_med3_f32 v104, v104, s20, v129
	v_med3_f32 v105, v105, s20, v129
	v_med3_f32 v106, v106, s20, v129
	v_med3_f32 v107, v107, s20, v129
	v_med3_f32 v108, v108, s20, v129
	v_med3_f32 v109, v109, s20, v129
	v_med3_f32 v110, v110, s20, v129
	v_med3_f32 v111, v111, s20, v129
	v_med3_f32 v112, v112, s20, v129
	v_med3_f32 v113, v113, s20, v129
	v_med3_f32 v114, v114, s20, v129
	v_med3_f32 v115, v115, s20, v129
	v_mov_b32_e32 v116, 0
	v_mov_b32_e32 v117, 0
	v_mov_b32_e32 v118, 0
	v_mov_b32_e32 v119, 0
	v_cvt_pk_fp8_f32 v116, v100, v101
	v_cvt_pk_fp8_f32 v117, v104, v105
	v_cvt_pk_fp8_f32 v118, v108, v109
	v_cvt_pk_fp8_f32 v119, v112, v113
	v_cvt_pk_fp8_f32 v116, v102, v103 op_sel:[0,0,1]
	v_cvt_pk_fp8_f32 v117, v106, v107 op_sel:[0,0,1]
	v_cvt_pk_fp8_f32 v118, v110, v111 op_sel:[0,0,1]
	v_cvt_pk_fp8_f32 v119, v114, v115 op_sel:[0,0,1]
	s_nop 0
	global_store_dwordx4 v128, v[116:119], s[14:15]
	s_waitcnt vmcnt(12)
	v_mul_f32_e32 v36, 0x43000000, v36
	v_mul_f32_e32 v37, 0x43000000, v37
	v_mul_f32_e32 v38, 0x43000000, v38
	v_mul_f32_e32 v39, 0x43000000, v39
	ds_write_b128 v120, v[36:39]
	v_mul_f32_e32 v40, 0x43000000, v40
	v_mul_f32_e32 v41, 0x43000000, v41
	v_mul_f32_e32 v42, 0x43000000, v42
	v_mul_f32_e32 v43, 0x43000000, v43
	ds_write_b128 v120, v[40:43] offset:1024
	v_mul_f32_e32 v44, 0x43000000, v44
	v_mul_f32_e32 v45, 0x43000000, v45
	v_mul_f32_e32 v46, 0x43000000, v46
	v_mul_f32_e32 v47, 0x43000000, v47
	ds_write_b128 v120, v[44:47] offset:2048
	v_mul_f32_e32 v48, 0x43000000, v48
	v_mul_f32_e32 v49, 0x43000000, v49
	v_mul_f32_e32 v50, 0x43000000, v50
	v_mul_f32_e32 v51, 0x43000000, v51
	ds_write_b128 v120, v[48:51] offset:3072
	v_mul_f32_e32 v52, 0x43000000, v52
	v_mul_f32_e32 v53, 0x43000000, v53
	v_mul_f32_e32 v54, 0x43000000, v54
	v_mul_f32_e32 v55, 0x43000000, v55
	ds_write_b128 v120, v[52:55] offset:4096
	v_mul_f32_e32 v56, 0x43000000, v56
	v_mul_f32_e32 v57, 0x43000000, v57
	v_mul_f32_e32 v58, 0x43000000, v58
	v_mul_f32_e32 v59, 0x43000000, v59
	ds_write_b128 v120, v[56:59] offset:5120
	v_mul_f32_e32 v60, 0x43000000, v60
	v_mul_f32_e32 v61, 0x43000000, v61
	v_mul_f32_e32 v62, 0x43000000, v62
	v_mul_f32_e32 v63, 0x43000000, v63
	ds_write_b128 v120, v[60:63] offset:6144
	v_mul_f32_e32 v64, 0x43000000, v64
	v_mul_f32_e32 v65, 0x43000000, v65
	v_mul_f32_e32 v66, 0x43000000, v66
	v_mul_f32_e32 v67, 0x43000000, v67
	ds_write_b128 v120, v[64:67] offset:7168
	s_waitcnt lgkmcnt(0)
	s_barrier
; #define GAS __attribute__((address_space(1)))
; #define LAS __attribute__((address_space(3)))
; #define LDS_WAIT() asm volatile("s_waitcnt lgkmcnt(0)" ::: "memory")
;     const int pr = item >> 1, kb = 2 * (pr / nblk) + (item & 1), nb = pr % nblk, k0 = 64 * kb, n0 = 32 * nb;
;     const int nr = n0 + (lane & 31); const int sc = MAP == 1 ? src_col_in(nr) : nr;
;     float v[32];
; #pragma unroll
;     for (int i = 0; i < 32; ++i) v[i] = sc >= 0 ? W[(size_t)(k0 + 2 * i + (lane >> 5)) * Nsrc + sc] : 0.f;
; #pragma unroll
;     for (int i = 0; i < 32; ++i) { const int k = k0 + 2 * i + (lane >> 5); float x = v[i] * wscale; if (KS) x *= (k < ksplit ? ksA[k] : ksB[k - ksplit]); scr[(2 * i + (lane >> 5)) * 33 + (lane & 31)] = x; }
;     LDS_WAIT(); asm volatile("" ::: "memory");
;     const int c = lane & 7;
; #pragma unroll
;     for (int j = 0; j < 4; ++j) { const int n = (lane >> 3) + 8 * j; const LAS float* s = scr + (8 * c) * 33 + n;
;         const unsigned long long o = (unsigned long long)pg8::pk4_fp8(s[0 * 33], s[1 * 33], s[2 * 33], s[3 * 33]) | ((unsigned long long)pg8::pk4_fp8(s[4 * 33], s[5 * 33], s[6 * 33], s[7 * 33]) << 32);
;         *(GAS unsigned long long*)(WT + (size_t)(n0 + n) * K + k0 + 8 * c) = o; }
;     LDS_WAIT(); asm volatile("" ::: "memory");
; }
; __global__ void __launch_bounds__(NWAVES * 64, 2) hybrid_fwd(Args args) {
;     ...
;             p0_transpose_item_f8<false>(args.in[16] + (size_t)l * FF * DM, FF, DM, DM / 32, (unsigned char*)(ws + WS_WDN + l * SZ_WDN), 128.f, args.in[16], args.in[16], 0, scr, r, lane);
	s_add_i32 s17, s16, 576
	s_min_u32 s17, s17, 0xbff
	s_lshr_b32 s18, s17, 5
	s_add_i32 s18, s18, 32
	s_and_b32 s19, s17, 31
	s_lshl_b32 s18, s18, 21
	s_lshl_b32 s19, s19, 9
	s_add_u32 s18, s18, s19
	s_add_u32 s12, s2, s18
	s_addc_u32 s13, s3, 0
	global_load_dwordx4 v[36:39], v126, s[12:13]
	s_add_u32 s12, s12, 0x8000
	s_addc_u32 s13, s13, 0
	global_load_dwordx4 v[40:43], v126, s[12:13]
	s_add_u32 s12, s12, 0x8000
	s_addc_u32 s13, s13, 0
	global_load_dwordx4 v[44:47], v126, s[12:13]
	s_add_u32 s12, s12, 0x8000
	s_addc_u32 s13, s13, 0
	global_load_dwordx4 v[48:51], v126, s[12:13]
	s_add_u32 s12, s12, 0x8000
	s_addc_u32 s13, s13, 0
	global_load_dwordx4 v[52:55], v126, s[12:13]
	s_add_u32 s12, s12, 0x8000
	s_addc_u32 s13, s13, 0
	global_load_dwordx4 v[56:59], v126, s[12:13]
	s_add_u32 s12, s12, 0x8000
	s_addc_u32 s13, s13, 0
	global_load_dwordx4 v[60:63], v126, s[12:13]
	s_add_u32 s12, s12, 0x8000
	s_addc_u32 s13, s13, 0
	global_load_dwordx4 v[64:67], v126, s[12:13]
	s_add_i32 s17, s16, 384
	s_min_u32 s17, s17, 0xbff
	s_lshr_b32 s18, s17, 5
	s_add_i32 s18, s18, 32
	s_and_b32 s19, s17, 31
	s_lshl_b32 s19, s19, 21
	s_lshl_b32 s18, s18, 7
	s_add_u32 s18, s18, s19
	s_add_u32 s14, s4, s18
	s_addc_u32 s15, s5, 0
	ds_read_b32 v100, v122
	ds_read_b32 v101, v122 offset:512
	ds_read_b32 v102, v122 offset:1024
	ds_read_b32 v103, v122 offset:1536
	ds_read_b32 v104, v122 offset:2048
	ds_read_b32 v105, v122 offset:2560
	ds_read_b32 v106, v122 offset:3072
	ds_read_b32 v107, v122 offset:3584
	ds_read_b32 v108, v122 offset:4096
	ds_read_b32 v109, v122 offset:4608
	ds_read_b32 v110, v122 offset:5120
	ds_read_b32 v111, v122 offset:5632
	ds_read_b32 v112, v122 offset:6144
	ds_read_b32 v113, v122 offset:6656
	ds_read_b32 v114, v122 offset:7168
	ds_read_b32 v115, v122 offset:7680
	s_waitcnt lgkmcnt(0)
	v_max_f32_e32 v100, v100, v100
	v_max_f32_e32 v101, v101, v101
	v_max_f32_e32 v102, v102, v102
	v_max_f32_e32 v103, v103, v103
	v_max_f32_e32 v104, v104, v104
	v_max_f32_e32 v105, v105, v105
	v_max_f32_e32 v106, v106, v106
	v_max_f32_e32 v107, v107, v107
	v_max_f32_e32 v108, v108, v108
	v_max_f32_e32 v109, v109, v109
	v_max_f32_e32 v110, v110, v110
	v_max_f32_e32 v111, v111, v111
	v_max_f32_e32 v112, v112, v112
	v_max_f32_e32 v113, v113, v113
	v_max_f32_e32 v114, v114, v114
	v_max_f32_e32 v115, v115, v115
	v_med3_f32 v100, v100, s20, v129
	v_med3_f32 v101, v101, s20, v129
	v_med3_f32 v102, v102, s20, v129
	v_med3_f32 v103, v103, s20, v129
	v_med3_f32 v104, v104, s20, v129
	v_med3_f32 v105, v105, s20, v129
	v_med3_f32 v106, v106, s20, v129
	v_med3_f32 v107, v107, s20, v129
	v_med3_f32 v108, v108, s20, v129
	v_med3_f32 v109, v109, s20, v129
	v_med3_f32 v110, v110, s20, v129
	v_med3_f32 v111, v111, s20, v129
	v_med3_f32 v112, v112, s20, v129
	v_med3_f32 v113, v113, s20, v129
	v_med3_f32 v114, v114, s20, v129
	v_med3_f32 v115, v115, s20, v129
	v_mov_b32_e32 v116, 0
	v_mov_b32_e32 v117, 0
	v_mov_b32_e32 v118, 0
	v_mov_b32_e32 v119, 0
	v_cvt_pk_fp8_f32 v116, v100, v101
	v_cvt_pk_fp8_f32 v117, v104, v105
	v_cvt_pk_fp8_f32 v118, v108, v109
	v_cvt_pk_fp8_f32 v119, v112, v113
	v_cvt_pk_fp8_f32 v116, v102, v103 op_sel:[0,0,1]
	v_cvt_pk_fp8_f32 v117, v106, v107 op_sel:[0,0,1]
	v_cvt_pk_fp8_f32 v118, v110, v111 op_sel:[0,0,1]
	v_cvt_pk_fp8_f32 v119, v114, v115 op_sel:[0,0,1]
	s_nop 0
	global_store_dwordx4 v127, v[116:119], s[14:15]
	ds_read_b32 v100, v124
	ds_read_b32 v101, v124 offset:512
	ds_read_b32 v102, v124 offset:1024
	ds_read_b32 v103, v124 offset:1536
	ds_read_b32 v104, v124 offset:2048
	ds_read_b32 v105, v124 offset:2560
	ds_read_b32 v106, v124 offset:3072
	ds_read_b32 v107, v124 offset:3584
	ds_read_b32 v108, v124 offset:4096
	ds_read_b32 v109, v124 offset:4608
	ds_read_b32 v110, v124 offset:5120
	ds_read_b32 v111, v124 offset:5632
	ds_read_b32 v112, v124 offset:6144
	ds_read_b32 v113, v124 offset:6656
	ds_read_b32 v114, v124 offset:7168
	ds_read_b32 v115, v124 offset:7680
	s_waitcnt lgkmcnt(0)
	v_max_f32_e32 v100, v100, v100
	v_max_f32_e32 v101, v101, v101
	v_max_f32_e32 v102, v102, v102
	v_max_f32_e32 v103, v103, v103
	v_max_f32_e32 v104, v104, v104
	v_max_f32_e32 v105, v105, v105
	v_max_f32_e32 v106, v106, v106
	v_max_f32_e32 v107, v107, v107
	v_max_f32_e32 v108, v108, v108
	v_max_f32_e32 v109, v109, v109
	v_max_f32_e32 v110, v110, v110
	v_max_f32_e32 v111, v111, v111
	v_max_f32_e32 v112, v112, v112
	v_max_f32_e32 v113, v113, v113
	v_max_f32_e32 v114, v114, v114
	v_max_f32_e32 v115, v115, v115
	v_med3_f32 v100, v100, s20, v129
	v_med3_f32 v101, v101, s20, v129
	v_med3_f32 v102, v102, s20, v129
	v_med3_f32 v103, v103, s20, v129
	v_med3_f32 v104, v104, s20, v129
	v_med3_f32 v105, v105, s20, v129
	v_med3_f32 v106, v106, s20, v129
	v_med3_f32 v107, v107, s20, v129
	v_med3_f32 v108, v108, s20, v129
	v_med3_f32 v109, v109, s20, v129
	v_med3_f32 v110, v110, s20, v129
	v_med3_f32 v111, v111, s20, v129
	v_med3_f32 v112, v112, s20, v129
	v_med3_f32 v113, v113, s20, v129
	v_med3_f32 v114, v114, s20, v129
	v_med3_f32 v115, v115, s20, v129
	v_mov_b32_e32 v116, 0
	v_mov_b32_e32 v117, 0
	v_mov_b32_e32 v118, 0
	v_mov_b32_e32 v119, 0
	v_cvt_pk_fp8_f32 v116, v100, v101
	v_cvt_pk_fp8_f32 v117, v104, v105
	v_cvt_pk_fp8_f32 v118, v108, v109
	v_cvt_pk_fp8_f32 v119, v112, v113
	v_cvt_pk_fp8_f32 v116, v102, v103 op_sel:[0,0,1]
	v_cvt_pk_fp8_f32 v117, v106, v107 op_sel:[0,0,1]
	v_cvt_pk_fp8_f32 v118, v110, v111 op_sel:[0,0,1]
	v_cvt_pk_fp8_f32 v119, v114, v115 op_sel:[0,0,1]
	s_nop 0
	global_store_dwordx4 v128, v[116:119], s[14:15]
	s_waitcnt vmcnt(12)
	v_mul_f32_e32 v68, 0x43000000, v68
	v_mul_f32_e32 v69, 0x43000000, v69
	v_mul_f32_e32 v70, 0x43000000, v70
	v_mul_f32_e32 v71, 0x43000000, v71
	ds_write_b128 v121, v[68:71]
	v_mul_f32_e32 v72, 0x43000000, v72
	v_mul_f32_e32 v73, 0x43000000, v73
	v_mul_f32_e32 v74, 0x43000000, v74
	v_mul_f32_e32 v75, 0x43000000, v75
	ds_write_b128 v121, v[72:75] offset:1024
	v_mul_f32_e32 v76, 0x43000000, v76
	v_mul_f32_e32 v77, 0x43000000, v77
	v_mul_f32_e32 v78, 0x43000000, v78
	v_mul_f32_e32 v79, 0x43000000, v79
	ds_write_b128 v121, v[76:79] offset:2048
	v_mul_f32_e32 v80, 0x43000000, v80
	v_mul_f32_e32 v81, 0x43000000, v81
	v_mul_f32_e32 v82, 0x43000000, v82
	v_mul_f32_e32 v83, 0x43000000, v83
	ds_write_b128 v121, v[80:83] offset:3072
	v_mul_f32_e32 v84, 0x43000000, v84
	v_mul_f32_e32 v85, 0x43000000, v85
	v_mul_f32_e32 v86, 0x43000000, v86
	v_mul_f32_e32 v87, 0x43000000, v87
	ds_write_b128 v121, v[84:87] offset:4096
	v_mul_f32_e32 v88, 0x43000000, v88
	v_mul_f32_e32 v89, 0x43000000, v89
	v_mul_f32_e32 v90, 0x43000000, v90
	v_mul_f32_e32 v91, 0x43000000, v91
	ds_write_b128 v121, v[88:91] offset:5120
	v_mul_f32_e32 v92, 0x43000000, v92
	v_mul_f32_e32 v93, 0x43000000, v93
	v_mul_f32_e32 v94, 0x43000000, v94
	v_mul_f32_e32 v95, 0x43000000, v95
	ds_write_b128 v121, v[92:95] offset:6144
	v_mul_f32_e32 v96, 0x43000000, v96
	v_mul_f32_e32 v97, 0x43000000, v97
	v_mul_f32_e32 v98, 0x43000000, v98
	v_mul_f32_e32 v99, 0x43000000, v99
	ds_write_b128 v121, v[96:99] offset:7168
	s_waitcnt lgkmcnt(0)
	s_barrier
; #define GAS __attribute__((address_space(1)))
; #define LAS __attribute__((address_space(3)))
; #define LDS_WAIT() asm volatile("s_waitcnt lgkmcnt(0)" ::: "memory")
;     const int pr = item >> 1, kb = 2 * (pr / nblk) + (item & 1), nb = pr % nblk, k0 = 64 * kb, n0 = 32 * nb;
;     const int nr = n0 + (lane & 31); const int sc = MAP == 1 ? src_col_in(nr) : nr;
;     float v[32];
; #pragma unroll
;     for (int i = 0; i < 32; ++i) v[i] = sc >= 0 ? W[(size_t)(k0 + 2 * i + (lane >> 5)) * Nsrc + sc] : 0.f;
; #pragma unroll
;     for (int i = 0; i < 32; ++i) { const int k = k0 + 2 * i + (lane >> 5); float x = v[i] * wscale; if (KS) x *= (k < ksplit ? ksA[k] : ksB[k - ksplit]); scr[(2 * i + (lane >> 5)) * 33 + (lane & 31)] = x; }
;     LDS_WAIT(); asm volatile("" ::: "memory");
;     const int c = lane & 7;
; #pragma unroll
;     for (int j = 0; j < 4; ++j) { const int n = (lane >> 3) + 8 * j; const LAS float* s = scr + (8 * c) * 33 + n;
;         const unsigned long long o = (unsigned long long)pg8::pk4_fp8(s[0 * 33], s[1 * 33], s[2 * 33], s[3 * 33]) | ((unsigned long long)pg8::pk4_fp8(s[4 * 33], s[5 * 33], s[6 * 33], s[7 * 33]) << 32);
;         *(GAS unsigned long long*)(WT + (size_t)(n0 + n) * K + k0 + 8 * c) = o; }
;     LDS_WAIT(); asm volatile("" ::: "memory");
; }
; __global__ void __launch_bounds__(NWAVES * 64, 2) hybrid_fwd(Args args) {
;     ...
;             p0_transpose_item_f8<false>(args.in[16] + (size_t)l * FF * DM, FF, DM, DM / 32, (unsigned char*)(ws + WS_WDN + l * SZ_WDN), 128.f, args.in[16], args.in[16], 0, scr, r, lane);
	s_add_i32 s17, s16, 672
	s_min_u32 s17, s17, 0xbff
	s_lshr_b32 s18, s17, 5
	s_add_i32 s18, s18, 32
	s_and_b32 s19, s17, 31
	s_lshl_b32 s18, s18, 21
	s_lshl_b32 s19, s19, 9
	s_add_u32 s18, s18, s19
	s_add_u32 s12, s2, s18
	s_addc_u32 s13, s3, 0
	global_load_dwordx4 v[68:71], v126, s[12:13]
	s_add_u32 s12, s12, 0x8000
	s_addc_u32 s13, s13, 0
	global_load_dwordx4 v[72:75], v126, s[12:13]
	s_add_u32 s12, s12, 0x8000
	s_addc_u32 s13, s13, 0
	global_load_dwordx4 v[76:79], v126, s[12:13]
	s_add_u32 s12, s12, 0x8000
	s_addc_u32 s13, s13, 0
	global_load_dwordx4 v[80:83], v126, s[12:13]
	s_add_u32 s12, s12, 0x8000
	s_addc_u32 s13, s13, 0
	global_load_dwordx4 v[84:87], v126, s[12:13]
	s_add_u32 s12, s12, 0x8000
	s_addc_u32 s13, s13, 0
	global_load_dwordx4 v[88:91], v126, s[12:13]
	s_add_u32 s12, s12, 0x8000
	s_addc_u32 s13, s13, 0
	global_load_dwordx4 v[92:95], v126, s[12:13]
	s_add_u32 s12, s12, 0x8000
	s_addc_u32 s13, s13, 0
	global_load_dwordx4 v[96:99], v126, s[12:13]
	s_add_i32 s17, s16, 480
	s_min_u32 s17, s17, 0xbff
	s_lshr_b32 s18, s17, 5
	s_add_i32 s18, s18, 32
	s_and_b32 s19, s17, 31
	s_lshl_b32 s19, s19, 21
	s_lshl_b32 s18, s18, 7
	s_add_u32 s18, s18, s19
	s_add_u32 s14, s4, s18
	s_addc_u32 s15, s5, 0
	ds_read_b32 v100, v123
	ds_read_b32 v101, v123 offset:512
	ds_read_b32 v102, v123 offset:1024
	ds_read_b32 v103, v123 offset:1536
	ds_read_b32 v104, v123 offset:2048
	ds_read_b32 v105, v123 offset:2560
	ds_read_b32 v106, v123 offset:3072
	ds_read_b32 v107, v123 offset:3584
	ds_read_b32 v108, v123 offset:4096
	ds_read_b32 v109, v123 offset:4608
	ds_read_b32 v110, v123 offset:5120
	ds_read_b32 v111, v123 offset:5632
	ds_read_b32 v112, v123 offset:6144
	ds_read_b32 v113, v123 offset:6656
	ds_read_b32 v114, v123 offset:7168
	ds_read_b32 v115, v123 offset:7680
	s_waitcnt lgkmcnt(0)
	v_max_f32_e32 v100, v100, v100
	v_max_f32_e32 v101, v101, v101
	v_max_f32_e32 v102, v102, v102
	v_max_f32_e32 v103, v103, v103
	v_max_f32_e32 v104, v104, v104
	v_max_f32_e32 v105, v105, v105
	v_max_f32_e32 v106, v106, v106
	v_max_f32_e32 v107, v107, v107
	v_max_f32_e32 v108, v108, v108
	v_max_f32_e32 v109, v109, v109
	v_max_f32_e32 v110, v110, v110
	v_max_f32_e32 v111, v111, v111
	v_max_f32_e32 v112, v112, v112
	v_max_f32_e32 v113, v113, v113
	v_max_f32_e32 v114, v114, v114
	v_max_f32_e32 v115, v115, v115
	v_med3_f32 v100, v100, s20, v129
	v_med3_f32 v101, v101, s20, v129
	v_med3_f32 v102, v102, s20, v129
	v_med3_f32 v103, v103, s20, v129
	v_med3_f32 v104, v104, s20, v129
	v_med3_f32 v105, v105, s20, v129
	v_med3_f32 v106, v106, s20, v129
	v_med3_f32 v107, v107, s20, v129
	v_med3_f32 v108, v108, s20, v129
	v_med3_f32 v109, v109, s20, v129
	v_med3_f32 v110, v110, s20, v129
	v_med3_f32 v111, v111, s20, v129
	v_med3_f32 v112, v112, s20, v129
	v_med3_f32 v113, v113, s20, v129
	v_med3_f32 v114, v114, s20, v129
	v_med3_f32 v115, v115, s20, v129
	v_mov_b32_e32 v116, 0
	v_mov_b32_e32 v117, 0
	v_mov_b32_e32 v118, 0
	v_mov_b32_e32 v119, 0
	v_cvt_pk_fp8_f32 v116, v100, v101
	v_cvt_pk_fp8_f32 v117, v104, v105
	v_cvt_pk_fp8_f32 v118, v108, v109
	v_cvt_pk_fp8_f32 v119, v112, v113
	v_cvt_pk_fp8_f32 v116, v102, v103 op_sel:[0,0,1]
	v_cvt_pk_fp8_f32 v117, v106, v107 op_sel:[0,0,1]
	v_cvt_pk_fp8_f32 v118, v110, v111 op_sel:[0,0,1]
	v_cvt_pk_fp8_f32 v119, v114, v115 op_sel:[0,0,1]
	s_nop 0
	global_store_dwordx4 v127, v[116:119], s[14:15]
	ds_read_b32 v100, v125
	ds_read_b32 v101, v125 offset:512
	ds_read_b32 v102, v125 offset:1024
	ds_read_b32 v103, v125 offset:1536
	ds_read_b32 v104, v125 offset:2048
	ds_read_b32 v105, v125 offset:2560
	ds_read_b32 v106, v125 offset:3072
	ds_read_b32 v107, v125 offset:3584
	ds_read_b32 v108, v125 offset:4096
	ds_read_b32 v109, v125 offset:4608
	ds_read_b32 v110, v125 offset:5120
	ds_read_b32 v111, v125 offset:5632
	ds_read_b32 v112, v125 offset:6144
	ds_read_b32 v113, v125 offset:6656
	ds_read_b32 v114, v125 offset:7168
	ds_read_b32 v115, v125 offset:7680
	s_waitcnt lgkmcnt(0)
	v_max_f32_e32 v100, v100, v100
	v_max_f32_e32 v101, v101, v101
	v_max_f32_e32 v102, v102, v102
	v_max_f32_e32 v103, v103, v103
	v_max_f32_e32 v104, v104, v104
	v_max_f32_e32 v105, v105, v105
	v_max_f32_e32 v106, v106, v106
	v_max_f32_e32 v107, v107, v107
	v_max_f32_e32 v108, v108, v108
	v_max_f32_e32 v109, v109, v109
	v_max_f32_e32 v110, v110, v110
	v_max_f32_e32 v111, v111, v111
	v_max_f32_e32 v112, v112, v112
	v_max_f32_e32 v113, v113, v113
	v_max_f32_e32 v114, v114, v114
	v_max_f32_e32 v115, v115, v115
	v_med3_f32 v100, v100, s20, v129
	v_med3_f32 v101, v101, s20, v129
	v_med3_f32 v102, v102, s20, v129
	v_med3_f32 v103, v103, s20, v129
	v_med3_f32 v104, v104, s20, v129
	v_med3_f32 v105, v105, s20, v129
	v_med3_f32 v106, v106, s20, v129
	v_med3_f32 v107, v107, s20, v129
	v_med3_f32 v108, v108, s20, v129
	v_med3_f32 v109, v109, s20, v129
	v_med3_f32 v110, v110, s20, v129
	v_med3_f32 v111, v111, s20, v129
	v_med3_f32 v112, v112, s20, v129
	v_med3_f32 v113, v113, s20, v129
	v_med3_f32 v114, v114, s20, v129
	v_med3_f32 v115, v115, s20, v129
	v_mov_b32_e32 v116, 0
	v_mov_b32_e32 v117, 0
	v_mov_b32_e32 v118, 0
	v_mov_b32_e32 v119, 0
	v_cvt_pk_fp8_f32 v116, v100, v101
	v_cvt_pk_fp8_f32 v117, v104, v105
	v_cvt_pk_fp8_f32 v118, v108, v109
	v_cvt_pk_fp8_f32 v119, v112, v113
	v_cvt_pk_fp8_f32 v116, v102, v103 op_sel:[0,0,1]
	v_cvt_pk_fp8_f32 v117, v106, v107 op_sel:[0,0,1]
	v_cvt_pk_fp8_f32 v118, v110, v111 op_sel:[0,0,1]
	v_cvt_pk_fp8_f32 v119, v114, v115 op_sel:[0,0,1]
	s_nop 0
	global_store_dwordx4 v128, v[116:119], s[14:15]
	s_waitcnt vmcnt(12)
	v_mul_f32_e32 v36, 0x43000000, v36
	v_mul_f32_e32 v37, 0x43000000, v37
	v_mul_f32_e32 v38, 0x43000000, v38
	v_mul_f32_e32 v39, 0x43000000, v39
	ds_write_b128 v120, v[36:39]
	v_mul_f32_e32 v40, 0x43000000, v40
	v_mul_f32_e32 v41, 0x43000000, v41
	v_mul_f32_e32 v42, 0x43000000, v42
	v_mul_f32_e32 v43, 0x43000000, v43
	ds_write_b128 v120, v[40:43] offset:1024
	v_mul_f32_e32 v44, 0x43000000, v44
	v_mul_f32_e32 v45, 0x43000000, v45
	v_mul_f32_e32 v46, 0x43000000, v46
	v_mul_f32_e32 v47, 0x43000000, v47
	ds_write_b128 v120, v[44:47] offset:2048
	v_mul_f32_e32 v48, 0x43000000, v48
	v_mul_f32_e32 v49, 0x43000000, v49
	v_mul_f32_e32 v50, 0x43000000, v50
	v_mul_f32_e32 v51, 0x43000000, v51
	ds_write_b128 v120, v[48:51] offset:3072
	v_mul_f32_e32 v52, 0x43000000, v52
	v_mul_f32_e32 v53, 0x43000000, v53
	v_mul_f32_e32 v54, 0x43000000, v54
	v_mul_f32_e32 v55, 0x43000000, v55
	ds_write_b128 v120, v[52:55] offset:4096
	v_mul_f32_e32 v56, 0x43000000, v56
	v_mul_f32_e32 v57, 0x43000000, v57
	v_mul_f32_e32 v58, 0x43000000, v58
	v_mul_f32_e32 v59, 0x43000000, v59
	ds_write_b128 v120, v[56:59] offset:5120
	v_mul_f32_e32 v60, 0x43000000, v60
	v_mul_f32_e32 v61, 0x43000000, v61
	v_mul_f32_e32 v62, 0x43000000, v62
	v_mul_f32_e32 v63, 0x43000000, v63
	ds_write_b128 v120, v[60:63] offset:6144
	v_mul_f32_e32 v64, 0x43000000, v64
	v_mul_f32_e32 v65, 0x43000000, v65
	v_mul_f32_e32 v66, 0x43000000, v66
	v_mul_f32_e32 v67, 0x43000000, v67
	ds_write_b128 v120, v[64:67] offset:7168
	s_waitcnt lgkmcnt(0)
	s_barrier
; #define GAS __attribute__((address_space(1)))
; #define LAS __attribute__((address_space(3)))
; #define LDS_WAIT() asm volatile("s_waitcnt lgkmcnt(0)" ::: "memory")
;     const int pr = item >> 1, kb = 2 * (pr / nblk) + (item & 1), nb = pr % nblk, k0 = 64 * kb, n0 = 32 * nb;
;     const int nr = n0 + (lane & 31); const int sc = MAP == 1 ? src_col_in(nr) : nr;
;     float v[32];
; #pragma unroll
;     for (int i = 0; i < 32; ++i) v[i] = sc >= 0 ? W[(size_t)(k0 + 2 * i + (lane >> 5)) * Nsrc + sc] : 0.f;
; #pragma unroll
;     for (int i = 0; i < 32; ++i) { const int k = k0 + 2 * i + (lane >> 5); float x = v[i] * wscale; if (KS) x *= (k < ksplit ? ksA[k] : ksB[k - ksplit]); scr[(2 * i + (lane >> 5)) * 33 + (lane & 31)] = x; }
;     LDS_WAIT(); asm volatile("" ::: "memory");
;     const int c = lane & 7;
; #pragma unroll
;     for (int j = 0; j < 4; ++j) { const int n = (lane >> 3) + 8 * j; const LAS float* s = scr + (8 * c) * 33 + n;
;         const unsigned long long o = (unsigned long long)pg8::pk4_fp8(s[0 * 33], s[1 * 33], s[2 * 33], s[3 * 33]) | ((unsigned long long)pg8::pk4_fp8(s[4 * 33], s[5 * 33], s[6 * 33], s[7 * 33]) << 32);
;         *(GAS unsigned long long*)(WT + (size_t)(n0 + n) * K + k0 + 8 * c) = o; }
;     LDS_WAIT(); asm volatile("" ::: "memory");
; }
; __global__ void __launch_bounds__(NWAVES * 64, 2) hybrid_fwd(Args args) {
;     ...
;             p0_transpose_item_f8<false>(args.in[16] + (size_t)l * FF * DM, FF, DM, DM / 32, (unsigned char*)(ws + WS_WDN + l * SZ_WDN), 128.f, args.in[16], args.in[16], 0, scr, r, lane);
	s_add_i32 s17, s16, 768
	s_min_u32 s17, s17, 0xbff
	s_lshr_b32 s18, s17, 5
	s_add_i32 s18, s18, 32
	s_and_b32 s19, s17, 31
	s_lshl_b32 s18, s18, 21
	s_lshl_b32 s19, s19, 9
	s_add_u32 s18, s18, s19
	s_add_u32 s12, s2, s18
	s_addc_u32 s13, s3, 0
	global_load_dwordx4 v[36:39], v126, s[12:13]
	s_add_u32 s12, s12, 0x8000
	s_addc_u32 s13, s13, 0
	global_load_dwordx4 v[40:43], v126, s[12:13]
	s_add_u32 s12, s12, 0x8000
	s_addc_u32 s13, s13, 0
	global_load_dwordx4 v[44:47], v126, s[12:13]
	s_add_u32 s12, s12, 0x8000
	s_addc_u32 s13, s13, 0
	global_load_dwordx4 v[48:51], v126, s[12:13]
	s_add_u32 s12, s12, 0x8000
	s_addc_u32 s13, s13, 0
	global_load_dwordx4 v[52:55], v126, s[12:13]
	s_add_u32 s12, s12, 0x8000
	s_addc_u32 s13, s13, 0
	global_load_dwordx4 v[56:59], v126, s[12:13]
	s_add_u32 s12, s12, 0x8000
	s_addc_u32 s13, s13, 0
	global_load_dwordx4 v[60:63], v126, s[12:13]
	s_add_u32 s12, s12, 0x8000
	s_addc_u32 s13, s13, 0
	global_load_dwordx4 v[64:67], v126, s[12:13]
	s_add_i32 s17, s16, 576
	s_min_u32 s17, s17, 0xbff
	s_lshr_b32 s18, s17, 5
	s_add_i32 s18, s18, 32
	s_and_b32 s19, s17, 31
	s_lshl_b32 s19, s19, 21
	s_lshl_b32 s18, s18, 7
	s_add_u32 s18, s18, s19
	s_add_u32 s14, s4, s18
	s_addc_u32 s15, s5, 0
	ds_read_b32 v100, v122
	ds_read_b32 v101, v122 offset:512
	ds_read_b32 v102, v122 offset:1024
	ds_read_b32 v103, v122 offset:1536
	ds_read_b32 v104, v122 offset:2048
	ds_read_b32 v105, v122 offset:2560
	ds_read_b32 v106, v122 offset:3072
	ds_read_b32 v107, v122 offset:3584
	ds_read_b32 v108, v122 offset:4096
	ds_read_b32 v109, v122 offset:4608
	ds_read_b32 v110, v122 offset:5120
	ds_read_b32 v111, v122 offset:5632
	ds_read_b32 v112, v122 offset:6144
	ds_read_b32 v113, v122 offset:6656
	ds_read_b32 v114, v122 offset:7168
	ds_read_b32 v115, v122 offset:7680
	s_waitcnt lgkmcnt(0)
	v_max_f32_e32 v100, v100, v100
	v_max_f32_e32 v101, v101, v101
	v_max_f32_e32 v102, v102, v102
	v_max_f32_e32 v103, v103, v103
	v_max_f32_e32 v104, v104, v104
	v_max_f32_e32 v105, v105, v105
	v_max_f32_e32 v106, v106, v106
	v_max_f32_e32 v107, v107, v107
	v_max_f32_e32 v108, v108, v108
	v_max_f32_e32 v109, v109, v109
	v_max_f32_e32 v110, v110, v110
	v_max_f32_e32 v111, v111, v111
	v_max_f32_e32 v112, v112, v112
	v_max_f32_e32 v113, v113, v113
	v_max_f32_e32 v114, v114, v114
	v_max_f32_e32 v115, v115, v115
	v_med3_f32 v100, v100, s20, v129
	v_med3_f32 v101, v101, s20, v129
	v_med3_f32 v102, v102, s20, v129
	v_med3_f32 v103, v103, s20, v129
	v_med3_f32 v104, v104, s20, v129
	v_med3_f32 v105, v105, s20, v129
	v_med3_f32 v106, v106, s20, v129
	v_med3_f32 v107, v107, s20, v129
	v_med3_f32 v108, v108, s20, v129
	v_med3_f32 v109, v109, s20, v129
	v_med3_f32 v110, v110, s20, v129
	v_med3_f32 v111, v111, s20, v129
	v_med3_f32 v112, v112, s20, v129
	v_med3_f32 v113, v113, s20, v129
	v_med3_f32 v114, v114, s20, v129
	v_med3_f32 v115, v115, s20, v129
	v_mov_b32_e32 v116, 0
	v_mov_b32_e32 v117, 0
	v_mov_b32_e32 v118, 0
	v_mov_b32_e32 v119, 0
	v_cvt_pk_fp8_f32 v116, v100, v101
	v_cvt_pk_fp8_f32 v117, v104, v105
	v_cvt_pk_fp8_f32 v118, v108, v109
	v_cvt_pk_fp8_f32 v119, v112, v113
	v_cvt_pk_fp8_f32 v116, v102, v103 op_sel:[0,0,1]
	v_cvt_pk_fp8_f32 v117, v106, v107 op_sel:[0,0,1]
	v_cvt_pk_fp8_f32 v118, v110, v111 op_sel:[0,0,1]
	v_cvt_pk_fp8_f32 v119, v114, v115 op_sel:[0,0,1]
	s_nop 0
	global_store_dwordx4 v127, v[116:119], s[14:15]
	ds_read_b32 v100, v124
	ds_read_b32 v101, v124 offset:512
	ds_read_b32 v102, v124 offset:1024
	ds_read_b32 v103, v124 offset:1536
	ds_read_b32 v104, v124 offset:2048
	ds_read_b32 v105, v124 offset:2560
	ds_read_b32 v106, v124 offset:3072
	ds_read_b32 v107, v124 offset:3584
	ds_read_b32 v108, v124 offset:4096
	ds_read_b32 v109, v124 offset:4608
	ds_read_b32 v110, v124 offset:5120
	ds_read_b32 v111, v124 offset:5632
	ds_read_b32 v112, v124 offset:6144
	ds_read_b32 v113, v124 offset:6656
	ds_read_b32 v114, v124 offset:7168
	ds_read_b32 v115, v124 offset:7680
	s_waitcnt lgkmcnt(0)
	v_max_f32_e32 v100, v100, v100
	v_max_f32_e32 v101, v101, v101
	v_max_f32_e32 v102, v102, v102
	v_max_f32_e32 v103, v103, v103
	v_max_f32_e32 v104, v104, v104
	v_max_f32_e32 v105, v105, v105
	v_max_f32_e32 v106, v106, v106
	v_max_f32_e32 v107, v107, v107
	v_max_f32_e32 v108, v108, v108
	v_max_f32_e32 v109, v109, v109
	v_max_f32_e32 v110, v110, v110
	v_max_f32_e32 v111, v111, v111
	v_max_f32_e32 v112, v112, v112
	v_max_f32_e32 v113, v113, v113
	v_max_f32_e32 v114, v114, v114
	v_max_f32_e32 v115, v115, v115
	v_med3_f32 v100, v100, s20, v129
	v_med3_f32 v101, v101, s20, v129
	v_med3_f32 v102, v102, s20, v129
	v_med3_f32 v103, v103, s20, v129
	v_med3_f32 v104, v104, s20, v129
	v_med3_f32 v105, v105, s20, v129
	v_med3_f32 v106, v106, s20, v129
	v_med3_f32 v107, v107, s20, v129
	v_med3_f32 v108, v108, s20, v129
	v_med3_f32 v109, v109, s20, v129
	v_med3_f32 v110, v110, s20, v129
	v_med3_f32 v111, v111, s20, v129
	v_med3_f32 v112, v112, s20, v129
	v_med3_f32 v113, v113, s20, v129
	v_med3_f32 v114, v114, s20, v129
	v_med3_f32 v115, v115, s20, v129
	v_mov_b32_e32 v116, 0
	v_mov_b32_e32 v117, 0
	v_mov_b32_e32 v118, 0
	v_mov_b32_e32 v119, 0
	v_cvt_pk_fp8_f32 v116, v100, v101
	v_cvt_pk_fp8_f32 v117, v104, v105
	v_cvt_pk_fp8_f32 v118, v108, v109
	v_cvt_pk_fp8_f32 v119, v112, v113
	v_cvt_pk_fp8_f32 v116, v102, v103 op_sel:[0,0,1]
	v_cvt_pk_fp8_f32 v117, v106, v107 op_sel:[0,0,1]
	v_cvt_pk_fp8_f32 v118, v110, v111 op_sel:[0,0,1]
	v_cvt_pk_fp8_f32 v119, v114, v115 op_sel:[0,0,1]
	s_nop 0
	global_store_dwordx4 v128, v[116:119], s[14:15]
	s_waitcnt vmcnt(12)
	v_mul_f32_e32 v68, 0x43000000, v68
	v_mul_f32_e32 v69, 0x43000000, v69
	v_mul_f32_e32 v70, 0x43000000, v70
	v_mul_f32_e32 v71, 0x43000000, v71
	ds_write_b128 v121, v[68:71]
	v_mul_f32_e32 v72, 0x43000000, v72
	v_mul_f32_e32 v73, 0x43000000, v73
	v_mul_f32_e32 v74, 0x43000000, v74
	v_mul_f32_e32 v75, 0x43000000, v75
	ds_write_b128 v121, v[72:75] offset:1024
	v_mul_f32_e32 v76, 0x43000000, v76
	v_mul_f32_e32 v77, 0x43000000, v77
	v_mul_f32_e32 v78, 0x43000000, v78
	v_mul_f32_e32 v79, 0x43000000, v79
	ds_write_b128 v121, v[76:79] offset:2048
	v_mul_f32_e32 v80, 0x43000000, v80
	v_mul_f32_e32 v81, 0x43000000, v81
	v_mul_f32_e32 v82, 0x43000000, v82
	v_mul_f32_e32 v83, 0x43000000, v83
	ds_write_b128 v121, v[80:83] offset:3072
	v_mul_f32_e32 v84, 0x43000000, v84
	v_mul_f32_e32 v85, 0x43000000, v85
	v_mul_f32_e32 v86, 0x43000000, v86
	v_mul_f32_e32 v87, 0x43000000, v87
	ds_write_b128 v121, v[84:87] offset:4096
	v_mul_f32_e32 v88, 0x43000000, v88
	v_mul_f32_e32 v89, 0x43000000, v89
	v_mul_f32_e32 v90, 0x43000000, v90
	v_mul_f32_e32 v91, 0x43000000, v91
	ds_write_b128 v121, v[88:91] offset:5120
	v_mul_f32_e32 v92, 0x43000000, v92
	v_mul_f32_e32 v93, 0x43000000, v93
	v_mul_f32_e32 v94, 0x43000000, v94
	v_mul_f32_e32 v95, 0x43000000, v95
	ds_write_b128 v121, v[92:95] offset:6144
	v_mul_f32_e32 v96, 0x43000000, v96
	v_mul_f32_e32 v97, 0x43000000, v97
	v_mul_f32_e32 v98, 0x43000000, v98
	v_mul_f32_e32 v99, 0x43000000, v99
	ds_write_b128 v121, v[96:99] offset:7168
	s_waitcnt lgkmcnt(0)
	s_barrier
; #define GAS __attribute__((address_space(1)))
; #define LAS __attribute__((address_space(3)))
; #define LDS_WAIT() asm volatile("s_waitcnt lgkmcnt(0)" ::: "memory")
;     const int pr = item >> 1, kb = 2 * (pr / nblk) + (item & 1), nb = pr % nblk, k0 = 64 * kb, n0 = 32 * nb;
;     const int nr = n0 + (lane & 31); const int sc = MAP == 1 ? src_col_in(nr) : nr;
;     float v[32];
; #pragma unroll
;     for (int i = 0; i < 32; ++i) v[i] = sc >= 0 ? W[(size_t)(k0 + 2 * i + (lane >> 5)) * Nsrc + sc] : 0.f;
; #pragma unroll
;     for (int i = 0; i < 32; ++i) { const int k = k0 + 2 * i + (lane >> 5); float x = v[i] * wscale; if (KS) x *= (k < ksplit ? ksA[k] : ksB[k - ksplit]); scr[(2 * i + (lane >> 5)) * 33 + (lane & 31)] = x; }
;     LDS_WAIT(); asm volatile("" ::: "memory");
;     const int c = lane & 7;
; #pragma unroll
;     for (int j = 0; j < 4; ++j) { const int n = (lane >> 3) + 8 * j; const LAS float* s = scr + (8 * c) * 33 + n;
;         const unsigned long long o = (unsigned long long)pg8::pk4_fp8(s[0 * 33], s[1 * 33], s[2 * 33], s[3 * 33]) | ((unsigned long long)pg8::pk4_fp8(s[4 * 33], s[5 * 33], s[6 * 33], s[7 * 33]) << 32);
;         *(GAS unsigned long long*)(WT + (size_t)(n0 + n) * K + k0 + 8 * c) = o; }
;     LDS_WAIT(); asm volatile("" ::: "memory");
; }
; __global__ void __launch_bounds__(NWAVES * 64, 2) hybrid_fwd(Args args) {
;     ...
;             p0_transpose_item_f8<false>(args.in[16] + (size_t)l * FF * DM, FF, DM, DM / 32, (unsigned char*)(ws + WS_WDN + l * SZ_WDN), 128.f, args.in[16], args.in[16], 0, scr, r, lane);
	s_add_i32 s17, s16, 864
	s_min_u32 s17, s17, 0xbff
	s_lshr_b32 s18, s17, 5
	s_add_i32 s18, s18, 32
	s_and_b32 s19, s17, 31
	s_lshl_b32 s18, s18, 21
	s_lshl_b32 s19, s19, 9
	s_add_u32 s18, s18, s19
	s_add_u32 s12, s2, s18
	s_addc_u32 s13, s3, 0
	global_load_dwordx4 v[68:71], v126, s[12:13]
	s_add_u32 s12, s12, 0x8000
	s_addc_u32 s13, s13, 0
	global_load_dwordx4 v[72:75], v126, s[12:13]
	s_add_u32 s12, s12, 0x8000
	s_addc_u32 s13, s13, 0
	global_load_dwordx4 v[76:79], v126, s[12:13]
	s_add_u32 s12, s12, 0x8000
	s_addc_u32 s13, s13, 0
	global_load_dwordx4 v[80:83], v126, s[12:13]
	s_add_u32 s12, s12, 0x8000
	s_addc_u32 s13, s13, 0
	global_load_dwordx4 v[84:87], v126, s[12:13]
	s_add_u32 s12, s12, 0x8000
	s_addc_u32 s13, s13, 0
	global_load_dwordx4 v[88:91], v126, s[12:13]
	s_add_u32 s12, s12, 0x8000
	s_addc_u32 s13, s13, 0
	global_load_dwordx4 v[92:95], v126, s[12:13]
	s_add_u32 s12, s12, 0x8000
	s_addc_u32 s13, s13, 0
	global_load_dwordx4 v[96:99], v126, s[12:13]
	s_add_i32 s17, s16, 672
	s_min_u32 s17, s17, 0xbff
	s_lshr_b32 s18, s17, 5
	s_add_i32 s18, s18, 32
	s_and_b32 s19, s17, 31
	s_lshl_b32 s19, s19, 21
	s_lshl_b32 s18, s18, 7
	s_add_u32 s18, s18, s19
	s_add_u32 s14, s4, s18
	s_addc_u32 s15, s5, 0
	ds_read_b32 v100, v123
	ds_read_b32 v101, v123 offset:512
	ds_read_b32 v102, v123 offset:1024
	ds_read_b32 v103, v123 offset:1536
	ds_read_b32 v104, v123 offset:2048
	ds_read_b32 v105, v123 offset:2560
	ds_read_b32 v106, v123 offset:3072
	ds_read_b32 v107, v123 offset:3584
	ds_read_b32 v108, v123 offset:4096
	ds_read_b32 v109, v123 offset:4608
	ds_read_b32 v110, v123 offset:5120
	ds_read_b32 v111, v123 offset:5632
	ds_read_b32 v112, v123 offset:6144
	ds_read_b32 v113, v123 offset:6656
	ds_read_b32 v114, v123 offset:7168
	ds_read_b32 v115, v123 offset:7680
	s_waitcnt lgkmcnt(0)
	v_max_f32_e32 v100, v100, v100
	v_max_f32_e32 v101, v101, v101
	v_max_f32_e32 v102, v102, v102
	v_max_f32_e32 v103, v103, v103
	v_max_f32_e32 v104, v104, v104
	v_max_f32_e32 v105, v105, v105
	v_max_f32_e32 v106, v106, v106
	v_max_f32_e32 v107, v107, v107
	v_max_f32_e32 v108, v108, v108
	v_max_f32_e32 v109, v109, v109
	v_max_f32_e32 v110, v110, v110
	v_max_f32_e32 v111, v111, v111
	v_max_f32_e32 v112, v112, v112
	v_max_f32_e32 v113, v113, v113
	v_max_f32_e32 v114, v114, v114
	v_max_f32_e32 v115, v115, v115
	v_med3_f32 v100, v100, s20, v129
	v_med3_f32 v101, v101, s20, v129
	v_med3_f32 v102, v102, s20, v129
	v_med3_f32 v103, v103, s20, v129
	v_med3_f32 v104, v104, s20, v129
	v_med3_f32 v105, v105, s20, v129
	v_med3_f32 v106, v106, s20, v129
	v_med3_f32 v107, v107, s20, v129
	v_med3_f32 v108, v108, s20, v129
	v_med3_f32 v109, v109, s20, v129
	v_med3_f32 v110, v110, s20, v129
	v_med3_f32 v111, v111, s20, v129
	v_med3_f32 v112, v112, s20, v129
	v_med3_f32 v113, v113, s20, v129
	v_med3_f32 v114, v114, s20, v129
	v_med3_f32 v115, v115, s20, v129
	v_mov_b32_e32 v116, 0
	v_mov_b32_e32 v117, 0
	v_mov_b32_e32 v118, 0
	v_mov_b32_e32 v119, 0
	v_cvt_pk_fp8_f32 v116, v100, v101
	v_cvt_pk_fp8_f32 v117, v104, v105
	v_cvt_pk_fp8_f32 v118, v108, v109
	v_cvt_pk_fp8_f32 v119, v112, v113
	v_cvt_pk_fp8_f32 v116, v102, v103 op_sel:[0,0,1]
	v_cvt_pk_fp8_f32 v117, v106, v107 op_sel:[0,0,1]
	v_cvt_pk_fp8_f32 v118, v110, v111 op_sel:[0,0,1]
	v_cvt_pk_fp8_f32 v119, v114, v115 op_sel:[0,0,1]
	s_nop 0
	global_store_dwordx4 v127, v[116:119], s[14:15]
	ds_read_b32 v100, v125
	ds_read_b32 v101, v125 offset:512
	ds_read_b32 v102, v125 offset:1024
	ds_read_b32 v103, v125 offset:1536
	ds_read_b32 v104, v125 offset:2048
	ds_read_b32 v105, v125 offset:2560
	ds_read_b32 v106, v125 offset:3072
	ds_read_b32 v107, v125 offset:3584
	ds_read_b32 v108, v125 offset:4096
	ds_read_b32 v109, v125 offset:4608
	ds_read_b32 v110, v125 offset:5120
	ds_read_b32 v111, v125 offset:5632
	ds_read_b32 v112, v125 offset:6144
	ds_read_b32 v113, v125 offset:6656
	ds_read_b32 v114, v125 offset:7168
	ds_read_b32 v115, v125 offset:7680
	s_waitcnt lgkmcnt(0)
	v_max_f32_e32 v100, v100, v100
	v_max_f32_e32 v101, v101, v101
	v_max_f32_e32 v102, v102, v102
	v_max_f32_e32 v103, v103, v103
	v_max_f32_e32 v104, v104, v104
	v_max_f32_e32 v105, v105, v105
	v_max_f32_e32 v106, v106, v106
	v_max_f32_e32 v107, v107, v107
	v_max_f32_e32 v108, v108, v108
	v_max_f32_e32 v109, v109, v109
	v_max_f32_e32 v110, v110, v110
	v_max_f32_e32 v111, v111, v111
	v_max_f32_e32 v112, v112, v112
	v_max_f32_e32 v113, v113, v113
	v_max_f32_e32 v114, v114, v114
	v_max_f32_e32 v115, v115, v115
	v_med3_f32 v100, v100, s20, v129
	v_med3_f32 v101, v101, s20, v129
	v_med3_f32 v102, v102, s20, v129
	v_med3_f32 v103, v103, s20, v129
	v_med3_f32 v104, v104, s20, v129
	v_med3_f32 v105, v105, s20, v129
	v_med3_f32 v106, v106, s20, v129
	v_med3_f32 v107, v107, s20, v129
	v_med3_f32 v108, v108, s20, v129
	v_med3_f32 v109, v109, s20, v129
	v_med3_f32 v110, v110, s20, v129
	v_med3_f32 v111, v111, s20, v129
	v_med3_f32 v112, v112, s20, v129
	v_med3_f32 v113, v113, s20, v129
	v_med3_f32 v114, v114, s20, v129
	v_med3_f32 v115, v115, s20, v129
	v_mov_b32_e32 v116, 0
	v_mov_b32_e32 v117, 0
	v_mov_b32_e32 v118, 0
	v_mov_b32_e32 v119, 0
	v_cvt_pk_fp8_f32 v116, v100, v101
	v_cvt_pk_fp8_f32 v117, v104, v105
	v_cvt_pk_fp8_f32 v118, v108, v109
	v_cvt_pk_fp8_f32 v119, v112, v113
	v_cvt_pk_fp8_f32 v116, v102, v103 op_sel:[0,0,1]
	v_cvt_pk_fp8_f32 v117, v106, v107 op_sel:[0,0,1]
	v_cvt_pk_fp8_f32 v118, v110, v111 op_sel:[0,0,1]
	v_cvt_pk_fp8_f32 v119, v114, v115 op_sel:[0,0,1]
	s_nop 0
	global_store_dwordx4 v128, v[116:119], s[14:15]
	s_waitcnt vmcnt(12)
	v_mul_f32_e32 v36, 0x43000000, v36
	v_mul_f32_e32 v37, 0x43000000, v37
	v_mul_f32_e32 v38, 0x43000000, v38
	v_mul_f32_e32 v39, 0x43000000, v39
	ds_write_b128 v120, v[36:39]
	v_mul_f32_e32 v40, 0x43000000, v40
	v_mul_f32_e32 v41, 0x43000000, v41
	v_mul_f32_e32 v42, 0x43000000, v42
	v_mul_f32_e32 v43, 0x43000000, v43
	ds_write_b128 v120, v[40:43] offset:1024
	v_mul_f32_e32 v44, 0x43000000, v44
	v_mul_f32_e32 v45, 0x43000000, v45
	v_mul_f32_e32 v46, 0x43000000, v46
	v_mul_f32_e32 v47, 0x43000000, v47
	ds_write_b128 v120, v[44:47] offset:2048
	v_mul_f32_e32 v48, 0x43000000, v48
	v_mul_f32_e32 v49, 0x43000000, v49
	v_mul_f32_e32 v50, 0x43000000, v50
	v_mul_f32_e32 v51, 0x43000000, v51
	ds_write_b128 v120, v[48:51] offset:3072
	v_mul_f32_e32 v52, 0x43000000, v52
	v_mul_f32_e32 v53, 0x43000000, v53
	v_mul_f32_e32 v54, 0x43000000, v54
	v_mul_f32_e32 v55, 0x43000000, v55
	ds_write_b128 v120, v[52:55] offset:4096
	v_mul_f32_e32 v56, 0x43000000, v56
	v_mul_f32_e32 v57, 0x43000000, v57
	v_mul_f32_e32 v58, 0x43000000, v58
	v_mul_f32_e32 v59, 0x43000000, v59
	ds_write_b128 v120, v[56:59] offset:5120
	v_mul_f32_e32 v60, 0x43000000, v60
	v_mul_f32_e32 v61, 0x43000000, v61
	v_mul_f32_e32 v62, 0x43000000, v62
	v_mul_f32_e32 v63, 0x43000000, v63
	ds_write_b128 v120, v[60:63] offset:6144
	v_mul_f32_e32 v64, 0x43000000, v64
	v_mul_f32_e32 v65, 0x43000000, v65
	v_mul_f32_e32 v66, 0x43000000, v66
	v_mul_f32_e32 v67, 0x43000000, v67
	ds_write_b128 v120, v[64:67] offset:7168
	s_waitcnt lgkmcnt(0)
	s_barrier
; #define GAS __attribute__((address_space(1)))
; #define LAS __attribute__((address_space(3)))
; #define LDS_WAIT() asm volatile("s_waitcnt lgkmcnt(0)" ::: "memory")
;     const int pr = item >> 1, kb = 2 * (pr / nblk) + (item & 1), nb = pr % nblk, k0 = 64 * kb, n0 = 32 * nb;
;     const int nr = n0 + (lane & 31); const int sc = MAP == 1 ? src_col_in(nr) : nr;
;     float v[32];
; #pragma unroll
;     for (int i = 0; i < 32; ++i) v[i] = sc >= 0 ? W[(size_t)(k0 + 2 * i + (lane >> 5)) * Nsrc + sc] : 0.f;
; #pragma unroll
;     for (int i = 0; i < 32; ++i) { const int k = k0 + 2 * i + (lane >> 5); float x = v[i] * wscale; if (KS) x *= (k < ksplit ? ksA[k] : ksB[k - ksplit]); scr[(2 * i + (lane >> 5)) * 33 + (lane & 31)] = x; }
;     LDS_WAIT(); asm volatile("" ::: "memory");
;     const int c = lane & 7;
; #pragma unroll
;     for (int j = 0; j < 4; ++j) { const int n = (lane >> 3) + 8 * j; const LAS float* s = scr + (8 * c) * 33 + n;
;         const unsigned long long o = (unsigned long long)pg8::pk4_fp8(s[0 * 33], s[1 * 33], s[2 * 33], s[3 * 33]) | ((unsigned long long)pg8::pk4_fp8(s[4 * 33], s[5 * 33], s[6 * 33], s[7 * 33]) << 32);
;         *(GAS unsigned long long*)(WT + (size_t)(n0 + n) * K + k0 + 8 * c) = o; }
;     LDS_WAIT(); asm volatile("" ::: "memory");
; }
; __global__ void __launch_bounds__(NWAVES * 64, 2) hybrid_fwd(Args args) {
;     ...
;             p0_transpose_item_f8<false>(args.in[16] + (size_t)l * FF * DM, FF, DM, DM / 32, (unsigned char*)(ws + WS_WDN + l * SZ_WDN), 128.f, args.in[16], args.in[16], 0, scr, r, lane);
	s_add_i32 s17, s16, 960
	s_min_u32 s17, s17, 0xbff
	s_lshr_b32 s18, s17, 5
	s_add_i32 s18, s18, 32
	s_and_b32 s19, s17, 31
	s_lshl_b32 s18, s18, 21
	s_lshl_b32 s19, s19, 9
	s_add_u32 s18, s18, s19
	s_add_u32 s12, s2, s18
	s_addc_u32 s13, s3, 0
	global_load_dwordx4 v[36:39], v126, s[12:13]
	s_add_u32 s12, s12, 0x8000
	s_addc_u32 s13, s13, 0
	global_load_dwordx4 v[40:43], v126, s[12:13]
	s_add_u32 s12, s12, 0x8000
	s_addc_u32 s13, s13, 0
	global_load_dwordx4 v[44:47], v126, s[12:13]
	s_add_u32 s12, s12, 0x8000
	s_addc_u32 s13, s13, 0
	global_load_dwordx4 v[48:51], v126, s[12:13]
	s_add_u32 s12, s12, 0x8000
	s_addc_u32 s13, s13, 0
	global_load_dwordx4 v[52:55], v126, s[12:13]
	s_add_u32 s12, s12, 0x8000
	s_addc_u32 s13, s13, 0
	global_load_dwordx4 v[56:59], v126, s[12:13]
	s_add_u32 s12, s12, 0x8000
	s_addc_u32 s13, s13, 0
	global_load_dwordx4 v[60:63], v126, s[12:13]
	s_add_u32 s12, s12, 0x8000
	s_addc_u32 s13, s13, 0
	global_load_dwordx4 v[64:67], v126, s[12:13]
	s_add_i32 s17, s16, 768
	s_min_u32 s17, s17, 0xbff
	s_lshr_b32 s18, s17, 5
	s_add_i32 s18, s18, 32
	s_and_b32 s19, s17, 31
	s_lshl_b32 s19, s19, 21
	s_lshl_b32 s18, s18, 7
	s_add_u32 s18, s18, s19
	s_add_u32 s14, s4, s18
	s_addc_u32 s15, s5, 0
	ds_read_b32 v100, v122
	ds_read_b32 v101, v122 offset:512
	ds_read_b32 v102, v122 offset:1024
	ds_read_b32 v103, v122 offset:1536
	ds_read_b32 v104, v122 offset:2048
	ds_read_b32 v105, v122 offset:2560
	ds_read_b32 v106, v122 offset:3072
	ds_read_b32 v107, v122 offset:3584
	ds_read_b32 v108, v122 offset:4096
	ds_read_b32 v109, v122 offset:4608
	ds_read_b32 v110, v122 offset:5120
	ds_read_b32 v111, v122 offset:5632
	ds_read_b32 v112, v122 offset:6144
	ds_read_b32 v113, v122 offset:6656
	ds_read_b32 v114, v122 offset:7168
	ds_read_b32 v115, v122 offset:7680
	s_waitcnt lgkmcnt(0)
	v_max_f32_e32 v100, v100, v100
	v_max_f32_e32 v101, v101, v101
	v_max_f32_e32 v102, v102, v102
	v_max_f32_e32 v103, v103, v103
	v_max_f32_e32 v104, v104, v104
	v_max_f32_e32 v105, v105, v105
	v_max_f32_e32 v106, v106, v106
	v_max_f32_e32 v107, v107, v107
	v_max_f32_e32 v108, v108, v108
	v_max_f32_e32 v109, v109, v109
	v_max_f32_e32 v110, v110, v110
	v_max_f32_e32 v111, v111, v111
	v_max_f32_e32 v112, v112, v112
	v_max_f32_e32 v113, v113, v113
	v_max_f32_e32 v114, v114, v114
	v_max_f32_e32 v115, v115, v115
	v_med3_f32 v100, v100, s20, v129
	v_med3_f32 v101, v101, s20, v129
	v_med3_f32 v102, v102, s20, v129
	v_med3_f32 v103, v103, s20, v129
	v_med3_f32 v104, v104, s20, v129
	v_med3_f32 v105, v105, s20, v129
	v_med3_f32 v106, v106, s20, v129
	v_med3_f32 v107, v107, s20, v129
	v_med3_f32 v108, v108, s20, v129
	v_med3_f32 v109, v109, s20, v129
	v_med3_f32 v110, v110, s20, v129
	v_med3_f32 v111, v111, s20, v129
	v_med3_f32 v112, v112, s20, v129
	v_med3_f32 v113, v113, s20, v129
	v_med3_f32 v114, v114, s20, v129
	v_med3_f32 v115, v115, s20, v129
	v_mov_b32_e32 v116, 0
	v_mov_b32_e32 v117, 0
	v_mov_b32_e32 v118, 0
	v_mov_b32_e32 v119, 0
	v_cvt_pk_fp8_f32 v116, v100, v101
	v_cvt_pk_fp8_f32 v117, v104, v105
	v_cvt_pk_fp8_f32 v118, v108, v109
	v_cvt_pk_fp8_f32 v119, v112, v113
	v_cvt_pk_fp8_f32 v116, v102, v103 op_sel:[0,0,1]
	v_cvt_pk_fp8_f32 v117, v106, v107 op_sel:[0,0,1]
	v_cvt_pk_fp8_f32 v118, v110, v111 op_sel:[0,0,1]
	v_cvt_pk_fp8_f32 v119, v114, v115 op_sel:[0,0,1]
	s_nop 0
	global_store_dwordx4 v127, v[116:119], s[14:15]
	ds_read_b32 v100, v124
	ds_read_b32 v101, v124 offset:512
	ds_read_b32 v102, v124 offset:1024
	ds_read_b32 v103, v124 offset:1536
	ds_read_b32 v104, v124 offset:2048
	ds_read_b32 v105, v124 offset:2560
	ds_read_b32 v106, v124 offset:3072
	ds_read_b32 v107, v124 offset:3584
	ds_read_b32 v108, v124 offset:4096
	ds_read_b32 v109, v124 offset:4608
	ds_read_b32 v110, v124 offset:5120
	ds_read_b32 v111, v124 offset:5632
	ds_read_b32 v112, v124 offset:6144
	ds_read_b32 v113, v124 offset:6656
	ds_read_b32 v114, v124 offset:7168
	ds_read_b32 v115, v124 offset:7680
	s_waitcnt lgkmcnt(0)
	v_max_f32_e32 v100, v100, v100
	v_max_f32_e32 v101, v101, v101
	v_max_f32_e32 v102, v102, v102
	v_max_f32_e32 v103, v103, v103
	v_max_f32_e32 v104, v104, v104
	v_max_f32_e32 v105, v105, v105
	v_max_f32_e32 v106, v106, v106
	v_max_f32_e32 v107, v107, v107
	v_max_f32_e32 v108, v108, v108
	v_max_f32_e32 v109, v109, v109
	v_max_f32_e32 v110, v110, v110
	v_max_f32_e32 v111, v111, v111
	v_max_f32_e32 v112, v112, v112
	v_max_f32_e32 v113, v113, v113
	v_max_f32_e32 v114, v114, v114
	v_max_f32_e32 v115, v115, v115
	v_med3_f32 v100, v100, s20, v129
	v_med3_f32 v101, v101, s20, v129
	v_med3_f32 v102, v102, s20, v129
	v_med3_f32 v103, v103, s20, v129
	v_med3_f32 v104, v104, s20, v129
	v_med3_f32 v105, v105, s20, v129
	v_med3_f32 v106, v106, s20, v129
	v_med3_f32 v107, v107, s20, v129
	v_med3_f32 v108, v108, s20, v129
	v_med3_f32 v109, v109, s20, v129
	v_med3_f32 v110, v110, s20, v129
	v_med3_f32 v111, v111, s20, v129
	v_med3_f32 v112, v112, s20, v129
	v_med3_f32 v113, v113, s20, v129
	v_med3_f32 v114, v114, s20, v129
	v_med3_f32 v115, v115, s20, v129
	v_mov_b32_e32 v116, 0
	v_mov_b32_e32 v117, 0
	v_mov_b32_e32 v118, 0
	v_mov_b32_e32 v119, 0
	v_cvt_pk_fp8_f32 v116, v100, v101
	v_cvt_pk_fp8_f32 v117, v104, v105
	v_cvt_pk_fp8_f32 v118, v108, v109
	v_cvt_pk_fp8_f32 v119, v112, v113
	v_cvt_pk_fp8_f32 v116, v102, v103 op_sel:[0,0,1]
	v_cvt_pk_fp8_f32 v117, v106, v107 op_sel:[0,0,1]
	v_cvt_pk_fp8_f32 v118, v110, v111 op_sel:[0,0,1]
	v_cvt_pk_fp8_f32 v119, v114, v115 op_sel:[0,0,1]
	s_nop 0
	global_store_dwordx4 v128, v[116:119], s[14:15]
	s_waitcnt vmcnt(12)
	v_mul_f32_e32 v68, 0x43000000, v68
	v_mul_f32_e32 v69, 0x43000000, v69
	v_mul_f32_e32 v70, 0x43000000, v70
	v_mul_f32_e32 v71, 0x43000000, v71
	ds_write_b128 v121, v[68:71]
	v_mul_f32_e32 v72, 0x43000000, v72
	v_mul_f32_e32 v73, 0x43000000, v73
	v_mul_f32_e32 v74, 0x43000000, v74
	v_mul_f32_e32 v75, 0x43000000, v75
	ds_write_b128 v121, v[72:75] offset:1024
	v_mul_f32_e32 v76, 0x43000000, v76
	v_mul_f32_e32 v77, 0x43000000, v77
	v_mul_f32_e32 v78, 0x43000000, v78
	v_mul_f32_e32 v79, 0x43000000, v79
	ds_write_b128 v121, v[76:79] offset:2048
	v_mul_f32_e32 v80, 0x43000000, v80
	v_mul_f32_e32 v81, 0x43000000, v81
	v_mul_f32_e32 v82, 0x43000000, v82
	v_mul_f32_e32 v83, 0x43000000, v83
	ds_write_b128 v121, v[80:83] offset:3072
	v_mul_f32_e32 v84, 0x43000000, v84
	v_mul_f32_e32 v85, 0x43000000, v85
	v_mul_f32_e32 v86, 0x43000000, v86
	v_mul_f32_e32 v87, 0x43000000, v87
	ds_write_b128 v121, v[84:87] offset:4096
	v_mul_f32_e32 v88, 0x43000000, v88
	v_mul_f32_e32 v89, 0x43000000, v89
	v_mul_f32_e32 v90, 0x43000000, v90
	v_mul_f32_e32 v91, 0x43000000, v91
	ds_write_b128 v121, v[88:91] offset:5120
	v_mul_f32_e32 v92, 0x43000000, v92
	v_mul_f32_e32 v93, 0x43000000, v93
	v_mul_f32_e32 v94, 0x43000000, v94
	v_mul_f32_e32 v95, 0x43000000, v95
	ds_write_b128 v121, v[92:95] offset:6144
	v_mul_f32_e32 v96, 0x43000000, v96
	v_mul_f32_e32 v97, 0x43000000, v97
	v_mul_f32_e32 v98, 0x43000000, v98
	v_mul_f32_e32 v99, 0x43000000, v99
	ds_write_b128 v121, v[96:99] offset:7168
	s_waitcnt lgkmcnt(0)
	s_barrier
; #define GAS __attribute__((address_space(1)))
; #define LAS __attribute__((address_space(3)))
; #define LDS_WAIT() asm volatile("s_waitcnt lgkmcnt(0)" ::: "memory")
;     const int pr = item >> 1, kb = 2 * (pr / nblk) + (item & 1), nb = pr % nblk, k0 = 64 * kb, n0 = 32 * nb;
;     const int nr = n0 + (lane & 31); const int sc = MAP == 1 ? src_col_in(nr) : nr;
;     float v[32];
; #pragma unroll
;     for (int i = 0; i < 32; ++i) v[i] = sc >= 0 ? W[(size_t)(k0 + 2 * i + (lane >> 5)) * Nsrc + sc] : 0.f;
; #pragma unroll
;     for (int i = 0; i < 32; ++i) { const int k = k0 + 2 * i + (lane >> 5); float x = v[i] * wscale; if (KS) x *= (k < ksplit ? ksA[k] : ksB[k - ksplit]); scr[(2 * i + (lane >> 5)) * 33 + (lane & 31)] = x; }
;     LDS_WAIT(); asm volatile("" ::: "memory");
;     const int c = lane & 7;
; #pragma unroll
;     for (int j = 0; j < 4; ++j) { const int n = (lane >> 3) + 8 * j; const LAS float* s = scr + (8 * c) * 33 + n;
;         const unsigned long long o = (unsigned long long)pg8::pk4_fp8(s[0 * 33], s[1 * 33], s[2 * 33], s[3 * 33]) | ((unsigned long long)pg8::pk4_fp8(s[4 * 33], s[5 * 33], s[6 * 33], s[7 * 33]) << 32);
;         *(GAS unsigned long long*)(WT + (size_t)(n0 + n) * K + k0 + 8 * c) = o; }
;     LDS_WAIT(); asm volatile("" ::: "memory");
; }
; __global__ void __launch_bounds__(NWAVES * 64, 2) hybrid_fwd(Args args) {
;     ...
;             p0_transpose_item_f8<false>(args.in[16] + (size_t)l * FF * DM, FF, DM, DM / 32, (unsigned char*)(ws + WS_WDN + l * SZ_WDN), 128.f, args.in[16], args.in[16], 0, scr, r, lane);
	s_add_i32 s17, s16, 1056
	s_min_u32 s17, s17, 0xbff
	s_lshr_b32 s18, s17, 5
	s_add_i32 s18, s18, 32
	s_and_b32 s19, s17, 31
	s_lshl_b32 s18, s18, 21
	s_lshl_b32 s19, s19, 9
	s_add_u32 s18, s18, s19
	s_add_u32 s12, s2, s18
	s_addc_u32 s13, s3, 0
	global_load_dwordx4 v[68:71], v126, s[12:13]
	s_add_u32 s12, s12, 0x8000
	s_addc_u32 s13, s13, 0
	global_load_dwordx4 v[72:75], v126, s[12:13]
	s_add_u32 s12, s12, 0x8000
	s_addc_u32 s13, s13, 0
	global_load_dwordx4 v[76:79], v126, s[12:13]
	s_add_u32 s12, s12, 0x8000
	s_addc_u32 s13, s13, 0
	global_load_dwordx4 v[80:83], v126, s[12:13]
	s_add_u32 s12, s12, 0x8000
	s_addc_u32 s13, s13, 0
	global_load_dwordx4 v[84:87], v126, s[12:13]
	s_add_u32 s12, s12, 0x8000
	s_addc_u32 s13, s13, 0
	global_load_dwordx4 v[88:91], v126, s[12:13]
	s_add_u32 s12, s12, 0x8000
	s_addc_u32 s13, s13, 0
	global_load_dwordx4 v[92:95], v126, s[12:13]
	s_add_u32 s12, s12, 0x8000
	s_addc_u32 s13, s13, 0
	global_load_dwordx4 v[96:99], v126, s[12:13]
	s_add_i32 s17, s16, 864
	s_min_u32 s17, s17, 0xbff
	s_lshr_b32 s18, s17, 5
	s_add_i32 s18, s18, 32
	s_and_b32 s19, s17, 31
	s_lshl_b32 s19, s19, 21
	s_lshl_b32 s18, s18, 7
	s_add_u32 s18, s18, s19
	s_add_u32 s14, s4, s18
	s_addc_u32 s15, s5, 0
	ds_read_b32 v100, v123
	ds_read_b32 v101, v123 offset:512
	ds_read_b32 v102, v123 offset:1024
	ds_read_b32 v103, v123 offset:1536
	ds_read_b32 v104, v123 offset:2048
	ds_read_b32 v105, v123 offset:2560
	ds_read_b32 v106, v123 offset:3072
	ds_read_b32 v107, v123 offset:3584
	ds_read_b32 v108, v123 offset:4096
	ds_read_b32 v109, v123 offset:4608
	ds_read_b32 v110, v123 offset:5120
	ds_read_b32 v111, v123 offset:5632
	ds_read_b32 v112, v123 offset:6144
	ds_read_b32 v113, v123 offset:6656
	ds_read_b32 v114, v123 offset:7168
	ds_read_b32 v115, v123 offset:7680
	s_waitcnt lgkmcnt(0)
	v_max_f32_e32 v100, v100, v100
	v_max_f32_e32 v101, v101, v101
	v_max_f32_e32 v102, v102, v102
	v_max_f32_e32 v103, v103, v103
	v_max_f32_e32 v104, v104, v104
	v_max_f32_e32 v105, v105, v105
	v_max_f32_e32 v106, v106, v106
	v_max_f32_e32 v107, v107, v107
	v_max_f32_e32 v108, v108, v108
	v_max_f32_e32 v109, v109, v109
	v_max_f32_e32 v110, v110, v110
	v_max_f32_e32 v111, v111, v111
	v_max_f32_e32 v112, v112, v112
	v_max_f32_e32 v113, v113, v113
	v_max_f32_e32 v114, v114, v114
	v_max_f32_e32 v115, v115, v115
	v_med3_f32 v100, v100, s20, v129
	v_med3_f32 v101, v101, s20, v129
	v_med3_f32 v102, v102, s20, v129
	v_med3_f32 v103, v103, s20, v129
	v_med3_f32 v104, v104, s20, v129
	v_med3_f32 v105, v105, s20, v129
	v_med3_f32 v106, v106, s20, v129
	v_med3_f32 v107, v107, s20, v129
	v_med3_f32 v108, v108, s20, v129
	v_med3_f32 v109, v109, s20, v129
	v_med3_f32 v110, v110, s20, v129
	v_med3_f32 v111, v111, s20, v129
	v_med3_f32 v112, v112, s20, v129
	v_med3_f32 v113, v113, s20, v129
	v_med3_f32 v114, v114, s20, v129
	v_med3_f32 v115, v115, s20, v129
	v_mov_b32_e32 v116, 0
	v_mov_b32_e32 v117, 0
	v_mov_b32_e32 v118, 0
	v_mov_b32_e32 v119, 0
	v_cvt_pk_fp8_f32 v116, v100, v101
	v_cvt_pk_fp8_f32 v117, v104, v105
	v_cvt_pk_fp8_f32 v118, v108, v109
	v_cvt_pk_fp8_f32 v119, v112, v113
	v_cvt_pk_fp8_f32 v116, v102, v103 op_sel:[0,0,1]
	v_cvt_pk_fp8_f32 v117, v106, v107 op_sel:[0,0,1]
	v_cvt_pk_fp8_f32 v118, v110, v111 op_sel:[0,0,1]
	v_cvt_pk_fp8_f32 v119, v114, v115 op_sel:[0,0,1]
	s_nop 0
	global_store_dwordx4 v127, v[116:119], s[14:15]
	ds_read_b32 v100, v125
	ds_read_b32 v101, v125 offset:512
	ds_read_b32 v102, v125 offset:1024
	ds_read_b32 v103, v125 offset:1536
	ds_read_b32 v104, v125 offset:2048
	ds_read_b32 v105, v125 offset:2560
	ds_read_b32 v106, v125 offset:3072
	ds_read_b32 v107, v125 offset:3584
	ds_read_b32 v108, v125 offset:4096
	ds_read_b32 v109, v125 offset:4608
	ds_read_b32 v110, v125 offset:5120
	ds_read_b32 v111, v125 offset:5632
	ds_read_b32 v112, v125 offset:6144
	ds_read_b32 v113, v125 offset:6656
	ds_read_b32 v114, v125 offset:7168
	ds_read_b32 v115, v125 offset:7680
	s_waitcnt lgkmcnt(0)
	v_max_f32_e32 v100, v100, v100
	v_max_f32_e32 v101, v101, v101
	v_max_f32_e32 v102, v102, v102
	v_max_f32_e32 v103, v103, v103
	v_max_f32_e32 v104, v104, v104
	v_max_f32_e32 v105, v105, v105
	v_max_f32_e32 v106, v106, v106
	v_max_f32_e32 v107, v107, v107
	v_max_f32_e32 v108, v108, v108
	v_max_f32_e32 v109, v109, v109
	v_max_f32_e32 v110, v110, v110
	v_max_f32_e32 v111, v111, v111
	v_max_f32_e32 v112, v112, v112
	v_max_f32_e32 v113, v113, v113
	v_max_f32_e32 v114, v114, v114
	v_max_f32_e32 v115, v115, v115
	v_med3_f32 v100, v100, s20, v129
	v_med3_f32 v101, v101, s20, v129
	v_med3_f32 v102, v102, s20, v129
	v_med3_f32 v103, v103, s20, v129
	v_med3_f32 v104, v104, s20, v129
	v_med3_f32 v105, v105, s20, v129
	v_med3_f32 v106, v106, s20, v129
	v_med3_f32 v107, v107, s20, v129
	v_med3_f32 v108, v108, s20, v129
	v_med3_f32 v109, v109, s20, v129
	v_med3_f32 v110, v110, s20, v129
	v_med3_f32 v111, v111, s20, v129
	v_med3_f32 v112, v112, s20, v129
	v_med3_f32 v113, v113, s20, v129
	v_med3_f32 v114, v114, s20, v129
	v_med3_f32 v115, v115, s20, v129
	v_mov_b32_e32 v116, 0
	v_mov_b32_e32 v117, 0
	v_mov_b32_e32 v118, 0
	v_mov_b32_e32 v119, 0
	v_cvt_pk_fp8_f32 v116, v100, v101
	v_cvt_pk_fp8_f32 v117, v104, v105
	v_cvt_pk_fp8_f32 v118, v108, v109
	v_cvt_pk_fp8_f32 v119, v112, v113
	v_cvt_pk_fp8_f32 v116, v102, v103 op_sel:[0,0,1]
	v_cvt_pk_fp8_f32 v117, v106, v107 op_sel:[0,0,1]
	v_cvt_pk_fp8_f32 v118, v110, v111 op_sel:[0,0,1]
	v_cvt_pk_fp8_f32 v119, v114, v115 op_sel:[0,0,1]
	s_nop 0
	global_store_dwordx4 v128, v[116:119], s[14:15]
	s_waitcnt vmcnt(12)
	v_mul_f32_e32 v36, 0x43000000, v36
	v_mul_f32_e32 v37, 0x43000000, v37
	v_mul_f32_e32 v38, 0x43000000, v38
	v_mul_f32_e32 v39, 0x43000000, v39
	ds_write_b128 v120, v[36:39]
	v_mul_f32_e32 v40, 0x43000000, v40
	v_mul_f32_e32 v41, 0x43000000, v41
	v_mul_f32_e32 v42, 0x43000000, v42
	v_mul_f32_e32 v43, 0x43000000, v43
	ds_write_b128 v120, v[40:43] offset:1024
	v_mul_f32_e32 v44, 0x43000000, v44
	v_mul_f32_e32 v45, 0x43000000, v45
	v_mul_f32_e32 v46, 0x43000000, v46
	v_mul_f32_e32 v47, 0x43000000, v47
	ds_write_b128 v120, v[44:47] offset:2048
	v_mul_f32_e32 v48, 0x43000000, v48
	v_mul_f32_e32 v49, 0x43000000, v49
	v_mul_f32_e32 v50, 0x43000000, v50
	v_mul_f32_e32 v51, 0x43000000, v51
	ds_write_b128 v120, v[48:51] offset:3072
	v_mul_f32_e32 v52, 0x43000000, v52
	v_mul_f32_e32 v53, 0x43000000, v53
	v_mul_f32_e32 v54, 0x43000000, v54
	v_mul_f32_e32 v55, 0x43000000, v55
	ds_write_b128 v120, v[52:55] offset:4096
	v_mul_f32_e32 v56, 0x43000000, v56
	v_mul_f32_e32 v57, 0x43000000, v57
	v_mul_f32_e32 v58, 0x43000000, v58
	v_mul_f32_e32 v59, 0x43000000, v59
	ds_write_b128 v120, v[56:59] offset:5120
	v_mul_f32_e32 v60, 0x43000000, v60
	v_mul_f32_e32 v61, 0x43000000, v61
	v_mul_f32_e32 v62, 0x43000000, v62
	v_mul_f32_e32 v63, 0x43000000, v63
	ds_write_b128 v120, v[60:63] offset:6144
	v_mul_f32_e32 v64, 0x43000000, v64
	v_mul_f32_e32 v65, 0x43000000, v65
	v_mul_f32_e32 v66, 0x43000000, v66
	v_mul_f32_e32 v67, 0x43000000, v67
	ds_write_b128 v120, v[64:67] offset:7168
	s_waitcnt lgkmcnt(0)
	s_barrier
; #define GAS __attribute__((address_space(1)))
; #define LAS __attribute__((address_space(3)))
; #define LDS_WAIT() asm volatile("s_waitcnt lgkmcnt(0)" ::: "memory")
;     const int pr = item >> 1, kb = 2 * (pr / nblk) + (item & 1), nb = pr % nblk, k0 = 64 * kb, n0 = 32 * nb;
;     const int nr = n0 + (lane & 31); const int sc = MAP == 1 ? src_col_in(nr) : nr;
;     float v[32];
; #pragma unroll
;     for (int i = 0; i < 32; ++i) v[i] = sc >= 0 ? W[(size_t)(k0 + 2 * i + (lane >> 5)) * Nsrc + sc] : 0.f;
; #pragma unroll
;     for (int i = 0; i < 32; ++i) { const int k = k0 + 2 * i + (lane >> 5); float x = v[i] * wscale; if (KS) x *= (k < ksplit ? ksA[k] : ksB[k - ksplit]); scr[(2 * i + (lane >> 5)) * 33 + (lane & 31)] = x; }
;     LDS_WAIT(); asm volatile("" ::: "memory");
;     const int c = lane & 7;
; #pragma unroll
;     for (int j = 0; j < 4; ++j) { const int n = (lane >> 3) + 8 * j; const LAS float* s = scr + (8 * c) * 33 + n;
;         const unsigned long long o = (unsigned long long)pg8::pk4_fp8(s[0 * 33], s[1 * 33], s[2 * 33], s[3 * 33]) | ((unsigned long long)pg8::pk4_fp8(s[4 * 33], s[5 * 33], s[6 * 33], s[7 * 33]) << 32);
;         *(GAS unsigned long long*)(WT + (size_t)(n0 + n) * K + k0 + 8 * c) = o; }
;     LDS_WAIT(); asm volatile("" ::: "memory");
; }
; __global__ void __launch_bounds__(NWAVES * 64, 2) hybrid_fwd(Args args) {
;     ...
;             p0_transpose_item_f8<false>(args.in[16] + (size_t)l * FF * DM, FF, DM, DM / 32, (unsigned char*)(ws + WS_WDN + l * SZ_WDN), 128.f, args.in[16], args.in[16], 0, scr, r, lane);
	s_add_i32 s17, s16, 1152
	s_min_u32 s17, s17, 0xbff
	s_lshr_b32 s18, s17, 5
	s_add_i32 s18, s18, 32
	s_and_b32 s19, s17, 31
	s_lshl_b32 s18, s18, 21
	s_lshl_b32 s19, s19, 9
	s_add_u32 s18, s18, s19
	s_add_u32 s12, s2, s18
	s_addc_u32 s13, s3, 0
	global_load_dwordx4 v[36:39], v126, s[12:13]
	s_add_u32 s12, s12, 0x8000
	s_addc_u32 s13, s13, 0
	global_load_dwordx4 v[40:43], v126, s[12:13]
	s_add_u32 s12, s12, 0x8000
	s_addc_u32 s13, s13, 0
	global_load_dwordx4 v[44:47], v126, s[12:13]
	s_add_u32 s12, s12, 0x8000
	s_addc_u32 s13, s13, 0
	global_load_dwordx4 v[48:51], v126, s[12:13]
	s_add_u32 s12, s12, 0x8000
	s_addc_u32 s13, s13, 0
	global_load_dwordx4 v[52:55], v126, s[12:13]
	s_add_u32 s12, s12, 0x8000
	s_addc_u32 s13, s13, 0
	global_load_dwordx4 v[56:59], v126, s[12:13]
	s_add_u32 s12, s12, 0x8000
	s_addc_u32 s13, s13, 0
	global_load_dwordx4 v[60:63], v126, s[12:13]
	s_add_u32 s12, s12, 0x8000
	s_addc_u32 s13, s13, 0
	global_load_dwordx4 v[64:67], v126, s[12:13]
	s_add_i32 s17, s16, 960
	s_min_u32 s17, s17, 0xbff
	s_lshr_b32 s18, s17, 5
	s_add_i32 s18, s18, 32
	s_and_b32 s19, s17, 31
	s_lshl_b32 s19, s19, 21
	s_lshl_b32 s18, s18, 7
	s_add_u32 s18, s18, s19
	s_add_u32 s14, s4, s18
	s_addc_u32 s15, s5, 0
	ds_read_b32 v100, v122
	ds_read_b32 v101, v122 offset:512
	ds_read_b32 v102, v122 offset:1024
	ds_read_b32 v103, v122 offset:1536
	ds_read_b32 v104, v122 offset:2048
	ds_read_b32 v105, v122 offset:2560
	ds_read_b32 v106, v122 offset:3072
	ds_read_b32 v107, v122 offset:3584
	ds_read_b32 v108, v122 offset:4096
	ds_read_b32 v109, v122 offset:4608
	ds_read_b32 v110, v122 offset:5120
	ds_read_b32 v111, v122 offset:5632
	ds_read_b32 v112, v122 offset:6144
	ds_read_b32 v113, v122 offset:6656
	ds_read_b32 v114, v122 offset:7168
	ds_read_b32 v115, v122 offset:7680
	s_waitcnt lgkmcnt(0)
	v_max_f32_e32 v100, v100, v100
	v_max_f32_e32 v101, v101, v101
	v_max_f32_e32 v102, v102, v102
	v_max_f32_e32 v103, v103, v103
	v_max_f32_e32 v104, v104, v104
	v_max_f32_e32 v105, v105, v105
	v_max_f32_e32 v106, v106, v106
	v_max_f32_e32 v107, v107, v107
	v_max_f32_e32 v108, v108, v108
	v_max_f32_e32 v109, v109, v109
	v_max_f32_e32 v110, v110, v110
	v_max_f32_e32 v111, v111, v111
	v_max_f32_e32 v112, v112, v112
	v_max_f32_e32 v113, v113, v113
	v_max_f32_e32 v114, v114, v114
	v_max_f32_e32 v115, v115, v115
	v_med3_f32 v100, v100, s20, v129
	v_med3_f32 v101, v101, s20, v129
	v_med3_f32 v102, v102, s20, v129
	v_med3_f32 v103, v103, s20, v129
	v_med3_f32 v104, v104, s20, v129
	v_med3_f32 v105, v105, s20, v129
	v_med3_f32 v106, v106, s20, v129
	v_med3_f32 v107, v107, s20, v129
	v_med3_f32 v108, v108, s20, v129
	v_med3_f32 v109, v109, s20, v129
	v_med3_f32 v110, v110, s20, v129
	v_med3_f32 v111, v111, s20, v129
	v_med3_f32 v112, v112, s20, v129
	v_med3_f32 v113, v113, s20, v129
	v_med3_f32 v114, v114, s20, v129
	v_med3_f32 v115, v115, s20, v129
	v_mov_b32_e32 v116, 0
	v_mov_b32_e32 v117, 0
	v_mov_b32_e32 v118, 0
	v_mov_b32_e32 v119, 0
	v_cvt_pk_fp8_f32 v116, v100, v101
	v_cvt_pk_fp8_f32 v117, v104, v105
	v_cvt_pk_fp8_f32 v118, v108, v109
	v_cvt_pk_fp8_f32 v119, v112, v113
	v_cvt_pk_fp8_f32 v116, v102, v103 op_sel:[0,0,1]
	v_cvt_pk_fp8_f32 v117, v106, v107 op_sel:[0,0,1]
	v_cvt_pk_fp8_f32 v118, v110, v111 op_sel:[0,0,1]
	v_cvt_pk_fp8_f32 v119, v114, v115 op_sel:[0,0,1]
	s_nop 0
	global_store_dwordx4 v127, v[116:119], s[14:15]
	ds_read_b32 v100, v124
	ds_read_b32 v101, v124 offset:512
	ds_read_b32 v102, v124 offset:1024
	ds_read_b32 v103, v124 offset:1536
	ds_read_b32 v104, v124 offset:2048
	ds_read_b32 v105, v124 offset:2560
	ds_read_b32 v106, v124 offset:3072
	ds_read_b32 v107, v124 offset:3584
	ds_read_b32 v108, v124 offset:4096
	ds_read_b32 v109, v124 offset:4608
	ds_read_b32 v110, v124 offset:5120
	ds_read_b32 v111, v124 offset:5632
	ds_read_b32 v112, v124 offset:6144
	ds_read_b32 v113, v124 offset:6656
	ds_read_b32 v114, v124 offset:7168
	ds_read_b32 v115, v124 offset:7680
	s_waitcnt lgkmcnt(0)
	v_max_f32_e32 v100, v100, v100
	v_max_f32_e32 v101, v101, v101
	v_max_f32_e32 v102, v102, v102
	v_max_f32_e32 v103, v103, v103
	v_max_f32_e32 v104, v104, v104
	v_max_f32_e32 v105, v105, v105
	v_max_f32_e32 v106, v106, v106
	v_max_f32_e32 v107, v107, v107
	v_max_f32_e32 v108, v108, v108
	v_max_f32_e32 v109, v109, v109
	v_max_f32_e32 v110, v110, v110
	v_max_f32_e32 v111, v111, v111
	v_max_f32_e32 v112, v112, v112
	v_max_f32_e32 v113, v113, v113
	v_max_f32_e32 v114, v114, v114
	v_max_f32_e32 v115, v115, v115
	v_med3_f32 v100, v100, s20, v129
	v_med3_f32 v101, v101, s20, v129
	v_med3_f32 v102, v102, s20, v129
	v_med3_f32 v103, v103, s20, v129
	v_med3_f32 v104, v104, s20, v129
	v_med3_f32 v105, v105, s20, v129
	v_med3_f32 v106, v106, s20, v129
	v_med3_f32 v107, v107, s20, v129
	v_med3_f32 v108, v108, s20, v129
	v_med3_f32 v109, v109, s20, v129
	v_med3_f32 v110, v110, s20, v129
	v_med3_f32 v111, v111, s20, v129
	v_med3_f32 v112, v112, s20, v129
	v_med3_f32 v113, v113, s20, v129
	v_med3_f32 v114, v114, s20, v129
	v_med3_f32 v115, v115, s20, v129
	v_mov_b32_e32 v116, 0
	v_mov_b32_e32 v117, 0
	v_mov_b32_e32 v118, 0
	v_mov_b32_e32 v119, 0
	v_cvt_pk_fp8_f32 v116, v100, v101
	v_cvt_pk_fp8_f32 v117, v104, v105
	v_cvt_pk_fp8_f32 v118, v108, v109
	v_cvt_pk_fp8_f32 v119, v112, v113
	v_cvt_pk_fp8_f32 v116, v102, v103 op_sel:[0,0,1]
	v_cvt_pk_fp8_f32 v117, v106, v107 op_sel:[0,0,1]
	v_cvt_pk_fp8_f32 v118, v110, v111 op_sel:[0,0,1]
	v_cvt_pk_fp8_f32 v119, v114, v115 op_sel:[0,0,1]
	s_nop 0
	global_store_dwordx4 v128, v[116:119], s[14:15]
	s_waitcnt vmcnt(12)
	v_mul_f32_e32 v68, 0x43000000, v68
	v_mul_f32_e32 v69, 0x43000000, v69
	v_mul_f32_e32 v70, 0x43000000, v70
	v_mul_f32_e32 v71, 0x43000000, v71
	ds_write_b128 v121, v[68:71]
	v_mul_f32_e32 v72, 0x43000000, v72
	v_mul_f32_e32 v73, 0x43000000, v73
	v_mul_f32_e32 v74, 0x43000000, v74
	v_mul_f32_e32 v75, 0x43000000, v75
	ds_write_b128 v121, v[72:75] offset:1024
	v_mul_f32_e32 v76, 0x43000000, v76
	v_mul_f32_e32 v77, 0x43000000, v77
	v_mul_f32_e32 v78, 0x43000000, v78
	v_mul_f32_e32 v79, 0x43000000, v79
	ds_write_b128 v121, v[76:79] offset:2048
	v_mul_f32_e32 v80, 0x43000000, v80
	v_mul_f32_e32 v81, 0x43000000, v81
	v_mul_f32_e32 v82, 0x43000000, v82
	v_mul_f32_e32 v83, 0x43000000, v83
	ds_write_b128 v121, v[80:83] offset:3072
	v_mul_f32_e32 v84, 0x43000000, v84
	v_mul_f32_e32 v85, 0x43000000, v85
	v_mul_f32_e32 v86, 0x43000000, v86
	v_mul_f32_e32 v87, 0x43000000, v87
	ds_write_b128 v121, v[84:87] offset:4096
	v_mul_f32_e32 v88, 0x43000000, v88
	v_mul_f32_e32 v89, 0x43000000, v89
	v_mul_f32_e32 v90, 0x43000000, v90
	v_mul_f32_e32 v91, 0x43000000, v91
	ds_write_b128 v121, v[88:91] offset:5120
	v_mul_f32_e32 v92, 0x43000000, v92
	v_mul_f32_e32 v93, 0x43000000, v93
	v_mul_f32_e32 v94, 0x43000000, v94
	v_mul_f32_e32 v95, 0x43000000, v95
	ds_write_b128 v121, v[92:95] offset:6144
	v_mul_f32_e32 v96, 0x43000000, v96
	v_mul_f32_e32 v97, 0x43000000, v97
	v_mul_f32_e32 v98, 0x43000000, v98
	v_mul_f32_e32 v99, 0x43000000, v99
	ds_write_b128 v121, v[96:99] offset:7168
	s_waitcnt lgkmcnt(0)
	s_barrier
; #define GAS __attribute__((address_space(1)))
; #define LAS __attribute__((address_space(3)))
; #define LDS_WAIT() asm volatile("s_waitcnt lgkmcnt(0)" ::: "memory")
;     const int pr = item >> 1, kb = 2 * (pr / nblk) + (item & 1), nb = pr % nblk, k0 = 64 * kb, n0 = 32 * nb;
;     const int nr = n0 + (lane & 31); const int sc = MAP == 1 ? src_col_in(nr) : nr;
;     float v[32];
; #pragma unroll
;     for (int i = 0; i < 32; ++i) v[i] = sc >= 0 ? W[(size_t)(k0 + 2 * i + (lane >> 5)) * Nsrc + sc] : 0.f;
; #pragma unroll
;     for (int i = 0; i < 32; ++i) { const int k = k0 + 2 * i + (lane >> 5); float x = v[i] * wscale; if (KS) x *= (k < ksplit ? ksA[k] : ksB[k - ksplit]); scr[(2 * i + (lane >> 5)) * 33 + (lane & 31)] = x; }
;     LDS_WAIT(); asm volatile("" ::: "memory");
;     const int c = lane & 7;
; #pragma unroll
;     for (int j = 0; j < 4; ++j) { const int n = (lane >> 3) + 8 * j; const LAS float* s = scr + (8 * c) * 33 + n;
;         const unsigned long long o = (unsigned long long)pg8::pk4_fp8(s[0 * 33], s[1 * 33], s[2 * 33], s[3 * 33]) | ((unsigned long long)pg8::pk4_fp8(s[4 * 33], s[5 * 33], s[6 * 33], s[7 * 33]) << 32);
;         *(GAS unsigned long long*)(WT + (size_t)(n0 + n) * K + k0 + 8 * c) = o; }
;     LDS_WAIT(); asm volatile("" ::: "memory");
; }
; __global__ void __launch_bounds__(NWAVES * 64, 2) hybrid_fwd(Args args) {
;     ...
;             p0_transpose_item_f8<false>(args.in[16] + (size_t)l * FF * DM, FF, DM, DM / 32, (unsigned char*)(ws + WS_WDN + l * SZ_WDN), 128.f, args.in[16], args.in[16], 0, scr, r, lane);
	s_add_i32 s17, s16, 1248
	s_min_u32 s17, s17, 0xbff
	s_lshr_b32 s18, s17, 5
	s_add_i32 s18, s18, 32
	s_and_b32 s19, s17, 31
	s_lshl_b32 s18, s18, 21
	s_lshl_b32 s19, s19, 9
	s_add_u32 s18, s18, s19
	s_add_u32 s12, s2, s18
	s_addc_u32 s13, s3, 0
	global_load_dwordx4 v[68:71], v126, s[12:13]
	s_add_u32 s12, s12, 0x8000
	s_addc_u32 s13, s13, 0
	global_load_dwordx4 v[72:75], v126, s[12:13]
	s_add_u32 s12, s12, 0x8000
	s_addc_u32 s13, s13, 0
	global_load_dwordx4 v[76:79], v126, s[12:13]
	s_add_u32 s12, s12, 0x8000
	s_addc_u32 s13, s13, 0
	global_load_dwordx4 v[80:83], v126, s[12:13]
	s_add_u32 s12, s12, 0x8000
	s_addc_u32 s13, s13, 0
	global_load_dwordx4 v[84:87], v126, s[12:13]
	s_add_u32 s12, s12, 0x8000
	s_addc_u32 s13, s13, 0
	global_load_dwordx4 v[88:91], v126, s[12:13]
	s_add_u32 s12, s12, 0x8000
	s_addc_u32 s13, s13, 0
	global_load_dwordx4 v[92:95], v126, s[12:13]
	s_add_u32 s12, s12, 0x8000
	s_addc_u32 s13, s13, 0
	global_load_dwordx4 v[96:99], v126, s[12:13]
	s_add_i32 s17, s16, 1056
	s_min_u32 s17, s17, 0xbff
	s_lshr_b32 s18, s17, 5
	s_add_i32 s18, s18, 32
	s_and_b32 s19, s17, 31
	s_lshl_b32 s19, s19, 21
	s_lshl_b32 s18, s18, 7
	s_add_u32 s18, s18, s19
	s_add_u32 s14, s4, s18
	s_addc_u32 s15, s5, 0
	ds_read_b32 v100, v123
	ds_read_b32 v101, v123 offset:512
	ds_read_b32 v102, v123 offset:1024
	ds_read_b32 v103, v123 offset:1536
	ds_read_b32 v104, v123 offset:2048
	ds_read_b32 v105, v123 offset:2560
	ds_read_b32 v106, v123 offset:3072
	ds_read_b32 v107, v123 offset:3584
	ds_read_b32 v108, v123 offset:4096
	ds_read_b32 v109, v123 offset:4608
	ds_read_b32 v110, v123 offset:5120
	ds_read_b32 v111, v123 offset:5632
	ds_read_b32 v112, v123 offset:6144
	ds_read_b32 v113, v123 offset:6656
	ds_read_b32 v114, v123 offset:7168
	ds_read_b32 v115, v123 offset:7680
	s_waitcnt lgkmcnt(0)
	v_max_f32_e32 v100, v100, v100
	v_max_f32_e32 v101, v101, v101
	v_max_f32_e32 v102, v102, v102
	v_max_f32_e32 v103, v103, v103
	v_max_f32_e32 v104, v104, v104
	v_max_f32_e32 v105, v105, v105
	v_max_f32_e32 v106, v106, v106
	v_max_f32_e32 v107, v107, v107
	v_max_f32_e32 v108, v108, v108
	v_max_f32_e32 v109, v109, v109
	v_max_f32_e32 v110, v110, v110
	v_max_f32_e32 v111, v111, v111
	v_max_f32_e32 v112, v112, v112
	v_max_f32_e32 v113, v113, v113
	v_max_f32_e32 v114, v114, v114
	v_max_f32_e32 v115, v115, v115
	v_med3_f32 v100, v100, s20, v129
	v_med3_f32 v101, v101, s20, v129
	v_med3_f32 v102, v102, s20, v129
	v_med3_f32 v103, v103, s20, v129
	v_med3_f32 v104, v104, s20, v129
	v_med3_f32 v105, v105, s20, v129
	v_med3_f32 v106, v106, s20, v129
	v_med3_f32 v107, v107, s20, v129
	v_med3_f32 v108, v108, s20, v129
	v_med3_f32 v109, v109, s20, v129
	v_med3_f32 v110, v110, s20, v129
	v_med3_f32 v111, v111, s20, v129
	v_med3_f32 v112, v112, s20, v129
	v_med3_f32 v113, v113, s20, v129
	v_med3_f32 v114, v114, s20, v129
	v_med3_f32 v115, v115, s20, v129
	v_mov_b32_e32 v116, 0
	v_mov_b32_e32 v117, 0
	v_mov_b32_e32 v118, 0
	v_mov_b32_e32 v119, 0
	v_cvt_pk_fp8_f32 v116, v100, v101
	v_cvt_pk_fp8_f32 v117, v104, v105
	v_cvt_pk_fp8_f32 v118, v108, v109
	v_cvt_pk_fp8_f32 v119, v112, v113
	v_cvt_pk_fp8_f32 v116, v102, v103 op_sel:[0,0,1]
	v_cvt_pk_fp8_f32 v117, v106, v107 op_sel:[0,0,1]
	v_cvt_pk_fp8_f32 v118, v110, v111 op_sel:[0,0,1]
	v_cvt_pk_fp8_f32 v119, v114, v115 op_sel:[0,0,1]
	s_nop 0
	global_store_dwordx4 v127, v[116:119], s[14:15]
	ds_read_b32 v100, v125
	ds_read_b32 v101, v125 offset:512
	ds_read_b32 v102, v125 offset:1024
	ds_read_b32 v103, v125 offset:1536
	ds_read_b32 v104, v125 offset:2048
	ds_read_b32 v105, v125 offset:2560
	ds_read_b32 v106, v125 offset:3072
	ds_read_b32 v107, v125 offset:3584
	ds_read_b32 v108, v125 offset:4096
	ds_read_b32 v109, v125 offset:4608
	ds_read_b32 v110, v125 offset:5120
	ds_read_b32 v111, v125 offset:5632
	ds_read_b32 v112, v125 offset:6144
	ds_read_b32 v113, v125 offset:6656
	ds_read_b32 v114, v125 offset:7168
	ds_read_b32 v115, v125 offset:7680
	s_waitcnt lgkmcnt(0)
	v_max_f32_e32 v100, v100, v100
	v_max_f32_e32 v101, v101, v101
	v_max_f32_e32 v102, v102, v102
	v_max_f32_e32 v103, v103, v103
	v_max_f32_e32 v104, v104, v104
	v_max_f32_e32 v105, v105, v105
	v_max_f32_e32 v106, v106, v106
	v_max_f32_e32 v107, v107, v107
	v_max_f32_e32 v108, v108, v108
	v_max_f32_e32 v109, v109, v109
	v_max_f32_e32 v110, v110, v110
	v_max_f32_e32 v111, v111, v111
	v_max_f32_e32 v112, v112, v112
	v_max_f32_e32 v113, v113, v113
	v_max_f32_e32 v114, v114, v114
	v_max_f32_e32 v115, v115, v115
	v_med3_f32 v100, v100, s20, v129
	v_med3_f32 v101, v101, s20, v129
	v_med3_f32 v102, v102, s20, v129
	v_med3_f32 v103, v103, s20, v129
	v_med3_f32 v104, v104, s20, v129
	v_med3_f32 v105, v105, s20, v129
	v_med3_f32 v106, v106, s20, v129
	v_med3_f32 v107, v107, s20, v129
	v_med3_f32 v108, v108, s20, v129
	v_med3_f32 v109, v109, s20, v129
	v_med3_f32 v110, v110, s20, v129
	v_med3_f32 v111, v111, s20, v129
	v_med3_f32 v112, v112, s20, v129
	v_med3_f32 v113, v113, s20, v129
	v_med3_f32 v114, v114, s20, v129
	v_med3_f32 v115, v115, s20, v129
	v_mov_b32_e32 v116, 0
	v_mov_b32_e32 v117, 0
	v_mov_b32_e32 v118, 0
	v_mov_b32_e32 v119, 0
	v_cvt_pk_fp8_f32 v116, v100, v101
	v_cvt_pk_fp8_f32 v117, v104, v105
	v_cvt_pk_fp8_f32 v118, v108, v109
	v_cvt_pk_fp8_f32 v119, v112, v113
	v_cvt_pk_fp8_f32 v116, v102, v103 op_sel:[0,0,1]
	v_cvt_pk_fp8_f32 v117, v106, v107 op_sel:[0,0,1]
	v_cvt_pk_fp8_f32 v118, v110, v111 op_sel:[0,0,1]
	v_cvt_pk_fp8_f32 v119, v114, v115 op_sel:[0,0,1]
	s_nop 0
	global_store_dwordx4 v128, v[116:119], s[14:15]
	s_waitcnt vmcnt(12)
	v_mul_f32_e32 v36, 0x43000000, v36
	v_mul_f32_e32 v37, 0x43000000, v37
	v_mul_f32_e32 v38, 0x43000000, v38
	v_mul_f32_e32 v39, 0x43000000, v39
	ds_write_b128 v120, v[36:39]
	v_mul_f32_e32 v40, 0x43000000, v40
	v_mul_f32_e32 v41, 0x43000000, v41
	v_mul_f32_e32 v42, 0x43000000, v42
	v_mul_f32_e32 v43, 0x43000000, v43
	ds_write_b128 v120, v[40:43] offset:1024
	v_mul_f32_e32 v44, 0x43000000, v44
	v_mul_f32_e32 v45, 0x43000000, v45
	v_mul_f32_e32 v46, 0x43000000, v46
	v_mul_f32_e32 v47, 0x43000000, v47
	ds_write_b128 v120, v[44:47] offset:2048
	v_mul_f32_e32 v48, 0x43000000, v48
	v_mul_f32_e32 v49, 0x43000000, v49
	v_mul_f32_e32 v50, 0x43000000, v50
	v_mul_f32_e32 v51, 0x43000000, v51
	ds_write_b128 v120, v[48:51] offset:3072
	v_mul_f32_e32 v52, 0x43000000, v52
	v_mul_f32_e32 v53, 0x43000000, v53
	v_mul_f32_e32 v54, 0x43000000, v54
	v_mul_f32_e32 v55, 0x43000000, v55
	ds_write_b128 v120, v[52:55] offset:4096
	v_mul_f32_e32 v56, 0x43000000, v56
	v_mul_f32_e32 v57, 0x43000000, v57
	v_mul_f32_e32 v58, 0x43000000, v58
	v_mul_f32_e32 v59, 0x43000000, v59
	ds_write_b128 v120, v[56:59] offset:5120
	v_mul_f32_e32 v60, 0x43000000, v60
	v_mul_f32_e32 v61, 0x43000000, v61
	v_mul_f32_e32 v62, 0x43000000, v62
	v_mul_f32_e32 v63, 0x43000000, v63
	ds_write_b128 v120, v[60:63] offset:6144
	v_mul_f32_e32 v64, 0x43000000, v64
	v_mul_f32_e32 v65, 0x43000000, v65
	v_mul_f32_e32 v66, 0x43000000, v66
	v_mul_f32_e32 v67, 0x43000000, v67
	ds_write_b128 v120, v[64:67] offset:7168
	s_waitcnt lgkmcnt(0)
	s_barrier
; #define GAS __attribute__((address_space(1)))
; #define LAS __attribute__((address_space(3)))
; #define LDS_WAIT() asm volatile("s_waitcnt lgkmcnt(0)" ::: "memory")
; __device__ __forceinline__ unsigned pk4_fp8(float a, float b, float c, float d) {
;     a = fminf(fmaxf(a, -448.f), 448.f); b = fminf(fmaxf(b, -448.f), 448.f); c = fminf(fmaxf(c, -448.f), 448.f); d = fminf(fmaxf(d, -448.f), 448.f);
;     int w = __builtin_amdgcn_cvt_pk_fp8_f32(a, b, 0, false); w = __builtin_amdgcn_cvt_pk_fp8_f32(c, d, w, true); return (unsigned)w; }
;     const int pr = item >> 1, kb = 2 * (pr / nblk) + (item & 1), nb = pr % nblk, k0 = 64 * kb, n0 = 32 * nb;
;     const int nr = n0 + (lane & 31); const int sc = MAP == 1 ? src_col_in(nr) : nr;
;     float v[32];
; #pragma unroll
;     for (int i = 0; i < 32; ++i) v[i] = sc >= 0 ? W[(size_t)(k0 + 2 * i + (lane >> 5)) * Nsrc + sc] : 0.f;
; #pragma unroll
;     for (int i = 0; i < 32; ++i) { const int k = k0 + 2 * i + (lane >> 5); float x = v[i] * wscale; if (KS) x *= (k < ksplit ? ksA[k] : ksB[k - ksplit]); scr[(2 * i + (lane >> 5)) * 33 + (lane & 31)] = x; }
;     LDS_WAIT(); asm volatile("" ::: "memory");
;     const int c = lane & 7;
; #pragma unroll
;     for (int j = 0; j < 4; ++j) { const int n = (lane >> 3) + 8 * j; const LAS float* s = scr + (8 * c) * 33 + n;
;         const unsigned long long o = (unsigned long long)pg8::pk4_fp8(s[0 * 33], s[1 * 33], s[2 * 33], s[3 * 33]) | ((unsigned long long)pg8::pk4_fp8(s[4 * 33], s[5 * 33], s[6 * 33], s[7 * 33]) << 32);
;         *(GAS unsigned long long*)(WT + (size_t)(n0 + n) * K + k0 + 8 * c) = o; }
;     LDS_WAIT(); asm volatile("" ::: "memory");
; }
	s_add_i32 s17, s16, 1344
	s_min_u32 s17, s17, 0xbff
	s_lshr_b32 s18, s17, 5
	s_add_i32 s18, s18, 32
	s_and_b32 s19, s17, 31
	s_lshl_b32 s18, s18, 21
	s_lshl_b32 s19, s19, 9
	s_add_u32 s18, s18, s19
	s_add_u32 s12, s2, s18
	s_addc_u32 s13, s3, 0
	global_load_dwordx4 v[36:39], v126, s[12:13]
	s_add_u32 s12, s12, 0x8000
	s_addc_u32 s13, s13, 0
	global_load_dwordx4 v[40:43], v126, s[12:13]
	s_add_u32 s12, s12, 0x8000
	s_addc_u32 s13, s13, 0
	global_load_dwordx4 v[44:47], v126, s[12:13]
	s_add_u32 s12, s12, 0x8000
	s_addc_u32 s13, s13, 0
	global_load_dwordx4 v[48:51], v126, s[12:13]
	s_add_u32 s12, s12, 0x8000
	s_addc_u32 s13, s13, 0
	global_load_dwordx4 v[52:55], v126, s[12:13]
	s_add_u32 s12, s12, 0x8000
	s_addc_u32 s13, s13, 0
	global_load_dwordx4 v[56:59], v126, s[12:13]
	s_add_u32 s12, s12, 0x8000
	s_addc_u32 s13, s13, 0
	global_load_dwordx4 v[60:63], v126, s[12:13]
	s_add_u32 s12, s12, 0x8000
	s_addc_u32 s13, s13, 0
	global_load_dwordx4 v[64:67], v126, s[12:13]
	s_add_i32 s17, s16, 1152
	s_min_u32 s17, s17, 0xbff
	s_lshr_b32 s18, s17, 5
	s_add_i32 s18, s18, 32
	s_and_b32 s19, s17, 31
	s_lshl_b32 s19, s19, 21
	s_lshl_b32 s18, s18, 7
	s_add_u32 s18, s18, s19
	s_add_u32 s14, s4, s18
	s_addc_u32 s15, s5, 0
	ds_read_b32 v100, v122
	ds_read_b32 v101, v122 offset:512
	ds_read_b32 v102, v122 offset:1024
	ds_read_b32 v103, v122 offset:1536
	ds_read_b32 v104, v122 offset:2048
	ds_read_b32 v105, v122 offset:2560
	ds_read_b32 v106, v122 offset:3072
	ds_read_b32 v107, v122 offset:3584
	ds_read_b32 v108, v122 offset:4096
	ds_read_b32 v109, v122 offset:4608
	ds_read_b32 v110, v122 offset:5120
	ds_read_b32 v111, v122 offset:5632
	ds_read_b32 v112, v122 offset:6144
	ds_read_b32 v113, v122 offset:6656
	ds_read_b32 v114, v122 offset:7168
	ds_read_b32 v115, v122 offset:7680
	s_waitcnt lgkmcnt(0)
	v_max_f32_e32 v100, v100, v100
	v_max_f32_e32 v101, v101, v101
	v_max_f32_e32 v102, v102, v102
	v_max_f32_e32 v103, v103, v103
	v_max_f32_e32 v104, v104, v104
	v_max_f32_e32 v105, v105, v105
	v_max_f32_e32 v106, v106, v106
	v_max_f32_e32 v107, v107, v107
	v_max_f32_e32 v108, v108, v108
	v_max_f32_e32 v109, v109, v109
	v_max_f32_e32 v110, v110, v110
	v_max_f32_e32 v111, v111, v111
	v_max_f32_e32 v112, v112, v112
	v_max_f32_e32 v113, v113, v113
	v_max_f32_e32 v114, v114, v114
	v_max_f32_e32 v115, v115, v115
	v_med3_f32 v100, v100, s20, v129
	v_med3_f32 v101, v101, s20, v129
	v_med3_f32 v102, v102, s20, v129
	v_med3_f32 v103, v103, s20, v129
	v_med3_f32 v104, v104, s20, v129
	v_med3_f32 v105, v105, s20, v129
	v_med3_f32 v106, v106, s20, v129
	v_med3_f32 v107, v107, s20, v129
	v_med3_f32 v108, v108, s20, v129
	v_med3_f32 v109, v109, s20, v129
	v_med3_f32 v110, v110, s20, v129
	v_med3_f32 v111, v111, s20, v129
	v_med3_f32 v112, v112, s20, v129
	v_med3_f32 v113, v113, s20, v129
	v_med3_f32 v114, v114, s20, v129
	v_med3_f32 v115, v115, s20, v129
	v_mov_b32_e32 v116, 0
	v_mov_b32_e32 v117, 0
	v_mov_b32_e32 v118, 0
	v_mov_b32_e32 v119, 0
	v_cvt_pk_fp8_f32 v116, v100, v101
	v_cvt_pk_fp8_f32 v117, v104, v105
	v_cvt_pk_fp8_f32 v118, v108, v109
	v_cvt_pk_fp8_f32 v119, v112, v113
	v_cvt_pk_fp8_f32 v116, v102, v103 op_sel:[0,0,1]
	v_cvt_pk_fp8_f32 v117, v106, v107 op_sel:[0,0,1]
	v_cvt_pk_fp8_f32 v118, v110, v111 op_sel:[0,0,1]
	v_cvt_pk_fp8_f32 v119, v114, v115 op_sel:[0,0,1]
	s_nop 0
	global_store_dwordx4 v127, v[116:119], s[14:15]
	ds_read_b32 v100, v124
	ds_read_b32 v101, v124 offset:512
	ds_read_b32 v102, v124 offset:1024
	ds_read_b32 v103, v124 offset:1536
	ds_read_b32 v104, v124 offset:2048
	ds_read_b32 v105, v124 offset:2560
	ds_read_b32 v106, v124 offset:3072
	ds_read_b32 v107, v124 offset:3584
	ds_read_b32 v108, v124 offset:4096
	ds_read_b32 v109, v124 offset:4608
	ds_read_b32 v110, v124 offset:5120
	ds_read_b32 v111, v124 offset:5632
	ds_read_b32 v112, v124 offset:6144
	ds_read_b32 v113, v124 offset:6656
	ds_read_b32 v114, v124 offset:7168
	ds_read_b32 v115, v124 offset:7680
	s_waitcnt lgkmcnt(0)
	v_max_f32_e32 v100, v100, v100
	v_max_f32_e32 v101, v101, v101
	v_max_f32_e32 v102, v102, v102
	v_max_f32_e32 v103, v103, v103
	v_max_f32_e32 v104, v104, v104
	v_max_f32_e32 v105, v105, v105
	v_max_f32_e32 v106, v106, v106
	v_max_f32_e32 v107, v107, v107
	v_max_f32_e32 v108, v108, v108
	v_max_f32_e32 v109, v109, v109
	v_max_f32_e32 v110, v110, v110
	v_max_f32_e32 v111, v111, v111
	v_max_f32_e32 v112, v112, v112
	v_max_f32_e32 v113, v113, v113
	v_max_f32_e32 v114, v114, v114
	v_max_f32_e32 v115, v115, v115
	v_med3_f32 v100, v100, s20, v129
	v_med3_f32 v101, v101, s20, v129
	v_med3_f32 v102, v102, s20, v129
	v_med3_f32 v103, v103, s20, v129
	v_med3_f32 v104, v104, s20, v129
	v_med3_f32 v105, v105, s20, v129
	v_med3_f32 v106, v106, s20, v129
	v_med3_f32 v107, v107, s20, v129
	v_med3_f32 v108, v108, s20, v129
	v_med3_f32 v109, v109, s20, v129
	v_med3_f32 v110, v110, s20, v129
	v_med3_f32 v111, v111, s20, v129
	v_med3_f32 v112, v112, s20, v129
	v_med3_f32 v113, v113, s20, v129
	v_med3_f32 v114, v114, s20, v129
	v_med3_f32 v115, v115, s20, v129
	v_mov_b32_e32 v116, 0
	v_mov_b32_e32 v117, 0
	v_mov_b32_e32 v118, 0
	v_mov_b32_e32 v119, 0
	v_cvt_pk_fp8_f32 v116, v100, v101
	v_cvt_pk_fp8_f32 v117, v104, v105
	v_cvt_pk_fp8_f32 v118, v108, v109
	v_cvt_pk_fp8_f32 v119, v112, v113
	v_cvt_pk_fp8_f32 v116, v102, v103 op_sel:[0,0,1]
	v_cvt_pk_fp8_f32 v117, v106, v107 op_sel:[0,0,1]
	v_cvt_pk_fp8_f32 v118, v110, v111 op_sel:[0,0,1]
	v_cvt_pk_fp8_f32 v119, v114, v115 op_sel:[0,0,1]
	s_nop 0
	global_store_dwordx4 v128, v[116:119], s[14:15]
	s_waitcnt vmcnt(12)
	v_mul_f32_e32 v68, 0x43000000, v68
	v_mul_f32_e32 v69, 0x43000000, v69
	v_mul_f32_e32 v70, 0x43000000, v70
	v_mul_f32_e32 v71, 0x43000000, v71
	ds_write_b128 v121, v[68:71]
	v_mul_f32_e32 v72, 0x43000000, v72
	v_mul_f32_e32 v73, 0x43000000, v73
	v_mul_f32_e32 v74, 0x43000000, v74
	v_mul_f32_e32 v75, 0x43000000, v75
	ds_write_b128 v121, v[72:75] offset:1024
	v_mul_f32_e32 v76, 0x43000000, v76
	v_mul_f32_e32 v77, 0x43000000, v77
	v_mul_f32_e32 v78, 0x43000000, v78
	v_mul_f32_e32 v79, 0x43000000, v79
	ds_write_b128 v121, v[76:79] offset:2048
	v_mul_f32_e32 v80, 0x43000000, v80
	v_mul_f32_e32 v81, 0x43000000, v81
	v_mul_f32_e32 v82, 0x43000000, v82
	v_mul_f32_e32 v83, 0x43000000, v83
	ds_write_b128 v121, v[80:83] offset:3072
	v_mul_f32_e32 v84, 0x43000000, v84
	v_mul_f32_e32 v85, 0x43000000, v85
	v_mul_f32_e32 v86, 0x43000000, v86
	v_mul_f32_e32 v87, 0x43000000, v87
	ds_write_b128 v121, v[84:87] offset:4096
	v_mul_f32_e32 v88, 0x43000000, v88
	v_mul_f32_e32 v89, 0x43000000, v89
	v_mul_f32_e32 v90, 0x43000000, v90
	v_mul_f32_e32 v91, 0x43000000, v91
	ds_write_b128 v121, v[88:91] offset:5120
	v_mul_f32_e32 v92, 0x43000000, v92
	v_mul_f32_e32 v93, 0x43000000, v93
	v_mul_f32_e32 v94, 0x43000000, v94
	v_mul_f32_e32 v95, 0x43000000, v95
	ds_write_b128 v121, v[92:95] offset:6144
	v_mul_f32_e32 v96, 0x43000000, v96
	v_mul_f32_e32 v97, 0x43000000, v97
	v_mul_f32_e32 v98, 0x43000000, v98
	v_mul_f32_e32 v99, 0x43000000, v99
	ds_write_b128 v121, v[96:99] offset:7168
	s_waitcnt lgkmcnt(0)
	s_barrier
; #define GAS __attribute__((address_space(1)))
; #define LAS __attribute__((address_space(3)))
; #define LDS_WAIT() asm volatile("s_waitcnt lgkmcnt(0)" ::: "memory")
; __device__ __forceinline__ unsigned pk4_fp8(float a, float b, float c, float d) {
;     a = fminf(fmaxf(a, -448.f), 448.f); b = fminf(fmaxf(b, -448.f), 448.f); c = fminf(fmaxf(c, -448.f), 448.f); d = fminf(fmaxf(d, -448.f), 448.f);
;     int w = __builtin_amdgcn_cvt_pk_fp8_f32(a, b, 0, false); w = __builtin_amdgcn_cvt_pk_fp8_f32(c, d, w, true); return (unsigned)w; }
;     const int pr = item >> 1, kb = 2 * (pr / nblk) + (item & 1), nb = pr % nblk, k0 = 64 * kb, n0 = 32 * nb;
;     const int nr = n0 + (lane & 31); const int sc = MAP == 1 ? src_col_in(nr) : nr;
;     float v[32];
; #pragma unroll
;     for (int i = 0; i < 32; ++i) v[i] = sc >= 0 ? W[(size_t)(k0 + 2 * i + (lane >> 5)) * Nsrc + sc] : 0.f;
; #pragma unroll
;     for (int i = 0; i < 32; ++i) { const int k = k0 + 2 * i + (lane >> 5); float x = v[i] * wscale; if (KS) x *= (k < ksplit ? ksA[k] : ksB[k - ksplit]); scr[(2 * i + (lane >> 5)) * 33 + (lane & 31)] = x; }
;     LDS_WAIT(); asm volatile("" ::: "memory");
;     const int c = lane & 7;
; #pragma unroll
;     for (int j = 0; j < 4; ++j) { const int n = (lane >> 3) + 8 * j; const LAS float* s = scr + (8 * c) * 33 + n;
;         const unsigned long long o = (unsigned long long)pg8::pk4_fp8(s[0 * 33], s[1 * 33], s[2 * 33], s[3 * 33]) | ((unsigned long long)pg8::pk4_fp8(s[4 * 33], s[5 * 33], s[6 * 33], s[7 * 33]) << 32);
;         *(GAS unsigned long long*)(WT + (size_t)(n0 + n) * K + k0 + 8 * c) = o; }
;     LDS_WAIT(); asm volatile("" ::: "memory");
; }
	s_add_i32 s17, s16, 1440
	s_min_u32 s17, s17, 0xbff
	s_lshr_b32 s18, s17, 5
	s_add_i32 s18, s18, 32
	s_and_b32 s19, s17, 31
	s_lshl_b32 s18, s18, 21
	s_lshl_b32 s19, s19, 9
	s_add_u32 s18, s18, s19
	s_add_u32 s12, s2, s18
	s_addc_u32 s13, s3, 0
	global_load_dwordx4 v[68:71], v126, s[12:13]
	s_add_u32 s12, s12, 0x8000
	s_addc_u32 s13, s13, 0
	global_load_dwordx4 v[72:75], v126, s[12:13]
	s_add_u32 s12, s12, 0x8000
	s_addc_u32 s13, s13, 0
	global_load_dwordx4 v[76:79], v126, s[12:13]
	s_add_u32 s12, s12, 0x8000
	s_addc_u32 s13, s13, 0
	global_load_dwordx4 v[80:83], v126, s[12:13]
	s_add_u32 s12, s12, 0x8000
	s_addc_u32 s13, s13, 0
	global_load_dwordx4 v[84:87], v126, s[12:13]
	s_add_u32 s12, s12, 0x8000
	s_addc_u32 s13, s13, 0
	global_load_dwordx4 v[88:91], v126, s[12:13]
	s_add_u32 s12, s12, 0x8000
	s_addc_u32 s13, s13, 0
	global_load_dwordx4 v[92:95], v126, s[12:13]
	s_add_u32 s12, s12, 0x8000
	s_addc_u32 s13, s13, 0
	global_load_dwordx4 v[96:99], v126, s[12:13]
	s_add_i32 s17, s16, 1248
	s_min_u32 s17, s17, 0xbff
	s_lshr_b32 s18, s17, 5
	s_add_i32 s18, s18, 32
	s_and_b32 s19, s17, 31
	s_lshl_b32 s19, s19, 21
	s_lshl_b32 s18, s18, 7
	s_add_u32 s18, s18, s19
	s_add_u32 s14, s4, s18
	s_addc_u32 s15, s5, 0
	ds_read_b32 v100, v123
	ds_read_b32 v101, v123 offset:512
	ds_read_b32 v102, v123 offset:1024
	ds_read_b32 v103, v123 offset:1536
	ds_read_b32 v104, v123 offset:2048
	ds_read_b32 v105, v123 offset:2560
	ds_read_b32 v106, v123 offset:3072
	ds_read_b32 v107, v123 offset:3584
	ds_read_b32 v108, v123 offset:4096
	ds_read_b32 v109, v123 offset:4608
	ds_read_b32 v110, v123 offset:5120
	ds_read_b32 v111, v123 offset:5632
	ds_read_b32 v112, v123 offset:6144
	ds_read_b32 v113, v123 offset:6656
	ds_read_b32 v114, v123 offset:7168
	ds_read_b32 v115, v123 offset:7680
	s_waitcnt lgkmcnt(0)
	v_max_f32_e32 v100, v100, v100
	v_max_f32_e32 v101, v101, v101
	v_max_f32_e32 v102, v102, v102
	v_max_f32_e32 v103, v103, v103
	v_max_f32_e32 v104, v104, v104
	v_max_f32_e32 v105, v105, v105
	v_max_f32_e32 v106, v106, v106
	v_max_f32_e32 v107, v107, v107
	v_max_f32_e32 v108, v108, v108
	v_max_f32_e32 v109, v109, v109
	v_max_f32_e32 v110, v110, v110
	v_max_f32_e32 v111, v111, v111
	v_max_f32_e32 v112, v112, v112
	v_max_f32_e32 v113, v113, v113
	v_max_f32_e32 v114, v114, v114
	v_max_f32_e32 v115, v115, v115
	v_med3_f32 v100, v100, s20, v129
	v_med3_f32 v101, v101, s20, v129
	v_med3_f32 v102, v102, s20, v129
	v_med3_f32 v103, v103, s20, v129
	v_med3_f32 v104, v104, s20, v129
	v_med3_f32 v105, v105, s20, v129
	v_med3_f32 v106, v106, s20, v129
	v_med3_f32 v107, v107, s20, v129
	v_med3_f32 v108, v108, s20, v129
	v_med3_f32 v109, v109, s20, v129
	v_med3_f32 v110, v110, s20, v129
	v_med3_f32 v111, v111, s20, v129
	v_med3_f32 v112, v112, s20, v129
	v_med3_f32 v113, v113, s20, v129
	v_med3_f32 v114, v114, s20, v129
	v_med3_f32 v115, v115, s20, v129
	v_mov_b32_e32 v116, 0
	v_mov_b32_e32 v117, 0
	v_mov_b32_e32 v118, 0
	v_mov_b32_e32 v119, 0
	v_cvt_pk_fp8_f32 v116, v100, v101
	v_cvt_pk_fp8_f32 v117, v104, v105
	v_cvt_pk_fp8_f32 v118, v108, v109
	v_cvt_pk_fp8_f32 v119, v112, v113
	v_cvt_pk_fp8_f32 v116, v102, v103 op_sel:[0,0,1]
	v_cvt_pk_fp8_f32 v117, v106, v107 op_sel:[0,0,1]
	v_cvt_pk_fp8_f32 v118, v110, v111 op_sel:[0,0,1]
	v_cvt_pk_fp8_f32 v119, v114, v115 op_sel:[0,0,1]
	s_nop 0
	global_store_dwordx4 v127, v[116:119], s[14:15]
	ds_read_b32 v100, v125
	ds_read_b32 v101, v125 offset:512
	ds_read_b32 v102, v125 offset:1024
	ds_read_b32 v103, v125 offset:1536
	ds_read_b32 v104, v125 offset:2048
	ds_read_b32 v105, v125 offset:2560
	ds_read_b32 v106, v125 offset:3072
	ds_read_b32 v107, v125 offset:3584
	ds_read_b32 v108, v125 offset:4096
	ds_read_b32 v109, v125 offset:4608
	ds_read_b32 v110, v125 offset:5120
	ds_read_b32 v111, v125 offset:5632
	ds_read_b32 v112, v125 offset:6144
	ds_read_b32 v113, v125 offset:6656
	ds_read_b32 v114, v125 offset:7168
	ds_read_b32 v115, v125 offset:7680
	s_waitcnt lgkmcnt(0)
	v_max_f32_e32 v100, v100, v100
	v_max_f32_e32 v101, v101, v101
	v_max_f32_e32 v102, v102, v102
	v_max_f32_e32 v103, v103, v103
	v_max_f32_e32 v104, v104, v104
	v_max_f32_e32 v105, v105, v105
	v_max_f32_e32 v106, v106, v106
	v_max_f32_e32 v107, v107, v107
	v_max_f32_e32 v108, v108, v108
	v_max_f32_e32 v109, v109, v109
	v_max_f32_e32 v110, v110, v110
	v_max_f32_e32 v111, v111, v111
	v_max_f32_e32 v112, v112, v112
	v_max_f32_e32 v113, v113, v113
	v_max_f32_e32 v114, v114, v114
	v_max_f32_e32 v115, v115, v115
	v_med3_f32 v100, v100, s20, v129
	v_med3_f32 v101, v101, s20, v129
	v_med3_f32 v102, v102, s20, v129
	v_med3_f32 v103, v103, s20, v129
	v_med3_f32 v104, v104, s20, v129
	v_med3_f32 v105, v105, s20, v129
	v_med3_f32 v106, v106, s20, v129
	v_med3_f32 v107, v107, s20, v129
	v_med3_f32 v108, v108, s20, v129
	v_med3_f32 v109, v109, s20, v129
	v_med3_f32 v110, v110, s20, v129
	v_med3_f32 v111, v111, s20, v129
	v_med3_f32 v112, v112, s20, v129
	v_med3_f32 v113, v113, s20, v129
	v_med3_f32 v114, v114, s20, v129
	v_med3_f32 v115, v115, s20, v129
	v_mov_b32_e32 v116, 0
	v_mov_b32_e32 v117, 0
	v_mov_b32_e32 v118, 0
	v_mov_b32_e32 v119, 0
	v_cvt_pk_fp8_f32 v116, v100, v101
	v_cvt_pk_fp8_f32 v117, v104, v105
	v_cvt_pk_fp8_f32 v118, v108, v109
	v_cvt_pk_fp8_f32 v119, v112, v113
	v_cvt_pk_fp8_f32 v116, v102, v103 op_sel:[0,0,1]
	v_cvt_pk_fp8_f32 v117, v106, v107 op_sel:[0,0,1]
	v_cvt_pk_fp8_f32 v118, v110, v111 op_sel:[0,0,1]
	v_cvt_pk_fp8_f32 v119, v114, v115 op_sel:[0,0,1]
	s_nop 0
	global_store_dwordx4 v128, v[116:119], s[14:15]
	s_waitcnt vmcnt(12)
	v_mul_f32_e32 v36, 0x43000000, v36
	v_mul_f32_e32 v37, 0x43000000, v37
	v_mul_f32_e32 v38, 0x43000000, v38
	v_mul_f32_e32 v39, 0x43000000, v39
	ds_write_b128 v120, v[36:39]
	v_mul_f32_e32 v40, 0x43000000, v40
	v_mul_f32_e32 v41, 0x43000000, v41
	v_mul_f32_e32 v42, 0x43000000, v42
	v_mul_f32_e32 v43, 0x43000000, v43
	ds_write_b128 v120, v[40:43] offset:1024
	v_mul_f32_e32 v44, 0x43000000, v44
	v_mul_f32_e32 v45, 0x43000000, v45
	v_mul_f32_e32 v46, 0x43000000, v46
	v_mul_f32_e32 v47, 0x43000000, v47
	ds_write_b128 v120, v[44:47] offset:2048
	v_mul_f32_e32 v48, 0x43000000, v48
	v_mul_f32_e32 v49, 0x43000000, v49
	v_mul_f32_e32 v50, 0x43000000, v50
	v_mul_f32_e32 v51, 0x43000000, v51
	ds_write_b128 v120, v[48:51] offset:3072
	v_mul_f32_e32 v52, 0x43000000, v52
	v_mul_f32_e32 v53, 0x43000000, v53
	v_mul_f32_e32 v54, 0x43000000, v54
	v_mul_f32_e32 v55, 0x43000000, v55
	ds_write_b128 v120, v[52:55] offset:4096
	v_mul_f32_e32 v56, 0x43000000, v56
	v_mul_f32_e32 v57, 0x43000000, v57
	v_mul_f32_e32 v58, 0x43000000, v58
	v_mul_f32_e32 v59, 0x43000000, v59
	ds_write_b128 v120, v[56:59] offset:5120
	v_mul_f32_e32 v60, 0x43000000, v60
	v_mul_f32_e32 v61, 0x43000000, v61
	v_mul_f32_e32 v62, 0x43000000, v62
	v_mul_f32_e32 v63, 0x43000000, v63
	ds_write_b128 v120, v[60:63] offset:6144
	v_mul_f32_e32 v64, 0x43000000, v64
	v_mul_f32_e32 v65, 0x43000000, v65
	v_mul_f32_e32 v66, 0x43000000, v66
	v_mul_f32_e32 v67, 0x43000000, v67
	ds_write_b128 v120, v[64:67] offset:7168
	s_waitcnt lgkmcnt(0)
	s_barrier
; #define GAS __attribute__((address_space(1)))
; #define LAS __attribute__((address_space(3)))
; #define LDS_WAIT() asm volatile("s_waitcnt lgkmcnt(0)" ::: "memory")
; __device__ __forceinline__ unsigned pk4_fp8(float a, float b, float c, float d) {
;     a = fminf(fmaxf(a, -448.f), 448.f); b = fminf(fmaxf(b, -448.f), 448.f); c = fminf(fmaxf(c, -448.f), 448.f); d = fminf(fmaxf(d, -448.f), 448.f);
;     int w = __builtin_amdgcn_cvt_pk_fp8_f32(a, b, 0, false); w = __builtin_amdgcn_cvt_pk_fp8_f32(c, d, w, true); return (unsigned)w; }
;     const int pr = item >> 1, kb = 2 * (pr / nblk) + (item & 1), nb = pr % nblk, k0 = 64 * kb, n0 = 32 * nb;
;     const int nr = n0 + (lane & 31); const int sc = MAP == 1 ? src_col_in(nr) : nr;
;     float v[32];
; #pragma unroll
;     for (int i = 0; i < 32; ++i) v[i] = sc >= 0 ? W[(size_t)(k0 + 2 * i + (lane >> 5)) * Nsrc + sc] : 0.f;
; #pragma unroll
;     for (int i = 0; i < 32; ++i) { const int k = k0 + 2 * i + (lane >> 5); float x = v[i] * wscale; if (KS) x *= (k < ksplit ? ksA[k] : ksB[k - ksplit]); scr[(2 * i + (lane >> 5)) * 33 + (lane & 31)] = x; }
;     LDS_WAIT(); asm volatile("" ::: "memory");
;     const int c = lane & 7;
; #pragma unroll
;     for (int j = 0; j < 4; ++j) { const int n = (lane >> 3) + 8 * j; const LAS float* s = scr + (8 * c) * 33 + n;
;         const unsigned long long o = (unsigned long long)pg8::pk4_fp8(s[0 * 33], s[1 * 33], s[2 * 33], s[3 * 33]) | ((unsigned long long)pg8::pk4_fp8(s[4 * 33], s[5 * 33], s[6 * 33], s[7 * 33]) << 32);
;         *(GAS unsigned long long*)(WT + (size_t)(n0 + n) * K + k0 + 8 * c) = o; }
;     LDS_WAIT(); asm volatile("" ::: "memory");
; }
	s_add_i32 s17, s16, 1536
	s_min_u32 s17, s17, 0xbff
	s_lshr_b32 s18, s17, 5
	s_add_i32 s18, s18, 32
	s_and_b32 s19, s17, 31
	s_lshl_b32 s18, s18, 21
	s_lshl_b32 s19, s19, 9
	s_add_u32 s18, s18, s19
	s_add_u32 s12, s2, s18
	s_addc_u32 s13, s3, 0
	global_load_dwordx4 v[36:39], v126, s[12:13]
	s_add_u32 s12, s12, 0x8000
	s_addc_u32 s13, s13, 0
	global_load_dwordx4 v[40:43], v126, s[12:13]
	s_add_u32 s12, s12, 0x8000
	s_addc_u32 s13, s13, 0
	global_load_dwordx4 v[44:47], v126, s[12:13]
	s_add_u32 s12, s12, 0x8000
	s_addc_u32 s13, s13, 0
	global_load_dwordx4 v[48:51], v126, s[12:13]
	s_add_u32 s12, s12, 0x8000
	s_addc_u32 s13, s13, 0
	global_load_dwordx4 v[52:55], v126, s[12:13]
	s_add_u32 s12, s12, 0x8000
	s_addc_u32 s13, s13, 0
	global_load_dwordx4 v[56:59], v126, s[12:13]
	s_add_u32 s12, s12, 0x8000
	s_addc_u32 s13, s13, 0
	global_load_dwordx4 v[60:63], v126, s[12:13]
	s_add_u32 s12, s12, 0x8000
	s_addc_u32 s13, s13, 0
	global_load_dwordx4 v[64:67], v126, s[12:13]
	s_add_i32 s17, s16, 1344
	s_min_u32 s17, s17, 0xbff
	s_lshr_b32 s18, s17, 5
	s_add_i32 s18, s18, 32
	s_and_b32 s19, s17, 31
	s_lshl_b32 s19, s19, 21
	s_lshl_b32 s18, s18, 7
	s_add_u32 s18, s18, s19
	s_add_u32 s14, s4, s18
	s_addc_u32 s15, s5, 0
	ds_read_b32 v100, v122
	ds_read_b32 v101, v122 offset:512
	ds_read_b32 v102, v122 offset:1024
	ds_read_b32 v103, v122 offset:1536
	ds_read_b32 v104, v122 offset:2048
	ds_read_b32 v105, v122 offset:2560
	ds_read_b32 v106, v122 offset:3072
	ds_read_b32 v107, v122 offset:3584
	ds_read_b32 v108, v122 offset:4096
	ds_read_b32 v109, v122 offset:4608
	ds_read_b32 v110, v122 offset:5120
	ds_read_b32 v111, v122 offset:5632
	ds_read_b32 v112, v122 offset:6144
	ds_read_b32 v113, v122 offset:6656
	ds_read_b32 v114, v122 offset:7168
	ds_read_b32 v115, v122 offset:7680
	s_waitcnt lgkmcnt(0)
	v_max_f32_e32 v100, v100, v100
	v_max_f32_e32 v101, v101, v101
	v_max_f32_e32 v102, v102, v102
	v_max_f32_e32 v103, v103, v103
	v_max_f32_e32 v104, v104, v104
	v_max_f32_e32 v105, v105, v105
	v_max_f32_e32 v106, v106, v106
	v_max_f32_e32 v107, v107, v107
	v_max_f32_e32 v108, v108, v108
	v_max_f32_e32 v109, v109, v109
	v_max_f32_e32 v110, v110, v110
	v_max_f32_e32 v111, v111, v111
	v_max_f32_e32 v112, v112, v112
	v_max_f32_e32 v113, v113, v113
	v_max_f32_e32 v114, v114, v114
	v_max_f32_e32 v115, v115, v115
	v_med3_f32 v100, v100, s20, v129
	v_med3_f32 v101, v101, s20, v129
	v_med3_f32 v102, v102, s20, v129
	v_med3_f32 v103, v103, s20, v129
	v_med3_f32 v104, v104, s20, v129
	v_med3_f32 v105, v105, s20, v129
	v_med3_f32 v106, v106, s20, v129
	v_med3_f32 v107, v107, s20, v129
	v_med3_f32 v108, v108, s20, v129
	v_med3_f32 v109, v109, s20, v129
	v_med3_f32 v110, v110, s20, v129
	v_med3_f32 v111, v111, s20, v129
	v_med3_f32 v112, v112, s20, v129
	v_med3_f32 v113, v113, s20, v129
	v_med3_f32 v114, v114, s20, v129
	v_med3_f32 v115, v115, s20, v129
	v_mov_b32_e32 v116, 0
	v_mov_b32_e32 v117, 0
	v_mov_b32_e32 v118, 0
	v_mov_b32_e32 v119, 0
	v_cvt_pk_fp8_f32 v116, v100, v101
	v_cvt_pk_fp8_f32 v117, v104, v105
	v_cvt_pk_fp8_f32 v118, v108, v109
	v_cvt_pk_fp8_f32 v119, v112, v113
	v_cvt_pk_fp8_f32 v116, v102, v103 op_sel:[0,0,1]
	v_cvt_pk_fp8_f32 v117, v106, v107 op_sel:[0,0,1]
	v_cvt_pk_fp8_f32 v118, v110, v111 op_sel:[0,0,1]
	v_cvt_pk_fp8_f32 v119, v114, v115 op_sel:[0,0,1]
	s_nop 0
	global_store_dwordx4 v127, v[116:119], s[14:15]
	ds_read_b32 v100, v124
	ds_read_b32 v101, v124 offset:512
	ds_read_b32 v102, v124 offset:1024
	ds_read_b32 v103, v124 offset:1536
	ds_read_b32 v104, v124 offset:2048
	ds_read_b32 v105, v124 offset:2560
	ds_read_b32 v106, v124 offset:3072
	ds_read_b32 v107, v124 offset:3584
	ds_read_b32 v108, v124 offset:4096
	ds_read_b32 v109, v124 offset:4608
	ds_read_b32 v110, v124 offset:5120
	ds_read_b32 v111, v124 offset:5632
	ds_read_b32 v112, v124 offset:6144
	ds_read_b32 v113, v124 offset:6656
	ds_read_b32 v114, v124 offset:7168
	ds_read_b32 v115, v124 offset:7680
	s_waitcnt lgkmcnt(0)
	v_max_f32_e32 v100, v100, v100
	v_max_f32_e32 v101, v101, v101
	v_max_f32_e32 v102, v102, v102
	v_max_f32_e32 v103, v103, v103
	v_max_f32_e32 v104, v104, v104
	v_max_f32_e32 v105, v105, v105
	v_max_f32_e32 v106, v106, v106
	v_max_f32_e32 v107, v107, v107
	v_max_f32_e32 v108, v108, v108
	v_max_f32_e32 v109, v109, v109
	v_max_f32_e32 v110, v110, v110
	v_max_f32_e32 v111, v111, v111
	v_max_f32_e32 v112, v112, v112
	v_max_f32_e32 v113, v113, v113
	v_max_f32_e32 v114, v114, v114
	v_max_f32_e32 v115, v115, v115
	v_med3_f32 v100, v100, s20, v129
	v_med3_f32 v101, v101, s20, v129
	v_med3_f32 v102, v102, s20, v129
	v_med3_f32 v103, v103, s20, v129
	v_med3_f32 v104, v104, s20, v129
	v_med3_f32 v105, v105, s20, v129
	v_med3_f32 v106, v106, s20, v129
	v_med3_f32 v107, v107, s20, v129
	v_med3_f32 v108, v108, s20, v129
	v_med3_f32 v109, v109, s20, v129
	v_med3_f32 v110, v110, s20, v129
	v_med3_f32 v111, v111, s20, v129
	v_med3_f32 v112, v112, s20, v129
	v_med3_f32 v113, v113, s20, v129
	v_med3_f32 v114, v114, s20, v129
	v_med3_f32 v115, v115, s20, v129
	v_mov_b32_e32 v116, 0
	v_mov_b32_e32 v117, 0
	v_mov_b32_e32 v118, 0
	v_mov_b32_e32 v119, 0
	v_cvt_pk_fp8_f32 v116, v100, v101
	v_cvt_pk_fp8_f32 v117, v104, v105
	v_cvt_pk_fp8_f32 v118, v108, v109
	v_cvt_pk_fp8_f32 v119, v112, v113
	v_cvt_pk_fp8_f32 v116, v102, v103 op_sel:[0,0,1]
	v_cvt_pk_fp8_f32 v117, v106, v107 op_sel:[0,0,1]
	v_cvt_pk_fp8_f32 v118, v110, v111 op_sel:[0,0,1]
	v_cvt_pk_fp8_f32 v119, v114, v115 op_sel:[0,0,1]
	s_nop 0
	global_store_dwordx4 v128, v[116:119], s[14:15]
	s_waitcnt vmcnt(12)
	v_mul_f32_e32 v68, 0x43000000, v68
	v_mul_f32_e32 v69, 0x43000000, v69
	v_mul_f32_e32 v70, 0x43000000, v70
	v_mul_f32_e32 v71, 0x43000000, v71
	ds_write_b128 v121, v[68:71]
	v_mul_f32_e32 v72, 0x43000000, v72
	v_mul_f32_e32 v73, 0x43000000, v73
	v_mul_f32_e32 v74, 0x43000000, v74
	v_mul_f32_e32 v75, 0x43000000, v75
	ds_write_b128 v121, v[72:75] offset:1024
	v_mul_f32_e32 v76, 0x43000000, v76
	v_mul_f32_e32 v77, 0x43000000, v77
	v_mul_f32_e32 v78, 0x43000000, v78
	v_mul_f32_e32 v79, 0x43000000, v79
	ds_write_b128 v121, v[76:79] offset:2048
	v_mul_f32_e32 v80, 0x43000000, v80
	v_mul_f32_e32 v81, 0x43000000, v81
	v_mul_f32_e32 v82, 0x43000000, v82
	v_mul_f32_e32 v83, 0x43000000, v83
	ds_write_b128 v121, v[80:83] offset:3072
	v_mul_f32_e32 v84, 0x43000000, v84
	v_mul_f32_e32 v85, 0x43000000, v85
	v_mul_f32_e32 v86, 0x43000000, v86
	v_mul_f32_e32 v87, 0x43000000, v87
	ds_write_b128 v121, v[84:87] offset:4096
	v_mul_f32_e32 v88, 0x43000000, v88
	v_mul_f32_e32 v89, 0x43000000, v89
	v_mul_f32_e32 v90, 0x43000000, v90
	v_mul_f32_e32 v91, 0x43000000, v91
	ds_write_b128 v121, v[88:91] offset:5120
	v_mul_f32_e32 v92, 0x43000000, v92
	v_mul_f32_e32 v93, 0x43000000, v93
	v_mul_f32_e32 v94, 0x43000000, v94
	v_mul_f32_e32 v95, 0x43000000, v95
	ds_write_b128 v121, v[92:95] offset:6144
	v_mul_f32_e32 v96, 0x43000000, v96
	v_mul_f32_e32 v97, 0x43000000, v97
	v_mul_f32_e32 v98, 0x43000000, v98
	v_mul_f32_e32 v99, 0x43000000, v99
	ds_write_b128 v121, v[96:99] offset:7168
	s_waitcnt lgkmcnt(0)
	s_barrier
; #define GAS __attribute__((address_space(1)))
; #define LAS __attribute__((address_space(3)))
; #define LDS_WAIT() asm volatile("s_waitcnt lgkmcnt(0)" ::: "memory")
; __device__ __forceinline__ unsigned pk4_fp8(float a, float b, float c, float d) {
;     a = fminf(fmaxf(a, -448.f), 448.f); b = fminf(fmaxf(b, -448.f), 448.f); c = fminf(fmaxf(c, -448.f), 448.f); d = fminf(fmaxf(d, -448.f), 448.f);
;     int w = __builtin_amdgcn_cvt_pk_fp8_f32(a, b, 0, false); w = __builtin_amdgcn_cvt_pk_fp8_f32(c, d, w, true); return (unsigned)w; }
;     const int pr = item >> 1, kb = 2 * (pr / nblk) + (item & 1), nb = pr % nblk, k0 = 64 * kb, n0 = 32 * nb;
;     const int nr = n0 + (lane & 31); const int sc = MAP == 1 ? src_col_in(nr) : nr;
;     float v[32];
; #pragma unroll
;     for (int i = 0; i < 32; ++i) v[i] = sc >= 0 ? W[(size_t)(k0 + 2 * i + (lane >> 5)) * Nsrc + sc] : 0.f;
; #pragma unroll
;     for (int i = 0; i < 32; ++i) { const int k = k0 + 2 * i + (lane >> 5); float x = v[i] * wscale; if (KS) x *= (k < ksplit ? ksA[k] : ksB[k - ksplit]); scr[(2 * i + (lane >> 5)) * 33 + (lane & 31)] = x; }
;     LDS_WAIT(); asm volatile("" ::: "memory");
;     const int c = lane & 7;
; #pragma unroll
;     for (int j = 0; j < 4; ++j) { const int n = (lane >> 3) + 8 * j; const LAS float* s = scr + (8 * c) * 33 + n;
;         const unsigned long long o = (unsigned long long)pg8::pk4_fp8(s[0 * 33], s[1 * 33], s[2 * 33], s[3 * 33]) | ((unsigned long long)pg8::pk4_fp8(s[4 * 33], s[5 * 33], s[6 * 33], s[7 * 33]) << 32);
;         *(GAS unsigned long long*)(WT + (size_t)(n0 + n) * K + k0 + 8 * c) = o; }
;     LDS_WAIT(); asm volatile("" ::: "memory");
; }
	s_add_i32 s17, s16, 1632
	s_min_u32 s17, s17, 0xbff
	s_lshr_b32 s18, s17, 5
	s_add_i32 s18, s18, 32
	s_and_b32 s19, s17, 31
	s_lshl_b32 s18, s18, 21
	s_lshl_b32 s19, s19, 9
	s_add_u32 s18, s18, s19
	s_add_u32 s12, s2, s18
	s_addc_u32 s13, s3, 0
	global_load_dwordx4 v[68:71], v126, s[12:13]
	s_add_u32 s12, s12, 0x8000
	s_addc_u32 s13, s13, 0
	global_load_dwordx4 v[72:75], v126, s[12:13]
	s_add_u32 s12, s12, 0x8000
	s_addc_u32 s13, s13, 0
	global_load_dwordx4 v[76:79], v126, s[12:13]
	s_add_u32 s12, s12, 0x8000
	s_addc_u32 s13, s13, 0
	global_load_dwordx4 v[80:83], v126, s[12:13]
	s_add_u32 s12, s12, 0x8000
	s_addc_u32 s13, s13, 0
	global_load_dwordx4 v[84:87], v126, s[12:13]
	s_add_u32 s12, s12, 0x8000
	s_addc_u32 s13, s13, 0
	global_load_dwordx4 v[88:91], v126, s[12:13]
	s_add_u32 s12, s12, 0x8000
	s_addc_u32 s13, s13, 0
	global_load_dwordx4 v[92:95], v126, s[12:13]
	s_add_u32 s12, s12, 0x8000
	s_addc_u32 s13, s13, 0
	global_load_dwordx4 v[96:99], v126, s[12:13]
	s_add_i32 s17, s16, 1440
	s_min_u32 s17, s17, 0xbff
	s_lshr_b32 s18, s17, 5
	s_add_i32 s18, s18, 32
	s_and_b32 s19, s17, 31
	s_lshl_b32 s19, s19, 21
	s_lshl_b32 s18, s18, 7
	s_add_u32 s18, s18, s19
	s_add_u32 s14, s4, s18
	s_addc_u32 s15, s5, 0
	ds_read_b32 v100, v123
	ds_read_b32 v101, v123 offset:512
	ds_read_b32 v102, v123 offset:1024
	ds_read_b32 v103, v123 offset:1536
	ds_read_b32 v104, v123 offset:2048
	ds_read_b32 v105, v123 offset:2560
	ds_read_b32 v106, v123 offset:3072
	ds_read_b32 v107, v123 offset:3584
	ds_read_b32 v108, v123 offset:4096
	ds_read_b32 v109, v123 offset:4608
	ds_read_b32 v110, v123 offset:5120
	ds_read_b32 v111, v123 offset:5632
	ds_read_b32 v112, v123 offset:6144
	ds_read_b32 v113, v123 offset:6656
	ds_read_b32 v114, v123 offset:7168
	ds_read_b32 v115, v123 offset:7680
	s_waitcnt lgkmcnt(0)
	v_max_f32_e32 v100, v100, v100
	v_max_f32_e32 v101, v101, v101
	v_max_f32_e32 v102, v102, v102
	v_max_f32_e32 v103, v103, v103
	v_max_f32_e32 v104, v104, v104
	v_max_f32_e32 v105, v105, v105
	v_max_f32_e32 v106, v106, v106
	v_max_f32_e32 v107, v107, v107
	v_max_f32_e32 v108, v108, v108
	v_max_f32_e32 v109, v109, v109
	v_max_f32_e32 v110, v110, v110
	v_max_f32_e32 v111, v111, v111
	v_max_f32_e32 v112, v112, v112
	v_max_f32_e32 v113, v113, v113
	v_max_f32_e32 v114, v114, v114
	v_max_f32_e32 v115, v115, v115
	v_med3_f32 v100, v100, s20, v129
	v_med3_f32 v101, v101, s20, v129
	v_med3_f32 v102, v102, s20, v129
	v_med3_f32 v103, v103, s20, v129
	v_med3_f32 v104, v104, s20, v129
	v_med3_f32 v105, v105, s20, v129
	v_med3_f32 v106, v106, s20, v129
	v_med3_f32 v107, v107, s20, v129
	v_med3_f32 v108, v108, s20, v129
	v_med3_f32 v109, v109, s20, v129
	v_med3_f32 v110, v110, s20, v129
	v_med3_f32 v111, v111, s20, v129
	v_med3_f32 v112, v112, s20, v129
	v_med3_f32 v113, v113, s20, v129
	v_med3_f32 v114, v114, s20, v129
	v_med3_f32 v115, v115, s20, v129
	v_mov_b32_e32 v116, 0
	v_mov_b32_e32 v117, 0
	v_mov_b32_e32 v118, 0
	v_mov_b32_e32 v119, 0
	v_cvt_pk_fp8_f32 v116, v100, v101
	v_cvt_pk_fp8_f32 v117, v104, v105
	v_cvt_pk_fp8_f32 v118, v108, v109
	v_cvt_pk_fp8_f32 v119, v112, v113
	v_cvt_pk_fp8_f32 v116, v102, v103 op_sel:[0,0,1]
	v_cvt_pk_fp8_f32 v117, v106, v107 op_sel:[0,0,1]
	v_cvt_pk_fp8_f32 v118, v110, v111 op_sel:[0,0,1]
	v_cvt_pk_fp8_f32 v119, v114, v115 op_sel:[0,0,1]
	s_nop 0
	global_store_dwordx4 v127, v[116:119], s[14:15]
	ds_read_b32 v100, v125
	ds_read_b32 v101, v125 offset:512
	ds_read_b32 v102, v125 offset:1024
	ds_read_b32 v103, v125 offset:1536
	ds_read_b32 v104, v125 offset:2048
	ds_read_b32 v105, v125 offset:2560
	ds_read_b32 v106, v125 offset:3072
	ds_read_b32 v107, v125 offset:3584
	ds_read_b32 v108, v125 offset:4096
	ds_read_b32 v109, v125 offset:4608
	ds_read_b32 v110, v125 offset:5120
	ds_read_b32 v111, v125 offset:5632
	ds_read_b32 v112, v125 offset:6144
	ds_read_b32 v113, v125 offset:6656
	ds_read_b32 v114, v125 offset:7168
	ds_read_b32 v115, v125 offset:7680
	s_waitcnt lgkmcnt(0)
	v_max_f32_e32 v100, v100, v100
	v_max_f32_e32 v101, v101, v101
	v_max_f32_e32 v102, v102, v102
	v_max_f32_e32 v103, v103, v103
	v_max_f32_e32 v104, v104, v104
	v_max_f32_e32 v105, v105, v105
	v_max_f32_e32 v106, v106, v106
	v_max_f32_e32 v107, v107, v107
	v_max_f32_e32 v108, v108, v108
	v_max_f32_e32 v109, v109, v109
	v_max_f32_e32 v110, v110, v110
	v_max_f32_e32 v111, v111, v111
	v_max_f32_e32 v112, v112, v112
	v_max_f32_e32 v113, v113, v113
	v_max_f32_e32 v114, v114, v114
	v_max_f32_e32 v115, v115, v115
	v_med3_f32 v100, v100, s20, v129
	v_med3_f32 v101, v101, s20, v129
	v_med3_f32 v102, v102, s20, v129
	v_med3_f32 v103, v103, s20, v129
	v_med3_f32 v104, v104, s20, v129
	v_med3_f32 v105, v105, s20, v129
	v_med3_f32 v106, v106, s20, v129
	v_med3_f32 v107, v107, s20, v129
	v_med3_f32 v108, v108, s20, v129
	v_med3_f32 v109, v109, s20, v129
	v_med3_f32 v110, v110, s20, v129
	v_med3_f32 v111, v111, s20, v129
	v_med3_f32 v112, v112, s20, v129
	v_med3_f32 v113, v113, s20, v129
	v_med3_f32 v114, v114, s20, v129
	v_med3_f32 v115, v115, s20, v129
	v_mov_b32_e32 v116, 0
	v_mov_b32_e32 v117, 0
	v_mov_b32_e32 v118, 0
	v_mov_b32_e32 v119, 0
	v_cvt_pk_fp8_f32 v116, v100, v101
	v_cvt_pk_fp8_f32 v117, v104, v105
	v_cvt_pk_fp8_f32 v118, v108, v109
	v_cvt_pk_fp8_f32 v119, v112, v113
	v_cvt_pk_fp8_f32 v116, v102, v103 op_sel:[0,0,1]
	v_cvt_pk_fp8_f32 v117, v106, v107 op_sel:[0,0,1]
	v_cvt_pk_fp8_f32 v118, v110, v111 op_sel:[0,0,1]
	v_cvt_pk_fp8_f32 v119, v114, v115 op_sel:[0,0,1]
	s_nop 0
	global_store_dwordx4 v128, v[116:119], s[14:15]
	s_waitcnt vmcnt(12)
	v_mul_f32_e32 v36, 0x43000000, v36
	v_mul_f32_e32 v37, 0x43000000, v37
	v_mul_f32_e32 v38, 0x43000000, v38
	v_mul_f32_e32 v39, 0x43000000, v39
	ds_write_b128 v120, v[36:39]
	v_mul_f32_e32 v40, 0x43000000, v40
	v_mul_f32_e32 v41, 0x43000000, v41
	v_mul_f32_e32 v42, 0x43000000, v42
	v_mul_f32_e32 v43, 0x43000000, v43
	ds_write_b128 v120, v[40:43] offset:1024
	v_mul_f32_e32 v44, 0x43000000, v44
	v_mul_f32_e32 v45, 0x43000000, v45
	v_mul_f32_e32 v46, 0x43000000, v46
	v_mul_f32_e32 v47, 0x43000000, v47
	ds_write_b128 v120, v[44:47] offset:2048
	v_mul_f32_e32 v48, 0x43000000, v48
	v_mul_f32_e32 v49, 0x43000000, v49
	v_mul_f32_e32 v50, 0x43000000, v50
	v_mul_f32_e32 v51, 0x43000000, v51
	ds_write_b128 v120, v[48:51] offset:3072
	v_mul_f32_e32 v52, 0x43000000, v52
	v_mul_f32_e32 v53, 0x43000000, v53
	v_mul_f32_e32 v54, 0x43000000, v54
	v_mul_f32_e32 v55, 0x43000000, v55
	ds_write_b128 v120, v[52:55] offset:4096
	v_mul_f32_e32 v56, 0x43000000, v56
	v_mul_f32_e32 v57, 0x43000000, v57
	v_mul_f32_e32 v58, 0x43000000, v58
	v_mul_f32_e32 v59, 0x43000000, v59
	ds_write_b128 v120, v[56:59] offset:5120
	v_mul_f32_e32 v60, 0x43000000, v60
	v_mul_f32_e32 v61, 0x43000000, v61
	v_mul_f32_e32 v62, 0x43000000, v62
	v_mul_f32_e32 v63, 0x43000000, v63
	ds_write_b128 v120, v[60:63] offset:6144
	v_mul_f32_e32 v64, 0x43000000, v64
	v_mul_f32_e32 v65, 0x43000000, v65
	v_mul_f32_e32 v66, 0x43000000, v66
	v_mul_f32_e32 v67, 0x43000000, v67
	ds_write_b128 v120, v[64:67] offset:7168
	s_waitcnt lgkmcnt(0)
	s_barrier
; #define GAS __attribute__((address_space(1)))
; #define LAS __attribute__((address_space(3)))
; #define LDS_WAIT() asm volatile("s_waitcnt lgkmcnt(0)" ::: "memory")
; __device__ __forceinline__ unsigned pk4_fp8(float a, float b, float c, float d) {
;     a = fminf(fmaxf(a, -448.f), 448.f); b = fminf(fmaxf(b, -448.f), 448.f); c = fminf(fmaxf(c, -448.f), 448.f); d = fminf(fmaxf(d, -448.f), 448.f);
;     int w = __builtin_amdgcn_cvt_pk_fp8_f32(a, b, 0, false); w = __builtin_amdgcn_cvt_pk_fp8_f32(c, d, w, true); return (unsigned)w; }
;     const int pr = item >> 1, kb = 2 * (pr / nblk) + (item & 1), nb = pr % nblk, k0 = 64 * kb, n0 = 32 * nb;
;     const int nr = n0 + (lane & 31); const int sc = MAP == 1 ? src_col_in(nr) : nr;
;     float v[32];
; #pragma unroll
;     for (int i = 0; i < 32; ++i) v[i] = sc >= 0 ? W[(size_t)(k0 + 2 * i + (lane >> 5)) * Nsrc + sc] : 0.f;
; #pragma unroll
;     for (int i = 0; i < 32; ++i) { const int k = k0 + 2 * i + (lane >> 5); float x = v[i] * wscale; if (KS) x *= (k < ksplit ? ksA[k] : ksB[k - ksplit]); scr[(2 * i + (lane >> 5)) * 33 + (lane & 31)] = x; }
;     LDS_WAIT(); asm volatile("" ::: "memory");
;     const int c = lane & 7;
; #pragma unroll
;     for (int j = 0; j < 4; ++j) { const int n = (lane >> 3) + 8 * j; const LAS float* s = scr + (8 * c) * 33 + n;
;         const unsigned long long o = (unsigned long long)pg8::pk4_fp8(s[0 * 33], s[1 * 33], s[2 * 33], s[3 * 33]) | ((unsigned long long)pg8::pk4_fp8(s[4 * 33], s[5 * 33], s[6 * 33], s[7 * 33]) << 32);
;         *(GAS unsigned long long*)(WT + (size_t)(n0 + n) * K + k0 + 8 * c) = o; }
;     LDS_WAIT(); asm volatile("" ::: "memory");
; }
	s_add_i32 s17, s16, 1728
	s_min_u32 s17, s17, 0xbff
	s_lshr_b32 s18, s17, 5
	s_add_i32 s18, s18, 32
	s_and_b32 s19, s17, 31
	s_lshl_b32 s18, s18, 21
	s_lshl_b32 s19, s19, 9
	s_add_u32 s18, s18, s19
	s_add_u32 s12, s2, s18
	s_addc_u32 s13, s3, 0
	global_load_dwordx4 v[36:39], v126, s[12:13]
	s_add_u32 s12, s12, 0x8000
	s_addc_u32 s13, s13, 0
	global_load_dwordx4 v[40:43], v126, s[12:13]
	s_add_u32 s12, s12, 0x8000
	s_addc_u32 s13, s13, 0
	global_load_dwordx4 v[44:47], v126, s[12:13]
	s_add_u32 s12, s12, 0x8000
	s_addc_u32 s13, s13, 0
	global_load_dwordx4 v[48:51], v126, s[12:13]
	s_add_u32 s12, s12, 0x8000
	s_addc_u32 s13, s13, 0
	global_load_dwordx4 v[52:55], v126, s[12:13]
	s_add_u32 s12, s12, 0x8000
	s_addc_u32 s13, s13, 0
	global_load_dwordx4 v[56:59], v126, s[12:13]
	s_add_u32 s12, s12, 0x8000
	s_addc_u32 s13, s13, 0
	global_load_dwordx4 v[60:63], v126, s[12:13]
	s_add_u32 s12, s12, 0x8000
	s_addc_u32 s13, s13, 0
	global_load_dwordx4 v[64:67], v126, s[12:13]
	s_add_i32 s17, s16, 1536
	s_min_u32 s17, s17, 0xbff
	s_lshr_b32 s18, s17, 5
	s_add_i32 s18, s18, 32
	s_and_b32 s19, s17, 31
	s_lshl_b32 s19, s19, 21
	s_lshl_b32 s18, s18, 7
	s_add_u32 s18, s18, s19
	s_add_u32 s14, s4, s18
	s_addc_u32 s15, s5, 0
	ds_read_b32 v100, v122
	ds_read_b32 v101, v122 offset:512
	ds_read_b32 v102, v122 offset:1024
	ds_read_b32 v103, v122 offset:1536
	ds_read_b32 v104, v122 offset:2048
	ds_read_b32 v105, v122 offset:2560
	ds_read_b32 v106, v122 offset:3072
	ds_read_b32 v107, v122 offset:3584
	ds_read_b32 v108, v122 offset:4096
	ds_read_b32 v109, v122 offset:4608
	ds_read_b32 v110, v122 offset:5120
	ds_read_b32 v111, v122 offset:5632
	ds_read_b32 v112, v122 offset:6144
	ds_read_b32 v113, v122 offset:6656
	ds_read_b32 v114, v122 offset:7168
	ds_read_b32 v115, v122 offset:7680
	s_waitcnt lgkmcnt(0)
	v_max_f32_e32 v100, v100, v100
	v_max_f32_e32 v101, v101, v101
	v_max_f32_e32 v102, v102, v102
	v_max_f32_e32 v103, v103, v103
	v_max_f32_e32 v104, v104, v104
	v_max_f32_e32 v105, v105, v105
	v_max_f32_e32 v106, v106, v106
	v_max_f32_e32 v107, v107, v107
	v_max_f32_e32 v108, v108, v108
	v_max_f32_e32 v109, v109, v109
	v_max_f32_e32 v110, v110, v110
	v_max_f32_e32 v111, v111, v111
	v_max_f32_e32 v112, v112, v112
	v_max_f32_e32 v113, v113, v113
	v_max_f32_e32 v114, v114, v114
	v_max_f32_e32 v115, v115, v115
	v_med3_f32 v100, v100, s20, v129
	v_med3_f32 v101, v101, s20, v129
	v_med3_f32 v102, v102, s20, v129
	v_med3_f32 v103, v103, s20, v129
	v_med3_f32 v104, v104, s20, v129
	v_med3_f32 v105, v105, s20, v129
	v_med3_f32 v106, v106, s20, v129
	v_med3_f32 v107, v107, s20, v129
	v_med3_f32 v108, v108, s20, v129
	v_med3_f32 v109, v109, s20, v129
	v_med3_f32 v110, v110, s20, v129
	v_med3_f32 v111, v111, s20, v129
	v_med3_f32 v112, v112, s20, v129
	v_med3_f32 v113, v113, s20, v129
	v_med3_f32 v114, v114, s20, v129
	v_med3_f32 v115, v115, s20, v129
	v_mov_b32_e32 v116, 0
	v_mov_b32_e32 v117, 0
	v_mov_b32_e32 v118, 0
	v_mov_b32_e32 v119, 0
	v_cvt_pk_fp8_f32 v116, v100, v101
	v_cvt_pk_fp8_f32 v117, v104, v105
	v_cvt_pk_fp8_f32 v118, v108, v109
	v_cvt_pk_fp8_f32 v119, v112, v113
	v_cvt_pk_fp8_f32 v116, v102, v103 op_sel:[0,0,1]
	v_cvt_pk_fp8_f32 v117, v106, v107 op_sel:[0,0,1]
	v_cvt_pk_fp8_f32 v118, v110, v111 op_sel:[0,0,1]
	v_cvt_pk_fp8_f32 v119, v114, v115 op_sel:[0,0,1]
	s_nop 0
	global_store_dwordx4 v127, v[116:119], s[14:15]
	ds_read_b32 v100, v124
	ds_read_b32 v101, v124 offset:512
	ds_read_b32 v102, v124 offset:1024
	ds_read_b32 v103, v124 offset:1536
	ds_read_b32 v104, v124 offset:2048
	ds_read_b32 v105, v124 offset:2560
	ds_read_b32 v106, v124 offset:3072
	ds_read_b32 v107, v124 offset:3584
	ds_read_b32 v108, v124 offset:4096
	ds_read_b32 v109, v124 offset:4608
	ds_read_b32 v110, v124 offset:5120
	ds_read_b32 v111, v124 offset:5632
	ds_read_b32 v112, v124 offset:6144
	ds_read_b32 v113, v124 offset:6656
	ds_read_b32 v114, v124 offset:7168
	ds_read_b32 v115, v124 offset:7680
	s_waitcnt lgkmcnt(0)
	v_max_f32_e32 v100, v100, v100
	v_max_f32_e32 v101, v101, v101
	v_max_f32_e32 v102, v102, v102
	v_max_f32_e32 v103, v103, v103
	v_max_f32_e32 v104, v104, v104
	v_max_f32_e32 v105, v105, v105
	v_max_f32_e32 v106, v106, v106
	v_max_f32_e32 v107, v107, v107
	v_max_f32_e32 v108, v108, v108
	v_max_f32_e32 v109, v109, v109
	v_max_f32_e32 v110, v110, v110
	v_max_f32_e32 v111, v111, v111
	v_max_f32_e32 v112, v112, v112
	v_max_f32_e32 v113, v113, v113
	v_max_f32_e32 v114, v114, v114
	v_max_f32_e32 v115, v115, v115
	v_med3_f32 v100, v100, s20, v129
	v_med3_f32 v101, v101, s20, v129
	v_med3_f32 v102, v102, s20, v129
	v_med3_f32 v103, v103, s20, v129
	v_med3_f32 v104, v104, s20, v129
	v_med3_f32 v105, v105, s20, v129
	v_med3_f32 v106, v106, s20, v129
	v_med3_f32 v107, v107, s20, v129
	v_med3_f32 v108, v108, s20, v129
	v_med3_f32 v109, v109, s20, v129
	v_med3_f32 v110, v110, s20, v129
	v_med3_f32 v111, v111, s20, v129
	v_med3_f32 v112, v112, s20, v129
	v_med3_f32 v113, v113, s20, v129
	v_med3_f32 v114, v114, s20, v129
	v_med3_f32 v115, v115, s20, v129
	v_mov_b32_e32 v116, 0
	v_mov_b32_e32 v117, 0
	v_mov_b32_e32 v118, 0
	v_mov_b32_e32 v119, 0
	v_cvt_pk_fp8_f32 v116, v100, v101
	v_cvt_pk_fp8_f32 v117, v104, v105
	v_cvt_pk_fp8_f32 v118, v108, v109
	v_cvt_pk_fp8_f32 v119, v112, v113
	v_cvt_pk_fp8_f32 v116, v102, v103 op_sel:[0,0,1]
	v_cvt_pk_fp8_f32 v117, v106, v107 op_sel:[0,0,1]
	v_cvt_pk_fp8_f32 v118, v110, v111 op_sel:[0,0,1]
	v_cvt_pk_fp8_f32 v119, v114, v115 op_sel:[0,0,1]
	s_nop 0
	global_store_dwordx4 v128, v[116:119], s[14:15]
	s_waitcnt vmcnt(12)
	v_mul_f32_e32 v68, 0x43000000, v68
	v_mul_f32_e32 v69, 0x43000000, v69
	v_mul_f32_e32 v70, 0x43000000, v70
	v_mul_f32_e32 v71, 0x43000000, v71
	ds_write_b128 v121, v[68:71]
	v_mul_f32_e32 v72, 0x43000000, v72
	v_mul_f32_e32 v73, 0x43000000, v73
	v_mul_f32_e32 v74, 0x43000000, v74
	v_mul_f32_e32 v75, 0x43000000, v75
	ds_write_b128 v121, v[72:75] offset:1024
	v_mul_f32_e32 v76, 0x43000000, v76
	v_mul_f32_e32 v77, 0x43000000, v77
	v_mul_f32_e32 v78, 0x43000000, v78
	v_mul_f32_e32 v79, 0x43000000, v79
	ds_write_b128 v121, v[76:79] offset:2048
	v_mul_f32_e32 v80, 0x43000000, v80
	v_mul_f32_e32 v81, 0x43000000, v81
	v_mul_f32_e32 v82, 0x43000000, v82
	v_mul_f32_e32 v83, 0x43000000, v83
	ds_write_b128 v121, v[80:83] offset:3072
	v_mul_f32_e32 v84, 0x43000000, v84
	v_mul_f32_e32 v85, 0x43000000, v85
	v_mul_f32_e32 v86, 0x43000000, v86
	v_mul_f32_e32 v87, 0x43000000, v87
	ds_write_b128 v121, v[84:87] offset:4096
	v_mul_f32_e32 v88, 0x43000000, v88
	v_mul_f32_e32 v89, 0x43000000, v89
	v_mul_f32_e32 v90, 0x43000000, v90
	v_mul_f32_e32 v91, 0x43000000, v91
	ds_write_b128 v121, v[88:91] offset:5120
	v_mul_f32_e32 v92, 0x43000000, v92
	v_mul_f32_e32 v93, 0x43000000, v93
	v_mul_f32_e32 v94, 0x43000000, v94
	v_mul_f32_e32 v95, 0x43000000, v95
	ds_write_b128 v121, v[92:95] offset:6144
	v_mul_f32_e32 v96, 0x43000000, v96
	v_mul_f32_e32 v97, 0x43000000, v97
	v_mul_f32_e32 v98, 0x43000000, v98
	v_mul_f32_e32 v99, 0x43000000, v99
	ds_write_b128 v121, v[96:99] offset:7168
	s_waitcnt lgkmcnt(0)
	s_barrier
; #define GAS __attribute__((address_space(1)))
; #define LAS __attribute__((address_space(3)))
; #define LDS_WAIT() asm volatile("s_waitcnt lgkmcnt(0)" ::: "memory")
; __device__ __forceinline__ unsigned pk4_fp8(float a, float b, float c, float d) {
;     a = fminf(fmaxf(a, -448.f), 448.f); b = fminf(fmaxf(b, -448.f), 448.f); c = fminf(fmaxf(c, -448.f), 448.f); d = fminf(fmaxf(d, -448.f), 448.f);
;     int w = __builtin_amdgcn_cvt_pk_fp8_f32(a, b, 0, false); w = __builtin_amdgcn_cvt_pk_fp8_f32(c, d, w, true); return (unsigned)w; }
;     const int pr = item >> 1, kb = 2 * (pr / nblk) + (item & 1), nb = pr % nblk, k0 = 64 * kb, n0 = 32 * nb;
;     const int nr = n0 + (lane & 31); const int sc = MAP == 1 ? src_col_in(nr) : nr;
;     float v[32];
; #pragma unroll
;     for (int i = 0; i < 32; ++i) v[i] = sc >= 0 ? W[(size_t)(k0 + 2 * i + (lane >> 5)) * Nsrc + sc] : 0.f;
; #pragma unroll
;     for (int i = 0; i < 32; ++i) { const int k = k0 + 2 * i + (lane >> 5); float x = v[i] * wscale; if (KS) x *= (k < ksplit ? ksA[k] : ksB[k - ksplit]); scr[(2 * i + (lane >> 5)) * 33 + (lane & 31)] = x; }
;     LDS_WAIT(); asm volatile("" ::: "memory");
;     const int c = lane & 7;
; #pragma unroll
;     for (int j = 0; j < 4; ++j) { const int n = (lane >> 3) + 8 * j; const LAS float* s = scr + (8 * c) * 33 + n;
;         const unsigned long long o = (unsigned long long)pg8::pk4_fp8(s[0 * 33], s[1 * 33], s[2 * 33], s[3 * 33]) | ((unsigned long long)pg8::pk4_fp8(s[4 * 33], s[5 * 33], s[6 * 33], s[7 * 33]) << 32);
;         *(GAS unsigned long long*)(WT + (size_t)(n0 + n) * K + k0 + 8 * c) = o; }
;     LDS_WAIT(); asm volatile("" ::: "memory");
; }
	s_add_i32 s17, s16, 1824
	s_min_u32 s17, s17, 0xbff
	s_lshr_b32 s18, s17, 5
	s_add_i32 s18, s18, 32
	s_and_b32 s19, s17, 31
	s_lshl_b32 s18, s18, 21
	s_lshl_b32 s19, s19, 9
	s_add_u32 s18, s18, s19
	s_add_u32 s12, s2, s18
	s_addc_u32 s13, s3, 0
	global_load_dwordx4 v[68:71], v126, s[12:13]
	s_add_u32 s12, s12, 0x8000
	s_addc_u32 s13, s13, 0
	global_load_dwordx4 v[72:75], v126, s[12:13]
	s_add_u32 s12, s12, 0x8000
	s_addc_u32 s13, s13, 0
	global_load_dwordx4 v[76:79], v126, s[12:13]
	s_add_u32 s12, s12, 0x8000
	s_addc_u32 s13, s13, 0
	global_load_dwordx4 v[80:83], v126, s[12:13]
	s_add_u32 s12, s12, 0x8000
	s_addc_u32 s13, s13, 0
	global_load_dwordx4 v[84:87], v126, s[12:13]
	s_add_u32 s12, s12, 0x8000
	s_addc_u32 s13, s13, 0
	global_load_dwordx4 v[88:91], v126, s[12:13]
	s_add_u32 s12, s12, 0x8000
	s_addc_u32 s13, s13, 0
	global_load_dwordx4 v[92:95], v126, s[12:13]
	s_add_u32 s12, s12, 0x8000
	s_addc_u32 s13, s13, 0
	global_load_dwordx4 v[96:99], v126, s[12:13]
	s_add_i32 s17, s16, 1632
	s_min_u32 s17, s17, 0xbff
	s_lshr_b32 s18, s17, 5
	s_add_i32 s18, s18, 32
	s_and_b32 s19, s17, 31
	s_lshl_b32 s19, s19, 21
	s_lshl_b32 s18, s18, 7
	s_add_u32 s18, s18, s19
	s_add_u32 s14, s4, s18
	s_addc_u32 s15, s5, 0
	ds_read_b32 v100, v123
	ds_read_b32 v101, v123 offset:512
	ds_read_b32 v102, v123 offset:1024
	ds_read_b32 v103, v123 offset:1536
	ds_read_b32 v104, v123 offset:2048
	ds_read_b32 v105, v123 offset:2560
	ds_read_b32 v106, v123 offset:3072
	ds_read_b32 v107, v123 offset:3584
	ds_read_b32 v108, v123 offset:4096
	ds_read_b32 v109, v123 offset:4608
	ds_read_b32 v110, v123 offset:5120
	ds_read_b32 v111, v123 offset:5632
	ds_read_b32 v112, v123 offset:6144
	ds_read_b32 v113, v123 offset:6656
	ds_read_b32 v114, v123 offset:7168
	ds_read_b32 v115, v123 offset:7680
	s_waitcnt lgkmcnt(0)
	v_max_f32_e32 v100, v100, v100
	v_max_f32_e32 v101, v101, v101
	v_max_f32_e32 v102, v102, v102
	v_max_f32_e32 v103, v103, v103
	v_max_f32_e32 v104, v104, v104
	v_max_f32_e32 v105, v105, v105
	v_max_f32_e32 v106, v106, v106
	v_max_f32_e32 v107, v107, v107
	v_max_f32_e32 v108, v108, v108
	v_max_f32_e32 v109, v109, v109
	v_max_f32_e32 v110, v110, v110
	v_max_f32_e32 v111, v111, v111
	v_max_f32_e32 v112, v112, v112
	v_max_f32_e32 v113, v113, v113
	v_max_f32_e32 v114, v114, v114
	v_max_f32_e32 v115, v115, v115
	v_med3_f32 v100, v100, s20, v129
	v_med3_f32 v101, v101, s20, v129
	v_med3_f32 v102, v102, s20, v129
	v_med3_f32 v103, v103, s20, v129
	v_med3_f32 v104, v104, s20, v129
	v_med3_f32 v105, v105, s20, v129
	v_med3_f32 v106, v106, s20, v129
	v_med3_f32 v107, v107, s20, v129
	v_med3_f32 v108, v108, s20, v129
	v_med3_f32 v109, v109, s20, v129
	v_med3_f32 v110, v110, s20, v129
	v_med3_f32 v111, v111, s20, v129
	v_med3_f32 v112, v112, s20, v129
	v_med3_f32 v113, v113, s20, v129
	v_med3_f32 v114, v114, s20, v129
	v_med3_f32 v115, v115, s20, v129
	v_mov_b32_e32 v116, 0
	v_mov_b32_e32 v117, 0
	v_mov_b32_e32 v118, 0
	v_mov_b32_e32 v119, 0
	v_cvt_pk_fp8_f32 v116, v100, v101
	v_cvt_pk_fp8_f32 v117, v104, v105
	v_cvt_pk_fp8_f32 v118, v108, v109
	v_cvt_pk_fp8_f32 v119, v112, v113
	v_cvt_pk_fp8_f32 v116, v102, v103 op_sel:[0,0,1]
	v_cvt_pk_fp8_f32 v117, v106, v107 op_sel:[0,0,1]
	v_cvt_pk_fp8_f32 v118, v110, v111 op_sel:[0,0,1]
	v_cvt_pk_fp8_f32 v119, v114, v115 op_sel:[0,0,1]
	s_nop 0
	global_store_dwordx4 v127, v[116:119], s[14:15]
	ds_read_b32 v100, v125
	ds_read_b32 v101, v125 offset:512
	ds_read_b32 v102, v125 offset:1024
	ds_read_b32 v103, v125 offset:1536
	ds_read_b32 v104, v125 offset:2048
	ds_read_b32 v105, v125 offset:2560
	ds_read_b32 v106, v125 offset:3072
	ds_read_b32 v107, v125 offset:3584
	ds_read_b32 v108, v125 offset:4096
	ds_read_b32 v109, v125 offset:4608
	ds_read_b32 v110, v125 offset:5120
	ds_read_b32 v111, v125 offset:5632
	ds_read_b32 v112, v125 offset:6144
	ds_read_b32 v113, v125 offset:6656
	ds_read_b32 v114, v125 offset:7168
	ds_read_b32 v115, v125 offset:7680
	s_waitcnt lgkmcnt(0)
	v_max_f32_e32 v100, v100, v100
	v_max_f32_e32 v101, v101, v101
	v_max_f32_e32 v102, v102, v102
	v_max_f32_e32 v103, v103, v103
	v_max_f32_e32 v104, v104, v104
	v_max_f32_e32 v105, v105, v105
	v_max_f32_e32 v106, v106, v106
	v_max_f32_e32 v107, v107, v107
	v_max_f32_e32 v108, v108, v108
	v_max_f32_e32 v109, v109, v109
	v_max_f32_e32 v110, v110, v110
	v_max_f32_e32 v111, v111, v111
	v_max_f32_e32 v112, v112, v112
	v_max_f32_e32 v113, v113, v113
	v_max_f32_e32 v114, v114, v114
	v_max_f32_e32 v115, v115, v115
	v_med3_f32 v100, v100, s20, v129
	v_med3_f32 v101, v101, s20, v129
	v_med3_f32 v102, v102, s20, v129
	v_med3_f32 v103, v103, s20, v129
	v_med3_f32 v104, v104, s20, v129
	v_med3_f32 v105, v105, s20, v129
	v_med3_f32 v106, v106, s20, v129
	v_med3_f32 v107, v107, s20, v129
	v_med3_f32 v108, v108, s20, v129
	v_med3_f32 v109, v109, s20, v129
	v_med3_f32 v110, v110, s20, v129
	v_med3_f32 v111, v111, s20, v129
	v_med3_f32 v112, v112, s20, v129
	v_med3_f32 v113, v113, s20, v129
	v_med3_f32 v114, v114, s20, v129
	v_med3_f32 v115, v115, s20, v129
	v_mov_b32_e32 v116, 0
	v_mov_b32_e32 v117, 0
	v_mov_b32_e32 v118, 0
	v_mov_b32_e32 v119, 0
	v_cvt_pk_fp8_f32 v116, v100, v101
	v_cvt_pk_fp8_f32 v117, v104, v105
	v_cvt_pk_fp8_f32 v118, v108, v109
	v_cvt_pk_fp8_f32 v119, v112, v113
	v_cvt_pk_fp8_f32 v116, v102, v103 op_sel:[0,0,1]
	v_cvt_pk_fp8_f32 v117, v106, v107 op_sel:[0,0,1]
	v_cvt_pk_fp8_f32 v118, v110, v111 op_sel:[0,0,1]
	v_cvt_pk_fp8_f32 v119, v114, v115 op_sel:[0,0,1]
	s_nop 0
	global_store_dwordx4 v128, v[116:119], s[14:15]
	s_waitcnt vmcnt(12)
	v_mul_f32_e32 v36, 0x43000000, v36
	v_mul_f32_e32 v37, 0x43000000, v37
	v_mul_f32_e32 v38, 0x43000000, v38
	v_mul_f32_e32 v39, 0x43000000, v39
	ds_write_b128 v120, v[36:39]
	v_mul_f32_e32 v40, 0x43000000, v40
	v_mul_f32_e32 v41, 0x43000000, v41
	v_mul_f32_e32 v42, 0x43000000, v42
	v_mul_f32_e32 v43, 0x43000000, v43
	ds_write_b128 v120, v[40:43] offset:1024
	v_mul_f32_e32 v44, 0x43000000, v44
	v_mul_f32_e32 v45, 0x43000000, v45
	v_mul_f32_e32 v46, 0x43000000, v46
	v_mul_f32_e32 v47, 0x43000000, v47
	ds_write_b128 v120, v[44:47] offset:2048
	v_mul_f32_e32 v48, 0x43000000, v48
	v_mul_f32_e32 v49, 0x43000000, v49
	v_mul_f32_e32 v50, 0x43000000, v50
	v_mul_f32_e32 v51, 0x43000000, v51
	ds_write_b128 v120, v[48:51] offset:3072
	v_mul_f32_e32 v52, 0x43000000, v52
	v_mul_f32_e32 v53, 0x43000000, v53
	v_mul_f32_e32 v54, 0x43000000, v54
	v_mul_f32_e32 v55, 0x43000000, v55
	ds_write_b128 v120, v[52:55] offset:4096
	v_mul_f32_e32 v56, 0x43000000, v56
	v_mul_f32_e32 v57, 0x43000000, v57
	v_mul_f32_e32 v58, 0x43000000, v58
	v_mul_f32_e32 v59, 0x43000000, v59
	ds_write_b128 v120, v[56:59] offset:5120
	v_mul_f32_e32 v60, 0x43000000, v60
	v_mul_f32_e32 v61, 0x43000000, v61
	v_mul_f32_e32 v62, 0x43000000, v62
	v_mul_f32_e32 v63, 0x43000000, v63
	ds_write_b128 v120, v[60:63] offset:6144
	v_mul_f32_e32 v64, 0x43000000, v64
	v_mul_f32_e32 v65, 0x43000000, v65
	v_mul_f32_e32 v66, 0x43000000, v66
	v_mul_f32_e32 v67, 0x43000000, v67
	ds_write_b128 v120, v[64:67] offset:7168
	s_waitcnt lgkmcnt(0)
	s_barrier
; #define GAS __attribute__((address_space(1)))
; #define LAS __attribute__((address_space(3)))
; #define LDS_WAIT() asm volatile("s_waitcnt lgkmcnt(0)" ::: "memory")
; __device__ __forceinline__ unsigned pk4_fp8(float a, float b, float c, float d) {
;     a = fminf(fmaxf(a, -448.f), 448.f); b = fminf(fmaxf(b, -448.f), 448.f); c = fminf(fmaxf(c, -448.f), 448.f); d = fminf(fmaxf(d, -448.f), 448.f);
;     int w = __builtin_amdgcn_cvt_pk_fp8_f32(a, b, 0, false); w = __builtin_amdgcn_cvt_pk_fp8_f32(c, d, w, true); return (unsigned)w; }
;     const int pr = item >> 1, kb = 2 * (pr / nblk) + (item & 1), nb = pr % nblk, k0 = 64 * kb, n0 = 32 * nb;
;     const int nr = n0 + (lane & 31); const int sc = MAP == 1 ? src_col_in(nr) : nr;
;     float v[32];
; #pragma unroll
;     for (int i = 0; i < 32; ++i) v[i] = sc >= 0 ? W[(size_t)(k0 + 2 * i + (lane >> 5)) * Nsrc + sc] : 0.f;
; #pragma unroll
;     for (int i = 0; i < 32; ++i) { const int k = k0 + 2 * i + (lane >> 5); float x = v[i] * wscale; if (KS) x *= (k < ksplit ? ksA[k] : ksB[k - ksplit]); scr[(2 * i + (lane >> 5)) * 33 + (lane & 31)] = x; }
;     LDS_WAIT(); asm volatile("" ::: "memory");
;     const int c = lane & 7;
; #pragma unroll
;     for (int j = 0; j < 4; ++j) { const int n = (lane >> 3) + 8 * j; const LAS float* s = scr + (8 * c) * 33 + n;
;         const unsigned long long o = (unsigned long long)pg8::pk4_fp8(s[0 * 33], s[1 * 33], s[2 * 33], s[3 * 33]) | ((unsigned long long)pg8::pk4_fp8(s[4 * 33], s[5 * 33], s[6 * 33], s[7 * 33]) << 32);
;         *(GAS unsigned long long*)(WT + (size_t)(n0 + n) * K + k0 + 8 * c) = o; }
;     LDS_WAIT(); asm volatile("" ::: "memory");
; }
	s_add_i32 s17, s16, 1920
	s_min_u32 s17, s17, 0xbff
	s_lshr_b32 s18, s17, 5
	s_add_i32 s18, s18, 32
	s_and_b32 s19, s17, 31
	s_lshl_b32 s18, s18, 21
	s_lshl_b32 s19, s19, 9
	s_add_u32 s18, s18, s19
	s_add_u32 s12, s2, s18
	s_addc_u32 s13, s3, 0
	global_load_dwordx4 v[36:39], v126, s[12:13]
	s_add_u32 s12, s12, 0x8000
	s_addc_u32 s13, s13, 0
	global_load_dwordx4 v[40:43], v126, s[12:13]
	s_add_u32 s12, s12, 0x8000
	s_addc_u32 s13, s13, 0
	global_load_dwordx4 v[44:47], v126, s[12:13]
	s_add_u32 s12, s12, 0x8000
	s_addc_u32 s13, s13, 0
	global_load_dwordx4 v[48:51], v126, s[12:13]
	s_add_u32 s12, s12, 0x8000
	s_addc_u32 s13, s13, 0
	global_load_dwordx4 v[52:55], v126, s[12:13]
	s_add_u32 s12, s12, 0x8000
	s_addc_u32 s13, s13, 0
	global_load_dwordx4 v[56:59], v126, s[12:13]
	s_add_u32 s12, s12, 0x8000
	s_addc_u32 s13, s13, 0
	global_load_dwordx4 v[60:63], v126, s[12:13]
	s_add_u32 s12, s12, 0x8000
	s_addc_u32 s13, s13, 0
	global_load_dwordx4 v[64:67], v126, s[12:13]
	s_add_i32 s17, s16, 1728
	s_min_u32 s17, s17, 0xbff
	s_lshr_b32 s18, s17, 5
	s_add_i32 s18, s18, 32
	s_and_b32 s19, s17, 31
	s_lshl_b32 s19, s19, 21
	s_lshl_b32 s18, s18, 7
	s_add_u32 s18, s18, s19
	s_add_u32 s14, s4, s18
	s_addc_u32 s15, s5, 0
	ds_read_b32 v100, v122
	ds_read_b32 v101, v122 offset:512
	ds_read_b32 v102, v122 offset:1024
	ds_read_b32 v103, v122 offset:1536
	ds_read_b32 v104, v122 offset:2048
	ds_read_b32 v105, v122 offset:2560
	ds_read_b32 v106, v122 offset:3072
	ds_read_b32 v107, v122 offset:3584
	ds_read_b32 v108, v122 offset:4096
	ds_read_b32 v109, v122 offset:4608
	ds_read_b32 v110, v122 offset:5120
	ds_read_b32 v111, v122 offset:5632
	ds_read_b32 v112, v122 offset:6144
	ds_read_b32 v113, v122 offset:6656
	ds_read_b32 v114, v122 offset:7168
	ds_read_b32 v115, v122 offset:7680
	s_waitcnt lgkmcnt(0)
	v_max_f32_e32 v100, v100, v100
	v_max_f32_e32 v101, v101, v101
	v_max_f32_e32 v102, v102, v102
	v_max_f32_e32 v103, v103, v103
	v_max_f32_e32 v104, v104, v104
	v_max_f32_e32 v105, v105, v105
	v_max_f32_e32 v106, v106, v106
	v_max_f32_e32 v107, v107, v107
	v_max_f32_e32 v108, v108, v108
	v_max_f32_e32 v109, v109, v109
	v_max_f32_e32 v110, v110, v110
	v_max_f32_e32 v111, v111, v111
	v_max_f32_e32 v112, v112, v112
	v_max_f32_e32 v113, v113, v113
	v_max_f32_e32 v114, v114, v114
	v_max_f32_e32 v115, v115, v115
	v_med3_f32 v100, v100, s20, v129
	v_med3_f32 v101, v101, s20, v129
	v_med3_f32 v102, v102, s20, v129
	v_med3_f32 v103, v103, s20, v129
	v_med3_f32 v104, v104, s20, v129
	v_med3_f32 v105, v105, s20, v129
	v_med3_f32 v106, v106, s20, v129
	v_med3_f32 v107, v107, s20, v129
	v_med3_f32 v108, v108, s20, v129
	v_med3_f32 v109, v109, s20, v129
	v_med3_f32 v110, v110, s20, v129
	v_med3_f32 v111, v111, s20, v129
	v_med3_f32 v112, v112, s20, v129
	v_med3_f32 v113, v113, s20, v129
	v_med3_f32 v114, v114, s20, v129
	v_med3_f32 v115, v115, s20, v129
	v_mov_b32_e32 v116, 0
	v_mov_b32_e32 v117, 0
	v_mov_b32_e32 v118, 0
	v_mov_b32_e32 v119, 0
	v_cvt_pk_fp8_f32 v116, v100, v101
	v_cvt_pk_fp8_f32 v117, v104, v105
	v_cvt_pk_fp8_f32 v118, v108, v109
	v_cvt_pk_fp8_f32 v119, v112, v113
	v_cvt_pk_fp8_f32 v116, v102, v103 op_sel:[0,0,1]
	v_cvt_pk_fp8_f32 v117, v106, v107 op_sel:[0,0,1]
	v_cvt_pk_fp8_f32 v118, v110, v111 op_sel:[0,0,1]
	v_cvt_pk_fp8_f32 v119, v114, v115 op_sel:[0,0,1]
	s_nop 0
	global_store_dwordx4 v127, v[116:119], s[14:15]
	ds_read_b32 v100, v124
	ds_read_b32 v101, v124 offset:512
	ds_read_b32 v102, v124 offset:1024
	ds_read_b32 v103, v124 offset:1536
	ds_read_b32 v104, v124 offset:2048
	ds_read_b32 v105, v124 offset:2560
	ds_read_b32 v106, v124 offset:3072
	ds_read_b32 v107, v124 offset:3584
	ds_read_b32 v108, v124 offset:4096
	ds_read_b32 v109, v124 offset:4608
	ds_read_b32 v110, v124 offset:5120
	ds_read_b32 v111, v124 offset:5632
	ds_read_b32 v112, v124 offset:6144
	ds_read_b32 v113, v124 offset:6656
	ds_read_b32 v114, v124 offset:7168
	ds_read_b32 v115, v124 offset:7680
	s_waitcnt lgkmcnt(0)
	v_max_f32_e32 v100, v100, v100
	v_max_f32_e32 v101, v101, v101
	v_max_f32_e32 v102, v102, v102
	v_max_f32_e32 v103, v103, v103
	v_max_f32_e32 v104, v104, v104
	v_max_f32_e32 v105, v105, v105
	v_max_f32_e32 v106, v106, v106
	v_max_f32_e32 v107, v107, v107
	v_max_f32_e32 v108, v108, v108
	v_max_f32_e32 v109, v109, v109
	v_max_f32_e32 v110, v110, v110
	v_max_f32_e32 v111, v111, v111
	v_max_f32_e32 v112, v112, v112
	v_max_f32_e32 v113, v113, v113
	v_max_f32_e32 v114, v114, v114
	v_max_f32_e32 v115, v115, v115
	v_med3_f32 v100, v100, s20, v129
	v_med3_f32 v101, v101, s20, v129
	v_med3_f32 v102, v102, s20, v129
	v_med3_f32 v103, v103, s20, v129
	v_med3_f32 v104, v104, s20, v129
	v_med3_f32 v105, v105, s20, v129
	v_med3_f32 v106, v106, s20, v129
	v_med3_f32 v107, v107, s20, v129
	v_med3_f32 v108, v108, s20, v129
	v_med3_f32 v109, v109, s20, v129
	v_med3_f32 v110, v110, s20, v129
	v_med3_f32 v111, v111, s20, v129
	v_med3_f32 v112, v112, s20, v129
	v_med3_f32 v113, v113, s20, v129
	v_med3_f32 v114, v114, s20, v129
	v_med3_f32 v115, v115, s20, v129
	v_mov_b32_e32 v116, 0
	v_mov_b32_e32 v117, 0
	v_mov_b32_e32 v118, 0
	v_mov_b32_e32 v119, 0
	v_cvt_pk_fp8_f32 v116, v100, v101
	v_cvt_pk_fp8_f32 v117, v104, v105
	v_cvt_pk_fp8_f32 v118, v108, v109
	v_cvt_pk_fp8_f32 v119, v112, v113
	v_cvt_pk_fp8_f32 v116, v102, v103 op_sel:[0,0,1]
	v_cvt_pk_fp8_f32 v117, v106, v107 op_sel:[0,0,1]
	v_cvt_pk_fp8_f32 v118, v110, v111 op_sel:[0,0,1]
	v_cvt_pk_fp8_f32 v119, v114, v115 op_sel:[0,0,1]
	s_nop 0
	global_store_dwordx4 v128, v[116:119], s[14:15]
	s_waitcnt vmcnt(12)
	v_mul_f32_e32 v68, 0x43000000, v68
	v_mul_f32_e32 v69, 0x43000000, v69
	v_mul_f32_e32 v70, 0x43000000, v70
	v_mul_f32_e32 v71, 0x43000000, v71
	ds_write_b128 v121, v[68:71]
	v_mul_f32_e32 v72, 0x43000000, v72
	v_mul_f32_e32 v73, 0x43000000, v73
	v_mul_f32_e32 v74, 0x43000000, v74
	v_mul_f32_e32 v75, 0x43000000, v75
	ds_write_b128 v121, v[72:75] offset:1024
	v_mul_f32_e32 v76, 0x43000000, v76
	v_mul_f32_e32 v77, 0x43000000, v77
	v_mul_f32_e32 v78, 0x43000000, v78
	v_mul_f32_e32 v79, 0x43000000, v79
	ds_write_b128 v121, v[76:79] offset:2048
	v_mul_f32_e32 v80, 0x43000000, v80
	v_mul_f32_e32 v81, 0x43000000, v81
	v_mul_f32_e32 v82, 0x43000000, v82
	v_mul_f32_e32 v83, 0x43000000, v83
	ds_write_b128 v121, v[80:83] offset:3072
	v_mul_f32_e32 v84, 0x43000000, v84
	v_mul_f32_e32 v85, 0x43000000, v85
	v_mul_f32_e32 v86, 0x43000000, v86
	v_mul_f32_e32 v87, 0x43000000, v87
	ds_write_b128 v121, v[84:87] offset:4096
	v_mul_f32_e32 v88, 0x43000000, v88
	v_mul_f32_e32 v89, 0x43000000, v89
	v_mul_f32_e32 v90, 0x43000000, v90
	v_mul_f32_e32 v91, 0x43000000, v91
	ds_write_b128 v121, v[88:91] offset:5120
	v_mul_f32_e32 v92, 0x43000000, v92
	v_mul_f32_e32 v93, 0x43000000, v93
	v_mul_f32_e32 v94, 0x43000000, v94
	v_mul_f32_e32 v95, 0x43000000, v95
	ds_write_b128 v121, v[92:95] offset:6144
	v_mul_f32_e32 v96, 0x43000000, v96
	v_mul_f32_e32 v97, 0x43000000, v97
	v_mul_f32_e32 v98, 0x43000000, v98
	v_mul_f32_e32 v99, 0x43000000, v99
	ds_write_b128 v121, v[96:99] offset:7168
	s_waitcnt lgkmcnt(0)
	s_barrier
; #define GAS __attribute__((address_space(1)))
; #define LAS __attribute__((address_space(3)))
; #define LDS_WAIT() asm volatile("s_waitcnt lgkmcnt(0)" ::: "memory")
; __device__ __forceinline__ unsigned pk4_fp8(float a, float b, float c, float d) {
;     a = fminf(fmaxf(a, -448.f), 448.f); b = fminf(fmaxf(b, -448.f), 448.f); c = fminf(fmaxf(c, -448.f), 448.f); d = fminf(fmaxf(d, -448.f), 448.f);
;     int w = __builtin_amdgcn_cvt_pk_fp8_f32(a, b, 0, false); w = __builtin_amdgcn_cvt_pk_fp8_f32(c, d, w, true); return (unsigned)w; }
;     const int pr = item >> 1, kb = 2 * (pr / nblk) + (item & 1), nb = pr % nblk, k0 = 64 * kb, n0 = 32 * nb;
;     const int nr = n0 + (lane & 31); const int sc = MAP == 1 ? src_col_in(nr) : nr;
;     float v[32];
; #pragma unroll
;     for (int i = 0; i < 32; ++i) v[i] = sc >= 0 ? W[(size_t)(k0 + 2 * i + (lane >> 5)) * Nsrc + sc] : 0.f;
; #pragma unroll
;     for (int i = 0; i < 32; ++i) { const int k = k0 + 2 * i + (lane >> 5); float x = v[i] * wscale; if (KS) x *= (k < ksplit ? ksA[k] : ksB[k - ksplit]); scr[(2 * i + (lane >> 5)) * 33 + (lane & 31)] = x; }
;     LDS_WAIT(); asm volatile("" ::: "memory");
;     const int c = lane & 7;
; #pragma unroll
;     for (int j = 0; j < 4; ++j) { const int n = (lane >> 3) + 8 * j; const LAS float* s = scr + (8 * c) * 33 + n;
;         const unsigned long long o = (unsigned long long)pg8::pk4_fp8(s[0 * 33], s[1 * 33], s[2 * 33], s[3 * 33]) | ((unsigned long long)pg8::pk4_fp8(s[4 * 33], s[5 * 33], s[6 * 33], s[7 * 33]) << 32);
;         *(GAS unsigned long long*)(WT + (size_t)(n0 + n) * K + k0 + 8 * c) = o; }
;     LDS_WAIT(); asm volatile("" ::: "memory");
; }
	s_add_i32 s17, s16, 2016
	s_min_u32 s17, s17, 0xbff
	s_lshr_b32 s18, s17, 5
	s_add_i32 s18, s18, 32
	s_and_b32 s19, s17, 31
	s_lshl_b32 s18, s18, 21
	s_lshl_b32 s19, s19, 9
	s_add_u32 s18, s18, s19
	s_add_u32 s12, s2, s18
	s_addc_u32 s13, s3, 0
	global_load_dwordx4 v[68:71], v126, s[12:13]
	s_add_u32 s12, s12, 0x8000
	s_addc_u32 s13, s13, 0
	global_load_dwordx4 v[72:75], v126, s[12:13]
	s_add_u32 s12, s12, 0x8000
	s_addc_u32 s13, s13, 0
	global_load_dwordx4 v[76:79], v126, s[12:13]
	s_add_u32 s12, s12, 0x8000
	s_addc_u32 s13, s13, 0
	global_load_dwordx4 v[80:83], v126, s[12:13]
	s_add_u32 s12, s12, 0x8000
	s_addc_u32 s13, s13, 0
	global_load_dwordx4 v[84:87], v126, s[12:13]
	s_add_u32 s12, s12, 0x8000
	s_addc_u32 s13, s13, 0
	global_load_dwordx4 v[88:91], v126, s[12:13]
	s_add_u32 s12, s12, 0x8000
	s_addc_u32 s13, s13, 0
	global_load_dwordx4 v[92:95], v126, s[12:13]
	s_add_u32 s12, s12, 0x8000
	s_addc_u32 s13, s13, 0
	global_load_dwordx4 v[96:99], v126, s[12:13]
	s_add_i32 s17, s16, 1824
	s_min_u32 s17, s17, 0xbff
	s_lshr_b32 s18, s17, 5
	s_add_i32 s18, s18, 32
	s_and_b32 s19, s17, 31
	s_lshl_b32 s19, s19, 21
	s_lshl_b32 s18, s18, 7
	s_add_u32 s18, s18, s19
	s_add_u32 s14, s4, s18
	s_addc_u32 s15, s5, 0
	ds_read_b32 v100, v123
	ds_read_b32 v101, v123 offset:512
	ds_read_b32 v102, v123 offset:1024
	ds_read_b32 v103, v123 offset:1536
	ds_read_b32 v104, v123 offset:2048
	ds_read_b32 v105, v123 offset:2560
	ds_read_b32 v106, v123 offset:3072
	ds_read_b32 v107, v123 offset:3584
	ds_read_b32 v108, v123 offset:4096
	ds_read_b32 v109, v123 offset:4608
	ds_read_b32 v110, v123 offset:5120
	ds_read_b32 v111, v123 offset:5632
	ds_read_b32 v112, v123 offset:6144
	ds_read_b32 v113, v123 offset:6656
	ds_read_b32 v114, v123 offset:7168
	ds_read_b32 v115, v123 offset:7680
	s_waitcnt lgkmcnt(0)
	v_max_f32_e32 v100, v100, v100
	v_max_f32_e32 v101, v101, v101
	v_max_f32_e32 v102, v102, v102
	v_max_f32_e32 v103, v103, v103
	v_max_f32_e32 v104, v104, v104
	v_max_f32_e32 v105, v105, v105
	v_max_f32_e32 v106, v106, v106
	v_max_f32_e32 v107, v107, v107
	v_max_f32_e32 v108, v108, v108
	v_max_f32_e32 v109, v109, v109
	v_max_f32_e32 v110, v110, v110
	v_max_f32_e32 v111, v111, v111
	v_max_f32_e32 v112, v112, v112
	v_max_f32_e32 v113, v113, v113
	v_max_f32_e32 v114, v114, v114
	v_max_f32_e32 v115, v115, v115
	v_med3_f32 v100, v100, s20, v129
	v_med3_f32 v101, v101, s20, v129
	v_med3_f32 v102, v102, s20, v129
	v_med3_f32 v103, v103, s20, v129
	v_med3_f32 v104, v104, s20, v129
	v_med3_f32 v105, v105, s20, v129
	v_med3_f32 v106, v106, s20, v129
	v_med3_f32 v107, v107, s20, v129
	v_med3_f32 v108, v108, s20, v129
	v_med3_f32 v109, v109, s20, v129
	v_med3_f32 v110, v110, s20, v129
	v_med3_f32 v111, v111, s20, v129
	v_med3_f32 v112, v112, s20, v129
	v_med3_f32 v113, v113, s20, v129
	v_med3_f32 v114, v114, s20, v129
	v_med3_f32 v115, v115, s20, v129
	v_mov_b32_e32 v116, 0
	v_mov_b32_e32 v117, 0
	v_mov_b32_e32 v118, 0
	v_mov_b32_e32 v119, 0
	v_cvt_pk_fp8_f32 v116, v100, v101
	v_cvt_pk_fp8_f32 v117, v104, v105
	v_cvt_pk_fp8_f32 v118, v108, v109
	v_cvt_pk_fp8_f32 v119, v112, v113
	v_cvt_pk_fp8_f32 v116, v102, v103 op_sel:[0,0,1]
	v_cvt_pk_fp8_f32 v117, v106, v107 op_sel:[0,0,1]
	v_cvt_pk_fp8_f32 v118, v110, v111 op_sel:[0,0,1]
	v_cvt_pk_fp8_f32 v119, v114, v115 op_sel:[0,0,1]
	s_nop 0
	global_store_dwordx4 v127, v[116:119], s[14:15]
	ds_read_b32 v100, v125
	ds_read_b32 v101, v125 offset:512
	ds_read_b32 v102, v125 offset:1024
	ds_read_b32 v103, v125 offset:1536
	ds_read_b32 v104, v125 offset:2048
	ds_read_b32 v105, v125 offset:2560
	ds_read_b32 v106, v125 offset:3072
	ds_read_b32 v107, v125 offset:3584
	ds_read_b32 v108, v125 offset:4096
	ds_read_b32 v109, v125 offset:4608
	ds_read_b32 v110, v125 offset:5120
	ds_read_b32 v111, v125 offset:5632
	ds_read_b32 v112, v125 offset:6144
	ds_read_b32 v113, v125 offset:6656
	ds_read_b32 v114, v125 offset:7168
	ds_read_b32 v115, v125 offset:7680
	s_waitcnt lgkmcnt(0)
	v_max_f32_e32 v100, v100, v100
	v_max_f32_e32 v101, v101, v101
	v_max_f32_e32 v102, v102, v102
	v_max_f32_e32 v103, v103, v103
	v_max_f32_e32 v104, v104, v104
	v_max_f32_e32 v105, v105, v105
	v_max_f32_e32 v106, v106, v106
	v_max_f32_e32 v107, v107, v107
	v_max_f32_e32 v108, v108, v108
	v_max_f32_e32 v109, v109, v109
	v_max_f32_e32 v110, v110, v110
	v_max_f32_e32 v111, v111, v111
	v_max_f32_e32 v112, v112, v112
	v_max_f32_e32 v113, v113, v113
	v_max_f32_e32 v114, v114, v114
	v_max_f32_e32 v115, v115, v115
	v_med3_f32 v100, v100, s20, v129
	v_med3_f32 v101, v101, s20, v129
	v_med3_f32 v102, v102, s20, v129
	v_med3_f32 v103, v103, s20, v129
	v_med3_f32 v104, v104, s20, v129
	v_med3_f32 v105, v105, s20, v129
	v_med3_f32 v106, v106, s20, v129
	v_med3_f32 v107, v107, s20, v129
	v_med3_f32 v108, v108, s20, v129
	v_med3_f32 v109, v109, s20, v129
	v_med3_f32 v110, v110, s20, v129
	v_med3_f32 v111, v111, s20, v129
	v_med3_f32 v112, v112, s20, v129
	v_med3_f32 v113, v113, s20, v129
	v_med3_f32 v114, v114, s20, v129
	v_med3_f32 v115, v115, s20, v129
	v_mov_b32_e32 v116, 0
	v_mov_b32_e32 v117, 0
	v_mov_b32_e32 v118, 0
	v_mov_b32_e32 v119, 0
	v_cvt_pk_fp8_f32 v116, v100, v101
	v_cvt_pk_fp8_f32 v117, v104, v105
	v_cvt_pk_fp8_f32 v118, v108, v109
	v_cvt_pk_fp8_f32 v119, v112, v113
	v_cvt_pk_fp8_f32 v116, v102, v103 op_sel:[0,0,1]
	v_cvt_pk_fp8_f32 v117, v106, v107 op_sel:[0,0,1]
	v_cvt_pk_fp8_f32 v118, v110, v111 op_sel:[0,0,1]
	v_cvt_pk_fp8_f32 v119, v114, v115 op_sel:[0,0,1]
	s_nop 0
	global_store_dwordx4 v128, v[116:119], s[14:15]
	s_waitcnt vmcnt(12)
	v_mul_f32_e32 v36, 0x43000000, v36
	v_mul_f32_e32 v37, 0x43000000, v37
	v_mul_f32_e32 v38, 0x43000000, v38
	v_mul_f32_e32 v39, 0x43000000, v39
	ds_write_b128 v120, v[36:39]
	v_mul_f32_e32 v40, 0x43000000, v40
	v_mul_f32_e32 v41, 0x43000000, v41
	v_mul_f32_e32 v42, 0x43000000, v42
	v_mul_f32_e32 v43, 0x43000000, v43
	ds_write_b128 v120, v[40:43] offset:1024
	v_mul_f32_e32 v44, 0x43000000, v44
	v_mul_f32_e32 v45, 0x43000000, v45
	v_mul_f32_e32 v46, 0x43000000, v46
	v_mul_f32_e32 v47, 0x43000000, v47
	ds_write_b128 v120, v[44:47] offset:2048
	v_mul_f32_e32 v48, 0x43000000, v48
	v_mul_f32_e32 v49, 0x43000000, v49
	v_mul_f32_e32 v50, 0x43000000, v50
	v_mul_f32_e32 v51, 0x43000000, v51
	ds_write_b128 v120, v[48:51] offset:3072
	v_mul_f32_e32 v52, 0x43000000, v52
	v_mul_f32_e32 v53, 0x43000000, v53
	v_mul_f32_e32 v54, 0x43000000, v54
	v_mul_f32_e32 v55, 0x43000000, v55
	ds_write_b128 v120, v[52:55] offset:4096
	v_mul_f32_e32 v56, 0x43000000, v56
	v_mul_f32_e32 v57, 0x43000000, v57
	v_mul_f32_e32 v58, 0x43000000, v58
	v_mul_f32_e32 v59, 0x43000000, v59
	ds_write_b128 v120, v[56:59] offset:5120
	v_mul_f32_e32 v60, 0x43000000, v60
	v_mul_f32_e32 v61, 0x43000000, v61
	v_mul_f32_e32 v62, 0x43000000, v62
	v_mul_f32_e32 v63, 0x43000000, v63
	ds_write_b128 v120, v[60:63] offset:6144
	v_mul_f32_e32 v64, 0x43000000, v64
	v_mul_f32_e32 v65, 0x43000000, v65
	v_mul_f32_e32 v66, 0x43000000, v66
	v_mul_f32_e32 v67, 0x43000000, v67
	ds_write_b128 v120, v[64:67] offset:7168
	s_waitcnt lgkmcnt(0)
	s_barrier
; #define GAS __attribute__((address_space(1)))
; #define LAS __attribute__((address_space(3)))
; #define LDS_WAIT() asm volatile("s_waitcnt lgkmcnt(0)" ::: "memory")
; __device__ __forceinline__ unsigned pk4_fp8(float a, float b, float c, float d) {
;     a = fminf(fmaxf(a, -448.f), 448.f); b = fminf(fmaxf(b, -448.f), 448.f); c = fminf(fmaxf(c, -448.f), 448.f); d = fminf(fmaxf(d, -448.f), 448.f);
;     int w = __builtin_amdgcn_cvt_pk_fp8_f32(a, b, 0, false); w = __builtin_amdgcn_cvt_pk_fp8_f32(c, d, w, true); return (unsigned)w; }
;     const int pr = item >> 1, kb = 2 * (pr / nblk) + (item & 1), nb = pr % nblk, k0 = 64 * kb, n0 = 32 * nb;
;     const int nr = n0 + (lane & 31); const int sc = MAP == 1 ? src_col_in(nr) : nr;
;     float v[32];
; #pragma unroll
;     for (int i = 0; i < 32; ++i) v[i] = sc >= 0 ? W[(size_t)(k0 + 2 * i + (lane >> 5)) * Nsrc + sc] : 0.f;
; #pragma unroll
;     for (int i = 0; i < 32; ++i) { const int k = k0 + 2 * i + (lane >> 5); float x = v[i] * wscale; if (KS) x *= (k < ksplit ? ksA[k] : ksB[k - ksplit]); scr[(2 * i + (lane >> 5)) * 33 + (lane & 31)] = x; }
;     LDS_WAIT(); asm volatile("" ::: "memory");
;     const int c = lane & 7;
; #pragma unroll
;     for (int j = 0; j < 4; ++j) { const int n = (lane >> 3) + 8 * j; const LAS float* s = scr + (8 * c) * 33 + n;
;         const unsigned long long o = (unsigned long long)pg8::pk4_fp8(s[0 * 33], s[1 * 33], s[2 * 33], s[3 * 33]) | ((unsigned long long)pg8::pk4_fp8(s[4 * 33], s[5 * 33], s[6 * 33], s[7 * 33]) << 32);
;         *(GAS unsigned long long*)(WT + (size_t)(n0 + n) * K + k0 + 8 * c) = o; }
;     LDS_WAIT(); asm volatile("" ::: "memory");
; }
	s_add_i32 s17, s16, 2112
	s_min_u32 s17, s17, 0xbff
	s_lshr_b32 s18, s17, 5
	s_add_i32 s18, s18, 32
	s_and_b32 s19, s17, 31
	s_lshl_b32 s18, s18, 21
	s_lshl_b32 s19, s19, 9
	s_add_u32 s18, s18, s19
	s_add_u32 s12, s2, s18
	s_addc_u32 s13, s3, 0
	global_load_dwordx4 v[36:39], v126, s[12:13]
	s_add_u32 s12, s12, 0x8000
	s_addc_u32 s13, s13, 0
	global_load_dwordx4 v[40:43], v126, s[12:13]
	s_add_u32 s12, s12, 0x8000
	s_addc_u32 s13, s13, 0
	global_load_dwordx4 v[44:47], v126, s[12:13]
	s_add_u32 s12, s12, 0x8000
	s_addc_u32 s13, s13, 0
	global_load_dwordx4 v[48:51], v126, s[12:13]
	s_add_u32 s12, s12, 0x8000
	s_addc_u32 s13, s13, 0
	global_load_dwordx4 v[52:55], v126, s[12:13]
	s_add_u32 s12, s12, 0x8000
	s_addc_u32 s13, s13, 0
	global_load_dwordx4 v[56:59], v126, s[12:13]
	s_add_u32 s12, s12, 0x8000
	s_addc_u32 s13, s13, 0
	global_load_dwordx4 v[60:63], v126, s[12:13]
	s_add_u32 s12, s12, 0x8000
	s_addc_u32 s13, s13, 0
	global_load_dwordx4 v[64:67], v126, s[12:13]
	s_add_i32 s17, s16, 1920
	s_min_u32 s17, s17, 0xbff
	s_lshr_b32 s18, s17, 5
	s_add_i32 s18, s18, 32
	s_and_b32 s19, s17, 31
	s_lshl_b32 s19, s19, 21
	s_lshl_b32 s18, s18, 7
	s_add_u32 s18, s18, s19
	s_add_u32 s14, s4, s18
	s_addc_u32 s15, s5, 0
	ds_read_b32 v100, v122
	ds_read_b32 v101, v122 offset:512
	ds_read_b32 v102, v122 offset:1024
	ds_read_b32 v103, v122 offset:1536
	ds_read_b32 v104, v122 offset:2048
	ds_read_b32 v105, v122 offset:2560
	ds_read_b32 v106, v122 offset:3072
	ds_read_b32 v107, v122 offset:3584
	ds_read_b32 v108, v122 offset:4096
	ds_read_b32 v109, v122 offset:4608
	ds_read_b32 v110, v122 offset:5120
	ds_read_b32 v111, v122 offset:5632
	ds_read_b32 v112, v122 offset:6144
	ds_read_b32 v113, v122 offset:6656
	ds_read_b32 v114, v122 offset:7168
	ds_read_b32 v115, v122 offset:7680
	s_waitcnt lgkmcnt(0)
	v_max_f32_e32 v100, v100, v100
	v_max_f32_e32 v101, v101, v101
	v_max_f32_e32 v102, v102, v102
	v_max_f32_e32 v103, v103, v103
	v_max_f32_e32 v104, v104, v104
	v_max_f32_e32 v105, v105, v105
	v_max_f32_e32 v106, v106, v106
	v_max_f32_e32 v107, v107, v107
	v_max_f32_e32 v108, v108, v108
	v_max_f32_e32 v109, v109, v109
	v_max_f32_e32 v110, v110, v110
	v_max_f32_e32 v111, v111, v111
	v_max_f32_e32 v112, v112, v112
	v_max_f32_e32 v113, v113, v113
	v_max_f32_e32 v114, v114, v114
	v_max_f32_e32 v115, v115, v115
	v_med3_f32 v100, v100, s20, v129
	v_med3_f32 v101, v101, s20, v129
	v_med3_f32 v102, v102, s20, v129
	v_med3_f32 v103, v103, s20, v129
	v_med3_f32 v104, v104, s20, v129
	v_med3_f32 v105, v105, s20, v129
	v_med3_f32 v106, v106, s20, v129
	v_med3_f32 v107, v107, s20, v129
	v_med3_f32 v108, v108, s20, v129
	v_med3_f32 v109, v109, s20, v129
	v_med3_f32 v110, v110, s20, v129
	v_med3_f32 v111, v111, s20, v129
	v_med3_f32 v112, v112, s20, v129
	v_med3_f32 v113, v113, s20, v129
	v_med3_f32 v114, v114, s20, v129
	v_med3_f32 v115, v115, s20, v129
	v_mov_b32_e32 v116, 0
	v_mov_b32_e32 v117, 0
	v_mov_b32_e32 v118, 0
	v_mov_b32_e32 v119, 0
	v_cvt_pk_fp8_f32 v116, v100, v101
	v_cvt_pk_fp8_f32 v117, v104, v105
	v_cvt_pk_fp8_f32 v118, v108, v109
	v_cvt_pk_fp8_f32 v119, v112, v113
	v_cvt_pk_fp8_f32 v116, v102, v103 op_sel:[0,0,1]
	v_cvt_pk_fp8_f32 v117, v106, v107 op_sel:[0,0,1]
	v_cvt_pk_fp8_f32 v118, v110, v111 op_sel:[0,0,1]
	v_cvt_pk_fp8_f32 v119, v114, v115 op_sel:[0,0,1]
	s_nop 0
	global_store_dwordx4 v127, v[116:119], s[14:15]
	ds_read_b32 v100, v124
	ds_read_b32 v101, v124 offset:512
	ds_read_b32 v102, v124 offset:1024
	ds_read_b32 v103, v124 offset:1536
	ds_read_b32 v104, v124 offset:2048
	ds_read_b32 v105, v124 offset:2560
	ds_read_b32 v106, v124 offset:3072
	ds_read_b32 v107, v124 offset:3584
	ds_read_b32 v108, v124 offset:4096
	ds_read_b32 v109, v124 offset:4608
	ds_read_b32 v110, v124 offset:5120
	ds_read_b32 v111, v124 offset:5632
	ds_read_b32 v112, v124 offset:6144
	ds_read_b32 v113, v124 offset:6656
	ds_read_b32 v114, v124 offset:7168
	ds_read_b32 v115, v124 offset:7680
	s_waitcnt lgkmcnt(0)
	v_max_f32_e32 v100, v100, v100
	v_max_f32_e32 v101, v101, v101
	v_max_f32_e32 v102, v102, v102
	v_max_f32_e32 v103, v103, v103
	v_max_f32_e32 v104, v104, v104
	v_max_f32_e32 v105, v105, v105
	v_max_f32_e32 v106, v106, v106
	v_max_f32_e32 v107, v107, v107
	v_max_f32_e32 v108, v108, v108
	v_max_f32_e32 v109, v109, v109
	v_max_f32_e32 v110, v110, v110
	v_max_f32_e32 v111, v111, v111
	v_max_f32_e32 v112, v112, v112
	v_max_f32_e32 v113, v113, v113
	v_max_f32_e32 v114, v114, v114
	v_max_f32_e32 v115, v115, v115
	v_med3_f32 v100, v100, s20, v129
	v_med3_f32 v101, v101, s20, v129
	v_med3_f32 v102, v102, s20, v129
	v_med3_f32 v103, v103, s20, v129
	v_med3_f32 v104, v104, s20, v129
	v_med3_f32 v105, v105, s20, v129
	v_med3_f32 v106, v106, s20, v129
	v_med3_f32 v107, v107, s20, v129
	v_med3_f32 v108, v108, s20, v129
	v_med3_f32 v109, v109, s20, v129
	v_med3_f32 v110, v110, s20, v129
	v_med3_f32 v111, v111, s20, v129
	v_med3_f32 v112, v112, s20, v129
	v_med3_f32 v113, v113, s20, v129
	v_med3_f32 v114, v114, s20, v129
	v_med3_f32 v115, v115, s20, v129
	v_mov_b32_e32 v116, 0
	v_mov_b32_e32 v117, 0
	v_mov_b32_e32 v118, 0
	v_mov_b32_e32 v119, 0
	v_cvt_pk_fp8_f32 v116, v100, v101
	v_cvt_pk_fp8_f32 v117, v104, v105
	v_cvt_pk_fp8_f32 v118, v108, v109
	v_cvt_pk_fp8_f32 v119, v112, v113
	v_cvt_pk_fp8_f32 v116, v102, v103 op_sel:[0,0,1]
	v_cvt_pk_fp8_f32 v117, v106, v107 op_sel:[0,0,1]
	v_cvt_pk_fp8_f32 v118, v110, v111 op_sel:[0,0,1]
	v_cvt_pk_fp8_f32 v119, v114, v115 op_sel:[0,0,1]
	s_nop 0
	global_store_dwordx4 v128, v[116:119], s[14:15]
	s_waitcnt vmcnt(12)
	v_mul_f32_e32 v68, 0x43000000, v68
	v_mul_f32_e32 v69, 0x43000000, v69
	v_mul_f32_e32 v70, 0x43000000, v70
	v_mul_f32_e32 v71, 0x43000000, v71
	ds_write_b128 v121, v[68:71]
	v_mul_f32_e32 v72, 0x43000000, v72
	v_mul_f32_e32 v73, 0x43000000, v73
	v_mul_f32_e32 v74, 0x43000000, v74
	v_mul_f32_e32 v75, 0x43000000, v75
	ds_write_b128 v121, v[72:75] offset:1024
	v_mul_f32_e32 v76, 0x43000000, v76
	v_mul_f32_e32 v77, 0x43000000, v77
	v_mul_f32_e32 v78, 0x43000000, v78
	v_mul_f32_e32 v79, 0x43000000, v79
	ds_write_b128 v121, v[76:79] offset:2048
	v_mul_f32_e32 v80, 0x43000000, v80
	v_mul_f32_e32 v81, 0x43000000, v81
	v_mul_f32_e32 v82, 0x43000000, v82
	v_mul_f32_e32 v83, 0x43000000, v83
	ds_write_b128 v121, v[80:83] offset:3072
	v_mul_f32_e32 v84, 0x43000000, v84
	v_mul_f32_e32 v85, 0x43000000, v85
	v_mul_f32_e32 v86, 0x43000000, v86
	v_mul_f32_e32 v87, 0x43000000, v87
	ds_write_b128 v121, v[84:87] offset:4096
	v_mul_f32_e32 v88, 0x43000000, v88
	v_mul_f32_e32 v89, 0x43000000, v89
	v_mul_f32_e32 v90, 0x43000000, v90
	v_mul_f32_e32 v91, 0x43000000, v91
	ds_write_b128 v121, v[88:91] offset:5120
	v_mul_f32_e32 v92, 0x43000000, v92
	v_mul_f32_e32 v93, 0x43000000, v93
	v_mul_f32_e32 v94, 0x43000000, v94
	v_mul_f32_e32 v95, 0x43000000, v95
	ds_write_b128 v121, v[92:95] offset:6144
	v_mul_f32_e32 v96, 0x43000000, v96
	v_mul_f32_e32 v97, 0x43000000, v97
	v_mul_f32_e32 v98, 0x43000000, v98
	v_mul_f32_e32 v99, 0x43000000, v99
	ds_write_b128 v121, v[96:99] offset:7168
	s_waitcnt lgkmcnt(0)
	s_barrier
; #define GAS __attribute__((address_space(1)))
; #define LAS __attribute__((address_space(3)))
; #define LDS_WAIT() asm volatile("s_waitcnt lgkmcnt(0)" ::: "memory")
; __device__ __forceinline__ unsigned pk4_fp8(float a, float b, float c, float d) {
;     a = fminf(fmaxf(a, -448.f), 448.f); b = fminf(fmaxf(b, -448.f), 448.f); c = fminf(fmaxf(c, -448.f), 448.f); d = fminf(fmaxf(d, -448.f), 448.f);
;     int w = __builtin_amdgcn_cvt_pk_fp8_f32(a, b, 0, false); w = __builtin_amdgcn_cvt_pk_fp8_f32(c, d, w, true); return (unsigned)w; }
;     const int pr = item >> 1, kb = 2 * (pr / nblk) + (item & 1), nb = pr % nblk, k0 = 64 * kb, n0 = 32 * nb;
;     const int nr = n0 + (lane & 31); const int sc = MAP == 1 ? src_col_in(nr) : nr;
;     float v[32];
; #pragma unroll
;     for (int i = 0; i < 32; ++i) v[i] = sc >= 0 ? W[(size_t)(k0 + 2 * i + (lane >> 5)) * Nsrc + sc] : 0.f;
; #pragma unroll
;     for (int i = 0; i < 32; ++i) { const int k = k0 + 2 * i + (lane >> 5); float x = v[i] * wscale; if (KS) x *= (k < ksplit ? ksA[k] : ksB[k - ksplit]); scr[(2 * i + (lane >> 5)) * 33 + (lane & 31)] = x; }
;     LDS_WAIT(); asm volatile("" ::: "memory");
;     const int c = lane & 7;
; #pragma unroll
;     for (int j = 0; j < 4; ++j) { const int n = (lane >> 3) + 8 * j; const LAS float* s = scr + (8 * c) * 33 + n;
;         const unsigned long long o = (unsigned long long)pg8::pk4_fp8(s[0 * 33], s[1 * 33], s[2 * 33], s[3 * 33]) | ((unsigned long long)pg8::pk4_fp8(s[4 * 33], s[5 * 33], s[6 * 33], s[7 * 33]) << 32);
;         *(GAS unsigned long long*)(WT + (size_t)(n0 + n) * K + k0 + 8 * c) = o; }
;     LDS_WAIT(); asm volatile("" ::: "memory");
; }
	s_add_i32 s17, s16, 2208
	s_min_u32 s17, s17, 0xbff
	s_lshr_b32 s18, s17, 5
	s_add_i32 s18, s18, 32
	s_and_b32 s19, s17, 31
	s_lshl_b32 s18, s18, 21
	s_lshl_b32 s19, s19, 9
	s_add_u32 s18, s18, s19
	s_add_u32 s12, s2, s18
	s_addc_u32 s13, s3, 0
	global_load_dwordx4 v[68:71], v126, s[12:13]
	s_add_u32 s12, s12, 0x8000
	s_addc_u32 s13, s13, 0
	global_load_dwordx4 v[72:75], v126, s[12:13]
	s_add_u32 s12, s12, 0x8000
	s_addc_u32 s13, s13, 0
	global_load_dwordx4 v[76:79], v126, s[12:13]
	s_add_u32 s12, s12, 0x8000
	s_addc_u32 s13, s13, 0
	global_load_dwordx4 v[80:83], v126, s[12:13]
	s_add_u32 s12, s12, 0x8000
	s_addc_u32 s13, s13, 0
	global_load_dwordx4 v[84:87], v126, s[12:13]
	s_add_u32 s12, s12, 0x8000
	s_addc_u32 s13, s13, 0
	global_load_dwordx4 v[88:91], v126, s[12:13]
	s_add_u32 s12, s12, 0x8000
	s_addc_u32 s13, s13, 0
	global_load_dwordx4 v[92:95], v126, s[12:13]
	s_add_u32 s12, s12, 0x8000
	s_addc_u32 s13, s13, 0
	global_load_dwordx4 v[96:99], v126, s[12:13]
	s_add_i32 s17, s16, 2016
	s_min_u32 s17, s17, 0xbff
	s_lshr_b32 s18, s17, 5
	s_add_i32 s18, s18, 32
	s_and_b32 s19, s17, 31
	s_lshl_b32 s19, s19, 21
	s_lshl_b32 s18, s18, 7
	s_add_u32 s18, s18, s19
	s_add_u32 s14, s4, s18
	s_addc_u32 s15, s5, 0
	ds_read_b32 v100, v123
	ds_read_b32 v101, v123 offset:512
	ds_read_b32 v102, v123 offset:1024
	ds_read_b32 v103, v123 offset:1536
	ds_read_b32 v104, v123 offset:2048
	ds_read_b32 v105, v123 offset:2560
	ds_read_b32 v106, v123 offset:3072
	ds_read_b32 v107, v123 offset:3584
	ds_read_b32 v108, v123 offset:4096
	ds_read_b32 v109, v123 offset:4608
	ds_read_b32 v110, v123 offset:5120
	ds_read_b32 v111, v123 offset:5632
	ds_read_b32 v112, v123 offset:6144
	ds_read_b32 v113, v123 offset:6656
	ds_read_b32 v114, v123 offset:7168
	ds_read_b32 v115, v123 offset:7680
	s_waitcnt lgkmcnt(0)
	v_max_f32_e32 v100, v100, v100
	v_max_f32_e32 v101, v101, v101
	v_max_f32_e32 v102, v102, v102
	v_max_f32_e32 v103, v103, v103
	v_max_f32_e32 v104, v104, v104
	v_max_f32_e32 v105, v105, v105
	v_max_f32_e32 v106, v106, v106
	v_max_f32_e32 v107, v107, v107
	v_max_f32_e32 v108, v108, v108
	v_max_f32_e32 v109, v109, v109
	v_max_f32_e32 v110, v110, v110
	v_max_f32_e32 v111, v111, v111
	v_max_f32_e32 v112, v112, v112
	v_max_f32_e32 v113, v113, v113
	v_max_f32_e32 v114, v114, v114
	v_max_f32_e32 v115, v115, v115
	v_med3_f32 v100, v100, s20, v129
	v_med3_f32 v101, v101, s20, v129
	v_med3_f32 v102, v102, s20, v129
	v_med3_f32 v103, v103, s20, v129
	v_med3_f32 v104, v104, s20, v129
	v_med3_f32 v105, v105, s20, v129
	v_med3_f32 v106, v106, s20, v129
	v_med3_f32 v107, v107, s20, v129
	v_med3_f32 v108, v108, s20, v129
	v_med3_f32 v109, v109, s20, v129
	v_med3_f32 v110, v110, s20, v129
	v_med3_f32 v111, v111, s20, v129
	v_med3_f32 v112, v112, s20, v129
	v_med3_f32 v113, v113, s20, v129
	v_med3_f32 v114, v114, s20, v129
	v_med3_f32 v115, v115, s20, v129
	v_mov_b32_e32 v116, 0
	v_mov_b32_e32 v117, 0
	v_mov_b32_e32 v118, 0
	v_mov_b32_e32 v119, 0
	v_cvt_pk_fp8_f32 v116, v100, v101
	v_cvt_pk_fp8_f32 v117, v104, v105
	v_cvt_pk_fp8_f32 v118, v108, v109
	v_cvt_pk_fp8_f32 v119, v112, v113
	v_cvt_pk_fp8_f32 v116, v102, v103 op_sel:[0,0,1]
	v_cvt_pk_fp8_f32 v117, v106, v107 op_sel:[0,0,1]
	v_cvt_pk_fp8_f32 v118, v110, v111 op_sel:[0,0,1]
	v_cvt_pk_fp8_f32 v119, v114, v115 op_sel:[0,0,1]
	s_nop 0
	global_store_dwordx4 v127, v[116:119], s[14:15]
	ds_read_b32 v100, v125
	ds_read_b32 v101, v125 offset:512
	ds_read_b32 v102, v125 offset:1024
	ds_read_b32 v103, v125 offset:1536
	ds_read_b32 v104, v125 offset:2048
	ds_read_b32 v105, v125 offset:2560
	ds_read_b32 v106, v125 offset:3072
	ds_read_b32 v107, v125 offset:3584
	ds_read_b32 v108, v125 offset:4096
	ds_read_b32 v109, v125 offset:4608
	ds_read_b32 v110, v125 offset:5120
	ds_read_b32 v111, v125 offset:5632
	ds_read_b32 v112, v125 offset:6144
	ds_read_b32 v113, v125 offset:6656
	ds_read_b32 v114, v125 offset:7168
	ds_read_b32 v115, v125 offset:7680
	s_waitcnt lgkmcnt(0)
	v_max_f32_e32 v100, v100, v100
	v_max_f32_e32 v101, v101, v101
	v_max_f32_e32 v102, v102, v102
	v_max_f32_e32 v103, v103, v103
	v_max_f32_e32 v104, v104, v104
	v_max_f32_e32 v105, v105, v105
	v_max_f32_e32 v106, v106, v106
	v_max_f32_e32 v107, v107, v107
	v_max_f32_e32 v108, v108, v108
	v_max_f32_e32 v109, v109, v109
	v_max_f32_e32 v110, v110, v110
	v_max_f32_e32 v111, v111, v111
	v_max_f32_e32 v112, v112, v112
	v_max_f32_e32 v113, v113, v113
	v_max_f32_e32 v114, v114, v114
	v_max_f32_e32 v115, v115, v115
	v_med3_f32 v100, v100, s20, v129
	v_med3_f32 v101, v101, s20, v129
	v_med3_f32 v102, v102, s20, v129
	v_med3_f32 v103, v103, s20, v129
	v_med3_f32 v104, v104, s20, v129
	v_med3_f32 v105, v105, s20, v129
	v_med3_f32 v106, v106, s20, v129
	v_med3_f32 v107, v107, s20, v129
	v_med3_f32 v108, v108, s20, v129
	v_med3_f32 v109, v109, s20, v129
	v_med3_f32 v110, v110, s20, v129
	v_med3_f32 v111, v111, s20, v129
	v_med3_f32 v112, v112, s20, v129
	v_med3_f32 v113, v113, s20, v129
	v_med3_f32 v114, v114, s20, v129
	v_med3_f32 v115, v115, s20, v129
	v_mov_b32_e32 v116, 0
	v_mov_b32_e32 v117, 0
	v_mov_b32_e32 v118, 0
	v_mov_b32_e32 v119, 0
	v_cvt_pk_fp8_f32 v116, v100, v101
	v_cvt_pk_fp8_f32 v117, v104, v105
	v_cvt_pk_fp8_f32 v118, v108, v109
	v_cvt_pk_fp8_f32 v119, v112, v113
	v_cvt_pk_fp8_f32 v116, v102, v103 op_sel:[0,0,1]
	v_cvt_pk_fp8_f32 v117, v106, v107 op_sel:[0,0,1]
	v_cvt_pk_fp8_f32 v118, v110, v111 op_sel:[0,0,1]
	v_cvt_pk_fp8_f32 v119, v114, v115 op_sel:[0,0,1]
	s_nop 0
	global_store_dwordx4 v128, v[116:119], s[14:15]
	s_waitcnt vmcnt(12)
	v_mul_f32_e32 v36, 0x43000000, v36
	v_mul_f32_e32 v37, 0x43000000, v37
	v_mul_f32_e32 v38, 0x43000000, v38
	v_mul_f32_e32 v39, 0x43000000, v39
	ds_write_b128 v120, v[36:39]
	v_mul_f32_e32 v40, 0x43000000, v40
	v_mul_f32_e32 v41, 0x43000000, v41
	v_mul_f32_e32 v42, 0x43000000, v42
	v_mul_f32_e32 v43, 0x43000000, v43
	ds_write_b128 v120, v[40:43] offset:1024
	v_mul_f32_e32 v44, 0x43000000, v44
	v_mul_f32_e32 v45, 0x43000000, v45
	v_mul_f32_e32 v46, 0x43000000, v46
	v_mul_f32_e32 v47, 0x43000000, v47
	ds_write_b128 v120, v[44:47] offset:2048
	v_mul_f32_e32 v48, 0x43000000, v48
	v_mul_f32_e32 v49, 0x43000000, v49
	v_mul_f32_e32 v50, 0x43000000, v50
	v_mul_f32_e32 v51, 0x43000000, v51
	ds_write_b128 v120, v[48:51] offset:3072
	v_mul_f32_e32 v52, 0x43000000, v52
	v_mul_f32_e32 v53, 0x43000000, v53
	v_mul_f32_e32 v54, 0x43000000, v54
	v_mul_f32_e32 v55, 0x43000000, v55
	ds_write_b128 v120, v[52:55] offset:4096
	v_mul_f32_e32 v56, 0x43000000, v56
	v_mul_f32_e32 v57, 0x43000000, v57
	v_mul_f32_e32 v58, 0x43000000, v58
	v_mul_f32_e32 v59, 0x43000000, v59
	ds_write_b128 v120, v[56:59] offset:5120
	v_mul_f32_e32 v60, 0x43000000, v60
	v_mul_f32_e32 v61, 0x43000000, v61
	v_mul_f32_e32 v62, 0x43000000, v62
	v_mul_f32_e32 v63, 0x43000000, v63
	ds_write_b128 v120, v[60:63] offset:6144
	v_mul_f32_e32 v64, 0x43000000, v64
	v_mul_f32_e32 v65, 0x43000000, v65
	v_mul_f32_e32 v66, 0x43000000, v66
	v_mul_f32_e32 v67, 0x43000000, v67
	ds_write_b128 v120, v[64:67] offset:7168
	s_waitcnt lgkmcnt(0)
	s_barrier
; #define GAS __attribute__((address_space(1)))
; #define LAS __attribute__((address_space(3)))
; #define LDS_WAIT() asm volatile("s_waitcnt lgkmcnt(0)" ::: "memory")
; __device__ __forceinline__ unsigned pk4_fp8(float a, float b, float c, float d) {
;     a = fminf(fmaxf(a, -448.f), 448.f); b = fminf(fmaxf(b, -448.f), 448.f); c = fminf(fmaxf(c, -448.f), 448.f); d = fminf(fmaxf(d, -448.f), 448.f);
;     int w = __builtin_amdgcn_cvt_pk_fp8_f32(a, b, 0, false); w = __builtin_amdgcn_cvt_pk_fp8_f32(c, d, w, true); return (unsigned)w; }
;     const int pr = item >> 1, kb = 2 * (pr / nblk) + (item & 1), nb = pr % nblk, k0 = 64 * kb, n0 = 32 * nb;
;     const int nr = n0 + (lane & 31); const int sc = MAP == 1 ? src_col_in(nr) : nr;
;     float v[32];
; #pragma unroll
;     for (int i = 0; i < 32; ++i) v[i] = sc >= 0 ? W[(size_t)(k0 + 2 * i + (lane >> 5)) * Nsrc + sc] : 0.f;
; #pragma unroll
;     for (int i = 0; i < 32; ++i) { const int k = k0 + 2 * i + (lane >> 5); float x = v[i] * wscale; if (KS) x *= (k < ksplit ? ksA[k] : ksB[k - ksplit]); scr[(2 * i + (lane >> 5)) * 33 + (lane & 31)] = x; }
;     LDS_WAIT(); asm volatile("" ::: "memory");
;     const int c = lane & 7;
; #pragma unroll
;     for (int j = 0; j < 4; ++j) { const int n = (lane >> 3) + 8 * j; const LAS float* s = scr + (8 * c) * 33 + n;
;         const unsigned long long o = (unsigned long long)pg8::pk4_fp8(s[0 * 33], s[1 * 33], s[2 * 33], s[3 * 33]) | ((unsigned long long)pg8::pk4_fp8(s[4 * 33], s[5 * 33], s[6 * 33], s[7 * 33]) << 32);
;         *(GAS unsigned long long*)(WT + (size_t)(n0 + n) * K + k0 + 8 * c) = o; }
;     LDS_WAIT(); asm volatile("" ::: "memory");
; }
	s_add_i32 s17, s16, 2304
	s_min_u32 s17, s17, 0xbff
	s_lshr_b32 s18, s17, 5
	s_add_i32 s18, s18, 32
	s_and_b32 s19, s17, 31
	s_lshl_b32 s18, s18, 21
	s_lshl_b32 s19, s19, 9
	s_add_u32 s18, s18, s19
	s_add_u32 s12, s2, s18
	s_addc_u32 s13, s3, 0
	global_load_dwordx4 v[36:39], v126, s[12:13]
	s_add_u32 s12, s12, 0x8000
	s_addc_u32 s13, s13, 0
	global_load_dwordx4 v[40:43], v126, s[12:13]
	s_add_u32 s12, s12, 0x8000
	s_addc_u32 s13, s13, 0
	global_load_dwordx4 v[44:47], v126, s[12:13]
	s_add_u32 s12, s12, 0x8000
	s_addc_u32 s13, s13, 0
	global_load_dwordx4 v[48:51], v126, s[12:13]
	s_add_u32 s12, s12, 0x8000
	s_addc_u32 s13, s13, 0
	global_load_dwordx4 v[52:55], v126, s[12:13]
	s_add_u32 s12, s12, 0x8000
	s_addc_u32 s13, s13, 0
	global_load_dwordx4 v[56:59], v126, s[12:13]
	s_add_u32 s12, s12, 0x8000
	s_addc_u32 s13, s13, 0
	global_load_dwordx4 v[60:63], v126, s[12:13]
	s_add_u32 s12, s12, 0x8000
	s_addc_u32 s13, s13, 0
	global_load_dwordx4 v[64:67], v126, s[12:13]
	s_add_i32 s17, s16, 2112
	s_min_u32 s17, s17, 0xbff
	s_lshr_b32 s18, s17, 5
	s_add_i32 s18, s18, 32
	s_and_b32 s19, s17, 31
	s_lshl_b32 s19, s19, 21
	s_lshl_b32 s18, s18, 7
	s_add_u32 s18, s18, s19
	s_add_u32 s14, s4, s18
	s_addc_u32 s15, s5, 0
	ds_read_b32 v100, v122
	ds_read_b32 v101, v122 offset:512
	ds_read_b32 v102, v122 offset:1024
	ds_read_b32 v103, v122 offset:1536
	ds_read_b32 v104, v122 offset:2048
	ds_read_b32 v105, v122 offset:2560
	ds_read_b32 v106, v122 offset:3072
	ds_read_b32 v107, v122 offset:3584
	ds_read_b32 v108, v122 offset:4096
	ds_read_b32 v109, v122 offset:4608
	ds_read_b32 v110, v122 offset:5120
	ds_read_b32 v111, v122 offset:5632
	ds_read_b32 v112, v122 offset:6144
	ds_read_b32 v113, v122 offset:6656
	ds_read_b32 v114, v122 offset:7168
	ds_read_b32 v115, v122 offset:7680
	s_waitcnt lgkmcnt(0)
	v_max_f32_e32 v100, v100, v100
	v_max_f32_e32 v101, v101, v101
	v_max_f32_e32 v102, v102, v102
	v_max_f32_e32 v103, v103, v103
	v_max_f32_e32 v104, v104, v104
	v_max_f32_e32 v105, v105, v105
	v_max_f32_e32 v106, v106, v106
	v_max_f32_e32 v107, v107, v107
	v_max_f32_e32 v108, v108, v108
	v_max_f32_e32 v109, v109, v109
	v_max_f32_e32 v110, v110, v110
	v_max_f32_e32 v111, v111, v111
	v_max_f32_e32 v112, v112, v112
	v_max_f32_e32 v113, v113, v113
	v_max_f32_e32 v114, v114, v114
	v_max_f32_e32 v115, v115, v115
	v_med3_f32 v100, v100, s20, v129
	v_med3_f32 v101, v101, s20, v129
	v_med3_f32 v102, v102, s20, v129
	v_med3_f32 v103, v103, s20, v129
	v_med3_f32 v104, v104, s20, v129
	v_med3_f32 v105, v105, s20, v129
	v_med3_f32 v106, v106, s20, v129
	v_med3_f32 v107, v107, s20, v129
	v_med3_f32 v108, v108, s20, v129
	v_med3_f32 v109, v109, s20, v129
	v_med3_f32 v110, v110, s20, v129
	v_med3_f32 v111, v111, s20, v129
	v_med3_f32 v112, v112, s20, v129
	v_med3_f32 v113, v113, s20, v129
	v_med3_f32 v114, v114, s20, v129
	v_med3_f32 v115, v115, s20, v129
	v_mov_b32_e32 v116, 0
	v_mov_b32_e32 v117, 0
	v_mov_b32_e32 v118, 0
	v_mov_b32_e32 v119, 0
	v_cvt_pk_fp8_f32 v116, v100, v101
	v_cvt_pk_fp8_f32 v117, v104, v105
	v_cvt_pk_fp8_f32 v118, v108, v109
	v_cvt_pk_fp8_f32 v119, v112, v113
	v_cvt_pk_fp8_f32 v116, v102, v103 op_sel:[0,0,1]
	v_cvt_pk_fp8_f32 v117, v106, v107 op_sel:[0,0,1]
	v_cvt_pk_fp8_f32 v118, v110, v111 op_sel:[0,0,1]
	v_cvt_pk_fp8_f32 v119, v114, v115 op_sel:[0,0,1]
	s_nop 0
	global_store_dwordx4 v127, v[116:119], s[14:15]
	ds_read_b32 v100, v124
	ds_read_b32 v101, v124 offset:512
	ds_read_b32 v102, v124 offset:1024
	ds_read_b32 v103, v124 offset:1536
	ds_read_b32 v104, v124 offset:2048
	ds_read_b32 v105, v124 offset:2560
	ds_read_b32 v106, v124 offset:3072
	ds_read_b32 v107, v124 offset:3584
	ds_read_b32 v108, v124 offset:4096
	ds_read_b32 v109, v124 offset:4608
	ds_read_b32 v110, v124 offset:5120
	ds_read_b32 v111, v124 offset:5632
	ds_read_b32 v112, v124 offset:6144
	ds_read_b32 v113, v124 offset:6656
	ds_read_b32 v114, v124 offset:7168
	ds_read_b32 v115, v124 offset:7680
	s_waitcnt lgkmcnt(0)
	v_max_f32_e32 v100, v100, v100
	v_max_f32_e32 v101, v101, v101
	v_max_f32_e32 v102, v102, v102
	v_max_f32_e32 v103, v103, v103
	v_max_f32_e32 v104, v104, v104
	v_max_f32_e32 v105, v105, v105
	v_max_f32_e32 v106, v106, v106
	v_max_f32_e32 v107, v107, v107
	v_max_f32_e32 v108, v108, v108
	v_max_f32_e32 v109, v109, v109
	v_max_f32_e32 v110, v110, v110
	v_max_f32_e32 v111, v111, v111
	v_max_f32_e32 v112, v112, v112
	v_max_f32_e32 v113, v113, v113
	v_max_f32_e32 v114, v114, v114
	v_max_f32_e32 v115, v115, v115
	v_med3_f32 v100, v100, s20, v129
	v_med3_f32 v101, v101, s20, v129
	v_med3_f32 v102, v102, s20, v129
	v_med3_f32 v103, v103, s20, v129
	v_med3_f32 v104, v104, s20, v129
	v_med3_f32 v105, v105, s20, v129
	v_med3_f32 v106, v106, s20, v129
	v_med3_f32 v107, v107, s20, v129
	v_med3_f32 v108, v108, s20, v129
	v_med3_f32 v109, v109, s20, v129
	v_med3_f32 v110, v110, s20, v129
	v_med3_f32 v111, v111, s20, v129
	v_med3_f32 v112, v112, s20, v129
	v_med3_f32 v113, v113, s20, v129
	v_med3_f32 v114, v114, s20, v129
	v_med3_f32 v115, v115, s20, v129
	v_mov_b32_e32 v116, 0
	v_mov_b32_e32 v117, 0
	v_mov_b32_e32 v118, 0
	v_mov_b32_e32 v119, 0
	v_cvt_pk_fp8_f32 v116, v100, v101
	v_cvt_pk_fp8_f32 v117, v104, v105
	v_cvt_pk_fp8_f32 v118, v108, v109
	v_cvt_pk_fp8_f32 v119, v112, v113
	v_cvt_pk_fp8_f32 v116, v102, v103 op_sel:[0,0,1]
	v_cvt_pk_fp8_f32 v117, v106, v107 op_sel:[0,0,1]
	v_cvt_pk_fp8_f32 v118, v110, v111 op_sel:[0,0,1]
	v_cvt_pk_fp8_f32 v119, v114, v115 op_sel:[0,0,1]
	s_nop 0
	global_store_dwordx4 v128, v[116:119], s[14:15]
	s_waitcnt vmcnt(12)
	v_mul_f32_e32 v68, 0x43000000, v68
	v_mul_f32_e32 v69, 0x43000000, v69
	v_mul_f32_e32 v70, 0x43000000, v70
	v_mul_f32_e32 v71, 0x43000000, v71
	ds_write_b128 v121, v[68:71]
	v_mul_f32_e32 v72, 0x43000000, v72
	v_mul_f32_e32 v73, 0x43000000, v73
	v_mul_f32_e32 v74, 0x43000000, v74
	v_mul_f32_e32 v75, 0x43000000, v75
	ds_write_b128 v121, v[72:75] offset:1024
	v_mul_f32_e32 v76, 0x43000000, v76
	v_mul_f32_e32 v77, 0x43000000, v77
	v_mul_f32_e32 v78, 0x43000000, v78
	v_mul_f32_e32 v79, 0x43000000, v79
	ds_write_b128 v121, v[76:79] offset:2048
	v_mul_f32_e32 v80, 0x43000000, v80
	v_mul_f32_e32 v81, 0x43000000, v81
	v_mul_f32_e32 v82, 0x43000000, v82
	v_mul_f32_e32 v83, 0x43000000, v83
	ds_write_b128 v121, v[80:83] offset:3072
	v_mul_f32_e32 v84, 0x43000000, v84
	v_mul_f32_e32 v85, 0x43000000, v85
	v_mul_f32_e32 v86, 0x43000000, v86
	v_mul_f32_e32 v87, 0x43000000, v87
	ds_write_b128 v121, v[84:87] offset:4096
	v_mul_f32_e32 v88, 0x43000000, v88
	v_mul_f32_e32 v89, 0x43000000, v89
	v_mul_f32_e32 v90, 0x43000000, v90
	v_mul_f32_e32 v91, 0x43000000, v91
	ds_write_b128 v121, v[88:91] offset:5120
	v_mul_f32_e32 v92, 0x43000000, v92
	v_mul_f32_e32 v93, 0x43000000, v93
	v_mul_f32_e32 v94, 0x43000000, v94
	v_mul_f32_e32 v95, 0x43000000, v95
	ds_write_b128 v121, v[92:95] offset:6144
	v_mul_f32_e32 v96, 0x43000000, v96
	v_mul_f32_e32 v97, 0x43000000, v97
	v_mul_f32_e32 v98, 0x43000000, v98
	v_mul_f32_e32 v99, 0x43000000, v99
	ds_write_b128 v121, v[96:99] offset:7168
	s_waitcnt lgkmcnt(0)
	s_barrier
; #define GAS __attribute__((address_space(1)))
; #define LAS __attribute__((address_space(3)))
; #define LDS_WAIT() asm volatile("s_waitcnt lgkmcnt(0)" ::: "memory")
; __device__ __forceinline__ unsigned pk4_fp8(float a, float b, float c, float d) {
;     a = fminf(fmaxf(a, -448.f), 448.f); b = fminf(fmaxf(b, -448.f), 448.f); c = fminf(fmaxf(c, -448.f), 448.f); d = fminf(fmaxf(d, -448.f), 448.f);
;     int w = __builtin_amdgcn_cvt_pk_fp8_f32(a, b, 0, false); w = __builtin_amdgcn_cvt_pk_fp8_f32(c, d, w, true); return (unsigned)w; }
;     const int pr = item >> 1, kb = 2 * (pr / nblk) + (item & 1), nb = pr % nblk, k0 = 64 * kb, n0 = 32 * nb;
;     const int nr = n0 + (lane & 31); const int sc = MAP == 1 ? src_col_in(nr) : nr;
;     float v[32];
; #pragma unroll
;     for (int i = 0; i < 32; ++i) v[i] = sc >= 0 ? W[(size_t)(k0 + 2 * i + (lane >> 5)) * Nsrc + sc] : 0.f;
; #pragma unroll
;     for (int i = 0; i < 32; ++i) { const int k = k0 + 2 * i + (lane >> 5); float x = v[i] * wscale; if (KS) x *= (k < ksplit ? ksA[k] : ksB[k - ksplit]); scr[(2 * i + (lane >> 5)) * 33 + (lane & 31)] = x; }
;     LDS_WAIT(); asm volatile("" ::: "memory");
;     const int c = lane & 7;
; #pragma unroll
;     for (int j = 0; j < 4; ++j) { const int n = (lane >> 3) + 8 * j; const LAS float* s = scr + (8 * c) * 33 + n;
;         const unsigned long long o = (unsigned long long)pg8::pk4_fp8(s[0 * 33], s[1 * 33], s[2 * 33], s[3 * 33]) | ((unsigned long long)pg8::pk4_fp8(s[4 * 33], s[5 * 33], s[6 * 33], s[7 * 33]) << 32);
;         *(GAS unsigned long long*)(WT + (size_t)(n0 + n) * K + k0 + 8 * c) = o; }
;     LDS_WAIT(); asm volatile("" ::: "memory");
; }
	s_add_i32 s17, s16, 2400
	s_min_u32 s17, s17, 0xbff
	s_lshr_b32 s18, s17, 5
	s_add_i32 s18, s18, 32
	s_and_b32 s19, s17, 31
	s_lshl_b32 s18, s18, 21
	s_lshl_b32 s19, s19, 9
	s_add_u32 s18, s18, s19
	s_add_u32 s12, s2, s18
	s_addc_u32 s13, s3, 0
	global_load_dwordx4 v[68:71], v126, s[12:13]
	s_add_u32 s12, s12, 0x8000
	s_addc_u32 s13, s13, 0
	global_load_dwordx4 v[72:75], v126, s[12:13]
	s_add_u32 s12, s12, 0x8000
	s_addc_u32 s13, s13, 0
	global_load_dwordx4 v[76:79], v126, s[12:13]
	s_add_u32 s12, s12, 0x8000
	s_addc_u32 s13, s13, 0
	global_load_dwordx4 v[80:83], v126, s[12:13]
	s_add_u32 s12, s12, 0x8000
	s_addc_u32 s13, s13, 0
	global_load_dwordx4 v[84:87], v126, s[12:13]
	s_add_u32 s12, s12, 0x8000
	s_addc_u32 s13, s13, 0
	global_load_dwordx4 v[88:91], v126, s[12:13]
	s_add_u32 s12, s12, 0x8000
	s_addc_u32 s13, s13, 0
	global_load_dwordx4 v[92:95], v126, s[12:13]
	s_add_u32 s12, s12, 0x8000
	s_addc_u32 s13, s13, 0
	global_load_dwordx4 v[96:99], v126, s[12:13]
	s_add_i32 s17, s16, 2208
	s_min_u32 s17, s17, 0xbff
	s_lshr_b32 s18, s17, 5
	s_add_i32 s18, s18, 32
	s_and_b32 s19, s17, 31
	s_lshl_b32 s19, s19, 21
	s_lshl_b32 s18, s18, 7
	s_add_u32 s18, s18, s19
	s_add_u32 s14, s4, s18
	s_addc_u32 s15, s5, 0
	ds_read_b32 v100, v123
	ds_read_b32 v101, v123 offset:512
	ds_read_b32 v102, v123 offset:1024
	ds_read_b32 v103, v123 offset:1536
	ds_read_b32 v104, v123 offset:2048
	ds_read_b32 v105, v123 offset:2560
	ds_read_b32 v106, v123 offset:3072
	ds_read_b32 v107, v123 offset:3584
	ds_read_b32 v108, v123 offset:4096
	ds_read_b32 v109, v123 offset:4608
	ds_read_b32 v110, v123 offset:5120
	ds_read_b32 v111, v123 offset:5632
	ds_read_b32 v112, v123 offset:6144
	ds_read_b32 v113, v123 offset:6656
	ds_read_b32 v114, v123 offset:7168
	ds_read_b32 v115, v123 offset:7680
	s_waitcnt lgkmcnt(0)
	v_max_f32_e32 v100, v100, v100
	v_max_f32_e32 v101, v101, v101
	v_max_f32_e32 v102, v102, v102
	v_max_f32_e32 v103, v103, v103
	v_max_f32_e32 v104, v104, v104
	v_max_f32_e32 v105, v105, v105
	v_max_f32_e32 v106, v106, v106
	v_max_f32_e32 v107, v107, v107
	v_max_f32_e32 v108, v108, v108
	v_max_f32_e32 v109, v109, v109
	v_max_f32_e32 v110, v110, v110
	v_max_f32_e32 v111, v111, v111
	v_max_f32_e32 v112, v112, v112
	v_max_f32_e32 v113, v113, v113
	v_max_f32_e32 v114, v114, v114
	v_max_f32_e32 v115, v115, v115
	v_med3_f32 v100, v100, s20, v129
	v_med3_f32 v101, v101, s20, v129
	v_med3_f32 v102, v102, s20, v129
	v_med3_f32 v103, v103, s20, v129
	v_med3_f32 v104, v104, s20, v129
	v_med3_f32 v105, v105, s20, v129
	v_med3_f32 v106, v106, s20, v129
	v_med3_f32 v107, v107, s20, v129
	v_med3_f32 v108, v108, s20, v129
	v_med3_f32 v109, v109, s20, v129
	v_med3_f32 v110, v110, s20, v129
	v_med3_f32 v111, v111, s20, v129
	v_med3_f32 v112, v112, s20, v129
	v_med3_f32 v113, v113, s20, v129
	v_med3_f32 v114, v114, s20, v129
	v_med3_f32 v115, v115, s20, v129
	v_mov_b32_e32 v116, 0
	v_mov_b32_e32 v117, 0
	v_mov_b32_e32 v118, 0
	v_mov_b32_e32 v119, 0
	v_cvt_pk_fp8_f32 v116, v100, v101
	v_cvt_pk_fp8_f32 v117, v104, v105
	v_cvt_pk_fp8_f32 v118, v108, v109
	v_cvt_pk_fp8_f32 v119, v112, v113
	v_cvt_pk_fp8_f32 v116, v102, v103 op_sel:[0,0,1]
	v_cvt_pk_fp8_f32 v117, v106, v107 op_sel:[0,0,1]
	v_cvt_pk_fp8_f32 v118, v110, v111 op_sel:[0,0,1]
	v_cvt_pk_fp8_f32 v119, v114, v115 op_sel:[0,0,1]
	s_nop 0
	global_store_dwordx4 v127, v[116:119], s[14:15]
	ds_read_b32 v100, v125
	ds_read_b32 v101, v125 offset:512
	ds_read_b32 v102, v125 offset:1024
	ds_read_b32 v103, v125 offset:1536
	ds_read_b32 v104, v125 offset:2048
	ds_read_b32 v105, v125 offset:2560
	ds_read_b32 v106, v125 offset:3072
	ds_read_b32 v107, v125 offset:3584
	ds_read_b32 v108, v125 offset:4096
	ds_read_b32 v109, v125 offset:4608
	ds_read_b32 v110, v125 offset:5120
	ds_read_b32 v111, v125 offset:5632
	ds_read_b32 v112, v125 offset:6144
	ds_read_b32 v113, v125 offset:6656
	ds_read_b32 v114, v125 offset:7168
	ds_read_b32 v115, v125 offset:7680
	s_waitcnt lgkmcnt(0)
	v_max_f32_e32 v100, v100, v100
	v_max_f32_e32 v101, v101, v101
	v_max_f32_e32 v102, v102, v102
	v_max_f32_e32 v103, v103, v103
	v_max_f32_e32 v104, v104, v104
	v_max_f32_e32 v105, v105, v105
	v_max_f32_e32 v106, v106, v106
	v_max_f32_e32 v107, v107, v107
	v_max_f32_e32 v108, v108, v108
	v_max_f32_e32 v109, v109, v109
	v_max_f32_e32 v110, v110, v110
	v_max_f32_e32 v111, v111, v111
	v_max_f32_e32 v112, v112, v112
	v_max_f32_e32 v113, v113, v113
	v_max_f32_e32 v114, v114, v114
	v_max_f32_e32 v115, v115, v115
	v_med3_f32 v100, v100, s20, v129
	v_med3_f32 v101, v101, s20, v129
	v_med3_f32 v102, v102, s20, v129
	v_med3_f32 v103, v103, s20, v129
	v_med3_f32 v104, v104, s20, v129
	v_med3_f32 v105, v105, s20, v129
	v_med3_f32 v106, v106, s20, v129
	v_med3_f32 v107, v107, s20, v129
	v_med3_f32 v108, v108, s20, v129
	v_med3_f32 v109, v109, s20, v129
	v_med3_f32 v110, v110, s20, v129
	v_med3_f32 v111, v111, s20, v129
	v_med3_f32 v112, v112, s20, v129
	v_med3_f32 v113, v113, s20, v129
	v_med3_f32 v114, v114, s20, v129
	v_med3_f32 v115, v115, s20, v129
	v_mov_b32_e32 v116, 0
	v_mov_b32_e32 v117, 0
	v_mov_b32_e32 v118, 0
	v_mov_b32_e32 v119, 0
	v_cvt_pk_fp8_f32 v116, v100, v101
	v_cvt_pk_fp8_f32 v117, v104, v105
	v_cvt_pk_fp8_f32 v118, v108, v109
	v_cvt_pk_fp8_f32 v119, v112, v113
	v_cvt_pk_fp8_f32 v116, v102, v103 op_sel:[0,0,1]
	v_cvt_pk_fp8_f32 v117, v106, v107 op_sel:[0,0,1]
	v_cvt_pk_fp8_f32 v118, v110, v111 op_sel:[0,0,1]
	v_cvt_pk_fp8_f32 v119, v114, v115 op_sel:[0,0,1]
	s_nop 0
	global_store_dwordx4 v128, v[116:119], s[14:15]
	s_waitcnt vmcnt(12)
	v_mul_f32_e32 v36, 0x43000000, v36
	v_mul_f32_e32 v37, 0x43000000, v37
	v_mul_f32_e32 v38, 0x43000000, v38
	v_mul_f32_e32 v39, 0x43000000, v39
	ds_write_b128 v120, v[36:39]
	v_mul_f32_e32 v40, 0x43000000, v40
	v_mul_f32_e32 v41, 0x43000000, v41
	v_mul_f32_e32 v42, 0x43000000, v42
	v_mul_f32_e32 v43, 0x43000000, v43
	ds_write_b128 v120, v[40:43] offset:1024
	v_mul_f32_e32 v44, 0x43000000, v44
	v_mul_f32_e32 v45, 0x43000000, v45
	v_mul_f32_e32 v46, 0x43000000, v46
	v_mul_f32_e32 v47, 0x43000000, v47
	ds_write_b128 v120, v[44:47] offset:2048
	v_mul_f32_e32 v48, 0x43000000, v48
	v_mul_f32_e32 v49, 0x43000000, v49
	v_mul_f32_e32 v50, 0x43000000, v50
	v_mul_f32_e32 v51, 0x43000000, v51
	ds_write_b128 v120, v[48:51] offset:3072
	v_mul_f32_e32 v52, 0x43000000, v52
	v_mul_f32_e32 v53, 0x43000000, v53
	v_mul_f32_e32 v54, 0x43000000, v54
	v_mul_f32_e32 v55, 0x43000000, v55
	ds_write_b128 v120, v[52:55] offset:4096
	v_mul_f32_e32 v56, 0x43000000, v56
	v_mul_f32_e32 v57, 0x43000000, v57
	v_mul_f32_e32 v58, 0x43000000, v58
	v_mul_f32_e32 v59, 0x43000000, v59
	ds_write_b128 v120, v[56:59] offset:5120
	v_mul_f32_e32 v60, 0x43000000, v60
	v_mul_f32_e32 v61, 0x43000000, v61
	v_mul_f32_e32 v62, 0x43000000, v62
	v_mul_f32_e32 v63, 0x43000000, v63
	ds_write_b128 v120, v[60:63] offset:6144
	v_mul_f32_e32 v64, 0x43000000, v64
	v_mul_f32_e32 v65, 0x43000000, v65
	v_mul_f32_e32 v66, 0x43000000, v66
	v_mul_f32_e32 v67, 0x43000000, v67
	ds_write_b128 v120, v[64:67] offset:7168
	s_waitcnt lgkmcnt(0)
	s_barrier
; #define GAS __attribute__((address_space(1)))
; #define LAS __attribute__((address_space(3)))
; #define LDS_WAIT() asm volatile("s_waitcnt lgkmcnt(0)" ::: "memory")
; __device__ __forceinline__ unsigned pk4_fp8(float a, float b, float c, float d) {
;     a = fminf(fmaxf(a, -448.f), 448.f); b = fminf(fmaxf(b, -448.f), 448.f); c = fminf(fmaxf(c, -448.f), 448.f); d = fminf(fmaxf(d, -448.f), 448.f);
;     int w = __builtin_amdgcn_cvt_pk_fp8_f32(a, b, 0, false); w = __builtin_amdgcn_cvt_pk_fp8_f32(c, d, w, true); return (unsigned)w; }
;     const int pr = item >> 1, kb = 2 * (pr / nblk) + (item & 1), nb = pr % nblk, k0 = 64 * kb, n0 = 32 * nb;
;     const int nr = n0 + (lane & 31); const int sc = MAP == 1 ? src_col_in(nr) : nr;
;     float v[32];
; #pragma unroll
;     for (int i = 0; i < 32; ++i) v[i] = sc >= 0 ? W[(size_t)(k0 + 2 * i + (lane >> 5)) * Nsrc + sc] : 0.f;
; #pragma unroll
;     for (int i = 0; i < 32; ++i) { const int k = k0 + 2 * i + (lane >> 5); float x = v[i] * wscale; if (KS) x *= (k < ksplit ? ksA[k] : ksB[k - ksplit]); scr[(2 * i + (lane >> 5)) * 33 + (lane & 31)] = x; }
;     LDS_WAIT(); asm volatile("" ::: "memory");
;     const int c = lane & 7;
; #pragma unroll
;     for (int j = 0; j < 4; ++j) { const int n = (lane >> 3) + 8 * j; const LAS float* s = scr + (8 * c) * 33 + n;
;         const unsigned long long o = (unsigned long long)pg8::pk4_fp8(s[0 * 33], s[1 * 33], s[2 * 33], s[3 * 33]) | ((unsigned long long)pg8::pk4_fp8(s[4 * 33], s[5 * 33], s[6 * 33], s[7 * 33]) << 32);
;         *(GAS unsigned long long*)(WT + (size_t)(n0 + n) * K + k0 + 8 * c) = o; }
;     LDS_WAIT(); asm volatile("" ::: "memory");
; }
	s_add_i32 s17, s16, 2496
	s_min_u32 s17, s17, 0xbff
	s_lshr_b32 s18, s17, 5
	s_add_i32 s18, s18, 32
	s_and_b32 s19, s17, 31
	s_lshl_b32 s18, s18, 21
	s_lshl_b32 s19, s19, 9
	s_add_u32 s18, s18, s19
	s_add_u32 s12, s2, s18
	s_addc_u32 s13, s3, 0
	global_load_dwordx4 v[36:39], v126, s[12:13]
	s_add_u32 s12, s12, 0x8000
	s_addc_u32 s13, s13, 0
	global_load_dwordx4 v[40:43], v126, s[12:13]
	s_add_u32 s12, s12, 0x8000
	s_addc_u32 s13, s13, 0
	global_load_dwordx4 v[44:47], v126, s[12:13]
	s_add_u32 s12, s12, 0x8000
	s_addc_u32 s13, s13, 0
	global_load_dwordx4 v[48:51], v126, s[12:13]
	s_add_u32 s12, s12, 0x8000
	s_addc_u32 s13, s13, 0
	global_load_dwordx4 v[52:55], v126, s[12:13]
	s_add_u32 s12, s12, 0x8000
	s_addc_u32 s13, s13, 0
	global_load_dwordx4 v[56:59], v126, s[12:13]
	s_add_u32 s12, s12, 0x8000
	s_addc_u32 s13, s13, 0
	global_load_dwordx4 v[60:63], v126, s[12:13]
	s_add_u32 s12, s12, 0x8000
	s_addc_u32 s13, s13, 0
	global_load_dwordx4 v[64:67], v126, s[12:13]
	s_add_i32 s17, s16, 2304
	s_min_u32 s17, s17, 0xbff
	s_lshr_b32 s18, s17, 5
	s_add_i32 s18, s18, 32
	s_and_b32 s19, s17, 31
	s_lshl_b32 s19, s19, 21
	s_lshl_b32 s18, s18, 7
	s_add_u32 s18, s18, s19
	s_add_u32 s14, s4, s18
	s_addc_u32 s15, s5, 0
	ds_read_b32 v100, v122
	ds_read_b32 v101, v122 offset:512
	ds_read_b32 v102, v122 offset:1024
	ds_read_b32 v103, v122 offset:1536
	ds_read_b32 v104, v122 offset:2048
	ds_read_b32 v105, v122 offset:2560
	ds_read_b32 v106, v122 offset:3072
	ds_read_b32 v107, v122 offset:3584
	ds_read_b32 v108, v122 offset:4096
	ds_read_b32 v109, v122 offset:4608
	ds_read_b32 v110, v122 offset:5120
	ds_read_b32 v111, v122 offset:5632
	ds_read_b32 v112, v122 offset:6144
	ds_read_b32 v113, v122 offset:6656
	ds_read_b32 v114, v122 offset:7168
	ds_read_b32 v115, v122 offset:7680
	s_waitcnt lgkmcnt(0)
	v_max_f32_e32 v100, v100, v100
	v_max_f32_e32 v101, v101, v101
	v_max_f32_e32 v102, v102, v102
	v_max_f32_e32 v103, v103, v103
	v_max_f32_e32 v104, v104, v104
	v_max_f32_e32 v105, v105, v105
	v_max_f32_e32 v106, v106, v106
	v_max_f32_e32 v107, v107, v107
	v_max_f32_e32 v108, v108, v108
	v_max_f32_e32 v109, v109, v109
	v_max_f32_e32 v110, v110, v110
	v_max_f32_e32 v111, v111, v111
	v_max_f32_e32 v112, v112, v112
	v_max_f32_e32 v113, v113, v113
	v_max_f32_e32 v114, v114, v114
	v_max_f32_e32 v115, v115, v115
	v_med3_f32 v100, v100, s20, v129
	v_med3_f32 v101, v101, s20, v129
	v_med3_f32 v102, v102, s20, v129
	v_med3_f32 v103, v103, s20, v129
	v_med3_f32 v104, v104, s20, v129
	v_med3_f32 v105, v105, s20, v129
	v_med3_f32 v106, v106, s20, v129
	v_med3_f32 v107, v107, s20, v129
	v_med3_f32 v108, v108, s20, v129
	v_med3_f32 v109, v109, s20, v129
	v_med3_f32 v110, v110, s20, v129
	v_med3_f32 v111, v111, s20, v129
	v_med3_f32 v112, v112, s20, v129
	v_med3_f32 v113, v113, s20, v129
	v_med3_f32 v114, v114, s20, v129
	v_med3_f32 v115, v115, s20, v129
	v_mov_b32_e32 v116, 0
	v_mov_b32_e32 v117, 0
	v_mov_b32_e32 v118, 0
	v_mov_b32_e32 v119, 0
	v_cvt_pk_fp8_f32 v116, v100, v101
	v_cvt_pk_fp8_f32 v117, v104, v105
	v_cvt_pk_fp8_f32 v118, v108, v109
	v_cvt_pk_fp8_f32 v119, v112, v113
	v_cvt_pk_fp8_f32 v116, v102, v103 op_sel:[0,0,1]
	v_cvt_pk_fp8_f32 v117, v106, v107 op_sel:[0,0,1]
	v_cvt_pk_fp8_f32 v118, v110, v111 op_sel:[0,0,1]
	v_cvt_pk_fp8_f32 v119, v114, v115 op_sel:[0,0,1]
	s_nop 0
	global_store_dwordx4 v127, v[116:119], s[14:15]
	ds_read_b32 v100, v124
	ds_read_b32 v101, v124 offset:512
	ds_read_b32 v102, v124 offset:1024
	ds_read_b32 v103, v124 offset:1536
	ds_read_b32 v104, v124 offset:2048
	ds_read_b32 v105, v124 offset:2560
	ds_read_b32 v106, v124 offset:3072
	ds_read_b32 v107, v124 offset:3584
	ds_read_b32 v108, v124 offset:4096
	ds_read_b32 v109, v124 offset:4608
	ds_read_b32 v110, v124 offset:5120
	ds_read_b32 v111, v124 offset:5632
	ds_read_b32 v112, v124 offset:6144
	ds_read_b32 v113, v124 offset:6656
	ds_read_b32 v114, v124 offset:7168
	ds_read_b32 v115, v124 offset:7680
	s_waitcnt lgkmcnt(0)
	v_max_f32_e32 v100, v100, v100
	v_max_f32_e32 v101, v101, v101
	v_max_f32_e32 v102, v102, v102
	v_max_f32_e32 v103, v103, v103
	v_max_f32_e32 v104, v104, v104
	v_max_f32_e32 v105, v105, v105
	v_max_f32_e32 v106, v106, v106
	v_max_f32_e32 v107, v107, v107
	v_max_f32_e32 v108, v108, v108
	v_max_f32_e32 v109, v109, v109
	v_max_f32_e32 v110, v110, v110
	v_max_f32_e32 v111, v111, v111
	v_max_f32_e32 v112, v112, v112
	v_max_f32_e32 v113, v113, v113
	v_max_f32_e32 v114, v114, v114
	v_max_f32_e32 v115, v115, v115
	v_med3_f32 v100, v100, s20, v129
	v_med3_f32 v101, v101, s20, v129
	v_med3_f32 v102, v102, s20, v129
	v_med3_f32 v103, v103, s20, v129
	v_med3_f32 v104, v104, s20, v129
	v_med3_f32 v105, v105, s20, v129
	v_med3_f32 v106, v106, s20, v129
	v_med3_f32 v107, v107, s20, v129
	v_med3_f32 v108, v108, s20, v129
	v_med3_f32 v109, v109, s20, v129
	v_med3_f32 v110, v110, s20, v129
	v_med3_f32 v111, v111, s20, v129
	v_med3_f32 v112, v112, s20, v129
	v_med3_f32 v113, v113, s20, v129
	v_med3_f32 v114, v114, s20, v129
	v_med3_f32 v115, v115, s20, v129
	v_mov_b32_e32 v116, 0
	v_mov_b32_e32 v117, 0
	v_mov_b32_e32 v118, 0
	v_mov_b32_e32 v119, 0
	v_cvt_pk_fp8_f32 v116, v100, v101
	v_cvt_pk_fp8_f32 v117, v104, v105
	v_cvt_pk_fp8_f32 v118, v108, v109
	v_cvt_pk_fp8_f32 v119, v112, v113
	v_cvt_pk_fp8_f32 v116, v102, v103 op_sel:[0,0,1]
	v_cvt_pk_fp8_f32 v117, v106, v107 op_sel:[0,0,1]
	v_cvt_pk_fp8_f32 v118, v110, v111 op_sel:[0,0,1]
	v_cvt_pk_fp8_f32 v119, v114, v115 op_sel:[0,0,1]
	s_nop 0
	global_store_dwordx4 v128, v[116:119], s[14:15]
	s_waitcnt vmcnt(12)
	v_mul_f32_e32 v68, 0x43000000, v68
	v_mul_f32_e32 v69, 0x43000000, v69
	v_mul_f32_e32 v70, 0x43000000, v70
	v_mul_f32_e32 v71, 0x43000000, v71
	ds_write_b128 v121, v[68:71]
	v_mul_f32_e32 v72, 0x43000000, v72
	v_mul_f32_e32 v73, 0x43000000, v73
	v_mul_f32_e32 v74, 0x43000000, v74
	v_mul_f32_e32 v75, 0x43000000, v75
	ds_write_b128 v121, v[72:75] offset:1024
	v_mul_f32_e32 v76, 0x43000000, v76
	v_mul_f32_e32 v77, 0x43000000, v77
	v_mul_f32_e32 v78, 0x43000000, v78
	v_mul_f32_e32 v79, 0x43000000, v79
	ds_write_b128 v121, v[76:79] offset:2048
	v_mul_f32_e32 v80, 0x43000000, v80
	v_mul_f32_e32 v81, 0x43000000, v81
	v_mul_f32_e32 v82, 0x43000000, v82
	v_mul_f32_e32 v83, 0x43000000, v83
	ds_write_b128 v121, v[80:83] offset:3072
	v_mul_f32_e32 v84, 0x43000000, v84
	v_mul_f32_e32 v85, 0x43000000, v85
	v_mul_f32_e32 v86, 0x43000000, v86
	v_mul_f32_e32 v87, 0x43000000, v87
	ds_write_b128 v121, v[84:87] offset:4096
	v_mul_f32_e32 v88, 0x43000000, v88
	v_mul_f32_e32 v89, 0x43000000, v89
	v_mul_f32_e32 v90, 0x43000000, v90
	v_mul_f32_e32 v91, 0x43000000, v91
	ds_write_b128 v121, v[88:91] offset:5120
	v_mul_f32_e32 v92, 0x43000000, v92
	v_mul_f32_e32 v93, 0x43000000, v93
	v_mul_f32_e32 v94, 0x43000000, v94
	v_mul_f32_e32 v95, 0x43000000, v95
	ds_write_b128 v121, v[92:95] offset:6144
	v_mul_f32_e32 v96, 0x43000000, v96
	v_mul_f32_e32 v97, 0x43000000, v97
	v_mul_f32_e32 v98, 0x43000000, v98
	v_mul_f32_e32 v99, 0x43000000, v99
	ds_write_b128 v121, v[96:99] offset:7168
	s_waitcnt lgkmcnt(0)
	s_barrier
; #define GAS __attribute__((address_space(1)))
; #define LAS __attribute__((address_space(3)))
; #define LDS_WAIT() asm volatile("s_waitcnt lgkmcnt(0)" ::: "memory")
; __device__ __forceinline__ unsigned pk4_fp8(float a, float b, float c, float d) {
;     a = fminf(fmaxf(a, -448.f), 448.f); b = fminf(fmaxf(b, -448.f), 448.f); c = fminf(fmaxf(c, -448.f), 448.f); d = fminf(fmaxf(d, -448.f), 448.f);
;     int w = __builtin_amdgcn_cvt_pk_fp8_f32(a, b, 0, false); w = __builtin_amdgcn_cvt_pk_fp8_f32(c, d, w, true); return (unsigned)w; }
;     const int pr = item >> 1, kb = 2 * (pr / nblk) + (item & 1), nb = pr % nblk, k0 = 64 * kb, n0 = 32 * nb;
;     const int nr = n0 + (lane & 31); const int sc = MAP == 1 ? src_col_in(nr) : nr;
;     float v[32];
; #pragma unroll
;     for (int i = 0; i < 32; ++i) v[i] = sc >= 0 ? W[(size_t)(k0 + 2 * i + (lane >> 5)) * Nsrc + sc] : 0.f;
; #pragma unroll
;     for (int i = 0; i < 32; ++i) { const int k = k0 + 2 * i + (lane >> 5); float x = v[i] * wscale; if (KS) x *= (k < ksplit ? ksA[k] : ksB[k - ksplit]); scr[(2 * i + (lane >> 5)) * 33 + (lane & 31)] = x; }
;     LDS_WAIT(); asm volatile("" ::: "memory");
;     const int c = lane & 7;
; #pragma unroll
;     for (int j = 0; j < 4; ++j) { const int n = (lane >> 3) + 8 * j; const LAS float* s = scr + (8 * c) * 33 + n;
;         const unsigned long long o = (unsigned long long)pg8::pk4_fp8(s[0 * 33], s[1 * 33], s[2 * 33], s[3 * 33]) | ((unsigned long long)pg8::pk4_fp8(s[4 * 33], s[5 * 33], s[6 * 33], s[7 * 33]) << 32);
;         *(GAS unsigned long long*)(WT + (size_t)(n0 + n) * K + k0 + 8 * c) = o; }
;     LDS_WAIT(); asm volatile("" ::: "memory");
; }
	s_add_i32 s17, s16, 2592
	s_min_u32 s17, s17, 0xbff
	s_lshr_b32 s18, s17, 5
	s_add_i32 s18, s18, 32
	s_and_b32 s19, s17, 31
	s_lshl_b32 s18, s18, 21
	s_lshl_b32 s19, s19, 9
	s_add_u32 s18, s18, s19
	s_add_u32 s12, s2, s18
	s_addc_u32 s13, s3, 0
	global_load_dwordx4 v[68:71], v126, s[12:13]
	s_add_u32 s12, s12, 0x8000
	s_addc_u32 s13, s13, 0
	global_load_dwordx4 v[72:75], v126, s[12:13]
	s_add_u32 s12, s12, 0x8000
	s_addc_u32 s13, s13, 0
	global_load_dwordx4 v[76:79], v126, s[12:13]
	s_add_u32 s12, s12, 0x8000
	s_addc_u32 s13, s13, 0
	global_load_dwordx4 v[80:83], v126, s[12:13]
	s_add_u32 s12, s12, 0x8000
	s_addc_u32 s13, s13, 0
	global_load_dwordx4 v[84:87], v126, s[12:13]
	s_add_u32 s12, s12, 0x8000
	s_addc_u32 s13, s13, 0
	global_load_dwordx4 v[88:91], v126, s[12:13]
	s_add_u32 s12, s12, 0x8000
	s_addc_u32 s13, s13, 0
	global_load_dwordx4 v[92:95], v126, s[12:13]
	s_add_u32 s12, s12, 0x8000
	s_addc_u32 s13, s13, 0
	global_load_dwordx4 v[96:99], v126, s[12:13]
	s_add_i32 s17, s16, 2400
	s_min_u32 s17, s17, 0xbff
	s_lshr_b32 s18, s17, 5
	s_add_i32 s18, s18, 32
	s_and_b32 s19, s17, 31
	s_lshl_b32 s19, s19, 21
	s_lshl_b32 s18, s18, 7
	s_add_u32 s18, s18, s19
	s_add_u32 s14, s4, s18
	s_addc_u32 s15, s5, 0
	ds_read_b32 v100, v123
	ds_read_b32 v101, v123 offset:512
	ds_read_b32 v102, v123 offset:1024
	ds_read_b32 v103, v123 offset:1536
	ds_read_b32 v104, v123 offset:2048
	ds_read_b32 v105, v123 offset:2560
	ds_read_b32 v106, v123 offset:3072
	ds_read_b32 v107, v123 offset:3584
	ds_read_b32 v108, v123 offset:4096
	ds_read_b32 v109, v123 offset:4608
	ds_read_b32 v110, v123 offset:5120
	ds_read_b32 v111, v123 offset:5632
	ds_read_b32 v112, v123 offset:6144
	ds_read_b32 v113, v123 offset:6656
	ds_read_b32 v114, v123 offset:7168
	ds_read_b32 v115, v123 offset:7680
	s_waitcnt lgkmcnt(0)
	v_max_f32_e32 v100, v100, v100
	v_max_f32_e32 v101, v101, v101
	v_max_f32_e32 v102, v102, v102
	v_max_f32_e32 v103, v103, v103
	v_max_f32_e32 v104, v104, v104
	v_max_f32_e32 v105, v105, v105
	v_max_f32_e32 v106, v106, v106
	v_max_f32_e32 v107, v107, v107
	v_max_f32_e32 v108, v108, v108
	v_max_f32_e32 v109, v109, v109
	v_max_f32_e32 v110, v110, v110
	v_max_f32_e32 v111, v111, v111
	v_max_f32_e32 v112, v112, v112
	v_max_f32_e32 v113, v113, v113
	v_max_f32_e32 v114, v114, v114
	v_max_f32_e32 v115, v115, v115
	v_med3_f32 v100, v100, s20, v129
	v_med3_f32 v101, v101, s20, v129
	v_med3_f32 v102, v102, s20, v129
	v_med3_f32 v103, v103, s20, v129
	v_med3_f32 v104, v104, s20, v129
	v_med3_f32 v105, v105, s20, v129
	v_med3_f32 v106, v106, s20, v129
	v_med3_f32 v107, v107, s20, v129
	v_med3_f32 v108, v108, s20, v129
	v_med3_f32 v109, v109, s20, v129
	v_med3_f32 v110, v110, s20, v129
	v_med3_f32 v111, v111, s20, v129
	v_med3_f32 v112, v112, s20, v129
	v_med3_f32 v113, v113, s20, v129
	v_med3_f32 v114, v114, s20, v129
	v_med3_f32 v115, v115, s20, v129
	v_mov_b32_e32 v116, 0
	v_mov_b32_e32 v117, 0
	v_mov_b32_e32 v118, 0
	v_mov_b32_e32 v119, 0
	v_cvt_pk_fp8_f32 v116, v100, v101
	v_cvt_pk_fp8_f32 v117, v104, v105
	v_cvt_pk_fp8_f32 v118, v108, v109
	v_cvt_pk_fp8_f32 v119, v112, v113
	v_cvt_pk_fp8_f32 v116, v102, v103 op_sel:[0,0,1]
	v_cvt_pk_fp8_f32 v117, v106, v107 op_sel:[0,0,1]
	v_cvt_pk_fp8_f32 v118, v110, v111 op_sel:[0,0,1]
	v_cvt_pk_fp8_f32 v119, v114, v115 op_sel:[0,0,1]
	s_nop 0
	global_store_dwordx4 v127, v[116:119], s[14:15]
	ds_read_b32 v100, v125
	ds_read_b32 v101, v125 offset:512
	ds_read_b32 v102, v125 offset:1024
	ds_read_b32 v103, v125 offset:1536
	ds_read_b32 v104, v125 offset:2048
	ds_read_b32 v105, v125 offset:2560
	ds_read_b32 v106, v125 offset:3072
	ds_read_b32 v107, v125 offset:3584
	ds_read_b32 v108, v125 offset:4096
	ds_read_b32 v109, v125 offset:4608
	ds_read_b32 v110, v125 offset:5120
	ds_read_b32 v111, v125 offset:5632
	ds_read_b32 v112, v125 offset:6144
	ds_read_b32 v113, v125 offset:6656
	ds_read_b32 v114, v125 offset:7168
	ds_read_b32 v115, v125 offset:7680
	s_waitcnt lgkmcnt(0)
	v_max_f32_e32 v100, v100, v100
	v_max_f32_e32 v101, v101, v101
	v_max_f32_e32 v102, v102, v102
	v_max_f32_e32 v103, v103, v103
	v_max_f32_e32 v104, v104, v104
	v_max_f32_e32 v105, v105, v105
	v_max_f32_e32 v106, v106, v106
	v_max_f32_e32 v107, v107, v107
	v_max_f32_e32 v108, v108, v108
	v_max_f32_e32 v109, v109, v109
	v_max_f32_e32 v110, v110, v110
	v_max_f32_e32 v111, v111, v111
	v_max_f32_e32 v112, v112, v112
	v_max_f32_e32 v113, v113, v113
	v_max_f32_e32 v114, v114, v114
	v_max_f32_e32 v115, v115, v115
	v_med3_f32 v100, v100, s20, v129
	v_med3_f32 v101, v101, s20, v129
	v_med3_f32 v102, v102, s20, v129
	v_med3_f32 v103, v103, s20, v129
	v_med3_f32 v104, v104, s20, v129
	v_med3_f32 v105, v105, s20, v129
	v_med3_f32 v106, v106, s20, v129
	v_med3_f32 v107, v107, s20, v129
	v_med3_f32 v108, v108, s20, v129
	v_med3_f32 v109, v109, s20, v129
	v_med3_f32 v110, v110, s20, v129
	v_med3_f32 v111, v111, s20, v129
	v_med3_f32 v112, v112, s20, v129
	v_med3_f32 v113, v113, s20, v129
	v_med3_f32 v114, v114, s20, v129
	v_med3_f32 v115, v115, s20, v129
	v_mov_b32_e32 v116, 0
	v_mov_b32_e32 v117, 0
	v_mov_b32_e32 v118, 0
	v_mov_b32_e32 v119, 0
	v_cvt_pk_fp8_f32 v116, v100, v101
	v_cvt_pk_fp8_f32 v117, v104, v105
	v_cvt_pk_fp8_f32 v118, v108, v109
	v_cvt_pk_fp8_f32 v119, v112, v113
	v_cvt_pk_fp8_f32 v116, v102, v103 op_sel:[0,0,1]
	v_cvt_pk_fp8_f32 v117, v106, v107 op_sel:[0,0,1]
	v_cvt_pk_fp8_f32 v118, v110, v111 op_sel:[0,0,1]
	v_cvt_pk_fp8_f32 v119, v114, v115 op_sel:[0,0,1]
	s_nop 0
	global_store_dwordx4 v128, v[116:119], s[14:15]
	s_waitcnt vmcnt(12)
	v_mul_f32_e32 v36, 0x43000000, v36
	v_mul_f32_e32 v37, 0x43000000, v37
	v_mul_f32_e32 v38, 0x43000000, v38
	v_mul_f32_e32 v39, 0x43000000, v39
	ds_write_b128 v120, v[36:39]
	v_mul_f32_e32 v40, 0x43000000, v40
	v_mul_f32_e32 v41, 0x43000000, v41
	v_mul_f32_e32 v42, 0x43000000, v42
	v_mul_f32_e32 v43, 0x43000000, v43
	ds_write_b128 v120, v[40:43] offset:1024
	v_mul_f32_e32 v44, 0x43000000, v44
	v_mul_f32_e32 v45, 0x43000000, v45
	v_mul_f32_e32 v46, 0x43000000, v46
	v_mul_f32_e32 v47, 0x43000000, v47
	ds_write_b128 v120, v[44:47] offset:2048
	v_mul_f32_e32 v48, 0x43000000, v48
	v_mul_f32_e32 v49, 0x43000000, v49
	v_mul_f32_e32 v50, 0x43000000, v50
	v_mul_f32_e32 v51, 0x43000000, v51
	ds_write_b128 v120, v[48:51] offset:3072
	v_mul_f32_e32 v52, 0x43000000, v52
	v_mul_f32_e32 v53, 0x43000000, v53
	v_mul_f32_e32 v54, 0x43000000, v54
	v_mul_f32_e32 v55, 0x43000000, v55
	ds_write_b128 v120, v[52:55] offset:4096
	v_mul_f32_e32 v56, 0x43000000, v56
	v_mul_f32_e32 v57, 0x43000000, v57
	v_mul_f32_e32 v58, 0x43000000, v58
	v_mul_f32_e32 v59, 0x43000000, v59
	ds_write_b128 v120, v[56:59] offset:5120
	v_mul_f32_e32 v60, 0x43000000, v60
	v_mul_f32_e32 v61, 0x43000000, v61
	v_mul_f32_e32 v62, 0x43000000, v62
	v_mul_f32_e32 v63, 0x43000000, v63
	ds_write_b128 v120, v[60:63] offset:6144
	v_mul_f32_e32 v64, 0x43000000, v64
	v_mul_f32_e32 v65, 0x43000000, v65
	v_mul_f32_e32 v66, 0x43000000, v66
	v_mul_f32_e32 v67, 0x43000000, v67
	ds_write_b128 v120, v[64:67] offset:7168
	s_waitcnt lgkmcnt(0)
	s_barrier
; #define GAS __attribute__((address_space(1)))
; #define LAS __attribute__((address_space(3)))
; #define LDS_WAIT() asm volatile("s_waitcnt lgkmcnt(0)" ::: "memory")
; __device__ __forceinline__ unsigned pk4_fp8(float a, float b, float c, float d) {
;     a = fminf(fmaxf(a, -448.f), 448.f); b = fminf(fmaxf(b, -448.f), 448.f); c = fminf(fmaxf(c, -448.f), 448.f); d = fminf(fmaxf(d, -448.f), 448.f);
;     int w = __builtin_amdgcn_cvt_pk_fp8_f32(a, b, 0, false); w = __builtin_amdgcn_cvt_pk_fp8_f32(c, d, w, true); return (unsigned)w; }
;     const int pr = item >> 1, kb = 2 * (pr / nblk) + (item & 1), nb = pr % nblk, k0 = 64 * kb, n0 = 32 * nb;
;     const int nr = n0 + (lane & 31); const int sc = MAP == 1 ? src_col_in(nr) : nr;
;     float v[32];
; #pragma unroll
;     for (int i = 0; i < 32; ++i) v[i] = sc >= 0 ? W[(size_t)(k0 + 2 * i + (lane >> 5)) * Nsrc + sc] : 0.f;
; #pragma unroll
;     for (int i = 0; i < 32; ++i) { const int k = k0 + 2 * i + (lane >> 5); float x = v[i] * wscale; if (KS) x *= (k < ksplit ? ksA[k] : ksB[k - ksplit]); scr[(2 * i + (lane >> 5)) * 33 + (lane & 31)] = x; }
;     LDS_WAIT(); asm volatile("" ::: "memory");
;     const int c = lane & 7;
; #pragma unroll
;     for (int j = 0; j < 4; ++j) { const int n = (lane >> 3) + 8 * j; const LAS float* s = scr + (8 * c) * 33 + n;
;         const unsigned long long o = (unsigned long long)pg8::pk4_fp8(s[0 * 33], s[1 * 33], s[2 * 33], s[3 * 33]) | ((unsigned long long)pg8::pk4_fp8(s[4 * 33], s[5 * 33], s[6 * 33], s[7 * 33]) << 32);
;         *(GAS unsigned long long*)(WT + (size_t)(n0 + n) * K + k0 + 8 * c) = o; }
;     LDS_WAIT(); asm volatile("" ::: "memory");
; }
	s_add_i32 s17, s16, 2688
	s_min_u32 s17, s17, 0xbff
	s_lshr_b32 s18, s17, 5
	s_add_i32 s18, s18, 32
	s_and_b32 s19, s17, 31
	s_lshl_b32 s18, s18, 21
	s_lshl_b32 s19, s19, 9
	s_add_u32 s18, s18, s19
	s_add_u32 s12, s2, s18
	s_addc_u32 s13, s3, 0
	global_load_dwordx4 v[36:39], v126, s[12:13]
	s_add_u32 s12, s12, 0x8000
	s_addc_u32 s13, s13, 0
	global_load_dwordx4 v[40:43], v126, s[12:13]
	s_add_u32 s12, s12, 0x8000
	s_addc_u32 s13, s13, 0
	global_load_dwordx4 v[44:47], v126, s[12:13]
	s_add_u32 s12, s12, 0x8000
	s_addc_u32 s13, s13, 0
	global_load_dwordx4 v[48:51], v126, s[12:13]
	s_add_u32 s12, s12, 0x8000
	s_addc_u32 s13, s13, 0
	global_load_dwordx4 v[52:55], v126, s[12:13]
	s_add_u32 s12, s12, 0x8000
	s_addc_u32 s13, s13, 0
	global_load_dwordx4 v[56:59], v126, s[12:13]
	s_add_u32 s12, s12, 0x8000
	s_addc_u32 s13, s13, 0
	global_load_dwordx4 v[60:63], v126, s[12:13]
	s_add_u32 s12, s12, 0x8000
	s_addc_u32 s13, s13, 0
	global_load_dwordx4 v[64:67], v126, s[12:13]
	s_add_i32 s17, s16, 2496
	s_min_u32 s17, s17, 0xbff
	s_lshr_b32 s18, s17, 5
	s_add_i32 s18, s18, 32
	s_and_b32 s19, s17, 31
	s_lshl_b32 s19, s19, 21
	s_lshl_b32 s18, s18, 7
	s_add_u32 s18, s18, s19
	s_add_u32 s14, s4, s18
	s_addc_u32 s15, s5, 0
	ds_read_b32 v100, v122
	ds_read_b32 v101, v122 offset:512
	ds_read_b32 v102, v122 offset:1024
	ds_read_b32 v103, v122 offset:1536
	ds_read_b32 v104, v122 offset:2048
	ds_read_b32 v105, v122 offset:2560
	ds_read_b32 v106, v122 offset:3072
	ds_read_b32 v107, v122 offset:3584
	ds_read_b32 v108, v122 offset:4096
	ds_read_b32 v109, v122 offset:4608
	ds_read_b32 v110, v122 offset:5120
	ds_read_b32 v111, v122 offset:5632
	ds_read_b32 v112, v122 offset:6144
	ds_read_b32 v113, v122 offset:6656
	ds_read_b32 v114, v122 offset:7168
	ds_read_b32 v115, v122 offset:7680
	s_waitcnt lgkmcnt(0)
	v_max_f32_e32 v100, v100, v100
	v_max_f32_e32 v101, v101, v101
	v_max_f32_e32 v102, v102, v102
	v_max_f32_e32 v103, v103, v103
	v_max_f32_e32 v104, v104, v104
	v_max_f32_e32 v105, v105, v105
	v_max_f32_e32 v106, v106, v106
	v_max_f32_e32 v107, v107, v107
	v_max_f32_e32 v108, v108, v108
	v_max_f32_e32 v109, v109, v109
	v_max_f32_e32 v110, v110, v110
	v_max_f32_e32 v111, v111, v111
	v_max_f32_e32 v112, v112, v112
	v_max_f32_e32 v113, v113, v113
	v_max_f32_e32 v114, v114, v114
	v_max_f32_e32 v115, v115, v115
	v_med3_f32 v100, v100, s20, v129
	v_med3_f32 v101, v101, s20, v129
	v_med3_f32 v102, v102, s20, v129
	v_med3_f32 v103, v103, s20, v129
	v_med3_f32 v104, v104, s20, v129
	v_med3_f32 v105, v105, s20, v129
	v_med3_f32 v106, v106, s20, v129
	v_med3_f32 v107, v107, s20, v129
	v_med3_f32 v108, v108, s20, v129
	v_med3_f32 v109, v109, s20, v129
	v_med3_f32 v110, v110, s20, v129
	v_med3_f32 v111, v111, s20, v129
	v_med3_f32 v112, v112, s20, v129
	v_med3_f32 v113, v113, s20, v129
	v_med3_f32 v114, v114, s20, v129
	v_med3_f32 v115, v115, s20, v129
	v_mov_b32_e32 v116, 0
	v_mov_b32_e32 v117, 0
	v_mov_b32_e32 v118, 0
	v_mov_b32_e32 v119, 0
	v_cvt_pk_fp8_f32 v116, v100, v101
	v_cvt_pk_fp8_f32 v117, v104, v105
	v_cvt_pk_fp8_f32 v118, v108, v109
	v_cvt_pk_fp8_f32 v119, v112, v113
	v_cvt_pk_fp8_f32 v116, v102, v103 op_sel:[0,0,1]
	v_cvt_pk_fp8_f32 v117, v106, v107 op_sel:[0,0,1]
	v_cvt_pk_fp8_f32 v118, v110, v111 op_sel:[0,0,1]
	v_cvt_pk_fp8_f32 v119, v114, v115 op_sel:[0,0,1]
	s_nop 0
	global_store_dwordx4 v127, v[116:119], s[14:15]
	ds_read_b32 v100, v124
	ds_read_b32 v101, v124 offset:512
	ds_read_b32 v102, v124 offset:1024
	ds_read_b32 v103, v124 offset:1536
	ds_read_b32 v104, v124 offset:2048
	ds_read_b32 v105, v124 offset:2560
	ds_read_b32 v106, v124 offset:3072
	ds_read_b32 v107, v124 offset:3584
	ds_read_b32 v108, v124 offset:4096
	ds_read_b32 v109, v124 offset:4608
	ds_read_b32 v110, v124 offset:5120
	ds_read_b32 v111, v124 offset:5632
	ds_read_b32 v112, v124 offset:6144
	ds_read_b32 v113, v124 offset:6656
	ds_read_b32 v114, v124 offset:7168
	ds_read_b32 v115, v124 offset:7680
	s_waitcnt lgkmcnt(0)
	v_max_f32_e32 v100, v100, v100
	v_max_f32_e32 v101, v101, v101
	v_max_f32_e32 v102, v102, v102
	v_max_f32_e32 v103, v103, v103
	v_max_f32_e32 v104, v104, v104
	v_max_f32_e32 v105, v105, v105
	v_max_f32_e32 v106, v106, v106
	v_max_f32_e32 v107, v107, v107
	v_max_f32_e32 v108, v108, v108
	v_max_f32_e32 v109, v109, v109
	v_max_f32_e32 v110, v110, v110
	v_max_f32_e32 v111, v111, v111
	v_max_f32_e32 v112, v112, v112
	v_max_f32_e32 v113, v113, v113
	v_max_f32_e32 v114, v114, v114
	v_max_f32_e32 v115, v115, v115
	v_med3_f32 v100, v100, s20, v129
	v_med3_f32 v101, v101, s20, v129
	v_med3_f32 v102, v102, s20, v129
	v_med3_f32 v103, v103, s20, v129
	v_med3_f32 v104, v104, s20, v129
	v_med3_f32 v105, v105, s20, v129
	v_med3_f32 v106, v106, s20, v129
	v_med3_f32 v107, v107, s20, v129
	v_med3_f32 v108, v108, s20, v129
	v_med3_f32 v109, v109, s20, v129
	v_med3_f32 v110, v110, s20, v129
	v_med3_f32 v111, v111, s20, v129
	v_med3_f32 v112, v112, s20, v129
	v_med3_f32 v113, v113, s20, v129
	v_med3_f32 v114, v114, s20, v129
	v_med3_f32 v115, v115, s20, v129
	v_mov_b32_e32 v116, 0
	v_mov_b32_e32 v117, 0
	v_mov_b32_e32 v118, 0
	v_mov_b32_e32 v119, 0
	v_cvt_pk_fp8_f32 v116, v100, v101
	v_cvt_pk_fp8_f32 v117, v104, v105
	v_cvt_pk_fp8_f32 v118, v108, v109
	v_cvt_pk_fp8_f32 v119, v112, v113
	v_cvt_pk_fp8_f32 v116, v102, v103 op_sel:[0,0,1]
	v_cvt_pk_fp8_f32 v117, v106, v107 op_sel:[0,0,1]
	v_cvt_pk_fp8_f32 v118, v110, v111 op_sel:[0,0,1]
	v_cvt_pk_fp8_f32 v119, v114, v115 op_sel:[0,0,1]
	s_nop 0
	global_store_dwordx4 v128, v[116:119], s[14:15]
	s_waitcnt vmcnt(12)
	v_mul_f32_e32 v68, 0x43000000, v68
	v_mul_f32_e32 v69, 0x43000000, v69
	v_mul_f32_e32 v70, 0x43000000, v70
	v_mul_f32_e32 v71, 0x43000000, v71
	ds_write_b128 v121, v[68:71]
	v_mul_f32_e32 v72, 0x43000000, v72
	v_mul_f32_e32 v73, 0x43000000, v73
	v_mul_f32_e32 v74, 0x43000000, v74
	v_mul_f32_e32 v75, 0x43000000, v75
	ds_write_b128 v121, v[72:75] offset:1024
	v_mul_f32_e32 v76, 0x43000000, v76
	v_mul_f32_e32 v77, 0x43000000, v77
	v_mul_f32_e32 v78, 0x43000000, v78
	v_mul_f32_e32 v79, 0x43000000, v79
	ds_write_b128 v121, v[76:79] offset:2048
	v_mul_f32_e32 v80, 0x43000000, v80
	v_mul_f32_e32 v81, 0x43000000, v81
	v_mul_f32_e32 v82, 0x43000000, v82
	v_mul_f32_e32 v83, 0x43000000, v83
	ds_write_b128 v121, v[80:83] offset:3072
	v_mul_f32_e32 v84, 0x43000000, v84
	v_mul_f32_e32 v85, 0x43000000, v85
	v_mul_f32_e32 v86, 0x43000000, v86
	v_mul_f32_e32 v87, 0x43000000, v87
	ds_write_b128 v121, v[84:87] offset:4096
	v_mul_f32_e32 v88, 0x43000000, v88
	v_mul_f32_e32 v89, 0x43000000, v89
	v_mul_f32_e32 v90, 0x43000000, v90
	v_mul_f32_e32 v91, 0x43000000, v91
	ds_write_b128 v121, v[88:91] offset:5120
	v_mul_f32_e32 v92, 0x43000000, v92
	v_mul_f32_e32 v93, 0x43000000, v93
	v_mul_f32_e32 v94, 0x43000000, v94
	v_mul_f32_e32 v95, 0x43000000, v95
	ds_write_b128 v121, v[92:95] offset:6144
	v_mul_f32_e32 v96, 0x43000000, v96
	v_mul_f32_e32 v97, 0x43000000, v97
	v_mul_f32_e32 v98, 0x43000000, v98
	v_mul_f32_e32 v99, 0x43000000, v99
	ds_write_b128 v121, v[96:99] offset:7168
	s_waitcnt lgkmcnt(0)
	s_barrier
; #define GAS __attribute__((address_space(1)))
; #define LAS __attribute__((address_space(3)))
; #define LDS_WAIT() asm volatile("s_waitcnt lgkmcnt(0)" ::: "memory")
; __device__ __forceinline__ unsigned pk4_fp8(float a, float b, float c, float d) {
;     a = fminf(fmaxf(a, -448.f), 448.f); b = fminf(fmaxf(b, -448.f), 448.f); c = fminf(fmaxf(c, -448.f), 448.f); d = fminf(fmaxf(d, -448.f), 448.f);
;     int w = __builtin_amdgcn_cvt_pk_fp8_f32(a, b, 0, false); w = __builtin_amdgcn_cvt_pk_fp8_f32(c, d, w, true); return (unsigned)w; }
;     const int pr = item >> 1, kb = 2 * (pr / nblk) + (item & 1), nb = pr % nblk, k0 = 64 * kb, n0 = 32 * nb;
;     const int nr = n0 + (lane & 31); const int sc = MAP == 1 ? src_col_in(nr) : nr;
;     float v[32];
; #pragma unroll
;     for (int i = 0; i < 32; ++i) v[i] = sc >= 0 ? W[(size_t)(k0 + 2 * i + (lane >> 5)) * Nsrc + sc] : 0.f;
; #pragma unroll
;     for (int i = 0; i < 32; ++i) { const int k = k0 + 2 * i + (lane >> 5); float x = v[i] * wscale; if (KS) x *= (k < ksplit ? ksA[k] : ksB[k - ksplit]); scr[(2 * i + (lane >> 5)) * 33 + (lane & 31)] = x; }
;     LDS_WAIT(); asm volatile("" ::: "memory");
;     const int c = lane & 7;
; #pragma unroll
;     for (int j = 0; j < 4; ++j) { const int n = (lane >> 3) + 8 * j; const LAS float* s = scr + (8 * c) * 33 + n;
;         const unsigned long long o = (unsigned long long)pg8::pk4_fp8(s[0 * 33], s[1 * 33], s[2 * 33], s[3 * 33]) | ((unsigned long long)pg8::pk4_fp8(s[4 * 33], s[5 * 33], s[6 * 33], s[7 * 33]) << 32);
;         *(GAS unsigned long long*)(WT + (size_t)(n0 + n) * K + k0 + 8 * c) = o; }
;     LDS_WAIT(); asm volatile("" ::: "memory");
; }
	s_add_i32 s17, s16, 2784
	s_min_u32 s17, s17, 0xbff
	s_lshr_b32 s18, s17, 5
	s_add_i32 s18, s18, 32
	s_and_b32 s19, s17, 31
	s_lshl_b32 s18, s18, 21
	s_lshl_b32 s19, s19, 9
	s_add_u32 s18, s18, s19
	s_add_u32 s12, s2, s18
	s_addc_u32 s13, s3, 0
	global_load_dwordx4 v[68:71], v126, s[12:13]
	s_add_u32 s12, s12, 0x8000
	s_addc_u32 s13, s13, 0
	global_load_dwordx4 v[72:75], v126, s[12:13]
	s_add_u32 s12, s12, 0x8000
	s_addc_u32 s13, s13, 0
	global_load_dwordx4 v[76:79], v126, s[12:13]
	s_add_u32 s12, s12, 0x8000
	s_addc_u32 s13, s13, 0
	global_load_dwordx4 v[80:83], v126, s[12:13]
	s_add_u32 s12, s12, 0x8000
	s_addc_u32 s13, s13, 0
	global_load_dwordx4 v[84:87], v126, s[12:13]
	s_add_u32 s12, s12, 0x8000
	s_addc_u32 s13, s13, 0
	global_load_dwordx4 v[88:91], v126, s[12:13]
	s_add_u32 s12, s12, 0x8000
	s_addc_u32 s13, s13, 0
	global_load_dwordx4 v[92:95], v126, s[12:13]
	s_add_u32 s12, s12, 0x8000
	s_addc_u32 s13, s13, 0
	global_load_dwordx4 v[96:99], v126, s[12:13]
	s_add_i32 s17, s16, 2592
	s_min_u32 s17, s17, 0xbff
	s_lshr_b32 s18, s17, 5
	s_add_i32 s18, s18, 32
	s_and_b32 s19, s17, 31
	s_lshl_b32 s19, s19, 21
	s_lshl_b32 s18, s18, 7
	s_add_u32 s18, s18, s19
	s_add_u32 s14, s4, s18
	s_addc_u32 s15, s5, 0
	ds_read_b32 v100, v123
	ds_read_b32 v101, v123 offset:512
	ds_read_b32 v102, v123 offset:1024
	ds_read_b32 v103, v123 offset:1536
	ds_read_b32 v104, v123 offset:2048
	ds_read_b32 v105, v123 offset:2560
	ds_read_b32 v106, v123 offset:3072
	ds_read_b32 v107, v123 offset:3584
	ds_read_b32 v108, v123 offset:4096
	ds_read_b32 v109, v123 offset:4608
	ds_read_b32 v110, v123 offset:5120
	ds_read_b32 v111, v123 offset:5632
	ds_read_b32 v112, v123 offset:6144
	ds_read_b32 v113, v123 offset:6656
	ds_read_b32 v114, v123 offset:7168
	ds_read_b32 v115, v123 offset:7680
	s_waitcnt lgkmcnt(0)
	v_max_f32_e32 v100, v100, v100
	v_max_f32_e32 v101, v101, v101
	v_max_f32_e32 v102, v102, v102
	v_max_f32_e32 v103, v103, v103
	v_max_f32_e32 v104, v104, v104
	v_max_f32_e32 v105, v105, v105
	v_max_f32_e32 v106, v106, v106
	v_max_f32_e32 v107, v107, v107
	v_max_f32_e32 v108, v108, v108
	v_max_f32_e32 v109, v109, v109
	v_max_f32_e32 v110, v110, v110
	v_max_f32_e32 v111, v111, v111
	v_max_f32_e32 v112, v112, v112
	v_max_f32_e32 v113, v113, v113
	v_max_f32_e32 v114, v114, v114
	v_max_f32_e32 v115, v115, v115
	v_med3_f32 v100, v100, s20, v129
	v_med3_f32 v101, v101, s20, v129
	v_med3_f32 v102, v102, s20, v129
	v_med3_f32 v103, v103, s20, v129
	v_med3_f32 v104, v104, s20, v129
	v_med3_f32 v105, v105, s20, v129
	v_med3_f32 v106, v106, s20, v129
	v_med3_f32 v107, v107, s20, v129
	v_med3_f32 v108, v108, s20, v129
	v_med3_f32 v109, v109, s20, v129
	v_med3_f32 v110, v110, s20, v129
	v_med3_f32 v111, v111, s20, v129
	v_med3_f32 v112, v112, s20, v129
	v_med3_f32 v113, v113, s20, v129
	v_med3_f32 v114, v114, s20, v129
	v_med3_f32 v115, v115, s20, v129
	v_mov_b32_e32 v116, 0
	v_mov_b32_e32 v117, 0
	v_mov_b32_e32 v118, 0
	v_mov_b32_e32 v119, 0
	v_cvt_pk_fp8_f32 v116, v100, v101
	v_cvt_pk_fp8_f32 v117, v104, v105
	v_cvt_pk_fp8_f32 v118, v108, v109
	v_cvt_pk_fp8_f32 v119, v112, v113
	v_cvt_pk_fp8_f32 v116, v102, v103 op_sel:[0,0,1]
	v_cvt_pk_fp8_f32 v117, v106, v107 op_sel:[0,0,1]
	v_cvt_pk_fp8_f32 v118, v110, v111 op_sel:[0,0,1]
	v_cvt_pk_fp8_f32 v119, v114, v115 op_sel:[0,0,1]
	s_nop 0
	global_store_dwordx4 v127, v[116:119], s[14:15]
	ds_read_b32 v100, v125
	ds_read_b32 v101, v125 offset:512
	ds_read_b32 v102, v125 offset:1024
	ds_read_b32 v103, v125 offset:1536
	ds_read_b32 v104, v125 offset:2048
	ds_read_b32 v105, v125 offset:2560
	ds_read_b32 v106, v125 offset:3072
	ds_read_b32 v107, v125 offset:3584
	ds_read_b32 v108, v125 offset:4096
	ds_read_b32 v109, v125 offset:4608
	ds_read_b32 v110, v125 offset:5120
	ds_read_b32 v111, v125 offset:5632
	ds_read_b32 v112, v125 offset:6144
	ds_read_b32 v113, v125 offset:6656
	ds_read_b32 v114, v125 offset:7168
	ds_read_b32 v115, v125 offset:7680
	s_waitcnt lgkmcnt(0)
	v_max_f32_e32 v100, v100, v100
	v_max_f32_e32 v101, v101, v101
	v_max_f32_e32 v102, v102, v102
	v_max_f32_e32 v103, v103, v103
	v_max_f32_e32 v104, v104, v104
	v_max_f32_e32 v105, v105, v105
	v_max_f32_e32 v106, v106, v106
	v_max_f32_e32 v107, v107, v107
	v_max_f32_e32 v108, v108, v108
	v_max_f32_e32 v109, v109, v109
	v_max_f32_e32 v110, v110, v110
	v_max_f32_e32 v111, v111, v111
	v_max_f32_e32 v112, v112, v112
	v_max_f32_e32 v113, v113, v113
	v_max_f32_e32 v114, v114, v114
	v_max_f32_e32 v115, v115, v115
	v_med3_f32 v100, v100, s20, v129
	v_med3_f32 v101, v101, s20, v129
	v_med3_f32 v102, v102, s20, v129
	v_med3_f32 v103, v103, s20, v129
	v_med3_f32 v104, v104, s20, v129
	v_med3_f32 v105, v105, s20, v129
	v_med3_f32 v106, v106, s20, v129
	v_med3_f32 v107, v107, s20, v129
	v_med3_f32 v108, v108, s20, v129
	v_med3_f32 v109, v109, s20, v129
	v_med3_f32 v110, v110, s20, v129
	v_med3_f32 v111, v111, s20, v129
	v_med3_f32 v112, v112, s20, v129
	v_med3_f32 v113, v113, s20, v129
	v_med3_f32 v114, v114, s20, v129
	v_med3_f32 v115, v115, s20, v129
	v_mov_b32_e32 v116, 0
	v_mov_b32_e32 v117, 0
	v_mov_b32_e32 v118, 0
	v_mov_b32_e32 v119, 0
	v_cvt_pk_fp8_f32 v116, v100, v101
	v_cvt_pk_fp8_f32 v117, v104, v105
	v_cvt_pk_fp8_f32 v118, v108, v109
	v_cvt_pk_fp8_f32 v119, v112, v113
	v_cvt_pk_fp8_f32 v116, v102, v103 op_sel:[0,0,1]
	v_cvt_pk_fp8_f32 v117, v106, v107 op_sel:[0,0,1]
	v_cvt_pk_fp8_f32 v118, v110, v111 op_sel:[0,0,1]
	v_cvt_pk_fp8_f32 v119, v114, v115 op_sel:[0,0,1]
	s_nop 0
	global_store_dwordx4 v128, v[116:119], s[14:15]
	s_waitcnt vmcnt(12)
	v_mul_f32_e32 v36, 0x43000000, v36
	v_mul_f32_e32 v37, 0x43000000, v37
	v_mul_f32_e32 v38, 0x43000000, v38
	v_mul_f32_e32 v39, 0x43000000, v39
	ds_write_b128 v120, v[36:39]
	v_mul_f32_e32 v40, 0x43000000, v40
	v_mul_f32_e32 v41, 0x43000000, v41
	v_mul_f32_e32 v42, 0x43000000, v42
	v_mul_f32_e32 v43, 0x43000000, v43
	ds_write_b128 v120, v[40:43] offset:1024
	v_mul_f32_e32 v44, 0x43000000, v44
	v_mul_f32_e32 v45, 0x43000000, v45
	v_mul_f32_e32 v46, 0x43000000, v46
	v_mul_f32_e32 v47, 0x43000000, v47
	ds_write_b128 v120, v[44:47] offset:2048
	v_mul_f32_e32 v48, 0x43000000, v48
	v_mul_f32_e32 v49, 0x43000000, v49
	v_mul_f32_e32 v50, 0x43000000, v50
	v_mul_f32_e32 v51, 0x43000000, v51
	ds_write_b128 v120, v[48:51] offset:3072
	v_mul_f32_e32 v52, 0x43000000, v52
	v_mul_f32_e32 v53, 0x43000000, v53
	v_mul_f32_e32 v54, 0x43000000, v54
	v_mul_f32_e32 v55, 0x43000000, v55
	ds_write_b128 v120, v[52:55] offset:4096
	v_mul_f32_e32 v56, 0x43000000, v56
	v_mul_f32_e32 v57, 0x43000000, v57
	v_mul_f32_e32 v58, 0x43000000, v58
	v_mul_f32_e32 v59, 0x43000000, v59
	ds_write_b128 v120, v[56:59] offset:5120
	v_mul_f32_e32 v60, 0x43000000, v60
	v_mul_f32_e32 v61, 0x43000000, v61
	v_mul_f32_e32 v62, 0x43000000, v62
	v_mul_f32_e32 v63, 0x43000000, v63
	ds_write_b128 v120, v[60:63] offset:6144
	v_mul_f32_e32 v64, 0x43000000, v64
	v_mul_f32_e32 v65, 0x43000000, v65
	v_mul_f32_e32 v66, 0x43000000, v66
	v_mul_f32_e32 v67, 0x43000000, v67
	ds_write_b128 v120, v[64:67] offset:7168
	s_waitcnt lgkmcnt(0)
	s_barrier
; #define GAS __attribute__((address_space(1)))
; #define LAS __attribute__((address_space(3)))
; #define LDS_WAIT() asm volatile("s_waitcnt lgkmcnt(0)" ::: "memory")
; __device__ __forceinline__ unsigned pk4_fp8(float a, float b, float c, float d) {
;     a = fminf(fmaxf(a, -448.f), 448.f); b = fminf(fmaxf(b, -448.f), 448.f); c = fminf(fmaxf(c, -448.f), 448.f); d = fminf(fmaxf(d, -448.f), 448.f);
;     int w = __builtin_amdgcn_cvt_pk_fp8_f32(a, b, 0, false); w = __builtin_amdgcn_cvt_pk_fp8_f32(c, d, w, true); return (unsigned)w; }
;     const int pr = item >> 1, kb = 2 * (pr / nblk) + (item & 1), nb = pr % nblk, k0 = 64 * kb, n0 = 32 * nb;
;     const int nr = n0 + (lane & 31); const int sc = MAP == 1 ? src_col_in(nr) : nr;
;     float v[32];
; #pragma unroll
;     for (int i = 0; i < 32; ++i) v[i] = sc >= 0 ? W[(size_t)(k0 + 2 * i + (lane >> 5)) * Nsrc + sc] : 0.f;
; #pragma unroll
;     for (int i = 0; i < 32; ++i) { const int k = k0 + 2 * i + (lane >> 5); float x = v[i] * wscale; if (KS) x *= (k < ksplit ? ksA[k] : ksB[k - ksplit]); scr[(2 * i + (lane >> 5)) * 33 + (lane & 31)] = x; }
;     LDS_WAIT(); asm volatile("" ::: "memory");
;     const int c = lane & 7;
; #pragma unroll
;     for (int j = 0; j < 4; ++j) { const int n = (lane >> 3) + 8 * j; const LAS float* s = scr + (8 * c) * 33 + n;
;         const unsigned long long o = (unsigned long long)pg8::pk4_fp8(s[0 * 33], s[1 * 33], s[2 * 33], s[3 * 33]) | ((unsigned long long)pg8::pk4_fp8(s[4 * 33], s[5 * 33], s[6 * 33], s[7 * 33]) << 32);
;         *(GAS unsigned long long*)(WT + (size_t)(n0 + n) * K + k0 + 8 * c) = o; }
;     LDS_WAIT(); asm volatile("" ::: "memory");
; }
	s_add_i32 s17, s16, 2880
	s_min_u32 s17, s17, 0xbff
	s_lshr_b32 s18, s17, 5
	s_add_i32 s18, s18, 32
	s_and_b32 s19, s17, 31
	s_lshl_b32 s18, s18, 21
	s_lshl_b32 s19, s19, 9
	s_add_u32 s18, s18, s19
	s_add_u32 s12, s2, s18
	s_addc_u32 s13, s3, 0
	global_load_dwordx4 v[36:39], v126, s[12:13]
	s_add_u32 s12, s12, 0x8000
	s_addc_u32 s13, s13, 0
	global_load_dwordx4 v[40:43], v126, s[12:13]
	s_add_u32 s12, s12, 0x8000
	s_addc_u32 s13, s13, 0
	global_load_dwordx4 v[44:47], v126, s[12:13]
	s_add_u32 s12, s12, 0x8000
	s_addc_u32 s13, s13, 0
	global_load_dwordx4 v[48:51], v126, s[12:13]
	s_add_u32 s12, s12, 0x8000
	s_addc_u32 s13, s13, 0
	global_load_dwordx4 v[52:55], v126, s[12:13]
	s_add_u32 s12, s12, 0x8000
	s_addc_u32 s13, s13, 0
	global_load_dwordx4 v[56:59], v126, s[12:13]
	s_add_u32 s12, s12, 0x8000
	s_addc_u32 s13, s13, 0
	global_load_dwordx4 v[60:63], v126, s[12:13]
	s_add_u32 s12, s12, 0x8000
	s_addc_u32 s13, s13, 0
	global_load_dwordx4 v[64:67], v126, s[12:13]
	s_add_i32 s17, s16, 2688
	s_min_u32 s17, s17, 0xbff
	s_lshr_b32 s18, s17, 5
	s_add_i32 s18, s18, 32
	s_and_b32 s19, s17, 31
	s_lshl_b32 s19, s19, 21
	s_lshl_b32 s18, s18, 7
	s_add_u32 s18, s18, s19
	s_add_u32 s14, s4, s18
	s_addc_u32 s15, s5, 0
	ds_read_b32 v100, v122
	ds_read_b32 v101, v122 offset:512
	ds_read_b32 v102, v122 offset:1024
	ds_read_b32 v103, v122 offset:1536
	ds_read_b32 v104, v122 offset:2048
	ds_read_b32 v105, v122 offset:2560
	ds_read_b32 v106, v122 offset:3072
	ds_read_b32 v107, v122 offset:3584
	ds_read_b32 v108, v122 offset:4096
	ds_read_b32 v109, v122 offset:4608
	ds_read_b32 v110, v122 offset:5120
	ds_read_b32 v111, v122 offset:5632
	ds_read_b32 v112, v122 offset:6144
	ds_read_b32 v113, v122 offset:6656
	ds_read_b32 v114, v122 offset:7168
	ds_read_b32 v115, v122 offset:7680
	s_waitcnt lgkmcnt(0)
	v_max_f32_e32 v100, v100, v100
	v_max_f32_e32 v101, v101, v101
	v_max_f32_e32 v102, v102, v102
	v_max_f32_e32 v103, v103, v103
	v_max_f32_e32 v104, v104, v104
	v_max_f32_e32 v105, v105, v105
	v_max_f32_e32 v106, v106, v106
	v_max_f32_e32 v107, v107, v107
	v_max_f32_e32 v108, v108, v108
	v_max_f32_e32 v109, v109, v109
	v_max_f32_e32 v110, v110, v110
	v_max_f32_e32 v111, v111, v111
	v_max_f32_e32 v112, v112, v112
	v_max_f32_e32 v113, v113, v113
	v_max_f32_e32 v114, v114, v114
	v_max_f32_e32 v115, v115, v115
	v_med3_f32 v100, v100, s20, v129
	v_med3_f32 v101, v101, s20, v129
	v_med3_f32 v102, v102, s20, v129
	v_med3_f32 v103, v103, s20, v129
	v_med3_f32 v104, v104, s20, v129
	v_med3_f32 v105, v105, s20, v129
	v_med3_f32 v106, v106, s20, v129
	v_med3_f32 v107, v107, s20, v129
	v_med3_f32 v108, v108, s20, v129
	v_med3_f32 v109, v109, s20, v129
	v_med3_f32 v110, v110, s20, v129
	v_med3_f32 v111, v111, s20, v129
	v_med3_f32 v112, v112, s20, v129
	v_med3_f32 v113, v113, s20, v129
	v_med3_f32 v114, v114, s20, v129
	v_med3_f32 v115, v115, s20, v129
	v_mov_b32_e32 v116, 0
	v_mov_b32_e32 v117, 0
	v_mov_b32_e32 v118, 0
	v_mov_b32_e32 v119, 0
	v_cvt_pk_fp8_f32 v116, v100, v101
	v_cvt_pk_fp8_f32 v117, v104, v105
	v_cvt_pk_fp8_f32 v118, v108, v109
	v_cvt_pk_fp8_f32 v119, v112, v113
	v_cvt_pk_fp8_f32 v116, v102, v103 op_sel:[0,0,1]
	v_cvt_pk_fp8_f32 v117, v106, v107 op_sel:[0,0,1]
	v_cvt_pk_fp8_f32 v118, v110, v111 op_sel:[0,0,1]
	v_cvt_pk_fp8_f32 v119, v114, v115 op_sel:[0,0,1]
	s_nop 0
	global_store_dwordx4 v127, v[116:119], s[14:15]
	ds_read_b32 v100, v124
	ds_read_b32 v101, v124 offset:512
	ds_read_b32 v102, v124 offset:1024
	ds_read_b32 v103, v124 offset:1536
	ds_read_b32 v104, v124 offset:2048
	ds_read_b32 v105, v124 offset:2560
	ds_read_b32 v106, v124 offset:3072
	ds_read_b32 v107, v124 offset:3584
	ds_read_b32 v108, v124 offset:4096
	ds_read_b32 v109, v124 offset:4608
	ds_read_b32 v110, v124 offset:5120
	ds_read_b32 v111, v124 offset:5632
	ds_read_b32 v112, v124 offset:6144
	ds_read_b32 v113, v124 offset:6656
	ds_read_b32 v114, v124 offset:7168
	ds_read_b32 v115, v124 offset:7680
	s_waitcnt lgkmcnt(0)
	v_max_f32_e32 v100, v100, v100
	v_max_f32_e32 v101, v101, v101
	v_max_f32_e32 v102, v102, v102
	v_max_f32_e32 v103, v103, v103
	v_max_f32_e32 v104, v104, v104
	v_max_f32_e32 v105, v105, v105
	v_max_f32_e32 v106, v106, v106
	v_max_f32_e32 v107, v107, v107
	v_max_f32_e32 v108, v108, v108
	v_max_f32_e32 v109, v109, v109
	v_max_f32_e32 v110, v110, v110
	v_max_f32_e32 v111, v111, v111
	v_max_f32_e32 v112, v112, v112
	v_max_f32_e32 v113, v113, v113
	v_max_f32_e32 v114, v114, v114
	v_max_f32_e32 v115, v115, v115
	v_med3_f32 v100, v100, s20, v129
	v_med3_f32 v101, v101, s20, v129
	v_med3_f32 v102, v102, s20, v129
	v_med3_f32 v103, v103, s20, v129
	v_med3_f32 v104, v104, s20, v129
	v_med3_f32 v105, v105, s20, v129
	v_med3_f32 v106, v106, s20, v129
	v_med3_f32 v107, v107, s20, v129
	v_med3_f32 v108, v108, s20, v129
	v_med3_f32 v109, v109, s20, v129
	v_med3_f32 v110, v110, s20, v129
	v_med3_f32 v111, v111, s20, v129
	v_med3_f32 v112, v112, s20, v129
	v_med3_f32 v113, v113, s20, v129
	v_med3_f32 v114, v114, s20, v129
	v_med3_f32 v115, v115, s20, v129
	v_mov_b32_e32 v116, 0
	v_mov_b32_e32 v117, 0
	v_mov_b32_e32 v118, 0
	v_mov_b32_e32 v119, 0
	v_cvt_pk_fp8_f32 v116, v100, v101
	v_cvt_pk_fp8_f32 v117, v104, v105
	v_cvt_pk_fp8_f32 v118, v108, v109
	v_cvt_pk_fp8_f32 v119, v112, v113
	v_cvt_pk_fp8_f32 v116, v102, v103 op_sel:[0,0,1]
	v_cvt_pk_fp8_f32 v117, v106, v107 op_sel:[0,0,1]
	v_cvt_pk_fp8_f32 v118, v110, v111 op_sel:[0,0,1]
	v_cvt_pk_fp8_f32 v119, v114, v115 op_sel:[0,0,1]
	s_nop 0
	global_store_dwordx4 v128, v[116:119], s[14:15]
	s_waitcnt vmcnt(12)
	v_mul_f32_e32 v68, 0x43000000, v68
	v_mul_f32_e32 v69, 0x43000000, v69
	v_mul_f32_e32 v70, 0x43000000, v70
	v_mul_f32_e32 v71, 0x43000000, v71
	ds_write_b128 v121, v[68:71]
	v_mul_f32_e32 v72, 0x43000000, v72
	v_mul_f32_e32 v73, 0x43000000, v73
	v_mul_f32_e32 v74, 0x43000000, v74
	v_mul_f32_e32 v75, 0x43000000, v75
	ds_write_b128 v121, v[72:75] offset:1024
	v_mul_f32_e32 v76, 0x43000000, v76
	v_mul_f32_e32 v77, 0x43000000, v77
	v_mul_f32_e32 v78, 0x43000000, v78
	v_mul_f32_e32 v79, 0x43000000, v79
	ds_write_b128 v121, v[76:79] offset:2048
	v_mul_f32_e32 v80, 0x43000000, v80
	v_mul_f32_e32 v81, 0x43000000, v81
	v_mul_f32_e32 v82, 0x43000000, v82
	v_mul_f32_e32 v83, 0x43000000, v83
	ds_write_b128 v121, v[80:83] offset:3072
	v_mul_f32_e32 v84, 0x43000000, v84
	v_mul_f32_e32 v85, 0x43000000, v85
	v_mul_f32_e32 v86, 0x43000000, v86
	v_mul_f32_e32 v87, 0x43000000, v87
	ds_write_b128 v121, v[84:87] offset:4096
	v_mul_f32_e32 v88, 0x43000000, v88
	v_mul_f32_e32 v89, 0x43000000, v89
	v_mul_f32_e32 v90, 0x43000000, v90
	v_mul_f32_e32 v91, 0x43000000, v91
	ds_write_b128 v121, v[88:91] offset:5120
	v_mul_f32_e32 v92, 0x43000000, v92
	v_mul_f32_e32 v93, 0x43000000, v93
	v_mul_f32_e32 v94, 0x43000000, v94
	v_mul_f32_e32 v95, 0x43000000, v95
	ds_write_b128 v121, v[92:95] offset:6144
	v_mul_f32_e32 v96, 0x43000000, v96
	v_mul_f32_e32 v97, 0x43000000, v97
	v_mul_f32_e32 v98, 0x43000000, v98
	v_mul_f32_e32 v99, 0x43000000, v99
	ds_write_b128 v121, v[96:99] offset:7168
	s_waitcnt lgkmcnt(0)
	s_barrier
; #define GAS __attribute__((address_space(1)))
; #define LAS __attribute__((address_space(3)))
; #define LDS_WAIT() asm volatile("s_waitcnt lgkmcnt(0)" ::: "memory")
;     ...
; #pragma unroll
;     for (int i = 0; i < 32; ++i) v[i] = sc >= 0 ? W[(size_t)(k0 + 2 * i + (lane >> 5)) * Nsrc + sc] : 0.f;
; #pragma unroll
;     for (int i = 0; i < 32; ++i) { const int k = k0 + 2 * i + (lane >> 5); float x = v[i] * wscale; if (KS) x *= (k < ksplit ? ksA[k] : ksB[k - ksplit]); scr[(2 * i + (lane >> 5)) * 33 + (lane & 31)] = x; }
;     LDS_WAIT(); asm volatile("" ::: "memory");
;     const int c = lane & 7;
; #pragma unroll
;     for (int j = 0; j < 4; ++j) { const int n = (lane >> 3) + 8 * j; const LAS float* s = scr + (8 * c) * 33 + n;
;         const unsigned long long o = (unsigned long long)pg8::pk4_fp8(s[0 * 33], s[1 * 33], s[2 * 33], s[3 * 33]) | ((unsigned long long)pg8::pk4_fp8(s[4 * 33], s[5 * 33], s[6 * 33], s[7 * 33]) << 32);
;         *(GAS unsigned long long*)(WT + (size_t)(n0 + n) * K + k0 + 8 * c) = o; }
; __global__ void __launch_bounds__(NWAVES * 64, 2) hybrid_fwd(Args args) {
;     ...
;             p0_transpose_item_f8<false>(args.in[16] + (size_t)l * FF * DM, FF, DM, DM / 32, (unsigned char*)(ws + WS_WDN + l * SZ_WDN), 128.f, args.in[16], args.in[16], 0, scr, r, lane);
	s_add_i32 s17, s16, 2976
	s_min_u32 s17, s17, 0xbff
	s_lshr_b32 s18, s17, 5
	s_add_i32 s18, s18, 32
	s_and_b32 s19, s17, 31
	s_lshl_b32 s18, s18, 21
	s_lshl_b32 s19, s19, 9
	s_add_u32 s18, s18, s19
	s_add_u32 s12, s2, s18
	s_addc_u32 s13, s3, 0
	global_load_dwordx4 v[68:71], v126, s[12:13]
	s_add_u32 s12, s12, 0x8000
	s_addc_u32 s13, s13, 0
	global_load_dwordx4 v[72:75], v126, s[12:13]
	s_add_u32 s12, s12, 0x8000
	s_addc_u32 s13, s13, 0
	global_load_dwordx4 v[76:79], v126, s[12:13]
	s_add_u32 s12, s12, 0x8000
	s_addc_u32 s13, s13, 0
	global_load_dwordx4 v[80:83], v126, s[12:13]
	s_add_u32 s12, s12, 0x8000
	s_addc_u32 s13, s13, 0
	global_load_dwordx4 v[84:87], v126, s[12:13]
	s_add_u32 s12, s12, 0x8000
	s_addc_u32 s13, s13, 0
	global_load_dwordx4 v[88:91], v126, s[12:13]
	s_add_u32 s12, s12, 0x8000
	s_addc_u32 s13, s13, 0
	global_load_dwordx4 v[92:95], v126, s[12:13]
	s_add_u32 s12, s12, 0x8000
	s_addc_u32 s13, s13, 0
	global_load_dwordx4 v[96:99], v126, s[12:13]
	s_add_i32 s17, s16, 2784
	s_min_u32 s17, s17, 0xbff
	s_lshr_b32 s18, s17, 5
	s_add_i32 s18, s18, 32
	s_and_b32 s19, s17, 31
	s_lshl_b32 s19, s19, 21
	s_lshl_b32 s18, s18, 7
	s_add_u32 s18, s18, s19
	s_add_u32 s14, s4, s18
	s_addc_u32 s15, s5, 0
	ds_read_b32 v100, v123
	ds_read_b32 v101, v123 offset:512
	ds_read_b32 v102, v123 offset:1024
	ds_read_b32 v103, v123 offset:1536
	ds_read_b32 v104, v123 offset:2048
	ds_read_b32 v105, v123 offset:2560
	ds_read_b32 v106, v123 offset:3072
	ds_read_b32 v107, v123 offset:3584
	ds_read_b32 v108, v123 offset:4096
	ds_read_b32 v109, v123 offset:4608
	ds_read_b32 v110, v123 offset:5120
	ds_read_b32 v111, v123 offset:5632
	ds_read_b32 v112, v123 offset:6144
	ds_read_b32 v113, v123 offset:6656
	ds_read_b32 v114, v123 offset:7168
	ds_read_b32 v115, v123 offset:7680
	s_waitcnt lgkmcnt(0)
	v_max_f32_e32 v100, v100, v100
	v_max_f32_e32 v101, v101, v101
	v_max_f32_e32 v102, v102, v102
	v_max_f32_e32 v103, v103, v103
	v_max_f32_e32 v104, v104, v104
	v_max_f32_e32 v105, v105, v105
	v_max_f32_e32 v106, v106, v106
	v_max_f32_e32 v107, v107, v107
	v_max_f32_e32 v108, v108, v108
	v_max_f32_e32 v109, v109, v109
	v_max_f32_e32 v110, v110, v110
	v_max_f32_e32 v111, v111, v111
	v_max_f32_e32 v112, v112, v112
	v_max_f32_e32 v113, v113, v113
	v_max_f32_e32 v114, v114, v114
	v_max_f32_e32 v115, v115, v115
	v_med3_f32 v100, v100, s20, v129
	v_med3_f32 v101, v101, s20, v129
	v_med3_f32 v102, v102, s20, v129
	v_med3_f32 v103, v103, s20, v129
	v_med3_f32 v104, v104, s20, v129
	v_med3_f32 v105, v105, s20, v129
	v_med3_f32 v106, v106, s20, v129
	v_med3_f32 v107, v107, s20, v129
	v_med3_f32 v108, v108, s20, v129
	v_med3_f32 v109, v109, s20, v129
	v_med3_f32 v110, v110, s20, v129
	v_med3_f32 v111, v111, s20, v129
	v_med3_f32 v112, v112, s20, v129
	v_med3_f32 v113, v113, s20, v129
	v_med3_f32 v114, v114, s20, v129
	v_med3_f32 v115, v115, s20, v129
	v_mov_b32_e32 v116, 0
	v_mov_b32_e32 v117, 0
	v_mov_b32_e32 v118, 0
	v_mov_b32_e32 v119, 0
	v_cvt_pk_fp8_f32 v116, v100, v101
	v_cvt_pk_fp8_f32 v117, v104, v105
	v_cvt_pk_fp8_f32 v118, v108, v109
	v_cvt_pk_fp8_f32 v119, v112, v113
	v_cvt_pk_fp8_f32 v116, v102, v103 op_sel:[0,0,1]
	v_cvt_pk_fp8_f32 v117, v106, v107 op_sel:[0,0,1]
	v_cvt_pk_fp8_f32 v118, v110, v111 op_sel:[0,0,1]
	v_cvt_pk_fp8_f32 v119, v114, v115 op_sel:[0,0,1]
	s_nop 0
	global_store_dwordx4 v127, v[116:119], s[14:15]
	ds_read_b32 v100, v125
	ds_read_b32 v101, v125 offset:512
	ds_read_b32 v102, v125 offset:1024
	ds_read_b32 v103, v125 offset:1536
	ds_read_b32 v104, v125 offset:2048
	ds_read_b32 v105, v125 offset:2560
	ds_read_b32 v106, v125 offset:3072
	ds_read_b32 v107, v125 offset:3584
	ds_read_b32 v108, v125 offset:4096
	ds_read_b32 v109, v125 offset:4608
	ds_read_b32 v110, v125 offset:5120
	ds_read_b32 v111, v125 offset:5632
	ds_read_b32 v112, v125 offset:6144
	ds_read_b32 v113, v125 offset:6656
	ds_read_b32 v114, v125 offset:7168
	ds_read_b32 v115, v125 offset:7680
	s_waitcnt lgkmcnt(0)
	v_max_f32_e32 v100, v100, v100
	v_max_f32_e32 v101, v101, v101
	v_max_f32_e32 v102, v102, v102
	v_max_f32_e32 v103, v103, v103
	v_max_f32_e32 v104, v104, v104
	v_max_f32_e32 v105, v105, v105
	v_max_f32_e32 v106, v106, v106
	v_max_f32_e32 v107, v107, v107
	v_max_f32_e32 v108, v108, v108
	v_max_f32_e32 v109, v109, v109
	v_max_f32_e32 v110, v110, v110
	v_max_f32_e32 v111, v111, v111
	v_max_f32_e32 v112, v112, v112
	v_max_f32_e32 v113, v113, v113
	v_max_f32_e32 v114, v114, v114
	v_max_f32_e32 v115, v115, v115
	v_med3_f32 v100, v100, s20, v129
	v_med3_f32 v101, v101, s20, v129
	v_med3_f32 v102, v102, s20, v129
	v_med3_f32 v103, v103, s20, v129
	v_med3_f32 v104, v104, s20, v129
	v_med3_f32 v105, v105, s20, v129
	v_med3_f32 v106, v106, s20, v129
	v_med3_f32 v107, v107, s20, v129
	v_med3_f32 v108, v108, s20, v129
	v_med3_f32 v109, v109, s20, v129
	v_med3_f32 v110, v110, s20, v129
	v_med3_f32 v111, v111, s20, v129
	v_med3_f32 v112, v112, s20, v129
	v_med3_f32 v113, v113, s20, v129
	v_med3_f32 v114, v114, s20, v129
	v_med3_f32 v115, v115, s20, v129
	v_mov_b32_e32 v116, 0
	v_mov_b32_e32 v117, 0
	v_mov_b32_e32 v118, 0
	v_mov_b32_e32 v119, 0
	v_cvt_pk_fp8_f32 v116, v100, v101
	v_cvt_pk_fp8_f32 v117, v104, v105
	v_cvt_pk_fp8_f32 v118, v108, v109
	v_cvt_pk_fp8_f32 v119, v112, v113
	v_cvt_pk_fp8_f32 v116, v102, v103 op_sel:[0,0,1]
	v_cvt_pk_fp8_f32 v117, v106, v107 op_sel:[0,0,1]
	v_cvt_pk_fp8_f32 v118, v110, v111 op_sel:[0,0,1]
	v_cvt_pk_fp8_f32 v119, v114, v115 op_sel:[0,0,1]
	s_nop 0
	global_store_dwordx4 v128, v[116:119], s[14:15]
	s_waitcnt vmcnt(12)
	v_mul_f32_e32 v36, 0x43000000, v36
	v_mul_f32_e32 v37, 0x43000000, v37
	v_mul_f32_e32 v38, 0x43000000, v38
	v_mul_f32_e32 v39, 0x43000000, v39
	ds_write_b128 v120, v[36:39]
	v_mul_f32_e32 v40, 0x43000000, v40
	v_mul_f32_e32 v41, 0x43000000, v41
	v_mul_f32_e32 v42, 0x43000000, v42
	v_mul_f32_e32 v43, 0x43000000, v43
	ds_write_b128 v120, v[40:43] offset:1024
	v_mul_f32_e32 v44, 0x43000000, v44
	v_mul_f32_e32 v45, 0x43000000, v45
	v_mul_f32_e32 v46, 0x43000000, v46
	v_mul_f32_e32 v47, 0x43000000, v47
	ds_write_b128 v120, v[44:47] offset:2048
	v_mul_f32_e32 v48, 0x43000000, v48
	v_mul_f32_e32 v49, 0x43000000, v49
	v_mul_f32_e32 v50, 0x43000000, v50
	v_mul_f32_e32 v51, 0x43000000, v51
	ds_write_b128 v120, v[48:51] offset:3072
	v_mul_f32_e32 v52, 0x43000000, v52
	v_mul_f32_e32 v53, 0x43000000, v53
	v_mul_f32_e32 v54, 0x43000000, v54
	v_mul_f32_e32 v55, 0x43000000, v55
	ds_write_b128 v120, v[52:55] offset:4096
	v_mul_f32_e32 v56, 0x43000000, v56
	v_mul_f32_e32 v57, 0x43000000, v57
	v_mul_f32_e32 v58, 0x43000000, v58
	v_mul_f32_e32 v59, 0x43000000, v59
	ds_write_b128 v120, v[56:59] offset:5120
	v_mul_f32_e32 v60, 0x43000000, v60
	v_mul_f32_e32 v61, 0x43000000, v61
	v_mul_f32_e32 v62, 0x43000000, v62
	v_mul_f32_e32 v63, 0x43000000, v63
	ds_write_b128 v120, v[60:63] offset:6144
	v_mul_f32_e32 v64, 0x43000000, v64
	v_mul_f32_e32 v65, 0x43000000, v65
	v_mul_f32_e32 v66, 0x43000000, v66
	v_mul_f32_e32 v67, 0x43000000, v67
	ds_write_b128 v120, v[64:67] offset:7168
	s_waitcnt lgkmcnt(0)
	s_barrier
; #define GAS __attribute__((address_space(1)))
; #define LAS __attribute__((address_space(3)))
; #define LDS_WAIT() asm volatile("s_waitcnt lgkmcnt(0)" ::: "memory")
;     ...
; #pragma unroll
;     for (int i = 0; i < 32; ++i) v[i] = sc >= 0 ? W[(size_t)(k0 + 2 * i + (lane >> 5)) * Nsrc + sc] : 0.f;
; #pragma unroll
;     for (int i = 0; i < 32; ++i) { const int k = k0 + 2 * i + (lane >> 5); float x = v[i] * wscale; if (KS) x *= (k < ksplit ? ksA[k] : ksB[k - ksplit]); scr[(2 * i + (lane >> 5)) * 33 + (lane & 31)] = x; }
;     LDS_WAIT(); asm volatile("" ::: "memory");
;     const int c = lane & 7;
; #pragma unroll
;     for (int j = 0; j < 4; ++j) { const int n = (lane >> 3) + 8 * j; const LAS float* s = scr + (8 * c) * 33 + n;
;         const unsigned long long o = (unsigned long long)pg8::pk4_fp8(s[0 * 33], s[1 * 33], s[2 * 33], s[3 * 33]) | ((unsigned long long)pg8::pk4_fp8(s[4 * 33], s[5 * 33], s[6 * 33], s[7 * 33]) << 32);
;         *(GAS unsigned long long*)(WT + (size_t)(n0 + n) * K + k0 + 8 * c) = o; }
; __global__ void __launch_bounds__(NWAVES * 64, 2) hybrid_fwd(Args args) {
;     ...
;             p0_transpose_item_f8<false>(args.in[16] + (size_t)l * FF * DM, FF, DM, DM / 32, (unsigned char*)(ws + WS_WDN + l * SZ_WDN), 128.f, args.in[16], args.in[16], 0, scr, r, lane);
	s_add_i32 s17, s16, 2880
	s_min_u32 s17, s17, 0xbff
	s_lshr_b32 s18, s17, 5
	s_add_i32 s18, s18, 32
	s_and_b32 s19, s17, 31
	s_lshl_b32 s19, s19, 21
	s_lshl_b32 s18, s18, 7
	s_add_u32 s18, s18, s19
	s_add_u32 s14, s4, s18
	s_addc_u32 s15, s5, 0
	ds_read_b32 v100, v122
	ds_read_b32 v101, v122 offset:512
	ds_read_b32 v102, v122 offset:1024
	ds_read_b32 v103, v122 offset:1536
	ds_read_b32 v104, v122 offset:2048
	ds_read_b32 v105, v122 offset:2560
	ds_read_b32 v106, v122 offset:3072
	ds_read_b32 v107, v122 offset:3584
	ds_read_b32 v108, v122 offset:4096
	ds_read_b32 v109, v122 offset:4608
	ds_read_b32 v110, v122 offset:5120
	ds_read_b32 v111, v122 offset:5632
	ds_read_b32 v112, v122 offset:6144
	ds_read_b32 v113, v122 offset:6656
	ds_read_b32 v114, v122 offset:7168
	ds_read_b32 v115, v122 offset:7680
	s_waitcnt lgkmcnt(0)
	v_max_f32_e32 v100, v100, v100
	v_max_f32_e32 v101, v101, v101
	v_max_f32_e32 v102, v102, v102
	v_max_f32_e32 v103, v103, v103
	v_max_f32_e32 v104, v104, v104
	v_max_f32_e32 v105, v105, v105
	v_max_f32_e32 v106, v106, v106
	v_max_f32_e32 v107, v107, v107
	v_max_f32_e32 v108, v108, v108
	v_max_f32_e32 v109, v109, v109
	v_max_f32_e32 v110, v110, v110
	v_max_f32_e32 v111, v111, v111
	v_max_f32_e32 v112, v112, v112
	v_max_f32_e32 v113, v113, v113
	v_max_f32_e32 v114, v114, v114
	v_max_f32_e32 v115, v115, v115
	v_med3_f32 v100, v100, s20, v129
	v_med3_f32 v101, v101, s20, v129
	v_med3_f32 v102, v102, s20, v129
	v_med3_f32 v103, v103, s20, v129
	v_med3_f32 v104, v104, s20, v129
	v_med3_f32 v105, v105, s20, v129
	v_med3_f32 v106, v106, s20, v129
	v_med3_f32 v107, v107, s20, v129
	v_med3_f32 v108, v108, s20, v129
	v_med3_f32 v109, v109, s20, v129
	v_med3_f32 v110, v110, s20, v129
	v_med3_f32 v111, v111, s20, v129
	v_med3_f32 v112, v112, s20, v129
	v_med3_f32 v113, v113, s20, v129
	v_med3_f32 v114, v114, s20, v129
	v_med3_f32 v115, v115, s20, v129
	v_mov_b32_e32 v116, 0
	v_mov_b32_e32 v117, 0
	v_mov_b32_e32 v118, 0
	v_mov_b32_e32 v119, 0
	v_cvt_pk_fp8_f32 v116, v100, v101
	v_cvt_pk_fp8_f32 v117, v104, v105
	v_cvt_pk_fp8_f32 v118, v108, v109
	v_cvt_pk_fp8_f32 v119, v112, v113
	v_cvt_pk_fp8_f32 v116, v102, v103 op_sel:[0,0,1]
	v_cvt_pk_fp8_f32 v117, v106, v107 op_sel:[0,0,1]
	v_cvt_pk_fp8_f32 v118, v110, v111 op_sel:[0,0,1]
	v_cvt_pk_fp8_f32 v119, v114, v115 op_sel:[0,0,1]
	s_nop 0
	global_store_dwordx4 v127, v[116:119], s[14:15]
	ds_read_b32 v100, v124
	ds_read_b32 v101, v124 offset:512
	ds_read_b32 v102, v124 offset:1024
	ds_read_b32 v103, v124 offset:1536
	ds_read_b32 v104, v124 offset:2048
	ds_read_b32 v105, v124 offset:2560
	ds_read_b32 v106, v124 offset:3072
	ds_read_b32 v107, v124 offset:3584
	ds_read_b32 v108, v124 offset:4096
	ds_read_b32 v109, v124 offset:4608
	ds_read_b32 v110, v124 offset:5120
	ds_read_b32 v111, v124 offset:5632
	ds_read_b32 v112, v124 offset:6144
	ds_read_b32 v113, v124 offset:6656
	ds_read_b32 v114, v124 offset:7168
	ds_read_b32 v115, v124 offset:7680
	s_waitcnt lgkmcnt(0)
	v_max_f32_e32 v100, v100, v100
	v_max_f32_e32 v101, v101, v101
	v_max_f32_e32 v102, v102, v102
	v_max_f32_e32 v103, v103, v103
	v_max_f32_e32 v104, v104, v104
	v_max_f32_e32 v105, v105, v105
	v_max_f32_e32 v106, v106, v106
	v_max_f32_e32 v107, v107, v107
	v_max_f32_e32 v108, v108, v108
	v_max_f32_e32 v109, v109, v109
	v_max_f32_e32 v110, v110, v110
	v_max_f32_e32 v111, v111, v111
	v_max_f32_e32 v112, v112, v112
	v_max_f32_e32 v113, v113, v113
	v_max_f32_e32 v114, v114, v114
	v_max_f32_e32 v115, v115, v115
	v_med3_f32 v100, v100, s20, v129
	v_med3_f32 v101, v101, s20, v129
	v_med3_f32 v102, v102, s20, v129
	v_med3_f32 v103, v103, s20, v129
	v_med3_f32 v104, v104, s20, v129
	v_med3_f32 v105, v105, s20, v129
	v_med3_f32 v106, v106, s20, v129
	v_med3_f32 v107, v107, s20, v129
	v_med3_f32 v108, v108, s20, v129
	v_med3_f32 v109, v109, s20, v129
	v_med3_f32 v110, v110, s20, v129
	v_med3_f32 v111, v111, s20, v129
	v_med3_f32 v112, v112, s20, v129
	v_med3_f32 v113, v113, s20, v129
	v_med3_f32 v114, v114, s20, v129
	v_med3_f32 v115, v115, s20, v129
	v_mov_b32_e32 v116, 0
	v_mov_b32_e32 v117, 0
	v_mov_b32_e32 v118, 0
	v_mov_b32_e32 v119, 0
	v_cvt_pk_fp8_f32 v116, v100, v101
	v_cvt_pk_fp8_f32 v117, v104, v105
	v_cvt_pk_fp8_f32 v118, v108, v109
	v_cvt_pk_fp8_f32 v119, v112, v113
	v_cvt_pk_fp8_f32 v116, v102, v103 op_sel:[0,0,1]
	v_cvt_pk_fp8_f32 v117, v106, v107 op_sel:[0,0,1]
	v_cvt_pk_fp8_f32 v118, v110, v111 op_sel:[0,0,1]
	v_cvt_pk_fp8_f32 v119, v114, v115 op_sel:[0,0,1]
	s_nop 0
	global_store_dwordx4 v128, v[116:119], s[14:15]
	s_waitcnt vmcnt(4)
	v_mul_f32_e32 v68, 0x43000000, v68
	v_mul_f32_e32 v69, 0x43000000, v69
	v_mul_f32_e32 v70, 0x43000000, v70
	v_mul_f32_e32 v71, 0x43000000, v71
	ds_write_b128 v121, v[68:71]
	v_mul_f32_e32 v72, 0x43000000, v72
	v_mul_f32_e32 v73, 0x43000000, v73
	v_mul_f32_e32 v74, 0x43000000, v74
	v_mul_f32_e32 v75, 0x43000000, v75
	ds_write_b128 v121, v[72:75] offset:1024
	v_mul_f32_e32 v76, 0x43000000, v76
	v_mul_f32_e32 v77, 0x43000000, v77
	v_mul_f32_e32 v78, 0x43000000, v78
	v_mul_f32_e32 v79, 0x43000000, v79
	ds_write_b128 v121, v[76:79] offset:2048
	v_mul_f32_e32 v80, 0x43000000, v80
	v_mul_f32_e32 v81, 0x43000000, v81
	v_mul_f32_e32 v82, 0x43000000, v82
	v_mul_f32_e32 v83, 0x43000000, v83
	ds_write_b128 v121, v[80:83] offset:3072
	v_mul_f32_e32 v84, 0x43000000, v84
	v_mul_f32_e32 v85, 0x43000000, v85
	v_mul_f32_e32 v86, 0x43000000, v86
	v_mul_f32_e32 v87, 0x43000000, v87
	ds_write_b128 v121, v[84:87] offset:4096
	v_mul_f32_e32 v88, 0x43000000, v88
	v_mul_f32_e32 v89, 0x43000000, v89
	v_mul_f32_e32 v90, 0x43000000, v90
	v_mul_f32_e32 v91, 0x43000000, v91
	ds_write_b128 v121, v[88:91] offset:5120
	v_mul_f32_e32 v92, 0x43000000, v92
	v_mul_f32_e32 v93, 0x43000000, v93
	v_mul_f32_e32 v94, 0x43000000, v94
	v_mul_f32_e32 v95, 0x43000000, v95
	ds_write_b128 v121, v[92:95] offset:6144
	v_mul_f32_e32 v96, 0x43000000, v96
	v_mul_f32_e32 v97, 0x43000000, v97
	v_mul_f32_e32 v98, 0x43000000, v98
	v_mul_f32_e32 v99, 0x43000000, v99
	ds_write_b128 v121, v[96:99] offset:7168
	s_waitcnt lgkmcnt(0)
	s_barrier
; #define GAS __attribute__((address_space(1)))
; #define LAS __attribute__((address_space(3)))
; #define LDS_WAIT() asm volatile("s_waitcnt lgkmcnt(0)" ::: "memory")
;     ...
; #pragma unroll
;     for (int i = 0; i < 32; ++i) v[i] = sc >= 0 ? W[(size_t)(k0 + 2 * i + (lane >> 5)) * Nsrc + sc] : 0.f;
; #pragma unroll
;     for (int i = 0; i < 32; ++i) { const int k = k0 + 2 * i + (lane >> 5); float x = v[i] * wscale; if (KS) x *= (k < ksplit ? ksA[k] : ksB[k - ksplit]); scr[(2 * i + (lane >> 5)) * 33 + (lane & 31)] = x; }
;     LDS_WAIT(); asm volatile("" ::: "memory");
;     const int c = lane & 7;
; #pragma unroll
;     for (int j = 0; j < 4; ++j) { const int n = (lane >> 3) + 8 * j; const LAS float* s = scr + (8 * c) * 33 + n;
;         const unsigned long long o = (unsigned long long)pg8::pk4_fp8(s[0 * 33], s[1 * 33], s[2 * 33], s[3 * 33]) | ((unsigned long long)pg8::pk4_fp8(s[4 * 33], s[5 * 33], s[6 * 33], s[7 * 33]) << 32);
;         *(GAS unsigned long long*)(WT + (size_t)(n0 + n) * K + k0 + 8 * c) = o; }
; __global__ void __launch_bounds__(NWAVES * 64, 2) hybrid_fwd(Args args) {
;     ...
;             p0_transpose_item_f8<false>(args.in[16] + (size_t)l * FF * DM, FF, DM, DM / 32, (unsigned char*)(ws + WS_WDN + l * SZ_WDN), 128.f, args.in[16], args.in[16], 0, scr, r, lane);
	s_add_i32 s17, s16, 2976
	s_min_u32 s17, s17, 0xbff
	s_lshr_b32 s18, s17, 5
	s_add_i32 s18, s18, 32
	s_and_b32 s19, s17, 31
	s_lshl_b32 s19, s19, 21
	s_lshl_b32 s18, s18, 7
	s_add_u32 s18, s18, s19
	s_add_u32 s14, s4, s18
	s_addc_u32 s15, s5, 0
	ds_read_b32 v100, v123
	ds_read_b32 v101, v123 offset:512
	ds_read_b32 v102, v123 offset:1024
	ds_read_b32 v103, v123 offset:1536
	ds_read_b32 v104, v123 offset:2048
	ds_read_b32 v105, v123 offset:2560
	ds_read_b32 v106, v123 offset:3072
	ds_read_b32 v107, v123 offset:3584
	ds_read_b32 v108, v123 offset:4096
	ds_read_b32 v109, v123 offset:4608
	ds_read_b32 v110, v123 offset:5120
	ds_read_b32 v111, v123 offset:5632
	ds_read_b32 v112, v123 offset:6144
	ds_read_b32 v113, v123 offset:6656
	ds_read_b32 v114, v123 offset:7168
	ds_read_b32 v115, v123 offset:7680
	s_waitcnt lgkmcnt(0)
	v_max_f32_e32 v100, v100, v100
	v_max_f32_e32 v101, v101, v101
	v_max_f32_e32 v102, v102, v102
	v_max_f32_e32 v103, v103, v103
	v_max_f32_e32 v104, v104, v104
	v_max_f32_e32 v105, v105, v105
	v_max_f32_e32 v106, v106, v106
	v_max_f32_e32 v107, v107, v107
	v_max_f32_e32 v108, v108, v108
	v_max_f32_e32 v109, v109, v109
	v_max_f32_e32 v110, v110, v110
	v_max_f32_e32 v111, v111, v111
	v_max_f32_e32 v112, v112, v112
	v_max_f32_e32 v113, v113, v113
	v_max_f32_e32 v114, v114, v114
	v_max_f32_e32 v115, v115, v115
	v_med3_f32 v100, v100, s20, v129
	v_med3_f32 v101, v101, s20, v129
	v_med3_f32 v102, v102, s20, v129
	v_med3_f32 v103, v103, s20, v129
	v_med3_f32 v104, v104, s20, v129
	v_med3_f32 v105, v105, s20, v129
	v_med3_f32 v106, v106, s20, v129
	v_med3_f32 v107, v107, s20, v129
	v_med3_f32 v108, v108, s20, v129
	v_med3_f32 v109, v109, s20, v129
	v_med3_f32 v110, v110, s20, v129
	v_med3_f32 v111, v111, s20, v129
	v_med3_f32 v112, v112, s20, v129
	v_med3_f32 v113, v113, s20, v129
	v_med3_f32 v114, v114, s20, v129
	v_med3_f32 v115, v115, s20, v129
	v_mov_b32_e32 v116, 0
	v_mov_b32_e32 v117, 0
	v_mov_b32_e32 v118, 0
	v_mov_b32_e32 v119, 0
	v_cvt_pk_fp8_f32 v116, v100, v101
	v_cvt_pk_fp8_f32 v117, v104, v105
	v_cvt_pk_fp8_f32 v118, v108, v109
	v_cvt_pk_fp8_f32 v119, v112, v113
	v_cvt_pk_fp8_f32 v116, v102, v103 op_sel:[0,0,1]
	v_cvt_pk_fp8_f32 v117, v106, v107 op_sel:[0,0,1]
	v_cvt_pk_fp8_f32 v118, v110, v111 op_sel:[0,0,1]
	v_cvt_pk_fp8_f32 v119, v114, v115 op_sel:[0,0,1]
	s_nop 0
	global_store_dwordx4 v127, v[116:119], s[14:15]
	ds_read_b32 v100, v125
	ds_read_b32 v101, v125 offset:512
	ds_read_b32 v102, v125 offset:1024
	ds_read_b32 v103, v125 offset:1536
	ds_read_b32 v104, v125 offset:2048
	ds_read_b32 v105, v125 offset:2560
	ds_read_b32 v106, v125 offset:3072
	ds_read_b32 v107, v125 offset:3584
	ds_read_b32 v108, v125 offset:4096
	ds_read_b32 v109, v125 offset:4608
	ds_read_b32 v110, v125 offset:5120
	ds_read_b32 v111, v125 offset:5632
	ds_read_b32 v112, v125 offset:6144
	ds_read_b32 v113, v125 offset:6656
	ds_read_b32 v114, v125 offset:7168
	ds_read_b32 v115, v125 offset:7680
	s_waitcnt lgkmcnt(0)
	v_max_f32_e32 v100, v100, v100
	v_max_f32_e32 v101, v101, v101
	v_max_f32_e32 v102, v102, v102
	v_max_f32_e32 v103, v103, v103
	v_max_f32_e32 v104, v104, v104
	v_max_f32_e32 v105, v105, v105
	v_max_f32_e32 v106, v106, v106
	v_max_f32_e32 v107, v107, v107
	v_max_f32_e32 v108, v108, v108
	v_max_f32_e32 v109, v109, v109
	v_max_f32_e32 v110, v110, v110
	v_max_f32_e32 v111, v111, v111
	v_max_f32_e32 v112, v112, v112
	v_max_f32_e32 v113, v113, v113
	v_max_f32_e32 v114, v114, v114
	v_max_f32_e32 v115, v115, v115
	v_med3_f32 v100, v100, s20, v129
	v_med3_f32 v101, v101, s20, v129
	v_med3_f32 v102, v102, s20, v129
	v_med3_f32 v103, v103, s20, v129
	v_med3_f32 v104, v104, s20, v129
	v_med3_f32 v105, v105, s20, v129
	v_med3_f32 v106, v106, s20, v129
	v_med3_f32 v107, v107, s20, v129
	v_med3_f32 v108, v108, s20, v129
	v_med3_f32 v109, v109, s20, v129
	v_med3_f32 v110, v110, s20, v129
	v_med3_f32 v111, v111, s20, v129
	v_med3_f32 v112, v112, s20, v129
	v_med3_f32 v113, v113, s20, v129
	v_med3_f32 v114, v114, s20, v129
	v_med3_f32 v115, v115, s20, v129
	v_mov_b32_e32 v116, 0
	v_mov_b32_e32 v117, 0
	v_mov_b32_e32 v118, 0
	v_mov_b32_e32 v119, 0
	v_cvt_pk_fp8_f32 v116, v100, v101
	v_cvt_pk_fp8_f32 v117, v104, v105
	v_cvt_pk_fp8_f32 v118, v108, v109
	v_cvt_pk_fp8_f32 v119, v112, v113
	v_cvt_pk_fp8_f32 v116, v102, v103 op_sel:[0,0,1]
	v_cvt_pk_fp8_f32 v117, v106, v107 op_sel:[0,0,1]
	v_cvt_pk_fp8_f32 v118, v110, v111 op_sel:[0,0,1]
	v_cvt_pk_fp8_f32 v119, v114, v115 op_sel:[0,0,1]
	s_nop 0
	global_store_dwordx4 v128, v[116:119], s[14:15]
	s_waitcnt vmcnt(0) lgkmcnt(0)
	s_barrier
